# NA: 64 exec-masked rpb LDS reads per unit hoisted to stage start + v_cndmask (on top of epires pipelining)
# baseline (speedup 1.0000x reference)
; #define LAS __attribute__((address_space(3)))
; template <bool LOCAL>
; __device__ __forceinline__ void na_unit(const bf16* P, const bf16* VT, bf16* YCAT, const LAS float* rpb_l, LAS bf16* buf, int b, int gr, int hp, int qblk, int tid) {
;     ...
;     const int qrow0 = LOCAL ? NCTX + b * SEQ + gr * 64 + 16 * qb : b * CTXL + qblk * 64 + 16 * qb;
;     const int r0 = min(max(gr - 4, 0), 24);
;     const int kc0 = qb == 0 ? 0 : qb == 1 ? 8 : qb == 2 ? 24 : 32;
;     const int qcol = 16 * qb + fr, cs = min(max(qcol - 8, 0), 48);
;     const LAS float* rpb = rpb_l + h * 15 * 31;
;     v4u ld[2][2];
;     const int lrow = (tid >> 3) & 63, lseg = tid & 7;
;     ...
;     bf16x8 qf[2];
; #pragma unroll
;     for (int ks = 0; ks < 2; ++ks) qf[ks] = *(const bf16x8*)(P + (size_t)(qrow0 + fr) * DINP + h * 64 + 32 * ks + 8 * fq);
;     f32x4 sl[16], sc[16];
;     float m = -1.0e30f, lsum = 0.f;
;     f32x4 o[4];
; #pragma unroll
;     for (int dt = 0; dt < 4; ++dt) o[dt] = (f32x4){0.f, 0.f, 0.f, 0.f};
;     NA_ISSUE(0); NA_ISSUE(1); NA_STORE(0);
;     __syncthreads();
; #pragma unroll
;     for (int sidx = 0; sidx < 2 * NCH; ++sidx) {
;         if (sidx + 2 < 2 * NCH) NA_ISSUE(sidx + 2);
;         const LAS bf16* cb = buf + (sidx & 1) * 9216 + hh * 4608;
;         if (sidx < NCH) {
;             const int c = sidx;
;             if (LOCAL && c < 8) {
; #pragma unroll
;                 for (int t2 = 0; t2 < 2; ++t2) {
;                     const LAS bf16* kp = cb + (kc0 + 16 * t2 + fr) * 72 + 8 * fq;
;                     f32x4 acc = {0.f, 0.f, 0.f, 0.f};
;                     acc = __builtin_amdgcn_mfma_f32_16x16x32_bf16(*(const LAS bf16x8*)(kp), qf[0], acc, 0, 0, 0);
;                     acc = __builtin_amdgcn_mfma_f32_16x16x32_bf16(*(const LAS bf16x8*)(kp + 32), qf[1], acc, 0, 0, 0);
;                     const LAS float* rb = rpb + (r0 + c - gr + 7) * 31 + 15 - qcol;
; #pragma unroll
;                     for (int e = 0; e < 4; ++e) { const int kcol = kc0 + 16 * t2 + 4 * fq + e; const bool ok = (kcol >= cs) && (kcol < cs + 16);
;                         const float sv = ok ? acc[e] * 0.125f + rb[ok ? kcol : qcol] : -1.0e30f; acc[e] = sv; m = fmaxf(m, sv); }
;                     sl[2 * (c < 8 ? c : 0) + t2] = acc; }
.LBB0_406:
	s_or_b64 exec, exec, s[0:1]
	s_bfe_u32 s19, s76, 0x50002
	v_sub_u32_e64 v3, s19, 4 clamp
	s_ashr_i32 s17, s76, 7
	v_readfirstlane_b32 s0, v3
	s_lshl_b32 s26, s17, 11
	s_min_u32 s20, s0, 24
	s_add_i32 s14, s26, 0x1000
	s_lshl_b32 s15, s20, 6
	s_or_b32 s16, s15, s14
	v_mov_b64_e32 v[18:19], s[8:9]
	v_and_b32_e32 v32, 7, v94
	v_or_b32_e32 v3, s16, v89
	s_and_b32 s18, s76, 3
	v_mad_i64_i32 v[4:5], s[0:1], v3, s70, v[18:19]
	v_lshlrev_b32_e32 v26, 4, v32
	v_mov_b32_e32 v27, v71
	v_lshl_add_u64 v[4:5], v[4:5], 0, v[26:27]
	s_lshl_b32 s2, s18, 8
	v_lshl_add_u64 v[4:5], v[4:5], 0, s[2:3]
	global_load_dwordx4 v[10:13], v[4:5], off offset:1024
	global_load_dwordx4 v[14:17], v[4:5], off offset:1152
	s_lshl_b32 s0, s19, 6
	v_lshl_or_b32 v31, v2, 4, v90
	v_lshl_add_u32 v33, s18, 1, v93
	s_or_b32 s0, s14, s0
	v_mad_u32_u24 v2, v89, s71, 0
	v_lshlrev_b32_e32 v72, 6, v33
	s_add_i32 s50, s26, 0x1040
	v_or_b32_e32 v74, s0, v31
	v_add_u32_e32 v75, v2, v26
	v_ashrrev_i32_e32 v73, 31, v72
	v_or_b32_e32 v4, s50, v89
	v_mad_i64_i32 v[2:3], s[0:1], v74, s70, v[18:19]
	v_add_u32_e32 v4, s15, v4
	v_lshl_add_u64 v[2:3], v[72:73], 1, v[2:3]
	v_mad_i64_i32 v[4:5], s[0:1], v4, s70, v[18:19]
	v_lshl_add_u64 v[2:3], v[2:3], 0, v[70:71]
	v_lshl_add_u64 v[20:21], v[4:5], 0, v[26:27]
	global_load_dwordx4 v[6:9], v[2:3], off
	s_nop 0
	global_load_dwordx4 v[2:5], v[2:3], off offset:64
	s_or_b32 s14, s26, s15
	s_addk_i32 s14, 0x1080
	v_or_b32_e32 v24, s14, v89
	v_mad_i64_i32 v[28:29], s[0:1], v24, s70, v[18:19]
	v_lshl_add_u64 v[26:27], v[28:29], 0, v[26:27]
	v_lshl_add_u64 v[22:23], v[20:21], 0, s[2:3]
	v_lshl_add_u64 v[26:27], v[26:27], 0, s[2:3]
	global_load_dwordx4 v[18:21], v[22:23], off offset:1024
	s_nop 0
	global_load_dwordx4 v[22:25], v[22:23], off offset:1152
	v_add_u32_e32 v30, v87, v70
	v_add_u32_e32 v34, v91, v90
	v_mad_u32_u24 v36, v34, s71, v30
	s_movk_i32 s0, 0x744
	v_mul_lo_u32 v33, v33, s0
	s_sub_i32 s0, s20, s19
	s_mulk_i32 s0, 0x7c
	v_sub_u32_e64 v35, v31, 8 clamp
	s_add_i32 s0, s0, 0
	v_min_u32_e32 v35, 48, v35
	v_lshlrev_b32_e32 v77, 2, v92
	v_add_u32_e32 v33, s0, v33
	v_lshlrev_b32_e32 v31, 2, v31
	v_sub_u32_e32 v31, v33, v31
	v_add_u32_e32 v33, v91, v77
	v_cmp_ge_u32_e32 vcc, v33, v35
	v_mov_b32_e32 v92, 0xf149f2ca
	v_lshl_add_u32 v31, v33, 2, v31
	v_mov_b32_e32 v93, 0xf149f2ca
	s_waitcnt vmcnt(5)
	ds_write_b128 v75, v[10:13]
	s_waitcnt vmcnt(4)
	ds_write_b128 v75, v[14:17] offset:9216
	s_waitcnt lgkmcnt(0)
	s_barrier
	ds_read_b32 v240, v31 offset:37792
	ds_read_b32 v241, v31 offset:37796
	ds_read_b32 v242, v31 offset:37800
	ds_read_b32 v243, v31 offset:37804
	ds_read_b32 v244, v31 offset:37856
	ds_read_b32 v245, v31 offset:37860
	ds_read_b32 v246, v31 offset:37864
	ds_read_b32 v247, v31 offset:37868
	global_load_dwordx4 v[10:13], v[26:27], off offset:1024
	global_load_dwordx4 v[14:17], v[26:27], off offset:1152
	ds_read_b128 v[26:29], v36
	ds_read_b128 v[38:41], v36 offset:64
	s_waitcnt vmcnt(5) lgkmcnt(1)
	v_mfma_f32_16x16x32_bf16 v[26:29], v[26:29], v[6:9], 0
	v_add_u32_e32 v36, 16, v35
	v_cmp_lt_u32_e64 s[0:1], v33, v36
	s_and_b64 s[28:29], vcc, s[0:1]
	s_waitcnt vmcnt(4) lgkmcnt(0)
	v_mfma_f32_16x16x32_bf16 v[26:29], v[38:41], v[2:5], v[26:29]
	s_nop 2
	s_waitcnt lgkmcnt(0)
	s_nop 3
	v_fmac_f32_e32 v240, 0x3e000000, v26
	v_cndmask_b32_e64 v93, v93, v240, s[28:29]
	s_nop 4
	v_or_b32_e32 v26, 1, v33
	v_cmp_ge_u32_e32 vcc, v26, v35
	v_cmp_lt_u32_e64 s[0:1], v26, v36
	s_and_b64 s[30:31], vcc, s[0:1]
	s_nop 2
	s_waitcnt lgkmcnt(0)
	v_fmac_f32_e32 v241, 0x3e000000, v27
	v_cndmask_b32_e64 v92, v92, v241, s[30:31]
	v_or_b32_e32 v26, 2, v33
	v_cmp_ge_u32_e32 vcc, v26, v35
	v_cmp_lt_u32_e64 s[0:1], v26, v36
	s_and_b64 s[34:35], vcc, s[0:1]
	v_mov_b32_e32 v94, 0xf149f2ca
	v_mov_b32_e32 v95, 0xf149f2ca
	s_nop 2
	s_waitcnt lgkmcnt(0)
	v_fmac_f32_e32 v242, 0x3e000000, v28
	v_cndmask_b32_e64 v95, v95, v242, s[34:35]
	v_or_b32_e32 v26, 3, v33
	v_cmp_ge_u32_e32 vcc, v26, v35
	v_cmp_lt_u32_e64 s[0:1], v26, v36
	s_and_b64 s[36:37], vcc, s[0:1]
	s_nop 2
	s_waitcnt lgkmcnt(0)
	v_fmac_f32_e32 v243, 0x3e000000, v29
	v_cndmask_b32_e64 v94, v94, v243, s[36:37]
	v_add_u32_e32 v37, 16, v91
	v_add_u32_e32 v33, v37, v90
	v_mad_u32_u24 v38, v33, s71, v30
	ds_read_b128 v[26:29], v38
	ds_read_b128 v[38:41], v38 offset:64
	v_add_u32_e32 v37, v37, v77
	v_cmp_ge_u32_e32 vcc, v37, v35
	v_cmp_lt_u32_e64 s[0:1], v37, v36
	s_waitcnt lgkmcnt(1)
	v_mfma_f32_16x16x32_bf16 v[26:29], v[26:29], v[6:9], 0
	s_and_b64 s[38:39], vcc, s[0:1]
	v_mov_b32_e32 v96, 0xf149f2ca
	v_mov_b32_e32 v97, 0xf149f2ca
	s_waitcnt lgkmcnt(0)
	v_mfma_f32_16x16x32_bf16 v[26:29], v[38:41], v[2:5], v[26:29]
	s_nop 2
	s_waitcnt lgkmcnt(0)
	s_nop 3
	v_fmac_f32_e32 v244, 0x3e000000, v26
	v_cndmask_b32_e64 v97, v97, v244, s[38:39]
	s_nop 4
	v_or_b32_e32 v26, 1, v37
	v_cmp_ge_u32_e32 vcc, v26, v35
	v_cmp_lt_u32_e64 s[0:1], v26, v36
	s_and_b64 s[44:45], vcc, s[0:1]
	s_nop 2
	s_waitcnt lgkmcnt(0)
	v_fmac_f32_e32 v245, 0x3e000000, v27
	v_cndmask_b32_e64 v96, v96, v245, s[44:45]
	v_or_b32_e32 v26, 2, v37
	v_cmp_ge_u32_e32 vcc, v26, v35
	v_cmp_lt_u32_e64 s[0:1], v26, v36
	s_and_b64 s[46:47], vcc, s[0:1]
	v_mov_b32_e32 v98, 0xf149f2ca
	v_mov_b32_e32 v100, 0xf149f2ca
	s_nop 2
	s_waitcnt lgkmcnt(0)
	v_fmac_f32_e32 v246, 0x3e000000, v28
	v_cndmask_b32_e64 v100, v100, v246, s[46:47]
	v_or_b32_e32 v26, 3, v37
	v_cmp_ge_u32_e32 vcc, v26, v35
	v_cmp_lt_u32_e64 s[0:1], v26, v36
	s_and_b64 s[64:65], vcc, s[0:1]
	s_nop 2
	s_waitcnt lgkmcnt(0)
	v_fmac_f32_e32 v247, 0x3e000000, v29
	v_cndmask_b32_e64 v98, v98, v247, s[64:65]
	v_mul_u32_u24_e32 v27, 0x90, v34
	v_lshlrev_b32_e32 v26, 3, v32
	v_add_u32_e32 v32, v30, v27
	s_waitcnt vmcnt(3)
	ds_write_b128 v75, v[18:21] offset:18432
	s_waitcnt vmcnt(2)
	ds_write_b128 v75, v[22:25] offset:27648
	s_waitcnt lgkmcnt(0)
	s_barrier
; #define LAS __attribute__((address_space(3)))
; template <bool LOCAL>
; __device__ __forceinline__ void na_unit(const bf16* P, const bf16* VT, bf16* YCAT, const LAS float* rpb_l, LAS bf16* buf, int b, int gr, int hp, int qblk, int tid) {
;     ...
;     for (int sidx = 0; sidx < 2 * NCH; ++sidx) {
;         if (sidx + 2 < 2 * NCH) NA_ISSUE(sidx + 2);
;         const LAS bf16* cb = buf + (sidx & 1) * 9216 + hh * 4608;
;         if (sidx < NCH) {
;             const int c = sidx;
;             if (LOCAL && c < 8) {
; #pragma unroll
;                 for (int t2 = 0; t2 < 2; ++t2) {
;                     const LAS bf16* kp = cb + (kc0 + 16 * t2 + fr) * 72 + 8 * fq;
;                     f32x4 acc = {0.f, 0.f, 0.f, 0.f};
;                     acc = __builtin_amdgcn_mfma_f32_16x16x32_bf16(*(const LAS bf16x8*)(kp), qf[0], acc, 0, 0, 0);
;                     acc = __builtin_amdgcn_mfma_f32_16x16x32_bf16(*(const LAS bf16x8*)(kp + 32), qf[1], acc, 0, 0, 0);
;                     const LAS float* rb = rpb + (r0 + c - gr + 7) * 31 + 15 - qcol;
; #pragma unroll
;                     for (int e = 0; e < 4; ++e) { const int kcol = kc0 + 16 * t2 + 4 * fq + e; const bool ok = (kcol >= cs) && (kcol < cs + 16);
;                         const float sv = ok ? acc[e] * 0.125f + rb[ok ? kcol : qcol] : -1.0e30f; acc[e] = sv; m = fmaxf(m, sv); }
;                     sl[2 * (c < 8 ? c : 0) + t2] = acc; }
	ds_read_b32 v240, v31 offset:37916
	ds_read_b32 v241, v31 offset:37920
	ds_read_b32 v242, v31 offset:37924
	ds_read_b32 v243, v31 offset:37928
	ds_read_b32 v244, v31 offset:37980
	ds_read_b32 v245, v31 offset:37984
	ds_read_b32 v246, v31 offset:37988
	ds_read_b32 v247, v31 offset:37992
	ds_read_b128 v[18:21], v32 offset:18432
	s_add_i32 s26, s26, s15
	s_add_i32 s0, s26, 0x10c0
	v_or_b32_e32 v24, s0, v89
	v_mov_b64_e32 v[22:23], s[8:9]
	s_lshl_b32 s1, s18, 7
	v_mad_i64_i32 v[22:23], s[18:19], v24, s70, v[22:23]
	v_lshlrev_b32_e32 v70, 1, v26
	v_lshl_add_u64 v[22:23], v[22:23], 0, v[70:71]
	s_lshl_b32 s2, s1, 1
	v_lshl_add_u64 v[22:23], v[22:23], 0, s[2:3]
	ds_read_b128 v[26:29], v32 offset:18496
	s_waitcnt lgkmcnt(1)
	v_mfma_f32_16x16x32_bf16 v[34:37], v[18:21], v[6:9], 0
	global_load_dwordx4 v[18:21], v[22:23], off offset:1024
	s_nop 0
	global_load_dwordx4 v[22:25], v[22:23], off offset:1152
	v_mov_b32_e32 v99, 0xf149f2ca
	v_mov_b32_e32 v101, 0xf149f2ca
	s_waitcnt lgkmcnt(0)
	v_mfma_f32_16x16x32_bf16 v[26:29], v[26:29], v[2:5], v[34:37]
	s_nop 2
	s_waitcnt lgkmcnt(0)
	s_nop 3
	v_fmac_f32_e32 v240, 0x3e000000, v26
	v_cndmask_b32_e64 v101, v101, v240, s[28:29]
	s_nop 2
	s_waitcnt lgkmcnt(0)
	s_nop 0
	v_fmac_f32_e32 v241, 0x3e000000, v27
	v_cndmask_b32_e64 v99, v99, v241, s[30:31]
	v_mov_b32_e32 v102, 0xf149f2ca
	v_mov_b32_e32 v103, 0xf149f2ca
	s_nop 2
	s_waitcnt lgkmcnt(0)
	v_fmac_f32_e32 v242, 0x3e000000, v28
	v_cndmask_b32_e64 v103, v103, v242, s[34:35]
	s_nop 2
	s_waitcnt lgkmcnt(0)
	v_fmac_f32_e32 v243, 0x3e000000, v29
	v_cndmask_b32_e64 v102, v102, v243, s[36:37]
	v_mul_u32_u24_e32 v26, 0x90, v33
	v_add_u32_e32 v33, v30, v26
	ds_read_b128 v[26:29], v33 offset:18432
	ds_read_b128 v[34:37], v33 offset:18496
	v_mov_b32_e32 v104, 0xf149f2ca
	v_mov_b32_e32 v106, 0xf149f2ca
	s_waitcnt lgkmcnt(1)
	v_mfma_f32_16x16x32_bf16 v[26:29], v[26:29], v[6:9], 0
	s_waitcnt lgkmcnt(0)
	v_mfma_f32_16x16x32_bf16 v[26:29], v[34:37], v[2:5], v[26:29]
	s_nop 2
	s_waitcnt lgkmcnt(0)
	s_nop 3
	v_fmac_f32_e32 v244, 0x3e000000, v26
	v_cndmask_b32_e64 v106, v106, v244, s[38:39]
	s_nop 2
	s_waitcnt lgkmcnt(0)
	s_nop 0
	v_fmac_f32_e32 v245, 0x3e000000, v27
	v_cndmask_b32_e64 v104, v104, v245, s[44:45]
	v_mov_b32_e32 v108, 0xf149f2ca
	v_mov_b32_e32 v110, 0xf149f2ca
	s_nop 2
	s_waitcnt lgkmcnt(0)
	v_fmac_f32_e32 v246, 0x3e000000, v28
	v_cndmask_b32_e64 v110, v110, v246, s[46:47]
	s_nop 2
	s_waitcnt lgkmcnt(0)
	v_fmac_f32_e32 v247, 0x3e000000, v29
	v_cndmask_b32_e64 v108, v108, v247, s[64:65]
	s_waitcnt vmcnt(3)
	ds_write_b128 v75, v[10:13]
	s_waitcnt vmcnt(2)
	ds_write_b128 v75, v[14:17] offset:9216
	s_waitcnt lgkmcnt(0)
	s_barrier
	ds_read_b32 v240, v31 offset:38040
	ds_read_b32 v241, v31 offset:38044
	ds_read_b32 v242, v31 offset:38048
	ds_read_b32 v243, v31 offset:38052
	ds_read_b32 v244, v31 offset:38104
	ds_read_b32 v245, v31 offset:38108
	ds_read_b32 v246, v31 offset:38112
	ds_read_b32 v247, v31 offset:38116
	ds_read_b128 v[10:13], v32
	ds_read_b128 v[26:29], v32 offset:64
	s_add_i32 s18, s26, 0x1100
	v_or_b32_e32 v16, s18, v89
	v_mov_b64_e32 v[14:15], s[8:9]
	v_mad_i64_i32 v[14:15], s[20:21], v16, s70, v[14:15]
	v_lshl_add_u64 v[14:15], v[14:15], 0, v[70:71]
	v_lshl_add_u64 v[14:15], v[14:15], 0, s[2:3]
	s_waitcnt lgkmcnt(1)
	v_mfma_f32_16x16x32_bf16 v[34:37], v[10:13], v[6:9], 0
	global_load_dwordx4 v[10:13], v[14:15], off offset:1024
	s_nop 0
	global_load_dwordx4 v[14:17], v[14:15], off offset:1152
	v_mov_b32_e32 v105, 0xf149f2ca
	v_mov_b32_e32 v107, 0xf149f2ca
	s_waitcnt lgkmcnt(0)
	v_mfma_f32_16x16x32_bf16 v[26:29], v[26:29], v[2:5], v[34:37]
	s_nop 2
	s_waitcnt lgkmcnt(0)
	s_nop 3
	v_fmac_f32_e32 v240, 0x3e000000, v26
	v_cndmask_b32_e64 v107, v107, v240, s[28:29]
	s_nop 2
	s_waitcnt lgkmcnt(0)
	s_nop 0
	v_fmac_f32_e32 v241, 0x3e000000, v27
	v_cndmask_b32_e64 v105, v105, v241, s[30:31]
	v_mov_b32_e32 v109, 0xf149f2ca
	v_mov_b32_e32 v111, 0xf149f2ca
	s_nop 2
	s_waitcnt lgkmcnt(0)
	v_fmac_f32_e32 v242, 0x3e000000, v28
	v_cndmask_b32_e64 v111, v111, v242, s[34:35]
	s_nop 2
	s_waitcnt lgkmcnt(0)
	v_fmac_f32_e32 v243, 0x3e000000, v29
	v_cndmask_b32_e64 v109, v109, v243, s[36:37]
	ds_read_b128 v[26:29], v33
	ds_read_b128 v[34:37], v33 offset:64
	v_mov_b32_e32 v112, 0xf149f2ca
	v_mov_b32_e32 v114, 0xf149f2ca
	s_waitcnt lgkmcnt(1)
	v_mfma_f32_16x16x32_bf16 v[26:29], v[26:29], v[6:9], 0
	s_waitcnt lgkmcnt(0)
	v_mfma_f32_16x16x32_bf16 v[26:29], v[34:37], v[2:5], v[26:29]
	s_nop 2
	s_waitcnt lgkmcnt(0)
	s_nop 3
	v_fmac_f32_e32 v244, 0x3e000000, v26
	v_cndmask_b32_e64 v114, v114, v244, s[38:39]
	s_nop 2
	s_waitcnt lgkmcnt(0)
	s_nop 0
	v_fmac_f32_e32 v245, 0x3e000000, v27
	v_cndmask_b32_e64 v112, v112, v245, s[44:45]
	v_mov_b32_e32 v113, 0xf149f2ca
	v_mov_b32_e32 v117, 0xf149f2ca
	s_nop 2
	s_waitcnt lgkmcnt(0)
	v_fmac_f32_e32 v246, 0x3e000000, v28
	v_cndmask_b32_e64 v117, v117, v246, s[46:47]
	s_nop 2
	s_waitcnt lgkmcnt(0)
	v_fmac_f32_e32 v247, 0x3e000000, v29
	v_cndmask_b32_e64 v113, v113, v247, s[64:65]
	s_waitcnt vmcnt(3)
	ds_write_b128 v75, v[18:21] offset:18432
	s_waitcnt vmcnt(2)
	ds_write_b128 v75, v[22:25] offset:27648
	s_waitcnt lgkmcnt(0)
	s_barrier
; #define LAS __attribute__((address_space(3)))
; template <bool LOCAL>
; __device__ __forceinline__ void na_unit(const bf16* P, const bf16* VT, bf16* YCAT, const LAS float* rpb_l, LAS bf16* buf, int b, int gr, int hp, int qblk, int tid) {
;     ...
;     for (int sidx = 0; sidx < 2 * NCH; ++sidx) {
;         if (sidx + 2 < 2 * NCH) NA_ISSUE(sidx + 2);
;         const LAS bf16* cb = buf + (sidx & 1) * 9216 + hh * 4608;
;         if (sidx < NCH) {
;             const int c = sidx;
;             if (LOCAL && c < 8) {
; #pragma unroll
;                 for (int t2 = 0; t2 < 2; ++t2) {
;                     const LAS bf16* kp = cb + (kc0 + 16 * t2 + fr) * 72 + 8 * fq;
;                     f32x4 acc = {0.f, 0.f, 0.f, 0.f};
;                     acc = __builtin_amdgcn_mfma_f32_16x16x32_bf16(*(const LAS bf16x8*)(kp), qf[0], acc, 0, 0, 0);
;                     acc = __builtin_amdgcn_mfma_f32_16x16x32_bf16(*(const LAS bf16x8*)(kp + 32), qf[1], acc, 0, 0, 0);
;                     const LAS float* rb = rpb + (r0 + c - gr + 7) * 31 + 15 - qcol;
; #pragma unroll
;                     for (int e = 0; e < 4; ++e) { const int kcol = kc0 + 16 * t2 + 4 * fq + e; const bool ok = (kcol >= cs) && (kcol < cs + 16);
;                         const float sv = ok ? acc[e] * 0.125f + rb[ok ? kcol : qcol] : -1.0e30f; acc[e] = sv; m = fmaxf(m, sv); }
;                     sl[2 * (c < 8 ? c : 0) + t2] = acc; }
	ds_read_b32 v240, v31 offset:38164
	ds_read_b32 v241, v31 offset:38168
	ds_read_b32 v242, v31 offset:38172
	ds_read_b32 v243, v31 offset:38176
	ds_read_b32 v244, v31 offset:38228
	ds_read_b32 v245, v31 offset:38232
	ds_read_b32 v246, v31 offset:38236
	ds_read_b32 v247, v31 offset:38240
	ds_read_b128 v[18:21], v32 offset:18432
	ds_read_b128 v[26:29], v32 offset:18496
	s_add_i32 s20, s26, 0x1140
	v_or_b32_e32 v24, s20, v89
	v_mov_b64_e32 v[22:23], s[8:9]
	v_mad_i64_i32 v[22:23], s[22:23], v24, s70, v[22:23]
	v_lshl_add_u64 v[22:23], v[22:23], 0, v[70:71]
	v_lshl_add_u64 v[22:23], v[22:23], 0, s[2:3]
	s_waitcnt lgkmcnt(1)
	v_mfma_f32_16x16x32_bf16 v[34:37], v[18:21], v[6:9], 0
	global_load_dwordx4 v[18:21], v[22:23], off offset:1024
	s_nop 0
	global_load_dwordx4 v[22:25], v[22:23], off offset:1152
	v_mov_b32_e32 v115, 0xf149f2ca
	v_mov_b32_e32 v116, 0xf149f2ca
	s_waitcnt lgkmcnt(0)
	v_mfma_f32_16x16x32_bf16 v[26:29], v[26:29], v[2:5], v[34:37]
	s_nop 2
	s_waitcnt lgkmcnt(0)
	s_nop 3
	v_fmac_f32_e32 v240, 0x3e000000, v26
	v_cndmask_b32_e64 v116, v116, v240, s[28:29]
	s_nop 2
	s_waitcnt lgkmcnt(0)
	s_nop 0
	v_fmac_f32_e32 v241, 0x3e000000, v27
	v_cndmask_b32_e64 v115, v115, v241, s[30:31]
	v_mov_b32_e32 v118, 0xf149f2ca
	v_mov_b32_e32 v119, 0xf149f2ca
	s_nop 2
	s_waitcnt lgkmcnt(0)
	v_fmac_f32_e32 v242, 0x3e000000, v28
	v_cndmask_b32_e64 v119, v119, v242, s[34:35]
	s_nop 2
	s_waitcnt lgkmcnt(0)
	v_fmac_f32_e32 v243, 0x3e000000, v29
	v_cndmask_b32_e64 v118, v118, v243, s[36:37]
	ds_read_b128 v[26:29], v33 offset:18432
	ds_read_b128 v[34:37], v33 offset:18496
	v_mov_b32_e32 v120, 0xf149f2ca
	v_mov_b32_e32 v122, 0xf149f2ca
	s_waitcnt lgkmcnt(1)
	v_mfma_f32_16x16x32_bf16 v[26:29], v[26:29], v[6:9], 0
	s_waitcnt lgkmcnt(0)
	v_mfma_f32_16x16x32_bf16 v[26:29], v[34:37], v[2:5], v[26:29]
	s_nop 2
	s_waitcnt lgkmcnt(0)
	s_nop 3
	v_fmac_f32_e32 v244, 0x3e000000, v26
	v_cndmask_b32_e64 v122, v122, v244, s[38:39]
	s_nop 2
	s_waitcnt lgkmcnt(0)
	s_nop 0
	v_fmac_f32_e32 v245, 0x3e000000, v27
	v_cndmask_b32_e64 v120, v120, v245, s[44:45]
	v_mov_b32_e32 v121, 0xf149f2ca
	v_mov_b32_e32 v125, 0xf149f2ca
	s_nop 2
	s_waitcnt lgkmcnt(0)
	v_fmac_f32_e32 v246, 0x3e000000, v28
	v_cndmask_b32_e64 v125, v125, v246, s[46:47]
	s_nop 2
	s_waitcnt lgkmcnt(0)
	v_fmac_f32_e32 v247, 0x3e000000, v29
	v_cndmask_b32_e64 v121, v121, v247, s[64:65]
	s_waitcnt vmcnt(3)
	ds_write_b128 v75, v[10:13]
	s_waitcnt vmcnt(2)
	ds_write_b128 v75, v[14:17] offset:9216
	s_waitcnt lgkmcnt(0)
	s_barrier
	ds_read_b32 v240, v31 offset:38288
	ds_read_b32 v241, v31 offset:38292
	ds_read_b32 v242, v31 offset:38296
	ds_read_b32 v243, v31 offset:38300
	ds_read_b32 v244, v31 offset:38352
	ds_read_b32 v245, v31 offset:38356
	ds_read_b32 v246, v31 offset:38360
	ds_read_b32 v247, v31 offset:38364
	ds_read_b128 v[10:13], v32
	ds_read_b128 v[26:29], v32 offset:64
	s_add_i32 s22, s26, 0x1180
	v_or_b32_e32 v16, s22, v89
	v_mov_b64_e32 v[14:15], s[8:9]
	v_mad_i64_i32 v[14:15], s[24:25], v16, s70, v[14:15]
	v_lshl_add_u64 v[14:15], v[14:15], 0, v[70:71]
	v_lshl_add_u64 v[14:15], v[14:15], 0, s[2:3]
	s_waitcnt lgkmcnt(1)
	v_mfma_f32_16x16x32_bf16 v[34:37], v[10:13], v[6:9], 0
	global_load_dwordx4 v[10:13], v[14:15], off offset:1024
	s_nop 0
	global_load_dwordx4 v[14:17], v[14:15], off offset:1152
	v_mov_b32_e32 v123, 0xf149f2ca
	v_mov_b32_e32 v124, 0xf149f2ca
	s_waitcnt lgkmcnt(0)
	v_mfma_f32_16x16x32_bf16 v[26:29], v[26:29], v[2:5], v[34:37]
	s_nop 2
	s_waitcnt lgkmcnt(0)
	s_nop 3
	v_fmac_f32_e32 v240, 0x3e000000, v26
	v_cndmask_b32_e64 v124, v124, v240, s[28:29]
	s_nop 2
	s_waitcnt lgkmcnt(0)
	s_nop 0
	v_fmac_f32_e32 v241, 0x3e000000, v27
	v_cndmask_b32_e64 v123, v123, v241, s[30:31]
	v_mov_b32_e32 v126, 0xf149f2ca
	v_mov_b32_e32 v127, 0xf149f2ca
	s_nop 2
	s_waitcnt lgkmcnt(0)
	v_fmac_f32_e32 v242, 0x3e000000, v28
	v_cndmask_b32_e64 v127, v127, v242, s[34:35]
	s_nop 2
	s_waitcnt lgkmcnt(0)
	v_fmac_f32_e32 v243, 0x3e000000, v29
	v_cndmask_b32_e64 v126, v126, v243, s[36:37]
	ds_read_b128 v[26:29], v33
	ds_read_b128 v[34:37], v33 offset:64
	v_mov_b32_e32 v128, 0xf149f2ca
	v_mov_b32_e32 v130, 0xf149f2ca
	s_waitcnt lgkmcnt(1)
	v_mfma_f32_16x16x32_bf16 v[26:29], v[26:29], v[6:9], 0
	s_waitcnt lgkmcnt(0)
	v_mfma_f32_16x16x32_bf16 v[26:29], v[34:37], v[2:5], v[26:29]
	s_nop 2
	s_waitcnt lgkmcnt(0)
	s_nop 3
	v_fmac_f32_e32 v244, 0x3e000000, v26
	v_cndmask_b32_e64 v130, v130, v244, s[38:39]
	s_nop 2
	s_waitcnt lgkmcnt(0)
	s_nop 0
	v_fmac_f32_e32 v245, 0x3e000000, v27
	v_cndmask_b32_e64 v128, v128, v245, s[44:45]
	v_mov_b32_e32 v129, 0xf149f2ca
	v_mov_b32_e32 v134, 0xf149f2ca
	s_nop 2
	s_waitcnt lgkmcnt(0)
	v_fmac_f32_e32 v246, 0x3e000000, v28
	v_cndmask_b32_e64 v134, v134, v246, s[46:47]
	s_nop 2
	s_waitcnt lgkmcnt(0)
	v_fmac_f32_e32 v247, 0x3e000000, v29
	v_cndmask_b32_e64 v129, v129, v247, s[64:65]
	s_waitcnt vmcnt(3)
	ds_write_b128 v75, v[18:21] offset:18432
	s_waitcnt vmcnt(2)
	ds_write_b128 v75, v[22:25] offset:27648
	s_waitcnt lgkmcnt(0)
	s_barrier
; #define LAS __attribute__((address_space(3)))
; template <bool LOCAL>
; __device__ __forceinline__ void na_unit(const bf16* P, const bf16* VT, bf16* YCAT, const LAS float* rpb_l, LAS bf16* buf, int b, int gr, int hp, int qblk, int tid) {
;     ...
;     for (int sidx = 0; sidx < 2 * NCH; ++sidx) {
;         if (sidx + 2 < 2 * NCH) NA_ISSUE(sidx + 2);
;         const LAS bf16* cb = buf + (sidx & 1) * 9216 + hh * 4608;
;         if (sidx < NCH) {
;             const int c = sidx;
;             if (LOCAL && c < 8) {
; #pragma unroll
;                 for (int t2 = 0; t2 < 2; ++t2) {
;                     const LAS bf16* kp = cb + (kc0 + 16 * t2 + fr) * 72 + 8 * fq;
;                     f32x4 acc = {0.f, 0.f, 0.f, 0.f};
;                     acc = __builtin_amdgcn_mfma_f32_16x16x32_bf16(*(const LAS bf16x8*)(kp), qf[0], acc, 0, 0, 0);
;                     acc = __builtin_amdgcn_mfma_f32_16x16x32_bf16(*(const LAS bf16x8*)(kp + 32), qf[1], acc, 0, 0, 0);
;                     const LAS float* rb = rpb + (r0 + c - gr + 7) * 31 + 15 - qcol;
; #pragma unroll
;                     for (int e = 0; e < 4; ++e) { const int kcol = kc0 + 16 * t2 + 4 * fq + e; const bool ok = (kcol >= cs) && (kcol < cs + 16);
;                         const float sv = ok ? acc[e] * 0.125f + rb[ok ? kcol : qcol] : -1.0e30f; acc[e] = sv; m = fmaxf(m, sv); }
;                     sl[2 * (c < 8 ? c : 0) + t2] = acc; }
	ds_read_b32 v240, v31 offset:38412
	ds_read_b32 v241, v31 offset:38416
	ds_read_b32 v242, v31 offset:38420
	ds_read_b32 v243, v31 offset:38424
	ds_read_b32 v244, v31 offset:38476
	ds_read_b32 v245, v31 offset:38480
	ds_read_b32 v246, v31 offset:38484
	ds_read_b32 v247, v31 offset:38488
	ds_read_b128 v[18:21], v32 offset:18432
	ds_read_b128 v[26:29], v32 offset:18496
	s_add_i32 s24, s26, 0x11c0
	v_or_b32_e32 v24, s24, v89
	v_mov_b64_e32 v[22:23], s[8:9]
	v_mad_i64_i32 v[22:23], s[26:27], v24, s70, v[22:23]
	v_lshl_add_u64 v[22:23], v[22:23], 0, v[70:71]
	v_lshl_add_u64 v[22:23], v[22:23], 0, s[2:3]
	s_waitcnt lgkmcnt(1)
	v_mfma_f32_16x16x32_bf16 v[34:37], v[18:21], v[6:9], 0
	global_load_dwordx4 v[18:21], v[22:23], off offset:1024
	s_nop 0
	global_load_dwordx4 v[22:25], v[22:23], off offset:1152
	v_mov_b32_e32 v131, 0xf149f2ca
	v_mov_b32_e32 v132, 0xf149f2ca
	s_waitcnt lgkmcnt(0)
	v_mfma_f32_16x16x32_bf16 v[26:29], v[26:29], v[2:5], v[34:37]
	s_nop 2
	s_waitcnt lgkmcnt(0)
	s_nop 3
	v_fmac_f32_e32 v240, 0x3e000000, v26
	v_cndmask_b32_e64 v132, v132, v240, s[28:29]
	s_nop 2
	s_waitcnt lgkmcnt(0)
	s_nop 0
	v_fmac_f32_e32 v241, 0x3e000000, v27
	v_cndmask_b32_e64 v131, v131, v241, s[30:31]
	v_mov_b32_e32 v135, 0xf149f2ca
	v_mov_b32_e32 v136, 0xf149f2ca
	s_nop 2
	s_waitcnt lgkmcnt(0)
	v_fmac_f32_e32 v242, 0x3e000000, v28
	v_cndmask_b32_e64 v136, v136, v242, s[34:35]
	s_nop 2
	s_waitcnt lgkmcnt(0)
	v_fmac_f32_e32 v243, 0x3e000000, v29
	v_cndmask_b32_e64 v135, v135, v243, s[36:37]
	ds_read_b128 v[26:29], v33 offset:18432
	ds_read_b128 v[34:37], v33 offset:18496
	v_mov_b32_e32 v138, 0xf149f2ca
	v_mov_b32_e32 v140, 0xf149f2ca
	s_waitcnt lgkmcnt(1)
	v_mfma_f32_16x16x32_bf16 v[26:29], v[26:29], v[6:9], 0
	s_waitcnt lgkmcnt(0)
	v_mfma_f32_16x16x32_bf16 v[26:29], v[34:37], v[2:5], v[26:29]
	s_nop 2
	s_waitcnt lgkmcnt(0)
	s_nop 3
	v_fmac_f32_e32 v244, 0x3e000000, v26
	v_cndmask_b32_e64 v140, v140, v244, s[38:39]
	s_nop 2
	s_waitcnt lgkmcnt(0)
	s_nop 0
	v_fmac_f32_e32 v245, 0x3e000000, v27
	v_cndmask_b32_e64 v138, v138, v245, s[44:45]
	v_mov_b32_e32 v139, 0xf149f2ca
	v_mov_b32_e32 v143, 0xf149f2ca
	s_nop 2
	s_waitcnt lgkmcnt(0)
	v_fmac_f32_e32 v246, 0x3e000000, v28
	v_cndmask_b32_e64 v143, v143, v246, s[46:47]
	s_nop 2
	s_waitcnt lgkmcnt(0)
	v_fmac_f32_e32 v247, 0x3e000000, v29
	v_cndmask_b32_e64 v139, v139, v247, s[64:65]
	s_waitcnt vmcnt(3)
	ds_write_b128 v75, v[10:13]
	s_waitcnt vmcnt(2)
	ds_write_b128 v75, v[14:17] offset:9216
	s_waitcnt lgkmcnt(0)
	s_barrier
	ds_read_b32 v240, v31 offset:38536
	ds_read_b32 v241, v31 offset:38540
	ds_read_b32 v242, v31 offset:38544
	ds_read_b32 v243, v31 offset:38548
	ds_read_b32 v244, v31 offset:38600
	ds_read_b32 v245, v31 offset:38604
	ds_read_b32 v246, v31 offset:38608
	ds_read_b32 v247, v31 offset:38612
	ds_read_b128 v[10:13], v32
	ds_read_b128 v[26:29], v32 offset:64
	s_lshl_b32 s26, s17, 8
	v_or_b32_e32 v34, s26, v89
	v_mov_b64_e32 v[14:15], s[8:9]
	v_mad_i64_i32 v[14:15], s[52:53], v34, s70, v[14:15]
	v_lshl_add_u64 v[14:15], v[14:15], 0, v[70:71]
	v_lshl_add_u64 v[14:15], v[14:15], 0, s[2:3]
	s_waitcnt lgkmcnt(1)
	v_mfma_f32_16x16x32_bf16 v[36:39], v[10:13], v[6:9], 0
	global_load_dwordx4 v[10:13], v[14:15], off offset:1024
	s_nop 0
	global_load_dwordx4 v[14:17], v[14:15], off offset:1152
	v_mov_b32_e32 v141, 0xf149f2ca
	v_mov_b32_e32 v142, 0xf149f2ca
	s_waitcnt lgkmcnt(0)
	v_mfma_f32_16x16x32_bf16 v[26:29], v[26:29], v[2:5], v[36:39]
	s_nop 2
	s_waitcnt lgkmcnt(0)
	s_nop 3
	v_fmac_f32_e32 v240, 0x3e000000, v26
	v_cndmask_b32_e64 v142, v142, v240, s[28:29]
	s_nop 2
	s_waitcnt lgkmcnt(0)
	s_nop 0
	v_fmac_f32_e32 v241, 0x3e000000, v27
	v_cndmask_b32_e64 v141, v141, v241, s[30:31]
	v_mov_b32_e32 v144, 0xf149f2ca
	v_mov_b32_e32 v145, 0xf149f2ca
	s_nop 2
	s_waitcnt lgkmcnt(0)
	v_fmac_f32_e32 v242, 0x3e000000, v28
	v_cndmask_b32_e64 v145, v145, v242, s[34:35]
	s_nop 2
	s_waitcnt lgkmcnt(0)
	v_fmac_f32_e32 v243, 0x3e000000, v29
	v_cndmask_b32_e64 v144, v144, v243, s[36:37]
	ds_read_b128 v[26:29], v33
	ds_read_b128 v[36:39], v33 offset:64
	v_mov_b32_e32 v148, 0xf149f2ca
	v_mov_b32_e32 v150, 0xf149f2ca
	s_waitcnt lgkmcnt(1)
	v_mfma_f32_16x16x32_bf16 v[26:29], v[26:29], v[6:9], 0
	s_waitcnt lgkmcnt(0)
	v_mfma_f32_16x16x32_bf16 v[26:29], v[36:39], v[2:5], v[26:29]
	s_nop 2
	s_waitcnt lgkmcnt(0)
	s_nop 3
	v_fmac_f32_e32 v244, 0x3e000000, v26
	v_cndmask_b32_e64 v150, v150, v244, s[38:39]
	s_nop 2
	s_waitcnt lgkmcnt(0)
	s_nop 0
	v_fmac_f32_e32 v245, 0x3e000000, v27
	v_cndmask_b32_e64 v148, v148, v245, s[44:45]
	v_mov_b32_e32 v149, 0xf149f2ca
	v_mov_b32_e32 v153, 0xf149f2ca
	s_nop 2
	s_waitcnt lgkmcnt(0)
	v_fmac_f32_e32 v246, 0x3e000000, v28
	v_cndmask_b32_e64 v153, v153, v246, s[46:47]
	s_nop 2
	s_waitcnt lgkmcnt(0)
	v_fmac_f32_e32 v247, 0x3e000000, v29
	v_cndmask_b32_e64 v149, v149, v247, s[64:65]
	s_waitcnt vmcnt(3)
	ds_write_b128 v75, v[18:21] offset:18432
	s_waitcnt vmcnt(2)
	ds_write_b128 v75, v[22:25] offset:27648
	s_waitcnt lgkmcnt(0)
	s_barrier
; #define LAS __attribute__((address_space(3)))
; template <bool LOCAL>
; __device__ __forceinline__ void na_unit(const bf16* P, const bf16* VT, bf16* YCAT, const LAS float* rpb_l, LAS bf16* buf, int b, int gr, int hp, int qblk, int tid) {
;     ...
;     for (int sidx = 0; sidx < 2 * NCH; ++sidx) {
;         if (sidx + 2 < 2 * NCH) NA_ISSUE(sidx + 2);
;         const LAS bf16* cb = buf + (sidx & 1) * 9216 + hh * 4608;
;         if (sidx < NCH) {
;             const int c = sidx;
;             if (LOCAL && c < 8) {
; #pragma unroll
;                 for (int t2 = 0; t2 < 2; ++t2) {
;                     const LAS bf16* kp = cb + (kc0 + 16 * t2 + fr) * 72 + 8 * fq;
;                     f32x4 acc = {0.f, 0.f, 0.f, 0.f};
;                     acc = __builtin_amdgcn_mfma_f32_16x16x32_bf16(*(const LAS bf16x8*)(kp), qf[0], acc, 0, 0, 0);
;                     acc = __builtin_amdgcn_mfma_f32_16x16x32_bf16(*(const LAS bf16x8*)(kp + 32), qf[1], acc, 0, 0, 0);
;                     const LAS float* rb = rpb + (r0 + c - gr + 7) * 31 + 15 - qcol;
; #pragma unroll
;                     for (int e = 0; e < 4; ++e) { const int kcol = kc0 + 16 * t2 + 4 * fq + e; const bool ok = (kcol >= cs) && (kcol < cs + 16);
;                         const float sv = ok ? acc[e] * 0.125f + rb[ok ? kcol : qcol] : -1.0e30f; acc[e] = sv; m = fmaxf(m, sv); }
;                     sl[2 * (c < 8 ? c : 0) + t2] = acc; }
;             } else {
;                 const int cc = c - NLOC;
; #pragma unroll
;                 for (int t4 = 0; t4 < 4; ++t4) {
;                     const LAS bf16* kp = cb + (16 * t4 + fr) * 72 + 8 * fq;
;                     f32x4 acc = {0.f, 0.f, 0.f, 0.f};
;                     acc = __builtin_amdgcn_mfma_f32_16x16x32_bf16(*(const LAS bf16x8*)(kp), qf[0], acc, 0, 0, 0);
;                     acc = __builtin_amdgcn_mfma_f32_16x16x32_bf16(*(const LAS bf16x8*)(kp + 32), qf[1], acc, 0, 0, 0);
; #pragma unroll
;                     for (int e = 0; e < 4; ++e) { acc[e] *= 0.125f; m = fmaxf(m, acc[e]); }
;                     sc[4 * (cc >= 0 ? cc : 0) + t4] = acc; }
;             }
;             if (sidx == NCH - 1) { m = fmaxf(m, __shfl_xor(m, 16)); m = fmaxf(m, __shfl_xor(m, 32)); }
	ds_read_b32 v240, v31 offset:38660
	ds_read_b32 v241, v31 offset:38664
	ds_read_b32 v242, v31 offset:38668
	ds_read_b32 v243, v31 offset:38672
	ds_read_b32 v244, v31 offset:38724
	ds_read_b32 v245, v31 offset:38728
	ds_read_b32 v246, v31 offset:38732
	ds_read_b32 v247, v31 offset:38736
	ds_read_b128 v[18:21], v32 offset:18432
	ds_read_b128 v[26:29], v32 offset:18496
	v_or_b32_e32 v24, 64, v34
	v_mov_b64_e32 v[22:23], s[8:9]
	v_mad_i64_i32 v[22:23], s[52:53], v24, s70, v[22:23]
	v_lshl_add_u64 v[22:23], v[22:23], 0, v[70:71]
	v_lshl_add_u64 v[22:23], v[22:23], 0, s[2:3]
	s_waitcnt lgkmcnt(1)
	v_mfma_f32_16x16x32_bf16 v[36:39], v[18:21], v[6:9], 0
	global_load_dwordx4 v[18:21], v[22:23], off offset:1024
	s_nop 0
	global_load_dwordx4 v[22:25], v[22:23], off offset:1152
	v_mov_b32_e32 v151, 0xf149f2ca
	v_mov_b32_e32 v152, 0xf149f2ca
	s_waitcnt lgkmcnt(0)
	v_mfma_f32_16x16x32_bf16 v[26:29], v[26:29], v[2:5], v[36:39]
	s_nop 2
	s_waitcnt lgkmcnt(0)
	s_nop 3
	v_fmac_f32_e32 v240, 0x3e000000, v26
	v_cndmask_b32_e64 v152, v152, v240, s[28:29]
	s_nop 2
	s_waitcnt lgkmcnt(0)
	s_nop 0
	v_fmac_f32_e32 v241, 0x3e000000, v27
	v_cndmask_b32_e64 v151, v151, v241, s[30:31]
	v_mov_b32_e32 v154, 0xf149f2ca
	v_mov_b32_e32 v155, 0xf149f2ca
	s_nop 2
	s_waitcnt lgkmcnt(0)
	v_fmac_f32_e32 v242, 0x3e000000, v28
	v_cndmask_b32_e64 v155, v155, v242, s[34:35]
	s_nop 2
	s_waitcnt lgkmcnt(0)
	v_fmac_f32_e32 v243, 0x3e000000, v29
	v_cndmask_b32_e64 v154, v154, v243, s[36:37]
	ds_read_b128 v[26:29], v33 offset:18432
	ds_read_b128 v[36:39], v33 offset:18496
	v_mov_b32_e32 v156, 0xf149f2ca
	v_mov_b32_e32 v158, 0xf149f2ca
	s_waitcnt lgkmcnt(1)
	v_mfma_f32_16x16x32_bf16 v[26:29], v[26:29], v[6:9], 0
	s_waitcnt lgkmcnt(0)
	v_mfma_f32_16x16x32_bf16 v[26:29], v[36:39], v[2:5], v[26:29]
	s_nop 2
	s_waitcnt lgkmcnt(0)
	s_nop 3
	v_fmac_f32_e32 v244, 0x3e000000, v26
	v_cndmask_b32_e64 v158, v158, v244, s[38:39]
	s_nop 2
	s_waitcnt lgkmcnt(0)
	s_nop 0
	v_fmac_f32_e32 v245, 0x3e000000, v27
	v_cndmask_b32_e64 v156, v156, v245, s[44:45]
	v_mov_b32_e32 v157, 0xf149f2ca
	v_mov_b32_e32 v160, 0xf149f2ca
	s_nop 2
	s_waitcnt lgkmcnt(0)
	v_fmac_f32_e32 v246, 0x3e000000, v28
	v_cndmask_b32_e64 v160, v160, v246, s[46:47]
	s_nop 2
	s_waitcnt lgkmcnt(0)
	v_fmac_f32_e32 v247, 0x3e000000, v29
	v_cndmask_b32_e64 v157, v157, v247, s[64:65]
	v_max3_f32 v26, v93, s73, v92
	v_max3_f32 v26, v26, v95, v94
	v_max3_f32 v26, v26, v97, v96
	v_max3_f32 v26, v26, v100, v98
	v_max3_f32 v26, v26, v101, v99
	v_max3_f32 v26, v26, v103, v102
	v_max3_f32 v26, v26, v106, v104
	v_max3_f32 v26, v26, v110, v108
	v_max3_f32 v26, v26, v107, v105
	v_max3_f32 v26, v26, v111, v109
	v_max3_f32 v26, v26, v114, v112
	v_max3_f32 v26, v26, v117, v113
	v_max3_f32 v26, v26, v116, v115
	v_max3_f32 v26, v26, v119, v118
	v_max3_f32 v26, v26, v122, v120
	v_max3_f32 v26, v26, v125, v121
	v_max3_f32 v26, v26, v124, v123
	v_max3_f32 v26, v26, v127, v126
	v_max3_f32 v26, v26, v130, v128
	v_max3_f32 v26, v26, v134, v129
	v_max3_f32 v26, v26, v132, v131
	v_max3_f32 v26, v26, v136, v135
	v_max3_f32 v26, v26, v140, v138
	v_max3_f32 v26, v26, v143, v139
	v_max3_f32 v26, v26, v142, v141
	v_max3_f32 v26, v26, v145, v144
	v_mad_u32_u24 v90, v90, s71, v30
	v_max3_f32 v26, v26, v150, v148
	s_waitcnt vmcnt(3)
	ds_write_b128 v75, v[10:13]
	s_waitcnt vmcnt(2)
	ds_write_b128 v75, v[14:17] offset:9216
	s_waitcnt lgkmcnt(0)
	s_barrier
	ds_read_b128 v[10:13], v90
	ds_read_b128 v[14:17], v90 offset:64
	v_max3_f32 v26, v26, v153, v149
	v_max3_f32 v26, v26, v152, v151
	v_max3_f32 v26, v26, v155, v154
	v_max3_f32 v26, v26, v158, v156
	v_max3_f32 v35, v26, v160, v157
	v_or_b32_e32 v26, 0x80, v34
	v_mov_b64_e32 v[44:45], s[8:9]
	v_mad_i64_i32 v[26:27], s[28:29], v26, s70, v[44:45]
	v_lshl_add_u64 v[26:27], v[26:27], 0, v[70:71]
	v_lshl_add_u64 v[30:31], v[26:27], 0, s[2:3]
	s_waitcnt lgkmcnt(1)
	v_mfma_f32_16x16x32_bf16 v[10:13], v[10:13], v[6:9], 0
	global_load_dwordx4 v[26:29], v[30:31], off offset:1024
	s_nop 0
	global_load_dwordx4 v[30:33], v[30:31], off offset:1152
	ds_read_b128 v[36:39], v90 offset:2304
	v_lshl_add_u64 v[78:79], s[4:5], 0, v[70:71]
	s_waitcnt lgkmcnt(1)
	v_mfma_f32_16x16x32_bf16 v[62:65], v[14:17], v[2:5], v[10:13]
	s_ashr_i32 s17, s16, 31
	v_mov_b32_e32 v81, v71
	v_cmp_lt_i32_e32 vcc, v84, v85
	ds_read_b128 v[10:13], v90 offset:2368
	v_add3_u32 v159, v87, v76, v88
	s_nop 2
	v_mul_f32_e32 v14, 0x3e000000, v62
	v_mul_f32_e32 v15, 0x3e000000, v63
	v_max3_f32 v35, v35, v14, v15
	v_mul_f32_e32 v40, 0x3e000000, v64
	s_waitcnt lgkmcnt(1)
	v_mfma_f32_16x16x32_bf16 v[14:17], v[36:39], v[6:9], 0
	v_mul_f32_e32 v36, 0x3e000000, v65
	v_max3_f32 v35, v35, v40, v36
	ds_read_b128 v[36:39], v90 offset:4608
	s_waitcnt lgkmcnt(1)
	v_mfma_f32_16x16x32_bf16 v[66:69], v[10:13], v[2:5], v[14:17]
	ds_read_b128 v[10:13], v90 offset:4672
	s_ashr_i32 s19, s18, 31
	s_ashr_i32 s21, s20, 31
	s_ashr_i32 s23, s22, 31
	s_ashr_i32 s25, s24, 31
	s_nop 2
	v_mul_f32_e32 v14, 0x3e000000, v66
	v_mul_f32_e32 v15, 0x3e000000, v67
	v_max3_f32 v35, v35, v14, v15
	s_waitcnt lgkmcnt(1)
	v_mfma_f32_16x16x32_bf16 v[14:17], v[36:39], v[6:9], 0
	v_mul_f32_e32 v40, 0x3e000000, v68
	v_mul_f32_e32 v41, 0x3e000000, v69
	v_max3_f32 v35, v35, v40, v41
	s_waitcnt lgkmcnt(0)
	v_mfma_f32_16x16x32_bf16 v[58:61], v[10:13], v[2:5], v[14:17]
	ds_read_b128 v[36:39], v90 offset:6912
	ds_read_b128 v[40:43], v90 offset:6976
	s_waitcnt vmcnt(3)
	ds_write_b128 v75, v[18:21] offset:18432
	s_waitcnt vmcnt(2)
	ds_write_b128 v75, v[22:25] offset:27648
	s_waitcnt lgkmcnt(0)
	s_nop 0
	v_mul_f32_e32 v10, 0x3e000000, v58
	v_mul_f32_e32 v11, 0x3e000000, v59
	v_max3_f32 v14, v35, v10, v11
	v_mfma_f32_16x16x32_bf16 v[10:13], v[36:39], v[6:9], 0
	v_mul_f32_e32 v15, 0x3e000000, v60
	v_mul_f32_e32 v16, 0x3e000000, v61
	v_max3_f32 v14, v14, v15, v16
	v_mfma_f32_16x16x32_bf16 v[54:57], v[40:43], v[2:5], v[10:13]
	s_barrier
; #define LAS __attribute__((address_space(3)))
; template <bool LOCAL>
; __device__ __forceinline__ void na_unit(const bf16* P, const bf16* VT, bf16* YCAT, const LAS float* rpb_l, LAS bf16* buf, int b, int gr, int hp, int qblk, int tid) {
;     ...
;             } else {
;                 const int cc = c - NLOC;
; #pragma unroll
;                 for (int t4 = 0; t4 < 4; ++t4) {
;                     const LAS bf16* kp = cb + (16 * t4 + fr) * 72 + 8 * fq;
;                     f32x4 acc = {0.f, 0.f, 0.f, 0.f};
;                     acc = __builtin_amdgcn_mfma_f32_16x16x32_bf16(*(const LAS bf16x8*)(kp), qf[0], acc, 0, 0, 0);
;                     acc = __builtin_amdgcn_mfma_f32_16x16x32_bf16(*(const LAS bf16x8*)(kp + 32), qf[1], acc, 0, 0, 0);
; #pragma unroll
;                     for (int e = 0; e < 4; ++e) { acc[e] *= 0.125f; m = fmaxf(m, acc[e]); }
;                     sc[4 * (cc >= 0 ? cc : 0) + t4] = acc; }
;             }
;             if (sidx == NCH - 1) { m = fmaxf(m, __shfl_xor(m, 16)); m = fmaxf(m, __shfl_xor(m, 32)); }
	v_or_b32_e32 v18, 0xc0, v34
	v_mad_i64_i32 v[18:19], s[28:29], v18, s70, v[44:45]
	v_lshl_add_u64 v[18:19], v[18:19], 0, v[70:71]
	s_nop 3
	v_mul_f32_e32 v10, 0x3e000000, v54
	v_mul_f32_e32 v11, 0x3e000000, v55
	v_max3_f32 v14, v14, v10, v11
	ds_read_b128 v[10:13], v90 offset:18432
	v_mul_f32_e32 v15, 0x3e000000, v56
	v_mul_f32_e32 v16, 0x3e000000, v57
	v_max3_f32 v35, v14, v15, v16
	ds_read_b128 v[14:17], v90 offset:18496
	v_lshl_add_u64 v[22:23], v[18:19], 0, s[2:3]
	s_waitcnt lgkmcnt(1)
	v_mfma_f32_16x16x32_bf16 v[10:13], v[10:13], v[6:9], 0
	global_load_dwordx4 v[18:21], v[22:23], off offset:1024
	global_load_dwordx4 v[162:165], v[22:23], off offset:1152
	ds_read_b128 v[22:25], v90 offset:20736
	s_ashr_i32 s27, s26, 31
	s_waitcnt lgkmcnt(1)
	v_mfma_f32_16x16x32_bf16 v[46:49], v[14:17], v[2:5], v[10:13]
	s_nop 2
	ds_read_b128 v[10:13], v90 offset:20800
	s_nop 3
	v_mul_f32_e32 v14, 0x3e000000, v46
	v_mul_f32_e32 v15, 0x3e000000, v47
	v_max3_f32 v34, v35, v14, v15
	v_mul_f32_e32 v35, 0x3e000000, v48
	s_waitcnt lgkmcnt(1)
	v_mfma_f32_16x16x32_bf16 v[14:17], v[22:25], v[6:9], 0
	v_mul_f32_e32 v22, 0x3e000000, v49
	v_max3_f32 v34, v34, v35, v22
	ds_read_b128 v[22:25], v90 offset:23040
	s_waitcnt lgkmcnt(1)
	v_mfma_f32_16x16x32_bf16 v[50:53], v[10:13], v[2:5], v[14:17]
	ds_read_b128 v[10:13], v90 offset:23104
	s_nop 6
	v_mul_f32_e32 v14, 0x3e000000, v50
	v_mul_f32_e32 v15, 0x3e000000, v51
	v_max3_f32 v34, v34, v14, v15
	s_waitcnt lgkmcnt(1)
	v_mfma_f32_16x16x32_bf16 v[14:17], v[22:25], v[6:9], 0
	v_mul_f32_e32 v35, 0x3e000000, v52
	v_mul_f32_e32 v36, 0x3e000000, v53
	v_max3_f32 v38, v34, v35, v36
	s_waitcnt lgkmcnt(0)
	v_mfma_f32_16x16x32_bf16 v[42:45], v[10:13], v[2:5], v[14:17]
	ds_read_b128 v[22:25], v90 offset:25344
	ds_read_b128 v[34:37], v90 offset:25408
	s_waitcnt vmcnt(3)
	ds_write_b128 v75, v[26:29]
	s_waitcnt vmcnt(2)
	ds_write_b128 v75, v[30:33] offset:9216
	s_waitcnt lgkmcnt(0)
	s_nop 0
	v_mul_f32_e32 v10, 0x3e000000, v42
	v_mul_f32_e32 v11, 0x3e000000, v43
	v_max3_f32 v14, v38, v10, v11
	v_mfma_f32_16x16x32_bf16 v[10:13], v[22:25], v[6:9], 0
	v_mul_f32_e32 v15, 0x3e000000, v44
	v_mul_f32_e32 v16, 0x3e000000, v45
	v_max3_f32 v14, v14, v15, v16
	v_mfma_f32_16x16x32_bf16 v[38:41], v[34:37], v[2:5], v[10:13]
	s_barrier
	v_add3_u32 v26, v89, s1, 64
	v_mul_u32_u24_e32 v26, 0x9000, v26
	v_lshl_add_u64 v[22:23], s[16:17], 1, v[78:79]
	s_nop 3
	v_mul_f32_e32 v10, 0x3e000000, v38
	v_mul_f32_e32 v11, 0x3e000000, v39
	v_max3_f32 v10, v14, v10, v11
	v_mul_f32_e32 v11, 0x3e000000, v40
	v_mul_f32_e32 v12, 0x3e000000, v41
	v_max3_f32 v34, v10, v11, v12
	v_or_b32_e32 v10, s1, v89
	v_mul_u32_u24_e32 v14, 0x9000, v10
	ds_read_b128 v[10:13], v90
	v_lshlrev_b32_e32 v70, 1, v14
	ds_read_b128 v[14:17], v90 offset:64
	v_lshlrev_b32_e32 v80, 1, v26
	v_lshl_add_u64 v[24:25], v[22:23], 0, v[70:71]
	v_lshl_add_u64 v[22:23], v[22:23], 0, v[80:81]
	s_waitcnt lgkmcnt(1)
	v_mfma_f32_16x16x32_bf16 v[10:13], v[10:13], v[6:9], 0
	global_load_dwordx4 v[166:169], v[24:25], off
	global_load_dwordx4 v[170:173], v[22:23], off
	ds_read_b128 v[22:25], v90 offset:2304
	s_add_i32 s16, s15, s50
	s_waitcnt lgkmcnt(1)
	v_mfma_f32_16x16x32_bf16 v[30:33], v[14:17], v[2:5], v[10:13]
	s_ashr_i32 s17, s16, 31
	s_ashr_i32 s15, s14, 31
	s_ashr_i32 s1, s0, 31
	ds_read_b128 v[10:13], v90 offset:2368
	s_nop 3
	v_mul_f32_e32 v14, 0x3e000000, v30
	v_mul_f32_e32 v15, 0x3e000000, v31
	v_max3_f32 v26, v34, v14, v15
	v_mul_f32_e32 v27, 0x3e000000, v32
	s_waitcnt lgkmcnt(1)
	v_mfma_f32_16x16x32_bf16 v[14:17], v[22:25], v[6:9], 0
	v_mul_f32_e32 v22, 0x3e000000, v33
	v_max3_f32 v26, v26, v27, v22
	ds_read_b128 v[22:25], v90 offset:4608
	s_waitcnt lgkmcnt(1)
	v_mfma_f32_16x16x32_bf16 v[34:37], v[10:13], v[2:5], v[14:17]
	ds_read_b128 v[10:13], v90 offset:4672
	s_nop 6
	v_mul_f32_e32 v14, 0x3e000000, v34
	v_mul_f32_e32 v15, 0x3e000000, v35
	v_max3_f32 v26, v26, v14, v15
	s_waitcnt lgkmcnt(1)
	v_mfma_f32_16x16x32_bf16 v[14:17], v[22:25], v[6:9], 0
	v_mul_f32_e32 v27, 0x3e000000, v36
	v_mul_f32_e32 v28, 0x3e000000, v37
	v_max3_f32 v89, v26, v27, v28
	s_waitcnt lgkmcnt(0)
	v_mfma_f32_16x16x32_bf16 v[26:29], v[10:13], v[2:5], v[14:17]
	ds_read_b128 v[22:25], v90 offset:6912
	ds_read_b128 v[174:177], v90 offset:6976
	s_waitcnt vmcnt(3)
	ds_write_b128 v75, v[18:21] offset:18432
	s_waitcnt vmcnt(2)
	ds_write_b128 v75, v[162:165] offset:27648
	s_waitcnt lgkmcnt(0)
	s_nop 0
	v_mul_f32_e32 v10, 0x3e000000, v26
	v_mul_f32_e32 v11, 0x3e000000, v27
	v_max3_f32 v14, v89, v10, v11
	v_mfma_f32_16x16x32_bf16 v[10:13], v[22:25], v[6:9], 0
	v_mul_f32_e32 v15, 0x3e000000, v28
	v_mul_f32_e32 v16, 0x3e000000, v29
	v_max3_f32 v14, v14, v15, v16
	v_mfma_f32_16x16x32_bf16 v[22:25], v[174:177], v[2:5], v[10:13]
	s_barrier
; #define LAS __attribute__((address_space(3)))
; __device__ __forceinline__ unsigned cvt_pk_bf16(float lo, float hi) { const float __attribute__((ext_vector_type(2))) v = {lo, hi}; return __builtin_bit_cast(unsigned, __builtin_convertvector(v, bf16x2_t)); }
; template <bool LOCAL>
; __device__ __forceinline__ void na_unit(const bf16* P, const bf16* VT, bf16* YCAT, const LAS float* rpb_l, LAS bf16* buf, int b, int gr, int hp, int qblk, int tid) {
;     ...
;                 const int cc = c - NLOC;
; #pragma unroll
;                 for (int t4 = 0; t4 < 4; ++t4) {
;                     const LAS bf16* kp = cb + (16 * t4 + fr) * 72 + 8 * fq;
;                     f32x4 acc = {0.f, 0.f, 0.f, 0.f};
;                     acc = __builtin_amdgcn_mfma_f32_16x16x32_bf16(*(const LAS bf16x8*)(kp), qf[0], acc, 0, 0, 0);
;                     acc = __builtin_amdgcn_mfma_f32_16x16x32_bf16(*(const LAS bf16x8*)(kp + 32), qf[1], acc, 0, 0, 0);
; #pragma unroll
;                     for (int e = 0; e < 4; ++e) { acc[e] *= 0.125f; m = fmaxf(m, acc[e]); }
;                     sc[4 * (cc >= 0 ? cc : 0) + t4] = acc; }
;             }
;             if (sidx == NCH - 1) { m = fmaxf(m, __shfl_xor(m, 16)); m = fmaxf(m, __shfl_xor(m, 32)); }
;         } else {
;             const int c = sidx - NCH;
;             if (LOCAL && c < 8) {
;                 float p[8];
; #pragma unroll
;                 for (int e = 0; e < 4; ++e) { p[e] = __expf(sl[2 * (c < 8 ? c : 0)][e] - m); p[4 + e] = __expf(sl[2 * (c < 8 ? c : 0) + 1][e] - m); }
; #pragma unroll
;                 for (int e = 0; e < 8; ++e) lsum += p[e];
;                 const bf16x8 pf = __builtin_bit_cast(bf16x8, (v4u){pg8::cvt_pk_bf16(p[0], p[1]), pg8::cvt_pk_bf16(p[2], p[3]), pg8::cvt_pk_bf16(p[4], p[5]), pg8::cvt_pk_bf16(p[6], p[7])});
; #pragma unroll
;                 for (int dt = 0; dt < 4; ++dt) { const LAS bf16* vp = cb + (16 * dt + fr) * 72 + kc0 + 4 * fq;
;                     o[dt] = __builtin_amdgcn_mfma_f32_16x16x32_bf16(frag44(vp, vp + 16), pf, o[dt], 0, 0, 0); }
	v_lshl_add_u64 v[18:19], s[16:17], 1, v[78:79]
	v_lshl_add_u64 v[20:21], v[18:19], 0, v[70:71]
	v_lshl_add_u64 v[18:19], v[18:19], 0, v[80:81]
	s_nop 3
	v_mul_f32_e32 v10, 0x3e000000, v22
	v_mul_f32_e32 v11, 0x3e000000, v23
	v_max3_f32 v14, v14, v10, v11
	ds_read_b128 v[10:13], v90 offset:18432
	v_mul_f32_e32 v15, 0x3e000000, v24
	v_mul_f32_e32 v16, 0x3e000000, v25
	v_max3_f32 v89, v14, v15, v16
	ds_read_b128 v[14:17], v90 offset:18496
	s_waitcnt lgkmcnt(1)
	v_mfma_f32_16x16x32_bf16 v[10:13], v[10:13], v[6:9], 0
	global_load_dwordx4 v[162:165], v[20:21], off
	global_load_dwordx4 v[174:177], v[18:19], off
	ds_read_b128 v[18:21], v90 offset:20736
	ds_read_b128 v[178:181], v90 offset:23040
	s_waitcnt lgkmcnt(2)
	v_mfma_f32_16x16x32_bf16 v[14:17], v[14:17], v[2:5], v[10:13]
	s_nop 2
	ds_read_b128 v[10:13], v90 offset:20800
	s_waitcnt lgkmcnt(2)
	v_mfma_f32_16x16x32_bf16 v[18:21], v[18:21], v[6:9], 0
	s_nop 1
	v_mul_f32_e32 v133, 0x3e000000, v14
	v_mul_f32_e32 v137, 0x3e000000, v15
	v_max3_f32 v89, v89, v133, v137
	s_waitcnt lgkmcnt(0)
	v_mfma_f32_16x16x32_bf16 v[18:21], v[10:13], v[2:5], v[18:21]
	ds_read_b128 v[10:13], v90 offset:23104
	ds_read_b128 v[182:185], v90 offset:25344
	ds_read_b128 v[186:189], v90 offset:25408
	v_mul_f32_e32 v133, 0x3e000000, v16
	v_mfma_f32_16x16x32_bf16 v[178:181], v[178:181], v[6:9], 0
	v_mul_f32_e32 v137, 0x3e000000, v17
	v_max3_f32 v89, v89, v133, v137
	s_nop 0
	v_mul_f32_e32 v133, 0x3e000000, v18
	s_waitcnt lgkmcnt(1)
	v_mfma_f32_16x16x32_bf16 v[6:9], v[182:185], v[6:9], 0
	v_mul_f32_e32 v137, 0x3e000000, v19
	v_max3_f32 v89, v89, v133, v137
	v_mul_f32_e32 v133, 0x3e000000, v20
	v_mfma_f32_16x16x32_bf16 v[10:13], v[10:13], v[2:5], v[178:181]
	v_mul_f32_e32 v137, 0x3e000000, v21
	v_max3_f32 v89, v89, v133, v137
	s_waitcnt vmcnt(3)
	ds_write_b128 v75, v[166:169]
	s_waitcnt vmcnt(2)
	ds_write_b128 v75, v[170:173] offset:9216
	s_waitcnt lgkmcnt(2)
	v_mfma_f32_16x16x32_bf16 v[2:5], v[186:189], v[2:5], v[6:9]
	v_mul_f32_e32 v90, 0x3e000000, v10
	v_mul_f32_e32 v133, 0x3e000000, v11
	v_max3_f32 v89, v89, v90, v133
	v_mul_f32_e32 v90, 0x3e000000, v12
	v_mul_f32_e32 v133, 0x3e000000, v13
	v_max3_f32 v89, v89, v90, v133
	s_nop 1
	v_mul_f32_e32 v6, 0x3e000000, v2
	v_mul_f32_e32 v7, 0x3e000000, v3
	v_max3_f32 v6, v89, v6, v7
	v_mul_f32_e32 v7, 0x3e000000, v4
	v_mul_f32_e32 v8, 0x3e000000, v5
	v_max3_f32 v6, v6, v7, v8
	v_cndmask_b32_e32 v7, v83, v84, vcc
	v_lshlrev_b32_e32 v89, 2, v7
	ds_bpermute_b32 v7, v89, v6
	v_cmp_lt_i32_e32 vcc, v86, v85
	v_lshl_add_u32 v8, v91, 1, v159
	v_lshl_add_u64 v[186:187], s[14:15], 1, v[78:79]
	v_lshl_add_u64 v[188:189], v[186:187], 0, v[70:71]
	s_waitcnt lgkmcnt(0)
	v_max_f32_e32 v7, v7, v7
	v_max_f32_e32 v6, v6, v7
	v_cndmask_b32_e32 v7, v83, v86, vcc
	v_lshlrev_b32_e32 v90, 2, v7
	ds_bpermute_b32 v7, v90, v6
	v_lshl_add_u64 v[190:191], v[186:187], 0, v[80:81]
	s_waitcnt lgkmcnt(0)
	s_barrier
	v_max_f32_e32 v7, v7, v7
	v_max_f32_e32 v137, v6, v7
	v_sub_f32_e32 v6, v93, v137
	v_mul_f32_e32 v6, 0x3fb8aa3b, v6
	v_exp_f32_e32 v133, v6
	v_sub_f32_e32 v6, v97, v137
	v_mul_f32_e32 v6, 0x3fb8aa3b, v6
	v_exp_f32_e32 v93, v6
	v_sub_f32_e32 v6, v92, v137
	v_mul_f32_e32 v6, 0x3fb8aa3b, v6
	v_exp_f32_e32 v97, v6
	v_sub_f32_e32 v6, v96, v137
	v_mul_f32_e32 v6, 0x3fb8aa3b, v6
	v_exp_f32_e32 v92, v6
	v_sub_f32_e32 v6, v95, v137
	v_mul_f32_e32 v6, 0x3fb8aa3b, v6
	v_exp_f32_e32 v96, v6
	v_sub_f32_e32 v6, v100, v137
	v_mul_f32_e32 v6, 0x3fb8aa3b, v6
	v_exp_f32_e32 v95, v6
	v_sub_f32_e32 v6, v94, v137
	v_mul_f32_e32 v6, 0x3fb8aa3b, v6
	v_exp_f32_e32 v100, v6
	v_sub_f32_e32 v6, v98, v137
	v_mul_f32_e32 v6, 0x3fb8aa3b, v6
	v_exp_f32_e32 v94, v6
	v_add_u32_e32 v7, 0x800, v8
	v_add_u32_e32 v6, 0x1000, v8
	ds_read2_b64 v[166:169], v8 offset1:4
	ds_read2_b64 v[178:181], v7 offset0:32 offset1:36
	ds_read2_b64 v[182:185], v6 offset0:64 offset1:68
	global_load_dwordx4 v[186:189], v[188:189], off
	s_nop 0
	global_load_dwordx4 v[190:193], v[190:191], off
	v_sub_f32_e32 v9, v101, v137
	v_mul_f32_e32 v9, 0x3fb8aa3b, v9
	v_add_u32_e32 v161, 0x1800, v8
	v_exp_f32_e32 v87, v9
	v_sub_f32_e32 v9, v106, v137
	ds_read2_b64 v[194:197], v161 offset0:96 offset1:100
	v_mul_f32_e32 v9, 0x3fb8aa3b, v9
	v_exp_f32_e32 v76, v9
	v_sub_f32_e32 v9, v99, v137
	v_mul_f32_e32 v9, 0x3fb8aa3b, v9
	v_exp_f32_e32 v91, v9
	v_sub_f32_e32 v9, v104, v137
	v_mul_f32_e32 v9, 0x3fb8aa3b, v9
	v_exp_f32_e32 v88, v9
	v_sub_f32_e32 v9, v103, v137
	v_mul_f32_e32 v9, 0x3fb8aa3b, v9
	v_exp_f32_e32 v99, v9
	v_sub_f32_e32 v9, v110, v137
	v_cvt_pk_bf16_f32 v170, v133, v97
	v_cvt_pk_bf16_f32 v171, v96, v100
	v_cvt_pk_bf16_f32 v172, v93, v92
	v_cvt_pk_bf16_f32 v173, v95, v94
	s_waitcnt vmcnt(3)
	ds_write_b128 v75, v[162:165] offset:18432
	s_waitcnt vmcnt(2)
	ds_write_b128 v75, v[174:177] offset:27648
	v_mul_f32_e32 v9, 0x3fb8aa3b, v9
	v_add_u32_e32 v163, 0x4800, v8
	v_add_u32_e32 v162, 0x5000, v8
	s_waitcnt lgkmcnt(5)
	v_mfma_f32_16x16x32_bf16 v[166:169], v[166:169], v[170:173], 0
	s_waitcnt lgkmcnt(0)
	s_barrier
; #define LAS __attribute__((address_space(3)))
; __device__ __forceinline__ unsigned cvt_pk_bf16(float lo, float hi) { const float __attribute__((ext_vector_type(2))) v = {lo, hi}; return __builtin_bit_cast(unsigned, __builtin_convertvector(v, bf16x2_t)); }
; template <bool LOCAL>
; __device__ __forceinline__ void na_unit(const bf16* P, const bf16* VT, bf16* YCAT, const LAS float* rpb_l, LAS bf16* buf, int b, int gr, int hp, int qblk, int tid) {
;     ...
;             const int c = sidx - NCH;
;             if (LOCAL && c < 8) {
;                 float p[8];
; #pragma unroll
;                 for (int e = 0; e < 4; ++e) { p[e] = __expf(sl[2 * (c < 8 ? c : 0)][e] - m); p[4 + e] = __expf(sl[2 * (c < 8 ? c : 0) + 1][e] - m); }
; #pragma unroll
;                 for (int e = 0; e < 8; ++e) lsum += p[e];
;                 const bf16x8 pf = __builtin_bit_cast(bf16x8, (v4u){pg8::cvt_pk_bf16(p[0], p[1]), pg8::cvt_pk_bf16(p[2], p[3]), pg8::cvt_pk_bf16(p[4], p[5]), pg8::cvt_pk_bf16(p[6], p[7])});
; #pragma unroll
;                 for (int dt = 0; dt < 4; ++dt) { const LAS bf16* vp = cb + (16 * dt + fr) * 72 + kc0 + 4 * fq;
;                     o[dt] = __builtin_amdgcn_mfma_f32_16x16x32_bf16(frag44(vp, vp + 16), pf, o[dt], 0, 0, 0); }
	v_mfma_f32_16x16x32_bf16 v[178:181], v[178:181], v[170:173], 0
	v_exp_f32_e32 v98, v9
	v_sub_f32_e32 v9, v102, v137
	ds_read2_b64 v[174:177], v163 offset1:4
	v_mfma_f32_16x16x32_bf16 v[182:185], v[182:185], v[170:173], 0
	v_mul_f32_e32 v9, 0x3fb8aa3b, v9
	v_exp_f32_e32 v101, v9
	v_sub_f32_e32 v9, v108, v137
	v_mfma_f32_16x16x32_bf16 v[170:173], v[194:197], v[170:173], 0
	ds_read2_b64 v[194:197], v162 offset0:32 offset1:36
	v_mul_f32_e32 v9, 0x3fb8aa3b, v9
	v_exp_f32_e32 v102, v9
	v_lshl_add_u64 v[164:165], s[0:1], 1, v[78:79]
	v_cvt_pk_bf16_f32 v198, v87, v91
	v_cvt_pk_bf16_f32 v199, v99, v101
	v_cvt_pk_bf16_f32 v200, v76, v88
	v_cvt_pk_bf16_f32 v201, v98, v102
	v_lshl_add_u64 v[202:203], v[164:165], 0, v[70:71]
	v_lshl_add_u64 v[204:205], v[164:165], 0, v[80:81]
	v_add_u32_e32 v164, 0x5800, v8
	s_waitcnt lgkmcnt(1)
	v_mfma_f32_16x16x32_bf16 v[166:169], v[174:177], v[198:201], v[166:169]
	v_sub_f32_e32 v9, v107, v137
	v_mul_f32_e32 v9, 0x3fb8aa3b, v9
	v_add_u32_e32 v165, 0x6000, v8
	s_waitcnt lgkmcnt(0)
	v_mfma_f32_16x16x32_bf16 v[174:177], v[194:197], v[198:201], v[178:181]
	v_exp_f32_e32 v104, v9
	v_sub_f32_e32 v9, v114, v137
	v_mul_f32_e32 v9, 0x3fb8aa3b, v9
	ds_read2_b64 v[178:181], v164 offset0:64 offset1:68
	global_load_dwordx4 v[194:197], v[202:203], off
	s_nop 0
	global_load_dwordx4 v[202:205], v[204:205], off
	s_waitcnt lgkmcnt(0)
	v_mfma_f32_16x16x32_bf16 v[178:181], v[178:181], v[198:201], v[182:185]
	s_nop 2
	ds_read2_b64 v[182:185], v165 offset0:96 offset1:100
	v_exp_f32_e32 v103, v9
	v_sub_f32_e32 v9, v105, v137
	v_mul_f32_e32 v9, 0x3fb8aa3b, v9
	v_exp_f32_e32 v106, v9
	v_sub_f32_e32 v9, v112, v137
	v_mul_f32_e32 v9, 0x3fb8aa3b, v9
	v_exp_f32_e32 v105, v9
	v_sub_f32_e32 v9, v111, v137
	v_mul_f32_e32 v9, 0x3fb8aa3b, v9
	v_exp_f32_e32 v108, v9
	v_sub_f32_e32 v9, v117, v137
	v_mul_f32_e32 v9, 0x3fb8aa3b, v9
	s_waitcnt lgkmcnt(0)
	v_mfma_f32_16x16x32_bf16 v[170:173], v[182:185], v[198:201], v[170:173]
	s_waitcnt vmcnt(3)
	ds_write_b128 v75, v[186:189]
	s_waitcnt vmcnt(2)
	ds_write_b128 v75, v[190:193] offset:9216
	s_waitcnt lgkmcnt(0)
	s_barrier
	v_exp_f32_e32 v107, v9
	v_sub_f32_e32 v9, v109, v137
	ds_read2_b64 v[182:185], v8 offset1:4
	ds_read2_b64 v[186:189], v7 offset0:32 offset1:36
	v_mul_f32_e32 v9, 0x3fb8aa3b, v9
	v_exp_f32_e32 v109, v9
	v_sub_f32_e32 v9, v113, v137
	v_mul_f32_e32 v9, 0x3fb8aa3b, v9
	v_exp_f32_e32 v110, v9
	v_lshl_add_u64 v[198:199], s[18:19], 1, v[78:79]
	v_cvt_pk_bf16_f32 v190, v104, v106
	v_cvt_pk_bf16_f32 v191, v108, v109
	v_cvt_pk_bf16_f32 v192, v103, v105
	v_cvt_pk_bf16_f32 v193, v107, v110
	v_lshl_add_u64 v[112:113], v[198:199], 0, v[70:71]
	v_lshl_add_u64 v[198:199], v[198:199], 0, v[80:81]
	s_waitcnt lgkmcnt(1)
	v_mfma_f32_16x16x32_bf16 v[166:169], v[182:185], v[190:193], v[166:169]
	ds_read2_b64 v[182:185], v6 offset0:64 offset1:68
	v_sub_f32_e32 v9, v116, v137
	v_mul_f32_e32 v9, 0x3fb8aa3b, v9
	s_waitcnt lgkmcnt(1)
	v_mfma_f32_16x16x32_bf16 v[174:177], v[186:189], v[190:193], v[174:177]
	global_load_dwordx4 v[186:189], v[112:113], off
	s_nop 0
	global_load_dwordx4 v[198:201], v[198:199], off
	v_exp_f32_e32 v112, v9
	v_sub_f32_e32 v9, v122, v137
	s_waitcnt lgkmcnt(0)
	v_mfma_f32_16x16x32_bf16 v[178:181], v[182:185], v[190:193], v[178:181]
	ds_read2_b64 v[182:185], v161 offset0:96 offset1:100
	v_mul_f32_e32 v9, 0x3fb8aa3b, v9
	v_exp_f32_e32 v111, v9
	v_sub_f32_e32 v9, v115, v137
	v_mul_f32_e32 v9, 0x3fb8aa3b, v9
	v_exp_f32_e32 v114, v9
	v_sub_f32_e32 v9, v120, v137
	v_mul_f32_e32 v9, 0x3fb8aa3b, v9
	v_exp_f32_e32 v113, v9
	v_sub_f32_e32 v9, v119, v137
	v_mul_f32_e32 v9, 0x3fb8aa3b, v9
	v_exp_f32_e32 v116, v9
	v_sub_f32_e32 v9, v125, v137
	v_mul_f32_e32 v9, 0x3fb8aa3b, v9
	s_waitcnt lgkmcnt(0)
	v_mfma_f32_16x16x32_bf16 v[170:173], v[182:185], v[190:193], v[170:173]
	s_waitcnt vmcnt(3)
	ds_write_b128 v75, v[194:197] offset:18432
	s_waitcnt vmcnt(2)
	ds_write_b128 v75, v[202:205] offset:27648
	s_waitcnt lgkmcnt(0)
	s_barrier
	v_exp_f32_e32 v115, v9
	v_sub_f32_e32 v9, v118, v137
	ds_read2_b64 v[182:185], v163 offset1:4
	v_mul_f32_e32 v9, 0x3fb8aa3b, v9
	v_exp_f32_e32 v117, v9
	v_sub_f32_e32 v9, v121, v137
	v_mul_f32_e32 v9, 0x3fb8aa3b, v9
	v_exp_f32_e32 v118, v9
	v_lshl_add_u64 v[202:203], s[20:21], 1, v[78:79]
	v_lshl_add_u64 v[204:205], v[202:203], 0, v[70:71]
	ds_read2_b64 v[190:193], v162 offset0:32 offset1:36
	v_cvt_pk_bf16_f32 v194, v112, v114
	v_cvt_pk_bf16_f32 v195, v116, v117
	v_cvt_pk_bf16_f32 v196, v111, v113
	v_cvt_pk_bf16_f32 v197, v115, v118
	v_lshl_add_u64 v[120:121], v[202:203], 0, v[80:81]
	v_sub_f32_e32 v9, v124, v137
	s_waitcnt lgkmcnt(1)
	v_mfma_f32_16x16x32_bf16 v[166:169], v[182:185], v[194:197], v[166:169]
	global_load_dwordx4 v[182:185], v[204:205], off
	s_nop 0
	global_load_dwordx4 v[202:205], v[120:121], off
	v_mul_f32_e32 v9, 0x3fb8aa3b, v9
	v_exp_f32_e32 v120, v9
	s_waitcnt lgkmcnt(0)
	v_mfma_f32_16x16x32_bf16 v[174:177], v[190:193], v[194:197], v[174:177]
	ds_read2_b64 v[190:193], v164 offset0:64 offset1:68
	v_sub_f32_e32 v9, v130, v137
	v_mul_f32_e32 v9, 0x3fb8aa3b, v9
	s_waitcnt lgkmcnt(0)
	v_mfma_f32_16x16x32_bf16 v[178:181], v[190:193], v[194:197], v[178:181]
	ds_read2_b64 v[190:193], v165 offset0:96 offset1:100
	v_exp_f32_e32 v119, v9
	v_sub_f32_e32 v9, v123, v137
	v_mul_f32_e32 v9, 0x3fb8aa3b, v9
	v_exp_f32_e32 v122, v9
	v_sub_f32_e32 v9, v128, v137
	v_mul_f32_e32 v9, 0x3fb8aa3b, v9
	v_exp_f32_e32 v121, v9
	v_sub_f32_e32 v9, v127, v137
	v_mul_f32_e32 v9, 0x3fb8aa3b, v9
	v_exp_f32_e32 v124, v9
	v_sub_f32_e32 v9, v134, v137
	v_mul_f32_e32 v9, 0x3fb8aa3b, v9
	s_waitcnt lgkmcnt(0)
	v_mfma_f32_16x16x32_bf16 v[170:173], v[190:193], v[194:197], v[170:173]
	s_waitcnt vmcnt(3)
	ds_write_b128 v75, v[186:189]
	s_waitcnt vmcnt(2)
	ds_write_b128 v75, v[198:201] offset:9216
	s_waitcnt lgkmcnt(0)
	s_barrier
; #define LAS __attribute__((address_space(3)))
; __device__ __forceinline__ unsigned cvt_pk_bf16(float lo, float hi) { const float __attribute__((ext_vector_type(2))) v = {lo, hi}; return __builtin_bit_cast(unsigned, __builtin_convertvector(v, bf16x2_t)); }
; template <bool LOCAL>
; __device__ __forceinline__ void na_unit(const bf16* P, const bf16* VT, bf16* YCAT, const LAS float* rpb_l, LAS bf16* buf, int b, int gr, int hp, int qblk, int tid) {
;     ...
;             const int c = sidx - NCH;
;             if (LOCAL && c < 8) {
;                 float p[8];
; #pragma unroll
;                 for (int e = 0; e < 4; ++e) { p[e] = __expf(sl[2 * (c < 8 ? c : 0)][e] - m); p[4 + e] = __expf(sl[2 * (c < 8 ? c : 0) + 1][e] - m); }
; #pragma unroll
;                 for (int e = 0; e < 8; ++e) lsum += p[e];
;                 const bf16x8 pf = __builtin_bit_cast(bf16x8, (v4u){pg8::cvt_pk_bf16(p[0], p[1]), pg8::cvt_pk_bf16(p[2], p[3]), pg8::cvt_pk_bf16(p[4], p[5]), pg8::cvt_pk_bf16(p[6], p[7])});
; #pragma unroll
;                 for (int dt = 0; dt < 4; ++dt) { const LAS bf16* vp = cb + (16 * dt + fr) * 72 + kc0 + 4 * fq;
;                     o[dt] = __builtin_amdgcn_mfma_f32_16x16x32_bf16(frag44(vp, vp + 16), pf, o[dt], 0, 0, 0); }
	v_exp_f32_e32 v123, v9
	v_sub_f32_e32 v9, v126, v137
	ds_read2_b64 v[186:189], v8 offset1:4
	ds_read2_b64 v[190:193], v7 offset0:32 offset1:36
	v_mul_f32_e32 v9, 0x3fb8aa3b, v9
	v_exp_f32_e32 v125, v9
	v_sub_f32_e32 v9, v129, v137
	v_mul_f32_e32 v9, 0x3fb8aa3b, v9
	v_exp_f32_e32 v126, v9
	v_lshl_add_u64 v[198:199], s[22:23], 1, v[78:79]
	v_cvt_pk_bf16_f32 v194, v120, v122
	v_cvt_pk_bf16_f32 v195, v124, v125
	v_cvt_pk_bf16_f32 v196, v119, v121
	v_cvt_pk_bf16_f32 v197, v123, v126
	v_lshl_add_u64 v[128:129], v[198:199], 0, v[70:71]
	v_lshl_add_u64 v[198:199], v[198:199], 0, v[80:81]
	s_waitcnt lgkmcnt(1)
	v_mfma_f32_16x16x32_bf16 v[166:169], v[186:189], v[194:197], v[166:169]
	ds_read2_b64 v[186:189], v6 offset0:64 offset1:68
	v_sub_f32_e32 v9, v132, v137
	v_mul_f32_e32 v9, 0x3fb8aa3b, v9
	s_waitcnt lgkmcnt(1)
	v_mfma_f32_16x16x32_bf16 v[174:177], v[190:193], v[194:197], v[174:177]
	global_load_dwordx4 v[190:193], v[128:129], off
	s_nop 0
	global_load_dwordx4 v[198:201], v[198:199], off
	v_exp_f32_e32 v128, v9
	v_sub_f32_e32 v9, v140, v137
	v_mul_f32_e32 v9, 0x3fb8aa3b, v9
	v_exp_f32_e32 v127, v9
	v_sub_f32_e32 v9, v131, v137
	v_mul_f32_e32 v9, 0x3fb8aa3b, v9
	v_exp_f32_e32 v130, v9
	v_sub_f32_e32 v9, v138, v137
	v_mul_f32_e32 v9, 0x3fb8aa3b, v9
	v_exp_f32_e32 v129, v9
	v_sub_f32_e32 v9, v136, v137
	v_mul_f32_e32 v9, 0x3fb8aa3b, v9
	v_exp_f32_e32 v132, v9
	v_sub_f32_e32 v9, v143, v137
	s_waitcnt lgkmcnt(0)
	v_mfma_f32_16x16x32_bf16 v[178:181], v[186:189], v[194:197], v[178:181]
	ds_read2_b64 v[186:189], v161 offset0:96 offset1:100
	v_mul_f32_e32 v9, 0x3fb8aa3b, v9
	s_waitcnt vmcnt(3)
	ds_write_b128 v75, v[182:185] offset:18432
	s_waitcnt vmcnt(2)
	ds_write_b128 v75, v[202:205] offset:27648
	s_waitcnt lgkmcnt(0)
	s_barrier
	v_exp_f32_e32 v131, v9
	v_sub_f32_e32 v9, v135, v137
	ds_read2_b64 v[182:185], v163 offset1:4
	v_mul_f32_e32 v9, 0x3fb8aa3b, v9
	v_exp_f32_e32 v134, v9
	v_sub_f32_e32 v9, v139, v137
	v_mul_f32_e32 v9, 0x3fb8aa3b, v9
	v_exp_f32_e32 v135, v9
	v_lshl_add_u64 v[202:203], s[24:25], 1, v[78:79]
	v_mfma_f32_16x16x32_bf16 v[170:173], v[186:189], v[194:197], v[170:173]
	v_lshl_add_u64 v[204:205], v[202:203], 0, v[70:71]
	ds_read2_b64 v[186:189], v162 offset0:32 offset1:36
	v_cvt_pk_bf16_f32 v194, v128, v130
	v_cvt_pk_bf16_f32 v195, v132, v134
	v_cvt_pk_bf16_f32 v196, v127, v129
	v_cvt_pk_bf16_f32 v197, v131, v135
	v_lshl_add_u64 v[138:139], v[202:203], 0, v[80:81]
	v_sub_f32_e32 v9, v142, v137
	s_waitcnt lgkmcnt(1)
	v_mfma_f32_16x16x32_bf16 v[166:169], v[182:185], v[194:197], v[166:169]
	global_load_dwordx4 v[182:185], v[204:205], off
	s_nop 0
	global_load_dwordx4 v[202:205], v[138:139], off
	v_mul_f32_e32 v9, 0x3fb8aa3b, v9
	v_exp_f32_e32 v138, v9
	s_waitcnt lgkmcnt(0)
	v_mfma_f32_16x16x32_bf16 v[174:177], v[186:189], v[194:197], v[174:177]
	ds_read2_b64 v[186:189], v164 offset0:64 offset1:68
	v_sub_f32_e32 v9, v150, v137
	v_mul_f32_e32 v9, 0x3fb8aa3b, v9
	s_waitcnt lgkmcnt(0)
	v_mfma_f32_16x16x32_bf16 v[178:181], v[186:189], v[194:197], v[178:181]
	ds_read2_b64 v[186:189], v165 offset0:96 offset1:100
	v_exp_f32_e32 v136, v9
	v_sub_f32_e32 v9, v141, v137
	v_mul_f32_e32 v9, 0x3fb8aa3b, v9
	v_exp_f32_e32 v140, v9
	v_sub_f32_e32 v9, v148, v137
	v_mul_f32_e32 v9, 0x3fb8aa3b, v9
	v_exp_f32_e32 v139, v9
	v_sub_f32_e32 v9, v145, v137
	v_mul_f32_e32 v9, 0x3fb8aa3b, v9
	s_waitcnt lgkmcnt(0)
	v_mfma_f32_16x16x32_bf16 v[170:173], v[186:189], v[194:197], v[170:173]
	s_waitcnt vmcnt(3)
	ds_write_b128 v75, v[190:193]
	s_waitcnt vmcnt(2)
	ds_write_b128 v75, v[198:201] offset:9216
	s_waitcnt lgkmcnt(0)
	s_barrier
	v_exp_f32_e32 v142, v9
	v_sub_f32_e32 v9, v153, v137
	ds_read2_b64 v[186:189], v8 offset1:4
	v_mul_f32_e32 v9, 0x3fb8aa3b, v9
	ds_read2_b64 v[194:197], v7 offset0:32 offset1:36
	v_exp_f32_e32 v141, v9
	v_sub_f32_e32 v9, v144, v137
	v_sub_f32_e32 v8, v149, v137
	v_mul_f32_e32 v9, 0x3fb8aa3b, v9
	v_mul_f32_e32 v8, 0x3fb8aa3b, v8
	v_exp_f32_e32 v143, v9
	v_exp_f32_e32 v144, v8
	v_cvt_pk_bf16_f32 v190, v138, v140
	v_cvt_pk_bf16_f32 v192, v136, v139
	v_cvt_pk_bf16_f32 v191, v142, v143
	v_cvt_pk_bf16_f32 v193, v141, v144
	v_lshl_add_u64 v[8:9], s[26:27], 1, v[78:79]
	v_sub_f32_e32 v148, v154, v137
	s_waitcnt lgkmcnt(1)
	v_mfma_f32_16x16x32_bf16 v[166:169], v[186:189], v[190:193], v[166:169]
	ds_read2_b64 v[186:189], v6 offset0:64 offset1:68
	v_lshl_add_u64 v[6:7], v[8:9], 0, v[70:71]
	v_lshl_add_u64 v[8:9], v[8:9], 0, v[80:81]
	s_waitcnt lgkmcnt(1)
	v_mfma_f32_16x16x32_bf16 v[174:177], v[194:197], v[190:193], v[174:177]
	global_load_dwordx4 v[194:197], v[6:7], off
	global_load_dwordx4 v[198:201], v[8:9], off
	ds_read2_b64 v[78:81], v161 offset0:96 offset1:100
	s_waitcnt vmcnt(3)
	ds_write_b128 v75, v[182:185] offset:18432
	s_waitcnt vmcnt(2)
	ds_write_b128 v75, v[202:205] offset:27648
	s_waitcnt lgkmcnt(2)
	v_mfma_f32_16x16x32_bf16 v[170:173], v[78:81], v[190:193], v[170:173]
	s_waitcnt lgkmcnt(0)
	s_barrier
; #define LAS __attribute__((address_space(3)))
; __device__ __forceinline__ unsigned cvt_pk_bf16(float lo, float hi) { const float __attribute__((ext_vector_type(2))) v = {lo, hi}; return __builtin_bit_cast(unsigned, __builtin_convertvector(v, bf16x2_t)); }
; template <bool LOCAL>
; __device__ __forceinline__ void na_unit(const bf16* P, const bf16* VT, bf16* YCAT, const LAS float* rpb_l, LAS bf16* buf, int b, int gr, int hp, int qblk, int tid) {
;     ...
;             const int c = sidx - NCH;
;             if (LOCAL && c < 8) {
;                 float p[8];
; #pragma unroll
;                 for (int e = 0; e < 4; ++e) { p[e] = __expf(sl[2 * (c < 8 ? c : 0)][e] - m); p[4 + e] = __expf(sl[2 * (c < 8 ? c : 0) + 1][e] - m); }
; #pragma unroll
;                 for (int e = 0; e < 8; ++e) lsum += p[e];
;                 const bf16x8 pf = __builtin_bit_cast(bf16x8, (v4u){pg8::cvt_pk_bf16(p[0], p[1]), pg8::cvt_pk_bf16(p[2], p[3]), pg8::cvt_pk_bf16(p[4], p[5]), pg8::cvt_pk_bf16(p[6], p[7])});
; #pragma unroll
;                 for (int dt = 0; dt < 4; ++dt) { const LAS bf16* vp = cb + (16 * dt + fr) * 72 + kc0 + 4 * fq;
;                     o[dt] = __builtin_amdgcn_mfma_f32_16x16x32_bf16(frag44(vp, vp + 16), pf, o[dt], 0, 0, 0); }
;             } else {
;                 const int cc = c - NLOC;
; #pragma unroll
;                 for (int p2 = 0; p2 < 2; ++p2) {
;                     float p[8];
; #pragma unroll
;                     for (int e = 0; e < 4; ++e) { p[e] = __expf(sc[4 * (cc >= 0 ? cc : 0) + 2 * p2][e] - m); p[4 + e] = __expf(sc[4 * (cc >= 0 ? cc : 0) + 2 * p2 + 1][e] - m); }
; #pragma unroll
;                     for (int e = 0; e < 8; ++e) lsum += p[e];
;                     const bf16x8 pf = __builtin_bit_cast(bf16x8, (v4u){pg8::cvt_pk_bf16(p[0], p[1]), pg8::cvt_pk_bf16(p[2], p[3]), pg8::cvt_pk_bf16(p[4], p[5]), pg8::cvt_pk_bf16(p[6], p[7])});
; #pragma unroll
;                     for (int dt = 0; dt < 4; ++dt) { const LAS bf16* vp = cb + (16 * dt + fr) * 72 + 32 * p2 + 4 * fq;
;                         o[dt] = __builtin_amdgcn_mfma_f32_16x16x32_bf16(frag44(vp, vp + 16), pf, o[dt], 0, 0, 0); }
	v_sub_f32_e32 v70, v152, v137
	v_sub_f32_e32 v79, v151, v137
	v_sub_f32_e32 v81, v155, v137
	ds_read2_b64 v[150:153], v163 offset1:4
	v_mul_f32_e32 v70, 0x3fb8aa3b, v70
	v_mul_f32_e32 v79, 0x3fb8aa3b, v79
	v_mul_f32_e32 v81, 0x3fb8aa3b, v81
	v_mul_f32_e32 v148, 0x3fb8aa3b, v148
	v_exp_f32_e32 v78, v70
	v_sub_f32_e32 v70, v158, v137
	v_exp_f32_e32 v80, v79
	v_sub_f32_e32 v79, v156, v137
	v_exp_f32_e32 v145, v81
	v_sub_f32_e32 v81, v160, v137
	v_exp_f32_e32 v149, v148
	v_sub_f32_e32 v148, v157, v137
	v_mul_f32_e32 v70, 0x3fb8aa3b, v70
	v_mul_f32_e32 v79, 0x3fb8aa3b, v79
	v_mul_f32_e32 v81, 0x3fb8aa3b, v81
	v_mul_f32_e32 v148, 0x3fb8aa3b, v148
	v_exp_f32_e32 v70, v70
	v_exp_f32_e32 v79, v79
	v_exp_f32_e32 v81, v81
	v_exp_f32_e32 v148, v148
	v_cvt_pk_bf16_f32 v154, v78, v80
	v_cvt_pk_bf16_f32 v155, v145, v149
	v_cvt_pk_bf16_f32 v156, v70, v79
	v_cvt_pk_bf16_f32 v157, v81, v148
	v_mfma_f32_16x16x32_bf16 v[178:181], v[186:189], v[190:193], v[178:181]
	v_fma_f32 v62, v62, s72, -v137
	v_fma_f32 v63, v63, s72, -v137
	v_fma_f32 v64, v64, s72, -v137
	s_waitcnt lgkmcnt(0)
	v_mfma_f32_16x16x32_bf16 v[166:169], v[150:153], v[154:157], v[166:169]
	ds_read2_b64 v[150:153], v162 offset0:32 offset1:36
	v_fma_f32 v65, v65, s72, -v137
	v_mul_f32_e32 v62, 0x3fb8aa3b, v62
	s_waitcnt lgkmcnt(0)
	v_mfma_f32_16x16x32_bf16 v[160:163], v[150:153], v[154:157], v[174:177]
	ds_read2_b64 v[150:153], v164 offset0:64 offset1:68
	v_mul_f32_e32 v63, 0x3fb8aa3b, v63
	v_mul_f32_e32 v64, 0x3fb8aa3b, v64
	s_waitcnt lgkmcnt(0)
	v_mfma_f32_16x16x32_bf16 v[174:177], v[150:153], v[154:157], v[178:181]
	ds_read2_b64 v[150:153], v165 offset0:96 offset1:100
	s_nop 1
	global_load_dwordx4 v[178:181], v[6:7], off offset:128
	global_load_dwordx4 v[182:185], v[8:9], off offset:128
	s_waitcnt vmcnt(3)
	ds_write_b128 v75, v[194:197]
	s_waitcnt vmcnt(2)
	ds_write_b128 v75, v[198:201] offset:9216
	s_waitcnt lgkmcnt(2)
	v_mfma_f32_16x16x32_bf16 v[152:155], v[150:153], v[154:157], v[170:173]
	s_waitcnt lgkmcnt(0)
	s_barrier
	s_nop 0
	ds_read2_b64 v[170:173], v159 offset1:4
	v_mul_f32_e32 v65, 0x3fb8aa3b, v65
	v_exp_f32_e32 v150, v62
	v_fma_f32 v62, v66, s72, -v137
	v_exp_f32_e32 v66, v63
	v_fma_f32 v63, v67, s72, -v137
	v_exp_f32_e32 v67, v64
	v_fma_f32 v64, v68, s72, -v137
	v_exp_f32_e32 v68, v65
	v_fma_f32 v65, v69, s72, -v137
	v_mul_f32_e32 v62, 0x3fb8aa3b, v62
	v_mul_f32_e32 v63, 0x3fb8aa3b, v63
	v_mul_f32_e32 v64, 0x3fb8aa3b, v64
	v_mul_f32_e32 v65, 0x3fb8aa3b, v65
	v_exp_f32_e32 v62, v62
	v_exp_f32_e32 v63, v63
	v_exp_f32_e32 v64, v64
	v_exp_f32_e32 v65, v65
	v_cvt_pk_bf16_f32 v186, v150, v66
	v_cvt_pk_bf16_f32 v187, v67, v68
	v_cvt_pk_bf16_f32 v188, v62, v63
	v_cvt_pk_bf16_f32 v189, v64, v65
	v_add_u32_e32 v151, 0x800, v159
	v_add_u32_e32 v156, 0x1000, v159
	s_waitcnt lgkmcnt(0)
	v_mfma_f32_16x16x32_bf16 v[164:167], v[170:173], v[186:189], v[166:169]
	v_add_u32_e32 v157, 0x1800, v159
	v_fma_f32 v58, v58, s72, -v137
	v_fma_f32 v54, v54, s72, -v137
	ds_read2_b64 v[168:171], v151 offset0:32 offset1:36
	s_waitcnt lgkmcnt(0)
	v_mfma_f32_16x16x32_bf16 v[160:163], v[168:171], v[186:189], v[160:163]
	ds_read2_b64 v[168:171], v156 offset0:64 offset1:68
	v_fma_f32 v59, v59, s72, -v137
	v_fma_f32 v55, v55, s72, -v137
	s_waitcnt lgkmcnt(0)
	v_mfma_f32_16x16x32_bf16 v[168:171], v[168:171], v[186:189], v[174:177]
	s_nop 2
	ds_read2_b64 v[172:175], v157 offset0:96 offset1:100
	v_fma_f32 v60, v60, s72, -v137
	v_fma_f32 v56, v56, s72, -v137
	s_waitcnt lgkmcnt(0)
	v_mfma_f32_16x16x32_bf16 v[152:155], v[172:175], v[186:189], v[152:155]
	ds_read2_b64 v[172:175], v159 offset0:8 offset1:12
	v_fma_f32 v61, v61, s72, -v137
	v_fma_f32 v57, v57, s72, -v137
	v_mul_f32_e32 v58, 0x3fb8aa3b, v58
	v_mul_f32_e32 v54, 0x3fb8aa3b, v54
	v_mul_f32_e32 v59, 0x3fb8aa3b, v59
	v_mul_f32_e32 v55, 0x3fb8aa3b, v55
	v_mul_f32_e32 v60, 0x3fb8aa3b, v60
	v_mul_f32_e32 v56, 0x3fb8aa3b, v56
	v_mul_f32_e32 v61, 0x3fb8aa3b, v61
	v_mul_f32_e32 v57, 0x3fb8aa3b, v57
	v_exp_f32_e32 v58, v58
	v_exp_f32_e32 v54, v54
	v_exp_f32_e32 v59, v59
	v_exp_f32_e32 v55, v55
	v_exp_f32_e32 v60, v60
	v_exp_f32_e32 v56, v56
	v_exp_f32_e32 v61, v61
	v_exp_f32_e32 v57, v57
	v_cvt_pk_bf16_f32 v186, v58, v59
	v_cvt_pk_bf16_f32 v188, v54, v55
	v_cvt_pk_bf16_f32 v187, v60, v61
	v_cvt_pk_bf16_f32 v189, v56, v57
	v_fma_f32 v46, v46, s72, -v137
	v_fma_f32 v47, v47, s72, -v137
	s_waitcnt lgkmcnt(0)
	v_mfma_f32_16x16x32_bf16 v[164:167], v[172:175], v[186:189], v[164:167]
	ds_read2_b64 v[172:175], v151 offset0:40 offset1:44
	v_fma_f32 v48, v48, s72, -v137
	v_mul_f32_e32 v46, 0x3fb8aa3b, v46
	s_waitcnt lgkmcnt(0)
	v_mfma_f32_16x16x32_bf16 v[160:163], v[172:175], v[186:189], v[160:163]
	ds_read2_b64 v[172:175], v156 offset0:72 offset1:76
	v_mul_f32_e32 v47, 0x3fb8aa3b, v47
	v_mul_f32_e32 v48, 0x3fb8aa3b, v48
	s_waitcnt lgkmcnt(0)
	v_mfma_f32_16x16x32_bf16 v[168:171], v[172:175], v[186:189], v[168:171]
	ds_read2_b64 v[172:175], v157 offset0:104 offset1:108
	v_exp_f32_e32 v69, v46
	v_fma_f32 v46, v50, s72, -v137
	v_exp_f32_e32 v50, v47
	v_fma_f32 v47, v51, s72, -v137
	v_exp_f32_e32 v51, v48
	v_fma_f32 v48, v52, s72, -v137
	v_add_u32_e32 v52, 0x4800, v159
	global_load_dwordx4 v[190:193], v[6:7], off offset:256
	global_load_dwordx4 v[194:197], v[8:9], off offset:256
	s_waitcnt lgkmcnt(0)
	v_mfma_f32_16x16x32_bf16 v[152:155], v[172:175], v[186:189], v[152:155]
	s_waitcnt vmcnt(3)
	ds_write_b128 v75, v[178:181] offset:18432
	s_waitcnt vmcnt(2)
	ds_write_b128 v75, v[182:185] offset:27648
	s_waitcnt lgkmcnt(0)
	s_barrier
; #define LAS __attribute__((address_space(3)))
; __device__ __forceinline__ unsigned cvt_pk_bf16(float lo, float hi) { const float __attribute__((ext_vector_type(2))) v = {lo, hi}; return __builtin_bit_cast(unsigned, __builtin_convertvector(v, bf16x2_t)); }
; template <bool LOCAL>
; __device__ __forceinline__ void na_unit(const bf16* P, const bf16* VT, bf16* YCAT, const LAS float* rpb_l, LAS bf16* buf, int b, int gr, int hp, int qblk, int tid) {
;     ...
;             } else {
;                 const int cc = c - NLOC;
; #pragma unroll
;                 for (int p2 = 0; p2 < 2; ++p2) {
;                     float p[8];
; #pragma unroll
;                     for (int e = 0; e < 4; ++e) { p[e] = __expf(sc[4 * (cc >= 0 ? cc : 0) + 2 * p2][e] - m); p[4 + e] = __expf(sc[4 * (cc >= 0 ? cc : 0) + 2 * p2 + 1][e] - m); }
; #pragma unroll
;                     for (int e = 0; e < 8; ++e) lsum += p[e];
;                     const bf16x8 pf = __builtin_bit_cast(bf16x8, (v4u){pg8::cvt_pk_bf16(p[0], p[1]), pg8::cvt_pk_bf16(p[2], p[3]), pg8::cvt_pk_bf16(p[4], p[5]), pg8::cvt_pk_bf16(p[6], p[7])});
; #pragma unroll
;                     for (int dt = 0; dt < 4; ++dt) { const LAS bf16* vp = cb + (16 * dt + fr) * 72 + 32 * p2 + 4 * fq;
;                         o[dt] = __builtin_amdgcn_mfma_f32_16x16x32_bf16(frag44(vp, vp + 16), pf, o[dt], 0, 0, 0); }
	v_fma_f32 v49, v49, s72, -v137
	ds_read2_b64 v[172:175], v52 offset1:4
	v_mul_f32_e32 v49, 0x3fb8aa3b, v49
	v_exp_f32_e32 v158, v49
	v_fma_f32 v49, v53, s72, -v137
	v_mul_f32_e32 v46, 0x3fb8aa3b, v46
	v_mul_f32_e32 v47, 0x3fb8aa3b, v47
	v_mul_f32_e32 v48, 0x3fb8aa3b, v48
	v_mul_f32_e32 v49, 0x3fb8aa3b, v49
	v_exp_f32_e32 v46, v46
	v_exp_f32_e32 v47, v47
	v_exp_f32_e32 v48, v48
	v_exp_f32_e32 v53, v49
	v_cvt_pk_bf16_f32 v176, v69, v50
	v_cvt_pk_bf16_f32 v177, v51, v158
	v_cvt_pk_bf16_f32 v178, v46, v47
	v_cvt_pk_bf16_f32 v179, v48, v53
	v_add_u32_e32 v180, 0x5000, v159
	v_add_u32_e32 v181, 0x5800, v159
	s_waitcnt lgkmcnt(0)
	v_mfma_f32_16x16x32_bf16 v[164:167], v[172:175], v[176:179], v[164:167]
	ds_read2_b64 v[172:175], v180 offset0:32 offset1:36
	v_add_u32_e32 v49, 0x6000, v159
	v_fma_f32 v38, v38, s72, -v137
	s_waitcnt lgkmcnt(0)
	v_mfma_f32_16x16x32_bf16 v[160:163], v[172:175], v[176:179], v[160:163]
	ds_read2_b64 v[172:175], v181 offset0:64 offset1:68
	v_mul_f32_e32 v38, 0x3fb8aa3b, v38
	v_fma_f32 v42, v42, s72, -v137
	s_waitcnt lgkmcnt(0)
	v_mfma_f32_16x16x32_bf16 v[168:171], v[172:175], v[176:179], v[168:171]
	ds_read2_b64 v[172:175], v49 offset0:96 offset1:100
	v_mul_f32_e32 v42, 0x3fb8aa3b, v42
	v_fma_f32 v30, v30, s72, -v137
	s_waitcnt lgkmcnt(0)
	v_mfma_f32_16x16x32_bf16 v[152:155], v[172:175], v[176:179], v[152:155]
	v_exp_f32_e32 v177, v38
	v_fma_f32 v38, v43, s72, -v137
	v_mul_f32_e32 v38, 0x3fb8aa3b, v38
	v_exp_f32_e32 v178, v38
	v_fma_f32 v38, v39, s72, -v137
	v_mul_f32_e32 v38, 0x3fb8aa3b, v38
	v_exp_f32_e32 v179, v38
	v_fma_f32 v38, v44, s72, -v137
	v_mul_f32_e32 v38, 0x3fb8aa3b, v38
	v_exp_f32_e32 v182, v38
	v_fma_f32 v38, v40, s72, -v137
	v_mul_f32_e32 v38, 0x3fb8aa3b, v38
	v_exp_f32_e32 v176, v42
	v_exp_f32_e32 v183, v38
	v_fma_f32 v38, v45, s72, -v137
	ds_read2_b64 v[42:45], v52 offset0:8 offset1:12
	v_mul_f32_e32 v38, 0x3fb8aa3b, v38
	v_exp_f32_e32 v184, v38
	v_fma_f32 v38, v41, s72, -v137
	v_mul_f32_e32 v38, 0x3fb8aa3b, v38
	v_exp_f32_e32 v185, v38
	v_cvt_pk_bf16_f32 v38, v176, v178
	v_cvt_pk_bf16_f32 v39, v182, v184
	v_cvt_pk_bf16_f32 v40, v177, v179
	v_cvt_pk_bf16_f32 v41, v183, v185
	v_mul_f32_e32 v30, 0x3fb8aa3b, v30
	v_fma_f32 v22, v22, s72, -v137
	s_waitcnt lgkmcnt(0)
	v_mfma_f32_16x16x32_bf16 v[42:45], v[42:45], v[38:41], v[164:167]
	v_mul_f32_e32 v22, 0x3fb8aa3b, v22
	v_fma_f32 v26, v26, s72, -v137
	v_mul_f32_e32 v26, 0x3fb8aa3b, v26
	ds_read2_b64 v[164:167], v180 offset0:40 offset1:44
	s_waitcnt lgkmcnt(0)
	v_mfma_f32_16x16x32_bf16 v[160:163], v[164:167], v[38:41], v[160:163]
	ds_read2_b64 v[164:167], v181 offset0:72 offset1:76
	v_fma_f32 v2, v2, s72, -v137
	v_mul_f32_e32 v2, 0x3fb8aa3b, v2
	s_waitcnt lgkmcnt(0)
	v_mfma_f32_16x16x32_bf16 v[164:167], v[164:167], v[38:41], v[168:171]
	s_nop 2
	ds_read2_b64 v[168:171], v49 offset0:104 offset1:108
	global_load_dwordx4 v[172:175], v[6:7], off offset:384
	s_nop 0
	global_load_dwordx4 v[6:9], v[8:9], off offset:384
	s_waitcnt vmcnt(3)
	ds_write_b128 v75, v[190:193]
	s_waitcnt vmcnt(2)
	ds_write_b128 v75, v[194:197] offset:9216
	s_waitcnt lgkmcnt(2)
	v_mfma_f32_16x16x32_bf16 v[38:41], v[168:171], v[38:41], v[152:155]
	v_exp_f32_e32 v168, v30
	v_fma_f32 v30, v34, s72, -v137
	v_mul_f32_e32 v30, 0x3fb8aa3b, v30
	v_exp_f32_e32 v169, v30
	v_fma_f32 v30, v31, s72, -v137
	v_mul_f32_e32 v30, 0x3fb8aa3b, v30
	v_exp_f32_e32 v170, v30
	v_fma_f32 v30, v35, s72, -v137
	v_mul_f32_e32 v30, 0x3fb8aa3b, v30
	v_exp_f32_e32 v171, v30
	v_fma_f32 v30, v32, s72, -v137
	v_mul_f32_e32 v30, 0x3fb8aa3b, v30
	v_exp_f32_e32 v186, v30
	v_fma_f32 v30, v36, s72, -v137
	v_mul_f32_e32 v30, 0x3fb8aa3b, v30
	v_exp_f32_e32 v187, v30
	v_fma_f32 v30, v33, s72, -v137
	s_waitcnt lgkmcnt(0)
	s_barrier
	v_mul_f32_e32 v34, 0x3fb8aa3b, v30
	ds_read2_b64 v[30:33], v159 offset1:4
	v_exp_f32_e32 v188, v34
	v_fma_f32 v34, v37, s72, -v137
	v_mul_f32_e32 v34, 0x3fb8aa3b, v34
	v_exp_f32_e32 v189, v34
	v_cvt_pk_bf16_f32 v34, v168, v170
	v_cvt_pk_bf16_f32 v35, v186, v188
	v_cvt_pk_bf16_f32 v36, v169, v171
	v_cvt_pk_bf16_f32 v37, v187, v189
	ds_read2_b64 v[152:155], v156 offset0:64 offset1:68
	v_fma_f32 v10, v10, s72, -v137
	s_waitcnt lgkmcnt(1)
	v_mfma_f32_16x16x32_bf16 v[30:33], v[30:33], v[34:37], v[42:45]
	v_mul_f32_e32 v10, 0x3fb8aa3b, v10
	s_nop 1
	ds_read2_b64 v[42:45], v151 offset0:32 offset1:36
	s_waitcnt lgkmcnt(0)
	v_mfma_f32_16x16x32_bf16 v[42:45], v[42:45], v[34:37], v[160:163]
	s_nop 2
	ds_read2_b64 v[160:163], v157 offset0:96 offset1:100
	v_mfma_f32_16x16x32_bf16 v[152:155], v[152:155], v[34:37], v[164:167]
	s_waitcnt lgkmcnt(0)
	v_mfma_f32_16x16x32_bf16 v[34:37], v[160:163], v[34:37], v[38:41]
	v_exp_f32_e32 v161, v22
	v_fma_f32 v22, v27, s72, -v137
	v_mul_f32_e32 v22, 0x3fb8aa3b, v22
	v_exp_f32_e32 v162, v22
	v_fma_f32 v22, v23, s72, -v137
	v_mul_f32_e32 v22, 0x3fb8aa3b, v22
	v_exp_f32_e32 v163, v22
	v_fma_f32 v22, v28, s72, -v137
	v_mul_f32_e32 v22, 0x3fb8aa3b, v22
	v_exp_f32_e32 v164, v22
	v_fma_f32 v22, v24, s72, -v137
	v_mul_f32_e32 v22, 0x3fb8aa3b, v22
	v_exp_f32_e32 v160, v26
	v_exp_f32_e32 v165, v22
	v_fma_f32 v22, v29, s72, -v137
	ds_read2_b64 v[26:29], v159 offset0:8 offset1:12
	v_mul_f32_e32 v22, 0x3fb8aa3b, v22
	v_exp_f32_e32 v159, v22
	v_fma_f32 v22, v25, s72, -v137
	v_mul_f32_e32 v22, 0x3fb8aa3b, v22
	v_exp_f32_e32 v166, v22
	v_cvt_pk_bf16_f32 v22, v160, v162
	v_cvt_pk_bf16_f32 v23, v164, v159
	v_cvt_pk_bf16_f32 v24, v161, v163
	v_cvt_pk_bf16_f32 v25, v165, v166
	ds_read2_b64 v[38:41], v156 offset0:72 offset1:76
	s_waitcnt lgkmcnt(1)
	v_mfma_f32_16x16x32_bf16 v[26:29], v[26:29], v[22:25], v[30:33]
	s_nop 2
	ds_read2_b64 v[30:33], v151 offset0:40 offset1:44
	s_waitcnt lgkmcnt(0)
	v_mfma_f32_16x16x32_bf16 v[30:33], v[30:33], v[22:25], v[42:45]
	s_nop 2
	ds_read2_b64 v[42:45], v157 offset0:104 offset1:108
	s_waitcnt vmcnt(1)
	ds_write_b128 v75, v[172:175] offset:18432
	s_waitcnt vmcnt(0)
	ds_write_b128 v75, v[6:9] offset:27648
	v_fma_f32 v6, v14, s72, -v137
	v_mul_f32_e32 v6, 0x3fb8aa3b, v6
	v_mfma_f32_16x16x32_bf16 v[38:41], v[38:41], v[22:25], v[152:155]
	s_waitcnt lgkmcnt(0)
	s_barrier
; #define LAS __attribute__((address_space(3)))
; __device__ __forceinline__ unsigned cvt_pk_bf16(float lo, float hi) { const float __attribute__((ext_vector_type(2))) v = {lo, hi}; return __builtin_bit_cast(unsigned, __builtin_convertvector(v, bf16x2_t)); }
; #define NA_STORE(sidx) do { LAS bf16* d_ = buf + ((sidx) & 1) * 9216; _Pragma("unroll") for (int q_ = 0; q_ < 2; ++q_) *(LAS v4u*)(d_ + q_ * 4608 + lrow * 72 + lseg * 8) = ld[(sidx) & 1][q_]; } while (0)
; template <bool LOCAL>
; __device__ __forceinline__ void na_unit(const bf16* P, const bf16* VT, bf16* YCAT, const LAS float* rpb_l, LAS bf16* buf, int b, int gr, int hp, int qblk, int tid) {
;     ...
;             } else {
;                 const int cc = c - NLOC;
; #pragma unroll
;                 for (int p2 = 0; p2 < 2; ++p2) {
;                     float p[8];
; #pragma unroll
;                     for (int e = 0; e < 4; ++e) { p[e] = __expf(sc[4 * (cc >= 0 ? cc : 0) + 2 * p2][e] - m); p[4 + e] = __expf(sc[4 * (cc >= 0 ? cc : 0) + 2 * p2 + 1][e] - m); }
; #pragma unroll
;                     for (int e = 0; e < 8; ++e) lsum += p[e];
;                     const bf16x8 pf = __builtin_bit_cast(bf16x8, (v4u){pg8::cvt_pk_bf16(p[0], p[1]), pg8::cvt_pk_bf16(p[2], p[3]), pg8::cvt_pk_bf16(p[4], p[5]), pg8::cvt_pk_bf16(p[6], p[7])});
; #pragma unroll
;                     for (int dt = 0; dt < 4; ++dt) { const LAS bf16* vp = cb + (16 * dt + fr) * 72 + 32 * p2 + 4 * fq;
;                         o[dt] = __builtin_amdgcn_mfma_f32_16x16x32_bf16(frag44(vp, vp + 16), pf, o[dt], 0, 0, 0); }
;                 }
;             }
;         }
;         if (sidx + 1 < 2 * NCH) NA_STORE(sidx + 1);
;         __syncthreads();
;     }
;     ...
;     lsum += __shfl_xor(lsum, 16); lsum += __shfl_xor(lsum, 32);
;     const float inv = 1.f / lsum;
	v_mfma_f32_16x16x32_bf16 v[22:25], v[42:45], v[22:25], v[34:37]
	v_ashrrev_i32_e32 v75, 31, v74
	s_nop 1
	v_exp_f32_e32 v34, v6
	v_fma_f32 v6, v18, s72, -v137
	v_mul_f32_e32 v6, 0x3fb8aa3b, v6
	v_exp_f32_e32 v35, v6
	v_fma_f32 v6, v15, s72, -v137
	v_mul_f32_e32 v6, 0x3fb8aa3b, v6
	v_exp_f32_e32 v36, v6
	v_fma_f32 v6, v19, s72, -v137
	v_mul_f32_e32 v6, 0x3fb8aa3b, v6
	v_exp_f32_e32 v37, v6
	v_fma_f32 v6, v16, s72, -v137
	v_mul_f32_e32 v6, 0x3fb8aa3b, v6
	v_exp_f32_e32 v42, v6
	v_fma_f32 v6, v20, s72, -v137
	v_mul_f32_e32 v6, 0x3fb8aa3b, v6
	v_exp_f32_e32 v43, v6
	v_fma_f32 v6, v17, s72, -v137
	v_mul_f32_e32 v14, 0x3fb8aa3b, v6
	ds_read2_b64 v[6:9], v52 offset1:4
	v_exp_f32_e32 v44, v14
	v_fma_f32 v14, v21, s72, -v137
	v_mul_f32_e32 v14, 0x3fb8aa3b, v14
	v_exp_f32_e32 v45, v14
	v_cvt_pk_bf16_f32 v14, v34, v36
	v_cvt_pk_bf16_f32 v15, v42, v44
	v_cvt_pk_bf16_f32 v16, v35, v37
	v_cvt_pk_bf16_f32 v17, v43, v45
	ds_read2_b64 v[18:21], v180 offset0:32 offset1:36
	s_waitcnt lgkmcnt(1)
	v_mfma_f32_16x16x32_bf16 v[6:9], v[6:9], v[14:17], v[26:29]
	s_nop 2
	ds_read2_b64 v[26:29], v181 offset0:64 offset1:68
	s_waitcnt lgkmcnt(0)
	v_mfma_f32_16x16x32_bf16 v[26:29], v[26:29], v[14:17], v[38:41]
	s_nop 2
	v_add_f32_e32 v38, 0, v133
	v_add_f32_e32 v38, v97, v38
	v_add_f32_e32 v38, v96, v38
	v_add_f32_e32 v38, v100, v38
	v_add_f32_e32 v38, v93, v38
	v_add_f32_e32 v38, v92, v38
	v_add_f32_e32 v38, v95, v38
	v_add_f32_e32 v38, v94, v38
	v_add_f32_e32 v38, v87, v38
	v_add_f32_e32 v38, v91, v38
	v_add_f32_e32 v38, v99, v38
	v_add_f32_e32 v38, v101, v38
	v_add_f32_e32 v38, v76, v38
	v_add_f32_e32 v38, v88, v38
	v_add_f32_e32 v38, v98, v38
	v_add_f32_e32 v38, v102, v38
	v_add_f32_e32 v38, v104, v38
	v_add_f32_e32 v38, v106, v38
	v_add_f32_e32 v38, v108, v38
	v_add_f32_e32 v38, v109, v38
	v_add_f32_e32 v38, v103, v38
	v_add_f32_e32 v38, v105, v38
	v_add_f32_e32 v38, v107, v38
	v_add_f32_e32 v38, v110, v38
	v_add_f32_e32 v38, v112, v38
	v_add_f32_e32 v38, v114, v38
	v_add_f32_e32 v38, v116, v38
	v_add_f32_e32 v38, v117, v38
	v_add_f32_e32 v38, v111, v38
	v_add_f32_e32 v38, v113, v38
	v_add_f32_e32 v38, v115, v38
	v_add_f32_e32 v38, v118, v38
	v_add_f32_e32 v38, v120, v38
	v_add_f32_e32 v38, v122, v38
	v_add_f32_e32 v38, v124, v38
	v_add_f32_e32 v38, v125, v38
	v_add_f32_e32 v38, v119, v38
	v_add_f32_e32 v38, v121, v38
	v_add_f32_e32 v38, v123, v38
	v_add_f32_e32 v38, v126, v38
	v_add_f32_e32 v38, v128, v38
	v_add_f32_e32 v38, v130, v38
	v_add_f32_e32 v38, v132, v38
	v_add_f32_e32 v38, v134, v38
	v_add_f32_e32 v38, v127, v38
	v_add_f32_e32 v38, v129, v38
	v_add_f32_e32 v38, v131, v38
	v_add_f32_e32 v38, v135, v38
	v_add_f32_e32 v38, v138, v38
	v_add_f32_e32 v38, v140, v38
	v_add_f32_e32 v38, v142, v38
	v_add_f32_e32 v38, v143, v38
	v_add_f32_e32 v38, v136, v38
	v_add_f32_e32 v38, v139, v38
	v_add_f32_e32 v38, v141, v38
	v_add_f32_e32 v38, v144, v38
	v_add_f32_e32 v38, v78, v38
	v_add_f32_e32 v38, v80, v38
	v_add_f32_e32 v38, v145, v38
	v_add_f32_e32 v38, v149, v38
	v_add_f32_e32 v38, v70, v38
	v_add_f32_e32 v38, v79, v38
	v_add_f32_e32 v38, v81, v38
	v_add_f32_e32 v38, v148, v38
	v_add_f32_e32 v38, v150, v38
	v_add_f32_e32 v38, v66, v38
	v_add_f32_e32 v38, v67, v38
	v_add_f32_e32 v38, v68, v38
	v_add_f32_e32 v38, v62, v38
	v_add_f32_e32 v38, v63, v38
	v_add_f32_e32 v38, v64, v38
	v_add_f32_e32 v38, v65, v38
	v_add_f32_e32 v38, v58, v38
	v_add_f32_e32 v38, v59, v38
	v_add_f32_e32 v38, v60, v38
	v_add_f32_e32 v38, v61, v38
	v_add_f32_e32 v38, v54, v38
	v_add_f32_e32 v38, v55, v38
	v_add_f32_e32 v38, v56, v38
	v_add_f32_e32 v38, v57, v38
	v_add_f32_e32 v38, v69, v38
	v_add_f32_e32 v38, v50, v38
	v_add_f32_e32 v38, v51, v38
	v_add_f32_e32 v38, v158, v38
	v_add_f32_e32 v38, v46, v38
	v_add_f32_e32 v38, v47, v38
	v_add_f32_e32 v38, v48, v38
	v_add_f32_e32 v38, v53, v38
	v_add_f32_e32 v38, v176, v38
	v_mfma_f32_16x16x32_bf16 v[18:21], v[18:21], v[14:17], v[30:33]
	v_add_f32_e32 v38, v178, v38
	v_add_f32_e32 v38, v182, v38
	v_add_f32_e32 v38, v184, v38
	ds_read2_b64 v[30:33], v49 offset0:96 offset1:100
	v_add_f32_e32 v38, v177, v38
	v_add_f32_e32 v38, v179, v38
	v_add_f32_e32 v38, v183, v38
	v_add_f32_e32 v38, v185, v38
	v_add_f32_e32 v38, v168, v38
	v_add_f32_e32 v38, v170, v38
	s_waitcnt lgkmcnt(0)
	v_mfma_f32_16x16x32_bf16 v[14:17], v[30:33], v[14:17], v[22:25]
	v_add_f32_e32 v38, v186, v38
	s_nop 1
	v_exp_f32_e32 v23, v2
	v_fma_f32 v2, v11, s72, -v137
	v_mul_f32_e32 v2, 0x3fb8aa3b, v2
	v_add_f32_e32 v38, v188, v38
	v_exp_f32_e32 v24, v2
	v_fma_f32 v2, v3, s72, -v137
	v_add_f32_e32 v38, v169, v38
	v_mul_f32_e32 v2, 0x3fb8aa3b, v2
	v_add_f32_e32 v38, v171, v38
	v_exp_f32_e32 v25, v2
	v_fma_f32 v2, v12, s72, -v137
	v_add_f32_e32 v38, v187, v38
	v_mul_f32_e32 v2, 0x3fb8aa3b, v2
	v_add_f32_e32 v38, v189, v38
	v_exp_f32_e32 v30, v2
	v_fma_f32 v2, v4, s72, -v137
	v_add_f32_e32 v38, v160, v38
	v_mul_f32_e32 v2, 0x3fb8aa3b, v2
	v_add_f32_e32 v38, v162, v38
	v_exp_f32_e32 v22, v10
	v_exp_f32_e32 v31, v2
	v_fma_f32 v2, v13, s72, -v137
	ds_read2_b64 v[10:13], v52 offset0:8 offset1:12
	v_add_f32_e32 v38, v164, v38
	v_mul_f32_e32 v2, 0x3fb8aa3b, v2
	v_add_f32_e32 v38, v159, v38
	v_exp_f32_e32 v32, v2
	v_fma_f32 v2, v5, s72, -v137
	v_add_f32_e32 v38, v161, v38
	v_mul_f32_e32 v2, 0x3fb8aa3b, v2
	v_add_f32_e32 v38, v163, v38
	v_exp_f32_e32 v33, v2
	v_add_f32_e32 v38, v165, v38
	v_add_f32_e32 v38, v166, v38
	v_add_f32_e32 v34, v34, v38
	v_add_f32_e32 v34, v36, v34
	v_cvt_pk_bf16_f32 v2, v22, v24
	v_cvt_pk_bf16_f32 v3, v30, v32
	v_cvt_pk_bf16_f32 v4, v23, v25
	v_cvt_pk_bf16_f32 v5, v31, v33
	v_add_f32_e32 v34, v42, v34
	v_add_f32_e32 v34, v44, v34
	s_waitcnt lgkmcnt(0)
	v_mfma_f32_16x16x32_bf16 v[6:9], v[10:13], v[2:5], v[6:9]
	ds_read2_b64 v[10:13], v180 offset0:40 offset1:44
	v_add_f32_e32 v34, v35, v34
	v_add_f32_e32 v34, v37, v34
	v_add_f32_e32 v34, v43, v34
	v_add_f32_e32 v34, v45, v34
	v_add_f32_e32 v22, v22, v34
	v_add_f32_e32 v22, v24, v22
	v_add_f32_e32 v22, v30, v22
	v_add_f32_e32 v22, v32, v22
	s_waitcnt lgkmcnt(0)
	v_mfma_f32_16x16x32_bf16 v[10:13], v[10:13], v[2:5], v[18:21]
	v_add_f32_e32 v22, v23, v22
	v_add_f32_e32 v22, v25, v22
	v_add_f32_e32 v22, v31, v22
	ds_read2_b64 v[18:21], v181 offset0:72 offset1:76
	v_add_f32_e32 v30, v33, v22
	ds_bpermute_b32 v31, v89, v30
	ds_read2_b64 v[22:25], v49 offset0:104 offset1:108
	s_waitcnt lgkmcnt(2)
	v_mfma_f32_16x16x32_bf16 v[18:21], v[18:21], v[2:5], v[26:29]
	s_waitcnt lgkmcnt(1)
	s_nop 1
	v_add_f32_e32 v26, v30, v31
	ds_bpermute_b32 v27, v90, v26
	v_lshlrev_b32_e32 v70, 1, v77
	s_waitcnt lgkmcnt(1)
	v_mfma_f32_16x16x32_bf16 v[14:17], v[22:25], v[2:5], v[14:17]
	s_waitcnt lgkmcnt(0)
	s_barrier
; __device__ __forceinline__ unsigned cvt_pk_bf16(float lo, float hi) { const float __attribute__((ext_vector_type(2))) v = {lo, hi}; return __builtin_bit_cast(unsigned, __builtin_convertvector(v, bf16x2_t)); }
; template <bool LOCAL>
; __device__ __forceinline__ void na_unit(const bf16* P, const bf16* VT, bf16* YCAT, const LAS float* rpb_l, LAS bf16* buf, int b, int gr, int hp, int qblk, int tid) {
;     ...
;     lsum += __shfl_xor(lsum, 16); lsum += __shfl_xor(lsum, 32);
;     const float inv = 1.f / lsum;
;     bf16* op = YCAT + (size_t)(qrow0 + fr) * D + 512 + h * 64 + 4 * fq;
; #pragma unroll
;     for (int dt = 0; dt < 4; ++dt) { v2u w; w.x = pg8::cvt_pk_bf16(o[dt][0] * inv, o[dt][1] * inv); w.y = pg8::cvt_pk_bf16(o[dt][2] * inv, o[dt][3] * inv); *(v2u*)(op + dt * 16) = w; }
	v_add_f32_e32 v2, v26, v27
	v_div_scale_f32 v3, s[0:1], v2, v2, 1.0
	v_rcp_f32_e32 v4, v3
	s_nop 0
	v_fma_f32 v5, -v3, v4, 1.0
	v_fmac_f32_e32 v4, v5, v4
	v_div_scale_f32 v5, vcc, 1.0, v2, 1.0
	v_mul_f32_e32 v22, v5, v4
	v_fma_f32 v23, -v3, v22, v5
	v_fmac_f32_e32 v22, v23, v4
	v_fma_f32 v3, -v3, v22, v5
	v_div_fmas_f32 v3, v3, v4, v22
	v_div_fixup_f32 v22, v3, v2, 1.0
	v_lshlrev_b64 v[2:3], 11, v[74:75]
	v_lshl_add_u64 v[2:3], s[10:11], 0, v[2:3]
	v_lshl_add_u64 v[2:3], v[72:73], 1, v[2:3]
	v_pk_mul_f32 v[6:7], v[6:7], v[22:23] op_sel_hi:[1,0]
	v_pk_mul_f32 v[8:9], v[8:9], v[22:23] op_sel_hi:[1,0]
	v_lshl_add_u64 v[4:5], v[2:3], 0, v[70:71]
	v_cvt_pk_bf16_f32 v6, v6, v7
	v_cvt_pk_bf16_f32 v7, v8, v9
	global_store_dwordx2 v[4:5], v[6:7], off offset:1024
	v_pk_mul_f32 v[6:7], v[10:11], v[22:23] op_sel_hi:[1,0]
	v_pk_mul_f32 v[8:9], v[12:13], v[22:23] op_sel_hi:[1,0]
	v_cvt_pk_bf16_f32 v6, v6, v7
	v_cvt_pk_bf16_f32 v7, v8, v9
	global_store_dwordx2 v[4:5], v[6:7], off offset:1056
	v_pk_mul_f32 v[6:7], v[18:19], v[22:23] op_sel_hi:[1,0]
	v_pk_mul_f32 v[8:9], v[20:21], v[22:23] op_sel_hi:[1,0]
	v_cvt_pk_bf16_f32 v6, v6, v7
	v_cvt_pk_bf16_f32 v7, v8, v9
	v_lshl_add_u64 v[2:3], v[4:5], 0, s[12:13]
	global_store_dwordx2 v[4:5], v[6:7], off offset:1088
	v_pk_mul_f32 v[4:5], v[14:15], v[22:23] op_sel_hi:[1,0]
	v_pk_mul_f32 v[6:7], v[16:17], v[22:23] op_sel_hi:[1,0]
	v_cvt_pk_bf16_f32 v4, v4, v5

; #define LAS __attribute__((address_space(3)))
; template <bool LOCAL>
; __device__ __forceinline__ void na_unit(const bf16* P, const bf16* VT, bf16* YCAT, const LAS float* rpb_l, LAS bf16* buf, int b, int gr, int hp, int qblk, int tid) {
;     ...
;     const int qrow0 = LOCAL ? NCTX + b * SEQ + gr * 64 + 16 * qb : b * CTXL + qblk * 64 + 16 * qb;
;     const int r0 = min(max(gr - 4, 0), 24);
;     const int kc0 = qb == 0 ? 0 : qb == 1 ? 8 : qb == 2 ? 24 : 32;
;     const int qcol = 16 * qb + fr, cs = min(max(qcol - 8, 0), 48);
;     const LAS float* rpb = rpb_l + h * 15 * 31;
;     v4u ld[2][2];
;     const int lrow = (tid >> 3) & 63, lseg = tid & 7;
;     ...
;     bf16x8 qf[2];
; #pragma unroll
;     for (int ks = 0; ks < 2; ++ks) qf[ks] = *(const bf16x8*)(P + (size_t)(qrow0 + fr) * DINP + h * 64 + 32 * ks + 8 * fq);
;     f32x4 sl[16], sc[16];
;     float m = -1.0e30f, lsum = 0.f;
;     f32x4 o[4];
; #pragma unroll
;     for (int dt = 0; dt < 4; ++dt) o[dt] = (f32x4){0.f, 0.f, 0.f, 0.f};
;     NA_ISSUE(0); NA_ISSUE(1); NA_STORE(0);
;     __syncthreads();
; #pragma unroll
;     for (int sidx = 0; sidx < 2 * NCH; ++sidx) {
;         if (sidx + 2 < 2 * NCH) NA_ISSUE(sidx + 2);
;         const LAS bf16* cb = buf + (sidx & 1) * 9216 + hh * 4608;
;         if (sidx < NCH) {
;             const int c = sidx;
;             if (LOCAL && c < 8) {
; #pragma unroll
;                 for (int t2 = 0; t2 < 2; ++t2) {
;                     const LAS bf16* kp = cb + (kc0 + 16 * t2 + fr) * 72 + 8 * fq;
;                     f32x4 acc = {0.f, 0.f, 0.f, 0.f};
;                     acc = __builtin_amdgcn_mfma_f32_16x16x32_bf16(*(const LAS bf16x8*)(kp), qf[0], acc, 0, 0, 0);
;                     acc = __builtin_amdgcn_mfma_f32_16x16x32_bf16(*(const LAS bf16x8*)(kp + 32), qf[1], acc, 0, 0, 0);
;                     const LAS float* rb = rpb + (r0 + c - gr + 7) * 31 + 15 - qcol;
; #pragma unroll
;                     for (int e = 0; e < 4; ++e) { const int kcol = kc0 + 16 * t2 + 4 * fq + e; const bool ok = (kcol >= cs) && (kcol < cs + 16);
;                         const float sv = ok ? acc[e] * 0.125f + rb[ok ? kcol : qcol] : -1.0e30f; acc[e] = sv; m = fmaxf(m, sv); }
;                     sl[2 * (c < 8 ? c : 0) + t2] = acc; }
.LBB0_645:
	s_or_b64 exec, exec, s[0:1]
	s_bfe_u32 s19, s76, 0x50002
	v_sub_u32_e64 v3, s19, 4 clamp
	s_ashr_i32 s17, s76, 7
	v_readfirstlane_b32 s0, v3
	s_lshl_b32 s26, s17, 11
	s_min_u32 s20, s0, 24
	s_add_i32 s14, s26, 0x1000
	s_lshl_b32 s15, s20, 6
	s_or_b32 s16, s15, s14
	v_mov_b64_e32 v[18:19], s[8:9]
	v_and_b32_e32 v32, 7, v93
	v_or_b32_e32 v3, s16, v88
	s_and_b32 s18, s76, 3
	v_mad_i64_i32 v[4:5], s[0:1], v3, s70, v[18:19]
	v_lshlrev_b32_e32 v26, 4, v32
	v_mov_b32_e32 v27, v71
	v_lshl_add_u64 v[4:5], v[4:5], 0, v[26:27]
	s_lshl_b32 s2, s18, 8
	v_lshl_add_u64 v[4:5], v[4:5], 0, s[2:3]
	global_load_dwordx4 v[10:13], v[4:5], off offset:1024
	global_load_dwordx4 v[14:17], v[4:5], off offset:1152
	s_lshl_b32 s0, s19, 6
	v_lshl_or_b32 v31, v2, 4, v89
	v_lshl_add_u32 v33, s18, 1, v92
	s_or_b32 s0, s14, s0
	v_mad_u32_u24 v2, v88, s71, 0
	v_lshlrev_b32_e32 v72, 6, v33
	s_add_i32 s50, s26, 0x1040
	v_or_b32_e32 v74, s0, v31
	v_add_u32_e32 v75, v2, v26
	v_ashrrev_i32_e32 v73, 31, v72
	v_or_b32_e32 v4, s50, v88
	v_mad_i64_i32 v[2:3], s[0:1], v74, s70, v[18:19]
	v_add_u32_e32 v4, s15, v4
	v_lshl_add_u64 v[2:3], v[72:73], 1, v[2:3]
	v_mad_i64_i32 v[4:5], s[0:1], v4, s70, v[18:19]
	v_lshl_add_u64 v[2:3], v[2:3], 0, v[70:71]
	v_lshl_add_u64 v[20:21], v[4:5], 0, v[26:27]
	global_load_dwordx4 v[6:9], v[2:3], off
	s_nop 0
	global_load_dwordx4 v[2:5], v[2:3], off offset:64
	s_or_b32 s14, s26, s15
	s_addk_i32 s14, 0x1080
	v_or_b32_e32 v24, s14, v88
	v_mad_i64_i32 v[28:29], s[0:1], v24, s70, v[18:19]
	v_lshl_add_u64 v[26:27], v[28:29], 0, v[26:27]
	v_lshl_add_u64 v[22:23], v[20:21], 0, s[2:3]
	v_lshl_add_u64 v[26:27], v[26:27], 0, s[2:3]
	global_load_dwordx4 v[18:21], v[22:23], off offset:1024
	s_nop 0
	global_load_dwordx4 v[22:25], v[22:23], off offset:1152
	v_add_u32_e32 v30, v86, v70
	v_add_u32_e32 v34, v90, v89
	v_mad_u32_u24 v36, v34, s71, v30
	s_movk_i32 s0, 0x744
	v_mul_lo_u32 v33, v33, s0
	s_sub_i32 s0, s20, s19
	s_mulk_i32 s0, 0x7c
	v_sub_u32_e64 v35, v31, 8 clamp
	s_add_i32 s0, s0, 0
	v_min_u32_e32 v35, 48, v35
	v_lshlrev_b32_e32 v77, 2, v91
	v_add_u32_e32 v33, s0, v33
	v_lshlrev_b32_e32 v31, 2, v31
	v_sub_u32_e32 v31, v33, v31
	v_add_u32_e32 v33, v90, v77
	v_cmp_ge_u32_e32 vcc, v33, v35
	v_mov_b32_e32 v91, 0xf149f2ca
	v_lshl_add_u32 v31, v33, 2, v31
	v_mov_b32_e32 v92, 0xf149f2ca
	s_waitcnt vmcnt(5)
	ds_write_b128 v75, v[10:13]
	s_waitcnt vmcnt(4)
	ds_write_b128 v75, v[14:17] offset:9216
	s_waitcnt lgkmcnt(0)
	s_barrier
	ds_read_b32 v240, v31 offset:37792
	ds_read_b32 v241, v31 offset:37796
	ds_read_b32 v242, v31 offset:37800
	ds_read_b32 v243, v31 offset:37804
	ds_read_b32 v244, v31 offset:37856
	ds_read_b32 v245, v31 offset:37860
	ds_read_b32 v246, v31 offset:37864
	ds_read_b32 v247, v31 offset:37868
	global_load_dwordx4 v[10:13], v[26:27], off offset:1024
	global_load_dwordx4 v[14:17], v[26:27], off offset:1152
	ds_read_b128 v[26:29], v36
	ds_read_b128 v[38:41], v36 offset:64
	s_waitcnt vmcnt(5) lgkmcnt(1)
	v_mfma_f32_16x16x32_bf16 v[26:29], v[26:29], v[6:9], 0
	v_add_u32_e32 v36, 16, v35
	v_cmp_lt_u32_e64 s[0:1], v33, v36
	s_and_b64 s[28:29], vcc, s[0:1]
	s_waitcnt vmcnt(4) lgkmcnt(0)
	v_mfma_f32_16x16x32_bf16 v[26:29], v[38:41], v[2:5], v[26:29]
	s_nop 2
	s_waitcnt lgkmcnt(0)
	s_nop 3
	v_fmac_f32_e32 v240, 0x3e000000, v26
	v_cndmask_b32_e64 v92, v92, v240, s[28:29]
	s_nop 4
	v_or_b32_e32 v26, 1, v33
	v_cmp_ge_u32_e32 vcc, v26, v35
	v_cmp_lt_u32_e64 s[0:1], v26, v36
	s_and_b64 s[30:31], vcc, s[0:1]
	s_nop 2
	s_waitcnt lgkmcnt(0)
	v_fmac_f32_e32 v241, 0x3e000000, v27
	v_cndmask_b32_e64 v91, v91, v241, s[30:31]
	v_or_b32_e32 v26, 2, v33
	v_cmp_ge_u32_e32 vcc, v26, v35
	v_cmp_lt_u32_e64 s[0:1], v26, v36
	s_and_b64 s[34:35], vcc, s[0:1]
	v_mov_b32_e32 v93, 0xf149f2ca
	v_mov_b32_e32 v94, 0xf149f2ca
	s_nop 2
	s_waitcnt lgkmcnt(0)
	v_fmac_f32_e32 v242, 0x3e000000, v28
	v_cndmask_b32_e64 v94, v94, v242, s[34:35]
	v_or_b32_e32 v26, 3, v33
	v_cmp_ge_u32_e32 vcc, v26, v35
	v_cmp_lt_u32_e64 s[0:1], v26, v36
	s_and_b64 s[36:37], vcc, s[0:1]
	s_nop 2
	s_waitcnt lgkmcnt(0)
	v_fmac_f32_e32 v243, 0x3e000000, v29
	v_cndmask_b32_e64 v93, v93, v243, s[36:37]
	v_add_u32_e32 v37, 16, v90
	v_add_u32_e32 v33, v37, v89
	v_mad_u32_u24 v38, v33, s71, v30
	ds_read_b128 v[26:29], v38
	ds_read_b128 v[38:41], v38 offset:64
	v_add_u32_e32 v37, v37, v77
	v_cmp_ge_u32_e32 vcc, v37, v35
	v_cmp_lt_u32_e64 s[0:1], v37, v36
	s_waitcnt lgkmcnt(1)
	v_mfma_f32_16x16x32_bf16 v[26:29], v[26:29], v[6:9], 0
	s_and_b64 s[38:39], vcc, s[0:1]
	v_mov_b32_e32 v95, 0xf149f2ca
	v_mov_b32_e32 v96, 0xf149f2ca
	s_waitcnt lgkmcnt(0)
	v_mfma_f32_16x16x32_bf16 v[26:29], v[38:41], v[2:5], v[26:29]
	s_nop 2
	s_waitcnt lgkmcnt(0)
	s_nop 3
	v_fmac_f32_e32 v244, 0x3e000000, v26
	v_cndmask_b32_e64 v96, v96, v244, s[38:39]
	s_nop 4
	v_or_b32_e32 v26, 1, v37
	v_cmp_ge_u32_e32 vcc, v26, v35
	v_cmp_lt_u32_e64 s[0:1], v26, v36
	s_and_b64 s[44:45], vcc, s[0:1]
	s_nop 2
	s_waitcnt lgkmcnt(0)
	v_fmac_f32_e32 v245, 0x3e000000, v27
	v_cndmask_b32_e64 v95, v95, v245, s[44:45]
	v_or_b32_e32 v26, 2, v37
	v_cmp_ge_u32_e32 vcc, v26, v35
	v_cmp_lt_u32_e64 s[0:1], v26, v36
	s_and_b64 s[46:47], vcc, s[0:1]
	v_mov_b32_e32 v97, 0xf149f2ca
	v_mov_b32_e32 v99, 0xf149f2ca
	s_nop 2
	s_waitcnt lgkmcnt(0)
	v_fmac_f32_e32 v246, 0x3e000000, v28
	v_cndmask_b32_e64 v99, v99, v246, s[46:47]
	v_or_b32_e32 v26, 3, v37
	v_cmp_ge_u32_e32 vcc, v26, v35
	v_cmp_lt_u32_e64 s[0:1], v26, v36
	s_and_b64 s[64:65], vcc, s[0:1]
	s_nop 2
	s_waitcnt lgkmcnt(0)
	v_fmac_f32_e32 v247, 0x3e000000, v29
	v_cndmask_b32_e64 v97, v97, v247, s[64:65]
	v_mul_u32_u24_e32 v27, 0x90, v34
	v_lshlrev_b32_e32 v26, 3, v32
	v_add_u32_e32 v32, v30, v27
	s_waitcnt vmcnt(3)
	ds_write_b128 v75, v[18:21] offset:18432
	s_waitcnt vmcnt(2)
	ds_write_b128 v75, v[22:25] offset:27648
	s_waitcnt lgkmcnt(0)
	s_barrier
; #define LAS __attribute__((address_space(3)))
; template <bool LOCAL>
; __device__ __forceinline__ void na_unit(const bf16* P, const bf16* VT, bf16* YCAT, const LAS float* rpb_l, LAS bf16* buf, int b, int gr, int hp, int qblk, int tid) {
;     ...
;     for (int sidx = 0; sidx < 2 * NCH; ++sidx) {
;         if (sidx + 2 < 2 * NCH) NA_ISSUE(sidx + 2);
;         const LAS bf16* cb = buf + (sidx & 1) * 9216 + hh * 4608;
;         if (sidx < NCH) {
;             const int c = sidx;
;             if (LOCAL && c < 8) {
; #pragma unroll
;                 for (int t2 = 0; t2 < 2; ++t2) {
;                     const LAS bf16* kp = cb + (kc0 + 16 * t2 + fr) * 72 + 8 * fq;
;                     f32x4 acc = {0.f, 0.f, 0.f, 0.f};
;                     acc = __builtin_amdgcn_mfma_f32_16x16x32_bf16(*(const LAS bf16x8*)(kp), qf[0], acc, 0, 0, 0);
;                     acc = __builtin_amdgcn_mfma_f32_16x16x32_bf16(*(const LAS bf16x8*)(kp + 32), qf[1], acc, 0, 0, 0);
;                     const LAS float* rb = rpb + (r0 + c - gr + 7) * 31 + 15 - qcol;
; #pragma unroll
;                     for (int e = 0; e < 4; ++e) { const int kcol = kc0 + 16 * t2 + 4 * fq + e; const bool ok = (kcol >= cs) && (kcol < cs + 16);
;                         const float sv = ok ? acc[e] * 0.125f + rb[ok ? kcol : qcol] : -1.0e30f; acc[e] = sv; m = fmaxf(m, sv); }
;                     sl[2 * (c < 8 ? c : 0) + t2] = acc; }
	ds_read_b32 v240, v31 offset:37916
	ds_read_b32 v241, v31 offset:37920
	ds_read_b32 v242, v31 offset:37924
	ds_read_b32 v243, v31 offset:37928
	ds_read_b32 v244, v31 offset:37980
	ds_read_b32 v245, v31 offset:37984
	ds_read_b32 v246, v31 offset:37988
	ds_read_b32 v247, v31 offset:37992
	ds_read_b128 v[18:21], v32 offset:18432
	s_add_i32 s26, s26, s15
	s_add_i32 s0, s26, 0x10c0
	v_or_b32_e32 v24, s0, v88
	v_mov_b64_e32 v[22:23], s[8:9]
	s_lshl_b32 s1, s18, 7
	v_mad_i64_i32 v[22:23], s[18:19], v24, s70, v[22:23]
	v_lshlrev_b32_e32 v70, 1, v26
	v_lshl_add_u64 v[22:23], v[22:23], 0, v[70:71]
	s_lshl_b32 s2, s1, 1
	v_lshl_add_u64 v[22:23], v[22:23], 0, s[2:3]
	ds_read_b128 v[26:29], v32 offset:18496
	s_waitcnt lgkmcnt(1)
	v_mfma_f32_16x16x32_bf16 v[34:37], v[18:21], v[6:9], 0
	global_load_dwordx4 v[18:21], v[22:23], off offset:1024
	s_nop 0
	global_load_dwordx4 v[22:25], v[22:23], off offset:1152
	v_mov_b32_e32 v98, 0xf149f2ca
	v_mov_b32_e32 v100, 0xf149f2ca
	s_waitcnt lgkmcnt(0)
	v_mfma_f32_16x16x32_bf16 v[26:29], v[26:29], v[2:5], v[34:37]
	s_nop 2
	s_waitcnt lgkmcnt(0)
	s_nop 3
	v_fmac_f32_e32 v240, 0x3e000000, v26
	v_cndmask_b32_e64 v100, v100, v240, s[28:29]
	s_nop 2
	s_waitcnt lgkmcnt(0)
	s_nop 0
	v_fmac_f32_e32 v241, 0x3e000000, v27
	v_cndmask_b32_e64 v98, v98, v241, s[30:31]
	v_mov_b32_e32 v101, 0xf149f2ca
	v_mov_b32_e32 v102, 0xf149f2ca
	s_nop 2
	s_waitcnt lgkmcnt(0)
	v_fmac_f32_e32 v242, 0x3e000000, v28
	v_cndmask_b32_e64 v102, v102, v242, s[34:35]
	s_nop 2
	s_waitcnt lgkmcnt(0)
	v_fmac_f32_e32 v243, 0x3e000000, v29
	v_cndmask_b32_e64 v101, v101, v243, s[36:37]
	v_mul_u32_u24_e32 v26, 0x90, v33
	v_add_u32_e32 v33, v30, v26
	ds_read_b128 v[26:29], v33 offset:18432
	ds_read_b128 v[34:37], v33 offset:18496
	v_mov_b32_e32 v103, 0xf149f2ca
	v_mov_b32_e32 v105, 0xf149f2ca
	s_waitcnt lgkmcnt(1)
	v_mfma_f32_16x16x32_bf16 v[26:29], v[26:29], v[6:9], 0
	s_waitcnt lgkmcnt(0)
	v_mfma_f32_16x16x32_bf16 v[26:29], v[34:37], v[2:5], v[26:29]
	s_nop 2
	s_waitcnt lgkmcnt(0)
	s_nop 3
	v_fmac_f32_e32 v244, 0x3e000000, v26
	v_cndmask_b32_e64 v105, v105, v244, s[38:39]
	s_nop 2
	s_waitcnt lgkmcnt(0)
	s_nop 0
	v_fmac_f32_e32 v245, 0x3e000000, v27
	v_cndmask_b32_e64 v103, v103, v245, s[44:45]
	v_mov_b32_e32 v107, 0xf149f2ca
	v_mov_b32_e32 v109, 0xf149f2ca
	s_nop 2
	s_waitcnt lgkmcnt(0)
	v_fmac_f32_e32 v246, 0x3e000000, v28
	v_cndmask_b32_e64 v109, v109, v246, s[46:47]
	s_nop 2
	s_waitcnt lgkmcnt(0)
	v_fmac_f32_e32 v247, 0x3e000000, v29
	v_cndmask_b32_e64 v107, v107, v247, s[64:65]
	s_waitcnt vmcnt(3)
	ds_write_b128 v75, v[10:13]
	s_waitcnt vmcnt(2)
	ds_write_b128 v75, v[14:17] offset:9216
	s_waitcnt lgkmcnt(0)
	s_barrier
	ds_read_b32 v240, v31 offset:38040
	ds_read_b32 v241, v31 offset:38044
	ds_read_b32 v242, v31 offset:38048
	ds_read_b32 v243, v31 offset:38052
	ds_read_b32 v244, v31 offset:38104
	ds_read_b32 v245, v31 offset:38108
	ds_read_b32 v246, v31 offset:38112
	ds_read_b32 v247, v31 offset:38116
	ds_read_b128 v[10:13], v32
	ds_read_b128 v[26:29], v32 offset:64
	s_add_i32 s18, s26, 0x1100
	v_or_b32_e32 v16, s18, v88
	v_mov_b64_e32 v[14:15], s[8:9]
	v_mad_i64_i32 v[14:15], s[20:21], v16, s70, v[14:15]
	v_lshl_add_u64 v[14:15], v[14:15], 0, v[70:71]
	v_lshl_add_u64 v[14:15], v[14:15], 0, s[2:3]
	s_waitcnt lgkmcnt(1)
	v_mfma_f32_16x16x32_bf16 v[34:37], v[10:13], v[6:9], 0
	global_load_dwordx4 v[10:13], v[14:15], off offset:1024
	s_nop 0
	global_load_dwordx4 v[14:17], v[14:15], off offset:1152
	v_mov_b32_e32 v104, 0xf149f2ca
	v_mov_b32_e32 v106, 0xf149f2ca
	s_waitcnt lgkmcnt(0)
	v_mfma_f32_16x16x32_bf16 v[26:29], v[26:29], v[2:5], v[34:37]
	s_nop 2
	s_waitcnt lgkmcnt(0)
	s_nop 3
	v_fmac_f32_e32 v240, 0x3e000000, v26
	v_cndmask_b32_e64 v106, v106, v240, s[28:29]
	s_nop 2
	s_waitcnt lgkmcnt(0)
	s_nop 0
	v_fmac_f32_e32 v241, 0x3e000000, v27
	v_cndmask_b32_e64 v104, v104, v241, s[30:31]
	v_mov_b32_e32 v108, 0xf149f2ca
	v_mov_b32_e32 v110, 0xf149f2ca
	s_nop 2
	s_waitcnt lgkmcnt(0)
	v_fmac_f32_e32 v242, 0x3e000000, v28
	v_cndmask_b32_e64 v110, v110, v242, s[34:35]
	s_nop 2
	s_waitcnt lgkmcnt(0)
	v_fmac_f32_e32 v243, 0x3e000000, v29
	v_cndmask_b32_e64 v108, v108, v243, s[36:37]
	ds_read_b128 v[26:29], v33
	ds_read_b128 v[34:37], v33 offset:64
	v_mov_b32_e32 v111, 0xf149f2ca
	v_mov_b32_e32 v113, 0xf149f2ca
	s_waitcnt lgkmcnt(1)
	v_mfma_f32_16x16x32_bf16 v[26:29], v[26:29], v[6:9], 0
	s_waitcnt lgkmcnt(0)
	v_mfma_f32_16x16x32_bf16 v[26:29], v[34:37], v[2:5], v[26:29]
	s_nop 2
	s_waitcnt lgkmcnt(0)
	s_nop 3
	v_fmac_f32_e32 v244, 0x3e000000, v26
	v_cndmask_b32_e64 v113, v113, v244, s[38:39]
	s_nop 2
	s_waitcnt lgkmcnt(0)
	s_nop 0
	v_fmac_f32_e32 v245, 0x3e000000, v27
	v_cndmask_b32_e64 v111, v111, v245, s[44:45]
	v_mov_b32_e32 v112, 0xf149f2ca
	v_mov_b32_e32 v116, 0xf149f2ca
	s_nop 2
	s_waitcnt lgkmcnt(0)
	v_fmac_f32_e32 v246, 0x3e000000, v28
	v_cndmask_b32_e64 v116, v116, v246, s[46:47]
	s_nop 2
	s_waitcnt lgkmcnt(0)
	v_fmac_f32_e32 v247, 0x3e000000, v29
	v_cndmask_b32_e64 v112, v112, v247, s[64:65]
	s_waitcnt vmcnt(3)
	ds_write_b128 v75, v[18:21] offset:18432
	s_waitcnt vmcnt(2)
	ds_write_b128 v75, v[22:25] offset:27648
	s_waitcnt lgkmcnt(0)
	s_barrier
; #define LAS __attribute__((address_space(3)))
; template <bool LOCAL>
; __device__ __forceinline__ void na_unit(const bf16* P, const bf16* VT, bf16* YCAT, const LAS float* rpb_l, LAS bf16* buf, int b, int gr, int hp, int qblk, int tid) {
;     ...
;     for (int sidx = 0; sidx < 2 * NCH; ++sidx) {
;         if (sidx + 2 < 2 * NCH) NA_ISSUE(sidx + 2);
;         const LAS bf16* cb = buf + (sidx & 1) * 9216 + hh * 4608;
;         if (sidx < NCH) {
;             const int c = sidx;
;             if (LOCAL && c < 8) {
; #pragma unroll
;                 for (int t2 = 0; t2 < 2; ++t2) {
;                     const LAS bf16* kp = cb + (kc0 + 16 * t2 + fr) * 72 + 8 * fq;
;                     f32x4 acc = {0.f, 0.f, 0.f, 0.f};
;                     acc = __builtin_amdgcn_mfma_f32_16x16x32_bf16(*(const LAS bf16x8*)(kp), qf[0], acc, 0, 0, 0);
;                     acc = __builtin_amdgcn_mfma_f32_16x16x32_bf16(*(const LAS bf16x8*)(kp + 32), qf[1], acc, 0, 0, 0);
;                     const LAS float* rb = rpb + (r0 + c - gr + 7) * 31 + 15 - qcol;
; #pragma unroll
;                     for (int e = 0; e < 4; ++e) { const int kcol = kc0 + 16 * t2 + 4 * fq + e; const bool ok = (kcol >= cs) && (kcol < cs + 16);
;                         const float sv = ok ? acc[e] * 0.125f + rb[ok ? kcol : qcol] : -1.0e30f; acc[e] = sv; m = fmaxf(m, sv); }
;                     sl[2 * (c < 8 ? c : 0) + t2] = acc; }
	ds_read_b32 v240, v31 offset:38164
	ds_read_b32 v241, v31 offset:38168
	ds_read_b32 v242, v31 offset:38172
	ds_read_b32 v243, v31 offset:38176
	ds_read_b32 v244, v31 offset:38228
	ds_read_b32 v245, v31 offset:38232
	ds_read_b32 v246, v31 offset:38236
	ds_read_b32 v247, v31 offset:38240
	ds_read_b128 v[18:21], v32 offset:18432
	ds_read_b128 v[26:29], v32 offset:18496
	s_add_i32 s20, s26, 0x1140
	v_or_b32_e32 v24, s20, v88
	v_mov_b64_e32 v[22:23], s[8:9]
	v_mad_i64_i32 v[22:23], s[22:23], v24, s70, v[22:23]
	v_lshl_add_u64 v[22:23], v[22:23], 0, v[70:71]
	v_lshl_add_u64 v[22:23], v[22:23], 0, s[2:3]
	s_waitcnt lgkmcnt(1)
	v_mfma_f32_16x16x32_bf16 v[34:37], v[18:21], v[6:9], 0
	global_load_dwordx4 v[18:21], v[22:23], off offset:1024
	s_nop 0
	global_load_dwordx4 v[22:25], v[22:23], off offset:1152
	v_mov_b32_e32 v114, 0xf149f2ca
	v_mov_b32_e32 v115, 0xf149f2ca
	s_waitcnt lgkmcnt(0)
	v_mfma_f32_16x16x32_bf16 v[26:29], v[26:29], v[2:5], v[34:37]
	s_nop 2
	s_waitcnt lgkmcnt(0)
	s_nop 3
	v_fmac_f32_e32 v240, 0x3e000000, v26
	v_cndmask_b32_e64 v115, v115, v240, s[28:29]
	s_nop 2
	s_waitcnt lgkmcnt(0)
	s_nop 0
	v_fmac_f32_e32 v241, 0x3e000000, v27
	v_cndmask_b32_e64 v114, v114, v241, s[30:31]
	v_mov_b32_e32 v117, 0xf149f2ca
	v_mov_b32_e32 v118, 0xf149f2ca
	s_nop 2
	s_waitcnt lgkmcnt(0)
	v_fmac_f32_e32 v242, 0x3e000000, v28
	v_cndmask_b32_e64 v118, v118, v242, s[34:35]
	s_nop 2
	s_waitcnt lgkmcnt(0)
	v_fmac_f32_e32 v243, 0x3e000000, v29
	v_cndmask_b32_e64 v117, v117, v243, s[36:37]
	ds_read_b128 v[26:29], v33 offset:18432
	ds_read_b128 v[34:37], v33 offset:18496
	v_mov_b32_e32 v119, 0xf149f2ca
	v_mov_b32_e32 v121, 0xf149f2ca
	s_waitcnt lgkmcnt(1)
	v_mfma_f32_16x16x32_bf16 v[26:29], v[26:29], v[6:9], 0
	s_waitcnt lgkmcnt(0)
	v_mfma_f32_16x16x32_bf16 v[26:29], v[34:37], v[2:5], v[26:29]
	s_nop 2
	s_waitcnt lgkmcnt(0)
	s_nop 3
	v_fmac_f32_e32 v244, 0x3e000000, v26
	v_cndmask_b32_e64 v121, v121, v244, s[38:39]
	s_nop 2
	s_waitcnt lgkmcnt(0)
	s_nop 0
	v_fmac_f32_e32 v245, 0x3e000000, v27
	v_cndmask_b32_e64 v119, v119, v245, s[44:45]
	v_mov_b32_e32 v120, 0xf149f2ca
	v_mov_b32_e32 v124, 0xf149f2ca
	s_nop 2
	s_waitcnt lgkmcnt(0)
	v_fmac_f32_e32 v246, 0x3e000000, v28
	v_cndmask_b32_e64 v124, v124, v246, s[46:47]
	s_nop 2
	s_waitcnt lgkmcnt(0)
	v_fmac_f32_e32 v247, 0x3e000000, v29
	v_cndmask_b32_e64 v120, v120, v247, s[64:65]
	s_waitcnt vmcnt(3)
	ds_write_b128 v75, v[10:13]
	s_waitcnt vmcnt(2)
	ds_write_b128 v75, v[14:17] offset:9216
	s_waitcnt lgkmcnt(0)
	s_barrier
	ds_read_b32 v240, v31 offset:38288
	ds_read_b32 v241, v31 offset:38292
	ds_read_b32 v242, v31 offset:38296
	ds_read_b32 v243, v31 offset:38300
	ds_read_b32 v244, v31 offset:38352
	ds_read_b32 v245, v31 offset:38356
	ds_read_b32 v246, v31 offset:38360
	ds_read_b32 v247, v31 offset:38364
	ds_read_b128 v[10:13], v32
	ds_read_b128 v[26:29], v32 offset:64
	s_add_i32 s22, s26, 0x1180
	v_or_b32_e32 v16, s22, v88
	v_mov_b64_e32 v[14:15], s[8:9]
	v_mad_i64_i32 v[14:15], s[24:25], v16, s70, v[14:15]
	v_lshl_add_u64 v[14:15], v[14:15], 0, v[70:71]
	v_lshl_add_u64 v[14:15], v[14:15], 0, s[2:3]
	s_waitcnt lgkmcnt(1)
	v_mfma_f32_16x16x32_bf16 v[34:37], v[10:13], v[6:9], 0
	global_load_dwordx4 v[10:13], v[14:15], off offset:1024
	s_nop 0
	global_load_dwordx4 v[14:17], v[14:15], off offset:1152
	v_mov_b32_e32 v122, 0xf149f2ca
	v_mov_b32_e32 v123, 0xf149f2ca
	s_waitcnt lgkmcnt(0)
	v_mfma_f32_16x16x32_bf16 v[26:29], v[26:29], v[2:5], v[34:37]
	s_nop 2
	s_waitcnt lgkmcnt(0)
	s_nop 3
	v_fmac_f32_e32 v240, 0x3e000000, v26
	v_cndmask_b32_e64 v123, v123, v240, s[28:29]
	s_nop 2
	s_waitcnt lgkmcnt(0)
	s_nop 0
	v_fmac_f32_e32 v241, 0x3e000000, v27
	v_cndmask_b32_e64 v122, v122, v241, s[30:31]
	v_mov_b32_e32 v125, 0xf149f2ca
	v_mov_b32_e32 v126, 0xf149f2ca
	s_nop 2
	s_waitcnt lgkmcnt(0)
	v_fmac_f32_e32 v242, 0x3e000000, v28
	v_cndmask_b32_e64 v126, v126, v242, s[34:35]
	s_nop 2
	s_waitcnt lgkmcnt(0)
	v_fmac_f32_e32 v243, 0x3e000000, v29
	v_cndmask_b32_e64 v125, v125, v243, s[36:37]
	ds_read_b128 v[26:29], v33
	ds_read_b128 v[34:37], v33 offset:64
	v_mov_b32_e32 v127, 0xf149f2ca
	v_mov_b32_e32 v129, 0xf149f2ca
	s_waitcnt lgkmcnt(1)
	v_mfma_f32_16x16x32_bf16 v[26:29], v[26:29], v[6:9], 0
	s_waitcnt lgkmcnt(0)
	v_mfma_f32_16x16x32_bf16 v[26:29], v[34:37], v[2:5], v[26:29]
	s_nop 2
	s_waitcnt lgkmcnt(0)
	s_nop 3
	v_fmac_f32_e32 v244, 0x3e000000, v26
	v_cndmask_b32_e64 v129, v129, v244, s[38:39]
	s_nop 2
	s_waitcnt lgkmcnt(0)
	s_nop 0
	v_fmac_f32_e32 v245, 0x3e000000, v27
	v_cndmask_b32_e64 v127, v127, v245, s[44:45]
	v_mov_b32_e32 v128, 0xf149f2ca
	v_mov_b32_e32 v133, 0xf149f2ca
	s_nop 2
	s_waitcnt lgkmcnt(0)
	v_fmac_f32_e32 v246, 0x3e000000, v28
	v_cndmask_b32_e64 v133, v133, v246, s[46:47]
	s_nop 2
	s_waitcnt lgkmcnt(0)
	v_fmac_f32_e32 v247, 0x3e000000, v29
	v_cndmask_b32_e64 v128, v128, v247, s[64:65]
	s_waitcnt vmcnt(3)
	ds_write_b128 v75, v[18:21] offset:18432
	s_waitcnt vmcnt(2)
	ds_write_b128 v75, v[22:25] offset:27648
	s_waitcnt lgkmcnt(0)
	s_barrier
; #define LAS __attribute__((address_space(3)))
; template <bool LOCAL>
; __device__ __forceinline__ void na_unit(const bf16* P, const bf16* VT, bf16* YCAT, const LAS float* rpb_l, LAS bf16* buf, int b, int gr, int hp, int qblk, int tid) {
;     ...
;     for (int sidx = 0; sidx < 2 * NCH; ++sidx) {
;         if (sidx + 2 < 2 * NCH) NA_ISSUE(sidx + 2);
;         const LAS bf16* cb = buf + (sidx & 1) * 9216 + hh * 4608;
;         if (sidx < NCH) {
;             const int c = sidx;
;             if (LOCAL && c < 8) {
; #pragma unroll
;                 for (int t2 = 0; t2 < 2; ++t2) {
;                     const LAS bf16* kp = cb + (kc0 + 16 * t2 + fr) * 72 + 8 * fq;
;                     f32x4 acc = {0.f, 0.f, 0.f, 0.f};
;                     acc = __builtin_amdgcn_mfma_f32_16x16x32_bf16(*(const LAS bf16x8*)(kp), qf[0], acc, 0, 0, 0);
;                     acc = __builtin_amdgcn_mfma_f32_16x16x32_bf16(*(const LAS bf16x8*)(kp + 32), qf[1], acc, 0, 0, 0);
;                     const LAS float* rb = rpb + (r0 + c - gr + 7) * 31 + 15 - qcol;
; #pragma unroll
;                     for (int e = 0; e < 4; ++e) { const int kcol = kc0 + 16 * t2 + 4 * fq + e; const bool ok = (kcol >= cs) && (kcol < cs + 16);
;                         const float sv = ok ? acc[e] * 0.125f + rb[ok ? kcol : qcol] : -1.0e30f; acc[e] = sv; m = fmaxf(m, sv); }
;                     sl[2 * (c < 8 ? c : 0) + t2] = acc; }
	ds_read_b32 v240, v31 offset:38412
	ds_read_b32 v241, v31 offset:38416
	ds_read_b32 v242, v31 offset:38420
	ds_read_b32 v243, v31 offset:38424
	ds_read_b32 v244, v31 offset:38476
	ds_read_b32 v245, v31 offset:38480
	ds_read_b32 v246, v31 offset:38484
	ds_read_b32 v247, v31 offset:38488
	ds_read_b128 v[18:21], v32 offset:18432
	ds_read_b128 v[26:29], v32 offset:18496
	s_add_i32 s24, s26, 0x11c0
	v_or_b32_e32 v24, s24, v88
	v_mov_b64_e32 v[22:23], s[8:9]
	v_mad_i64_i32 v[22:23], s[26:27], v24, s70, v[22:23]
	v_lshl_add_u64 v[22:23], v[22:23], 0, v[70:71]
	v_lshl_add_u64 v[22:23], v[22:23], 0, s[2:3]
	s_waitcnt lgkmcnt(1)
	v_mfma_f32_16x16x32_bf16 v[34:37], v[18:21], v[6:9], 0
	global_load_dwordx4 v[18:21], v[22:23], off offset:1024
	s_nop 0
	global_load_dwordx4 v[22:25], v[22:23], off offset:1152
	v_mov_b32_e32 v130, 0xf149f2ca
	v_mov_b32_e32 v131, 0xf149f2ca
	s_waitcnt lgkmcnt(0)
	v_mfma_f32_16x16x32_bf16 v[26:29], v[26:29], v[2:5], v[34:37]
	s_nop 2
	s_waitcnt lgkmcnt(0)
	s_nop 3
	v_fmac_f32_e32 v240, 0x3e000000, v26
	v_cndmask_b32_e64 v131, v131, v240, s[28:29]
	s_nop 2
	s_waitcnt lgkmcnt(0)
	s_nop 0
	v_fmac_f32_e32 v241, 0x3e000000, v27
	v_cndmask_b32_e64 v130, v130, v241, s[30:31]
	v_mov_b32_e32 v134, 0xf149f2ca
	v_mov_b32_e32 v135, 0xf149f2ca
	s_nop 2
	s_waitcnt lgkmcnt(0)
	v_fmac_f32_e32 v242, 0x3e000000, v28
	v_cndmask_b32_e64 v135, v135, v242, s[34:35]
	s_nop 2
	s_waitcnt lgkmcnt(0)
	v_fmac_f32_e32 v243, 0x3e000000, v29
	v_cndmask_b32_e64 v134, v134, v243, s[36:37]
	ds_read_b128 v[26:29], v33 offset:18432
	ds_read_b128 v[34:37], v33 offset:18496
	v_mov_b32_e32 v137, 0xf149f2ca
	v_mov_b32_e32 v139, 0xf149f2ca
	s_waitcnt lgkmcnt(1)
	v_mfma_f32_16x16x32_bf16 v[26:29], v[26:29], v[6:9], 0
	s_waitcnt lgkmcnt(0)
	v_mfma_f32_16x16x32_bf16 v[26:29], v[34:37], v[2:5], v[26:29]
	s_nop 2
	s_waitcnt lgkmcnt(0)
	s_nop 3
	v_fmac_f32_e32 v244, 0x3e000000, v26
	v_cndmask_b32_e64 v139, v139, v244, s[38:39]
	s_nop 2
	s_waitcnt lgkmcnt(0)
	s_nop 0
	v_fmac_f32_e32 v245, 0x3e000000, v27
	v_cndmask_b32_e64 v137, v137, v245, s[44:45]
	v_mov_b32_e32 v138, 0xf149f2ca
	v_mov_b32_e32 v142, 0xf149f2ca
	s_nop 2
	s_waitcnt lgkmcnt(0)
	v_fmac_f32_e32 v246, 0x3e000000, v28
	v_cndmask_b32_e64 v142, v142, v246, s[46:47]
	s_nop 2
	s_waitcnt lgkmcnt(0)
	v_fmac_f32_e32 v247, 0x3e000000, v29
	v_cndmask_b32_e64 v138, v138, v247, s[64:65]
	s_waitcnt vmcnt(3)
	ds_write_b128 v75, v[10:13]
	s_waitcnt vmcnt(2)
	ds_write_b128 v75, v[14:17] offset:9216
	s_waitcnt lgkmcnt(0)
	s_barrier
	ds_read_b32 v240, v31 offset:38536
	ds_read_b32 v241, v31 offset:38540
	ds_read_b32 v242, v31 offset:38544
	ds_read_b32 v243, v31 offset:38548
	ds_read_b32 v244, v31 offset:38600
	ds_read_b32 v245, v31 offset:38604
	ds_read_b32 v246, v31 offset:38608
	ds_read_b32 v247, v31 offset:38612
	ds_read_b128 v[10:13], v32
	ds_read_b128 v[26:29], v32 offset:64
	s_lshl_b32 s26, s17, 8
	v_or_b32_e32 v34, s26, v88
	v_mov_b64_e32 v[14:15], s[8:9]
	v_mad_i64_i32 v[14:15], s[52:53], v34, s70, v[14:15]
	v_lshl_add_u64 v[14:15], v[14:15], 0, v[70:71]
	v_lshl_add_u64 v[14:15], v[14:15], 0, s[2:3]
	s_waitcnt lgkmcnt(1)
	v_mfma_f32_16x16x32_bf16 v[36:39], v[10:13], v[6:9], 0
	global_load_dwordx4 v[10:13], v[14:15], off offset:1024
	s_nop 0
	global_load_dwordx4 v[14:17], v[14:15], off offset:1152
	v_mov_b32_e32 v140, 0xf149f2ca
	v_mov_b32_e32 v141, 0xf149f2ca
	s_waitcnt lgkmcnt(0)
	v_mfma_f32_16x16x32_bf16 v[26:29], v[26:29], v[2:5], v[36:39]
	s_nop 2
	s_waitcnt lgkmcnt(0)
	s_nop 3
	v_fmac_f32_e32 v240, 0x3e000000, v26
	v_cndmask_b32_e64 v141, v141, v240, s[28:29]
	s_nop 2
	s_waitcnt lgkmcnt(0)
	s_nop 0
	v_fmac_f32_e32 v241, 0x3e000000, v27
	v_cndmask_b32_e64 v140, v140, v241, s[30:31]
	v_mov_b32_e32 v143, 0xf149f2ca
	v_mov_b32_e32 v144, 0xf149f2ca
	s_nop 2
	s_waitcnt lgkmcnt(0)
	v_fmac_f32_e32 v242, 0x3e000000, v28
	v_cndmask_b32_e64 v144, v144, v242, s[34:35]
	s_nop 2
	s_waitcnt lgkmcnt(0)
	v_fmac_f32_e32 v243, 0x3e000000, v29
	v_cndmask_b32_e64 v143, v143, v243, s[36:37]
	ds_read_b128 v[26:29], v33
	ds_read_b128 v[36:39], v33 offset:64
	v_mov_b32_e32 v145, 0xf149f2ca
	v_mov_b32_e32 v149, 0xf149f2ca
	s_waitcnt lgkmcnt(1)
	v_mfma_f32_16x16x32_bf16 v[26:29], v[26:29], v[6:9], 0
	s_waitcnt lgkmcnt(0)
	v_mfma_f32_16x16x32_bf16 v[26:29], v[36:39], v[2:5], v[26:29]
	s_nop 2
	s_waitcnt lgkmcnt(0)
	s_nop 3
	v_fmac_f32_e32 v244, 0x3e000000, v26
	v_cndmask_b32_e64 v149, v149, v244, s[38:39]
	s_nop 2
	s_waitcnt lgkmcnt(0)
	s_nop 0
	v_fmac_f32_e32 v245, 0x3e000000, v27
	v_cndmask_b32_e64 v145, v145, v245, s[44:45]
	v_mov_b32_e32 v148, 0xf149f2ca
	v_mov_b32_e32 v152, 0xf149f2ca
	s_nop 2
	s_waitcnt lgkmcnt(0)
	v_fmac_f32_e32 v246, 0x3e000000, v28
	v_cndmask_b32_e64 v152, v152, v246, s[46:47]
	s_nop 2
	s_waitcnt lgkmcnt(0)
	v_fmac_f32_e32 v247, 0x3e000000, v29
	v_cndmask_b32_e64 v148, v148, v247, s[64:65]
	s_waitcnt vmcnt(3)
	ds_write_b128 v75, v[18:21] offset:18432
	s_waitcnt vmcnt(2)
	ds_write_b128 v75, v[22:25] offset:27648
	s_waitcnt lgkmcnt(0)
	s_barrier
; #define LAS __attribute__((address_space(3)))
; template <bool LOCAL>
; __device__ __forceinline__ void na_unit(const bf16* P, const bf16* VT, bf16* YCAT, const LAS float* rpb_l, LAS bf16* buf, int b, int gr, int hp, int qblk, int tid) {
;     ...
;     for (int sidx = 0; sidx < 2 * NCH; ++sidx) {
;         if (sidx + 2 < 2 * NCH) NA_ISSUE(sidx + 2);
;         const LAS bf16* cb = buf + (sidx & 1) * 9216 + hh * 4608;
;         if (sidx < NCH) {
;             const int c = sidx;
;             if (LOCAL && c < 8) {
; #pragma unroll
;                 for (int t2 = 0; t2 < 2; ++t2) {
;                     const LAS bf16* kp = cb + (kc0 + 16 * t2 + fr) * 72 + 8 * fq;
;                     f32x4 acc = {0.f, 0.f, 0.f, 0.f};
;                     acc = __builtin_amdgcn_mfma_f32_16x16x32_bf16(*(const LAS bf16x8*)(kp), qf[0], acc, 0, 0, 0);
;                     acc = __builtin_amdgcn_mfma_f32_16x16x32_bf16(*(const LAS bf16x8*)(kp + 32), qf[1], acc, 0, 0, 0);
;                     const LAS float* rb = rpb + (r0 + c - gr + 7) * 31 + 15 - qcol;
; #pragma unroll
;                     for (int e = 0; e < 4; ++e) { const int kcol = kc0 + 16 * t2 + 4 * fq + e; const bool ok = (kcol >= cs) && (kcol < cs + 16);
;                         const float sv = ok ? acc[e] * 0.125f + rb[ok ? kcol : qcol] : -1.0e30f; acc[e] = sv; m = fmaxf(m, sv); }
;                     sl[2 * (c < 8 ? c : 0) + t2] = acc; }
;             } else {
;                 const int cc = c - NLOC;
; #pragma unroll
;                 for (int t4 = 0; t4 < 4; ++t4) {
;                     const LAS bf16* kp = cb + (16 * t4 + fr) * 72 + 8 * fq;
;                     f32x4 acc = {0.f, 0.f, 0.f, 0.f};
;                     acc = __builtin_amdgcn_mfma_f32_16x16x32_bf16(*(const LAS bf16x8*)(kp), qf[0], acc, 0, 0, 0);
;                     acc = __builtin_amdgcn_mfma_f32_16x16x32_bf16(*(const LAS bf16x8*)(kp + 32), qf[1], acc, 0, 0, 0);
; #pragma unroll
;                     for (int e = 0; e < 4; ++e) { acc[e] *= 0.125f; m = fmaxf(m, acc[e]); }
;                     sc[4 * (cc >= 0 ? cc : 0) + t4] = acc; }
;             }
;             if (sidx == NCH - 1) { m = fmaxf(m, __shfl_xor(m, 16)); m = fmaxf(m, __shfl_xor(m, 32)); }
	ds_read_b32 v240, v31 offset:38660
	ds_read_b32 v241, v31 offset:38664
	ds_read_b32 v242, v31 offset:38668
	ds_read_b32 v243, v31 offset:38672
	ds_read_b32 v244, v31 offset:38724
	ds_read_b32 v245, v31 offset:38728
	ds_read_b32 v246, v31 offset:38732
	ds_read_b32 v247, v31 offset:38736
	ds_read_b128 v[18:21], v32 offset:18432
	ds_read_b128 v[26:29], v32 offset:18496
	v_or_b32_e32 v24, 64, v34
	v_mov_b64_e32 v[22:23], s[8:9]
	v_mad_i64_i32 v[22:23], s[52:53], v24, s70, v[22:23]
	v_lshl_add_u64 v[22:23], v[22:23], 0, v[70:71]
	v_lshl_add_u64 v[22:23], v[22:23], 0, s[2:3]
	s_waitcnt lgkmcnt(1)
	v_mfma_f32_16x16x32_bf16 v[36:39], v[18:21], v[6:9], 0
	global_load_dwordx4 v[18:21], v[22:23], off offset:1024
	s_nop 0
	global_load_dwordx4 v[22:25], v[22:23], off offset:1152
	v_mov_b32_e32 v150, 0xf149f2ca
	v_mov_b32_e32 v151, 0xf149f2ca
	s_waitcnt lgkmcnt(0)
	v_mfma_f32_16x16x32_bf16 v[26:29], v[26:29], v[2:5], v[36:39]
	s_nop 2
	s_waitcnt lgkmcnt(0)
	s_nop 3
	v_fmac_f32_e32 v240, 0x3e000000, v26
	v_cndmask_b32_e64 v151, v151, v240, s[28:29]
	s_nop 2
	s_waitcnt lgkmcnt(0)
	s_nop 0
	v_fmac_f32_e32 v241, 0x3e000000, v27
	v_cndmask_b32_e64 v150, v150, v241, s[30:31]
	v_mov_b32_e32 v153, 0xf149f2ca
	v_mov_b32_e32 v154, 0xf149f2ca
	s_nop 2
	s_waitcnt lgkmcnt(0)
	v_fmac_f32_e32 v242, 0x3e000000, v28
	v_cndmask_b32_e64 v154, v154, v242, s[34:35]
	s_nop 2
	s_waitcnt lgkmcnt(0)
	v_fmac_f32_e32 v243, 0x3e000000, v29
	v_cndmask_b32_e64 v153, v153, v243, s[36:37]
	ds_read_b128 v[26:29], v33 offset:18432
	ds_read_b128 v[36:39], v33 offset:18496
	v_mov_b32_e32 v155, 0xf149f2ca
	v_mov_b32_e32 v157, 0xf149f2ca
	s_waitcnt lgkmcnt(1)
	v_mfma_f32_16x16x32_bf16 v[26:29], v[26:29], v[6:9], 0
	s_waitcnt lgkmcnt(0)
	v_mfma_f32_16x16x32_bf16 v[26:29], v[36:39], v[2:5], v[26:29]
	s_nop 2
	s_waitcnt lgkmcnt(0)
	s_nop 3
	v_fmac_f32_e32 v244, 0x3e000000, v26
	v_cndmask_b32_e64 v157, v157, v244, s[38:39]
	s_nop 2
	s_waitcnt lgkmcnt(0)
	s_nop 0
	v_fmac_f32_e32 v245, 0x3e000000, v27
	v_cndmask_b32_e64 v155, v155, v245, s[44:45]
	v_mov_b32_e32 v156, 0xf149f2ca
	v_mov_b32_e32 v159, 0xf149f2ca
	s_nop 2
	s_waitcnt lgkmcnt(0)
	v_fmac_f32_e32 v246, 0x3e000000, v28
	v_cndmask_b32_e64 v159, v159, v246, s[46:47]
	s_nop 2
	s_waitcnt lgkmcnt(0)
	v_fmac_f32_e32 v247, 0x3e000000, v29
	v_cndmask_b32_e64 v156, v156, v247, s[64:65]
	v_max3_f32 v26, v92, s73, v91
	v_max3_f32 v26, v26, v94, v93
	v_max3_f32 v26, v26, v96, v95
	v_max3_f32 v26, v26, v99, v97
	v_max3_f32 v26, v26, v100, v98
	v_max3_f32 v26, v26, v102, v101
	v_max3_f32 v26, v26, v105, v103
	v_max3_f32 v26, v26, v109, v107
	v_max3_f32 v26, v26, v106, v104
	v_max3_f32 v26, v26, v110, v108
	v_max3_f32 v26, v26, v113, v111
	v_max3_f32 v26, v26, v116, v112
	v_max3_f32 v26, v26, v115, v114
	v_max3_f32 v26, v26, v118, v117
	v_max3_f32 v26, v26, v121, v119
	v_max3_f32 v26, v26, v124, v120
	v_max3_f32 v26, v26, v123, v122
	v_max3_f32 v26, v26, v126, v125
	v_max3_f32 v26, v26, v129, v127
	v_max3_f32 v26, v26, v133, v128
	v_max3_f32 v26, v26, v131, v130
	v_max3_f32 v26, v26, v135, v134
	v_max3_f32 v26, v26, v139, v137
	v_max3_f32 v26, v26, v142, v138
	v_max3_f32 v26, v26, v141, v140
	v_max3_f32 v26, v26, v144, v143
	v_mad_u32_u24 v89, v89, s71, v30
	v_max3_f32 v26, v26, v149, v145
	s_waitcnt vmcnt(3)
	ds_write_b128 v75, v[10:13]
	s_waitcnt vmcnt(2)
	ds_write_b128 v75, v[14:17] offset:9216
	s_waitcnt lgkmcnt(0)
	s_barrier
	ds_read_b128 v[10:13], v89
	ds_read_b128 v[14:17], v89 offset:64
	v_max3_f32 v26, v26, v152, v148
	v_max3_f32 v26, v26, v151, v150
	v_max3_f32 v26, v26, v154, v153
	v_max3_f32 v26, v26, v157, v155
	v_max3_f32 v35, v26, v159, v156
	v_or_b32_e32 v26, 0x80, v34
	v_mov_b64_e32 v[44:45], s[8:9]
	v_mad_i64_i32 v[26:27], s[28:29], v26, s70, v[44:45]
	v_lshl_add_u64 v[26:27], v[26:27], 0, v[70:71]
	v_lshl_add_u64 v[30:31], v[26:27], 0, s[2:3]
	s_waitcnt lgkmcnt(1)
	v_mfma_f32_16x16x32_bf16 v[10:13], v[10:13], v[6:9], 0
	global_load_dwordx4 v[26:29], v[30:31], off offset:1024
	s_nop 0
	global_load_dwordx4 v[30:33], v[30:31], off offset:1152
	ds_read_b128 v[36:39], v89 offset:2304
	v_lshl_add_u64 v[78:79], s[4:5], 0, v[70:71]
	s_waitcnt lgkmcnt(1)
	v_mfma_f32_16x16x32_bf16 v[62:65], v[14:17], v[2:5], v[10:13]
	s_ashr_i32 s17, s16, 31
	v_mov_b32_e32 v81, v71
	v_cmp_lt_i32_e32 vcc, v83, v84
	ds_read_b128 v[10:13], v89 offset:2368
	v_add3_u32 v158, v86, v76, v87
	s_nop 2
	v_mul_f32_e32 v14, 0x3e000000, v62
	v_mul_f32_e32 v15, 0x3e000000, v63
	v_max3_f32 v35, v35, v14, v15
	v_mul_f32_e32 v40, 0x3e000000, v64
	s_waitcnt lgkmcnt(1)
	v_mfma_f32_16x16x32_bf16 v[14:17], v[36:39], v[6:9], 0
	v_mul_f32_e32 v36, 0x3e000000, v65
	v_max3_f32 v35, v35, v40, v36
	ds_read_b128 v[36:39], v89 offset:4608
	s_waitcnt lgkmcnt(1)
	v_mfma_f32_16x16x32_bf16 v[66:69], v[10:13], v[2:5], v[14:17]
	ds_read_b128 v[10:13], v89 offset:4672
	s_ashr_i32 s19, s18, 31
	s_ashr_i32 s21, s20, 31
	s_ashr_i32 s23, s22, 31
	s_ashr_i32 s25, s24, 31
	s_nop 2
	v_mul_f32_e32 v14, 0x3e000000, v66
	v_mul_f32_e32 v15, 0x3e000000, v67
	v_max3_f32 v35, v35, v14, v15
	s_waitcnt lgkmcnt(1)
	v_mfma_f32_16x16x32_bf16 v[14:17], v[36:39], v[6:9], 0
	v_mul_f32_e32 v40, 0x3e000000, v68
	v_mul_f32_e32 v41, 0x3e000000, v69
	v_max3_f32 v35, v35, v40, v41
	s_waitcnt lgkmcnt(0)
	v_mfma_f32_16x16x32_bf16 v[58:61], v[10:13], v[2:5], v[14:17]
	ds_read_b128 v[36:39], v89 offset:6912
	ds_read_b128 v[40:43], v89 offset:6976
	s_waitcnt vmcnt(3)
	ds_write_b128 v75, v[18:21] offset:18432
	s_waitcnt vmcnt(2)
	ds_write_b128 v75, v[22:25] offset:27648
	s_waitcnt lgkmcnt(0)
	s_nop 0
	v_mul_f32_e32 v10, 0x3e000000, v58
	v_mul_f32_e32 v11, 0x3e000000, v59
	v_max3_f32 v14, v35, v10, v11
	v_mfma_f32_16x16x32_bf16 v[10:13], v[36:39], v[6:9], 0
	v_mul_f32_e32 v15, 0x3e000000, v60
	v_mul_f32_e32 v16, 0x3e000000, v61
	v_max3_f32 v14, v14, v15, v16
	v_mfma_f32_16x16x32_bf16 v[54:57], v[40:43], v[2:5], v[10:13]
	s_barrier
; #define LAS __attribute__((address_space(3)))
; template <bool LOCAL>
; __device__ __forceinline__ void na_unit(const bf16* P, const bf16* VT, bf16* YCAT, const LAS float* rpb_l, LAS bf16* buf, int b, int gr, int hp, int qblk, int tid) {
;     ...
;             } else {
;                 const int cc = c - NLOC;
; #pragma unroll
;                 for (int t4 = 0; t4 < 4; ++t4) {
;                     const LAS bf16* kp = cb + (16 * t4 + fr) * 72 + 8 * fq;
;                     f32x4 acc = {0.f, 0.f, 0.f, 0.f};
;                     acc = __builtin_amdgcn_mfma_f32_16x16x32_bf16(*(const LAS bf16x8*)(kp), qf[0], acc, 0, 0, 0);
;                     acc = __builtin_amdgcn_mfma_f32_16x16x32_bf16(*(const LAS bf16x8*)(kp + 32), qf[1], acc, 0, 0, 0);
; #pragma unroll
;                     for (int e = 0; e < 4; ++e) { acc[e] *= 0.125f; m = fmaxf(m, acc[e]); }
;                     sc[4 * (cc >= 0 ? cc : 0) + t4] = acc; }
;             }
;             if (sidx == NCH - 1) { m = fmaxf(m, __shfl_xor(m, 16)); m = fmaxf(m, __shfl_xor(m, 32)); }
	v_or_b32_e32 v18, 0xc0, v34
	v_mad_i64_i32 v[18:19], s[28:29], v18, s70, v[44:45]
	v_lshl_add_u64 v[18:19], v[18:19], 0, v[70:71]
	s_nop 3
	v_mul_f32_e32 v10, 0x3e000000, v54
	v_mul_f32_e32 v11, 0x3e000000, v55
	v_max3_f32 v14, v14, v10, v11
	ds_read_b128 v[10:13], v89 offset:18432
	v_mul_f32_e32 v15, 0x3e000000, v56
	v_mul_f32_e32 v16, 0x3e000000, v57
	v_max3_f32 v35, v14, v15, v16
	ds_read_b128 v[14:17], v89 offset:18496
	v_lshl_add_u64 v[22:23], v[18:19], 0, s[2:3]
	s_waitcnt lgkmcnt(1)
	v_mfma_f32_16x16x32_bf16 v[10:13], v[10:13], v[6:9], 0
	global_load_dwordx4 v[18:21], v[22:23], off offset:1024
	global_load_dwordx4 v[160:163], v[22:23], off offset:1152
	ds_read_b128 v[22:25], v89 offset:20736
	s_ashr_i32 s27, s26, 31
	s_waitcnt lgkmcnt(1)
	v_mfma_f32_16x16x32_bf16 v[46:49], v[14:17], v[2:5], v[10:13]
	s_nop 2
	ds_read_b128 v[10:13], v89 offset:20800
	s_nop 3
	v_mul_f32_e32 v14, 0x3e000000, v46
	v_mul_f32_e32 v15, 0x3e000000, v47
	v_max3_f32 v34, v35, v14, v15
	v_mul_f32_e32 v35, 0x3e000000, v48
	s_waitcnt lgkmcnt(1)
	v_mfma_f32_16x16x32_bf16 v[14:17], v[22:25], v[6:9], 0
	v_mul_f32_e32 v22, 0x3e000000, v49
	v_max3_f32 v34, v34, v35, v22
	ds_read_b128 v[22:25], v89 offset:23040
	s_waitcnt lgkmcnt(1)
	v_mfma_f32_16x16x32_bf16 v[50:53], v[10:13], v[2:5], v[14:17]
	ds_read_b128 v[10:13], v89 offset:23104
	s_nop 6
	v_mul_f32_e32 v14, 0x3e000000, v50
	v_mul_f32_e32 v15, 0x3e000000, v51
	v_max3_f32 v34, v34, v14, v15
	s_waitcnt lgkmcnt(1)
	v_mfma_f32_16x16x32_bf16 v[14:17], v[22:25], v[6:9], 0
	v_mul_f32_e32 v35, 0x3e000000, v52
	v_mul_f32_e32 v36, 0x3e000000, v53
	v_max3_f32 v38, v34, v35, v36
	s_waitcnt lgkmcnt(0)
	v_mfma_f32_16x16x32_bf16 v[42:45], v[10:13], v[2:5], v[14:17]
	ds_read_b128 v[22:25], v89 offset:25344
	ds_read_b128 v[34:37], v89 offset:25408
	s_waitcnt vmcnt(3)
	ds_write_b128 v75, v[26:29]
	s_waitcnt vmcnt(2)
	ds_write_b128 v75, v[30:33] offset:9216
	s_waitcnt lgkmcnt(0)
	s_nop 0
	v_mul_f32_e32 v10, 0x3e000000, v42
	v_mul_f32_e32 v11, 0x3e000000, v43
	v_max3_f32 v14, v38, v10, v11
	v_mfma_f32_16x16x32_bf16 v[10:13], v[22:25], v[6:9], 0
	v_mul_f32_e32 v15, 0x3e000000, v44
	v_mul_f32_e32 v16, 0x3e000000, v45
	v_max3_f32 v14, v14, v15, v16
	v_mfma_f32_16x16x32_bf16 v[38:41], v[34:37], v[2:5], v[10:13]
	s_barrier
	v_add3_u32 v26, v88, s1, 64
	v_mul_u32_u24_e32 v26, 0x9000, v26
	v_lshl_add_u64 v[22:23], s[16:17], 1, v[78:79]
	s_nop 3
	v_mul_f32_e32 v10, 0x3e000000, v38
	v_mul_f32_e32 v11, 0x3e000000, v39
	v_max3_f32 v10, v14, v10, v11
	v_mul_f32_e32 v11, 0x3e000000, v40
	v_mul_f32_e32 v12, 0x3e000000, v41
	v_max3_f32 v34, v10, v11, v12
	v_or_b32_e32 v10, s1, v88
	v_mul_u32_u24_e32 v14, 0x9000, v10
	ds_read_b128 v[10:13], v89
	v_lshlrev_b32_e32 v70, 1, v14
	ds_read_b128 v[14:17], v89 offset:64
	v_lshlrev_b32_e32 v80, 1, v26
	v_lshl_add_u64 v[24:25], v[22:23], 0, v[70:71]
	v_lshl_add_u64 v[22:23], v[22:23], 0, v[80:81]
	s_waitcnt lgkmcnt(1)
	v_mfma_f32_16x16x32_bf16 v[10:13], v[10:13], v[6:9], 0
	global_load_dwordx4 v[164:167], v[24:25], off
	global_load_dwordx4 v[168:171], v[22:23], off
	ds_read_b128 v[22:25], v89 offset:2304
	s_add_i32 s16, s15, s50
	s_waitcnt lgkmcnt(1)
	v_mfma_f32_16x16x32_bf16 v[30:33], v[14:17], v[2:5], v[10:13]
	s_ashr_i32 s17, s16, 31
	s_ashr_i32 s15, s14, 31
	v_lshl_add_u64 v[86:87], s[14:15], 1, v[78:79]
	ds_read_b128 v[10:13], v89 offset:2368
	s_ashr_i32 s1, s0, 31
	s_nop 2
	v_mul_f32_e32 v14, 0x3e000000, v30
	v_mul_f32_e32 v15, 0x3e000000, v31
	v_max3_f32 v26, v34, v14, v15
	v_mul_f32_e32 v27, 0x3e000000, v32
	s_waitcnt lgkmcnt(1)
	v_mfma_f32_16x16x32_bf16 v[14:17], v[22:25], v[6:9], 0
	v_mul_f32_e32 v22, 0x3e000000, v33
	v_max3_f32 v26, v26, v27, v22
	ds_read_b128 v[22:25], v89 offset:4608
	s_waitcnt lgkmcnt(1)
	v_mfma_f32_16x16x32_bf16 v[34:37], v[10:13], v[2:5], v[14:17]
	ds_read_b128 v[10:13], v89 offset:4672
	s_nop 6
	v_mul_f32_e32 v14, 0x3e000000, v34
	v_mul_f32_e32 v15, 0x3e000000, v35
	v_max3_f32 v26, v26, v14, v15
	s_waitcnt lgkmcnt(1)
	v_mfma_f32_16x16x32_bf16 v[14:17], v[22:25], v[6:9], 0
	v_mul_f32_e32 v27, 0x3e000000, v36
	v_mul_f32_e32 v28, 0x3e000000, v37
	v_max3_f32 v88, v26, v27, v28
	s_waitcnt lgkmcnt(0)
	v_mfma_f32_16x16x32_bf16 v[26:29], v[10:13], v[2:5], v[14:17]
	ds_read_b128 v[22:25], v89 offset:6912
	ds_read_b128 v[172:175], v89 offset:6976
	s_waitcnt vmcnt(3)
	ds_write_b128 v75, v[18:21] offset:18432
	s_waitcnt vmcnt(2)
	ds_write_b128 v75, v[160:163] offset:27648
	s_waitcnt lgkmcnt(0)
	s_nop 0
	v_mul_f32_e32 v10, 0x3e000000, v26
	v_mul_f32_e32 v11, 0x3e000000, v27
	v_max3_f32 v14, v88, v10, v11
	v_mfma_f32_16x16x32_bf16 v[10:13], v[22:25], v[6:9], 0
	v_mul_f32_e32 v15, 0x3e000000, v28
	v_mul_f32_e32 v16, 0x3e000000, v29
	v_max3_f32 v14, v14, v15, v16
	v_mfma_f32_16x16x32_bf16 v[22:25], v[172:175], v[2:5], v[10:13]
	s_barrier
; #define LAS __attribute__((address_space(3)))
; __device__ __forceinline__ unsigned cvt_pk_bf16(float lo, float hi) { const float __attribute__((ext_vector_type(2))) v = {lo, hi}; return __builtin_bit_cast(unsigned, __builtin_convertvector(v, bf16x2_t)); }
; template <bool LOCAL>
; __device__ __forceinline__ void na_unit(const bf16* P, const bf16* VT, bf16* YCAT, const LAS float* rpb_l, LAS bf16* buf, int b, int gr, int hp, int qblk, int tid) {
;     ...
;                 const int cc = c - NLOC;
; #pragma unroll
;                 for (int t4 = 0; t4 < 4; ++t4) {
;                     const LAS bf16* kp = cb + (16 * t4 + fr) * 72 + 8 * fq;
;                     f32x4 acc = {0.f, 0.f, 0.f, 0.f};
;                     acc = __builtin_amdgcn_mfma_f32_16x16x32_bf16(*(const LAS bf16x8*)(kp), qf[0], acc, 0, 0, 0);
;                     acc = __builtin_amdgcn_mfma_f32_16x16x32_bf16(*(const LAS bf16x8*)(kp + 32), qf[1], acc, 0, 0, 0);
; #pragma unroll
;                     for (int e = 0; e < 4; ++e) { acc[e] *= 0.125f; m = fmaxf(m, acc[e]); }
;                     sc[4 * (cc >= 0 ? cc : 0) + t4] = acc; }
;             }
;             if (sidx == NCH - 1) { m = fmaxf(m, __shfl_xor(m, 16)); m = fmaxf(m, __shfl_xor(m, 32)); }
;         } else {
;             const int c = sidx - NCH;
;             if (LOCAL && c < 8) {
;                 float p[8];
; #pragma unroll
;                 for (int e = 0; e < 4; ++e) { p[e] = __expf(sl[2 * (c < 8 ? c : 0)][e] - m); p[4 + e] = __expf(sl[2 * (c < 8 ? c : 0) + 1][e] - m); }
; #pragma unroll
;                 for (int e = 0; e < 8; ++e) lsum += p[e];
;                 const bf16x8 pf = __builtin_bit_cast(bf16x8, (v4u){pg8::cvt_pk_bf16(p[0], p[1]), pg8::cvt_pk_bf16(p[2], p[3]), pg8::cvt_pk_bf16(p[4], p[5]), pg8::cvt_pk_bf16(p[6], p[7])});
; #pragma unroll
;                 for (int dt = 0; dt < 4; ++dt) { const LAS bf16* vp = cb + (16 * dt + fr) * 72 + kc0 + 4 * fq;
;                     o[dt] = __builtin_amdgcn_mfma_f32_16x16x32_bf16(frag44(vp, vp + 16), pf, o[dt], 0, 0, 0); }
	v_lshl_add_u64 v[18:19], s[16:17], 1, v[78:79]
	v_lshl_add_u64 v[20:21], v[18:19], 0, v[70:71]
	v_lshl_add_u64 v[18:19], v[18:19], 0, v[80:81]
	s_nop 3
	v_mul_f32_e32 v10, 0x3e000000, v22
	v_mul_f32_e32 v11, 0x3e000000, v23
	v_max3_f32 v14, v14, v10, v11
	ds_read_b128 v[10:13], v89 offset:18432
	v_mul_f32_e32 v15, 0x3e000000, v24
	v_mul_f32_e32 v16, 0x3e000000, v25
	v_max3_f32 v88, v14, v15, v16
	ds_read_b128 v[14:17], v89 offset:18496
	s_waitcnt lgkmcnt(1)
	v_mfma_f32_16x16x32_bf16 v[10:13], v[10:13], v[6:9], 0
	global_load_dwordx4 v[172:175], v[20:21], off
	global_load_dwordx4 v[176:179], v[18:19], off
	ds_read_b128 v[18:21], v89 offset:20736
	ds_read_b128 v[160:163], v89 offset:23040
	s_waitcnt lgkmcnt(2)
	v_mfma_f32_16x16x32_bf16 v[14:17], v[14:17], v[2:5], v[10:13]
	s_nop 2
	ds_read_b128 v[10:13], v89 offset:20800
	s_waitcnt lgkmcnt(2)
	v_mfma_f32_16x16x32_bf16 v[18:21], v[18:21], v[6:9], 0
	s_nop 1
	v_mul_f32_e32 v132, 0x3e000000, v14
	v_mul_f32_e32 v136, 0x3e000000, v15
	v_max3_f32 v88, v88, v132, v136
	s_waitcnt lgkmcnt(0)
	v_mfma_f32_16x16x32_bf16 v[18:21], v[10:13], v[2:5], v[18:21]
	ds_read_b128 v[10:13], v89 offset:23104
	ds_read_b128 v[180:183], v89 offset:25344
	ds_read_b128 v[184:187], v89 offset:25408
	v_mul_f32_e32 v132, 0x3e000000, v16
	v_mfma_f32_16x16x32_bf16 v[160:163], v[160:163], v[6:9], 0
	v_mul_f32_e32 v136, 0x3e000000, v17
	v_max3_f32 v88, v88, v132, v136
	s_nop 0
	v_mul_f32_e32 v132, 0x3e000000, v18
	s_waitcnt lgkmcnt(1)
	v_mfma_f32_16x16x32_bf16 v[6:9], v[180:183], v[6:9], 0
	v_mul_f32_e32 v136, 0x3e000000, v19
	v_max3_f32 v88, v88, v132, v136
	v_mul_f32_e32 v132, 0x3e000000, v20
	v_mfma_f32_16x16x32_bf16 v[10:13], v[10:13], v[2:5], v[160:163]
	v_mul_f32_e32 v136, 0x3e000000, v21
	v_max3_f32 v88, v88, v132, v136
	s_waitcnt vmcnt(3)
	ds_write_b128 v75, v[164:167]
	s_waitcnt vmcnt(2)
	ds_write_b128 v75, v[168:171] offset:9216
	s_waitcnt lgkmcnt(2)
	v_mfma_f32_16x16x32_bf16 v[2:5], v[184:187], v[2:5], v[6:9]
	v_mul_f32_e32 v89, 0x3e000000, v10
	v_mul_f32_e32 v132, 0x3e000000, v11
	v_max3_f32 v88, v88, v89, v132
	v_mul_f32_e32 v89, 0x3e000000, v12
	v_mul_f32_e32 v132, 0x3e000000, v13
	v_max3_f32 v88, v88, v89, v132
	s_nop 1
	v_mul_f32_e32 v6, 0x3e000000, v2
	v_mul_f32_e32 v7, 0x3e000000, v3
	v_max3_f32 v6, v88, v6, v7
	v_mul_f32_e32 v7, 0x3e000000, v4
	v_mul_f32_e32 v8, 0x3e000000, v5
	v_max3_f32 v6, v6, v7, v8
	v_cndmask_b32_e32 v7, v82, v83, vcc
	v_lshlrev_b32_e32 v88, 2, v7
	ds_bpermute_b32 v7, v88, v6
	v_cmp_lt_i32_e32 vcc, v85, v84
	v_lshl_add_u32 v8, v90, 1, v158
	s_waitcnt lgkmcnt(0)
	s_barrier
	v_max_f32_e32 v7, v7, v7
	v_max_f32_e32 v6, v6, v7
	v_cndmask_b32_e32 v7, v82, v85, vcc
	v_lshlrev_b32_e32 v89, 2, v7
	ds_bpermute_b32 v7, v89, v6
	s_waitcnt lgkmcnt(0)
	ds_read2_b64 v[160:163], v8 offset1:4
	v_max_f32_e32 v7, v7, v7
	v_max_f32_e32 v136, v6, v7
	v_sub_f32_e32 v6, v92, v136
	v_mul_f32_e32 v6, 0x3fb8aa3b, v6
	v_exp_f32_e32 v132, v6
	v_sub_f32_e32 v6, v96, v136
	v_mul_f32_e32 v6, 0x3fb8aa3b, v6
	v_exp_f32_e32 v92, v6
	v_sub_f32_e32 v6, v91, v136
	v_mul_f32_e32 v6, 0x3fb8aa3b, v6
	v_exp_f32_e32 v96, v6
	v_sub_f32_e32 v6, v95, v136
	v_mul_f32_e32 v6, 0x3fb8aa3b, v6
	v_exp_f32_e32 v91, v6
	v_sub_f32_e32 v6, v94, v136
	v_mul_f32_e32 v6, 0x3fb8aa3b, v6
	v_exp_f32_e32 v95, v6
	v_sub_f32_e32 v6, v99, v136
	v_mul_f32_e32 v6, 0x3fb8aa3b, v6
	v_exp_f32_e32 v94, v6
	v_sub_f32_e32 v6, v93, v136
	v_mul_f32_e32 v6, 0x3fb8aa3b, v6
	v_exp_f32_e32 v99, v6
	v_sub_f32_e32 v6, v97, v136
	v_mul_f32_e32 v6, 0x3fb8aa3b, v6
	v_exp_f32_e32 v93, v6
	v_cvt_pk_bf16_f32 v164, v132, v96
	v_cvt_pk_bf16_f32 v165, v95, v99
	v_cvt_pk_bf16_f32 v166, v92, v91
	v_cvt_pk_bf16_f32 v167, v94, v93
	v_add_u32_e32 v7, 0x800, v8
	v_add_u32_e32 v6, 0x1000, v8
	s_waitcnt lgkmcnt(0)
	v_mfma_f32_16x16x32_bf16 v[184:187], v[160:163], v[164:167], 0
	v_lshl_add_u64 v[160:161], v[86:87], 0, v[70:71]
	ds_read2_b64 v[168:171], v7 offset0:32 offset1:36
	ds_read2_b64 v[180:183], v6 offset0:64 offset1:68
	v_lshl_add_u64 v[86:87], v[86:87], 0, v[80:81]
	global_load_dwordx4 v[188:191], v[160:161], off
	global_load_dwordx4 v[192:195], v[86:87], off
	v_sub_f32_e32 v9, v100, v136
	v_mul_f32_e32 v9, 0x3fb8aa3b, v9
	v_add_u32_e32 v160, 0x1800, v8
	v_exp_f32_e32 v86, v9
	v_sub_f32_e32 v9, v105, v136
	ds_read2_b64 v[196:199], v160 offset0:96 offset1:100
	v_mul_f32_e32 v9, 0x3fb8aa3b, v9
	v_exp_f32_e32 v76, v9
	v_sub_f32_e32 v9, v98, v136
	v_mul_f32_e32 v9, 0x3fb8aa3b, v9
	v_exp_f32_e32 v90, v9
	v_sub_f32_e32 v9, v103, v136
	v_mul_f32_e32 v9, 0x3fb8aa3b, v9
	v_exp_f32_e32 v87, v9
	v_sub_f32_e32 v9, v102, v136
	v_mul_f32_e32 v9, 0x3fb8aa3b, v9
	v_exp_f32_e32 v98, v9
	v_sub_f32_e32 v9, v109, v136
	v_mul_f32_e32 v9, 0x3fb8aa3b, v9
	v_add_u32_e32 v162, 0x4800, v8
	s_waitcnt lgkmcnt(2)
	v_mfma_f32_16x16x32_bf16 v[168:171], v[168:171], v[164:167], 0
	s_waitcnt vmcnt(3)
	ds_write_b128 v75, v[172:175] offset:18432
	s_waitcnt vmcnt(2)
	ds_write_b128 v75, v[176:179] offset:27648
	s_waitcnt lgkmcnt(0)
	s_barrier
; #define LAS __attribute__((address_space(3)))
; __device__ __forceinline__ unsigned cvt_pk_bf16(float lo, float hi) { const float __attribute__((ext_vector_type(2))) v = {lo, hi}; return __builtin_bit_cast(unsigned, __builtin_convertvector(v, bf16x2_t)); }
; template <bool LOCAL>
; __device__ __forceinline__ void na_unit(const bf16* P, const bf16* VT, bf16* YCAT, const LAS float* rpb_l, LAS bf16* buf, int b, int gr, int hp, int qblk, int tid) {
;     ...
;             if (LOCAL && c < 8) {
;                 float p[8];
; #pragma unroll
;                 for (int e = 0; e < 4; ++e) { p[e] = __expf(sl[2 * (c < 8 ? c : 0)][e] - m); p[4 + e] = __expf(sl[2 * (c < 8 ? c : 0) + 1][e] - m); }
; #pragma unroll
;                 for (int e = 0; e < 8; ++e) lsum += p[e];
;                 const bf16x8 pf = __builtin_bit_cast(bf16x8, (v4u){pg8::cvt_pk_bf16(p[0], p[1]), pg8::cvt_pk_bf16(p[2], p[3]), pg8::cvt_pk_bf16(p[4], p[5]), pg8::cvt_pk_bf16(p[6], p[7])});
; #pragma unroll
;                 for (int dt = 0; dt < 4; ++dt) { const LAS bf16* vp = cb + (16 * dt + fr) * 72 + kc0 + 4 * fq;
;                     o[dt] = __builtin_amdgcn_mfma_f32_16x16x32_bf16(frag44(vp, vp + 16), pf, o[dt], 0, 0, 0); }
;             } else {
;                 const int cc = c - NLOC;
; #pragma unroll
;                 for (int p2 = 0; p2 < 2; ++p2) {
;                     float p[8];
; #pragma unroll
;                     for (int e = 0; e < 4; ++e) { p[e] = __expf(sc[4 * (cc >= 0 ? cc : 0) + 2 * p2][e] - m); p[4 + e] = __expf(sc[4 * (cc >= 0 ? cc : 0) + 2 * p2 + 1][e] - m); }
; #pragma unroll
;                     for (int e = 0; e < 8; ++e) lsum += p[e];
;                     const bf16x8 pf = __builtin_bit_cast(bf16x8, (v4u){pg8::cvt_pk_bf16(p[0], p[1]), pg8::cvt_pk_bf16(p[2], p[3]), pg8::cvt_pk_bf16(p[4], p[5]), pg8::cvt_pk_bf16(p[6], p[7])});
; #pragma unroll
;                     for (int dt = 0; dt < 4; ++dt) { const LAS bf16* vp = cb + (16 * dt + fr) * 72 + 32 * p2 + 4 * fq;
;                         o[dt] = __builtin_amdgcn_mfma_f32_16x16x32_bf16(frag44(vp, vp + 16), pf, o[dt], 0, 0, 0); }
;                 }
;             }
;         }
;         if (sidx + 1 < 2 * NCH) NA_STORE(sidx + 1);
;         __syncthreads();
	v_mfma_f32_16x16x32_bf16 v[180:183], v[180:183], v[164:167], 0
	v_exp_f32_e32 v97, v9
	v_sub_f32_e32 v9, v101, v136
	v_mfma_f32_16x16x32_bf16 v[196:199], v[196:199], v[164:167], 0
	ds_read2_b64 v[164:167], v162 offset1:4
	v_add_u32_e32 v161, 0x5000, v8
	v_mul_f32_e32 v9, 0x3fb8aa3b, v9
	ds_read2_b64 v[172:175], v161 offset0:32 offset1:36
	v_exp_f32_e32 v100, v9
	v_sub_f32_e32 v9, v107, v136
	v_mul_f32_e32 v9, 0x3fb8aa3b, v9
	v_exp_f32_e32 v101, v9
	v_cvt_pk_bf16_f32 v176, v86, v90
	v_cvt_pk_bf16_f32 v177, v98, v100
	v_cvt_pk_bf16_f32 v178, v76, v87
	v_cvt_pk_bf16_f32 v179, v97, v101
	v_lshl_add_u64 v[102:103], s[0:1], 1, v[78:79]
	v_add_u32_e32 v163, 0x5800, v8
	s_waitcnt lgkmcnt(1)
	v_mfma_f32_16x16x32_bf16 v[184:187], v[164:167], v[176:179], v[184:187]
	v_lshl_add_u64 v[164:165], v[102:103], 0, v[70:71]
	v_lshl_add_u64 v[102:103], v[102:103], 0, v[80:81]
	v_sub_f32_e32 v9, v106, v136
	s_waitcnt lgkmcnt(0)
	v_mfma_f32_16x16x32_bf16 v[166:169], v[172:175], v[176:179], v[168:171]
	v_mul_f32_e32 v9, 0x3fb8aa3b, v9
	v_fma_f32 v62, v62, s72, -v136
	v_fma_f32 v63, v63, s72, -v136
	ds_read2_b64 v[170:173], v163 offset0:64 offset1:68
	global_load_dwordx4 v[200:203], v[164:165], off
	global_load_dwordx4 v[204:207], v[102:103], off
	v_add_u32_e32 v164, 0x6000, v8
	v_exp_f32_e32 v103, v9
	v_sub_f32_e32 v9, v113, v136
	s_waitcnt lgkmcnt(0)
	v_mfma_f32_16x16x32_bf16 v[170:173], v[170:173], v[176:179], v[180:183]
	s_nop 2
	ds_read2_b64 v[180:183], v164 offset0:96 offset1:100
	v_mul_f32_e32 v9, 0x3fb8aa3b, v9
	v_exp_f32_e32 v102, v9
	v_sub_f32_e32 v9, v104, v136
	v_mul_f32_e32 v9, 0x3fb8aa3b, v9
	v_exp_f32_e32 v105, v9
	v_sub_f32_e32 v9, v111, v136
	v_mul_f32_e32 v9, 0x3fb8aa3b, v9
	v_exp_f32_e32 v104, v9
	v_sub_f32_e32 v9, v110, v136
	v_mul_f32_e32 v9, 0x3fb8aa3b, v9
	v_exp_f32_e32 v107, v9
	v_sub_f32_e32 v9, v116, v136
	v_mul_f32_e32 v9, 0x3fb8aa3b, v9
	s_waitcnt lgkmcnt(0)
	v_mfma_f32_16x16x32_bf16 v[174:177], v[180:183], v[176:179], v[196:199]
	s_waitcnt vmcnt(3)
	ds_write_b128 v75, v[188:191]
	s_waitcnt vmcnt(2)
	ds_write_b128 v75, v[192:195] offset:9216
	s_waitcnt lgkmcnt(0)
	s_barrier
	v_exp_f32_e32 v106, v9
	v_sub_f32_e32 v9, v108, v136
	ds_read2_b64 v[178:181], v8 offset1:4
	v_mul_f32_e32 v9, 0x3fb8aa3b, v9
	v_exp_f32_e32 v108, v9
	v_sub_f32_e32 v9, v112, v136
	v_mul_f32_e32 v9, 0x3fb8aa3b, v9
	v_exp_f32_e32 v109, v9
	v_lshl_add_u64 v[192:193], s[18:19], 1, v[78:79]
	v_cvt_pk_bf16_f32 v188, v103, v105
	v_cvt_pk_bf16_f32 v189, v107, v108
	v_cvt_pk_bf16_f32 v190, v102, v104
	v_cvt_pk_bf16_f32 v191, v106, v109
	v_lshl_add_u64 v[196:197], v[192:193], 0, v[80:81]
	ds_read2_b64 v[110:113], v7 offset0:32 offset1:36
	s_waitcnt lgkmcnt(1)
	v_mfma_f32_16x16x32_bf16 v[178:181], v[178:181], v[188:191], v[184:187]
	v_sub_f32_e32 v9, v115, v136
	v_mul_f32_e32 v9, 0x3fb8aa3b, v9
	v_fma_f32 v64, v64, s72, -v136
	v_lshl_add_u64 v[186:187], v[192:193], 0, v[70:71]
	ds_read2_b64 v[182:185], v6 offset0:64 offset1:68
	global_load_dwordx4 v[192:195], v[186:187], off
	s_nop 0
	global_load_dwordx4 v[196:199], v[196:197], off
	s_waitcnt lgkmcnt(1)
	v_mfma_f32_16x16x32_bf16 v[166:169], v[110:113], v[188:191], v[166:169]
	ds_read2_b64 v[110:113], v160 offset0:96 offset1:100
	s_waitcnt vmcnt(3)
	ds_write_b128 v75, v[200:203] offset:18432
	s_waitcnt vmcnt(2)
	ds_write_b128 v75, v[204:207] offset:27648
	s_waitcnt lgkmcnt(2)
	v_mfma_f32_16x16x32_bf16 v[174:177], v[110:113], v[188:191], v[174:177]
	v_exp_f32_e32 v111, v9
	v_sub_f32_e32 v9, v121, v136
	v_mul_f32_e32 v9, 0x3fb8aa3b, v9
	v_exp_f32_e32 v110, v9
	v_sub_f32_e32 v9, v114, v136
	v_mul_f32_e32 v9, 0x3fb8aa3b, v9
	v_exp_f32_e32 v113, v9
	v_sub_f32_e32 v9, v119, v136
	v_mul_f32_e32 v9, 0x3fb8aa3b, v9
	v_exp_f32_e32 v112, v9
	v_sub_f32_e32 v9, v118, v136
	v_mul_f32_e32 v9, 0x3fb8aa3b, v9
	v_exp_f32_e32 v115, v9
	v_sub_f32_e32 v9, v124, v136
	v_mul_f32_e32 v9, 0x3fb8aa3b, v9
	v_exp_f32_e32 v114, v9
	v_sub_f32_e32 v9, v117, v136
	v_mul_f32_e32 v9, 0x3fb8aa3b, v9
	v_mfma_f32_16x16x32_bf16 v[170:173], v[182:185], v[188:191], v[170:173]
	s_waitcnt lgkmcnt(0)
	s_barrier
	v_exp_f32_e32 v116, v9
	ds_read2_b64 v[182:185], v162 offset1:4
	v_sub_f32_e32 v9, v120, v136
	ds_read2_b64 v[118:121], v161 offset0:32 offset1:36
	v_mul_f32_e32 v9, 0x3fb8aa3b, v9
	v_exp_f32_e32 v117, v9
	v_lshl_add_u64 v[190:191], s[20:21], 1, v[78:79]
	v_lshl_add_u64 v[200:201], v[190:191], 0, v[70:71]
	v_cvt_pk_bf16_f32 v186, v111, v113
	v_cvt_pk_bf16_f32 v187, v115, v116
	v_cvt_pk_bf16_f32 v188, v110, v112
	v_cvt_pk_bf16_f32 v189, v114, v117
	v_lshl_add_u64 v[190:191], v[190:191], 0, v[80:81]
	v_sub_f32_e32 v9, v123, v136
	s_waitcnt lgkmcnt(1)
	v_mfma_f32_16x16x32_bf16 v[178:181], v[182:185], v[186:189], v[178:181]
	global_load_dwordx4 v[182:185], v[200:201], off
	s_nop 0
	global_load_dwordx4 v[200:203], v[190:191], off
	v_mul_f32_e32 v9, 0x3fb8aa3b, v9
	v_fma_f32 v65, v65, s72, -v136
	s_waitcnt lgkmcnt(0)
	v_mfma_f32_16x16x32_bf16 v[166:169], v[118:121], v[186:189], v[166:169]
	ds_read2_b64 v[118:121], v163 offset0:64 offset1:68
	v_mul_f32_e32 v62, 0x3fb8aa3b, v62
	v_mul_f32_e32 v63, 0x3fb8aa3b, v63
	s_waitcnt lgkmcnt(0)
	v_mfma_f32_16x16x32_bf16 v[170:173], v[118:121], v[186:189], v[170:173]
	ds_read2_b64 v[118:121], v164 offset0:96 offset1:100
	s_waitcnt vmcnt(3)
	ds_write_b128 v75, v[192:195]
	s_waitcnt vmcnt(2)
	ds_write_b128 v75, v[196:199] offset:9216
	s_waitcnt lgkmcnt(0)
	v_mfma_f32_16x16x32_bf16 v[174:177], v[118:121], v[186:189], v[174:177]
	v_exp_f32_e32 v119, v9
	v_sub_f32_e32 v9, v129, v136
	v_mul_f32_e32 v9, 0x3fb8aa3b, v9
	v_exp_f32_e32 v118, v9
	v_sub_f32_e32 v9, v122, v136
	v_mul_f32_e32 v9, 0x3fb8aa3b, v9
	v_exp_f32_e32 v121, v9
	v_sub_f32_e32 v9, v127, v136
	v_mul_f32_e32 v9, 0x3fb8aa3b, v9
	v_exp_f32_e32 v120, v9
	v_sub_f32_e32 v9, v126, v136
	v_mul_f32_e32 v9, 0x3fb8aa3b, v9
	v_exp_f32_e32 v123, v9
	v_sub_f32_e32 v9, v133, v136
	v_mul_f32_e32 v9, 0x3fb8aa3b, v9
	s_barrier
; #define LAS __attribute__((address_space(3)))
; __device__ __forceinline__ unsigned cvt_pk_bf16(float lo, float hi) { const float __attribute__((ext_vector_type(2))) v = {lo, hi}; return __builtin_bit_cast(unsigned, __builtin_convertvector(v, bf16x2_t)); }
; template <bool LOCAL>
; __device__ __forceinline__ void na_unit(const bf16* P, const bf16* VT, bf16* YCAT, const LAS float* rpb_l, LAS bf16* buf, int b, int gr, int hp, int qblk, int tid) {
;     ...
;             if (LOCAL && c < 8) {
;                 float p[8];
; #pragma unroll
;                 for (int e = 0; e < 4; ++e) { p[e] = __expf(sl[2 * (c < 8 ? c : 0)][e] - m); p[4 + e] = __expf(sl[2 * (c < 8 ? c : 0) + 1][e] - m); }
; #pragma unroll
;                 for (int e = 0; e < 8; ++e) lsum += p[e];
;                 const bf16x8 pf = __builtin_bit_cast(bf16x8, (v4u){pg8::cvt_pk_bf16(p[0], p[1]), pg8::cvt_pk_bf16(p[2], p[3]), pg8::cvt_pk_bf16(p[4], p[5]), pg8::cvt_pk_bf16(p[6], p[7])});
; #pragma unroll
;                 for (int dt = 0; dt < 4; ++dt) { const LAS bf16* vp = cb + (16 * dt + fr) * 72 + kc0 + 4 * fq;
;                     o[dt] = __builtin_amdgcn_mfma_f32_16x16x32_bf16(frag44(vp, vp + 16), pf, o[dt], 0, 0, 0); }
;             } else {
;                 const int cc = c - NLOC;
; #pragma unroll
;                 for (int p2 = 0; p2 < 2; ++p2) {
;                     float p[8];
; #pragma unroll
;                     for (int e = 0; e < 4; ++e) { p[e] = __expf(sc[4 * (cc >= 0 ? cc : 0) + 2 * p2][e] - m); p[4 + e] = __expf(sc[4 * (cc >= 0 ? cc : 0) + 2 * p2 + 1][e] - m); }
; #pragma unroll
;                     for (int e = 0; e < 8; ++e) lsum += p[e];
;                     const bf16x8 pf = __builtin_bit_cast(bf16x8, (v4u){pg8::cvt_pk_bf16(p[0], p[1]), pg8::cvt_pk_bf16(p[2], p[3]), pg8::cvt_pk_bf16(p[4], p[5]), pg8::cvt_pk_bf16(p[6], p[7])});
; #pragma unroll
;                     for (int dt = 0; dt < 4; ++dt) { const LAS bf16* vp = cb + (16 * dt + fr) * 72 + 32 * p2 + 4 * fq;
;                         o[dt] = __builtin_amdgcn_mfma_f32_16x16x32_bf16(frag44(vp, vp + 16), pf, o[dt], 0, 0, 0); }
;                 }
;             }
;         }
;         if (sidx + 1 < 2 * NCH) NA_STORE(sidx + 1);
;         __syncthreads();
	v_exp_f32_e32 v122, v9
	v_sub_f32_e32 v9, v125, v136
	ds_read2_b64 v[186:189], v8 offset1:4
	v_mul_f32_e32 v9, 0x3fb8aa3b, v9
	v_exp_f32_e32 v124, v9
	v_sub_f32_e32 v9, v128, v136
	v_mul_f32_e32 v9, 0x3fb8aa3b, v9
	v_exp_f32_e32 v125, v9
	v_lshl_add_u64 v[194:195], s[22:23], 1, v[78:79]
	v_cvt_pk_bf16_f32 v190, v119, v121
	v_cvt_pk_bf16_f32 v191, v123, v124
	v_cvt_pk_bf16_f32 v192, v118, v120
	v_cvt_pk_bf16_f32 v193, v122, v125
	v_lshl_add_u64 v[196:197], v[194:195], 0, v[70:71]
	ds_read2_b64 v[126:129], v7 offset0:32 offset1:36
	s_waitcnt lgkmcnt(1)
	v_mfma_f32_16x16x32_bf16 v[178:181], v[186:189], v[190:193], v[178:181]
	ds_read2_b64 v[186:189], v6 offset0:64 offset1:68
	v_lshl_add_u64 v[198:199], v[194:195], 0, v[80:81]
	global_load_dwordx4 v[194:197], v[196:197], off
	s_nop 0
	global_load_dwordx4 v[204:207], v[198:199], off
	s_waitcnt lgkmcnt(1)
	v_mfma_f32_16x16x32_bf16 v[166:169], v[126:129], v[190:193], v[166:169]
	ds_read2_b64 v[126:129], v160 offset0:96 offset1:100
	v_sub_f32_e32 v9, v131, v136
	v_mul_f32_e32 v9, 0x3fb8aa3b, v9
	s_waitcnt lgkmcnt(0)
	v_mfma_f32_16x16x32_bf16 v[174:177], v[126:129], v[190:193], v[174:177]
	v_exp_f32_e32 v127, v9
	v_sub_f32_e32 v9, v139, v136
	v_mul_f32_e32 v9, 0x3fb8aa3b, v9
	v_exp_f32_e32 v126, v9
	v_sub_f32_e32 v9, v130, v136
	v_mul_f32_e32 v9, 0x3fb8aa3b, v9
	v_exp_f32_e32 v129, v9
	v_sub_f32_e32 v9, v137, v136
	v_mul_f32_e32 v9, 0x3fb8aa3b, v9
	v_exp_f32_e32 v128, v9
	v_sub_f32_e32 v9, v135, v136
	v_mul_f32_e32 v9, 0x3fb8aa3b, v9
	v_exp_f32_e32 v131, v9
	v_sub_f32_e32 v9, v142, v136
	v_mul_f32_e32 v9, 0x3fb8aa3b, v9
	v_mfma_f32_16x16x32_bf16 v[170:173], v[186:189], v[190:193], v[170:173]
	s_waitcnt vmcnt(3)
	ds_write_b128 v75, v[182:185] offset:18432
	s_waitcnt vmcnt(2)
	ds_write_b128 v75, v[200:203] offset:27648
	s_waitcnt lgkmcnt(0)
	s_barrier
	v_exp_f32_e32 v130, v9
	v_sub_f32_e32 v9, v134, v136
	ds_read2_b64 v[182:185], v162 offset1:4
	ds_read2_b64 v[186:189], v161 offset0:32 offset1:36
	v_mul_f32_e32 v9, 0x3fb8aa3b, v9
	v_exp_f32_e32 v133, v9
	v_sub_f32_e32 v9, v138, v136
	v_mul_f32_e32 v9, 0x3fb8aa3b, v9
	v_exp_f32_e32 v134, v9
	v_lshl_add_u64 v[198:199], s[24:25], 1, v[78:79]
	v_lshl_add_u64 v[200:201], v[198:199], 0, v[70:71]
	v_cvt_pk_bf16_f32 v190, v127, v129
	v_cvt_pk_bf16_f32 v191, v131, v133
	v_cvt_pk_bf16_f32 v192, v126, v128
	v_cvt_pk_bf16_f32 v193, v130, v134
	v_lshl_add_u64 v[138:139], v[198:199], 0, v[80:81]
	v_sub_f32_e32 v9, v141, v136
	s_waitcnt lgkmcnt(1)
	v_mfma_f32_16x16x32_bf16 v[178:181], v[182:185], v[190:193], v[178:181]
	global_load_dwordx4 v[182:185], v[200:201], off
	s_nop 0
	global_load_dwordx4 v[198:201], v[138:139], off
	v_mul_f32_e32 v9, 0x3fb8aa3b, v9
	v_exp_f32_e32 v137, v9
	s_waitcnt lgkmcnt(0)
	v_mfma_f32_16x16x32_bf16 v[166:169], v[186:189], v[190:193], v[166:169]
	ds_read2_b64 v[186:189], v163 offset0:64 offset1:68
	v_sub_f32_e32 v9, v149, v136
	v_mul_f32_e32 v9, 0x3fb8aa3b, v9
	s_waitcnt lgkmcnt(0)
	v_mfma_f32_16x16x32_bf16 v[170:173], v[186:189], v[190:193], v[170:173]
	ds_read2_b64 v[186:189], v164 offset0:96 offset1:100
	v_exp_f32_e32 v135, v9
	v_sub_f32_e32 v9, v140, v136
	v_mul_f32_e32 v9, 0x3fb8aa3b, v9
	v_exp_f32_e32 v139, v9
	v_sub_f32_e32 v9, v145, v136
	v_mul_f32_e32 v9, 0x3fb8aa3b, v9
	v_exp_f32_e32 v138, v9
	v_sub_f32_e32 v9, v144, v136
	v_mul_f32_e32 v9, 0x3fb8aa3b, v9
	s_waitcnt lgkmcnt(0)
	v_mfma_f32_16x16x32_bf16 v[174:177], v[186:189], v[190:193], v[174:177]
	s_waitcnt vmcnt(3)
	ds_write_b128 v75, v[194:197]
	s_waitcnt vmcnt(2)
	ds_write_b128 v75, v[204:207] offset:9216
	s_waitcnt lgkmcnt(0)
	s_barrier
	v_exp_f32_e32 v141, v9
	v_sub_f32_e32 v9, v152, v136
	ds_read2_b64 v[186:189], v8 offset1:4
	v_mul_f32_e32 v9, 0x3fb8aa3b, v9
	ds_read2_b64 v[194:197], v7 offset0:32 offset1:36
	v_exp_f32_e32 v140, v9
	v_sub_f32_e32 v9, v143, v136
	v_sub_f32_e32 v8, v148, v136
	v_mul_f32_e32 v9, 0x3fb8aa3b, v9
	v_mul_f32_e32 v8, 0x3fb8aa3b, v8
	v_exp_f32_e32 v142, v9
	v_exp_f32_e32 v143, v8
	v_cvt_pk_bf16_f32 v190, v137, v139
	v_cvt_pk_bf16_f32 v192, v135, v138
	v_cvt_pk_bf16_f32 v191, v141, v142
	v_cvt_pk_bf16_f32 v193, v140, v143
	v_lshl_add_u64 v[8:9], s[26:27], 1, v[78:79]
	v_sub_f32_e32 v145, v153, v136
	s_waitcnt lgkmcnt(1)
	v_mfma_f32_16x16x32_bf16 v[178:181], v[186:189], v[190:193], v[178:181]
	ds_read2_b64 v[186:189], v6 offset0:64 offset1:68
	v_lshl_add_u64 v[6:7], v[8:9], 0, v[70:71]
	v_lshl_add_u64 v[8:9], v[8:9], 0, v[80:81]
	s_waitcnt lgkmcnt(1)
	v_mfma_f32_16x16x32_bf16 v[166:169], v[194:197], v[190:193], v[166:169]
	global_load_dwordx4 v[194:197], v[6:7], off
	global_load_dwordx4 v[202:205], v[8:9], off
	ds_read2_b64 v[78:81], v160 offset0:96 offset1:100
	s_waitcnt vmcnt(3)
	ds_write_b128 v75, v[182:185] offset:18432
	s_waitcnt vmcnt(2)
	ds_write_b128 v75, v[198:201] offset:27648
	s_waitcnt lgkmcnt(2)
	v_mfma_f32_16x16x32_bf16 v[174:177], v[78:81], v[190:193], v[174:177]
	s_waitcnt lgkmcnt(0)
	s_barrier
; #define LAS __attribute__((address_space(3)))
; __device__ __forceinline__ unsigned cvt_pk_bf16(float lo, float hi) { const float __attribute__((ext_vector_type(2))) v = {lo, hi}; return __builtin_bit_cast(unsigned, __builtin_convertvector(v, bf16x2_t)); }
; template <bool LOCAL>
; __device__ __forceinline__ void na_unit(const bf16* P, const bf16* VT, bf16* YCAT, const LAS float* rpb_l, LAS bf16* buf, int b, int gr, int hp, int qblk, int tid) {
;     ...
;             if (LOCAL && c < 8) {
;                 float p[8];
; #pragma unroll
;                 for (int e = 0; e < 4; ++e) { p[e] = __expf(sl[2 * (c < 8 ? c : 0)][e] - m); p[4 + e] = __expf(sl[2 * (c < 8 ? c : 0) + 1][e] - m); }
; #pragma unroll
;                 for (int e = 0; e < 8; ++e) lsum += p[e];
;                 const bf16x8 pf = __builtin_bit_cast(bf16x8, (v4u){pg8::cvt_pk_bf16(p[0], p[1]), pg8::cvt_pk_bf16(p[2], p[3]), pg8::cvt_pk_bf16(p[4], p[5]), pg8::cvt_pk_bf16(p[6], p[7])});
; #pragma unroll
;                 for (int dt = 0; dt < 4; ++dt) { const LAS bf16* vp = cb + (16 * dt + fr) * 72 + kc0 + 4 * fq;
;                     o[dt] = __builtin_amdgcn_mfma_f32_16x16x32_bf16(frag44(vp, vp + 16), pf, o[dt], 0, 0, 0); }
;             } else {
;                 const int cc = c - NLOC;
; #pragma unroll
;                 for (int p2 = 0; p2 < 2; ++p2) {
;                     float p[8];
; #pragma unroll
;                     for (int e = 0; e < 4; ++e) { p[e] = __expf(sc[4 * (cc >= 0 ? cc : 0) + 2 * p2][e] - m); p[4 + e] = __expf(sc[4 * (cc >= 0 ? cc : 0) + 2 * p2 + 1][e] - m); }
; #pragma unroll
;                     for (int e = 0; e < 8; ++e) lsum += p[e];
;                     const bf16x8 pf = __builtin_bit_cast(bf16x8, (v4u){pg8::cvt_pk_bf16(p[0], p[1]), pg8::cvt_pk_bf16(p[2], p[3]), pg8::cvt_pk_bf16(p[4], p[5]), pg8::cvt_pk_bf16(p[6], p[7])});
; #pragma unroll
;                     for (int dt = 0; dt < 4; ++dt) { const LAS bf16* vp = cb + (16 * dt + fr) * 72 + 32 * p2 + 4 * fq;
;                         o[dt] = __builtin_amdgcn_mfma_f32_16x16x32_bf16(frag44(vp, vp + 16), pf, o[dt], 0, 0, 0); }
;                 }
	v_sub_f32_e32 v70, v151, v136
	v_sub_f32_e32 v79, v150, v136
	v_sub_f32_e32 v81, v154, v136
	ds_read2_b64 v[150:153], v162 offset1:4
	v_mul_f32_e32 v70, 0x3fb8aa3b, v70
	v_mul_f32_e32 v79, 0x3fb8aa3b, v79
	v_mul_f32_e32 v81, 0x3fb8aa3b, v81
	v_mul_f32_e32 v145, 0x3fb8aa3b, v145
	v_exp_f32_e32 v78, v70
	v_sub_f32_e32 v70, v157, v136
	v_exp_f32_e32 v80, v79
	v_sub_f32_e32 v79, v155, v136
	v_exp_f32_e32 v144, v81
	v_sub_f32_e32 v81, v159, v136
	v_exp_f32_e32 v148, v145
	v_sub_f32_e32 v145, v156, v136
	v_mul_f32_e32 v70, 0x3fb8aa3b, v70
	v_mul_f32_e32 v79, 0x3fb8aa3b, v79
	v_mul_f32_e32 v81, 0x3fb8aa3b, v81
	v_mul_f32_e32 v145, 0x3fb8aa3b, v145
	v_exp_f32_e32 v70, v70
	v_exp_f32_e32 v79, v79
	v_exp_f32_e32 v81, v81
	v_exp_f32_e32 v145, v145
	v_cvt_pk_bf16_f32 v154, v78, v80
	v_cvt_pk_bf16_f32 v155, v144, v148
	v_cvt_pk_bf16_f32 v156, v70, v79
	v_cvt_pk_bf16_f32 v157, v81, v145
	v_mfma_f32_16x16x32_bf16 v[170:173], v[186:189], v[190:193], v[170:173]
	v_mul_f32_e32 v64, 0x3fb8aa3b, v64
	v_mul_f32_e32 v65, 0x3fb8aa3b, v65
	v_exp_f32_e32 v149, v62
	s_waitcnt lgkmcnt(0)
	v_mfma_f32_16x16x32_bf16 v[150:153], v[150:153], v[154:157], v[178:181]
	v_fma_f32 v62, v66, s72, -v136
	v_exp_f32_e32 v66, v63
	v_fma_f32 v63, v67, s72, -v136
	ds_read2_b64 v[178:181], v161 offset0:32 offset1:36
	ds_read2_b64 v[160:163], v163 offset0:64 offset1:68
	s_waitcnt lgkmcnt(0)
	v_mfma_f32_16x16x32_bf16 v[160:163], v[160:163], v[154:157], v[170:173]
	s_nop 2
	ds_read2_b64 v[170:173], v164 offset0:96 offset1:100
	v_exp_f32_e32 v67, v64
	v_fma_f32 v64, v68, s72, -v136
	v_mfma_f32_16x16x32_bf16 v[166:169], v[178:181], v[154:157], v[166:169]
	global_load_dwordx4 v[178:181], v[6:7], off offset:128
	global_load_dwordx4 v[182:185], v[8:9], off offset:128
	s_waitcnt vmcnt(3)
	ds_write_b128 v75, v[194:197]
	s_waitcnt vmcnt(2)
	ds_write_b128 v75, v[202:205] offset:9216
	s_waitcnt lgkmcnt(0)
	v_mfma_f32_16x16x32_bf16 v[154:157], v[170:173], v[154:157], v[174:177]
	s_barrier
	ds_read2_b64 v[170:173], v158 offset1:4
	v_exp_f32_e32 v68, v65
	v_fma_f32 v65, v69, s72, -v136
	v_mul_f32_e32 v62, 0x3fb8aa3b, v62
	v_mul_f32_e32 v63, 0x3fb8aa3b, v63
	v_mul_f32_e32 v64, 0x3fb8aa3b, v64
	v_mul_f32_e32 v65, 0x3fb8aa3b, v65
	v_exp_f32_e32 v62, v62
	v_exp_f32_e32 v63, v63
	v_exp_f32_e32 v64, v64
	v_exp_f32_e32 v65, v65
	v_cvt_pk_bf16_f32 v174, v149, v66
	v_cvt_pk_bf16_f32 v175, v67, v68
	v_cvt_pk_bf16_f32 v176, v62, v63
	v_cvt_pk_bf16_f32 v177, v64, v65
	v_add_u32_e32 v159, 0x800, v158
	v_add_u32_e32 v194, 0x1000, v158
	s_waitcnt lgkmcnt(0)
	v_mfma_f32_16x16x32_bf16 v[150:153], v[170:173], v[174:177], v[150:153]
	ds_read2_b64 v[170:173], v159 offset0:32 offset1:36
	v_add_u32_e32 v195, 0x1800, v158
	v_fma_f32 v58, v58, s72, -v136
	s_waitcnt lgkmcnt(0)
	v_mfma_f32_16x16x32_bf16 v[164:167], v[170:173], v[174:177], v[166:169]
	s_nop 2
	ds_read2_b64 v[168:171], v194 offset0:64 offset1:68
	v_fma_f32 v54, v54, s72, -v136
	v_fma_f32 v59, v59, s72, -v136
	s_waitcnt lgkmcnt(0)
	v_mfma_f32_16x16x32_bf16 v[160:163], v[168:171], v[174:177], v[160:163]
	ds_read2_b64 v[168:171], v195 offset0:96 offset1:100
	v_fma_f32 v55, v55, s72, -v136
	v_fma_f32 v60, v60, s72, -v136
	s_waitcnt lgkmcnt(0)
	v_mfma_f32_16x16x32_bf16 v[154:157], v[168:171], v[174:177], v[154:157]
	ds_read2_b64 v[168:171], v158 offset0:8 offset1:12
	v_fma_f32 v56, v56, s72, -v136
	v_fma_f32 v61, v61, s72, -v136
	v_fma_f32 v57, v57, s72, -v136
	v_mul_f32_e32 v58, 0x3fb8aa3b, v58
	v_mul_f32_e32 v54, 0x3fb8aa3b, v54
	v_mul_f32_e32 v59, 0x3fb8aa3b, v59
	v_mul_f32_e32 v55, 0x3fb8aa3b, v55
	v_mul_f32_e32 v60, 0x3fb8aa3b, v60
	v_mul_f32_e32 v56, 0x3fb8aa3b, v56
	v_mul_f32_e32 v61, 0x3fb8aa3b, v61
	v_mul_f32_e32 v57, 0x3fb8aa3b, v57
	v_exp_f32_e32 v58, v58
	v_exp_f32_e32 v54, v54
	v_exp_f32_e32 v59, v59
	v_exp_f32_e32 v55, v55
	v_exp_f32_e32 v60, v60
	v_exp_f32_e32 v56, v56
	v_exp_f32_e32 v61, v61
	v_exp_f32_e32 v57, v57
	v_cvt_pk_bf16_f32 v172, v58, v59
	v_cvt_pk_bf16_f32 v174, v54, v55
	v_cvt_pk_bf16_f32 v173, v60, v61
	v_cvt_pk_bf16_f32 v175, v56, v57
	v_fma_f32 v46, v46, s72, -v136
	v_fma_f32 v47, v47, s72, -v136
	s_waitcnt lgkmcnt(0)
	v_mfma_f32_16x16x32_bf16 v[150:153], v[168:171], v[172:175], v[150:153]
	ds_read2_b64 v[168:171], v159 offset0:40 offset1:44
	v_fma_f32 v48, v48, s72, -v136
	v_mul_f32_e32 v46, 0x3fb8aa3b, v46
	s_waitcnt lgkmcnt(0)
	v_mfma_f32_16x16x32_bf16 v[164:167], v[168:171], v[172:175], v[164:167]
	ds_read2_b64 v[168:171], v194 offset0:72 offset1:76
	v_mul_f32_e32 v47, 0x3fb8aa3b, v47
	v_mul_f32_e32 v48, 0x3fb8aa3b, v48
	s_waitcnt lgkmcnt(0)
	v_mfma_f32_16x16x32_bf16 v[160:163], v[168:171], v[172:175], v[160:163]
	ds_read2_b64 v[168:171], v195 offset0:104 offset1:108
	v_exp_f32_e32 v69, v46
	v_fma_f32 v46, v50, s72, -v136
	v_exp_f32_e32 v50, v47
	v_fma_f32 v47, v51, s72, -v136
	v_exp_f32_e32 v51, v48
	v_fma_f32 v48, v52, s72, -v136
	v_add_u32_e32 v52, 0x4800, v158
	global_load_dwordx4 v[186:189], v[6:7], off offset:256
	global_load_dwordx4 v[190:193], v[8:9], off offset:256
	s_waitcnt lgkmcnt(0)
	v_mfma_f32_16x16x32_bf16 v[154:157], v[168:171], v[172:175], v[154:157]
	s_waitcnt vmcnt(3)
	ds_write_b128 v75, v[178:181] offset:18432
	s_waitcnt vmcnt(2)
	ds_write_b128 v75, v[182:185] offset:27648
	s_waitcnt lgkmcnt(0)
	s_barrier
; #define LAS __attribute__((address_space(3)))
; __device__ __forceinline__ unsigned cvt_pk_bf16(float lo, float hi) { const float __attribute__((ext_vector_type(2))) v = {lo, hi}; return __builtin_bit_cast(unsigned, __builtin_convertvector(v, bf16x2_t)); }
; #define NA_STORE(sidx) do { LAS bf16* d_ = buf + ((sidx) & 1) * 9216; _Pragma("unroll") for (int q_ = 0; q_ < 2; ++q_) *(LAS v4u*)(d_ + q_ * 4608 + lrow * 72 + lseg * 8) = ld[(sidx) & 1][q_]; } while (0)
; template <bool LOCAL>
; __device__ __forceinline__ void na_unit(const bf16* P, const bf16* VT, bf16* YCAT, const LAS float* rpb_l, LAS bf16* buf, int b, int gr, int hp, int qblk, int tid) {
;     ...
;             } else {
;                 const int cc = c - NLOC;
; #pragma unroll
;                 for (int p2 = 0; p2 < 2; ++p2) {
;                     float p[8];
; #pragma unroll
;                     for (int e = 0; e < 4; ++e) { p[e] = __expf(sc[4 * (cc >= 0 ? cc : 0) + 2 * p2][e] - m); p[4 + e] = __expf(sc[4 * (cc >= 0 ? cc : 0) + 2 * p2 + 1][e] - m); }
; #pragma unroll
;                     for (int e = 0; e < 8; ++e) lsum += p[e];
;                     const bf16x8 pf = __builtin_bit_cast(bf16x8, (v4u){pg8::cvt_pk_bf16(p[0], p[1]), pg8::cvt_pk_bf16(p[2], p[3]), pg8::cvt_pk_bf16(p[4], p[5]), pg8::cvt_pk_bf16(p[6], p[7])});
; #pragma unroll
;                     for (int dt = 0; dt < 4; ++dt) { const LAS bf16* vp = cb + (16 * dt + fr) * 72 + 32 * p2 + 4 * fq;
;                         o[dt] = __builtin_amdgcn_mfma_f32_16x16x32_bf16(frag44(vp, vp + 16), pf, o[dt], 0, 0, 0); }
;                 }
;             }
;         }
;         if (sidx + 1 < 2 * NCH) NA_STORE(sidx + 1);
;         __syncthreads();
	v_fma_f32 v49, v49, s72, -v136
	ds_read2_b64 v[168:171], v52 offset1:4
	v_mul_f32_e32 v49, 0x3fb8aa3b, v49
	v_exp_f32_e32 v176, v49
	v_fma_f32 v49, v53, s72, -v136
	v_mul_f32_e32 v46, 0x3fb8aa3b, v46
	v_mul_f32_e32 v47, 0x3fb8aa3b, v47
	v_mul_f32_e32 v48, 0x3fb8aa3b, v48
	v_mul_f32_e32 v49, 0x3fb8aa3b, v49
	v_exp_f32_e32 v46, v46
	v_exp_f32_e32 v47, v47
	v_exp_f32_e32 v48, v48
	v_exp_f32_e32 v53, v49
	v_cvt_pk_bf16_f32 v172, v69, v50
	v_cvt_pk_bf16_f32 v173, v51, v176
	v_cvt_pk_bf16_f32 v174, v46, v47
	v_cvt_pk_bf16_f32 v175, v48, v53
	v_add_u32_e32 v177, 0x5000, v158
	v_add_u32_e32 v178, 0x5800, v158
	s_waitcnt lgkmcnt(0)
	v_mfma_f32_16x16x32_bf16 v[150:153], v[168:171], v[172:175], v[150:153]
	ds_read2_b64 v[168:171], v177 offset0:32 offset1:36
	v_add_u32_e32 v49, 0x6000, v158
	v_fma_f32 v38, v38, s72, -v136
	s_waitcnt lgkmcnt(0)
	v_mfma_f32_16x16x32_bf16 v[164:167], v[168:171], v[172:175], v[164:167]
	ds_read2_b64 v[168:171], v178 offset0:64 offset1:68
	v_mul_f32_e32 v38, 0x3fb8aa3b, v38
	v_fma_f32 v42, v42, s72, -v136
	s_waitcnt lgkmcnt(0)
	v_mfma_f32_16x16x32_bf16 v[160:163], v[168:171], v[172:175], v[160:163]
	ds_read2_b64 v[168:171], v49 offset0:96 offset1:100
	v_mul_f32_e32 v42, 0x3fb8aa3b, v42
	v_fma_f32 v30, v30, s72, -v136
	s_waitcnt lgkmcnt(0)
	v_mfma_f32_16x16x32_bf16 v[154:157], v[168:171], v[172:175], v[154:157]
	v_exp_f32_e32 v173, v38
	v_fma_f32 v38, v43, s72, -v136
	v_mul_f32_e32 v38, 0x3fb8aa3b, v38
	v_exp_f32_e32 v174, v38
	v_fma_f32 v38, v39, s72, -v136
	v_mul_f32_e32 v38, 0x3fb8aa3b, v38
	v_exp_f32_e32 v175, v38
	v_fma_f32 v38, v44, s72, -v136
	v_mul_f32_e32 v38, 0x3fb8aa3b, v38
	v_exp_f32_e32 v179, v38
	v_fma_f32 v38, v40, s72, -v136
	v_mul_f32_e32 v38, 0x3fb8aa3b, v38
	v_exp_f32_e32 v172, v42
	v_exp_f32_e32 v180, v38
	v_fma_f32 v38, v45, s72, -v136
	ds_read2_b64 v[42:45], v52 offset0:8 offset1:12
	v_mul_f32_e32 v38, 0x3fb8aa3b, v38
	v_exp_f32_e32 v181, v38
	v_fma_f32 v38, v41, s72, -v136
	v_mul_f32_e32 v38, 0x3fb8aa3b, v38
	v_exp_f32_e32 v182, v38
	v_cvt_pk_bf16_f32 v38, v172, v174
	v_cvt_pk_bf16_f32 v39, v179, v181
	v_cvt_pk_bf16_f32 v40, v173, v175
	v_cvt_pk_bf16_f32 v41, v180, v182
	v_mul_f32_e32 v30, 0x3fb8aa3b, v30
	v_fma_f32 v22, v22, s72, -v136
	s_waitcnt lgkmcnt(0)
	v_mfma_f32_16x16x32_bf16 v[42:45], v[42:45], v[38:41], v[150:153]
	v_mul_f32_e32 v22, 0x3fb8aa3b, v22
	v_fma_f32 v26, v26, s72, -v136
	v_mul_f32_e32 v26, 0x3fb8aa3b, v26
	ds_read2_b64 v[150:153], v177 offset0:40 offset1:44
	s_waitcnt lgkmcnt(0)
	v_mfma_f32_16x16x32_bf16 v[150:153], v[150:153], v[38:41], v[164:167]
	s_nop 2
	ds_read2_b64 v[164:167], v178 offset0:72 offset1:76
	v_fma_f32 v2, v2, s72, -v136
	v_mul_f32_e32 v2, 0x3fb8aa3b, v2
	s_waitcnt lgkmcnt(0)
	v_mfma_f32_16x16x32_bf16 v[160:163], v[164:167], v[38:41], v[160:163]
	ds_read2_b64 v[164:167], v49 offset0:104 offset1:108
	global_load_dwordx4 v[168:171], v[6:7], off offset:384
	s_nop 0
	global_load_dwordx4 v[6:9], v[8:9], off offset:384
	s_waitcnt vmcnt(3)
	ds_write_b128 v75, v[186:189]
	s_waitcnt vmcnt(2)
	ds_write_b128 v75, v[190:193] offset:9216
	s_waitcnt lgkmcnt(2)
	v_mfma_f32_16x16x32_bf16 v[38:41], v[164:167], v[38:41], v[154:157]
	v_exp_f32_e32 v164, v30
	v_fma_f32 v30, v34, s72, -v136
	v_mul_f32_e32 v30, 0x3fb8aa3b, v30
	v_exp_f32_e32 v165, v30
	v_fma_f32 v30, v31, s72, -v136
	v_mul_f32_e32 v30, 0x3fb8aa3b, v30
	v_exp_f32_e32 v166, v30
	v_fma_f32 v30, v35, s72, -v136
	v_mul_f32_e32 v30, 0x3fb8aa3b, v30
	v_exp_f32_e32 v167, v30
	v_fma_f32 v30, v32, s72, -v136
	v_mul_f32_e32 v30, 0x3fb8aa3b, v30
	v_exp_f32_e32 v183, v30
	v_fma_f32 v30, v36, s72, -v136
	v_mul_f32_e32 v30, 0x3fb8aa3b, v30
	v_exp_f32_e32 v184, v30
	v_fma_f32 v30, v33, s72, -v136
	s_waitcnt lgkmcnt(0)
	s_barrier
	v_mul_f32_e32 v34, 0x3fb8aa3b, v30
	ds_read2_b64 v[30:33], v158 offset1:4
	v_exp_f32_e32 v185, v34
	v_fma_f32 v34, v37, s72, -v136
	v_mul_f32_e32 v34, 0x3fb8aa3b, v34
	v_exp_f32_e32 v186, v34
	v_cvt_pk_bf16_f32 v34, v164, v166
	v_cvt_pk_bf16_f32 v35, v183, v185
	v_cvt_pk_bf16_f32 v36, v165, v167
	v_cvt_pk_bf16_f32 v37, v184, v186
	ds_read2_b64 v[154:157], v195 offset0:96 offset1:100
	v_fma_f32 v10, v10, s72, -v136
	s_waitcnt lgkmcnt(1)
	v_mfma_f32_16x16x32_bf16 v[30:33], v[30:33], v[34:37], v[42:45]
	v_mul_f32_e32 v10, 0x3fb8aa3b, v10
	s_nop 1
	ds_read2_b64 v[42:45], v159 offset0:32 offset1:36
	s_waitcnt lgkmcnt(0)
	v_mfma_f32_16x16x32_bf16 v[42:45], v[42:45], v[34:37], v[150:153]
	s_nop 2
	ds_read2_b64 v[150:153], v194 offset0:64 offset1:68
	s_waitcnt lgkmcnt(0)
	v_mfma_f32_16x16x32_bf16 v[150:153], v[150:153], v[34:37], v[160:163]
	v_mfma_f32_16x16x32_bf16 v[34:37], v[154:157], v[34:37], v[38:41]
	v_exp_f32_e32 v155, v22
	v_fma_f32 v22, v27, s72, -v136
	v_mul_f32_e32 v22, 0x3fb8aa3b, v22
	v_exp_f32_e32 v156, v22
	v_fma_f32 v22, v23, s72, -v136
	v_mul_f32_e32 v22, 0x3fb8aa3b, v22
	v_exp_f32_e32 v157, v22
	v_fma_f32 v22, v28, s72, -v136
	v_mul_f32_e32 v22, 0x3fb8aa3b, v22
	v_exp_f32_e32 v160, v22
	v_fma_f32 v22, v24, s72, -v136
	v_mul_f32_e32 v22, 0x3fb8aa3b, v22
	v_exp_f32_e32 v154, v26
	v_exp_f32_e32 v161, v22
	v_fma_f32 v22, v29, s72, -v136
	ds_read2_b64 v[26:29], v158 offset0:8 offset1:12
	v_mul_f32_e32 v22, 0x3fb8aa3b, v22
	v_exp_f32_e32 v158, v22
	v_fma_f32 v22, v25, s72, -v136
	v_mul_f32_e32 v22, 0x3fb8aa3b, v22
	v_exp_f32_e32 v162, v22
	v_cvt_pk_bf16_f32 v22, v154, v156
	v_cvt_pk_bf16_f32 v23, v160, v158
	v_cvt_pk_bf16_f32 v24, v155, v157
	v_cvt_pk_bf16_f32 v25, v161, v162
	ds_read2_b64 v[38:41], v194 offset0:72 offset1:76
	s_waitcnt lgkmcnt(1)
	v_mfma_f32_16x16x32_bf16 v[26:29], v[26:29], v[22:25], v[30:33]
	s_nop 2
	ds_read2_b64 v[30:33], v159 offset0:40 offset1:44
	s_waitcnt lgkmcnt(0)
	v_mfma_f32_16x16x32_bf16 v[30:33], v[30:33], v[22:25], v[42:45]
	s_nop 2
	ds_read2_b64 v[42:45], v195 offset0:104 offset1:108
	s_waitcnt vmcnt(1)
	ds_write_b128 v75, v[168:171] offset:18432
	s_waitcnt vmcnt(0)
	ds_write_b128 v75, v[6:9] offset:27648
	v_fma_f32 v6, v14, s72, -v136
	v_mul_f32_e32 v6, 0x3fb8aa3b, v6
	v_mfma_f32_16x16x32_bf16 v[38:41], v[38:41], v[22:25], v[150:153]
	s_waitcnt lgkmcnt(0)
	s_barrier
; #define LAS __attribute__((address_space(3)))
; __device__ __forceinline__ unsigned cvt_pk_bf16(float lo, float hi) { const float __attribute__((ext_vector_type(2))) v = {lo, hi}; return __builtin_bit_cast(unsigned, __builtin_convertvector(v, bf16x2_t)); }
; #define NA_STORE(sidx) do { LAS bf16* d_ = buf + ((sidx) & 1) * 9216; _Pragma("unroll") for (int q_ = 0; q_ < 2; ++q_) *(LAS v4u*)(d_ + q_ * 4608 + lrow * 72 + lseg * 8) = ld[(sidx) & 1][q_]; } while (0)
; template <bool LOCAL>
; __device__ __forceinline__ void na_unit(const bf16* P, const bf16* VT, bf16* YCAT, const LAS float* rpb_l, LAS bf16* buf, int b, int gr, int hp, int qblk, int tid) {
;     ...
;             } else {
;                 const int cc = c - NLOC;
; #pragma unroll
;                 for (int p2 = 0; p2 < 2; ++p2) {
;                     float p[8];
; #pragma unroll
;                     for (int e = 0; e < 4; ++e) { p[e] = __expf(sc[4 * (cc >= 0 ? cc : 0) + 2 * p2][e] - m); p[4 + e] = __expf(sc[4 * (cc >= 0 ? cc : 0) + 2 * p2 + 1][e] - m); }
; #pragma unroll
;                     for (int e = 0; e < 8; ++e) lsum += p[e];
;                     const bf16x8 pf = __builtin_bit_cast(bf16x8, (v4u){pg8::cvt_pk_bf16(p[0], p[1]), pg8::cvt_pk_bf16(p[2], p[3]), pg8::cvt_pk_bf16(p[4], p[5]), pg8::cvt_pk_bf16(p[6], p[7])});
; #pragma unroll
;                     for (int dt = 0; dt < 4; ++dt) { const LAS bf16* vp = cb + (16 * dt + fr) * 72 + 32 * p2 + 4 * fq;
;                         o[dt] = __builtin_amdgcn_mfma_f32_16x16x32_bf16(frag44(vp, vp + 16), pf, o[dt], 0, 0, 0); }
;                 }
;             }
;         }
;         if (sidx + 1 < 2 * NCH) NA_STORE(sidx + 1);
;         __syncthreads();
;     }
;     ...
;     lsum += __shfl_xor(lsum, 16); lsum += __shfl_xor(lsum, 32);
	v_mfma_f32_16x16x32_bf16 v[22:25], v[42:45], v[22:25], v[34:37]
	v_ashrrev_i32_e32 v75, 31, v74
	s_nop 1
	v_exp_f32_e32 v34, v6
	v_fma_f32 v6, v18, s72, -v136
	v_mul_f32_e32 v6, 0x3fb8aa3b, v6
	v_exp_f32_e32 v35, v6
	v_fma_f32 v6, v15, s72, -v136
	v_mul_f32_e32 v6, 0x3fb8aa3b, v6
	v_exp_f32_e32 v36, v6
	v_fma_f32 v6, v19, s72, -v136
	v_mul_f32_e32 v6, 0x3fb8aa3b, v6
	v_exp_f32_e32 v37, v6
	v_fma_f32 v6, v16, s72, -v136
	v_mul_f32_e32 v6, 0x3fb8aa3b, v6
	v_exp_f32_e32 v42, v6
	v_fma_f32 v6, v20, s72, -v136
	v_mul_f32_e32 v6, 0x3fb8aa3b, v6
	v_exp_f32_e32 v43, v6
	v_fma_f32 v6, v17, s72, -v136
	v_mul_f32_e32 v14, 0x3fb8aa3b, v6
	ds_read2_b64 v[6:9], v52 offset1:4
	v_exp_f32_e32 v44, v14
	v_fma_f32 v14, v21, s72, -v136
	v_mul_f32_e32 v14, 0x3fb8aa3b, v14
	v_exp_f32_e32 v45, v14
	v_cvt_pk_bf16_f32 v14, v34, v36
	v_cvt_pk_bf16_f32 v15, v42, v44
	v_cvt_pk_bf16_f32 v16, v35, v37
	v_cvt_pk_bf16_f32 v17, v43, v45
	ds_read2_b64 v[18:21], v177 offset0:32 offset1:36
	s_waitcnt lgkmcnt(1)
	v_mfma_f32_16x16x32_bf16 v[6:9], v[6:9], v[14:17], v[26:29]
	s_nop 2
	ds_read2_b64 v[26:29], v178 offset0:64 offset1:68
	s_waitcnt lgkmcnt(0)
	v_mfma_f32_16x16x32_bf16 v[26:29], v[26:29], v[14:17], v[38:41]
	s_nop 2
	v_add_f32_e32 v38, 0, v132
	v_add_f32_e32 v38, v96, v38
	v_add_f32_e32 v38, v95, v38
	v_add_f32_e32 v38, v99, v38
	v_add_f32_e32 v38, v92, v38
	v_add_f32_e32 v38, v91, v38
	v_add_f32_e32 v38, v94, v38
	v_add_f32_e32 v38, v93, v38
	v_add_f32_e32 v38, v86, v38
	v_add_f32_e32 v38, v90, v38
	v_add_f32_e32 v38, v98, v38
	v_add_f32_e32 v38, v100, v38
	v_add_f32_e32 v38, v76, v38
	v_add_f32_e32 v38, v87, v38
	v_add_f32_e32 v38, v97, v38
	v_add_f32_e32 v38, v101, v38
	v_add_f32_e32 v38, v103, v38
	v_add_f32_e32 v38, v105, v38
	v_add_f32_e32 v38, v107, v38
	v_add_f32_e32 v38, v108, v38
	v_add_f32_e32 v38, v102, v38
	v_add_f32_e32 v38, v104, v38
	v_add_f32_e32 v38, v106, v38
	v_add_f32_e32 v38, v109, v38
	v_add_f32_e32 v38, v111, v38
	v_add_f32_e32 v38, v113, v38
	v_add_f32_e32 v38, v115, v38
	v_add_f32_e32 v38, v116, v38
	v_add_f32_e32 v38, v110, v38
	v_add_f32_e32 v38, v112, v38
	v_add_f32_e32 v38, v114, v38
	v_add_f32_e32 v38, v117, v38
	v_add_f32_e32 v38, v119, v38
	v_add_f32_e32 v38, v121, v38
	v_add_f32_e32 v38, v123, v38
	v_add_f32_e32 v38, v124, v38
	v_add_f32_e32 v38, v118, v38
	v_add_f32_e32 v38, v120, v38
	v_add_f32_e32 v38, v122, v38
	v_add_f32_e32 v38, v125, v38
	v_add_f32_e32 v38, v127, v38
	v_add_f32_e32 v38, v129, v38
	v_add_f32_e32 v38, v131, v38
	v_add_f32_e32 v38, v133, v38
	v_add_f32_e32 v38, v126, v38
	v_add_f32_e32 v38, v128, v38
	v_add_f32_e32 v38, v130, v38
	v_add_f32_e32 v38, v134, v38
	v_add_f32_e32 v38, v137, v38
	v_add_f32_e32 v38, v139, v38
	v_add_f32_e32 v38, v141, v38
	v_add_f32_e32 v38, v142, v38
	v_add_f32_e32 v38, v135, v38
	v_add_f32_e32 v38, v138, v38
	v_add_f32_e32 v38, v140, v38
	v_add_f32_e32 v38, v143, v38
	v_add_f32_e32 v38, v78, v38
	v_add_f32_e32 v38, v80, v38
	v_add_f32_e32 v38, v144, v38
	v_add_f32_e32 v38, v148, v38
	v_add_f32_e32 v38, v70, v38
	v_add_f32_e32 v38, v79, v38
	v_add_f32_e32 v38, v81, v38
	v_add_f32_e32 v38, v145, v38
	v_add_f32_e32 v38, v149, v38
	v_add_f32_e32 v38, v66, v38
	v_add_f32_e32 v38, v67, v38
	v_add_f32_e32 v38, v68, v38
	v_add_f32_e32 v38, v62, v38
	v_add_f32_e32 v38, v63, v38
	v_add_f32_e32 v38, v64, v38
	v_add_f32_e32 v38, v65, v38
	v_add_f32_e32 v38, v58, v38
	v_add_f32_e32 v38, v59, v38
	v_add_f32_e32 v38, v60, v38
	v_add_f32_e32 v38, v61, v38
	v_add_f32_e32 v38, v54, v38
	v_add_f32_e32 v38, v55, v38
	v_add_f32_e32 v38, v56, v38
	v_add_f32_e32 v38, v57, v38
	v_add_f32_e32 v38, v69, v38
	v_add_f32_e32 v38, v50, v38
	v_add_f32_e32 v38, v51, v38
	v_add_f32_e32 v38, v176, v38
	v_add_f32_e32 v38, v46, v38
	v_add_f32_e32 v38, v47, v38
	v_add_f32_e32 v38, v48, v38
	v_add_f32_e32 v38, v53, v38
	v_add_f32_e32 v38, v172, v38
	v_mfma_f32_16x16x32_bf16 v[18:21], v[18:21], v[14:17], v[30:33]
	v_add_f32_e32 v38, v174, v38
	v_add_f32_e32 v38, v179, v38
	v_add_f32_e32 v38, v181, v38
	ds_read2_b64 v[30:33], v49 offset0:96 offset1:100
	v_add_f32_e32 v38, v173, v38
	v_add_f32_e32 v38, v175, v38
	v_add_f32_e32 v38, v180, v38
	v_add_f32_e32 v38, v182, v38
	v_add_f32_e32 v38, v164, v38
	v_add_f32_e32 v38, v166, v38
	s_waitcnt lgkmcnt(0)
	v_mfma_f32_16x16x32_bf16 v[14:17], v[30:33], v[14:17], v[22:25]
	v_add_f32_e32 v38, v183, v38
	s_nop 1
	v_exp_f32_e32 v23, v2
	v_fma_f32 v2, v11, s72, -v136
	v_mul_f32_e32 v2, 0x3fb8aa3b, v2
	v_add_f32_e32 v38, v185, v38
	v_exp_f32_e32 v24, v2
	v_fma_f32 v2, v3, s72, -v136
	v_add_f32_e32 v38, v165, v38
	v_mul_f32_e32 v2, 0x3fb8aa3b, v2
	v_add_f32_e32 v38, v167, v38
	v_exp_f32_e32 v25, v2
	v_fma_f32 v2, v12, s72, -v136
	v_add_f32_e32 v38, v184, v38
	v_mul_f32_e32 v2, 0x3fb8aa3b, v2
	v_add_f32_e32 v38, v186, v38
	v_exp_f32_e32 v30, v2
	v_fma_f32 v2, v4, s72, -v136
	v_add_f32_e32 v38, v154, v38
	v_mul_f32_e32 v2, 0x3fb8aa3b, v2
	v_add_f32_e32 v38, v156, v38
	v_exp_f32_e32 v22, v10
	v_exp_f32_e32 v31, v2
	v_fma_f32 v2, v13, s72, -v136
	ds_read2_b64 v[10:13], v52 offset0:8 offset1:12
	v_add_f32_e32 v38, v160, v38
	v_mul_f32_e32 v2, 0x3fb8aa3b, v2
	v_add_f32_e32 v38, v158, v38
	v_exp_f32_e32 v32, v2
	v_fma_f32 v2, v5, s72, -v136
	v_add_f32_e32 v38, v155, v38
	v_mul_f32_e32 v2, 0x3fb8aa3b, v2
	v_add_f32_e32 v38, v157, v38
	v_exp_f32_e32 v33, v2
	v_add_f32_e32 v38, v161, v38
	v_add_f32_e32 v38, v162, v38
	v_add_f32_e32 v34, v34, v38
	v_add_f32_e32 v34, v36, v34
	v_cvt_pk_bf16_f32 v2, v22, v24
	v_cvt_pk_bf16_f32 v3, v30, v32
	v_cvt_pk_bf16_f32 v4, v23, v25
	v_cvt_pk_bf16_f32 v5, v31, v33
	v_add_f32_e32 v34, v42, v34
	v_add_f32_e32 v34, v44, v34
	s_waitcnt lgkmcnt(0)
	v_mfma_f32_16x16x32_bf16 v[6:9], v[10:13], v[2:5], v[6:9]
	ds_read2_b64 v[10:13], v177 offset0:40 offset1:44
	v_add_f32_e32 v34, v35, v34
	v_add_f32_e32 v34, v37, v34
	v_add_f32_e32 v34, v43, v34
	v_add_f32_e32 v34, v45, v34
	v_add_f32_e32 v22, v22, v34
	v_add_f32_e32 v22, v24, v22
	v_add_f32_e32 v22, v30, v22
	v_add_f32_e32 v22, v32, v22
	s_waitcnt lgkmcnt(0)
	v_mfma_f32_16x16x32_bf16 v[10:13], v[10:13], v[2:5], v[18:21]
	v_add_f32_e32 v22, v23, v22
	v_add_f32_e32 v22, v25, v22
	v_add_f32_e32 v22, v31, v22
	ds_read2_b64 v[18:21], v178 offset0:72 offset1:76
	v_add_f32_e32 v30, v33, v22
	ds_bpermute_b32 v31, v88, v30
	ds_read2_b64 v[22:25], v49 offset0:104 offset1:108
	s_waitcnt lgkmcnt(2)
	v_mfma_f32_16x16x32_bf16 v[18:21], v[18:21], v[2:5], v[26:29]
	s_waitcnt lgkmcnt(1)
	s_nop 1
	v_add_f32_e32 v26, v30, v31
	ds_bpermute_b32 v27, v89, v26
	v_lshlrev_b32_e32 v70, 1, v77
	s_waitcnt lgkmcnt(1)
	v_mfma_f32_16x16x32_bf16 v[14:17], v[22:25], v[2:5], v[14:17]
	s_waitcnt lgkmcnt(0)
	s_barrier
; __device__ __forceinline__ unsigned cvt_pk_bf16(float lo, float hi) { const float __attribute__((ext_vector_type(2))) v = {lo, hi}; return __builtin_bit_cast(unsigned, __builtin_convertvector(v, bf16x2_t)); }
; template <bool LOCAL>
; __device__ __forceinline__ void na_unit(const bf16* P, const bf16* VT, bf16* YCAT, const LAS float* rpb_l, LAS bf16* buf, int b, int gr, int hp, int qblk, int tid) {
;     ...
;     lsum += __shfl_xor(lsum, 16); lsum += __shfl_xor(lsum, 32);
;     const float inv = 1.f / lsum;
;     bf16* op = YCAT + (size_t)(qrow0 + fr) * D + 512 + h * 64 + 4 * fq;
; #pragma unroll
;     for (int dt = 0; dt < 4; ++dt) { v2u w; w.x = pg8::cvt_pk_bf16(o[dt][0] * inv, o[dt][1] * inv); w.y = pg8::cvt_pk_bf16(o[dt][2] * inv, o[dt][3] * inv); *(v2u*)(op + dt * 16) = w; }
	v_add_f32_e32 v2, v26, v27
	v_div_scale_f32 v3, s[0:1], v2, v2, 1.0
	v_rcp_f32_e32 v4, v3
	s_nop 0
	v_fma_f32 v5, -v3, v4, 1.0
	v_fmac_f32_e32 v4, v5, v4
	v_div_scale_f32 v5, vcc, 1.0, v2, 1.0
	v_mul_f32_e32 v22, v5, v4
	v_fma_f32 v23, -v3, v22, v5
	v_fmac_f32_e32 v22, v23, v4
	v_fma_f32 v3, -v3, v22, v5
	v_div_fmas_f32 v3, v3, v4, v22
	v_div_fixup_f32 v22, v3, v2, 1.0
	v_lshlrev_b64 v[2:3], 11, v[74:75]
	v_lshl_add_u64 v[2:3], s[10:11], 0, v[2:3]
	v_lshl_add_u64 v[2:3], v[72:73], 1, v[2:3]
	v_pk_mul_f32 v[6:7], v[6:7], v[22:23] op_sel_hi:[1,0]
	v_pk_mul_f32 v[8:9], v[8:9], v[22:23] op_sel_hi:[1,0]
	v_lshl_add_u64 v[4:5], v[2:3], 0, v[70:71]
	v_cvt_pk_bf16_f32 v6, v6, v7
	v_cvt_pk_bf16_f32 v7, v8, v9
	global_store_dwordx2 v[4:5], v[6:7], off offset:1024
	v_pk_mul_f32 v[6:7], v[10:11], v[22:23] op_sel_hi:[1,0]
	v_pk_mul_f32 v[8:9], v[12:13], v[22:23] op_sel_hi:[1,0]
	v_cvt_pk_bf16_f32 v6, v6, v7
	v_cvt_pk_bf16_f32 v7, v8, v9
	global_store_dwordx2 v[4:5], v[6:7], off offset:1056
	v_pk_mul_f32 v[6:7], v[18:19], v[22:23] op_sel_hi:[1,0]
	v_pk_mul_f32 v[8:9], v[20:21], v[22:23] op_sel_hi:[1,0]
	v_cvt_pk_bf16_f32 v6, v6, v7
	v_cvt_pk_bf16_f32 v7, v8, v9
	v_lshl_add_u64 v[2:3], v[4:5], 0, s[12:13]
	global_store_dwordx2 v[4:5], v[6:7], off offset:1088
	v_pk_mul_f32 v[4:5], v[14:15], v[22:23] op_sel_hi:[1,0]
	v_pk_mul_f32 v[6:7], v[16:17], v[22:23] op_sel_hi:[1,0]
	v_cvt_pk_bf16_f32 v4, v4, v5

; #define LAS __attribute__((address_space(3)))
; template <bool LOCAL>
; __device__ __forceinline__ void na_unit(const bf16* P, const bf16* VT, bf16* YCAT, const LAS float* rpb_l, LAS bf16* buf, int b, int gr, int hp, int qblk, int tid) {
;     ...
;     const int lane = tid & 63, wv = tid >> 6, fr = lane & 15, fq = lane >> 4, hh = wv >> 2, qb = wv & 3, h = 2 * hp + hh;
;     const int qrow0 = LOCAL ? NCTX + b * SEQ + gr * 64 + 16 * qb : b * CTXL + qblk * 64 + 16 * qb;
;     const int r0 = min(max(gr - 4, 0), 24);
;     const int kc0 = qb == 0 ? 0 : qb == 1 ? 8 : qb == 2 ? 24 : 32;
;     const int qcol = 16 * qb + fr, cs = min(max(qcol - 8, 0), 48);
;     const LAS float* rpb = rpb_l + h * 15 * 31;
;     v4u ld[2][2];
;     const int lrow = (tid >> 3) & 63, lseg = tid & 7;
;     ...
;     bf16x8 qf[2];
; #pragma unroll
;     for (int ks = 0; ks < 2; ++ks) qf[ks] = *(const bf16x8*)(P + (size_t)(qrow0 + fr) * DINP + h * 64 + 32 * ks + 8 * fq);
;     f32x4 sl[16], sc[16];
;     float m = -1.0e30f, lsum = 0.f;
;     f32x4 o[4];
; #pragma unroll
;     for (int dt = 0; dt < 4; ++dt) o[dt] = (f32x4){0.f, 0.f, 0.f, 0.f};
;     NA_ISSUE(0); NA_ISSUE(1); NA_STORE(0);
;     __syncthreads();
; #pragma unroll
;     for (int sidx = 0; sidx < 2 * NCH; ++sidx) {
;         if (sidx + 2 < 2 * NCH) NA_ISSUE(sidx + 2);
;         const LAS bf16* cb = buf + (sidx & 1) * 9216 + hh * 4608;
;         if (sidx < NCH) {
;             const int c = sidx;
;             if (LOCAL && c < 8) {
; #pragma unroll
;                 for (int t2 = 0; t2 < 2; ++t2) {
;                     const LAS bf16* kp = cb + (kc0 + 16 * t2 + fr) * 72 + 8 * fq;
;                     f32x4 acc = {0.f, 0.f, 0.f, 0.f};
;                     acc = __builtin_amdgcn_mfma_f32_16x16x32_bf16(*(const LAS bf16x8*)(kp), qf[0], acc, 0, 0, 0);
;                     acc = __builtin_amdgcn_mfma_f32_16x16x32_bf16(*(const LAS bf16x8*)(kp + 32), qf[1], acc, 0, 0, 0);
;                     const LAS float* rb = rpb + (r0 + c - gr + 7) * 31 + 15 - qcol;
; #pragma unroll
;                     for (int e = 0; e < 4; ++e) { const int kcol = kc0 + 16 * t2 + 4 * fq + e; const bool ok = (kcol >= cs) && (kcol < cs + 16);
;                         const float sv = ok ? acc[e] * 0.125f + rb[ok ? kcol : qcol] : -1.0e30f; acc[e] = sv; m = fmaxf(m, sv); }
;                     sl[2 * (c < 8 ? c : 0) + t2] = acc; }
.LBB0_1507:
	s_or_b64 exec, exec, s[0:1]
	s_bfe_u32 s19, s76, 0x50002
	v_sub_u32_e64 v3, s19, 4 clamp
	s_ashr_i32 s17, s76, 7
	v_readfirstlane_b32 s0, v3
	s_lshl_b32 s26, s17, 11
	s_min_u32 s20, s0, 24
	s_add_i32 s14, s26, 0x1000
	s_lshl_b32 s15, s20, 6
	s_or_b32 s16, s15, s14
	v_mov_b64_e32 v[18:19], s[8:9]
	v_and_b32_e32 v32, 7, v93
	v_or_b32_e32 v3, s16, v88
	s_and_b32 s18, s76, 3
	v_mad_i64_i32 v[4:5], s[0:1], v3, s69, v[18:19]
	v_lshlrev_b32_e32 v26, 4, v32
	v_mov_b32_e32 v27, v71
	v_lshl_add_u64 v[4:5], v[4:5], 0, v[26:27]
	s_lshl_b32 s2, s18, 8
	v_lshl_add_u64 v[4:5], v[4:5], 0, s[2:3]
	global_load_dwordx4 v[10:13], v[4:5], off offset:1024
	global_load_dwordx4 v[14:17], v[4:5], off offset:1152
	s_lshl_b32 s0, s19, 6
	v_lshl_or_b32 v31, v2, 4, v89
	v_lshl_add_u32 v33, s18, 1, v92
	s_or_b32 s0, s14, s0
	v_mad_u32_u24 v2, v88, s70, 0
	v_lshlrev_b32_e32 v72, 6, v33
	s_add_i32 s50, s26, 0x1040
	v_or_b32_e32 v74, s0, v31
	v_add_u32_e32 v75, v2, v26
	v_ashrrev_i32_e32 v73, 31, v72
	v_or_b32_e32 v4, s50, v88
	v_mad_i64_i32 v[2:3], s[0:1], v74, s69, v[18:19]
	v_add_u32_e32 v4, s15, v4
	v_lshl_add_u64 v[2:3], v[72:73], 1, v[2:3]
	v_mad_i64_i32 v[4:5], s[0:1], v4, s69, v[18:19]
	v_lshl_add_u64 v[2:3], v[2:3], 0, v[70:71]
	v_lshl_add_u64 v[20:21], v[4:5], 0, v[26:27]
	global_load_dwordx4 v[6:9], v[2:3], off
	s_nop 0
	global_load_dwordx4 v[2:5], v[2:3], off offset:64
	s_or_b32 s14, s26, s15
	s_addk_i32 s14, 0x1080
	v_or_b32_e32 v24, s14, v88
	v_mad_i64_i32 v[28:29], s[0:1], v24, s69, v[18:19]
	v_lshl_add_u64 v[26:27], v[28:29], 0, v[26:27]
	v_lshl_add_u64 v[22:23], v[20:21], 0, s[2:3]
	v_lshl_add_u64 v[26:27], v[26:27], 0, s[2:3]
	global_load_dwordx4 v[18:21], v[22:23], off offset:1024
	s_nop 0
	global_load_dwordx4 v[22:25], v[22:23], off offset:1152
	v_add_u32_e32 v30, v86, v70
	v_add_u32_e32 v34, v90, v89
	v_mad_u32_u24 v36, v34, s70, v30
	s_movk_i32 s0, 0x744
	v_mul_lo_u32 v33, v33, s0
	s_sub_i32 s0, s20, s19
	s_mulk_i32 s0, 0x7c
	v_sub_u32_e64 v35, v31, 8 clamp
	s_add_i32 s0, s0, 0
	v_min_u32_e32 v35, 48, v35
	v_lshlrev_b32_e32 v77, 2, v91
	v_add_u32_e32 v33, s0, v33
	v_lshlrev_b32_e32 v31, 2, v31
	v_sub_u32_e32 v31, v33, v31
	v_add_u32_e32 v33, v90, v77
	v_cmp_ge_u32_e32 vcc, v33, v35
	v_mov_b32_e32 v91, 0xf149f2ca
	v_lshl_add_u32 v31, v33, 2, v31
	v_mov_b32_e32 v92, 0xf149f2ca
	s_waitcnt vmcnt(5)
	ds_write_b128 v75, v[10:13]
	s_waitcnt vmcnt(4)
	ds_write_b128 v75, v[14:17] offset:9216
	s_waitcnt lgkmcnt(0)
	s_barrier
	ds_read_b32 v240, v31 offset:37792
	ds_read_b32 v241, v31 offset:37796
	ds_read_b32 v242, v31 offset:37800
	ds_read_b32 v243, v31 offset:37804
	ds_read_b32 v244, v31 offset:37856
	ds_read_b32 v245, v31 offset:37860
	ds_read_b32 v246, v31 offset:37864
	ds_read_b32 v247, v31 offset:37868
	global_load_dwordx4 v[10:13], v[26:27], off offset:1024
	global_load_dwordx4 v[14:17], v[26:27], off offset:1152
	ds_read_b128 v[26:29], v36
	ds_read_b128 v[38:41], v36 offset:64
	s_waitcnt vmcnt(5) lgkmcnt(1)
	v_mfma_f32_16x16x32_bf16 v[26:29], v[26:29], v[6:9], 0
	v_add_u32_e32 v36, 16, v35
	v_cmp_lt_u32_e64 s[0:1], v33, v36
	s_and_b64 s[28:29], vcc, s[0:1]
	s_waitcnt vmcnt(4) lgkmcnt(0)
	v_mfma_f32_16x16x32_bf16 v[26:29], v[38:41], v[2:5], v[26:29]
	s_nop 2
	s_waitcnt lgkmcnt(0)
	s_nop 3
	v_fmac_f32_e32 v240, 0x3e000000, v26
	v_cndmask_b32_e64 v92, v92, v240, s[28:29]
	s_nop 4
	v_or_b32_e32 v26, 1, v33
	v_cmp_ge_u32_e32 vcc, v26, v35
	v_cmp_lt_u32_e64 s[0:1], v26, v36
	s_and_b64 s[30:31], vcc, s[0:1]
	s_nop 2
	s_waitcnt lgkmcnt(0)
	v_fmac_f32_e32 v241, 0x3e000000, v27
	v_cndmask_b32_e64 v91, v91, v241, s[30:31]
	v_or_b32_e32 v26, 2, v33
	v_cmp_ge_u32_e32 vcc, v26, v35
	v_cmp_lt_u32_e64 s[0:1], v26, v36
	s_and_b64 s[34:35], vcc, s[0:1]
	v_mov_b32_e32 v93, 0xf149f2ca
	v_mov_b32_e32 v94, 0xf149f2ca
	s_nop 2
	s_waitcnt lgkmcnt(0)
	v_fmac_f32_e32 v242, 0x3e000000, v28
	v_cndmask_b32_e64 v94, v94, v242, s[34:35]
	v_or_b32_e32 v26, 3, v33
	v_cmp_ge_u32_e32 vcc, v26, v35
	v_cmp_lt_u32_e64 s[0:1], v26, v36
	s_and_b64 s[36:37], vcc, s[0:1]
	s_nop 2
	s_waitcnt lgkmcnt(0)
	v_fmac_f32_e32 v243, 0x3e000000, v29
	v_cndmask_b32_e64 v93, v93, v243, s[36:37]
	v_add_u32_e32 v37, 16, v90
	v_add_u32_e32 v33, v37, v89
	v_mad_u32_u24 v38, v33, s70, v30
	ds_read_b128 v[26:29], v38
	ds_read_b128 v[38:41], v38 offset:64
	v_add_u32_e32 v37, v37, v77
	v_cmp_ge_u32_e32 vcc, v37, v35
	v_cmp_lt_u32_e64 s[0:1], v37, v36
	s_waitcnt lgkmcnt(1)
	v_mfma_f32_16x16x32_bf16 v[26:29], v[26:29], v[6:9], 0
	s_and_b64 s[38:39], vcc, s[0:1]
	v_mov_b32_e32 v95, 0xf149f2ca
	v_mov_b32_e32 v96, 0xf149f2ca
	s_waitcnt lgkmcnt(0)
	v_mfma_f32_16x16x32_bf16 v[26:29], v[38:41], v[2:5], v[26:29]
	s_nop 2
	s_waitcnt lgkmcnt(0)
	s_nop 3
	v_fmac_f32_e32 v244, 0x3e000000, v26
	v_cndmask_b32_e64 v96, v96, v244, s[38:39]
	s_nop 4
	v_or_b32_e32 v26, 1, v37
	v_cmp_ge_u32_e32 vcc, v26, v35
	v_cmp_lt_u32_e64 s[0:1], v26, v36
	s_and_b64 s[44:45], vcc, s[0:1]
	s_nop 2
	s_waitcnt lgkmcnt(0)
	v_fmac_f32_e32 v245, 0x3e000000, v27
	v_cndmask_b32_e64 v95, v95, v245, s[44:45]
	v_or_b32_e32 v26, 2, v37
	v_cmp_ge_u32_e32 vcc, v26, v35
	v_cmp_lt_u32_e64 s[0:1], v26, v36
	s_and_b64 s[46:47], vcc, s[0:1]
	v_mov_b32_e32 v97, 0xf149f2ca
	v_mov_b32_e32 v99, 0xf149f2ca
	s_nop 2
	s_waitcnt lgkmcnt(0)
	v_fmac_f32_e32 v246, 0x3e000000, v28
	v_cndmask_b32_e64 v99, v99, v246, s[46:47]
	v_or_b32_e32 v26, 3, v37
	v_cmp_ge_u32_e32 vcc, v26, v35
	v_cmp_lt_u32_e64 s[0:1], v26, v36
	s_and_b64 s[48:49], vcc, s[0:1]
	s_nop 2
	s_waitcnt lgkmcnt(0)
	v_fmac_f32_e32 v247, 0x3e000000, v29
	v_cndmask_b32_e64 v97, v97, v247, s[48:49]
	v_mul_u32_u24_e32 v27, 0x90, v34
	v_lshlrev_b32_e32 v26, 3, v32
	v_add_u32_e32 v32, v30, v27
	s_waitcnt vmcnt(3)
	ds_write_b128 v75, v[18:21] offset:18432
	s_waitcnt vmcnt(2)
	ds_write_b128 v75, v[22:25] offset:27648
	s_waitcnt lgkmcnt(0)
	s_barrier
; #define LAS __attribute__((address_space(3)))
; template <bool LOCAL>
; __device__ __forceinline__ void na_unit(const bf16* P, const bf16* VT, bf16* YCAT, const LAS float* rpb_l, LAS bf16* buf, int b, int gr, int hp, int qblk, int tid) {
;     ...
;     for (int sidx = 0; sidx < 2 * NCH; ++sidx) {
;         if (sidx + 2 < 2 * NCH) NA_ISSUE(sidx + 2);
;         const LAS bf16* cb = buf + (sidx & 1) * 9216 + hh * 4608;
;         if (sidx < NCH) {
;             const int c = sidx;
;             if (LOCAL && c < 8) {
; #pragma unroll
;                 for (int t2 = 0; t2 < 2; ++t2) {
;                     const LAS bf16* kp = cb + (kc0 + 16 * t2 + fr) * 72 + 8 * fq;
;                     f32x4 acc = {0.f, 0.f, 0.f, 0.f};
;                     acc = __builtin_amdgcn_mfma_f32_16x16x32_bf16(*(const LAS bf16x8*)(kp), qf[0], acc, 0, 0, 0);
;                     acc = __builtin_amdgcn_mfma_f32_16x16x32_bf16(*(const LAS bf16x8*)(kp + 32), qf[1], acc, 0, 0, 0);
;                     const LAS float* rb = rpb + (r0 + c - gr + 7) * 31 + 15 - qcol;
; #pragma unroll
;                     for (int e = 0; e < 4; ++e) { const int kcol = kc0 + 16 * t2 + 4 * fq + e; const bool ok = (kcol >= cs) && (kcol < cs + 16);
;                         const float sv = ok ? acc[e] * 0.125f + rb[ok ? kcol : qcol] : -1.0e30f; acc[e] = sv; m = fmaxf(m, sv); }
;                     sl[2 * (c < 8 ? c : 0) + t2] = acc; }
	ds_read_b32 v240, v31 offset:37916
	ds_read_b32 v241, v31 offset:37920
	ds_read_b32 v242, v31 offset:37924
	ds_read_b32 v243, v31 offset:37928
	ds_read_b32 v244, v31 offset:37980
	ds_read_b32 v245, v31 offset:37984
	ds_read_b32 v246, v31 offset:37988
	ds_read_b32 v247, v31 offset:37992
	ds_read_b128 v[18:21], v32 offset:18432
	s_add_i32 s26, s26, s15
	s_add_i32 s0, s26, 0x10c0
	v_or_b32_e32 v24, s0, v88
	v_mov_b64_e32 v[22:23], s[8:9]
	s_lshl_b32 s1, s18, 7
	v_mad_i64_i32 v[22:23], s[18:19], v24, s69, v[22:23]
	v_lshlrev_b32_e32 v70, 1, v26
	v_lshl_add_u64 v[22:23], v[22:23], 0, v[70:71]
	s_lshl_b32 s2, s1, 1
	v_lshl_add_u64 v[22:23], v[22:23], 0, s[2:3]
	ds_read_b128 v[26:29], v32 offset:18496
	s_waitcnt lgkmcnt(1)
	v_mfma_f32_16x16x32_bf16 v[34:37], v[18:21], v[6:9], 0
	global_load_dwordx4 v[18:21], v[22:23], off offset:1024
	s_nop 0
	global_load_dwordx4 v[22:25], v[22:23], off offset:1152
	v_mov_b32_e32 v98, 0xf149f2ca
	v_mov_b32_e32 v100, 0xf149f2ca
	s_waitcnt lgkmcnt(0)
	v_mfma_f32_16x16x32_bf16 v[26:29], v[26:29], v[2:5], v[34:37]
	s_nop 2
	s_waitcnt lgkmcnt(0)
	s_nop 3
	v_fmac_f32_e32 v240, 0x3e000000, v26
	v_cndmask_b32_e64 v100, v100, v240, s[28:29]
	s_nop 2
	s_waitcnt lgkmcnt(0)
	s_nop 0
	v_fmac_f32_e32 v241, 0x3e000000, v27
	v_cndmask_b32_e64 v98, v98, v241, s[30:31]
	v_mov_b32_e32 v101, 0xf149f2ca
	v_mov_b32_e32 v102, 0xf149f2ca
	s_nop 2
	s_waitcnt lgkmcnt(0)
	v_fmac_f32_e32 v242, 0x3e000000, v28
	v_cndmask_b32_e64 v102, v102, v242, s[34:35]
	s_nop 2
	s_waitcnt lgkmcnt(0)
	v_fmac_f32_e32 v243, 0x3e000000, v29
	v_cndmask_b32_e64 v101, v101, v243, s[36:37]
	v_mul_u32_u24_e32 v26, 0x90, v33
	v_add_u32_e32 v33, v30, v26
	ds_read_b128 v[26:29], v33 offset:18432
	ds_read_b128 v[34:37], v33 offset:18496
	v_mov_b32_e32 v103, 0xf149f2ca
	v_mov_b32_e32 v105, 0xf149f2ca
	s_waitcnt lgkmcnt(1)
	v_mfma_f32_16x16x32_bf16 v[26:29], v[26:29], v[6:9], 0
	s_waitcnt lgkmcnt(0)
	v_mfma_f32_16x16x32_bf16 v[26:29], v[34:37], v[2:5], v[26:29]
	s_nop 2
	s_waitcnt lgkmcnt(0)
	s_nop 3
	v_fmac_f32_e32 v244, 0x3e000000, v26
	v_cndmask_b32_e64 v105, v105, v244, s[38:39]
	s_nop 2
	s_waitcnt lgkmcnt(0)
	s_nop 0
	v_fmac_f32_e32 v245, 0x3e000000, v27
	v_cndmask_b32_e64 v103, v103, v245, s[44:45]
	v_mov_b32_e32 v107, 0xf149f2ca
	v_mov_b32_e32 v109, 0xf149f2ca
	s_nop 2
	s_waitcnt lgkmcnt(0)
	v_fmac_f32_e32 v246, 0x3e000000, v28
	v_cndmask_b32_e64 v109, v109, v246, s[46:47]
	s_nop 2
	s_waitcnt lgkmcnt(0)
	v_fmac_f32_e32 v247, 0x3e000000, v29
	v_cndmask_b32_e64 v107, v107, v247, s[48:49]
	s_waitcnt vmcnt(3)
	ds_write_b128 v75, v[10:13]
	s_waitcnt vmcnt(2)
	ds_write_b128 v75, v[14:17] offset:9216
	s_waitcnt lgkmcnt(0)
	s_barrier
	ds_read_b32 v240, v31 offset:38040
	ds_read_b32 v241, v31 offset:38044
	ds_read_b32 v242, v31 offset:38048
	ds_read_b32 v243, v31 offset:38052
	ds_read_b32 v244, v31 offset:38104
	ds_read_b32 v245, v31 offset:38108
	ds_read_b32 v246, v31 offset:38112
	ds_read_b32 v247, v31 offset:38116
	ds_read_b128 v[10:13], v32
	ds_read_b128 v[26:29], v32 offset:64
	s_add_i32 s18, s26, 0x1100
	v_or_b32_e32 v16, s18, v88
	v_mov_b64_e32 v[14:15], s[8:9]
	v_mad_i64_i32 v[14:15], s[20:21], v16, s69, v[14:15]
	v_lshl_add_u64 v[14:15], v[14:15], 0, v[70:71]
	v_lshl_add_u64 v[14:15], v[14:15], 0, s[2:3]
	s_waitcnt lgkmcnt(1)
	v_mfma_f32_16x16x32_bf16 v[34:37], v[10:13], v[6:9], 0
	global_load_dwordx4 v[10:13], v[14:15], off offset:1024
	s_nop 0
	global_load_dwordx4 v[14:17], v[14:15], off offset:1152
	v_mov_b32_e32 v104, 0xf149f2ca
	v_mov_b32_e32 v106, 0xf149f2ca
	s_waitcnt lgkmcnt(0)
	v_mfma_f32_16x16x32_bf16 v[26:29], v[26:29], v[2:5], v[34:37]
	s_nop 2
	s_waitcnt lgkmcnt(0)
	s_nop 3
	v_fmac_f32_e32 v240, 0x3e000000, v26
	v_cndmask_b32_e64 v106, v106, v240, s[28:29]
	s_nop 2
	s_waitcnt lgkmcnt(0)
	s_nop 0
	v_fmac_f32_e32 v241, 0x3e000000, v27
	v_cndmask_b32_e64 v104, v104, v241, s[30:31]
	v_mov_b32_e32 v108, 0xf149f2ca
	v_mov_b32_e32 v110, 0xf149f2ca
	s_nop 2
	s_waitcnt lgkmcnt(0)
	v_fmac_f32_e32 v242, 0x3e000000, v28
	v_cndmask_b32_e64 v110, v110, v242, s[34:35]
	s_nop 2
	s_waitcnt lgkmcnt(0)
	v_fmac_f32_e32 v243, 0x3e000000, v29
	v_cndmask_b32_e64 v108, v108, v243, s[36:37]
	ds_read_b128 v[26:29], v33
	ds_read_b128 v[34:37], v33 offset:64
	v_mov_b32_e32 v111, 0xf149f2ca
	v_mov_b32_e32 v113, 0xf149f2ca
	s_waitcnt lgkmcnt(1)
	v_mfma_f32_16x16x32_bf16 v[26:29], v[26:29], v[6:9], 0
	s_waitcnt lgkmcnt(0)
	v_mfma_f32_16x16x32_bf16 v[26:29], v[34:37], v[2:5], v[26:29]
	s_nop 2
	s_waitcnt lgkmcnt(0)
	s_nop 3
	v_fmac_f32_e32 v244, 0x3e000000, v26
	v_cndmask_b32_e64 v113, v113, v244, s[38:39]
	s_nop 2
	s_waitcnt lgkmcnt(0)
	s_nop 0
	v_fmac_f32_e32 v245, 0x3e000000, v27
	v_cndmask_b32_e64 v111, v111, v245, s[44:45]
	v_mov_b32_e32 v112, 0xf149f2ca
	v_mov_b32_e32 v116, 0xf149f2ca
	s_nop 2
	s_waitcnt lgkmcnt(0)
	v_fmac_f32_e32 v246, 0x3e000000, v28
	v_cndmask_b32_e64 v116, v116, v246, s[46:47]
	s_nop 2
	s_waitcnt lgkmcnt(0)
	v_fmac_f32_e32 v247, 0x3e000000, v29
	v_cndmask_b32_e64 v112, v112, v247, s[48:49]
	s_waitcnt vmcnt(3)
	ds_write_b128 v75, v[18:21] offset:18432
	s_waitcnt vmcnt(2)
	ds_write_b128 v75, v[22:25] offset:27648
	s_waitcnt lgkmcnt(0)
	s_barrier
; #define LAS __attribute__((address_space(3)))
; template <bool LOCAL>
; __device__ __forceinline__ void na_unit(const bf16* P, const bf16* VT, bf16* YCAT, const LAS float* rpb_l, LAS bf16* buf, int b, int gr, int hp, int qblk, int tid) {
;     ...
;     for (int sidx = 0; sidx < 2 * NCH; ++sidx) {
;         if (sidx + 2 < 2 * NCH) NA_ISSUE(sidx + 2);
;         const LAS bf16* cb = buf + (sidx & 1) * 9216 + hh * 4608;
;         if (sidx < NCH) {
;             const int c = sidx;
;             if (LOCAL && c < 8) {
; #pragma unroll
;                 for (int t2 = 0; t2 < 2; ++t2) {
;                     const LAS bf16* kp = cb + (kc0 + 16 * t2 + fr) * 72 + 8 * fq;
;                     f32x4 acc = {0.f, 0.f, 0.f, 0.f};
;                     acc = __builtin_amdgcn_mfma_f32_16x16x32_bf16(*(const LAS bf16x8*)(kp), qf[0], acc, 0, 0, 0);
;                     acc = __builtin_amdgcn_mfma_f32_16x16x32_bf16(*(const LAS bf16x8*)(kp + 32), qf[1], acc, 0, 0, 0);
;                     const LAS float* rb = rpb + (r0 + c - gr + 7) * 31 + 15 - qcol;
; #pragma unroll
;                     for (int e = 0; e < 4; ++e) { const int kcol = kc0 + 16 * t2 + 4 * fq + e; const bool ok = (kcol >= cs) && (kcol < cs + 16);
;                         const float sv = ok ? acc[e] * 0.125f + rb[ok ? kcol : qcol] : -1.0e30f; acc[e] = sv; m = fmaxf(m, sv); }
;                     sl[2 * (c < 8 ? c : 0) + t2] = acc; }
	ds_read_b32 v240, v31 offset:38164
	ds_read_b32 v241, v31 offset:38168
	ds_read_b32 v242, v31 offset:38172
	ds_read_b32 v243, v31 offset:38176
	ds_read_b32 v244, v31 offset:38228
	ds_read_b32 v245, v31 offset:38232
	ds_read_b32 v246, v31 offset:38236
	ds_read_b32 v247, v31 offset:38240
	ds_read_b128 v[18:21], v32 offset:18432
	ds_read_b128 v[26:29], v32 offset:18496
	s_add_i32 s20, s26, 0x1140
	v_or_b32_e32 v24, s20, v88
	v_mov_b64_e32 v[22:23], s[8:9]
	v_mad_i64_i32 v[22:23], s[22:23], v24, s69, v[22:23]
	v_lshl_add_u64 v[22:23], v[22:23], 0, v[70:71]
	v_lshl_add_u64 v[22:23], v[22:23], 0, s[2:3]
	s_waitcnt lgkmcnt(1)
	v_mfma_f32_16x16x32_bf16 v[34:37], v[18:21], v[6:9], 0
	global_load_dwordx4 v[18:21], v[22:23], off offset:1024
	s_nop 0
	global_load_dwordx4 v[22:25], v[22:23], off offset:1152
	v_mov_b32_e32 v114, 0xf149f2ca
	v_mov_b32_e32 v115, 0xf149f2ca
	s_waitcnt lgkmcnt(0)
	v_mfma_f32_16x16x32_bf16 v[26:29], v[26:29], v[2:5], v[34:37]
	s_nop 2
	s_waitcnt lgkmcnt(0)
	s_nop 3
	v_fmac_f32_e32 v240, 0x3e000000, v26
	v_cndmask_b32_e64 v115, v115, v240, s[28:29]
	s_nop 2
	s_waitcnt lgkmcnt(0)
	s_nop 0
	v_fmac_f32_e32 v241, 0x3e000000, v27
	v_cndmask_b32_e64 v114, v114, v241, s[30:31]
	v_mov_b32_e32 v117, 0xf149f2ca
	v_mov_b32_e32 v118, 0xf149f2ca
	s_nop 2
	s_waitcnt lgkmcnt(0)
	v_fmac_f32_e32 v242, 0x3e000000, v28
	v_cndmask_b32_e64 v118, v118, v242, s[34:35]
	s_nop 2
	s_waitcnt lgkmcnt(0)
	v_fmac_f32_e32 v243, 0x3e000000, v29
	v_cndmask_b32_e64 v117, v117, v243, s[36:37]
	ds_read_b128 v[26:29], v33 offset:18432
	ds_read_b128 v[34:37], v33 offset:18496
	v_mov_b32_e32 v119, 0xf149f2ca
	v_mov_b32_e32 v121, 0xf149f2ca
	s_waitcnt lgkmcnt(1)
	v_mfma_f32_16x16x32_bf16 v[26:29], v[26:29], v[6:9], 0
	s_waitcnt lgkmcnt(0)
	v_mfma_f32_16x16x32_bf16 v[26:29], v[34:37], v[2:5], v[26:29]
	s_nop 2
	s_waitcnt lgkmcnt(0)
	s_nop 3
	v_fmac_f32_e32 v244, 0x3e000000, v26
	v_cndmask_b32_e64 v121, v121, v244, s[38:39]
	s_nop 2
	s_waitcnt lgkmcnt(0)
	s_nop 0
	v_fmac_f32_e32 v245, 0x3e000000, v27
	v_cndmask_b32_e64 v119, v119, v245, s[44:45]
	v_mov_b32_e32 v120, 0xf149f2ca
	v_mov_b32_e32 v124, 0xf149f2ca
	s_nop 2
	s_waitcnt lgkmcnt(0)
	v_fmac_f32_e32 v246, 0x3e000000, v28
	v_cndmask_b32_e64 v124, v124, v246, s[46:47]
	s_nop 2
	s_waitcnt lgkmcnt(0)
	v_fmac_f32_e32 v247, 0x3e000000, v29
	v_cndmask_b32_e64 v120, v120, v247, s[48:49]
	s_waitcnt vmcnt(3)
	ds_write_b128 v75, v[10:13]
	s_waitcnt vmcnt(2)
	ds_write_b128 v75, v[14:17] offset:9216
	s_waitcnt lgkmcnt(0)
	s_barrier
	ds_read_b32 v240, v31 offset:38288
	ds_read_b32 v241, v31 offset:38292
	ds_read_b32 v242, v31 offset:38296
	ds_read_b32 v243, v31 offset:38300
	ds_read_b32 v244, v31 offset:38352
	ds_read_b32 v245, v31 offset:38356
	ds_read_b32 v246, v31 offset:38360
	ds_read_b32 v247, v31 offset:38364
	ds_read_b128 v[10:13], v32
	ds_read_b128 v[26:29], v32 offset:64
	s_add_i32 s22, s26, 0x1180
	v_or_b32_e32 v16, s22, v88
	v_mov_b64_e32 v[14:15], s[8:9]
	v_mad_i64_i32 v[14:15], s[24:25], v16, s69, v[14:15]
	v_lshl_add_u64 v[14:15], v[14:15], 0, v[70:71]
	v_lshl_add_u64 v[14:15], v[14:15], 0, s[2:3]
	s_waitcnt lgkmcnt(1)
	v_mfma_f32_16x16x32_bf16 v[34:37], v[10:13], v[6:9], 0
	global_load_dwordx4 v[10:13], v[14:15], off offset:1024
	s_nop 0
	global_load_dwordx4 v[14:17], v[14:15], off offset:1152
	v_mov_b32_e32 v122, 0xf149f2ca
	v_mov_b32_e32 v123, 0xf149f2ca
	s_waitcnt lgkmcnt(0)
	v_mfma_f32_16x16x32_bf16 v[26:29], v[26:29], v[2:5], v[34:37]
	s_nop 2
	s_waitcnt lgkmcnt(0)
	s_nop 3
	v_fmac_f32_e32 v240, 0x3e000000, v26
	v_cndmask_b32_e64 v123, v123, v240, s[28:29]
	s_nop 2
	s_waitcnt lgkmcnt(0)
	s_nop 0
	v_fmac_f32_e32 v241, 0x3e000000, v27
	v_cndmask_b32_e64 v122, v122, v241, s[30:31]
	v_mov_b32_e32 v125, 0xf149f2ca
	v_mov_b32_e32 v126, 0xf149f2ca
	s_nop 2
	s_waitcnt lgkmcnt(0)
	v_fmac_f32_e32 v242, 0x3e000000, v28
	v_cndmask_b32_e64 v126, v126, v242, s[34:35]
	s_nop 2
	s_waitcnt lgkmcnt(0)
	v_fmac_f32_e32 v243, 0x3e000000, v29
	v_cndmask_b32_e64 v125, v125, v243, s[36:37]
	ds_read_b128 v[26:29], v33
	ds_read_b128 v[34:37], v33 offset:64
	v_mov_b32_e32 v127, 0xf149f2ca
	v_mov_b32_e32 v129, 0xf149f2ca
	s_waitcnt lgkmcnt(1)
	v_mfma_f32_16x16x32_bf16 v[26:29], v[26:29], v[6:9], 0
	s_waitcnt lgkmcnt(0)
	v_mfma_f32_16x16x32_bf16 v[26:29], v[34:37], v[2:5], v[26:29]
	s_nop 2
	s_waitcnt lgkmcnt(0)
	s_nop 3
	v_fmac_f32_e32 v244, 0x3e000000, v26
	v_cndmask_b32_e64 v129, v129, v244, s[38:39]
	s_nop 2
	s_waitcnt lgkmcnt(0)
	s_nop 0
	v_fmac_f32_e32 v245, 0x3e000000, v27
	v_cndmask_b32_e64 v127, v127, v245, s[44:45]
	v_mov_b32_e32 v128, 0xf149f2ca
	v_mov_b32_e32 v133, 0xf149f2ca
	s_nop 2
	s_waitcnt lgkmcnt(0)
	v_fmac_f32_e32 v246, 0x3e000000, v28
	v_cndmask_b32_e64 v133, v133, v246, s[46:47]
	s_nop 2
	s_waitcnt lgkmcnt(0)
	v_fmac_f32_e32 v247, 0x3e000000, v29
	v_cndmask_b32_e64 v128, v128, v247, s[48:49]
	s_waitcnt vmcnt(3)
	ds_write_b128 v75, v[18:21] offset:18432
	s_waitcnt vmcnt(2)
	ds_write_b128 v75, v[22:25] offset:27648
	s_waitcnt lgkmcnt(0)
	s_barrier
; #define LAS __attribute__((address_space(3)))
; template <bool LOCAL>
; __device__ __forceinline__ void na_unit(const bf16* P, const bf16* VT, bf16* YCAT, const LAS float* rpb_l, LAS bf16* buf, int b, int gr, int hp, int qblk, int tid) {
;     ...
;     for (int sidx = 0; sidx < 2 * NCH; ++sidx) {
;         if (sidx + 2 < 2 * NCH) NA_ISSUE(sidx + 2);
;         const LAS bf16* cb = buf + (sidx & 1) * 9216 + hh * 4608;
;         if (sidx < NCH) {
;             const int c = sidx;
;             if (LOCAL && c < 8) {
; #pragma unroll
;                 for (int t2 = 0; t2 < 2; ++t2) {
;                     const LAS bf16* kp = cb + (kc0 + 16 * t2 + fr) * 72 + 8 * fq;
;                     f32x4 acc = {0.f, 0.f, 0.f, 0.f};
;                     acc = __builtin_amdgcn_mfma_f32_16x16x32_bf16(*(const LAS bf16x8*)(kp), qf[0], acc, 0, 0, 0);
;                     acc = __builtin_amdgcn_mfma_f32_16x16x32_bf16(*(const LAS bf16x8*)(kp + 32), qf[1], acc, 0, 0, 0);
;                     const LAS float* rb = rpb + (r0 + c - gr + 7) * 31 + 15 - qcol;
; #pragma unroll
;                     for (int e = 0; e < 4; ++e) { const int kcol = kc0 + 16 * t2 + 4 * fq + e; const bool ok = (kcol >= cs) && (kcol < cs + 16);
;                         const float sv = ok ? acc[e] * 0.125f + rb[ok ? kcol : qcol] : -1.0e30f; acc[e] = sv; m = fmaxf(m, sv); }
;                     sl[2 * (c < 8 ? c : 0) + t2] = acc; }
	ds_read_b32 v240, v31 offset:38412
	ds_read_b32 v241, v31 offset:38416
	ds_read_b32 v242, v31 offset:38420
	ds_read_b32 v243, v31 offset:38424
	ds_read_b32 v244, v31 offset:38476
	ds_read_b32 v245, v31 offset:38480
	ds_read_b32 v246, v31 offset:38484
	ds_read_b32 v247, v31 offset:38488
	ds_read_b128 v[18:21], v32 offset:18432
	ds_read_b128 v[26:29], v32 offset:18496
	s_add_i32 s24, s26, 0x11c0
	v_or_b32_e32 v24, s24, v88
	v_mov_b64_e32 v[22:23], s[8:9]
	v_mad_i64_i32 v[22:23], s[26:27], v24, s69, v[22:23]
	v_lshl_add_u64 v[22:23], v[22:23], 0, v[70:71]
	v_lshl_add_u64 v[22:23], v[22:23], 0, s[2:3]
	s_waitcnt lgkmcnt(1)
	v_mfma_f32_16x16x32_bf16 v[34:37], v[18:21], v[6:9], 0
	global_load_dwordx4 v[18:21], v[22:23], off offset:1024
	s_nop 0
	global_load_dwordx4 v[22:25], v[22:23], off offset:1152
	v_mov_b32_e32 v130, 0xf149f2ca
	v_mov_b32_e32 v132, 0xf149f2ca
	s_waitcnt lgkmcnt(0)
	v_mfma_f32_16x16x32_bf16 v[26:29], v[26:29], v[2:5], v[34:37]
	s_nop 2
	s_waitcnt lgkmcnt(0)
	s_nop 3
	v_fmac_f32_e32 v240, 0x3e000000, v26
	v_cndmask_b32_e64 v132, v132, v240, s[28:29]
	s_nop 2
	s_waitcnt lgkmcnt(0)
	s_nop 0
	v_fmac_f32_e32 v241, 0x3e000000, v27
	v_cndmask_b32_e64 v130, v130, v241, s[30:31]
	v_mov_b32_e32 v134, 0xf149f2ca
	v_mov_b32_e32 v135, 0xf149f2ca
	s_nop 2
	s_waitcnt lgkmcnt(0)
	v_fmac_f32_e32 v242, 0x3e000000, v28
	v_cndmask_b32_e64 v135, v135, v242, s[34:35]
	s_nop 2
	s_waitcnt lgkmcnt(0)
	v_fmac_f32_e32 v243, 0x3e000000, v29
	v_cndmask_b32_e64 v134, v134, v243, s[36:37]
	ds_read_b128 v[26:29], v33 offset:18432
	ds_read_b128 v[34:37], v33 offset:18496
	v_mov_b32_e32 v137, 0xf149f2ca
	v_mov_b32_e32 v139, 0xf149f2ca
	s_waitcnt lgkmcnt(1)
	v_mfma_f32_16x16x32_bf16 v[26:29], v[26:29], v[6:9], 0
	s_waitcnt lgkmcnt(0)
	v_mfma_f32_16x16x32_bf16 v[26:29], v[34:37], v[2:5], v[26:29]
	s_nop 2
	s_waitcnt lgkmcnt(0)
	s_nop 3
	v_fmac_f32_e32 v244, 0x3e000000, v26
	v_cndmask_b32_e64 v139, v139, v244, s[38:39]
	s_nop 2
	s_waitcnt lgkmcnt(0)
	s_nop 0
	v_fmac_f32_e32 v245, 0x3e000000, v27
	v_cndmask_b32_e64 v137, v137, v245, s[44:45]
	v_mov_b32_e32 v138, 0xf149f2ca
	v_mov_b32_e32 v142, 0xf149f2ca
	s_nop 2
	s_waitcnt lgkmcnt(0)
	v_fmac_f32_e32 v246, 0x3e000000, v28
	v_cndmask_b32_e64 v142, v142, v246, s[46:47]
	s_nop 2
	s_waitcnt lgkmcnt(0)
	v_fmac_f32_e32 v247, 0x3e000000, v29
	v_cndmask_b32_e64 v138, v138, v247, s[48:49]
	s_waitcnt vmcnt(3)
	ds_write_b128 v75, v[10:13]
	s_waitcnt vmcnt(2)
	ds_write_b128 v75, v[14:17] offset:9216
	s_waitcnt lgkmcnt(0)
	s_barrier
	ds_read_b32 v240, v31 offset:38536
	ds_read_b32 v241, v31 offset:38540
	ds_read_b32 v242, v31 offset:38544
	ds_read_b32 v243, v31 offset:38548
	ds_read_b32 v244, v31 offset:38600
	ds_read_b32 v245, v31 offset:38604
	ds_read_b32 v246, v31 offset:38608
	ds_read_b32 v247, v31 offset:38612
	ds_read_b128 v[10:13], v32
	ds_read_b128 v[26:29], v32 offset:64
	s_lshl_b32 s26, s17, 8
	v_or_b32_e32 v34, s26, v88
	v_mov_b64_e32 v[14:15], s[8:9]
	v_mad_i64_i32 v[14:15], s[52:53], v34, s69, v[14:15]
	v_lshl_add_u64 v[14:15], v[14:15], 0, v[70:71]
	v_lshl_add_u64 v[14:15], v[14:15], 0, s[2:3]
	s_waitcnt lgkmcnt(1)
	v_mfma_f32_16x16x32_bf16 v[36:39], v[10:13], v[6:9], 0
	global_load_dwordx4 v[10:13], v[14:15], off offset:1024
	s_nop 0
	global_load_dwordx4 v[14:17], v[14:15], off offset:1152
	v_mov_b32_e32 v140, 0xf149f2ca
	v_mov_b32_e32 v141, 0xf149f2ca
	s_waitcnt lgkmcnt(0)
	v_mfma_f32_16x16x32_bf16 v[26:29], v[26:29], v[2:5], v[36:39]
	s_nop 2
	s_waitcnt lgkmcnt(0)
	s_nop 3
	v_fmac_f32_e32 v240, 0x3e000000, v26
	v_cndmask_b32_e64 v141, v141, v240, s[28:29]
	s_nop 2
	s_waitcnt lgkmcnt(0)
	s_nop 0
	v_fmac_f32_e32 v241, 0x3e000000, v27
	v_cndmask_b32_e64 v140, v140, v241, s[30:31]
	v_mov_b32_e32 v143, 0xf149f2ca
	v_mov_b32_e32 v144, 0xf149f2ca
	s_nop 2
	s_waitcnt lgkmcnt(0)
	v_fmac_f32_e32 v242, 0x3e000000, v28
	v_cndmask_b32_e64 v144, v144, v242, s[34:35]
	s_nop 2
	s_waitcnt lgkmcnt(0)
	v_fmac_f32_e32 v243, 0x3e000000, v29
	v_cndmask_b32_e64 v143, v143, v243, s[36:37]
	ds_read_b128 v[26:29], v33
	ds_read_b128 v[36:39], v33 offset:64
	v_mov_b32_e32 v145, 0xf149f2ca
	v_mov_b32_e32 v147, 0xf149f2ca
	s_waitcnt lgkmcnt(1)
	v_mfma_f32_16x16x32_bf16 v[26:29], v[26:29], v[6:9], 0
	s_waitcnt lgkmcnt(0)
	v_mfma_f32_16x16x32_bf16 v[26:29], v[36:39], v[2:5], v[26:29]
	s_nop 2
	s_waitcnt lgkmcnt(0)
	s_nop 3
	v_fmac_f32_e32 v244, 0x3e000000, v26
	v_cndmask_b32_e64 v147, v147, v244, s[38:39]
	s_nop 2
	s_waitcnt lgkmcnt(0)
	s_nop 0
	v_fmac_f32_e32 v245, 0x3e000000, v27
	v_cndmask_b32_e64 v145, v145, v245, s[44:45]
	v_mov_b32_e32 v146, 0xf149f2ca
	v_mov_b32_e32 v150, 0xf149f2ca
	s_nop 2
	s_waitcnt lgkmcnt(0)
	v_fmac_f32_e32 v246, 0x3e000000, v28
	v_cndmask_b32_e64 v150, v150, v246, s[46:47]
	s_nop 2
	s_waitcnt lgkmcnt(0)
	v_fmac_f32_e32 v247, 0x3e000000, v29
	v_cndmask_b32_e64 v146, v146, v247, s[48:49]
	s_waitcnt vmcnt(3)
	ds_write_b128 v75, v[18:21] offset:18432
	s_waitcnt vmcnt(2)
	ds_write_b128 v75, v[22:25] offset:27648
	s_waitcnt lgkmcnt(0)
	s_barrier
; #define LAS __attribute__((address_space(3)))
; template <bool LOCAL>
; __device__ __forceinline__ void na_unit(const bf16* P, const bf16* VT, bf16* YCAT, const LAS float* rpb_l, LAS bf16* buf, int b, int gr, int hp, int qblk, int tid) {
;     ...
;     for (int sidx = 0; sidx < 2 * NCH; ++sidx) {
;         if (sidx + 2 < 2 * NCH) NA_ISSUE(sidx + 2);
;         const LAS bf16* cb = buf + (sidx & 1) * 9216 + hh * 4608;
;         if (sidx < NCH) {
;             const int c = sidx;
;             if (LOCAL && c < 8) {
; #pragma unroll
;                 for (int t2 = 0; t2 < 2; ++t2) {
;                     const LAS bf16* kp = cb + (kc0 + 16 * t2 + fr) * 72 + 8 * fq;
;                     f32x4 acc = {0.f, 0.f, 0.f, 0.f};
;                     acc = __builtin_amdgcn_mfma_f32_16x16x32_bf16(*(const LAS bf16x8*)(kp), qf[0], acc, 0, 0, 0);
;                     acc = __builtin_amdgcn_mfma_f32_16x16x32_bf16(*(const LAS bf16x8*)(kp + 32), qf[1], acc, 0, 0, 0);
;                     const LAS float* rb = rpb + (r0 + c - gr + 7) * 31 + 15 - qcol;
; #pragma unroll
;                     for (int e = 0; e < 4; ++e) { const int kcol = kc0 + 16 * t2 + 4 * fq + e; const bool ok = (kcol >= cs) && (kcol < cs + 16);
;                         const float sv = ok ? acc[e] * 0.125f + rb[ok ? kcol : qcol] : -1.0e30f; acc[e] = sv; m = fmaxf(m, sv); }
;                     sl[2 * (c < 8 ? c : 0) + t2] = acc; }
;             } else {
;                 const int cc = c - NLOC;
; #pragma unroll
;                 for (int t4 = 0; t4 < 4; ++t4) {
;                     const LAS bf16* kp = cb + (16 * t4 + fr) * 72 + 8 * fq;
;                     f32x4 acc = {0.f, 0.f, 0.f, 0.f};
;                     acc = __builtin_amdgcn_mfma_f32_16x16x32_bf16(*(const LAS bf16x8*)(kp), qf[0], acc, 0, 0, 0);
;                     acc = __builtin_amdgcn_mfma_f32_16x16x32_bf16(*(const LAS bf16x8*)(kp + 32), qf[1], acc, 0, 0, 0);
; #pragma unroll
;                     for (int e = 0; e < 4; ++e) { acc[e] *= 0.125f; m = fmaxf(m, acc[e]); }
;                     sc[4 * (cc >= 0 ? cc : 0) + t4] = acc; }
;             }
;             if (sidx == NCH - 1) { m = fmaxf(m, __shfl_xor(m, 16)); m = fmaxf(m, __shfl_xor(m, 32)); }
	ds_read_b32 v240, v31 offset:38660
	ds_read_b32 v241, v31 offset:38664
	ds_read_b32 v242, v31 offset:38668
	ds_read_b32 v243, v31 offset:38672
	ds_read_b32 v244, v31 offset:38724
	ds_read_b32 v245, v31 offset:38728
	ds_read_b32 v246, v31 offset:38732
	ds_read_b32 v247, v31 offset:38736
	ds_read_b128 v[18:21], v32 offset:18432
	ds_read_b128 v[26:29], v32 offset:18496
	v_or_b32_e32 v24, 64, v34
	v_mov_b64_e32 v[22:23], s[8:9]
	v_mad_i64_i32 v[22:23], s[52:53], v24, s69, v[22:23]
	v_lshl_add_u64 v[22:23], v[22:23], 0, v[70:71]
	v_lshl_add_u64 v[22:23], v[22:23], 0, s[2:3]
	s_waitcnt lgkmcnt(1)
	v_mfma_f32_16x16x32_bf16 v[36:39], v[18:21], v[6:9], 0
	global_load_dwordx4 v[18:21], v[22:23], off offset:1024
	s_nop 0
	global_load_dwordx4 v[22:25], v[22:23], off offset:1152
	v_mov_b32_e32 v148, 0xf149f2ca
	v_mov_b32_e32 v149, 0xf149f2ca
	s_waitcnt lgkmcnt(0)
	v_mfma_f32_16x16x32_bf16 v[26:29], v[26:29], v[2:5], v[36:39]
	s_nop 2
	s_waitcnt lgkmcnt(0)
	s_nop 3
	v_fmac_f32_e32 v240, 0x3e000000, v26
	v_cndmask_b32_e64 v149, v149, v240, s[28:29]
	s_nop 2
	s_waitcnt lgkmcnt(0)
	s_nop 0
	v_fmac_f32_e32 v241, 0x3e000000, v27
	v_cndmask_b32_e64 v148, v148, v241, s[30:31]
	v_mov_b32_e32 v151, 0xf149f2ca
	v_mov_b32_e32 v152, 0xf149f2ca
	s_nop 2
	s_waitcnt lgkmcnt(0)
	v_fmac_f32_e32 v242, 0x3e000000, v28
	v_cndmask_b32_e64 v152, v152, v242, s[34:35]
	s_nop 2
	s_waitcnt lgkmcnt(0)
	v_fmac_f32_e32 v243, 0x3e000000, v29
	v_cndmask_b32_e64 v151, v151, v243, s[36:37]
	ds_read_b128 v[26:29], v33 offset:18432
	ds_read_b128 v[36:39], v33 offset:18496
	v_mov_b32_e32 v153, 0xf149f2ca
	v_mov_b32_e32 v155, 0xf149f2ca
	s_waitcnt lgkmcnt(1)
	v_mfma_f32_16x16x32_bf16 v[26:29], v[26:29], v[6:9], 0
	s_waitcnt lgkmcnt(0)
	v_mfma_f32_16x16x32_bf16 v[26:29], v[36:39], v[2:5], v[26:29]
	s_nop 2
	s_waitcnt lgkmcnt(0)
	s_nop 3
	v_fmac_f32_e32 v244, 0x3e000000, v26
	v_cndmask_b32_e64 v155, v155, v244, s[38:39]
	s_nop 2
	s_waitcnt lgkmcnt(0)
	s_nop 0
	v_fmac_f32_e32 v245, 0x3e000000, v27
	v_cndmask_b32_e64 v153, v153, v245, s[44:45]
	v_mov_b32_e32 v154, 0xf149f2ca
	v_mov_b32_e32 v157, 0xf149f2ca
	s_nop 2
	s_waitcnt lgkmcnt(0)
	v_fmac_f32_e32 v246, 0x3e000000, v28
	v_cndmask_b32_e64 v157, v157, v246, s[46:47]
	s_nop 2
	s_waitcnt lgkmcnt(0)
	v_fmac_f32_e32 v247, 0x3e000000, v29
	v_cndmask_b32_e64 v154, v154, v247, s[48:49]
	v_max3_f32 v26, v92, s74, v91
	v_max3_f32 v26, v26, v94, v93
	v_max3_f32 v26, v26, v96, v95
	v_max3_f32 v26, v26, v99, v97
	v_max3_f32 v26, v26, v100, v98
	v_max3_f32 v26, v26, v102, v101
	v_max3_f32 v26, v26, v105, v103
	v_max3_f32 v26, v26, v109, v107
	v_max3_f32 v26, v26, v106, v104
	v_max3_f32 v26, v26, v110, v108
	v_max3_f32 v26, v26, v113, v111
	v_max3_f32 v26, v26, v116, v112
	v_max3_f32 v26, v26, v115, v114
	v_max3_f32 v26, v26, v118, v117
	v_max3_f32 v26, v26, v121, v119
	v_max3_f32 v26, v26, v124, v120
	v_max3_f32 v26, v26, v123, v122
	v_max3_f32 v26, v26, v126, v125
	v_max3_f32 v26, v26, v129, v127
	v_max3_f32 v26, v26, v133, v128
	v_max3_f32 v26, v26, v132, v130
	v_max3_f32 v26, v26, v135, v134
	v_max3_f32 v26, v26, v139, v137
	v_max3_f32 v26, v26, v142, v138
	v_max3_f32 v26, v26, v141, v140
	v_max3_f32 v26, v26, v144, v143
	v_mad_u32_u24 v89, v89, s70, v30
	v_max3_f32 v26, v26, v147, v145
	s_waitcnt vmcnt(3)
	ds_write_b128 v75, v[10:13]
	s_waitcnt vmcnt(2)
	ds_write_b128 v75, v[14:17] offset:9216
	s_waitcnt lgkmcnt(0)
	s_barrier
	ds_read_b128 v[10:13], v89
	ds_read_b128 v[14:17], v89 offset:64
	v_max3_f32 v26, v26, v150, v146
	v_max3_f32 v26, v26, v149, v148
	v_max3_f32 v26, v26, v152, v151
	v_max3_f32 v26, v26, v155, v153
	v_max3_f32 v35, v26, v157, v154
	v_or_b32_e32 v26, 0x80, v34
	v_mov_b64_e32 v[44:45], s[8:9]
	v_mad_i64_i32 v[26:27], s[28:29], v26, s69, v[44:45]
	v_lshl_add_u64 v[26:27], v[26:27], 0, v[70:71]
	v_lshl_add_u64 v[30:31], v[26:27], 0, s[2:3]
	s_waitcnt lgkmcnt(1)
	v_mfma_f32_16x16x32_bf16 v[10:13], v[10:13], v[6:9], 0
	global_load_dwordx4 v[26:29], v[30:31], off offset:1024
	s_nop 0
	global_load_dwordx4 v[30:33], v[30:31], off offset:1152
	ds_read_b128 v[36:39], v89 offset:2304
	v_lshl_add_u64 v[78:79], s[4:5], 0, v[70:71]
	s_waitcnt lgkmcnt(1)
	v_mfma_f32_16x16x32_bf16 v[62:65], v[14:17], v[2:5], v[10:13]
	s_ashr_i32 s17, s16, 31
	v_mov_b32_e32 v81, v71
	v_cmp_lt_i32_e32 vcc, v83, v84
	ds_read_b128 v[10:13], v89 offset:2368
	v_add3_u32 v156, v86, v76, v87
	s_nop 2
	v_mul_f32_e32 v14, 0x3e000000, v62
	v_mul_f32_e32 v15, 0x3e000000, v63
	v_max3_f32 v35, v35, v14, v15
	v_mul_f32_e32 v40, 0x3e000000, v64
	s_waitcnt lgkmcnt(1)
	v_mfma_f32_16x16x32_bf16 v[14:17], v[36:39], v[6:9], 0
	v_mul_f32_e32 v36, 0x3e000000, v65
	v_max3_f32 v35, v35, v40, v36
	ds_read_b128 v[36:39], v89 offset:4608
	s_waitcnt lgkmcnt(1)
	v_mfma_f32_16x16x32_bf16 v[66:69], v[10:13], v[2:5], v[14:17]
	ds_read_b128 v[10:13], v89 offset:4672
	s_ashr_i32 s19, s18, 31
	s_ashr_i32 s21, s20, 31
	s_ashr_i32 s23, s22, 31
	s_ashr_i32 s25, s24, 31
	s_nop 2
	v_mul_f32_e32 v14, 0x3e000000, v66
	v_mul_f32_e32 v15, 0x3e000000, v67
	v_max3_f32 v35, v35, v14, v15
	s_waitcnt lgkmcnt(1)
	v_mfma_f32_16x16x32_bf16 v[14:17], v[36:39], v[6:9], 0
	v_mul_f32_e32 v40, 0x3e000000, v68
	v_mul_f32_e32 v41, 0x3e000000, v69
	v_max3_f32 v35, v35, v40, v41
	s_waitcnt lgkmcnt(0)
	v_mfma_f32_16x16x32_bf16 v[58:61], v[10:13], v[2:5], v[14:17]
	ds_read_b128 v[36:39], v89 offset:6912
	ds_read_b128 v[40:43], v89 offset:6976
	s_waitcnt vmcnt(3)
	ds_write_b128 v75, v[18:21] offset:18432
	s_waitcnt vmcnt(2)
	ds_write_b128 v75, v[22:25] offset:27648
	s_waitcnt lgkmcnt(0)
	s_nop 0
	v_mul_f32_e32 v10, 0x3e000000, v58
	v_mul_f32_e32 v11, 0x3e000000, v59
	v_max3_f32 v14, v35, v10, v11
	v_mfma_f32_16x16x32_bf16 v[10:13], v[36:39], v[6:9], 0
	v_mul_f32_e32 v15, 0x3e000000, v60
	v_mul_f32_e32 v16, 0x3e000000, v61
	v_max3_f32 v14, v14, v15, v16
	v_mfma_f32_16x16x32_bf16 v[54:57], v[40:43], v[2:5], v[10:13]
	s_barrier
; #define LAS __attribute__((address_space(3)))
; template <bool LOCAL>
; __device__ __forceinline__ void na_unit(const bf16* P, const bf16* VT, bf16* YCAT, const LAS float* rpb_l, LAS bf16* buf, int b, int gr, int hp, int qblk, int tid) {
;     ...
;                 const int cc = c - NLOC;
; #pragma unroll
;                 for (int t4 = 0; t4 < 4; ++t4) {
;                     const LAS bf16* kp = cb + (16 * t4 + fr) * 72 + 8 * fq;
;                     f32x4 acc = {0.f, 0.f, 0.f, 0.f};
;                     acc = __builtin_amdgcn_mfma_f32_16x16x32_bf16(*(const LAS bf16x8*)(kp), qf[0], acc, 0, 0, 0);
;                     acc = __builtin_amdgcn_mfma_f32_16x16x32_bf16(*(const LAS bf16x8*)(kp + 32), qf[1], acc, 0, 0, 0);
; #pragma unroll
;                     for (int e = 0; e < 4; ++e) { acc[e] *= 0.125f; m = fmaxf(m, acc[e]); }
;                     sc[4 * (cc >= 0 ? cc : 0) + t4] = acc; }
;             }
;             if (sidx == NCH - 1) { m = fmaxf(m, __shfl_xor(m, 16)); m = fmaxf(m, __shfl_xor(m, 32)); }
	v_or_b32_e32 v18, 0xc0, v34
	v_mad_i64_i32 v[18:19], s[28:29], v18, s69, v[44:45]
	v_lshl_add_u64 v[18:19], v[18:19], 0, v[70:71]
	s_nop 3
	v_mul_f32_e32 v10, 0x3e000000, v54
	v_mul_f32_e32 v11, 0x3e000000, v55
	v_max3_f32 v14, v14, v10, v11
	ds_read_b128 v[10:13], v89 offset:18432
	v_mul_f32_e32 v15, 0x3e000000, v56
	v_mul_f32_e32 v16, 0x3e000000, v57
	v_max3_f32 v35, v14, v15, v16
	ds_read_b128 v[14:17], v89 offset:18496
	v_lshl_add_u64 v[22:23], v[18:19], 0, s[2:3]
	s_waitcnt lgkmcnt(1)
	v_mfma_f32_16x16x32_bf16 v[10:13], v[10:13], v[6:9], 0
	global_load_dwordx4 v[18:21], v[22:23], off offset:1024
	global_load_dwordx4 v[158:161], v[22:23], off offset:1152
	ds_read_b128 v[22:25], v89 offset:20736
	s_ashr_i32 s27, s26, 31
	s_waitcnt lgkmcnt(1)
	v_mfma_f32_16x16x32_bf16 v[46:49], v[14:17], v[2:5], v[10:13]
	s_nop 2
	ds_read_b128 v[10:13], v89 offset:20800
	s_nop 3
	v_mul_f32_e32 v14, 0x3e000000, v46
	v_mul_f32_e32 v15, 0x3e000000, v47
	v_max3_f32 v34, v35, v14, v15
	v_mul_f32_e32 v35, 0x3e000000, v48
	s_waitcnt lgkmcnt(1)
	v_mfma_f32_16x16x32_bf16 v[14:17], v[22:25], v[6:9], 0
	v_mul_f32_e32 v22, 0x3e000000, v49
	v_max3_f32 v34, v34, v35, v22
	ds_read_b128 v[22:25], v89 offset:23040
	s_waitcnt lgkmcnt(1)
	v_mfma_f32_16x16x32_bf16 v[50:53], v[10:13], v[2:5], v[14:17]
	ds_read_b128 v[10:13], v89 offset:23104
	s_nop 6
	v_mul_f32_e32 v14, 0x3e000000, v50
	v_mul_f32_e32 v15, 0x3e000000, v51
	v_max3_f32 v34, v34, v14, v15
	s_waitcnt lgkmcnt(1)
	v_mfma_f32_16x16x32_bf16 v[14:17], v[22:25], v[6:9], 0
	v_mul_f32_e32 v35, 0x3e000000, v52
	v_mul_f32_e32 v36, 0x3e000000, v53
	v_max3_f32 v38, v34, v35, v36
	s_waitcnt lgkmcnt(0)
	v_mfma_f32_16x16x32_bf16 v[42:45], v[10:13], v[2:5], v[14:17]
	ds_read_b128 v[22:25], v89 offset:25344
	ds_read_b128 v[34:37], v89 offset:25408
	s_waitcnt vmcnt(3)
	ds_write_b128 v75, v[26:29]
	s_waitcnt vmcnt(2)
	ds_write_b128 v75, v[30:33] offset:9216
	s_waitcnt lgkmcnt(0)
	s_nop 0
	v_mul_f32_e32 v10, 0x3e000000, v42
	v_mul_f32_e32 v11, 0x3e000000, v43
	v_max3_f32 v14, v38, v10, v11
	v_mfma_f32_16x16x32_bf16 v[10:13], v[22:25], v[6:9], 0
	v_mul_f32_e32 v15, 0x3e000000, v44
	v_mul_f32_e32 v16, 0x3e000000, v45
	v_max3_f32 v14, v14, v15, v16
	v_mfma_f32_16x16x32_bf16 v[38:41], v[34:37], v[2:5], v[10:13]
	s_barrier
	v_add3_u32 v26, v88, s1, 64
	v_mul_u32_u24_e32 v26, 0x9000, v26
	v_lshl_add_u64 v[22:23], s[16:17], 1, v[78:79]
	s_nop 3
	v_mul_f32_e32 v10, 0x3e000000, v38
	v_mul_f32_e32 v11, 0x3e000000, v39
	v_max3_f32 v10, v14, v10, v11
	v_mul_f32_e32 v11, 0x3e000000, v40
	v_mul_f32_e32 v12, 0x3e000000, v41
	v_max3_f32 v34, v10, v11, v12
	v_or_b32_e32 v10, s1, v88
	v_mul_u32_u24_e32 v14, 0x9000, v10
	ds_read_b128 v[10:13], v89
	v_lshlrev_b32_e32 v70, 1, v14
	ds_read_b128 v[14:17], v89 offset:64
	v_lshlrev_b32_e32 v80, 1, v26
	v_lshl_add_u64 v[24:25], v[22:23], 0, v[70:71]
	v_lshl_add_u64 v[22:23], v[22:23], 0, v[80:81]
	s_waitcnt lgkmcnt(1)
	v_mfma_f32_16x16x32_bf16 v[10:13], v[10:13], v[6:9], 0
	global_load_dwordx4 v[162:165], v[24:25], off
	global_load_dwordx4 v[166:169], v[22:23], off
	ds_read_b128 v[22:25], v89 offset:2304
	s_add_i32 s16, s15, s50
	s_waitcnt lgkmcnt(1)
	v_mfma_f32_16x16x32_bf16 v[30:33], v[14:17], v[2:5], v[10:13]
	s_ashr_i32 s17, s16, 31
	s_ashr_i32 s15, s14, 31
	v_lshl_add_u64 v[86:87], s[14:15], 1, v[78:79]
	ds_read_b128 v[10:13], v89 offset:2368
	s_ashr_i32 s1, s0, 31
	s_nop 2
	v_mul_f32_e32 v14, 0x3e000000, v30
	v_mul_f32_e32 v15, 0x3e000000, v31
	v_max3_f32 v26, v34, v14, v15
	v_mul_f32_e32 v27, 0x3e000000, v32
	s_waitcnt lgkmcnt(1)
	v_mfma_f32_16x16x32_bf16 v[14:17], v[22:25], v[6:9], 0
	v_mul_f32_e32 v22, 0x3e000000, v33
	v_max3_f32 v26, v26, v27, v22
	ds_read_b128 v[22:25], v89 offset:4608
	s_waitcnt lgkmcnt(1)
	v_mfma_f32_16x16x32_bf16 v[34:37], v[10:13], v[2:5], v[14:17]
	ds_read_b128 v[10:13], v89 offset:4672
	s_nop 6
	v_mul_f32_e32 v14, 0x3e000000, v34
	v_mul_f32_e32 v15, 0x3e000000, v35
	v_max3_f32 v26, v26, v14, v15
	s_waitcnt lgkmcnt(1)
	v_mfma_f32_16x16x32_bf16 v[14:17], v[22:25], v[6:9], 0
	v_mul_f32_e32 v27, 0x3e000000, v36
	v_mul_f32_e32 v28, 0x3e000000, v37
	v_max3_f32 v88, v26, v27, v28
	s_waitcnt lgkmcnt(0)
	v_mfma_f32_16x16x32_bf16 v[26:29], v[10:13], v[2:5], v[14:17]
	ds_read_b128 v[22:25], v89 offset:6912
	ds_read_b128 v[170:173], v89 offset:6976
	s_waitcnt vmcnt(3)
	ds_write_b128 v75, v[18:21] offset:18432
	s_waitcnt vmcnt(2)
	ds_write_b128 v75, v[158:161] offset:27648
	s_waitcnt lgkmcnt(0)
	s_nop 0
	v_mul_f32_e32 v10, 0x3e000000, v26
	v_mul_f32_e32 v11, 0x3e000000, v27
	v_max3_f32 v14, v88, v10, v11
	v_mfma_f32_16x16x32_bf16 v[10:13], v[22:25], v[6:9], 0
	v_mul_f32_e32 v15, 0x3e000000, v28
	v_mul_f32_e32 v16, 0x3e000000, v29
	v_max3_f32 v14, v14, v15, v16
	v_mfma_f32_16x16x32_bf16 v[22:25], v[170:173], v[2:5], v[10:13]
	s_barrier
; #define LAS __attribute__((address_space(3)))
; __device__ __forceinline__ unsigned cvt_pk_bf16(float lo, float hi) { const float __attribute__((ext_vector_type(2))) v = {lo, hi}; return __builtin_bit_cast(unsigned, __builtin_convertvector(v, bf16x2_t)); }
; template <bool LOCAL>
; __device__ __forceinline__ void na_unit(const bf16* P, const bf16* VT, bf16* YCAT, const LAS float* rpb_l, LAS bf16* buf, int b, int gr, int hp, int qblk, int tid) {
;     ...
;                 const int cc = c - NLOC;
; #pragma unroll
;                 for (int t4 = 0; t4 < 4; ++t4) {
;                     const LAS bf16* kp = cb + (16 * t4 + fr) * 72 + 8 * fq;
;                     f32x4 acc = {0.f, 0.f, 0.f, 0.f};
;                     acc = __builtin_amdgcn_mfma_f32_16x16x32_bf16(*(const LAS bf16x8*)(kp), qf[0], acc, 0, 0, 0);
;                     acc = __builtin_amdgcn_mfma_f32_16x16x32_bf16(*(const LAS bf16x8*)(kp + 32), qf[1], acc, 0, 0, 0);
; #pragma unroll
;                     for (int e = 0; e < 4; ++e) { acc[e] *= 0.125f; m = fmaxf(m, acc[e]); }
;                     sc[4 * (cc >= 0 ? cc : 0) + t4] = acc; }
;             }
;             if (sidx == NCH - 1) { m = fmaxf(m, __shfl_xor(m, 16)); m = fmaxf(m, __shfl_xor(m, 32)); }
;         } else {
;             const int c = sidx - NCH;
;             if (LOCAL && c < 8) {
;                 float p[8];
; #pragma unroll
;                 for (int e = 0; e < 4; ++e) { p[e] = __expf(sl[2 * (c < 8 ? c : 0)][e] - m); p[4 + e] = __expf(sl[2 * (c < 8 ? c : 0) + 1][e] - m); }
; #pragma unroll
;                 for (int e = 0; e < 8; ++e) lsum += p[e];
;                 const bf16x8 pf = __builtin_bit_cast(bf16x8, (v4u){pg8::cvt_pk_bf16(p[0], p[1]), pg8::cvt_pk_bf16(p[2], p[3]), pg8::cvt_pk_bf16(p[4], p[5]), pg8::cvt_pk_bf16(p[6], p[7])});
; #pragma unroll
;                 for (int dt = 0; dt < 4; ++dt) { const LAS bf16* vp = cb + (16 * dt + fr) * 72 + kc0 + 4 * fq;
;                     o[dt] = __builtin_amdgcn_mfma_f32_16x16x32_bf16(frag44(vp, vp + 16), pf, o[dt], 0, 0, 0); }
	v_lshl_add_u64 v[18:19], s[16:17], 1, v[78:79]
	v_lshl_add_u64 v[20:21], v[18:19], 0, v[70:71]
	v_lshl_add_u64 v[18:19], v[18:19], 0, v[80:81]
	s_nop 3
	v_mul_f32_e32 v10, 0x3e000000, v22
	v_mul_f32_e32 v11, 0x3e000000, v23
	v_max3_f32 v14, v14, v10, v11
	ds_read_b128 v[10:13], v89 offset:18432
	v_mul_f32_e32 v15, 0x3e000000, v24
	v_mul_f32_e32 v16, 0x3e000000, v25
	v_max3_f32 v88, v14, v15, v16
	ds_read_b128 v[14:17], v89 offset:18496
	s_waitcnt lgkmcnt(1)
	v_mfma_f32_16x16x32_bf16 v[10:13], v[10:13], v[6:9], 0
	global_load_dwordx4 v[170:173], v[20:21], off
	global_load_dwordx4 v[174:177], v[18:19], off
	ds_read_b128 v[18:21], v89 offset:20736
	ds_read_b128 v[158:161], v89 offset:23040
	s_waitcnt lgkmcnt(2)
	v_mfma_f32_16x16x32_bf16 v[14:17], v[14:17], v[2:5], v[10:13]
	s_nop 2
	ds_read_b128 v[10:13], v89 offset:20800
	s_waitcnt lgkmcnt(2)
	v_mfma_f32_16x16x32_bf16 v[18:21], v[18:21], v[6:9], 0
	s_nop 1
	v_mul_f32_e32 v131, 0x3e000000, v14
	v_mul_f32_e32 v136, 0x3e000000, v15
	v_max3_f32 v88, v88, v131, v136
	s_waitcnt lgkmcnt(0)
	v_mfma_f32_16x16x32_bf16 v[18:21], v[10:13], v[2:5], v[18:21]
	ds_read_b128 v[10:13], v89 offset:23104
	ds_read_b128 v[178:181], v89 offset:25344
	ds_read_b128 v[182:185], v89 offset:25408
	v_mul_f32_e32 v131, 0x3e000000, v16
	v_mfma_f32_16x16x32_bf16 v[158:161], v[158:161], v[6:9], 0
	v_mul_f32_e32 v136, 0x3e000000, v17
	v_max3_f32 v88, v88, v131, v136
	s_nop 0
	v_mul_f32_e32 v131, 0x3e000000, v18
	s_waitcnt lgkmcnt(1)
	v_mfma_f32_16x16x32_bf16 v[6:9], v[178:181], v[6:9], 0
	v_mul_f32_e32 v136, 0x3e000000, v19
	v_max3_f32 v88, v88, v131, v136
	v_mul_f32_e32 v131, 0x3e000000, v20
	v_mfma_f32_16x16x32_bf16 v[10:13], v[10:13], v[2:5], v[158:161]
	v_mul_f32_e32 v136, 0x3e000000, v21
	v_max3_f32 v88, v88, v131, v136
	s_waitcnt vmcnt(3)
	ds_write_b128 v75, v[162:165]
	s_waitcnt vmcnt(2)
	ds_write_b128 v75, v[166:169] offset:9216
	s_waitcnt lgkmcnt(2)
	v_mfma_f32_16x16x32_bf16 v[2:5], v[182:185], v[2:5], v[6:9]
	v_mul_f32_e32 v89, 0x3e000000, v10
	v_mul_f32_e32 v131, 0x3e000000, v11
	v_max3_f32 v88, v88, v89, v131
	v_mul_f32_e32 v89, 0x3e000000, v12
	v_mul_f32_e32 v131, 0x3e000000, v13
	v_max3_f32 v88, v88, v89, v131
	s_nop 1
	v_mul_f32_e32 v6, 0x3e000000, v2
	v_mul_f32_e32 v7, 0x3e000000, v3
	v_max3_f32 v6, v88, v6, v7
	v_mul_f32_e32 v7, 0x3e000000, v4
	v_mul_f32_e32 v8, 0x3e000000, v5
	v_max3_f32 v6, v6, v7, v8
	v_cndmask_b32_e32 v7, v82, v83, vcc
	v_lshlrev_b32_e32 v88, 2, v7
	ds_bpermute_b32 v7, v88, v6
	v_cmp_lt_i32_e32 vcc, v85, v84
	v_lshl_add_u32 v8, v90, 1, v156
	s_waitcnt lgkmcnt(0)
	s_barrier
	v_max_f32_e32 v7, v7, v7
	v_max_f32_e32 v6, v6, v7
	v_cndmask_b32_e32 v7, v82, v85, vcc
	v_lshlrev_b32_e32 v89, 2, v7
	ds_bpermute_b32 v7, v89, v6
	s_waitcnt lgkmcnt(0)
	ds_read2_b64 v[158:161], v8 offset1:4
	v_max_f32_e32 v7, v7, v7
	v_max_f32_e32 v136, v6, v7
	v_sub_f32_e32 v6, v92, v136
	v_mul_f32_e32 v6, 0x3fb8aa3b, v6
	v_exp_f32_e32 v131, v6
	v_sub_f32_e32 v6, v96, v136
	v_mul_f32_e32 v6, 0x3fb8aa3b, v6
	v_exp_f32_e32 v92, v6
	v_sub_f32_e32 v6, v91, v136
	v_mul_f32_e32 v6, 0x3fb8aa3b, v6
	v_exp_f32_e32 v96, v6
	v_sub_f32_e32 v6, v95, v136
	v_mul_f32_e32 v6, 0x3fb8aa3b, v6
	v_exp_f32_e32 v91, v6
	v_sub_f32_e32 v6, v94, v136
	v_mul_f32_e32 v6, 0x3fb8aa3b, v6
	v_exp_f32_e32 v95, v6
	v_sub_f32_e32 v6, v99, v136
	v_mul_f32_e32 v6, 0x3fb8aa3b, v6
	v_exp_f32_e32 v94, v6
	v_sub_f32_e32 v6, v93, v136
	v_mul_f32_e32 v6, 0x3fb8aa3b, v6
	v_exp_f32_e32 v99, v6
	v_sub_f32_e32 v6, v97, v136
	v_mul_f32_e32 v6, 0x3fb8aa3b, v6
	v_exp_f32_e32 v93, v6
	v_cvt_pk_bf16_f32 v162, v131, v96
	v_cvt_pk_bf16_f32 v163, v95, v99
	v_cvt_pk_bf16_f32 v164, v92, v91
	v_cvt_pk_bf16_f32 v165, v94, v93
	v_add_u32_e32 v7, 0x800, v8
	v_add_u32_e32 v6, 0x1000, v8
	s_waitcnt lgkmcnt(0)
	v_mfma_f32_16x16x32_bf16 v[182:185], v[158:161], v[162:165], 0
	v_lshl_add_u64 v[158:159], v[86:87], 0, v[70:71]
	ds_read2_b64 v[166:169], v7 offset0:32 offset1:36
	ds_read2_b64 v[178:181], v6 offset0:64 offset1:68
	v_lshl_add_u64 v[86:87], v[86:87], 0, v[80:81]
	global_load_dwordx4 v[186:189], v[158:159], off
	global_load_dwordx4 v[190:193], v[86:87], off
	v_sub_f32_e32 v9, v100, v136
	v_mul_f32_e32 v9, 0x3fb8aa3b, v9
	v_add_u32_e32 v158, 0x1800, v8
	v_exp_f32_e32 v86, v9
	v_sub_f32_e32 v9, v105, v136
	ds_read2_b64 v[194:197], v158 offset0:96 offset1:100
	v_mul_f32_e32 v9, 0x3fb8aa3b, v9
	v_exp_f32_e32 v76, v9
	v_sub_f32_e32 v9, v98, v136
	v_mul_f32_e32 v9, 0x3fb8aa3b, v9
	v_exp_f32_e32 v90, v9
	v_sub_f32_e32 v9, v103, v136
	v_mul_f32_e32 v9, 0x3fb8aa3b, v9
	v_exp_f32_e32 v87, v9
	v_sub_f32_e32 v9, v102, v136
	v_mul_f32_e32 v9, 0x3fb8aa3b, v9
	v_exp_f32_e32 v98, v9
	v_sub_f32_e32 v9, v109, v136
	v_mul_f32_e32 v9, 0x3fb8aa3b, v9
	v_add_u32_e32 v160, 0x4800, v8
	s_waitcnt lgkmcnt(2)
	v_mfma_f32_16x16x32_bf16 v[166:169], v[166:169], v[162:165], 0
	s_waitcnt vmcnt(3)
	ds_write_b128 v75, v[170:173] offset:18432
	s_waitcnt vmcnt(2)
	ds_write_b128 v75, v[174:177] offset:27648
	s_waitcnt lgkmcnt(0)
	s_barrier
; #define LAS __attribute__((address_space(3)))
; __device__ __forceinline__ unsigned cvt_pk_bf16(float lo, float hi) { const float __attribute__((ext_vector_type(2))) v = {lo, hi}; return __builtin_bit_cast(unsigned, __builtin_convertvector(v, bf16x2_t)); }
; template <bool LOCAL>
; __device__ __forceinline__ void na_unit(const bf16* P, const bf16* VT, bf16* YCAT, const LAS float* rpb_l, LAS bf16* buf, int b, int gr, int hp, int qblk, int tid) {
;     ...
;             if (LOCAL && c < 8) {
;                 float p[8];
; #pragma unroll
;                 for (int e = 0; e < 4; ++e) { p[e] = __expf(sl[2 * (c < 8 ? c : 0)][e] - m); p[4 + e] = __expf(sl[2 * (c < 8 ? c : 0) + 1][e] - m); }
; #pragma unroll
;                 for (int e = 0; e < 8; ++e) lsum += p[e];
;                 const bf16x8 pf = __builtin_bit_cast(bf16x8, (v4u){pg8::cvt_pk_bf16(p[0], p[1]), pg8::cvt_pk_bf16(p[2], p[3]), pg8::cvt_pk_bf16(p[4], p[5]), pg8::cvt_pk_bf16(p[6], p[7])});
; #pragma unroll
;                 for (int dt = 0; dt < 4; ++dt) { const LAS bf16* vp = cb + (16 * dt + fr) * 72 + kc0 + 4 * fq;
;                     o[dt] = __builtin_amdgcn_mfma_f32_16x16x32_bf16(frag44(vp, vp + 16), pf, o[dt], 0, 0, 0); }
;             } else {
;                 const int cc = c - NLOC;
; #pragma unroll
;                 for (int p2 = 0; p2 < 2; ++p2) {
;                     float p[8];
; #pragma unroll
;                     for (int e = 0; e < 4; ++e) { p[e] = __expf(sc[4 * (cc >= 0 ? cc : 0) + 2 * p2][e] - m); p[4 + e] = __expf(sc[4 * (cc >= 0 ? cc : 0) + 2 * p2 + 1][e] - m); }
; #pragma unroll
;                     for (int e = 0; e < 8; ++e) lsum += p[e];
;                     const bf16x8 pf = __builtin_bit_cast(bf16x8, (v4u){pg8::cvt_pk_bf16(p[0], p[1]), pg8::cvt_pk_bf16(p[2], p[3]), pg8::cvt_pk_bf16(p[4], p[5]), pg8::cvt_pk_bf16(p[6], p[7])});
; #pragma unroll
;                     for (int dt = 0; dt < 4; ++dt) { const LAS bf16* vp = cb + (16 * dt + fr) * 72 + 32 * p2 + 4 * fq;
;                         o[dt] = __builtin_amdgcn_mfma_f32_16x16x32_bf16(frag44(vp, vp + 16), pf, o[dt], 0, 0, 0); }
;                 }
;             }
;         }
;         if (sidx + 1 < 2 * NCH) NA_STORE(sidx + 1);
;         __syncthreads();
	v_mfma_f32_16x16x32_bf16 v[178:181], v[178:181], v[162:165], 0
	v_exp_f32_e32 v97, v9
	v_sub_f32_e32 v9, v101, v136
	v_mfma_f32_16x16x32_bf16 v[194:197], v[194:197], v[162:165], 0
	ds_read2_b64 v[162:165], v160 offset1:4
	v_add_u32_e32 v159, 0x5000, v8
	v_mul_f32_e32 v9, 0x3fb8aa3b, v9
	ds_read2_b64 v[170:173], v159 offset0:32 offset1:36
	v_exp_f32_e32 v100, v9
	v_sub_f32_e32 v9, v107, v136
	v_mul_f32_e32 v9, 0x3fb8aa3b, v9
	v_exp_f32_e32 v101, v9
	v_cvt_pk_bf16_f32 v174, v86, v90
	v_cvt_pk_bf16_f32 v175, v98, v100
	v_cvt_pk_bf16_f32 v176, v76, v87
	v_cvt_pk_bf16_f32 v177, v97, v101
	v_lshl_add_u64 v[102:103], s[0:1], 1, v[78:79]
	v_add_u32_e32 v161, 0x5800, v8
	s_waitcnt lgkmcnt(1)
	v_mfma_f32_16x16x32_bf16 v[182:185], v[162:165], v[174:177], v[182:185]
	v_lshl_add_u64 v[162:163], v[102:103], 0, v[70:71]
	v_lshl_add_u64 v[102:103], v[102:103], 0, v[80:81]
	v_sub_f32_e32 v9, v106, v136
	s_waitcnt lgkmcnt(0)
	v_mfma_f32_16x16x32_bf16 v[164:167], v[170:173], v[174:177], v[166:169]
	v_mul_f32_e32 v9, 0x3fb8aa3b, v9
	v_fma_f32 v62, v62, s71, -v136
	v_fma_f32 v63, v63, s71, -v136
	ds_read2_b64 v[168:171], v161 offset0:64 offset1:68
	global_load_dwordx4 v[198:201], v[162:163], off
	global_load_dwordx4 v[202:205], v[102:103], off
	v_add_u32_e32 v162, 0x6000, v8
	v_exp_f32_e32 v103, v9
	v_sub_f32_e32 v9, v113, v136
	s_waitcnt lgkmcnt(0)
	v_mfma_f32_16x16x32_bf16 v[168:171], v[168:171], v[174:177], v[178:181]
	s_nop 2
	ds_read2_b64 v[178:181], v162 offset0:96 offset1:100
	v_mul_f32_e32 v9, 0x3fb8aa3b, v9
	v_exp_f32_e32 v102, v9
	v_sub_f32_e32 v9, v104, v136
	v_mul_f32_e32 v9, 0x3fb8aa3b, v9
	v_exp_f32_e32 v105, v9
	v_sub_f32_e32 v9, v111, v136
	v_mul_f32_e32 v9, 0x3fb8aa3b, v9
	v_exp_f32_e32 v104, v9
	v_sub_f32_e32 v9, v110, v136
	v_mul_f32_e32 v9, 0x3fb8aa3b, v9
	v_exp_f32_e32 v107, v9
	v_sub_f32_e32 v9, v116, v136
	v_mul_f32_e32 v9, 0x3fb8aa3b, v9
	s_waitcnt lgkmcnt(0)
	v_mfma_f32_16x16x32_bf16 v[172:175], v[178:181], v[174:177], v[194:197]
	s_waitcnt vmcnt(3)
	ds_write_b128 v75, v[186:189]
	s_waitcnt vmcnt(2)
	ds_write_b128 v75, v[190:193] offset:9216
	s_waitcnt lgkmcnt(0)
	s_barrier
	v_exp_f32_e32 v106, v9
	v_sub_f32_e32 v9, v108, v136
	ds_read2_b64 v[176:179], v8 offset1:4
	v_mul_f32_e32 v9, 0x3fb8aa3b, v9
	v_exp_f32_e32 v108, v9
	v_sub_f32_e32 v9, v112, v136
	v_mul_f32_e32 v9, 0x3fb8aa3b, v9
	v_exp_f32_e32 v109, v9
	v_lshl_add_u64 v[190:191], s[18:19], 1, v[78:79]
	v_cvt_pk_bf16_f32 v186, v103, v105
	v_cvt_pk_bf16_f32 v187, v107, v108
	v_cvt_pk_bf16_f32 v188, v102, v104
	v_cvt_pk_bf16_f32 v189, v106, v109
	v_lshl_add_u64 v[194:195], v[190:191], 0, v[80:81]
	ds_read2_b64 v[110:113], v7 offset0:32 offset1:36
	s_waitcnt lgkmcnt(1)
	v_mfma_f32_16x16x32_bf16 v[176:179], v[176:179], v[186:189], v[182:185]
	v_sub_f32_e32 v9, v115, v136
	v_mul_f32_e32 v9, 0x3fb8aa3b, v9
	v_fma_f32 v64, v64, s71, -v136
	v_lshl_add_u64 v[184:185], v[190:191], 0, v[70:71]
	ds_read2_b64 v[180:183], v6 offset0:64 offset1:68
	global_load_dwordx4 v[190:193], v[184:185], off
	s_nop 0
	global_load_dwordx4 v[194:197], v[194:195], off
	s_waitcnt lgkmcnt(1)
	v_mfma_f32_16x16x32_bf16 v[164:167], v[110:113], v[186:189], v[164:167]
	ds_read2_b64 v[110:113], v158 offset0:96 offset1:100
	s_waitcnt vmcnt(3)
	ds_write_b128 v75, v[198:201] offset:18432
	s_waitcnt vmcnt(2)
	ds_write_b128 v75, v[202:205] offset:27648
	s_waitcnt lgkmcnt(2)
	v_mfma_f32_16x16x32_bf16 v[172:175], v[110:113], v[186:189], v[172:175]
	v_exp_f32_e32 v111, v9
	v_sub_f32_e32 v9, v121, v136
	v_mul_f32_e32 v9, 0x3fb8aa3b, v9
	v_exp_f32_e32 v110, v9
	v_sub_f32_e32 v9, v114, v136
	v_mul_f32_e32 v9, 0x3fb8aa3b, v9
	v_exp_f32_e32 v113, v9
	v_sub_f32_e32 v9, v119, v136
	v_mul_f32_e32 v9, 0x3fb8aa3b, v9
	v_exp_f32_e32 v112, v9
	v_sub_f32_e32 v9, v118, v136
	v_mul_f32_e32 v9, 0x3fb8aa3b, v9
	v_exp_f32_e32 v115, v9
	v_sub_f32_e32 v9, v124, v136
	v_mul_f32_e32 v9, 0x3fb8aa3b, v9
	v_exp_f32_e32 v114, v9
	v_sub_f32_e32 v9, v117, v136
	v_mul_f32_e32 v9, 0x3fb8aa3b, v9
	v_mfma_f32_16x16x32_bf16 v[168:171], v[180:183], v[186:189], v[168:171]
	s_waitcnt lgkmcnt(0)
	s_barrier
	v_exp_f32_e32 v116, v9
	ds_read2_b64 v[180:183], v160 offset1:4
	v_sub_f32_e32 v9, v120, v136
	ds_read2_b64 v[118:121], v159 offset0:32 offset1:36
	v_mul_f32_e32 v9, 0x3fb8aa3b, v9
	v_exp_f32_e32 v117, v9
	v_lshl_add_u64 v[188:189], s[20:21], 1, v[78:79]
	v_lshl_add_u64 v[198:199], v[188:189], 0, v[70:71]
	v_cvt_pk_bf16_f32 v184, v111, v113
	v_cvt_pk_bf16_f32 v185, v115, v116
	v_cvt_pk_bf16_f32 v186, v110, v112
	v_cvt_pk_bf16_f32 v187, v114, v117
	v_lshl_add_u64 v[188:189], v[188:189], 0, v[80:81]
	v_sub_f32_e32 v9, v123, v136
	s_waitcnt lgkmcnt(1)
	v_mfma_f32_16x16x32_bf16 v[176:179], v[180:183], v[184:187], v[176:179]
	global_load_dwordx4 v[180:183], v[198:199], off
	s_nop 0
	global_load_dwordx4 v[198:201], v[188:189], off
	v_mul_f32_e32 v9, 0x3fb8aa3b, v9
	v_fma_f32 v65, v65, s71, -v136
	s_waitcnt lgkmcnt(0)
	v_mfma_f32_16x16x32_bf16 v[164:167], v[118:121], v[184:187], v[164:167]
	ds_read2_b64 v[118:121], v161 offset0:64 offset1:68
	v_mul_f32_e32 v62, 0x3fb8aa3b, v62
	v_mul_f32_e32 v63, 0x3fb8aa3b, v63
	s_waitcnt lgkmcnt(0)
	v_mfma_f32_16x16x32_bf16 v[168:171], v[118:121], v[184:187], v[168:171]
	ds_read2_b64 v[118:121], v162 offset0:96 offset1:100
	s_waitcnt vmcnt(3)
	ds_write_b128 v75, v[190:193]
	s_waitcnt vmcnt(2)
	ds_write_b128 v75, v[194:197] offset:9216
	s_waitcnt lgkmcnt(0)
	v_mfma_f32_16x16x32_bf16 v[172:175], v[118:121], v[184:187], v[172:175]
	v_exp_f32_e32 v119, v9
	v_sub_f32_e32 v9, v129, v136
	v_mul_f32_e32 v9, 0x3fb8aa3b, v9
	v_exp_f32_e32 v118, v9
	v_sub_f32_e32 v9, v122, v136
	v_mul_f32_e32 v9, 0x3fb8aa3b, v9
	v_exp_f32_e32 v121, v9
	v_sub_f32_e32 v9, v127, v136
	v_mul_f32_e32 v9, 0x3fb8aa3b, v9
	v_exp_f32_e32 v120, v9
	v_sub_f32_e32 v9, v126, v136
	v_mul_f32_e32 v9, 0x3fb8aa3b, v9
	v_exp_f32_e32 v123, v9
	v_sub_f32_e32 v9, v133, v136
	v_mul_f32_e32 v9, 0x3fb8aa3b, v9
	s_barrier
; #define LAS __attribute__((address_space(3)))
; __device__ __forceinline__ unsigned cvt_pk_bf16(float lo, float hi) { const float __attribute__((ext_vector_type(2))) v = {lo, hi}; return __builtin_bit_cast(unsigned, __builtin_convertvector(v, bf16x2_t)); }
; template <bool LOCAL>
; __device__ __forceinline__ void na_unit(const bf16* P, const bf16* VT, bf16* YCAT, const LAS float* rpb_l, LAS bf16* buf, int b, int gr, int hp, int qblk, int tid) {
;     ...
;             if (LOCAL && c < 8) {
;                 float p[8];
; #pragma unroll
;                 for (int e = 0; e < 4; ++e) { p[e] = __expf(sl[2 * (c < 8 ? c : 0)][e] - m); p[4 + e] = __expf(sl[2 * (c < 8 ? c : 0) + 1][e] - m); }
; #pragma unroll
;                 for (int e = 0; e < 8; ++e) lsum += p[e];
;                 const bf16x8 pf = __builtin_bit_cast(bf16x8, (v4u){pg8::cvt_pk_bf16(p[0], p[1]), pg8::cvt_pk_bf16(p[2], p[3]), pg8::cvt_pk_bf16(p[4], p[5]), pg8::cvt_pk_bf16(p[6], p[7])});
; #pragma unroll
;                 for (int dt = 0; dt < 4; ++dt) { const LAS bf16* vp = cb + (16 * dt + fr) * 72 + kc0 + 4 * fq;
;                     o[dt] = __builtin_amdgcn_mfma_f32_16x16x32_bf16(frag44(vp, vp + 16), pf, o[dt], 0, 0, 0); }
;             } else {
;                 const int cc = c - NLOC;
; #pragma unroll
;                 for (int p2 = 0; p2 < 2; ++p2) {
;                     float p[8];
; #pragma unroll
;                     for (int e = 0; e < 4; ++e) { p[e] = __expf(sc[4 * (cc >= 0 ? cc : 0) + 2 * p2][e] - m); p[4 + e] = __expf(sc[4 * (cc >= 0 ? cc : 0) + 2 * p2 + 1][e] - m); }
; #pragma unroll
;                     for (int e = 0; e < 8; ++e) lsum += p[e];
;                     const bf16x8 pf = __builtin_bit_cast(bf16x8, (v4u){pg8::cvt_pk_bf16(p[0], p[1]), pg8::cvt_pk_bf16(p[2], p[3]), pg8::cvt_pk_bf16(p[4], p[5]), pg8::cvt_pk_bf16(p[6], p[7])});
; #pragma unroll
;                     for (int dt = 0; dt < 4; ++dt) { const LAS bf16* vp = cb + (16 * dt + fr) * 72 + 32 * p2 + 4 * fq;
;                         o[dt] = __builtin_amdgcn_mfma_f32_16x16x32_bf16(frag44(vp, vp + 16), pf, o[dt], 0, 0, 0); }
;                 }
;             }
;         }
;         if (sidx + 1 < 2 * NCH) NA_STORE(sidx + 1);
;         __syncthreads();
	v_exp_f32_e32 v122, v9
	v_sub_f32_e32 v9, v125, v136
	ds_read2_b64 v[184:187], v8 offset1:4
	v_mul_f32_e32 v9, 0x3fb8aa3b, v9
	v_exp_f32_e32 v124, v9
	v_sub_f32_e32 v9, v128, v136
	v_mul_f32_e32 v9, 0x3fb8aa3b, v9
	v_exp_f32_e32 v125, v9
	v_lshl_add_u64 v[192:193], s[22:23], 1, v[78:79]
	v_cvt_pk_bf16_f32 v188, v119, v121
	v_cvt_pk_bf16_f32 v189, v123, v124
	v_cvt_pk_bf16_f32 v190, v118, v120
	v_cvt_pk_bf16_f32 v191, v122, v125
	v_lshl_add_u64 v[194:195], v[192:193], 0, v[70:71]
	ds_read2_b64 v[126:129], v7 offset0:32 offset1:36
	s_waitcnt lgkmcnt(1)
	v_mfma_f32_16x16x32_bf16 v[176:179], v[184:187], v[188:191], v[176:179]
	ds_read2_b64 v[184:187], v6 offset0:64 offset1:68
	v_lshl_add_u64 v[196:197], v[192:193], 0, v[80:81]
	global_load_dwordx4 v[192:195], v[194:195], off
	s_nop 0
	global_load_dwordx4 v[202:205], v[196:197], off
	s_waitcnt lgkmcnt(1)
	v_mfma_f32_16x16x32_bf16 v[164:167], v[126:129], v[188:191], v[164:167]
	ds_read2_b64 v[126:129], v158 offset0:96 offset1:100
	v_sub_f32_e32 v9, v132, v136
	v_mul_f32_e32 v9, 0x3fb8aa3b, v9
	s_waitcnt lgkmcnt(0)
	v_mfma_f32_16x16x32_bf16 v[172:175], v[126:129], v[188:191], v[172:175]
	v_exp_f32_e32 v127, v9
	v_sub_f32_e32 v9, v139, v136
	v_mul_f32_e32 v9, 0x3fb8aa3b, v9
	v_exp_f32_e32 v126, v9
	v_sub_f32_e32 v9, v130, v136
	v_mul_f32_e32 v9, 0x3fb8aa3b, v9
	v_exp_f32_e32 v129, v9
	v_sub_f32_e32 v9, v137, v136
	v_mul_f32_e32 v9, 0x3fb8aa3b, v9
	v_exp_f32_e32 v128, v9
	v_sub_f32_e32 v9, v135, v136
	v_mul_f32_e32 v9, 0x3fb8aa3b, v9
	v_exp_f32_e32 v132, v9
	v_sub_f32_e32 v9, v142, v136
	v_mul_f32_e32 v9, 0x3fb8aa3b, v9
	v_mfma_f32_16x16x32_bf16 v[168:171], v[184:187], v[188:191], v[168:171]
	s_waitcnt vmcnt(3)
	ds_write_b128 v75, v[180:183] offset:18432
	s_waitcnt vmcnt(2)
	ds_write_b128 v75, v[198:201] offset:27648
	s_waitcnt lgkmcnt(0)
	s_barrier
	v_exp_f32_e32 v130, v9
	v_sub_f32_e32 v9, v134, v136
	ds_read2_b64 v[180:183], v160 offset1:4
	ds_read2_b64 v[184:187], v159 offset0:32 offset1:36
	v_mul_f32_e32 v9, 0x3fb8aa3b, v9
	v_exp_f32_e32 v133, v9
	v_sub_f32_e32 v9, v138, v136
	v_mul_f32_e32 v9, 0x3fb8aa3b, v9
	v_exp_f32_e32 v134, v9
	v_lshl_add_u64 v[196:197], s[24:25], 1, v[78:79]
	v_lshl_add_u64 v[198:199], v[196:197], 0, v[70:71]
	v_cvt_pk_bf16_f32 v188, v127, v129
	v_cvt_pk_bf16_f32 v189, v132, v133
	v_cvt_pk_bf16_f32 v190, v126, v128
	v_cvt_pk_bf16_f32 v191, v130, v134
	v_lshl_add_u64 v[138:139], v[196:197], 0, v[80:81]
	v_sub_f32_e32 v9, v141, v136
	s_waitcnt lgkmcnt(1)
	v_mfma_f32_16x16x32_bf16 v[176:179], v[180:183], v[188:191], v[176:179]
	global_load_dwordx4 v[180:183], v[198:199], off
	s_nop 0
	global_load_dwordx4 v[196:199], v[138:139], off
	v_mul_f32_e32 v9, 0x3fb8aa3b, v9
	v_exp_f32_e32 v137, v9
	s_waitcnt lgkmcnt(0)
	v_mfma_f32_16x16x32_bf16 v[164:167], v[184:187], v[188:191], v[164:167]
	ds_read2_b64 v[184:187], v161 offset0:64 offset1:68
	v_sub_f32_e32 v9, v147, v136
	v_mul_f32_e32 v9, 0x3fb8aa3b, v9
	s_waitcnt lgkmcnt(0)
	v_mfma_f32_16x16x32_bf16 v[168:171], v[184:187], v[188:191], v[168:171]
	ds_read2_b64 v[184:187], v162 offset0:96 offset1:100
	v_exp_f32_e32 v135, v9
	v_sub_f32_e32 v9, v140, v136
	v_mul_f32_e32 v9, 0x3fb8aa3b, v9
	v_exp_f32_e32 v139, v9
	v_sub_f32_e32 v9, v145, v136
	v_mul_f32_e32 v9, 0x3fb8aa3b, v9
	v_exp_f32_e32 v138, v9
	v_sub_f32_e32 v9, v144, v136
	v_mul_f32_e32 v9, 0x3fb8aa3b, v9
	s_waitcnt lgkmcnt(0)
	v_mfma_f32_16x16x32_bf16 v[172:175], v[184:187], v[188:191], v[172:175]
	s_waitcnt vmcnt(3)
	ds_write_b128 v75, v[192:195]
	s_waitcnt vmcnt(2)
	ds_write_b128 v75, v[202:205] offset:9216
	s_waitcnt lgkmcnt(0)
	s_barrier
	v_exp_f32_e32 v141, v9
	v_sub_f32_e32 v9, v150, v136
	ds_read2_b64 v[184:187], v8 offset1:4
	v_mul_f32_e32 v9, 0x3fb8aa3b, v9
	ds_read2_b64 v[188:191], v7 offset0:32 offset1:36
	v_exp_f32_e32 v140, v9
	v_sub_f32_e32 v9, v143, v136
	v_sub_f32_e32 v8, v146, v136
	v_mul_f32_e32 v9, 0x3fb8aa3b, v9
	v_mul_f32_e32 v8, 0x3fb8aa3b, v8
	v_exp_f32_e32 v142, v9
	v_exp_f32_e32 v143, v8
	v_cvt_pk_bf16_f32 v144, v137, v139
	v_cvt_pk_bf16_f32 v146, v135, v138
	v_cvt_pk_bf16_f32 v145, v141, v142
	v_cvt_pk_bf16_f32 v147, v140, v143
	v_lshl_add_u64 v[8:9], s[26:27], 1, v[78:79]
	v_mul_f32_e32 v64, 0x3fb8aa3b, v64
	s_waitcnt lgkmcnt(1)
	v_mfma_f32_16x16x32_bf16 v[176:179], v[184:187], v[144:147], v[176:179]
	ds_read2_b64 v[184:187], v6 offset0:64 offset1:68
	v_lshl_add_u64 v[6:7], v[8:9], 0, v[70:71]
	v_lshl_add_u64 v[8:9], v[8:9], 0, v[80:81]
	s_waitcnt lgkmcnt(1)
	v_mfma_f32_16x16x32_bf16 v[164:167], v[188:191], v[144:147], v[164:167]
	global_load_dwordx4 v[188:191], v[6:7], off
	global_load_dwordx4 v[192:195], v[8:9], off
	ds_read2_b64 v[78:81], v158 offset0:96 offset1:100
	s_waitcnt vmcnt(3)
	ds_write_b128 v75, v[180:183] offset:18432
	s_waitcnt vmcnt(2)
	ds_write_b128 v75, v[196:199] offset:27648
	s_waitcnt lgkmcnt(3)
	v_mfma_f32_16x16x32_bf16 v[168:171], v[184:187], v[144:147], v[168:171]
	s_waitcnt lgkmcnt(0)
	s_barrier
; #define LAS __attribute__((address_space(3)))
; __device__ __forceinline__ unsigned cvt_pk_bf16(float lo, float hi) { const float __attribute__((ext_vector_type(2))) v = {lo, hi}; return __builtin_bit_cast(unsigned, __builtin_convertvector(v, bf16x2_t)); }
; template <bool LOCAL>
; __device__ __forceinline__ void na_unit(const bf16* P, const bf16* VT, bf16* YCAT, const LAS float* rpb_l, LAS bf16* buf, int b, int gr, int hp, int qblk, int tid) {
;     ...
;             if (LOCAL && c < 8) {
;                 float p[8];
; #pragma unroll
;                 for (int e = 0; e < 4; ++e) { p[e] = __expf(sl[2 * (c < 8 ? c : 0)][e] - m); p[4 + e] = __expf(sl[2 * (c < 8 ? c : 0) + 1][e] - m); }
; #pragma unroll
;                 for (int e = 0; e < 8; ++e) lsum += p[e];
;                 const bf16x8 pf = __builtin_bit_cast(bf16x8, (v4u){pg8::cvt_pk_bf16(p[0], p[1]), pg8::cvt_pk_bf16(p[2], p[3]), pg8::cvt_pk_bf16(p[4], p[5]), pg8::cvt_pk_bf16(p[6], p[7])});
; #pragma unroll
;                 for (int dt = 0; dt < 4; ++dt) { const LAS bf16* vp = cb + (16 * dt + fr) * 72 + kc0 + 4 * fq;
;                     o[dt] = __builtin_amdgcn_mfma_f32_16x16x32_bf16(frag44(vp, vp + 16), pf, o[dt], 0, 0, 0); }
;             } else {
;                 const int cc = c - NLOC;
; #pragma unroll
;                 for (int p2 = 0; p2 < 2; ++p2) {
;                     float p[8];
; #pragma unroll
;                     for (int e = 0; e < 4; ++e) { p[e] = __expf(sc[4 * (cc >= 0 ? cc : 0) + 2 * p2][e] - m); p[4 + e] = __expf(sc[4 * (cc >= 0 ? cc : 0) + 2 * p2 + 1][e] - m); }
; #pragma unroll
;                     for (int e = 0; e < 8; ++e) lsum += p[e];
;                     const bf16x8 pf = __builtin_bit_cast(bf16x8, (v4u){pg8::cvt_pk_bf16(p[0], p[1]), pg8::cvt_pk_bf16(p[2], p[3]), pg8::cvt_pk_bf16(p[4], p[5]), pg8::cvt_pk_bf16(p[6], p[7])});
; #pragma unroll
;                     for (int dt = 0; dt < 4; ++dt) { const LAS bf16* vp = cb + (16 * dt + fr) * 72 + 32 * p2 + 4 * fq;
;                         o[dt] = __builtin_amdgcn_mfma_f32_16x16x32_bf16(frag44(vp, vp + 16), pf, o[dt], 0, 0, 0); }
;                 }
	v_mfma_f32_16x16x32_bf16 v[172:175], v[78:81], v[144:147], v[172:175]
	v_sub_f32_e32 v70, v149, v136
	v_sub_f32_e32 v79, v148, v136
	v_sub_f32_e32 v81, v152, v136
	v_sub_f32_e32 v145, v151, v136
	ds_read2_b64 v[148:151], v160 offset1:4
	v_mul_f32_e32 v70, 0x3fb8aa3b, v70
	v_mul_f32_e32 v79, 0x3fb8aa3b, v79
	v_mul_f32_e32 v81, 0x3fb8aa3b, v81
	v_mul_f32_e32 v145, 0x3fb8aa3b, v145
	v_exp_f32_e32 v78, v70
	v_sub_f32_e32 v70, v155, v136
	v_exp_f32_e32 v80, v79
	v_sub_f32_e32 v79, v153, v136
	v_exp_f32_e32 v144, v81
	v_sub_f32_e32 v81, v157, v136
	v_exp_f32_e32 v146, v145
	v_sub_f32_e32 v145, v154, v136
	v_mul_f32_e32 v70, 0x3fb8aa3b, v70
	v_mul_f32_e32 v79, 0x3fb8aa3b, v79
	v_mul_f32_e32 v81, 0x3fb8aa3b, v81
	v_mul_f32_e32 v145, 0x3fb8aa3b, v145
	v_exp_f32_e32 v70, v70
	v_exp_f32_e32 v79, v79
	v_exp_f32_e32 v81, v81
	v_exp_f32_e32 v145, v145
	v_cvt_pk_bf16_f32 v152, v78, v80
	v_cvt_pk_bf16_f32 v153, v144, v146
	v_cvt_pk_bf16_f32 v154, v70, v79
	v_cvt_pk_bf16_f32 v155, v81, v145
	v_mul_f32_e32 v65, 0x3fb8aa3b, v65
	v_exp_f32_e32 v147, v62
	s_waitcnt lgkmcnt(0)
	v_mfma_f32_16x16x32_bf16 v[148:151], v[148:151], v[152:155], v[176:179]
	v_fma_f32 v62, v66, s71, -v136
	v_exp_f32_e32 v66, v63
	v_fma_f32 v63, v67, s71, -v136
	ds_read2_b64 v[176:179], v159 offset0:32 offset1:36
	ds_read2_b64 v[158:161], v161 offset0:64 offset1:68
	s_waitcnt lgkmcnt(0)
	v_mfma_f32_16x16x32_bf16 v[158:161], v[158:161], v[152:155], v[168:171]
	s_nop 2
	ds_read2_b64 v[168:171], v162 offset0:96 offset1:100
	v_exp_f32_e32 v67, v64
	v_fma_f32 v64, v68, s71, -v136
	v_mfma_f32_16x16x32_bf16 v[164:167], v[176:179], v[152:155], v[164:167]
	global_load_dwordx4 v[176:179], v[6:7], off offset:128
	global_load_dwordx4 v[180:183], v[8:9], off offset:128
	s_waitcnt vmcnt(3)
	ds_write_b128 v75, v[188:191]
	s_waitcnt vmcnt(2)
	ds_write_b128 v75, v[192:195] offset:9216
	s_waitcnt lgkmcnt(0)
	v_mfma_f32_16x16x32_bf16 v[152:155], v[168:171], v[152:155], v[172:175]
	s_barrier
	ds_read2_b64 v[168:171], v156 offset1:4
	v_exp_f32_e32 v68, v65
	v_fma_f32 v65, v69, s71, -v136
	v_mul_f32_e32 v62, 0x3fb8aa3b, v62
	v_mul_f32_e32 v63, 0x3fb8aa3b, v63
	v_mul_f32_e32 v64, 0x3fb8aa3b, v64
	v_mul_f32_e32 v65, 0x3fb8aa3b, v65
	v_exp_f32_e32 v62, v62
	v_exp_f32_e32 v63, v63
	v_exp_f32_e32 v64, v64
	v_exp_f32_e32 v65, v65
	v_cvt_pk_bf16_f32 v172, v147, v66
	v_cvt_pk_bf16_f32 v173, v67, v68
	v_cvt_pk_bf16_f32 v174, v62, v63
	v_cvt_pk_bf16_f32 v175, v64, v65
	v_add_u32_e32 v157, 0x800, v156
	v_add_u32_e32 v192, 0x1000, v156
	s_waitcnt lgkmcnt(0)
	v_mfma_f32_16x16x32_bf16 v[148:151], v[168:171], v[172:175], v[148:151]
	ds_read2_b64 v[168:171], v157 offset0:32 offset1:36
	v_add_u32_e32 v193, 0x1800, v156
	v_fma_f32 v58, v58, s71, -v136
	s_waitcnt lgkmcnt(0)
	v_mfma_f32_16x16x32_bf16 v[162:165], v[168:171], v[172:175], v[164:167]
	s_nop 2
	ds_read2_b64 v[166:169], v192 offset0:64 offset1:68
	v_fma_f32 v54, v54, s71, -v136
	v_fma_f32 v59, v59, s71, -v136
	s_waitcnt lgkmcnt(0)
	v_mfma_f32_16x16x32_bf16 v[158:161], v[166:169], v[172:175], v[158:161]
	ds_read2_b64 v[166:169], v193 offset0:96 offset1:100
	v_fma_f32 v55, v55, s71, -v136
	v_fma_f32 v60, v60, s71, -v136
	s_waitcnt lgkmcnt(0)
	v_mfma_f32_16x16x32_bf16 v[152:155], v[166:169], v[172:175], v[152:155]
	ds_read2_b64 v[166:169], v156 offset0:8 offset1:12
	v_fma_f32 v56, v56, s71, -v136
	v_fma_f32 v61, v61, s71, -v136
	v_fma_f32 v57, v57, s71, -v136
	v_mul_f32_e32 v58, 0x3fb8aa3b, v58
	v_mul_f32_e32 v54, 0x3fb8aa3b, v54
	v_mul_f32_e32 v59, 0x3fb8aa3b, v59
	v_mul_f32_e32 v55, 0x3fb8aa3b, v55
	v_mul_f32_e32 v60, 0x3fb8aa3b, v60
	v_mul_f32_e32 v56, 0x3fb8aa3b, v56
	v_mul_f32_e32 v61, 0x3fb8aa3b, v61
	v_mul_f32_e32 v57, 0x3fb8aa3b, v57
	v_exp_f32_e32 v58, v58
	v_exp_f32_e32 v54, v54
	v_exp_f32_e32 v59, v59
	v_exp_f32_e32 v55, v55
	v_exp_f32_e32 v60, v60
	v_exp_f32_e32 v56, v56
	v_exp_f32_e32 v61, v61
	v_exp_f32_e32 v57, v57
	v_cvt_pk_bf16_f32 v170, v58, v59
	v_cvt_pk_bf16_f32 v172, v54, v55
	v_cvt_pk_bf16_f32 v171, v60, v61
	v_cvt_pk_bf16_f32 v173, v56, v57
	v_fma_f32 v46, v46, s71, -v136
	v_fma_f32 v47, v47, s71, -v136
	s_waitcnt lgkmcnt(0)
	v_mfma_f32_16x16x32_bf16 v[148:151], v[166:169], v[170:173], v[148:151]
	ds_read2_b64 v[166:169], v157 offset0:40 offset1:44
	v_fma_f32 v48, v48, s71, -v136
	v_mul_f32_e32 v46, 0x3fb8aa3b, v46
	s_waitcnt lgkmcnt(0)
	v_mfma_f32_16x16x32_bf16 v[162:165], v[166:169], v[170:173], v[162:165]
	ds_read2_b64 v[166:169], v192 offset0:72 offset1:76
	v_mul_f32_e32 v47, 0x3fb8aa3b, v47
	v_mul_f32_e32 v48, 0x3fb8aa3b, v48
	s_waitcnt lgkmcnt(0)
	v_mfma_f32_16x16x32_bf16 v[158:161], v[166:169], v[170:173], v[158:161]
	ds_read2_b64 v[166:169], v193 offset0:104 offset1:108
	v_exp_f32_e32 v69, v46
	v_fma_f32 v46, v50, s71, -v136
	v_exp_f32_e32 v50, v47
	v_fma_f32 v47, v51, s71, -v136
	v_exp_f32_e32 v51, v48
	v_fma_f32 v48, v52, s71, -v136
	v_add_u32_e32 v52, 0x4800, v156
	global_load_dwordx4 v[184:187], v[6:7], off offset:256
	global_load_dwordx4 v[188:191], v[8:9], off offset:256
	s_waitcnt lgkmcnt(0)
	v_mfma_f32_16x16x32_bf16 v[152:155], v[166:169], v[170:173], v[152:155]
	s_waitcnt vmcnt(3)
	ds_write_b128 v75, v[176:179] offset:18432
	s_waitcnt vmcnt(2)
	ds_write_b128 v75, v[180:183] offset:27648
	s_waitcnt lgkmcnt(0)
	s_barrier
; #define LAS __attribute__((address_space(3)))
; __device__ __forceinline__ unsigned cvt_pk_bf16(float lo, float hi) { const float __attribute__((ext_vector_type(2))) v = {lo, hi}; return __builtin_bit_cast(unsigned, __builtin_convertvector(v, bf16x2_t)); }
; #define NA_STORE(sidx) do { LAS bf16* d_ = buf + ((sidx) & 1) * 9216; _Pragma("unroll") for (int q_ = 0; q_ < 2; ++q_) *(LAS v4u*)(d_ + q_ * 4608 + lrow * 72 + lseg * 8) = ld[(sidx) & 1][q_]; } while (0)
; template <bool LOCAL>
; __device__ __forceinline__ void na_unit(const bf16* P, const bf16* VT, bf16* YCAT, const LAS float* rpb_l, LAS bf16* buf, int b, int gr, int hp, int qblk, int tid) {
;     ...
;             } else {
;                 const int cc = c - NLOC;
; #pragma unroll
;                 for (int p2 = 0; p2 < 2; ++p2) {
;                     float p[8];
; #pragma unroll
;                     for (int e = 0; e < 4; ++e) { p[e] = __expf(sc[4 * (cc >= 0 ? cc : 0) + 2 * p2][e] - m); p[4 + e] = __expf(sc[4 * (cc >= 0 ? cc : 0) + 2 * p2 + 1][e] - m); }
; #pragma unroll
;                     for (int e = 0; e < 8; ++e) lsum += p[e];
;                     const bf16x8 pf = __builtin_bit_cast(bf16x8, (v4u){pg8::cvt_pk_bf16(p[0], p[1]), pg8::cvt_pk_bf16(p[2], p[3]), pg8::cvt_pk_bf16(p[4], p[5]), pg8::cvt_pk_bf16(p[6], p[7])});
; #pragma unroll
;                     for (int dt = 0; dt < 4; ++dt) { const LAS bf16* vp = cb + (16 * dt + fr) * 72 + 32 * p2 + 4 * fq;
;                         o[dt] = __builtin_amdgcn_mfma_f32_16x16x32_bf16(frag44(vp, vp + 16), pf, o[dt], 0, 0, 0); }
;                 }
;             }
;         }
;         if (sidx + 1 < 2 * NCH) NA_STORE(sidx + 1);
;         __syncthreads();
	v_fma_f32 v49, v49, s71, -v136
	ds_read2_b64 v[166:169], v52 offset1:4
	v_mul_f32_e32 v49, 0x3fb8aa3b, v49
	v_exp_f32_e32 v174, v49
	v_fma_f32 v49, v53, s71, -v136
	v_mul_f32_e32 v46, 0x3fb8aa3b, v46
	v_mul_f32_e32 v47, 0x3fb8aa3b, v47
	v_mul_f32_e32 v48, 0x3fb8aa3b, v48
	v_mul_f32_e32 v49, 0x3fb8aa3b, v49
	v_exp_f32_e32 v46, v46
	v_exp_f32_e32 v47, v47
	v_exp_f32_e32 v48, v48
	v_exp_f32_e32 v53, v49
	v_cvt_pk_bf16_f32 v170, v69, v50
	v_cvt_pk_bf16_f32 v171, v51, v174
	v_cvt_pk_bf16_f32 v172, v46, v47
	v_cvt_pk_bf16_f32 v173, v48, v53
	v_add_u32_e32 v175, 0x5000, v156
	v_add_u32_e32 v176, 0x5800, v156
	s_waitcnt lgkmcnt(0)
	v_mfma_f32_16x16x32_bf16 v[148:151], v[166:169], v[170:173], v[148:151]
	ds_read2_b64 v[166:169], v175 offset0:32 offset1:36
	v_add_u32_e32 v49, 0x6000, v156
	v_fma_f32 v38, v38, s71, -v136
	s_waitcnt lgkmcnt(0)
	v_mfma_f32_16x16x32_bf16 v[162:165], v[166:169], v[170:173], v[162:165]
	ds_read2_b64 v[166:169], v176 offset0:64 offset1:68
	v_mul_f32_e32 v38, 0x3fb8aa3b, v38
	v_fma_f32 v42, v42, s71, -v136
	s_waitcnt lgkmcnt(0)
	v_mfma_f32_16x16x32_bf16 v[158:161], v[166:169], v[170:173], v[158:161]
	ds_read2_b64 v[166:169], v49 offset0:96 offset1:100
	v_mul_f32_e32 v42, 0x3fb8aa3b, v42
	v_fma_f32 v30, v30, s71, -v136
	s_waitcnt lgkmcnt(0)
	v_mfma_f32_16x16x32_bf16 v[152:155], v[166:169], v[170:173], v[152:155]
	v_exp_f32_e32 v171, v38
	v_fma_f32 v38, v43, s71, -v136
	v_mul_f32_e32 v38, 0x3fb8aa3b, v38
	v_exp_f32_e32 v172, v38
	v_fma_f32 v38, v39, s71, -v136
	v_mul_f32_e32 v38, 0x3fb8aa3b, v38
	v_exp_f32_e32 v173, v38
	v_fma_f32 v38, v44, s71, -v136
	v_mul_f32_e32 v38, 0x3fb8aa3b, v38
	v_exp_f32_e32 v177, v38
	v_fma_f32 v38, v40, s71, -v136
	v_mul_f32_e32 v38, 0x3fb8aa3b, v38
	v_exp_f32_e32 v170, v42
	v_exp_f32_e32 v178, v38
	v_fma_f32 v38, v45, s71, -v136
	ds_read2_b64 v[42:45], v52 offset0:8 offset1:12
	v_mul_f32_e32 v38, 0x3fb8aa3b, v38
	v_exp_f32_e32 v179, v38
	v_fma_f32 v38, v41, s71, -v136
	v_mul_f32_e32 v38, 0x3fb8aa3b, v38
	v_exp_f32_e32 v180, v38
	v_cvt_pk_bf16_f32 v38, v170, v172
	v_cvt_pk_bf16_f32 v39, v177, v179
	v_cvt_pk_bf16_f32 v40, v171, v173
	v_cvt_pk_bf16_f32 v41, v178, v180
	v_mul_f32_e32 v30, 0x3fb8aa3b, v30
	v_fma_f32 v22, v22, s71, -v136
	s_waitcnt lgkmcnt(0)
	v_mfma_f32_16x16x32_bf16 v[42:45], v[42:45], v[38:41], v[148:151]
	v_mul_f32_e32 v22, 0x3fb8aa3b, v22
	v_fma_f32 v26, v26, s71, -v136
	v_mul_f32_e32 v26, 0x3fb8aa3b, v26
	ds_read2_b64 v[148:151], v175 offset0:40 offset1:44
	s_waitcnt lgkmcnt(0)
	v_mfma_f32_16x16x32_bf16 v[148:151], v[148:151], v[38:41], v[162:165]
	s_nop 2
	ds_read2_b64 v[162:165], v176 offset0:72 offset1:76
	v_fma_f32 v2, v2, s71, -v136
	v_mul_f32_e32 v2, 0x3fb8aa3b, v2
	s_waitcnt lgkmcnt(0)
	v_mfma_f32_16x16x32_bf16 v[158:161], v[162:165], v[38:41], v[158:161]
	ds_read2_b64 v[162:165], v49 offset0:104 offset1:108
	global_load_dwordx4 v[166:169], v[6:7], off offset:384
	s_nop 0
	global_load_dwordx4 v[6:9], v[8:9], off offset:384
	s_waitcnt vmcnt(3)
	ds_write_b128 v75, v[184:187]
	s_waitcnt vmcnt(2)
	ds_write_b128 v75, v[188:191] offset:9216
	s_waitcnt lgkmcnt(2)
	v_mfma_f32_16x16x32_bf16 v[38:41], v[162:165], v[38:41], v[152:155]
	v_exp_f32_e32 v162, v30
	v_fma_f32 v30, v34, s71, -v136
	v_mul_f32_e32 v30, 0x3fb8aa3b, v30
	v_exp_f32_e32 v163, v30
	v_fma_f32 v30, v31, s71, -v136
	v_mul_f32_e32 v30, 0x3fb8aa3b, v30
	v_exp_f32_e32 v164, v30
	v_fma_f32 v30, v35, s71, -v136
	v_mul_f32_e32 v30, 0x3fb8aa3b, v30
	v_exp_f32_e32 v165, v30
	v_fma_f32 v30, v32, s71, -v136
	v_mul_f32_e32 v30, 0x3fb8aa3b, v30
	v_exp_f32_e32 v181, v30
	v_fma_f32 v30, v36, s71, -v136
	v_mul_f32_e32 v30, 0x3fb8aa3b, v30
	v_exp_f32_e32 v182, v30
	v_fma_f32 v30, v33, s71, -v136
	s_waitcnt lgkmcnt(0)
	s_barrier
	v_mul_f32_e32 v34, 0x3fb8aa3b, v30
	ds_read2_b64 v[30:33], v156 offset1:4
	v_exp_f32_e32 v183, v34
	v_fma_f32 v34, v37, s71, -v136
	v_mul_f32_e32 v34, 0x3fb8aa3b, v34
	v_exp_f32_e32 v184, v34
	v_cvt_pk_bf16_f32 v34, v162, v164
	v_cvt_pk_bf16_f32 v35, v181, v183
	v_cvt_pk_bf16_f32 v36, v163, v165
	v_cvt_pk_bf16_f32 v37, v182, v184
	ds_read2_b64 v[152:155], v193 offset0:96 offset1:100
	v_fma_f32 v10, v10, s71, -v136
	s_waitcnt lgkmcnt(1)
	v_mfma_f32_16x16x32_bf16 v[30:33], v[30:33], v[34:37], v[42:45]
	v_mul_f32_e32 v10, 0x3fb8aa3b, v10
	s_nop 1
	ds_read2_b64 v[42:45], v157 offset0:32 offset1:36
	s_waitcnt lgkmcnt(0)
	v_mfma_f32_16x16x32_bf16 v[42:45], v[42:45], v[34:37], v[148:151]
	s_nop 2
	ds_read2_b64 v[148:151], v192 offset0:64 offset1:68
	s_waitcnt lgkmcnt(0)
	v_mfma_f32_16x16x32_bf16 v[148:151], v[148:151], v[34:37], v[158:161]
	v_mfma_f32_16x16x32_bf16 v[34:37], v[152:155], v[34:37], v[38:41]
	v_exp_f32_e32 v153, v22
	v_fma_f32 v22, v27, s71, -v136
	v_mul_f32_e32 v22, 0x3fb8aa3b, v22
	v_exp_f32_e32 v154, v22
	v_fma_f32 v22, v23, s71, -v136
	v_mul_f32_e32 v22, 0x3fb8aa3b, v22
	v_exp_f32_e32 v155, v22
	v_fma_f32 v22, v28, s71, -v136
	v_mul_f32_e32 v22, 0x3fb8aa3b, v22
	v_exp_f32_e32 v158, v22
	v_fma_f32 v22, v24, s71, -v136
	v_mul_f32_e32 v22, 0x3fb8aa3b, v22
	v_exp_f32_e32 v152, v26
	v_exp_f32_e32 v159, v22
	v_fma_f32 v22, v29, s71, -v136
	ds_read2_b64 v[26:29], v156 offset0:8 offset1:12
	v_mul_f32_e32 v22, 0x3fb8aa3b, v22
	v_exp_f32_e32 v156, v22
	v_fma_f32 v22, v25, s71, -v136
	v_mul_f32_e32 v22, 0x3fb8aa3b, v22
	v_exp_f32_e32 v160, v22
	v_cvt_pk_bf16_f32 v22, v152, v154
	v_cvt_pk_bf16_f32 v23, v158, v156
	v_cvt_pk_bf16_f32 v24, v153, v155
	v_cvt_pk_bf16_f32 v25, v159, v160
	ds_read2_b64 v[38:41], v192 offset0:72 offset1:76
	s_waitcnt lgkmcnt(1)
	v_mfma_f32_16x16x32_bf16 v[26:29], v[26:29], v[22:25], v[30:33]
	s_nop 2
	ds_read2_b64 v[30:33], v157 offset0:40 offset1:44
	s_waitcnt lgkmcnt(0)
	v_mfma_f32_16x16x32_bf16 v[30:33], v[30:33], v[22:25], v[42:45]
	s_nop 2
	ds_read2_b64 v[42:45], v193 offset0:104 offset1:108
	s_waitcnt vmcnt(1)
	ds_write_b128 v75, v[166:169] offset:18432
	s_waitcnt vmcnt(0)
	ds_write_b128 v75, v[6:9] offset:27648
	v_fma_f32 v6, v14, s71, -v136
	v_mul_f32_e32 v6, 0x3fb8aa3b, v6
	v_mfma_f32_16x16x32_bf16 v[38:41], v[38:41], v[22:25], v[148:151]
	s_waitcnt lgkmcnt(0)
	s_barrier
; #define LAS __attribute__((address_space(3)))
; __device__ __forceinline__ unsigned cvt_pk_bf16(float lo, float hi) { const float __attribute__((ext_vector_type(2))) v = {lo, hi}; return __builtin_bit_cast(unsigned, __builtin_convertvector(v, bf16x2_t)); }
; #define NA_STORE(sidx) do { LAS bf16* d_ = buf + ((sidx) & 1) * 9216; _Pragma("unroll") for (int q_ = 0; q_ < 2; ++q_) *(LAS v4u*)(d_ + q_ * 4608 + lrow * 72 + lseg * 8) = ld[(sidx) & 1][q_]; } while (0)
; template <bool LOCAL>
; __device__ __forceinline__ void na_unit(const bf16* P, const bf16* VT, bf16* YCAT, const LAS float* rpb_l, LAS bf16* buf, int b, int gr, int hp, int qblk, int tid) {
;     ...
;             } else {
;                 const int cc = c - NLOC;
; #pragma unroll
;                 for (int p2 = 0; p2 < 2; ++p2) {
;                     float p[8];
; #pragma unroll
;                     for (int e = 0; e < 4; ++e) { p[e] = __expf(sc[4 * (cc >= 0 ? cc : 0) + 2 * p2][e] - m); p[4 + e] = __expf(sc[4 * (cc >= 0 ? cc : 0) + 2 * p2 + 1][e] - m); }
; #pragma unroll
;                     for (int e = 0; e < 8; ++e) lsum += p[e];
;                     const bf16x8 pf = __builtin_bit_cast(bf16x8, (v4u){pg8::cvt_pk_bf16(p[0], p[1]), pg8::cvt_pk_bf16(p[2], p[3]), pg8::cvt_pk_bf16(p[4], p[5]), pg8::cvt_pk_bf16(p[6], p[7])});
; #pragma unroll
;                     for (int dt = 0; dt < 4; ++dt) { const LAS bf16* vp = cb + (16 * dt + fr) * 72 + 32 * p2 + 4 * fq;
;                         o[dt] = __builtin_amdgcn_mfma_f32_16x16x32_bf16(frag44(vp, vp + 16), pf, o[dt], 0, 0, 0); }
;                 }
;             }
;         }
;         if (sidx + 1 < 2 * NCH) NA_STORE(sidx + 1);
;         __syncthreads();
;     }
;     ...
;     lsum += __shfl_xor(lsum, 16); lsum += __shfl_xor(lsum, 32);
	v_mfma_f32_16x16x32_bf16 v[22:25], v[42:45], v[22:25], v[34:37]
	v_ashrrev_i32_e32 v75, 31, v74
	s_nop 1
	v_exp_f32_e32 v34, v6
	v_fma_f32 v6, v18, s71, -v136
	v_mul_f32_e32 v6, 0x3fb8aa3b, v6
	v_exp_f32_e32 v35, v6
	v_fma_f32 v6, v15, s71, -v136
	v_mul_f32_e32 v6, 0x3fb8aa3b, v6
	v_exp_f32_e32 v36, v6
	v_fma_f32 v6, v19, s71, -v136
	v_mul_f32_e32 v6, 0x3fb8aa3b, v6
	v_exp_f32_e32 v37, v6
	v_fma_f32 v6, v16, s71, -v136
	v_mul_f32_e32 v6, 0x3fb8aa3b, v6
	v_exp_f32_e32 v42, v6
	v_fma_f32 v6, v20, s71, -v136
	v_mul_f32_e32 v6, 0x3fb8aa3b, v6
	v_exp_f32_e32 v43, v6
	v_fma_f32 v6, v17, s71, -v136
	v_mul_f32_e32 v14, 0x3fb8aa3b, v6
	ds_read2_b64 v[6:9], v52 offset1:4
	v_exp_f32_e32 v44, v14
	v_fma_f32 v14, v21, s71, -v136
	v_mul_f32_e32 v14, 0x3fb8aa3b, v14
	v_exp_f32_e32 v45, v14
	v_cvt_pk_bf16_f32 v14, v34, v36
	v_cvt_pk_bf16_f32 v15, v42, v44
	v_cvt_pk_bf16_f32 v16, v35, v37
	v_cvt_pk_bf16_f32 v17, v43, v45
	ds_read2_b64 v[18:21], v175 offset0:32 offset1:36
	s_waitcnt lgkmcnt(1)
	v_mfma_f32_16x16x32_bf16 v[6:9], v[6:9], v[14:17], v[26:29]
	s_nop 2
	ds_read2_b64 v[26:29], v176 offset0:64 offset1:68
	s_waitcnt lgkmcnt(0)
	v_mfma_f32_16x16x32_bf16 v[26:29], v[26:29], v[14:17], v[38:41]
	s_nop 2
	v_add_f32_e32 v38, 0, v131
	v_add_f32_e32 v38, v96, v38
	v_add_f32_e32 v38, v95, v38
	v_add_f32_e32 v38, v99, v38
	v_add_f32_e32 v38, v92, v38
	v_add_f32_e32 v38, v91, v38
	v_add_f32_e32 v38, v94, v38
	v_add_f32_e32 v38, v93, v38
	v_add_f32_e32 v38, v86, v38
	v_add_f32_e32 v38, v90, v38
	v_add_f32_e32 v38, v98, v38
	v_add_f32_e32 v38, v100, v38
	v_add_f32_e32 v38, v76, v38
	v_add_f32_e32 v38, v87, v38
	v_add_f32_e32 v38, v97, v38
	v_add_f32_e32 v38, v101, v38
	v_add_f32_e32 v38, v103, v38
	v_add_f32_e32 v38, v105, v38
	v_add_f32_e32 v38, v107, v38
	v_add_f32_e32 v38, v108, v38
	v_add_f32_e32 v38, v102, v38
	v_add_f32_e32 v38, v104, v38
	v_add_f32_e32 v38, v106, v38
	v_add_f32_e32 v38, v109, v38
	v_add_f32_e32 v38, v111, v38
	v_add_f32_e32 v38, v113, v38
	v_add_f32_e32 v38, v115, v38
	v_add_f32_e32 v38, v116, v38
	v_add_f32_e32 v38, v110, v38
	v_add_f32_e32 v38, v112, v38
	v_add_f32_e32 v38, v114, v38
	v_add_f32_e32 v38, v117, v38
	v_add_f32_e32 v38, v119, v38
	v_add_f32_e32 v38, v121, v38
	v_add_f32_e32 v38, v123, v38
	v_add_f32_e32 v38, v124, v38
	v_add_f32_e32 v38, v118, v38
	v_add_f32_e32 v38, v120, v38
	v_add_f32_e32 v38, v122, v38
	v_add_f32_e32 v38, v125, v38
	v_add_f32_e32 v38, v127, v38
	v_add_f32_e32 v38, v129, v38
	v_add_f32_e32 v38, v132, v38
	v_add_f32_e32 v38, v133, v38
	v_add_f32_e32 v38, v126, v38
	v_add_f32_e32 v38, v128, v38
	v_add_f32_e32 v38, v130, v38
	v_add_f32_e32 v38, v134, v38
	v_add_f32_e32 v38, v137, v38
	v_add_f32_e32 v38, v139, v38
	v_add_f32_e32 v38, v141, v38
	v_add_f32_e32 v38, v142, v38
	v_add_f32_e32 v38, v135, v38
	v_add_f32_e32 v38, v138, v38
	v_add_f32_e32 v38, v140, v38
	v_add_f32_e32 v38, v143, v38
	v_add_f32_e32 v38, v78, v38
	v_add_f32_e32 v38, v80, v38
	v_add_f32_e32 v38, v144, v38
	v_add_f32_e32 v38, v146, v38
	v_add_f32_e32 v38, v70, v38
	v_add_f32_e32 v38, v79, v38
	v_add_f32_e32 v38, v81, v38
	v_add_f32_e32 v38, v145, v38
	v_add_f32_e32 v38, v147, v38
	v_add_f32_e32 v38, v66, v38
	v_add_f32_e32 v38, v67, v38
	v_add_f32_e32 v38, v68, v38
	v_add_f32_e32 v38, v62, v38
	v_add_f32_e32 v38, v63, v38
	v_add_f32_e32 v38, v64, v38
	v_add_f32_e32 v38, v65, v38
	v_add_f32_e32 v38, v58, v38
	v_add_f32_e32 v38, v59, v38
	v_add_f32_e32 v38, v60, v38
	v_add_f32_e32 v38, v61, v38
	v_add_f32_e32 v38, v54, v38
	v_add_f32_e32 v38, v55, v38
	v_add_f32_e32 v38, v56, v38
	v_add_f32_e32 v38, v57, v38
	v_add_f32_e32 v38, v69, v38
	v_add_f32_e32 v38, v50, v38
	v_add_f32_e32 v38, v51, v38
	v_add_f32_e32 v38, v174, v38
	v_add_f32_e32 v38, v46, v38
	v_add_f32_e32 v38, v47, v38
	v_add_f32_e32 v38, v48, v38
	v_add_f32_e32 v38, v53, v38
	v_add_f32_e32 v38, v170, v38
	v_mfma_f32_16x16x32_bf16 v[18:21], v[18:21], v[14:17], v[30:33]
	v_add_f32_e32 v38, v172, v38
	v_add_f32_e32 v38, v177, v38
	v_add_f32_e32 v38, v179, v38
	ds_read2_b64 v[30:33], v49 offset0:96 offset1:100
	v_add_f32_e32 v38, v171, v38
	v_add_f32_e32 v38, v173, v38
	v_add_f32_e32 v38, v178, v38
	v_add_f32_e32 v38, v180, v38
	v_add_f32_e32 v38, v162, v38
	v_add_f32_e32 v38, v164, v38
	s_waitcnt lgkmcnt(0)
	v_mfma_f32_16x16x32_bf16 v[14:17], v[30:33], v[14:17], v[22:25]
	v_add_f32_e32 v38, v181, v38
	s_nop 1
	v_exp_f32_e32 v23, v2
	v_fma_f32 v2, v11, s71, -v136
	v_mul_f32_e32 v2, 0x3fb8aa3b, v2
	v_add_f32_e32 v38, v183, v38
	v_exp_f32_e32 v24, v2
	v_fma_f32 v2, v3, s71, -v136
	v_add_f32_e32 v38, v163, v38
	v_mul_f32_e32 v2, 0x3fb8aa3b, v2
	v_add_f32_e32 v38, v165, v38
	v_exp_f32_e32 v25, v2
	v_fma_f32 v2, v12, s71, -v136
	v_add_f32_e32 v38, v182, v38
	v_mul_f32_e32 v2, 0x3fb8aa3b, v2
	v_add_f32_e32 v38, v184, v38
	v_exp_f32_e32 v30, v2
	v_fma_f32 v2, v4, s71, -v136
	v_add_f32_e32 v38, v152, v38
	v_mul_f32_e32 v2, 0x3fb8aa3b, v2
	v_add_f32_e32 v38, v154, v38
	v_exp_f32_e32 v22, v10
	v_exp_f32_e32 v31, v2
	v_fma_f32 v2, v13, s71, -v136
	ds_read2_b64 v[10:13], v52 offset0:8 offset1:12
	v_add_f32_e32 v38, v158, v38
	v_mul_f32_e32 v2, 0x3fb8aa3b, v2
	v_add_f32_e32 v38, v156, v38
	v_exp_f32_e32 v32, v2
	v_fma_f32 v2, v5, s71, -v136
	v_add_f32_e32 v38, v153, v38
	v_mul_f32_e32 v2, 0x3fb8aa3b, v2
	v_add_f32_e32 v38, v155, v38
	v_exp_f32_e32 v33, v2
	v_add_f32_e32 v38, v159, v38
	v_add_f32_e32 v38, v160, v38
	v_add_f32_e32 v34, v34, v38
	v_add_f32_e32 v34, v36, v34
	v_cvt_pk_bf16_f32 v2, v22, v24
	v_cvt_pk_bf16_f32 v3, v30, v32
	v_cvt_pk_bf16_f32 v4, v23, v25
	v_cvt_pk_bf16_f32 v5, v31, v33
	v_add_f32_e32 v34, v42, v34
	v_add_f32_e32 v34, v44, v34
	s_waitcnt lgkmcnt(0)
	v_mfma_f32_16x16x32_bf16 v[6:9], v[10:13], v[2:5], v[6:9]
	ds_read2_b64 v[10:13], v175 offset0:40 offset1:44
	v_add_f32_e32 v34, v35, v34
	v_add_f32_e32 v34, v37, v34
	v_add_f32_e32 v34, v43, v34
	v_add_f32_e32 v34, v45, v34
	v_add_f32_e32 v22, v22, v34
	v_add_f32_e32 v22, v24, v22
	v_add_f32_e32 v22, v30, v22
	v_add_f32_e32 v22, v32, v22
	s_waitcnt lgkmcnt(0)
	v_mfma_f32_16x16x32_bf16 v[10:13], v[10:13], v[2:5], v[18:21]
	v_add_f32_e32 v22, v23, v22
	v_add_f32_e32 v22, v25, v22
	v_add_f32_e32 v22, v31, v22
	ds_read2_b64 v[18:21], v176 offset0:72 offset1:76
	v_add_f32_e32 v30, v33, v22
	ds_bpermute_b32 v31, v88, v30
	ds_read2_b64 v[22:25], v49 offset0:104 offset1:108
	s_waitcnt lgkmcnt(2)
	v_mfma_f32_16x16x32_bf16 v[18:21], v[18:21], v[2:5], v[26:29]
	s_waitcnt lgkmcnt(1)
	s_nop 1
	v_add_f32_e32 v26, v30, v31
	ds_bpermute_b32 v27, v89, v26
	v_lshlrev_b32_e32 v70, 1, v77
	s_waitcnt lgkmcnt(1)
	v_mfma_f32_16x16x32_bf16 v[14:17], v[22:25], v[2:5], v[14:17]
	s_waitcnt lgkmcnt(0)
	s_barrier
; __device__ __forceinline__ unsigned cvt_pk_bf16(float lo, float hi) { const float __attribute__((ext_vector_type(2))) v = {lo, hi}; return __builtin_bit_cast(unsigned, __builtin_convertvector(v, bf16x2_t)); }
; template <bool LOCAL>
; __device__ __forceinline__ void na_unit(const bf16* P, const bf16* VT, bf16* YCAT, const LAS float* rpb_l, LAS bf16* buf, int b, int gr, int hp, int qblk, int tid) {
;     ...
;     lsum += __shfl_xor(lsum, 16); lsum += __shfl_xor(lsum, 32);
;     const float inv = 1.f / lsum;
;     bf16* op = YCAT + (size_t)(qrow0 + fr) * D + 512 + h * 64 + 4 * fq;
; #pragma unroll
;     for (int dt = 0; dt < 4; ++dt) { v2u w; w.x = pg8::cvt_pk_bf16(o[dt][0] * inv, o[dt][1] * inv); w.y = pg8::cvt_pk_bf16(o[dt][2] * inv, o[dt][3] * inv); *(v2u*)(op + dt * 16) = w; }
	v_add_f32_e32 v2, v26, v27
	v_div_scale_f32 v3, s[0:1], v2, v2, 1.0
	v_rcp_f32_e32 v4, v3
	s_nop 0
	v_fma_f32 v5, -v3, v4, 1.0
	v_fmac_f32_e32 v4, v5, v4
	v_div_scale_f32 v5, vcc, 1.0, v2, 1.0
	v_mul_f32_e32 v22, v5, v4
	v_fma_f32 v23, -v3, v22, v5
	v_fmac_f32_e32 v22, v23, v4
	v_fma_f32 v3, -v3, v22, v5
	v_div_fmas_f32 v3, v3, v4, v22
	v_div_fixup_f32 v22, v3, v2, 1.0
	v_lshlrev_b64 v[2:3], 11, v[74:75]
	v_lshl_add_u64 v[2:3], s[10:11], 0, v[2:3]
	v_lshl_add_u64 v[2:3], v[72:73], 1, v[2:3]
	v_pk_mul_f32 v[6:7], v[6:7], v[22:23] op_sel_hi:[1,0]
	v_pk_mul_f32 v[8:9], v[8:9], v[22:23] op_sel_hi:[1,0]
	v_lshl_add_u64 v[4:5], v[2:3], 0, v[70:71]
	v_cvt_pk_bf16_f32 v6, v6, v7
	v_cvt_pk_bf16_f32 v7, v8, v9
	global_store_dwordx2 v[4:5], v[6:7], off offset:1024
	v_pk_mul_f32 v[6:7], v[10:11], v[22:23] op_sel_hi:[1,0]
	v_pk_mul_f32 v[8:9], v[12:13], v[22:23] op_sel_hi:[1,0]
	v_cvt_pk_bf16_f32 v6, v6, v7
	v_cvt_pk_bf16_f32 v7, v8, v9
	global_store_dwordx2 v[4:5], v[6:7], off offset:1056
	v_pk_mul_f32 v[6:7], v[18:19], v[22:23] op_sel_hi:[1,0]
	v_pk_mul_f32 v[8:9], v[20:21], v[22:23] op_sel_hi:[1,0]
	v_cvt_pk_bf16_f32 v6, v6, v7
	v_cvt_pk_bf16_f32 v7, v8, v9
	v_lshl_add_u64 v[2:3], v[4:5], 0, s[12:13]
	global_store_dwordx2 v[4:5], v[6:7], off offset:1088
	v_pk_mul_f32 v[4:5], v[14:15], v[22:23] op_sel_hi:[1,0]
	v_pk_mul_f32 v[6:7], v[16:17], v[22:23] op_sel_hi:[1,0]
	v_cvt_pk_bf16_f32 v4, v4, v5

; #define LAS __attribute__((address_space(3)))
; template <bool LOCAL>
; __device__ __forceinline__ void na_unit(const bf16* P, const bf16* VT, bf16* YCAT, const LAS float* rpb_l, LAS bf16* buf, int b, int gr, int hp, int qblk, int tid) {
;     ...
;     const int lane = tid & 63, wv = tid >> 6, fr = lane & 15, fq = lane >> 4, hh = wv >> 2, qb = wv & 3, h = 2 * hp + hh;
;     const int qrow0 = LOCAL ? NCTX + b * SEQ + gr * 64 + 16 * qb : b * CTXL + qblk * 64 + 16 * qb;
;     const int r0 = min(max(gr - 4, 0), 24);
;     const int kc0 = qb == 0 ? 0 : qb == 1 ? 8 : qb == 2 ? 24 : 32;
;     const int qcol = 16 * qb + fr, cs = min(max(qcol - 8, 0), 48);
;     const LAS float* rpb = rpb_l + h * 15 * 31;
;     v4u ld[2][2];
;     const int lrow = (tid >> 3) & 63, lseg = tid & 7;
;     ...
;     bf16x8 qf[2];
; #pragma unroll
;     for (int ks = 0; ks < 2; ++ks) qf[ks] = *(const bf16x8*)(P + (size_t)(qrow0 + fr) * DINP + h * 64 + 32 * ks + 8 * fq);
;     f32x4 sl[16], sc[16];
;     float m = -1.0e30f, lsum = 0.f;
;     f32x4 o[4];
; #pragma unroll
;     for (int dt = 0; dt < 4; ++dt) o[dt] = (f32x4){0.f, 0.f, 0.f, 0.f};
;     NA_ISSUE(0); NA_ISSUE(1); NA_STORE(0);
;     __syncthreads();
; #pragma unroll
;     for (int sidx = 0; sidx < 2 * NCH; ++sidx) {
;         if (sidx + 2 < 2 * NCH) NA_ISSUE(sidx + 2);
;         const LAS bf16* cb = buf + (sidx & 1) * 9216 + hh * 4608;
;         if (sidx < NCH) {
;             const int c = sidx;
;             if (LOCAL && c < 8) {
; #pragma unroll
;                 for (int t2 = 0; t2 < 2; ++t2) {
;                     const LAS bf16* kp = cb + (kc0 + 16 * t2 + fr) * 72 + 8 * fq;
;                     f32x4 acc = {0.f, 0.f, 0.f, 0.f};
;                     acc = __builtin_amdgcn_mfma_f32_16x16x32_bf16(*(const LAS bf16x8*)(kp), qf[0], acc, 0, 0, 0);
;                     acc = __builtin_amdgcn_mfma_f32_16x16x32_bf16(*(const LAS bf16x8*)(kp + 32), qf[1], acc, 0, 0, 0);
;                     const LAS float* rb = rpb + (r0 + c - gr + 7) * 31 + 15 - qcol;
; #pragma unroll
;                     for (int e = 0; e < 4; ++e) { const int kcol = kc0 + 16 * t2 + 4 * fq + e; const bool ok = (kcol >= cs) && (kcol < cs + 16);
;                         const float sv = ok ? acc[e] * 0.125f + rb[ok ? kcol : qcol] : -1.0e30f; acc[e] = sv; m = fmaxf(m, sv); }
;                     sl[2 * (c < 8 ? c : 0) + t2] = acc; }
.LBB0_1746:
	s_or_b64 exec, exec, s[0:1]
	s_bfe_u32 s19, s75, 0x50002
	v_sub_u32_e64 v3, s19, 4 clamp
	s_ashr_i32 s17, s75, 7
	v_readfirstlane_b32 s0, v3
	s_lshl_b32 s26, s17, 11
	s_min_u32 s20, s0, 24
	s_add_i32 s14, s26, 0x1000
	s_lshl_b32 s15, s20, 6
	s_or_b32 s16, s15, s14
	v_mov_b64_e32 v[18:19], s[8:9]
	v_and_b32_e32 v32, 7, v92
	v_or_b32_e32 v3, s16, v87
	s_and_b32 s18, s75, 3
	v_mad_i64_i32 v[4:5], s[0:1], v3, s69, v[18:19]
	v_lshlrev_b32_e32 v26, 4, v32
	v_mov_b32_e32 v27, v71
	v_lshl_add_u64 v[4:5], v[4:5], 0, v[26:27]
	s_lshl_b32 s2, s18, 8
	v_lshl_add_u64 v[4:5], v[4:5], 0, s[2:3]
	global_load_dwordx4 v[10:13], v[4:5], off offset:1024
	global_load_dwordx4 v[14:17], v[4:5], off offset:1152
	s_lshl_b32 s0, s19, 6
	v_lshl_or_b32 v31, v2, 4, v88
	v_lshl_add_u32 v33, s18, 1, v91
	s_or_b32 s0, s14, s0
	v_mad_u32_u24 v2, v87, s70, 0
	v_lshlrev_b32_e32 v72, 6, v33
	s_add_i32 s50, s26, 0x1040
	v_or_b32_e32 v74, s0, v31
	v_add_u32_e32 v75, v2, v26
	v_ashrrev_i32_e32 v73, 31, v72
	v_or_b32_e32 v4, s50, v87
	v_mad_i64_i32 v[2:3], s[0:1], v74, s69, v[18:19]
	v_add_u32_e32 v4, s15, v4
	v_lshl_add_u64 v[2:3], v[72:73], 1, v[2:3]
	v_mad_i64_i32 v[4:5], s[0:1], v4, s69, v[18:19]
	v_lshl_add_u64 v[2:3], v[2:3], 0, v[70:71]
	v_lshl_add_u64 v[20:21], v[4:5], 0, v[26:27]
	global_load_dwordx4 v[6:9], v[2:3], off
	s_nop 0
	global_load_dwordx4 v[2:5], v[2:3], off offset:64
	s_or_b32 s14, s26, s15
	s_addk_i32 s14, 0x1080
	v_or_b32_e32 v24, s14, v87
	v_mad_i64_i32 v[28:29], s[0:1], v24, s69, v[18:19]
	v_lshl_add_u64 v[26:27], v[28:29], 0, v[26:27]
	v_lshl_add_u64 v[22:23], v[20:21], 0, s[2:3]
	v_lshl_add_u64 v[26:27], v[26:27], 0, s[2:3]
	global_load_dwordx4 v[18:21], v[22:23], off offset:1024
	s_nop 0
	global_load_dwordx4 v[22:25], v[22:23], off offset:1152
	v_add_u32_e32 v30, v85, v70
	v_add_u32_e32 v34, v89, v88
	v_mad_u32_u24 v36, v34, s70, v30
	s_movk_i32 s0, 0x744
	v_mul_lo_u32 v33, v33, s0
	s_sub_i32 s0, s20, s19
	s_mulk_i32 s0, 0x7c
	v_sub_u32_e64 v35, v31, 8 clamp
	s_add_i32 s0, s0, 0
	v_min_u32_e32 v35, 48, v35
	v_lshlrev_b32_e32 v77, 2, v90
	v_add_u32_e32 v33, s0, v33
	v_lshlrev_b32_e32 v31, 2, v31
	v_sub_u32_e32 v31, v33, v31
	v_add_u32_e32 v33, v89, v77
	v_cmp_ge_u32_e32 vcc, v33, v35
	v_mov_b32_e32 v90, 0xf149f2ca
	v_lshl_add_u32 v31, v33, 2, v31
	v_mov_b32_e32 v91, 0xf149f2ca
	s_waitcnt vmcnt(5)
	ds_write_b128 v75, v[10:13]
	s_waitcnt vmcnt(4)
	ds_write_b128 v75, v[14:17] offset:9216
	s_waitcnt lgkmcnt(0)
	s_barrier
	ds_read_b32 v240, v31 offset:37792
	ds_read_b32 v241, v31 offset:37796
	ds_read_b32 v242, v31 offset:37800
	ds_read_b32 v243, v31 offset:37804
	ds_read_b32 v244, v31 offset:37856
	ds_read_b32 v245, v31 offset:37860
	ds_read_b32 v246, v31 offset:37864
	ds_read_b32 v247, v31 offset:37868
	global_load_dwordx4 v[10:13], v[26:27], off offset:1024
	global_load_dwordx4 v[14:17], v[26:27], off offset:1152
	ds_read_b128 v[26:29], v36
	ds_read_b128 v[38:41], v36 offset:64
	s_waitcnt vmcnt(5) lgkmcnt(1)
	v_mfma_f32_16x16x32_bf16 v[26:29], v[26:29], v[6:9], 0
	v_add_u32_e32 v36, 16, v35
	v_cmp_lt_u32_e64 s[0:1], v33, v36
	s_and_b64 s[28:29], vcc, s[0:1]
	s_waitcnt vmcnt(4) lgkmcnt(0)
	v_mfma_f32_16x16x32_bf16 v[26:29], v[38:41], v[2:5], v[26:29]
	s_nop 2
	s_waitcnt lgkmcnt(0)
	s_nop 3
	v_fmac_f32_e32 v240, 0x3e000000, v26
	v_cndmask_b32_e64 v91, v91, v240, s[28:29]
	s_nop 4
	v_or_b32_e32 v26, 1, v33
	v_cmp_ge_u32_e32 vcc, v26, v35
	v_cmp_lt_u32_e64 s[0:1], v26, v36
	s_and_b64 s[30:31], vcc, s[0:1]
	s_nop 2
	s_waitcnt lgkmcnt(0)
	v_fmac_f32_e32 v241, 0x3e000000, v27
	v_cndmask_b32_e64 v90, v90, v241, s[30:31]
	v_or_b32_e32 v26, 2, v33
	v_cmp_ge_u32_e32 vcc, v26, v35
	v_cmp_lt_u32_e64 s[0:1], v26, v36
	s_and_b64 s[34:35], vcc, s[0:1]
	v_mov_b32_e32 v92, 0xf149f2ca
	v_mov_b32_e32 v93, 0xf149f2ca
	s_nop 2
	s_waitcnt lgkmcnt(0)
	v_fmac_f32_e32 v242, 0x3e000000, v28
	v_cndmask_b32_e64 v93, v93, v242, s[34:35]
	v_or_b32_e32 v26, 3, v33
	v_cmp_ge_u32_e32 vcc, v26, v35
	v_cmp_lt_u32_e64 s[0:1], v26, v36
	s_and_b64 s[36:37], vcc, s[0:1]
	s_nop 2
	s_waitcnt lgkmcnt(0)
	v_fmac_f32_e32 v243, 0x3e000000, v29
	v_cndmask_b32_e64 v92, v92, v243, s[36:37]
	v_add_u32_e32 v37, 16, v89
	v_add_u32_e32 v33, v37, v88
	v_mad_u32_u24 v38, v33, s70, v30
	ds_read_b128 v[26:29], v38
	ds_read_b128 v[38:41], v38 offset:64
	v_add_u32_e32 v37, v37, v77
	v_cmp_ge_u32_e32 vcc, v37, v35
	v_cmp_lt_u32_e64 s[0:1], v37, v36
	s_waitcnt lgkmcnt(1)
	v_mfma_f32_16x16x32_bf16 v[26:29], v[26:29], v[6:9], 0
	s_and_b64 s[38:39], vcc, s[0:1]
	v_mov_b32_e32 v94, 0xf149f2ca
	v_mov_b32_e32 v95, 0xf149f2ca
	s_waitcnt lgkmcnt(0)
	v_mfma_f32_16x16x32_bf16 v[26:29], v[38:41], v[2:5], v[26:29]
	s_nop 2
	s_waitcnt lgkmcnt(0)
	s_nop 3
	v_fmac_f32_e32 v244, 0x3e000000, v26
	v_cndmask_b32_e64 v95, v95, v244, s[38:39]
	s_nop 4
	v_or_b32_e32 v26, 1, v37
	v_cmp_ge_u32_e32 vcc, v26, v35
	v_cmp_lt_u32_e64 s[0:1], v26, v36
	s_and_b64 s[44:45], vcc, s[0:1]
	s_nop 2
	s_waitcnt lgkmcnt(0)
	v_fmac_f32_e32 v245, 0x3e000000, v27
	v_cndmask_b32_e64 v94, v94, v245, s[44:45]
	v_or_b32_e32 v26, 2, v37
	v_cmp_ge_u32_e32 vcc, v26, v35
	v_cmp_lt_u32_e64 s[0:1], v26, v36
	s_and_b64 s[46:47], vcc, s[0:1]
	v_mov_b32_e32 v96, 0xf149f2ca
	v_mov_b32_e32 v98, 0xf149f2ca
	s_nop 2
	s_waitcnt lgkmcnt(0)
	v_fmac_f32_e32 v246, 0x3e000000, v28
	v_cndmask_b32_e64 v98, v98, v246, s[46:47]
	v_or_b32_e32 v26, 3, v37
	v_cmp_ge_u32_e32 vcc, v26, v35
	v_cmp_lt_u32_e64 s[0:1], v26, v36
	s_and_b64 s[48:49], vcc, s[0:1]
	s_nop 2
	s_waitcnt lgkmcnt(0)
	v_fmac_f32_e32 v247, 0x3e000000, v29
	v_cndmask_b32_e64 v96, v96, v247, s[48:49]
	v_mul_u32_u24_e32 v27, 0x90, v34
	v_lshlrev_b32_e32 v26, 3, v32
	v_add_u32_e32 v32, v30, v27
	s_waitcnt vmcnt(3)
	ds_write_b128 v75, v[18:21] offset:18432
	s_waitcnt vmcnt(2)
	ds_write_b128 v75, v[22:25] offset:27648
	s_waitcnt lgkmcnt(0)
	s_barrier
; #define LAS __attribute__((address_space(3)))
; template <bool LOCAL>
; __device__ __forceinline__ void na_unit(const bf16* P, const bf16* VT, bf16* YCAT, const LAS float* rpb_l, LAS bf16* buf, int b, int gr, int hp, int qblk, int tid) {
;     ...
;         if (sidx < NCH) {
;             const int c = sidx;
;             if (LOCAL && c < 8) {
; #pragma unroll
;                 for (int t2 = 0; t2 < 2; ++t2) {
;                     const LAS bf16* kp = cb + (kc0 + 16 * t2 + fr) * 72 + 8 * fq;
;                     f32x4 acc = {0.f, 0.f, 0.f, 0.f};
;                     acc = __builtin_amdgcn_mfma_f32_16x16x32_bf16(*(const LAS bf16x8*)(kp), qf[0], acc, 0, 0, 0);
;                     acc = __builtin_amdgcn_mfma_f32_16x16x32_bf16(*(const LAS bf16x8*)(kp + 32), qf[1], acc, 0, 0, 0);
;                     const LAS float* rb = rpb + (r0 + c - gr + 7) * 31 + 15 - qcol;
; #pragma unroll
;                     for (int e = 0; e < 4; ++e) { const int kcol = kc0 + 16 * t2 + 4 * fq + e; const bool ok = (kcol >= cs) && (kcol < cs + 16);
;                         const float sv = ok ? acc[e] * 0.125f + rb[ok ? kcol : qcol] : -1.0e30f; acc[e] = sv; m = fmaxf(m, sv); }
;                     sl[2 * (c < 8 ? c : 0) + t2] = acc; }
	ds_read_b32 v240, v31 offset:37916
	ds_read_b32 v241, v31 offset:37920
	ds_read_b32 v242, v31 offset:37924
	ds_read_b32 v243, v31 offset:37928
	ds_read_b32 v244, v31 offset:37980
	ds_read_b32 v245, v31 offset:37984
	ds_read_b32 v246, v31 offset:37988
	ds_read_b32 v247, v31 offset:37992
	ds_read_b128 v[18:21], v32 offset:18432
	s_add_i32 s26, s26, s15
	s_add_i32 s0, s26, 0x10c0
	v_or_b32_e32 v24, s0, v87
	v_mov_b64_e32 v[22:23], s[8:9]
	s_lshl_b32 s1, s18, 7
	v_mad_i64_i32 v[22:23], s[18:19], v24, s69, v[22:23]
	v_lshlrev_b32_e32 v70, 1, v26
	v_lshl_add_u64 v[22:23], v[22:23], 0, v[70:71]
	s_lshl_b32 s2, s1, 1
	v_lshl_add_u64 v[22:23], v[22:23], 0, s[2:3]
	ds_read_b128 v[26:29], v32 offset:18496
	s_waitcnt lgkmcnt(1)
	v_mfma_f32_16x16x32_bf16 v[34:37], v[18:21], v[6:9], 0
	global_load_dwordx4 v[18:21], v[22:23], off offset:1024
	s_nop 0
	global_load_dwordx4 v[22:25], v[22:23], off offset:1152
	v_mov_b32_e32 v97, 0xf149f2ca
	v_mov_b32_e32 v99, 0xf149f2ca
	s_waitcnt lgkmcnt(0)
	v_mfma_f32_16x16x32_bf16 v[26:29], v[26:29], v[2:5], v[34:37]
	s_nop 2
	s_waitcnt lgkmcnt(0)
	s_nop 3
	v_fmac_f32_e32 v240, 0x3e000000, v26
	v_cndmask_b32_e64 v99, v99, v240, s[28:29]
	s_nop 2
	s_waitcnt lgkmcnt(0)
	s_nop 0
	v_fmac_f32_e32 v241, 0x3e000000, v27
	v_cndmask_b32_e64 v97, v97, v241, s[30:31]
	v_mov_b32_e32 v100, 0xf149f2ca
	v_mov_b32_e32 v101, 0xf149f2ca
	s_nop 2
	s_waitcnt lgkmcnt(0)
	v_fmac_f32_e32 v242, 0x3e000000, v28
	v_cndmask_b32_e64 v101, v101, v242, s[34:35]
	s_nop 2
	s_waitcnt lgkmcnt(0)
	v_fmac_f32_e32 v243, 0x3e000000, v29
	v_cndmask_b32_e64 v100, v100, v243, s[36:37]
	v_mul_u32_u24_e32 v26, 0x90, v33
	v_add_u32_e32 v33, v30, v26
	ds_read_b128 v[26:29], v33 offset:18432
	ds_read_b128 v[34:37], v33 offset:18496
	v_mov_b32_e32 v102, 0xf149f2ca
	v_mov_b32_e32 v104, 0xf149f2ca
	s_waitcnt lgkmcnt(1)
	v_mfma_f32_16x16x32_bf16 v[26:29], v[26:29], v[6:9], 0
	s_waitcnt lgkmcnt(0)
	v_mfma_f32_16x16x32_bf16 v[26:29], v[34:37], v[2:5], v[26:29]
	s_nop 2
	s_waitcnt lgkmcnt(0)
	s_nop 3
	v_fmac_f32_e32 v244, 0x3e000000, v26
	v_cndmask_b32_e64 v104, v104, v244, s[38:39]
	s_nop 2
	s_waitcnt lgkmcnt(0)
	s_nop 0
	v_fmac_f32_e32 v245, 0x3e000000, v27
	v_cndmask_b32_e64 v102, v102, v245, s[44:45]
	v_mov_b32_e32 v106, 0xf149f2ca
	v_mov_b32_e32 v108, 0xf149f2ca
	s_nop 2
	s_waitcnt lgkmcnt(0)
	v_fmac_f32_e32 v246, 0x3e000000, v28
	v_cndmask_b32_e64 v108, v108, v246, s[46:47]
	s_nop 2
	s_waitcnt lgkmcnt(0)
	v_fmac_f32_e32 v247, 0x3e000000, v29
	v_cndmask_b32_e64 v106, v106, v247, s[48:49]
	s_waitcnt vmcnt(3)
	ds_write_b128 v75, v[10:13]
	s_waitcnt vmcnt(2)
	ds_write_b128 v75, v[14:17] offset:9216
	s_waitcnt lgkmcnt(0)
	s_barrier
	ds_read_b32 v240, v31 offset:38040
	ds_read_b32 v241, v31 offset:38044
	ds_read_b32 v242, v31 offset:38048
	ds_read_b32 v243, v31 offset:38052
	ds_read_b32 v244, v31 offset:38104
	ds_read_b32 v245, v31 offset:38108
	ds_read_b32 v246, v31 offset:38112
	ds_read_b32 v247, v31 offset:38116
	ds_read_b128 v[10:13], v32
	ds_read_b128 v[26:29], v32 offset:64
	s_add_i32 s18, s26, 0x1100
	v_or_b32_e32 v16, s18, v87
	v_mov_b64_e32 v[14:15], s[8:9]
	v_mad_i64_i32 v[14:15], s[20:21], v16, s69, v[14:15]
	v_lshl_add_u64 v[14:15], v[14:15], 0, v[70:71]
	v_lshl_add_u64 v[14:15], v[14:15], 0, s[2:3]
	s_waitcnt lgkmcnt(1)
	v_mfma_f32_16x16x32_bf16 v[34:37], v[10:13], v[6:9], 0
	global_load_dwordx4 v[10:13], v[14:15], off offset:1024
	s_nop 0
	global_load_dwordx4 v[14:17], v[14:15], off offset:1152
	v_mov_b32_e32 v103, 0xf149f2ca
	v_mov_b32_e32 v105, 0xf149f2ca
	s_waitcnt lgkmcnt(0)
	v_mfma_f32_16x16x32_bf16 v[26:29], v[26:29], v[2:5], v[34:37]
	s_nop 2
	s_waitcnt lgkmcnt(0)
	s_nop 3
	v_fmac_f32_e32 v240, 0x3e000000, v26
	v_cndmask_b32_e64 v105, v105, v240, s[28:29]
	s_nop 2
	s_waitcnt lgkmcnt(0)
	s_nop 0
	v_fmac_f32_e32 v241, 0x3e000000, v27
	v_cndmask_b32_e64 v103, v103, v241, s[30:31]
	v_mov_b32_e32 v107, 0xf149f2ca
	v_mov_b32_e32 v109, 0xf149f2ca
	s_nop 2
	s_waitcnt lgkmcnt(0)
	v_fmac_f32_e32 v242, 0x3e000000, v28
	v_cndmask_b32_e64 v109, v109, v242, s[34:35]
	s_nop 2
	s_waitcnt lgkmcnt(0)
	v_fmac_f32_e32 v243, 0x3e000000, v29
	v_cndmask_b32_e64 v107, v107, v243, s[36:37]
	ds_read_b128 v[26:29], v33
	ds_read_b128 v[34:37], v33 offset:64
	v_mov_b32_e32 v110, 0xf149f2ca
	v_mov_b32_e32 v112, 0xf149f2ca
	s_waitcnt lgkmcnt(1)
	v_mfma_f32_16x16x32_bf16 v[26:29], v[26:29], v[6:9], 0
	s_waitcnt lgkmcnt(0)
	v_mfma_f32_16x16x32_bf16 v[26:29], v[34:37], v[2:5], v[26:29]
	s_nop 2
	s_waitcnt lgkmcnt(0)
	s_nop 3
	v_fmac_f32_e32 v244, 0x3e000000, v26
	v_cndmask_b32_e64 v112, v112, v244, s[38:39]
	s_nop 2
	s_waitcnt lgkmcnt(0)
	s_nop 0
	v_fmac_f32_e32 v245, 0x3e000000, v27
	v_cndmask_b32_e64 v110, v110, v245, s[44:45]
	v_mov_b32_e32 v111, 0xf149f2ca
	v_mov_b32_e32 v115, 0xf149f2ca
	s_nop 2
	s_waitcnt lgkmcnt(0)
	v_fmac_f32_e32 v246, 0x3e000000, v28
	v_cndmask_b32_e64 v115, v115, v246, s[46:47]
	s_nop 2
	s_waitcnt lgkmcnt(0)
	v_fmac_f32_e32 v247, 0x3e000000, v29
	v_cndmask_b32_e64 v111, v111, v247, s[48:49]
	s_waitcnt vmcnt(3)
	ds_write_b128 v75, v[18:21] offset:18432
	s_waitcnt vmcnt(2)
	ds_write_b128 v75, v[22:25] offset:27648
	s_waitcnt lgkmcnt(0)
	s_barrier
; #define LAS __attribute__((address_space(3)))
; template <bool LOCAL>
; __device__ __forceinline__ void na_unit(const bf16* P, const bf16* VT, bf16* YCAT, const LAS float* rpb_l, LAS bf16* buf, int b, int gr, int hp, int qblk, int tid) {
;     ...
;         if (sidx < NCH) {
;             const int c = sidx;
;             if (LOCAL && c < 8) {
; #pragma unroll
;                 for (int t2 = 0; t2 < 2; ++t2) {
;                     const LAS bf16* kp = cb + (kc0 + 16 * t2 + fr) * 72 + 8 * fq;
;                     f32x4 acc = {0.f, 0.f, 0.f, 0.f};
;                     acc = __builtin_amdgcn_mfma_f32_16x16x32_bf16(*(const LAS bf16x8*)(kp), qf[0], acc, 0, 0, 0);
;                     acc = __builtin_amdgcn_mfma_f32_16x16x32_bf16(*(const LAS bf16x8*)(kp + 32), qf[1], acc, 0, 0, 0);
;                     const LAS float* rb = rpb + (r0 + c - gr + 7) * 31 + 15 - qcol;
; #pragma unroll
;                     for (int e = 0; e < 4; ++e) { const int kcol = kc0 + 16 * t2 + 4 * fq + e; const bool ok = (kcol >= cs) && (kcol < cs + 16);
;                         const float sv = ok ? acc[e] * 0.125f + rb[ok ? kcol : qcol] : -1.0e30f; acc[e] = sv; m = fmaxf(m, sv); }
;                     sl[2 * (c < 8 ? c : 0) + t2] = acc; }
	ds_read_b32 v240, v31 offset:38164
	ds_read_b32 v241, v31 offset:38168
	ds_read_b32 v242, v31 offset:38172
	ds_read_b32 v243, v31 offset:38176
	ds_read_b32 v244, v31 offset:38228
	ds_read_b32 v245, v31 offset:38232
	ds_read_b32 v246, v31 offset:38236
	ds_read_b32 v247, v31 offset:38240
	ds_read_b128 v[18:21], v32 offset:18432
	ds_read_b128 v[26:29], v32 offset:18496
	s_add_i32 s20, s26, 0x1140
	v_or_b32_e32 v24, s20, v87
	v_mov_b64_e32 v[22:23], s[8:9]
	v_mad_i64_i32 v[22:23], s[22:23], v24, s69, v[22:23]
	v_lshl_add_u64 v[22:23], v[22:23], 0, v[70:71]
	v_lshl_add_u64 v[22:23], v[22:23], 0, s[2:3]
	s_waitcnt lgkmcnt(1)
	v_mfma_f32_16x16x32_bf16 v[34:37], v[18:21], v[6:9], 0
	global_load_dwordx4 v[18:21], v[22:23], off offset:1024
	s_nop 0
	global_load_dwordx4 v[22:25], v[22:23], off offset:1152
	v_mov_b32_e32 v113, 0xf149f2ca
	v_mov_b32_e32 v114, 0xf149f2ca
	s_waitcnt lgkmcnt(0)
	v_mfma_f32_16x16x32_bf16 v[26:29], v[26:29], v[2:5], v[34:37]
	s_nop 2
	s_waitcnt lgkmcnt(0)
	s_nop 3
	v_fmac_f32_e32 v240, 0x3e000000, v26
	v_cndmask_b32_e64 v114, v114, v240, s[28:29]
	s_nop 2
	s_waitcnt lgkmcnt(0)
	s_nop 0
	v_fmac_f32_e32 v241, 0x3e000000, v27
	v_cndmask_b32_e64 v113, v113, v241, s[30:31]
	v_mov_b32_e32 v116, 0xf149f2ca
	v_mov_b32_e32 v117, 0xf149f2ca
	s_nop 2
	s_waitcnt lgkmcnt(0)
	v_fmac_f32_e32 v242, 0x3e000000, v28
	v_cndmask_b32_e64 v117, v117, v242, s[34:35]
	s_nop 2
	s_waitcnt lgkmcnt(0)
	v_fmac_f32_e32 v243, 0x3e000000, v29
	v_cndmask_b32_e64 v116, v116, v243, s[36:37]
	ds_read_b128 v[26:29], v33 offset:18432
	ds_read_b128 v[34:37], v33 offset:18496
	v_mov_b32_e32 v118, 0xf149f2ca
	v_mov_b32_e32 v120, 0xf149f2ca
	s_waitcnt lgkmcnt(1)
	v_mfma_f32_16x16x32_bf16 v[26:29], v[26:29], v[6:9], 0
	s_waitcnt lgkmcnt(0)
	v_mfma_f32_16x16x32_bf16 v[26:29], v[34:37], v[2:5], v[26:29]
	s_nop 2
	s_waitcnt lgkmcnt(0)
	s_nop 3
	v_fmac_f32_e32 v244, 0x3e000000, v26
	v_cndmask_b32_e64 v120, v120, v244, s[38:39]
	s_nop 2
	s_waitcnt lgkmcnt(0)
	s_nop 0
	v_fmac_f32_e32 v245, 0x3e000000, v27
	v_cndmask_b32_e64 v118, v118, v245, s[44:45]
	v_mov_b32_e32 v119, 0xf149f2ca
	v_mov_b32_e32 v123, 0xf149f2ca
	s_nop 2
	s_waitcnt lgkmcnt(0)
	v_fmac_f32_e32 v246, 0x3e000000, v28
	v_cndmask_b32_e64 v123, v123, v246, s[46:47]
	s_nop 2
	s_waitcnt lgkmcnt(0)
	v_fmac_f32_e32 v247, 0x3e000000, v29
	v_cndmask_b32_e64 v119, v119, v247, s[48:49]
	s_waitcnt vmcnt(3)
	ds_write_b128 v75, v[10:13]
	s_waitcnt vmcnt(2)
	ds_write_b128 v75, v[14:17] offset:9216
	s_waitcnt lgkmcnt(0)
	s_barrier
	ds_read_b32 v240, v31 offset:38288
	ds_read_b32 v241, v31 offset:38292
	ds_read_b32 v242, v31 offset:38296
	ds_read_b32 v243, v31 offset:38300
	ds_read_b32 v244, v31 offset:38352
	ds_read_b32 v245, v31 offset:38356
	ds_read_b32 v246, v31 offset:38360
	ds_read_b32 v247, v31 offset:38364
	ds_read_b128 v[10:13], v32
	ds_read_b128 v[26:29], v32 offset:64
	s_add_i32 s22, s26, 0x1180
	v_or_b32_e32 v16, s22, v87
	v_mov_b64_e32 v[14:15], s[8:9]
	v_mad_i64_i32 v[14:15], s[24:25], v16, s69, v[14:15]
	v_lshl_add_u64 v[14:15], v[14:15], 0, v[70:71]
	v_lshl_add_u64 v[14:15], v[14:15], 0, s[2:3]
	s_waitcnt lgkmcnt(1)
	v_mfma_f32_16x16x32_bf16 v[34:37], v[10:13], v[6:9], 0
	global_load_dwordx4 v[10:13], v[14:15], off offset:1024
	s_nop 0
	global_load_dwordx4 v[14:17], v[14:15], off offset:1152
	v_mov_b32_e32 v121, 0xf149f2ca
	v_mov_b32_e32 v122, 0xf149f2ca
	s_waitcnt lgkmcnt(0)
	v_mfma_f32_16x16x32_bf16 v[26:29], v[26:29], v[2:5], v[34:37]
	s_nop 2
	s_waitcnt lgkmcnt(0)
	s_nop 3
	v_fmac_f32_e32 v240, 0x3e000000, v26
	v_cndmask_b32_e64 v122, v122, v240, s[28:29]
	s_nop 2
	s_waitcnt lgkmcnt(0)
	s_nop 0
	v_fmac_f32_e32 v241, 0x3e000000, v27
	v_cndmask_b32_e64 v121, v121, v241, s[30:31]
	v_mov_b32_e32 v124, 0xf149f2ca
	v_mov_b32_e32 v125, 0xf149f2ca
	s_nop 2
	s_waitcnt lgkmcnt(0)
	v_fmac_f32_e32 v242, 0x3e000000, v28
	v_cndmask_b32_e64 v125, v125, v242, s[34:35]
	s_nop 2
	s_waitcnt lgkmcnt(0)
	v_fmac_f32_e32 v243, 0x3e000000, v29
	v_cndmask_b32_e64 v124, v124, v243, s[36:37]
	ds_read_b128 v[26:29], v33
	ds_read_b128 v[34:37], v33 offset:64
	v_mov_b32_e32 v126, 0xf149f2ca
	v_mov_b32_e32 v128, 0xf149f2ca
	s_waitcnt lgkmcnt(1)
	v_mfma_f32_16x16x32_bf16 v[26:29], v[26:29], v[6:9], 0
	s_waitcnt lgkmcnt(0)
	v_mfma_f32_16x16x32_bf16 v[26:29], v[34:37], v[2:5], v[26:29]
	s_nop 2
	s_waitcnt lgkmcnt(0)
	s_nop 3
	v_fmac_f32_e32 v244, 0x3e000000, v26
	v_cndmask_b32_e64 v128, v128, v244, s[38:39]
	s_nop 2
	s_waitcnt lgkmcnt(0)
	s_nop 0
	v_fmac_f32_e32 v245, 0x3e000000, v27
	v_cndmask_b32_e64 v126, v126, v245, s[44:45]
	v_mov_b32_e32 v127, 0xf149f2ca
	v_mov_b32_e32 v132, 0xf149f2ca
	s_nop 2
	s_waitcnt lgkmcnt(0)
	v_fmac_f32_e32 v246, 0x3e000000, v28
	v_cndmask_b32_e64 v132, v132, v246, s[46:47]
	s_nop 2
	s_waitcnt lgkmcnt(0)
	v_fmac_f32_e32 v247, 0x3e000000, v29
	v_cndmask_b32_e64 v127, v127, v247, s[48:49]
	s_waitcnt vmcnt(3)
	ds_write_b128 v75, v[18:21] offset:18432
	s_waitcnt vmcnt(2)
	ds_write_b128 v75, v[22:25] offset:27648
	s_waitcnt lgkmcnt(0)
	s_barrier
; #define LAS __attribute__((address_space(3)))
; template <bool LOCAL>
; __device__ __forceinline__ void na_unit(const bf16* P, const bf16* VT, bf16* YCAT, const LAS float* rpb_l, LAS bf16* buf, int b, int gr, int hp, int qblk, int tid) {
;     ...
;         if (sidx < NCH) {
;             const int c = sidx;
;             if (LOCAL && c < 8) {
; #pragma unroll
;                 for (int t2 = 0; t2 < 2; ++t2) {
;                     const LAS bf16* kp = cb + (kc0 + 16 * t2 + fr) * 72 + 8 * fq;
;                     f32x4 acc = {0.f, 0.f, 0.f, 0.f};
;                     acc = __builtin_amdgcn_mfma_f32_16x16x32_bf16(*(const LAS bf16x8*)(kp), qf[0], acc, 0, 0, 0);
;                     acc = __builtin_amdgcn_mfma_f32_16x16x32_bf16(*(const LAS bf16x8*)(kp + 32), qf[1], acc, 0, 0, 0);
;                     const LAS float* rb = rpb + (r0 + c - gr + 7) * 31 + 15 - qcol;
; #pragma unroll
;                     for (int e = 0; e < 4; ++e) { const int kcol = kc0 + 16 * t2 + 4 * fq + e; const bool ok = (kcol >= cs) && (kcol < cs + 16);
;                         const float sv = ok ? acc[e] * 0.125f + rb[ok ? kcol : qcol] : -1.0e30f; acc[e] = sv; m = fmaxf(m, sv); }
;                     sl[2 * (c < 8 ? c : 0) + t2] = acc; }
	ds_read_b32 v240, v31 offset:38412
	ds_read_b32 v241, v31 offset:38416
	ds_read_b32 v242, v31 offset:38420
	ds_read_b32 v243, v31 offset:38424
	ds_read_b32 v244, v31 offset:38476
	ds_read_b32 v245, v31 offset:38480
	ds_read_b32 v246, v31 offset:38484
	ds_read_b32 v247, v31 offset:38488
	ds_read_b128 v[18:21], v32 offset:18432
	ds_read_b128 v[26:29], v32 offset:18496
	s_add_i32 s24, s26, 0x11c0
	v_or_b32_e32 v24, s24, v87
	v_mov_b64_e32 v[22:23], s[8:9]
	v_mad_i64_i32 v[22:23], s[26:27], v24, s69, v[22:23]
	v_lshl_add_u64 v[22:23], v[22:23], 0, v[70:71]
	v_lshl_add_u64 v[22:23], v[22:23], 0, s[2:3]
	s_waitcnt lgkmcnt(1)
	v_mfma_f32_16x16x32_bf16 v[34:37], v[18:21], v[6:9], 0
	global_load_dwordx4 v[18:21], v[22:23], off offset:1024
	s_nop 0
	global_load_dwordx4 v[22:25], v[22:23], off offset:1152
	v_mov_b32_e32 v129, 0xf149f2ca
	v_mov_b32_e32 v131, 0xf149f2ca
	s_waitcnt lgkmcnt(0)
	v_mfma_f32_16x16x32_bf16 v[26:29], v[26:29], v[2:5], v[34:37]
	s_nop 2
	s_waitcnt lgkmcnt(0)
	s_nop 3
	v_fmac_f32_e32 v240, 0x3e000000, v26
	v_cndmask_b32_e64 v131, v131, v240, s[28:29]
	s_nop 2
	s_waitcnt lgkmcnt(0)
	s_nop 0
	v_fmac_f32_e32 v241, 0x3e000000, v27
	v_cndmask_b32_e64 v129, v129, v241, s[30:31]
	v_mov_b32_e32 v133, 0xf149f2ca
	v_mov_b32_e32 v134, 0xf149f2ca
	s_nop 2
	s_waitcnt lgkmcnt(0)
	v_fmac_f32_e32 v242, 0x3e000000, v28
	v_cndmask_b32_e64 v134, v134, v242, s[34:35]
	s_nop 2
	s_waitcnt lgkmcnt(0)
	v_fmac_f32_e32 v243, 0x3e000000, v29
	v_cndmask_b32_e64 v133, v133, v243, s[36:37]
	ds_read_b128 v[26:29], v33 offset:18432
	ds_read_b128 v[34:37], v33 offset:18496
	v_mov_b32_e32 v136, 0xf149f2ca
	v_mov_b32_e32 v138, 0xf149f2ca
	s_waitcnt lgkmcnt(1)
	v_mfma_f32_16x16x32_bf16 v[26:29], v[26:29], v[6:9], 0
	s_waitcnt lgkmcnt(0)
	v_mfma_f32_16x16x32_bf16 v[26:29], v[34:37], v[2:5], v[26:29]
	s_nop 2
	s_waitcnt lgkmcnt(0)
	s_nop 3
	v_fmac_f32_e32 v244, 0x3e000000, v26
	v_cndmask_b32_e64 v138, v138, v244, s[38:39]
	s_nop 2
	s_waitcnt lgkmcnt(0)
	s_nop 0
	v_fmac_f32_e32 v245, 0x3e000000, v27
	v_cndmask_b32_e64 v136, v136, v245, s[44:45]
	v_mov_b32_e32 v137, 0xf149f2ca
	v_mov_b32_e32 v141, 0xf149f2ca
	s_nop 2
	s_waitcnt lgkmcnt(0)
	v_fmac_f32_e32 v246, 0x3e000000, v28
	v_cndmask_b32_e64 v141, v141, v246, s[46:47]
	s_nop 2
	s_waitcnt lgkmcnt(0)
	v_fmac_f32_e32 v247, 0x3e000000, v29
	v_cndmask_b32_e64 v137, v137, v247, s[48:49]
	s_waitcnt vmcnt(3)
	ds_write_b128 v75, v[10:13]
	s_waitcnt vmcnt(2)
	ds_write_b128 v75, v[14:17] offset:9216
	s_waitcnt lgkmcnt(0)
	s_barrier
	ds_read_b32 v240, v31 offset:38536
	ds_read_b32 v241, v31 offset:38540
	ds_read_b32 v242, v31 offset:38544
	ds_read_b32 v243, v31 offset:38548
	ds_read_b32 v244, v31 offset:38600
	ds_read_b32 v245, v31 offset:38604
	ds_read_b32 v246, v31 offset:38608
	ds_read_b32 v247, v31 offset:38612
	ds_read_b128 v[10:13], v32
	ds_read_b128 v[26:29], v32 offset:64
	s_lshl_b32 s26, s17, 8
	v_or_b32_e32 v34, s26, v87
	v_mov_b64_e32 v[14:15], s[8:9]
	v_mad_i64_i32 v[14:15], s[52:53], v34, s69, v[14:15]
	v_lshl_add_u64 v[14:15], v[14:15], 0, v[70:71]
	v_lshl_add_u64 v[14:15], v[14:15], 0, s[2:3]
	s_waitcnt lgkmcnt(1)
	v_mfma_f32_16x16x32_bf16 v[36:39], v[10:13], v[6:9], 0
	global_load_dwordx4 v[10:13], v[14:15], off offset:1024
	s_nop 0
	global_load_dwordx4 v[14:17], v[14:15], off offset:1152
	v_mov_b32_e32 v139, 0xf149f2ca
	v_mov_b32_e32 v140, 0xf149f2ca
	s_waitcnt lgkmcnt(0)
	v_mfma_f32_16x16x32_bf16 v[26:29], v[26:29], v[2:5], v[36:39]
	s_nop 2
	s_waitcnt lgkmcnt(0)
	s_nop 3
	v_fmac_f32_e32 v240, 0x3e000000, v26
	v_cndmask_b32_e64 v140, v140, v240, s[28:29]
	s_nop 2
	s_waitcnt lgkmcnt(0)
	s_nop 0
	v_fmac_f32_e32 v241, 0x3e000000, v27
	v_cndmask_b32_e64 v139, v139, v241, s[30:31]
	v_mov_b32_e32 v142, 0xf149f2ca
	v_mov_b32_e32 v143, 0xf149f2ca
	s_nop 2
	s_waitcnt lgkmcnt(0)
	v_fmac_f32_e32 v242, 0x3e000000, v28
	v_cndmask_b32_e64 v143, v143, v242, s[34:35]
	s_nop 2
	s_waitcnt lgkmcnt(0)
	v_fmac_f32_e32 v243, 0x3e000000, v29
	v_cndmask_b32_e64 v142, v142, v243, s[36:37]
	ds_read_b128 v[26:29], v33
	ds_read_b128 v[36:39], v33 offset:64
	v_mov_b32_e32 v144, 0xf149f2ca
	v_mov_b32_e32 v146, 0xf149f2ca
	s_waitcnt lgkmcnt(1)
	v_mfma_f32_16x16x32_bf16 v[26:29], v[26:29], v[6:9], 0
	s_waitcnt lgkmcnt(0)
	v_mfma_f32_16x16x32_bf16 v[26:29], v[36:39], v[2:5], v[26:29]
	s_nop 2
	s_waitcnt lgkmcnt(0)
	s_nop 3
	v_fmac_f32_e32 v244, 0x3e000000, v26
	v_cndmask_b32_e64 v146, v146, v244, s[38:39]
	s_nop 2
	s_waitcnt lgkmcnt(0)
	s_nop 0
	v_fmac_f32_e32 v245, 0x3e000000, v27
	v_cndmask_b32_e64 v144, v144, v245, s[44:45]
	v_mov_b32_e32 v145, 0xf149f2ca
	v_mov_b32_e32 v149, 0xf149f2ca
	s_nop 2
	s_waitcnt lgkmcnt(0)
	v_fmac_f32_e32 v246, 0x3e000000, v28
	v_cndmask_b32_e64 v149, v149, v246, s[46:47]
	s_nop 2
	s_waitcnt lgkmcnt(0)
	v_fmac_f32_e32 v247, 0x3e000000, v29
	v_cndmask_b32_e64 v145, v145, v247, s[48:49]
	s_waitcnt vmcnt(3)
	ds_write_b128 v75, v[18:21] offset:18432
	s_waitcnt vmcnt(2)
	ds_write_b128 v75, v[22:25] offset:27648
	s_waitcnt lgkmcnt(0)
	s_barrier
; #define LAS __attribute__((address_space(3)))
; template <bool LOCAL>
; __device__ __forceinline__ void na_unit(const bf16* P, const bf16* VT, bf16* YCAT, const LAS float* rpb_l, LAS bf16* buf, int b, int gr, int hp, int qblk, int tid) {
;     ...
;         if (sidx < NCH) {
;             const int c = sidx;
;             if (LOCAL && c < 8) {
; #pragma unroll
;                 for (int t2 = 0; t2 < 2; ++t2) {
;                     const LAS bf16* kp = cb + (kc0 + 16 * t2 + fr) * 72 + 8 * fq;
;                     f32x4 acc = {0.f, 0.f, 0.f, 0.f};
;                     acc = __builtin_amdgcn_mfma_f32_16x16x32_bf16(*(const LAS bf16x8*)(kp), qf[0], acc, 0, 0, 0);
;                     acc = __builtin_amdgcn_mfma_f32_16x16x32_bf16(*(const LAS bf16x8*)(kp + 32), qf[1], acc, 0, 0, 0);
;                     const LAS float* rb = rpb + (r0 + c - gr + 7) * 31 + 15 - qcol;
; #pragma unroll
;                     for (int e = 0; e < 4; ++e) { const int kcol = kc0 + 16 * t2 + 4 * fq + e; const bool ok = (kcol >= cs) && (kcol < cs + 16);
;                         const float sv = ok ? acc[e] * 0.125f + rb[ok ? kcol : qcol] : -1.0e30f; acc[e] = sv; m = fmaxf(m, sv); }
;                     sl[2 * (c < 8 ? c : 0) + t2] = acc; }
;             } else {
;                 const int cc = c - NLOC;
; #pragma unroll
;                 for (int t4 = 0; t4 < 4; ++t4) {
;                     const LAS bf16* kp = cb + (16 * t4 + fr) * 72 + 8 * fq;
;                     f32x4 acc = {0.f, 0.f, 0.f, 0.f};
;                     acc = __builtin_amdgcn_mfma_f32_16x16x32_bf16(*(const LAS bf16x8*)(kp), qf[0], acc, 0, 0, 0);
;                     acc = __builtin_amdgcn_mfma_f32_16x16x32_bf16(*(const LAS bf16x8*)(kp + 32), qf[1], acc, 0, 0, 0);
; #pragma unroll
;                     for (int e = 0; e < 4; ++e) { acc[e] *= 0.125f; m = fmaxf(m, acc[e]); }
;                     sc[4 * (cc >= 0 ? cc : 0) + t4] = acc; }
;             }
;             if (sidx == NCH - 1) { m = fmaxf(m, __shfl_xor(m, 16)); m = fmaxf(m, __shfl_xor(m, 32)); }
	ds_read_b32 v240, v31 offset:38660
	ds_read_b32 v241, v31 offset:38664
	ds_read_b32 v242, v31 offset:38668
	ds_read_b32 v243, v31 offset:38672
	ds_read_b32 v244, v31 offset:38724
	ds_read_b32 v245, v31 offset:38728
	ds_read_b32 v246, v31 offset:38732
	ds_read_b32 v247, v31 offset:38736
	ds_read_b128 v[18:21], v32 offset:18432
	ds_read_b128 v[26:29], v32 offset:18496
	v_or_b32_e32 v24, 64, v34
	v_mov_b64_e32 v[22:23], s[8:9]
	v_mad_i64_i32 v[22:23], s[52:53], v24, s69, v[22:23]
	v_lshl_add_u64 v[22:23], v[22:23], 0, v[70:71]
	v_lshl_add_u64 v[22:23], v[22:23], 0, s[2:3]
	s_waitcnt lgkmcnt(1)
	v_mfma_f32_16x16x32_bf16 v[36:39], v[18:21], v[6:9], 0
	global_load_dwordx4 v[18:21], v[22:23], off offset:1024
	s_nop 0
	global_load_dwordx4 v[22:25], v[22:23], off offset:1152
	v_mov_b32_e32 v147, 0xf149f2ca
	v_mov_b32_e32 v148, 0xf149f2ca
	s_waitcnt lgkmcnt(0)
	v_mfma_f32_16x16x32_bf16 v[26:29], v[26:29], v[2:5], v[36:39]
	s_nop 2
	s_waitcnt lgkmcnt(0)
	s_nop 3
	v_fmac_f32_e32 v240, 0x3e000000, v26
	v_cndmask_b32_e64 v148, v148, v240, s[28:29]
	s_nop 2
	s_waitcnt lgkmcnt(0)
	s_nop 0
	v_fmac_f32_e32 v241, 0x3e000000, v27
	v_cndmask_b32_e64 v147, v147, v241, s[30:31]
	v_mov_b32_e32 v150, 0xf149f2ca
	v_mov_b32_e32 v151, 0xf149f2ca
	s_nop 2
	s_waitcnt lgkmcnt(0)
	v_fmac_f32_e32 v242, 0x3e000000, v28
	v_cndmask_b32_e64 v151, v151, v242, s[34:35]
	s_nop 2
	s_waitcnt lgkmcnt(0)
	v_fmac_f32_e32 v243, 0x3e000000, v29
	v_cndmask_b32_e64 v150, v150, v243, s[36:37]
	ds_read_b128 v[26:29], v33 offset:18432
	ds_read_b128 v[36:39], v33 offset:18496
	v_mov_b32_e32 v152, 0xf149f2ca
	v_mov_b32_e32 v154, 0xf149f2ca
	s_waitcnt lgkmcnt(1)
	v_mfma_f32_16x16x32_bf16 v[26:29], v[26:29], v[6:9], 0
	s_waitcnt lgkmcnt(0)
	v_mfma_f32_16x16x32_bf16 v[26:29], v[36:39], v[2:5], v[26:29]
	s_nop 2
	s_waitcnt lgkmcnt(0)
	s_nop 3
	v_fmac_f32_e32 v244, 0x3e000000, v26
	v_cndmask_b32_e64 v154, v154, v244, s[38:39]
	s_nop 2
	s_waitcnt lgkmcnt(0)
	s_nop 0
	v_fmac_f32_e32 v245, 0x3e000000, v27
	v_cndmask_b32_e64 v152, v152, v245, s[44:45]
	v_mov_b32_e32 v153, 0xf149f2ca
	v_mov_b32_e32 v156, 0xf149f2ca
	s_nop 2
	s_waitcnt lgkmcnt(0)
	v_fmac_f32_e32 v246, 0x3e000000, v28
	v_cndmask_b32_e64 v156, v156, v246, s[46:47]
	s_nop 2
	s_waitcnt lgkmcnt(0)
	v_fmac_f32_e32 v247, 0x3e000000, v29
	v_cndmask_b32_e64 v153, v153, v247, s[48:49]
	v_max3_f32 v26, v91, s74, v90
	v_max3_f32 v26, v26, v93, v92
	v_max3_f32 v26, v26, v95, v94
	v_max3_f32 v26, v26, v98, v96
	v_max3_f32 v26, v26, v99, v97
	v_max3_f32 v26, v26, v101, v100
	v_max3_f32 v26, v26, v104, v102
	v_max3_f32 v26, v26, v108, v106
	v_max3_f32 v26, v26, v105, v103
	v_max3_f32 v26, v26, v109, v107
	v_max3_f32 v26, v26, v112, v110
	v_max3_f32 v26, v26, v115, v111
	v_max3_f32 v26, v26, v114, v113
	v_max3_f32 v26, v26, v117, v116
	v_max3_f32 v26, v26, v120, v118
	v_max3_f32 v26, v26, v123, v119
	v_max3_f32 v26, v26, v122, v121
	v_max3_f32 v26, v26, v125, v124
	v_max3_f32 v26, v26, v128, v126
	v_max3_f32 v26, v26, v132, v127
	v_max3_f32 v26, v26, v131, v129
	v_max3_f32 v26, v26, v134, v133
	v_max3_f32 v26, v26, v138, v136
	v_max3_f32 v26, v26, v141, v137
	v_max3_f32 v26, v26, v140, v139
	v_max3_f32 v26, v26, v143, v142
	v_mad_u32_u24 v88, v88, s70, v30
	v_max3_f32 v26, v26, v146, v144
	s_waitcnt vmcnt(3)
	ds_write_b128 v75, v[10:13]
	s_waitcnt vmcnt(2)
	ds_write_b128 v75, v[14:17] offset:9216
	s_waitcnt lgkmcnt(0)
	s_barrier
	ds_read_b128 v[10:13], v88
	ds_read_b128 v[14:17], v88 offset:64
	v_max3_f32 v26, v26, v149, v145
	v_max3_f32 v26, v26, v148, v147
	v_max3_f32 v26, v26, v151, v150
	v_max3_f32 v26, v26, v154, v152
	v_max3_f32 v35, v26, v156, v153
	v_or_b32_e32 v26, 0x80, v34
	v_mov_b64_e32 v[44:45], s[8:9]
	v_mad_i64_i32 v[26:27], s[28:29], v26, s69, v[44:45]
	v_lshl_add_u64 v[26:27], v[26:27], 0, v[70:71]
	v_lshl_add_u64 v[30:31], v[26:27], 0, s[2:3]
	s_waitcnt lgkmcnt(1)
	v_mfma_f32_16x16x32_bf16 v[10:13], v[10:13], v[6:9], 0
	global_load_dwordx4 v[26:29], v[30:31], off offset:1024
	s_nop 0
	global_load_dwordx4 v[30:33], v[30:31], off offset:1152
	ds_read_b128 v[36:39], v88 offset:2304
	v_lshl_add_u64 v[78:79], s[4:5], 0, v[70:71]
	s_waitcnt lgkmcnt(1)
	v_mfma_f32_16x16x32_bf16 v[62:65], v[14:17], v[2:5], v[10:13]
	s_ashr_i32 s17, s16, 31
	v_mov_b32_e32 v81, v71
	v_cmp_lt_i32_e32 vcc, v82, v83
	ds_read_b128 v[10:13], v88 offset:2368
	v_add3_u32 v155, v85, v76, v86
	s_nop 2
	v_mul_f32_e32 v14, 0x3e000000, v62
	v_mul_f32_e32 v15, 0x3e000000, v63
	v_max3_f32 v35, v35, v14, v15
	v_mul_f32_e32 v40, 0x3e000000, v64
	s_waitcnt lgkmcnt(1)
	v_mfma_f32_16x16x32_bf16 v[14:17], v[36:39], v[6:9], 0
	v_mul_f32_e32 v36, 0x3e000000, v65
	v_max3_f32 v35, v35, v40, v36
	ds_read_b128 v[36:39], v88 offset:4608
	s_waitcnt lgkmcnt(1)
	v_mfma_f32_16x16x32_bf16 v[66:69], v[10:13], v[2:5], v[14:17]
	ds_read_b128 v[10:13], v88 offset:4672
	s_ashr_i32 s19, s18, 31
	s_ashr_i32 s21, s20, 31
	s_ashr_i32 s23, s22, 31
	s_ashr_i32 s25, s24, 31
	s_nop 2
	v_mul_f32_e32 v14, 0x3e000000, v66
	v_mul_f32_e32 v15, 0x3e000000, v67
	v_max3_f32 v35, v35, v14, v15
	s_waitcnt lgkmcnt(1)
	v_mfma_f32_16x16x32_bf16 v[14:17], v[36:39], v[6:9], 0
	v_mul_f32_e32 v40, 0x3e000000, v68
	v_mul_f32_e32 v41, 0x3e000000, v69
	v_max3_f32 v35, v35, v40, v41
	s_waitcnt lgkmcnt(0)
	v_mfma_f32_16x16x32_bf16 v[58:61], v[10:13], v[2:5], v[14:17]
	ds_read_b128 v[36:39], v88 offset:6912
	ds_read_b128 v[40:43], v88 offset:6976
	s_waitcnt vmcnt(3)
	ds_write_b128 v75, v[18:21] offset:18432
	s_waitcnt vmcnt(2)
	ds_write_b128 v75, v[22:25] offset:27648
	s_waitcnt lgkmcnt(0)
	s_nop 0
	v_mul_f32_e32 v10, 0x3e000000, v58
	v_mul_f32_e32 v11, 0x3e000000, v59
	v_max3_f32 v14, v35, v10, v11
	v_mfma_f32_16x16x32_bf16 v[10:13], v[36:39], v[6:9], 0
	v_mul_f32_e32 v15, 0x3e000000, v60
	v_mul_f32_e32 v16, 0x3e000000, v61
	v_max3_f32 v14, v14, v15, v16
	v_mfma_f32_16x16x32_bf16 v[54:57], v[40:43], v[2:5], v[10:13]
	s_barrier
; #define LAS __attribute__((address_space(3)))
; template <bool LOCAL>
; __device__ __forceinline__ void na_unit(const bf16* P, const bf16* VT, bf16* YCAT, const LAS float* rpb_l, LAS bf16* buf, int b, int gr, int hp, int qblk, int tid) {
;     ...
;                 const int cc = c - NLOC;
; #pragma unroll
;                 for (int t4 = 0; t4 < 4; ++t4) {
;                     const LAS bf16* kp = cb + (16 * t4 + fr) * 72 + 8 * fq;
;                     f32x4 acc = {0.f, 0.f, 0.f, 0.f};
;                     acc = __builtin_amdgcn_mfma_f32_16x16x32_bf16(*(const LAS bf16x8*)(kp), qf[0], acc, 0, 0, 0);
;                     acc = __builtin_amdgcn_mfma_f32_16x16x32_bf16(*(const LAS bf16x8*)(kp + 32), qf[1], acc, 0, 0, 0);
; #pragma unroll
;                     for (int e = 0; e < 4; ++e) { acc[e] *= 0.125f; m = fmaxf(m, acc[e]); }
;                     sc[4 * (cc >= 0 ? cc : 0) + t4] = acc; }
;             }
;             if (sidx == NCH - 1) { m = fmaxf(m, __shfl_xor(m, 16)); m = fmaxf(m, __shfl_xor(m, 32)); }
	v_or_b32_e32 v18, 0xc0, v34
	v_mad_i64_i32 v[18:19], s[28:29], v18, s69, v[44:45]
	v_lshl_add_u64 v[18:19], v[18:19], 0, v[70:71]
	s_nop 3
	v_mul_f32_e32 v10, 0x3e000000, v54
	v_mul_f32_e32 v11, 0x3e000000, v55
	v_max3_f32 v14, v14, v10, v11
	ds_read_b128 v[10:13], v88 offset:18432
	v_mul_f32_e32 v15, 0x3e000000, v56
	v_mul_f32_e32 v16, 0x3e000000, v57
	v_max3_f32 v35, v14, v15, v16
	ds_read_b128 v[14:17], v88 offset:18496
	v_lshl_add_u64 v[22:23], v[18:19], 0, s[2:3]
	s_waitcnt lgkmcnt(1)
	v_mfma_f32_16x16x32_bf16 v[10:13], v[10:13], v[6:9], 0
	global_load_dwordx4 v[18:21], v[22:23], off offset:1024
	global_load_dwordx4 v[158:161], v[22:23], off offset:1152
	ds_read_b128 v[22:25], v88 offset:20736
	s_ashr_i32 s27, s26, 31
	s_waitcnt lgkmcnt(1)
	v_mfma_f32_16x16x32_bf16 v[46:49], v[14:17], v[2:5], v[10:13]
	s_nop 2
	ds_read_b128 v[10:13], v88 offset:20800
	s_nop 3
	v_mul_f32_e32 v14, 0x3e000000, v46
	v_mul_f32_e32 v15, 0x3e000000, v47
	v_max3_f32 v34, v35, v14, v15
	v_mul_f32_e32 v35, 0x3e000000, v48
	s_waitcnt lgkmcnt(1)
	v_mfma_f32_16x16x32_bf16 v[14:17], v[22:25], v[6:9], 0
	v_mul_f32_e32 v22, 0x3e000000, v49
	v_max3_f32 v34, v34, v35, v22
	ds_read_b128 v[22:25], v88 offset:23040
	s_waitcnt lgkmcnt(1)
	v_mfma_f32_16x16x32_bf16 v[50:53], v[10:13], v[2:5], v[14:17]
	ds_read_b128 v[10:13], v88 offset:23104
	s_nop 6
	v_mul_f32_e32 v14, 0x3e000000, v50
	v_mul_f32_e32 v15, 0x3e000000, v51
	v_max3_f32 v34, v34, v14, v15
	s_waitcnt lgkmcnt(1)
	v_mfma_f32_16x16x32_bf16 v[14:17], v[22:25], v[6:9], 0
	v_mul_f32_e32 v35, 0x3e000000, v52
	v_mul_f32_e32 v36, 0x3e000000, v53
	v_max3_f32 v38, v34, v35, v36
	s_waitcnt lgkmcnt(0)
	v_mfma_f32_16x16x32_bf16 v[42:45], v[10:13], v[2:5], v[14:17]
	ds_read_b128 v[22:25], v88 offset:25344
	ds_read_b128 v[34:37], v88 offset:25408
	s_waitcnt vmcnt(3)
	ds_write_b128 v75, v[26:29]
	s_waitcnt vmcnt(2)
	ds_write_b128 v75, v[30:33] offset:9216
	s_waitcnt lgkmcnt(0)
	s_nop 0
	v_mul_f32_e32 v10, 0x3e000000, v42
	v_mul_f32_e32 v11, 0x3e000000, v43
	v_max3_f32 v14, v38, v10, v11
	v_mfma_f32_16x16x32_bf16 v[10:13], v[22:25], v[6:9], 0
	v_mul_f32_e32 v15, 0x3e000000, v44
	v_mul_f32_e32 v16, 0x3e000000, v45
	v_max3_f32 v14, v14, v15, v16
	v_mfma_f32_16x16x32_bf16 v[38:41], v[34:37], v[2:5], v[10:13]
	s_barrier
	v_add3_u32 v26, v87, s1, 64
	v_mul_u32_u24_e32 v26, 0x9000, v26
	v_lshl_add_u64 v[22:23], s[16:17], 1, v[78:79]
	s_nop 3
	v_mul_f32_e32 v10, 0x3e000000, v38
	v_mul_f32_e32 v11, 0x3e000000, v39
	v_max3_f32 v10, v14, v10, v11
	v_mul_f32_e32 v11, 0x3e000000, v40
	v_mul_f32_e32 v12, 0x3e000000, v41
	v_max3_f32 v34, v10, v11, v12
	v_or_b32_e32 v10, s1, v87
	v_mul_u32_u24_e32 v14, 0x9000, v10
	ds_read_b128 v[10:13], v88
	v_lshlrev_b32_e32 v70, 1, v14
	ds_read_b128 v[14:17], v88 offset:64
	v_lshlrev_b32_e32 v80, 1, v26
	v_lshl_add_u64 v[24:25], v[22:23], 0, v[70:71]
	v_lshl_add_u64 v[22:23], v[22:23], 0, v[80:81]
	s_waitcnt lgkmcnt(1)
	v_mfma_f32_16x16x32_bf16 v[10:13], v[10:13], v[6:9], 0
	global_load_dwordx4 v[162:165], v[24:25], off
	global_load_dwordx4 v[166:169], v[22:23], off
	ds_read_b128 v[22:25], v88 offset:2304
	s_add_i32 s16, s15, s50
	s_waitcnt lgkmcnt(1)
	v_mfma_f32_16x16x32_bf16 v[30:33], v[14:17], v[2:5], v[10:13]
	s_ashr_i32 s17, s16, 31
	s_ashr_i32 s15, s14, 31
	s_ashr_i32 s1, s0, 31
	ds_read_b128 v[10:13], v88 offset:2368
	s_nop 3
	v_mul_f32_e32 v14, 0x3e000000, v30
	v_mul_f32_e32 v15, 0x3e000000, v31
	v_max3_f32 v26, v34, v14, v15
	v_mul_f32_e32 v27, 0x3e000000, v32
	s_waitcnt lgkmcnt(1)
	v_mfma_f32_16x16x32_bf16 v[14:17], v[22:25], v[6:9], 0
	v_mul_f32_e32 v22, 0x3e000000, v33
	v_max3_f32 v26, v26, v27, v22
	ds_read_b128 v[22:25], v88 offset:4608
	s_waitcnt lgkmcnt(1)
	v_mfma_f32_16x16x32_bf16 v[34:37], v[10:13], v[2:5], v[14:17]
	ds_read_b128 v[10:13], v88 offset:4672
	s_nop 6
	v_mul_f32_e32 v14, 0x3e000000, v34
	v_mul_f32_e32 v15, 0x3e000000, v35
	v_max3_f32 v26, v26, v14, v15
	s_waitcnt lgkmcnt(1)
	v_mfma_f32_16x16x32_bf16 v[14:17], v[22:25], v[6:9], 0
	v_mul_f32_e32 v27, 0x3e000000, v36
	v_mul_f32_e32 v28, 0x3e000000, v37
	v_max3_f32 v87, v26, v27, v28
	s_waitcnt lgkmcnt(0)
	v_mfma_f32_16x16x32_bf16 v[26:29], v[10:13], v[2:5], v[14:17]
	ds_read_b128 v[22:25], v88 offset:6912
	ds_read_b128 v[170:173], v88 offset:6976
	s_waitcnt vmcnt(3)
	ds_write_b128 v75, v[18:21] offset:18432
	s_waitcnt vmcnt(2)
	ds_write_b128 v75, v[158:161] offset:27648
	s_waitcnt lgkmcnt(0)
	s_nop 0
	v_mul_f32_e32 v10, 0x3e000000, v26
	v_mul_f32_e32 v11, 0x3e000000, v27
	v_max3_f32 v14, v87, v10, v11
	v_mfma_f32_16x16x32_bf16 v[10:13], v[22:25], v[6:9], 0
	v_mul_f32_e32 v15, 0x3e000000, v28
	v_mul_f32_e32 v16, 0x3e000000, v29
	v_max3_f32 v14, v14, v15, v16
	v_mfma_f32_16x16x32_bf16 v[22:25], v[170:173], v[2:5], v[10:13]
	s_barrier
; #define LAS __attribute__((address_space(3)))
; __device__ __forceinline__ unsigned cvt_pk_bf16(float lo, float hi) { const float __attribute__((ext_vector_type(2))) v = {lo, hi}; return __builtin_bit_cast(unsigned, __builtin_convertvector(v, bf16x2_t)); }
; template <bool LOCAL>
; __device__ __forceinline__ void na_unit(const bf16* P, const bf16* VT, bf16* YCAT, const LAS float* rpb_l, LAS bf16* buf, int b, int gr, int hp, int qblk, int tid) {
;     ...
;                 const int cc = c - NLOC;
; #pragma unroll
;                 for (int t4 = 0; t4 < 4; ++t4) {
;                     const LAS bf16* kp = cb + (16 * t4 + fr) * 72 + 8 * fq;
;                     f32x4 acc = {0.f, 0.f, 0.f, 0.f};
;                     acc = __builtin_amdgcn_mfma_f32_16x16x32_bf16(*(const LAS bf16x8*)(kp), qf[0], acc, 0, 0, 0);
;                     acc = __builtin_amdgcn_mfma_f32_16x16x32_bf16(*(const LAS bf16x8*)(kp + 32), qf[1], acc, 0, 0, 0);
; #pragma unroll
;                     for (int e = 0; e < 4; ++e) { acc[e] *= 0.125f; m = fmaxf(m, acc[e]); }
;                     sc[4 * (cc >= 0 ? cc : 0) + t4] = acc; }
;             }
;             if (sidx == NCH - 1) { m = fmaxf(m, __shfl_xor(m, 16)); m = fmaxf(m, __shfl_xor(m, 32)); }
;         } else {
;             const int c = sidx - NCH;
;             if (LOCAL && c < 8) {
;                 float p[8];
; #pragma unroll
;                 for (int e = 0; e < 4; ++e) { p[e] = __expf(sl[2 * (c < 8 ? c : 0)][e] - m); p[4 + e] = __expf(sl[2 * (c < 8 ? c : 0) + 1][e] - m); }
; #pragma unroll
;                 for (int e = 0; e < 8; ++e) lsum += p[e];
;                 const bf16x8 pf = __builtin_bit_cast(bf16x8, (v4u){pg8::cvt_pk_bf16(p[0], p[1]), pg8::cvt_pk_bf16(p[2], p[3]), pg8::cvt_pk_bf16(p[4], p[5]), pg8::cvt_pk_bf16(p[6], p[7])});
; #pragma unroll
;                 for (int dt = 0; dt < 4; ++dt) { const LAS bf16* vp = cb + (16 * dt + fr) * 72 + kc0 + 4 * fq;
;                     o[dt] = __builtin_amdgcn_mfma_f32_16x16x32_bf16(frag44(vp, vp + 16), pf, o[dt], 0, 0, 0); }
	v_lshl_add_u64 v[18:19], s[16:17], 1, v[78:79]
	v_lshl_add_u64 v[20:21], v[18:19], 0, v[70:71]
	v_lshl_add_u64 v[18:19], v[18:19], 0, v[80:81]
	s_nop 3
	v_mul_f32_e32 v10, 0x3e000000, v22
	v_mul_f32_e32 v11, 0x3e000000, v23
	v_max3_f32 v14, v14, v10, v11
	ds_read_b128 v[10:13], v88 offset:18432
	v_mul_f32_e32 v15, 0x3e000000, v24
	v_mul_f32_e32 v16, 0x3e000000, v25
	v_max3_f32 v87, v14, v15, v16
	ds_read_b128 v[14:17], v88 offset:18496
	s_waitcnt lgkmcnt(1)
	v_mfma_f32_16x16x32_bf16 v[10:13], v[10:13], v[6:9], 0
	global_load_dwordx4 v[158:161], v[20:21], off
	global_load_dwordx4 v[170:173], v[18:19], off
	ds_read_b128 v[18:21], v88 offset:20736
	ds_read_b128 v[174:177], v88 offset:23040
	s_waitcnt lgkmcnt(2)
	v_mfma_f32_16x16x32_bf16 v[14:17], v[14:17], v[2:5], v[10:13]
	s_nop 2
	ds_read_b128 v[10:13], v88 offset:20800
	s_waitcnt lgkmcnt(2)
	v_mfma_f32_16x16x32_bf16 v[18:21], v[18:21], v[6:9], 0
	s_nop 1
	v_mul_f32_e32 v130, 0x3e000000, v14
	v_mul_f32_e32 v135, 0x3e000000, v15
	v_max3_f32 v87, v87, v130, v135
	s_waitcnt lgkmcnt(0)
	v_mfma_f32_16x16x32_bf16 v[18:21], v[10:13], v[2:5], v[18:21]
	ds_read_b128 v[10:13], v88 offset:23104
	ds_read_b128 v[178:181], v88 offset:25344
	ds_read_b128 v[182:185], v88 offset:25408
	v_mul_f32_e32 v130, 0x3e000000, v16
	v_mfma_f32_16x16x32_bf16 v[174:177], v[174:177], v[6:9], 0
	v_mul_f32_e32 v135, 0x3e000000, v17
	v_max3_f32 v87, v87, v130, v135
	s_nop 0
	v_mul_f32_e32 v130, 0x3e000000, v18
	s_waitcnt lgkmcnt(1)
	v_mfma_f32_16x16x32_bf16 v[6:9], v[178:181], v[6:9], 0
	v_mul_f32_e32 v135, 0x3e000000, v19
	v_max3_f32 v87, v87, v130, v135
	v_mul_f32_e32 v130, 0x3e000000, v20
	v_mfma_f32_16x16x32_bf16 v[10:13], v[10:13], v[2:5], v[174:177]
	v_mul_f32_e32 v135, 0x3e000000, v21
	v_max3_f32 v87, v87, v130, v135
	s_waitcnt vmcnt(3)
	ds_write_b128 v75, v[162:165]
	s_waitcnt vmcnt(2)
	ds_write_b128 v75, v[166:169] offset:9216
	s_waitcnt lgkmcnt(2)
	v_mfma_f32_16x16x32_bf16 v[2:5], v[182:185], v[2:5], v[6:9]
	v_mul_f32_e32 v88, 0x3e000000, v10
	v_mul_f32_e32 v130, 0x3e000000, v11
	v_max3_f32 v87, v87, v88, v130
	v_mul_f32_e32 v88, 0x3e000000, v12
	v_mul_f32_e32 v130, 0x3e000000, v13
	v_max3_f32 v87, v87, v88, v130
	s_nop 1
	v_mul_f32_e32 v6, 0x3e000000, v2
	v_mul_f32_e32 v7, 0x3e000000, v3
	v_max3_f32 v6, v87, v6, v7
	v_mul_f32_e32 v7, 0x3e000000, v4
	v_mul_f32_e32 v8, 0x3e000000, v5
	v_max3_f32 v6, v6, v7, v8
	v_cndmask_b32_e32 v7, v1, v82, vcc
	v_lshlrev_b32_e32 v87, 2, v7
	ds_bpermute_b32 v7, v87, v6
	v_cmp_lt_i32_e32 vcc, v84, v83
	v_lshl_add_u32 v8, v89, 1, v155
	v_lshl_add_u64 v[182:183], s[14:15], 1, v[78:79]
	v_lshl_add_u64 v[184:185], v[182:183], 0, v[70:71]
	s_waitcnt lgkmcnt(0)
	v_max_f32_e32 v7, v7, v7
	v_max_f32_e32 v6, v6, v7
	v_cndmask_b32_e32 v7, v1, v84, vcc
	v_lshlrev_b32_e32 v88, 2, v7
	ds_bpermute_b32 v7, v88, v6
	v_lshl_add_u64 v[186:187], v[182:183], 0, v[80:81]
	s_waitcnt lgkmcnt(0)
	s_barrier
	v_max_f32_e32 v7, v7, v7
	v_max_f32_e32 v135, v6, v7
	v_sub_f32_e32 v6, v91, v135
	v_mul_f32_e32 v6, 0x3fb8aa3b, v6
	v_exp_f32_e32 v130, v6
	v_sub_f32_e32 v6, v95, v135
	v_mul_f32_e32 v6, 0x3fb8aa3b, v6
	v_exp_f32_e32 v91, v6
	v_sub_f32_e32 v6, v90, v135
	v_mul_f32_e32 v6, 0x3fb8aa3b, v6
	v_exp_f32_e32 v95, v6
	v_sub_f32_e32 v6, v94, v135
	v_mul_f32_e32 v6, 0x3fb8aa3b, v6
	v_exp_f32_e32 v90, v6
	v_sub_f32_e32 v6, v93, v135
	v_mul_f32_e32 v6, 0x3fb8aa3b, v6
	v_exp_f32_e32 v94, v6
	v_sub_f32_e32 v6, v98, v135
	v_mul_f32_e32 v6, 0x3fb8aa3b, v6
	v_exp_f32_e32 v93, v6
	v_sub_f32_e32 v6, v92, v135
	v_mul_f32_e32 v6, 0x3fb8aa3b, v6
	v_exp_f32_e32 v98, v6
	v_sub_f32_e32 v6, v96, v135
	v_mul_f32_e32 v6, 0x3fb8aa3b, v6
	v_exp_f32_e32 v92, v6
	v_add_u32_e32 v7, 0x800, v8
	v_add_u32_e32 v6, 0x1000, v8
	ds_read2_b64 v[162:165], v8 offset1:4
	ds_read2_b64 v[174:177], v7 offset0:32 offset1:36
	ds_read2_b64 v[178:181], v6 offset0:64 offset1:68
	global_load_dwordx4 v[182:185], v[184:185], off
	s_nop 0
	global_load_dwordx4 v[186:189], v[186:187], off
	v_sub_f32_e32 v9, v99, v135
	v_mul_f32_e32 v9, 0x3fb8aa3b, v9
	v_add_u32_e32 v157, 0x1800, v8
	v_exp_f32_e32 v85, v9
	v_sub_f32_e32 v9, v104, v135
	ds_read2_b64 v[190:193], v157 offset0:96 offset1:100
	v_mul_f32_e32 v9, 0x3fb8aa3b, v9
	v_exp_f32_e32 v76, v9
	v_sub_f32_e32 v9, v97, v135
	v_mul_f32_e32 v9, 0x3fb8aa3b, v9
	v_exp_f32_e32 v89, v9
	v_sub_f32_e32 v9, v102, v135
	v_mul_f32_e32 v9, 0x3fb8aa3b, v9
	v_exp_f32_e32 v86, v9
	v_sub_f32_e32 v9, v101, v135
	v_mul_f32_e32 v9, 0x3fb8aa3b, v9
	v_exp_f32_e32 v97, v9
	v_sub_f32_e32 v9, v108, v135
	v_cvt_pk_bf16_f32 v166, v130, v95
	v_cvt_pk_bf16_f32 v167, v94, v98
	v_cvt_pk_bf16_f32 v168, v91, v90
	v_cvt_pk_bf16_f32 v169, v93, v92
	s_waitcnt vmcnt(3)
	ds_write_b128 v75, v[158:161] offset:18432
	s_waitcnt vmcnt(2)
	ds_write_b128 v75, v[170:173] offset:27648
	v_mul_f32_e32 v9, 0x3fb8aa3b, v9
	v_add_u32_e32 v159, 0x4800, v8
	v_add_u32_e32 v158, 0x5000, v8
	s_waitcnt lgkmcnt(5)
	v_mfma_f32_16x16x32_bf16 v[162:165], v[162:165], v[166:169], 0
	s_waitcnt lgkmcnt(0)
	s_barrier
; #define LAS __attribute__((address_space(3)))
; __device__ __forceinline__ unsigned cvt_pk_bf16(float lo, float hi) { const float __attribute__((ext_vector_type(2))) v = {lo, hi}; return __builtin_bit_cast(unsigned, __builtin_convertvector(v, bf16x2_t)); }
; template <bool LOCAL>
; __device__ __forceinline__ void na_unit(const bf16* P, const bf16* VT, bf16* YCAT, const LAS float* rpb_l, LAS bf16* buf, int b, int gr, int hp, int qblk, int tid) {
;     ...
;             const int c = sidx - NCH;
;             if (LOCAL && c < 8) {
;                 float p[8];
; #pragma unroll
;                 for (int e = 0; e < 4; ++e) { p[e] = __expf(sl[2 * (c < 8 ? c : 0)][e] - m); p[4 + e] = __expf(sl[2 * (c < 8 ? c : 0) + 1][e] - m); }
; #pragma unroll
;                 for (int e = 0; e < 8; ++e) lsum += p[e];
;                 const bf16x8 pf = __builtin_bit_cast(bf16x8, (v4u){pg8::cvt_pk_bf16(p[0], p[1]), pg8::cvt_pk_bf16(p[2], p[3]), pg8::cvt_pk_bf16(p[4], p[5]), pg8::cvt_pk_bf16(p[6], p[7])});
; #pragma unroll
;                 for (int dt = 0; dt < 4; ++dt) { const LAS bf16* vp = cb + (16 * dt + fr) * 72 + kc0 + 4 * fq;
;                     o[dt] = __builtin_amdgcn_mfma_f32_16x16x32_bf16(frag44(vp, vp + 16), pf, o[dt], 0, 0, 0); }
	v_mfma_f32_16x16x32_bf16 v[174:177], v[174:177], v[166:169], 0
	v_exp_f32_e32 v96, v9
	v_sub_f32_e32 v9, v100, v135
	ds_read2_b64 v[170:173], v159 offset1:4
	v_mfma_f32_16x16x32_bf16 v[178:181], v[178:181], v[166:169], 0
	v_mul_f32_e32 v9, 0x3fb8aa3b, v9
	v_exp_f32_e32 v99, v9
	v_sub_f32_e32 v9, v106, v135
	v_mfma_f32_16x16x32_bf16 v[166:169], v[190:193], v[166:169], 0
	ds_read2_b64 v[190:193], v158 offset0:32 offset1:36
	v_mul_f32_e32 v9, 0x3fb8aa3b, v9
	v_exp_f32_e32 v100, v9
	v_lshl_add_u64 v[160:161], s[0:1], 1, v[78:79]
	v_cvt_pk_bf16_f32 v194, v85, v89
	v_cvt_pk_bf16_f32 v195, v97, v99
	v_cvt_pk_bf16_f32 v196, v76, v86
	v_cvt_pk_bf16_f32 v197, v96, v100
	v_lshl_add_u64 v[198:199], v[160:161], 0, v[70:71]
	v_lshl_add_u64 v[200:201], v[160:161], 0, v[80:81]
	v_add_u32_e32 v160, 0x5800, v8
	s_waitcnt lgkmcnt(1)
	v_mfma_f32_16x16x32_bf16 v[162:165], v[170:173], v[194:197], v[162:165]
	v_sub_f32_e32 v9, v105, v135
	v_mul_f32_e32 v9, 0x3fb8aa3b, v9
	v_add_u32_e32 v161, 0x6000, v8
	s_waitcnt lgkmcnt(0)
	v_mfma_f32_16x16x32_bf16 v[170:173], v[190:193], v[194:197], v[174:177]
	v_exp_f32_e32 v102, v9
	v_sub_f32_e32 v9, v112, v135
	v_mul_f32_e32 v9, 0x3fb8aa3b, v9
	ds_read2_b64 v[174:177], v160 offset0:64 offset1:68
	global_load_dwordx4 v[190:193], v[198:199], off
	s_nop 0
	global_load_dwordx4 v[198:201], v[200:201], off
	s_waitcnt lgkmcnt(0)
	v_mfma_f32_16x16x32_bf16 v[174:177], v[174:177], v[194:197], v[178:181]
	s_nop 2
	ds_read2_b64 v[178:181], v161 offset0:96 offset1:100
	v_exp_f32_e32 v101, v9
	v_sub_f32_e32 v9, v103, v135
	v_mul_f32_e32 v9, 0x3fb8aa3b, v9
	v_exp_f32_e32 v104, v9
	v_sub_f32_e32 v9, v110, v135
	v_mul_f32_e32 v9, 0x3fb8aa3b, v9
	v_exp_f32_e32 v103, v9
	v_sub_f32_e32 v9, v109, v135
	v_mul_f32_e32 v9, 0x3fb8aa3b, v9
	v_exp_f32_e32 v106, v9
	v_sub_f32_e32 v9, v115, v135
	v_mul_f32_e32 v9, 0x3fb8aa3b, v9
	s_waitcnt lgkmcnt(0)
	v_mfma_f32_16x16x32_bf16 v[166:169], v[178:181], v[194:197], v[166:169]
	s_waitcnt vmcnt(3)
	ds_write_b128 v75, v[182:185]
	s_waitcnt vmcnt(2)
	ds_write_b128 v75, v[186:189] offset:9216
	s_waitcnt lgkmcnt(0)
	s_barrier
	v_exp_f32_e32 v105, v9
	v_sub_f32_e32 v9, v107, v135
	ds_read2_b64 v[178:181], v8 offset1:4
	ds_read2_b64 v[182:185], v7 offset0:32 offset1:36
	v_mul_f32_e32 v9, 0x3fb8aa3b, v9
	v_exp_f32_e32 v107, v9
	v_sub_f32_e32 v9, v111, v135
	v_mul_f32_e32 v9, 0x3fb8aa3b, v9
	v_exp_f32_e32 v108, v9
	v_lshl_add_u64 v[194:195], s[18:19], 1, v[78:79]
	v_cvt_pk_bf16_f32 v186, v102, v104
	v_cvt_pk_bf16_f32 v187, v106, v107
	v_cvt_pk_bf16_f32 v188, v101, v103
	v_cvt_pk_bf16_f32 v189, v105, v108
	v_lshl_add_u64 v[110:111], v[194:195], 0, v[70:71]
	v_lshl_add_u64 v[194:195], v[194:195], 0, v[80:81]
	s_waitcnt lgkmcnt(1)
	v_mfma_f32_16x16x32_bf16 v[162:165], v[178:181], v[186:189], v[162:165]
	ds_read2_b64 v[178:181], v6 offset0:64 offset1:68
	v_sub_f32_e32 v9, v114, v135
	v_mul_f32_e32 v9, 0x3fb8aa3b, v9
	s_waitcnt lgkmcnt(1)
	v_mfma_f32_16x16x32_bf16 v[170:173], v[182:185], v[186:189], v[170:173]
	global_load_dwordx4 v[182:185], v[110:111], off
	s_nop 0
	global_load_dwordx4 v[194:197], v[194:195], off
	v_exp_f32_e32 v110, v9
	v_sub_f32_e32 v9, v120, v135
	s_waitcnt lgkmcnt(0)
	v_mfma_f32_16x16x32_bf16 v[174:177], v[178:181], v[186:189], v[174:177]
	ds_read2_b64 v[178:181], v157 offset0:96 offset1:100
	v_mul_f32_e32 v9, 0x3fb8aa3b, v9
	v_exp_f32_e32 v109, v9
	v_sub_f32_e32 v9, v113, v135
	v_mul_f32_e32 v9, 0x3fb8aa3b, v9
	v_exp_f32_e32 v112, v9
	v_sub_f32_e32 v9, v118, v135
	v_mul_f32_e32 v9, 0x3fb8aa3b, v9
	v_exp_f32_e32 v111, v9
	v_sub_f32_e32 v9, v117, v135
	v_mul_f32_e32 v9, 0x3fb8aa3b, v9
	v_exp_f32_e32 v114, v9
	v_sub_f32_e32 v9, v123, v135
	v_mul_f32_e32 v9, 0x3fb8aa3b, v9
	s_waitcnt lgkmcnt(0)
	v_mfma_f32_16x16x32_bf16 v[166:169], v[178:181], v[186:189], v[166:169]
	s_waitcnt vmcnt(3)
	ds_write_b128 v75, v[190:193] offset:18432
	s_waitcnt vmcnt(2)
	ds_write_b128 v75, v[198:201] offset:27648
	s_waitcnt lgkmcnt(0)
	s_barrier
	v_exp_f32_e32 v113, v9
	v_sub_f32_e32 v9, v116, v135
	ds_read2_b64 v[178:181], v159 offset1:4
	v_mul_f32_e32 v9, 0x3fb8aa3b, v9
	v_exp_f32_e32 v115, v9
	v_sub_f32_e32 v9, v119, v135
	v_mul_f32_e32 v9, 0x3fb8aa3b, v9
	v_exp_f32_e32 v116, v9
	v_lshl_add_u64 v[198:199], s[20:21], 1, v[78:79]
	v_lshl_add_u64 v[200:201], v[198:199], 0, v[70:71]
	ds_read2_b64 v[186:189], v158 offset0:32 offset1:36
	v_cvt_pk_bf16_f32 v190, v110, v112
	v_cvt_pk_bf16_f32 v191, v114, v115
	v_cvt_pk_bf16_f32 v192, v109, v111
	v_cvt_pk_bf16_f32 v193, v113, v116
	v_lshl_add_u64 v[118:119], v[198:199], 0, v[80:81]
	v_sub_f32_e32 v9, v122, v135
	s_waitcnt lgkmcnt(1)
	v_mfma_f32_16x16x32_bf16 v[162:165], v[178:181], v[190:193], v[162:165]
	global_load_dwordx4 v[178:181], v[200:201], off
	s_nop 0
	global_load_dwordx4 v[198:201], v[118:119], off
	v_mul_f32_e32 v9, 0x3fb8aa3b, v9
	v_exp_f32_e32 v118, v9
	s_waitcnt lgkmcnt(0)
	v_mfma_f32_16x16x32_bf16 v[170:173], v[186:189], v[190:193], v[170:173]
	ds_read2_b64 v[186:189], v160 offset0:64 offset1:68
	v_sub_f32_e32 v9, v128, v135
	v_mul_f32_e32 v9, 0x3fb8aa3b, v9
	s_waitcnt lgkmcnt(0)
	v_mfma_f32_16x16x32_bf16 v[174:177], v[186:189], v[190:193], v[174:177]
	ds_read2_b64 v[186:189], v161 offset0:96 offset1:100
	v_exp_f32_e32 v117, v9
	v_sub_f32_e32 v9, v121, v135
	v_mul_f32_e32 v9, 0x3fb8aa3b, v9
	v_exp_f32_e32 v120, v9
	v_sub_f32_e32 v9, v126, v135
	v_mul_f32_e32 v9, 0x3fb8aa3b, v9
	v_exp_f32_e32 v119, v9
	v_sub_f32_e32 v9, v125, v135
	v_mul_f32_e32 v9, 0x3fb8aa3b, v9
	v_exp_f32_e32 v122, v9
	v_sub_f32_e32 v9, v132, v135
	v_mul_f32_e32 v9, 0x3fb8aa3b, v9
	s_waitcnt lgkmcnt(0)
	v_mfma_f32_16x16x32_bf16 v[166:169], v[186:189], v[190:193], v[166:169]
	s_waitcnt vmcnt(3)
	ds_write_b128 v75, v[182:185]
	s_waitcnt vmcnt(2)
	ds_write_b128 v75, v[194:197] offset:9216
	s_waitcnt lgkmcnt(0)
	s_barrier
; #define LAS __attribute__((address_space(3)))
; __device__ __forceinline__ unsigned cvt_pk_bf16(float lo, float hi) { const float __attribute__((ext_vector_type(2))) v = {lo, hi}; return __builtin_bit_cast(unsigned, __builtin_convertvector(v, bf16x2_t)); }
; template <bool LOCAL>
; __device__ __forceinline__ void na_unit(const bf16* P, const bf16* VT, bf16* YCAT, const LAS float* rpb_l, LAS bf16* buf, int b, int gr, int hp, int qblk, int tid) {
;     ...
;             const int c = sidx - NCH;
;             if (LOCAL && c < 8) {
;                 float p[8];
; #pragma unroll
;                 for (int e = 0; e < 4; ++e) { p[e] = __expf(sl[2 * (c < 8 ? c : 0)][e] - m); p[4 + e] = __expf(sl[2 * (c < 8 ? c : 0) + 1][e] - m); }
; #pragma unroll
;                 for (int e = 0; e < 8; ++e) lsum += p[e];
;                 const bf16x8 pf = __builtin_bit_cast(bf16x8, (v4u){pg8::cvt_pk_bf16(p[0], p[1]), pg8::cvt_pk_bf16(p[2], p[3]), pg8::cvt_pk_bf16(p[4], p[5]), pg8::cvt_pk_bf16(p[6], p[7])});
; #pragma unroll
;                 for (int dt = 0; dt < 4; ++dt) { const LAS bf16* vp = cb + (16 * dt + fr) * 72 + kc0 + 4 * fq;
;                     o[dt] = __builtin_amdgcn_mfma_f32_16x16x32_bf16(frag44(vp, vp + 16), pf, o[dt], 0, 0, 0); }
	v_exp_f32_e32 v121, v9
	v_sub_f32_e32 v9, v124, v135
	ds_read2_b64 v[182:185], v8 offset1:4
	ds_read2_b64 v[186:189], v7 offset0:32 offset1:36
	v_mul_f32_e32 v9, 0x3fb8aa3b, v9
	v_exp_f32_e32 v123, v9
	v_sub_f32_e32 v9, v127, v135
	v_mul_f32_e32 v9, 0x3fb8aa3b, v9
	v_exp_f32_e32 v124, v9
	v_lshl_add_u64 v[194:195], s[22:23], 1, v[78:79]
	v_cvt_pk_bf16_f32 v190, v118, v120
	v_cvt_pk_bf16_f32 v191, v122, v123
	v_cvt_pk_bf16_f32 v192, v117, v119
	v_cvt_pk_bf16_f32 v193, v121, v124
	v_lshl_add_u64 v[126:127], v[194:195], 0, v[70:71]
	v_lshl_add_u64 v[194:195], v[194:195], 0, v[80:81]
	s_waitcnt lgkmcnt(1)
	v_mfma_f32_16x16x32_bf16 v[162:165], v[182:185], v[190:193], v[162:165]
	ds_read2_b64 v[182:185], v6 offset0:64 offset1:68
	v_sub_f32_e32 v9, v131, v135
	v_mul_f32_e32 v9, 0x3fb8aa3b, v9
	s_waitcnt lgkmcnt(1)
	v_mfma_f32_16x16x32_bf16 v[170:173], v[186:189], v[190:193], v[170:173]
	global_load_dwordx4 v[186:189], v[126:127], off
	s_nop 0
	global_load_dwordx4 v[194:197], v[194:195], off
	v_exp_f32_e32 v126, v9
	v_sub_f32_e32 v9, v138, v135
	v_mul_f32_e32 v9, 0x3fb8aa3b, v9
	v_exp_f32_e32 v125, v9
	v_sub_f32_e32 v9, v129, v135
	v_mul_f32_e32 v9, 0x3fb8aa3b, v9
	v_exp_f32_e32 v128, v9
	v_sub_f32_e32 v9, v136, v135
	v_mul_f32_e32 v9, 0x3fb8aa3b, v9
	v_exp_f32_e32 v127, v9
	v_sub_f32_e32 v9, v134, v135
	v_mul_f32_e32 v9, 0x3fb8aa3b, v9
	v_exp_f32_e32 v131, v9
	v_sub_f32_e32 v9, v141, v135
	s_waitcnt lgkmcnt(0)
	v_mfma_f32_16x16x32_bf16 v[174:177], v[182:185], v[190:193], v[174:177]
	ds_read2_b64 v[182:185], v157 offset0:96 offset1:100
	v_mul_f32_e32 v9, 0x3fb8aa3b, v9
	s_waitcnt vmcnt(3)
	ds_write_b128 v75, v[178:181] offset:18432
	s_waitcnt vmcnt(2)
	ds_write_b128 v75, v[198:201] offset:27648
	s_waitcnt lgkmcnt(0)
	s_barrier
	v_exp_f32_e32 v129, v9
	v_sub_f32_e32 v9, v133, v135
	ds_read2_b64 v[178:181], v159 offset1:4
	v_mul_f32_e32 v9, 0x3fb8aa3b, v9
	v_exp_f32_e32 v132, v9
	v_sub_f32_e32 v9, v137, v135
	v_mul_f32_e32 v9, 0x3fb8aa3b, v9
	v_exp_f32_e32 v133, v9
	v_lshl_add_u64 v[198:199], s[24:25], 1, v[78:79]
	v_mfma_f32_16x16x32_bf16 v[166:169], v[182:185], v[190:193], v[166:169]
	v_lshl_add_u64 v[200:201], v[198:199], 0, v[70:71]
	ds_read2_b64 v[182:185], v158 offset0:32 offset1:36
	v_cvt_pk_bf16_f32 v190, v126, v128
	v_cvt_pk_bf16_f32 v191, v131, v132
	v_cvt_pk_bf16_f32 v192, v125, v127
	v_cvt_pk_bf16_f32 v193, v129, v133
	v_lshl_add_u64 v[136:137], v[198:199], 0, v[80:81]
	v_sub_f32_e32 v9, v140, v135
	s_waitcnt lgkmcnt(1)
	v_mfma_f32_16x16x32_bf16 v[162:165], v[178:181], v[190:193], v[162:165]
	global_load_dwordx4 v[178:181], v[200:201], off
	s_nop 0
	global_load_dwordx4 v[198:201], v[136:137], off
	v_mul_f32_e32 v9, 0x3fb8aa3b, v9
	v_exp_f32_e32 v136, v9
	s_waitcnt lgkmcnt(0)
	v_mfma_f32_16x16x32_bf16 v[170:173], v[182:185], v[190:193], v[170:173]
	ds_read2_b64 v[182:185], v160 offset0:64 offset1:68
	v_sub_f32_e32 v9, v146, v135
	v_mul_f32_e32 v9, 0x3fb8aa3b, v9
	s_waitcnt lgkmcnt(0)
	v_mfma_f32_16x16x32_bf16 v[174:177], v[182:185], v[190:193], v[174:177]
	ds_read2_b64 v[182:185], v161 offset0:96 offset1:100
	v_exp_f32_e32 v134, v9
	v_sub_f32_e32 v9, v139, v135
	v_mul_f32_e32 v9, 0x3fb8aa3b, v9
	v_exp_f32_e32 v138, v9
	v_sub_f32_e32 v9, v144, v135
	v_mul_f32_e32 v9, 0x3fb8aa3b, v9
	v_exp_f32_e32 v137, v9
	v_sub_f32_e32 v9, v143, v135
	v_mul_f32_e32 v9, 0x3fb8aa3b, v9
	s_waitcnt lgkmcnt(0)
	v_mfma_f32_16x16x32_bf16 v[166:169], v[182:185], v[190:193], v[166:169]
	s_waitcnt vmcnt(3)
	ds_write_b128 v75, v[186:189]
	s_waitcnt vmcnt(2)
	ds_write_b128 v75, v[194:197] offset:9216
	s_waitcnt lgkmcnt(0)
	s_barrier
	v_exp_f32_e32 v140, v9
	v_sub_f32_e32 v9, v149, v135
	ds_read2_b64 v[182:185], v8 offset1:4
	v_mul_f32_e32 v9, 0x3fb8aa3b, v9
	ds_read2_b64 v[190:193], v7 offset0:32 offset1:36
	v_exp_f32_e32 v139, v9
	v_sub_f32_e32 v9, v142, v135
	v_sub_f32_e32 v8, v145, v135
	v_mul_f32_e32 v9, 0x3fb8aa3b, v9
	v_mul_f32_e32 v8, 0x3fb8aa3b, v8
	v_exp_f32_e32 v141, v9
	v_exp_f32_e32 v142, v8
	v_cvt_pk_bf16_f32 v186, v136, v138
	v_cvt_pk_bf16_f32 v188, v134, v137
	v_cvt_pk_bf16_f32 v187, v140, v141
	v_cvt_pk_bf16_f32 v189, v139, v142
	v_lshl_add_u64 v[8:9], s[26:27], 1, v[78:79]
	v_sub_f32_e32 v144, v150, v135
	s_waitcnt lgkmcnt(1)
	v_mfma_f32_16x16x32_bf16 v[162:165], v[182:185], v[186:189], v[162:165]
	ds_read2_b64 v[182:185], v6 offset0:64 offset1:68
	v_lshl_add_u64 v[6:7], v[8:9], 0, v[70:71]
	v_lshl_add_u64 v[8:9], v[8:9], 0, v[80:81]
	s_waitcnt lgkmcnt(1)
	v_mfma_f32_16x16x32_bf16 v[170:173], v[190:193], v[186:189], v[170:173]
	global_load_dwordx4 v[190:193], v[6:7], off
	global_load_dwordx4 v[194:197], v[8:9], off
	ds_read2_b64 v[78:81], v157 offset0:96 offset1:100
	s_waitcnt vmcnt(3)
	ds_write_b128 v75, v[178:181] offset:18432
	s_waitcnt vmcnt(2)
	ds_write_b128 v75, v[198:201] offset:27648
	s_waitcnt lgkmcnt(2)
	v_mfma_f32_16x16x32_bf16 v[166:169], v[78:81], v[186:189], v[166:169]
	s_waitcnt lgkmcnt(0)
	s_barrier
; #define LAS __attribute__((address_space(3)))
; __device__ __forceinline__ unsigned cvt_pk_bf16(float lo, float hi) { const float __attribute__((ext_vector_type(2))) v = {lo, hi}; return __builtin_bit_cast(unsigned, __builtin_convertvector(v, bf16x2_t)); }
; template <bool LOCAL>
; __device__ __forceinline__ void na_unit(const bf16* P, const bf16* VT, bf16* YCAT, const LAS float* rpb_l, LAS bf16* buf, int b, int gr, int hp, int qblk, int tid) {
;     ...
;             const int c = sidx - NCH;
;             if (LOCAL && c < 8) {
;                 float p[8];
; #pragma unroll
;                 for (int e = 0; e < 4; ++e) { p[e] = __expf(sl[2 * (c < 8 ? c : 0)][e] - m); p[4 + e] = __expf(sl[2 * (c < 8 ? c : 0) + 1][e] - m); }
; #pragma unroll
;                 for (int e = 0; e < 8; ++e) lsum += p[e];
;                 const bf16x8 pf = __builtin_bit_cast(bf16x8, (v4u){pg8::cvt_pk_bf16(p[0], p[1]), pg8::cvt_pk_bf16(p[2], p[3]), pg8::cvt_pk_bf16(p[4], p[5]), pg8::cvt_pk_bf16(p[6], p[7])});
; #pragma unroll
;                 for (int dt = 0; dt < 4; ++dt) { const LAS bf16* vp = cb + (16 * dt + fr) * 72 + kc0 + 4 * fq;
;                     o[dt] = __builtin_amdgcn_mfma_f32_16x16x32_bf16(frag44(vp, vp + 16), pf, o[dt], 0, 0, 0); }
;             } else {
;                 const int cc = c - NLOC;
; #pragma unroll
;                 for (int p2 = 0; p2 < 2; ++p2) {
;                     float p[8];
; #pragma unroll
;                     for (int e = 0; e < 4; ++e) { p[e] = __expf(sc[4 * (cc >= 0 ? cc : 0) + 2 * p2][e] - m); p[4 + e] = __expf(sc[4 * (cc >= 0 ? cc : 0) + 2 * p2 + 1][e] - m); }
; #pragma unroll
;                     for (int e = 0; e < 8; ++e) lsum += p[e];
;                     const bf16x8 pf = __builtin_bit_cast(bf16x8, (v4u){pg8::cvt_pk_bf16(p[0], p[1]), pg8::cvt_pk_bf16(p[2], p[3]), pg8::cvt_pk_bf16(p[4], p[5]), pg8::cvt_pk_bf16(p[6], p[7])});
; #pragma unroll
;                     for (int dt = 0; dt < 4; ++dt) { const LAS bf16* vp = cb + (16 * dt + fr) * 72 + 32 * p2 + 4 * fq;
;                         o[dt] = __builtin_amdgcn_mfma_f32_16x16x32_bf16(frag44(vp, vp + 16), pf, o[dt], 0, 0, 0); }
;                 }
	v_sub_f32_e32 v70, v148, v135
	v_sub_f32_e32 v79, v147, v135
	v_sub_f32_e32 v81, v151, v135
	ds_read2_b64 v[146:149], v159 offset1:4
	v_mul_f32_e32 v70, 0x3fb8aa3b, v70
	v_mul_f32_e32 v79, 0x3fb8aa3b, v79
	v_mul_f32_e32 v81, 0x3fb8aa3b, v81
	v_mul_f32_e32 v144, 0x3fb8aa3b, v144
	v_exp_f32_e32 v78, v70
	v_sub_f32_e32 v70, v154, v135
	v_exp_f32_e32 v80, v79
	v_sub_f32_e32 v79, v152, v135
	v_exp_f32_e32 v143, v81
	v_sub_f32_e32 v81, v156, v135
	v_exp_f32_e32 v145, v144
	v_sub_f32_e32 v144, v153, v135
	v_mul_f32_e32 v70, 0x3fb8aa3b, v70
	v_mul_f32_e32 v79, 0x3fb8aa3b, v79
	v_mul_f32_e32 v81, 0x3fb8aa3b, v81
	v_mul_f32_e32 v144, 0x3fb8aa3b, v144
	v_exp_f32_e32 v70, v70
	v_exp_f32_e32 v79, v79
	v_exp_f32_e32 v81, v81
	v_exp_f32_e32 v144, v144
	v_cvt_pk_bf16_f32 v150, v78, v80
	v_cvt_pk_bf16_f32 v151, v143, v145
	v_cvt_pk_bf16_f32 v152, v70, v79
	v_cvt_pk_bf16_f32 v153, v81, v144
	v_mfma_f32_16x16x32_bf16 v[174:177], v[182:185], v[186:189], v[174:177]
	v_fma_f32 v62, v62, s71, -v135
	v_fma_f32 v63, v63, s71, -v135
	v_fma_f32 v64, v64, s71, -v135
	s_waitcnt lgkmcnt(0)
	v_mfma_f32_16x16x32_bf16 v[162:165], v[146:149], v[150:153], v[162:165]
	ds_read2_b64 v[146:149], v158 offset0:32 offset1:36
	v_fma_f32 v65, v65, s71, -v135
	v_mul_f32_e32 v62, 0x3fb8aa3b, v62
	s_waitcnt lgkmcnt(0)
	v_mfma_f32_16x16x32_bf16 v[156:159], v[146:149], v[150:153], v[170:173]
	ds_read2_b64 v[146:149], v160 offset0:64 offset1:68
	v_mul_f32_e32 v63, 0x3fb8aa3b, v63
	v_mul_f32_e32 v64, 0x3fb8aa3b, v64
	s_waitcnt lgkmcnt(0)
	v_mfma_f32_16x16x32_bf16 v[170:173], v[146:149], v[150:153], v[174:177]
	ds_read2_b64 v[146:149], v161 offset0:96 offset1:100
	s_nop 1
	global_load_dwordx4 v[174:177], v[6:7], off offset:128
	global_load_dwordx4 v[178:181], v[8:9], off offset:128
	s_waitcnt vmcnt(3)
	ds_write_b128 v75, v[190:193]
	s_waitcnt vmcnt(2)
	ds_write_b128 v75, v[194:197] offset:9216
	s_waitcnt lgkmcnt(2)
	v_mfma_f32_16x16x32_bf16 v[148:151], v[146:149], v[150:153], v[166:169]
	s_waitcnt lgkmcnt(0)
	s_barrier
	s_nop 0
	ds_read2_b64 v[166:169], v155 offset1:4
	v_mul_f32_e32 v65, 0x3fb8aa3b, v65
	v_exp_f32_e32 v146, v62
	v_fma_f32 v62, v66, s71, -v135
	v_exp_f32_e32 v66, v63
	v_fma_f32 v63, v67, s71, -v135
	v_exp_f32_e32 v67, v64
	v_fma_f32 v64, v68, s71, -v135
	v_exp_f32_e32 v68, v65
	v_fma_f32 v65, v69, s71, -v135
	v_mul_f32_e32 v62, 0x3fb8aa3b, v62
	v_mul_f32_e32 v63, 0x3fb8aa3b, v63
	v_mul_f32_e32 v64, 0x3fb8aa3b, v64
	v_mul_f32_e32 v65, 0x3fb8aa3b, v65
	v_exp_f32_e32 v62, v62
	v_exp_f32_e32 v63, v63
	v_exp_f32_e32 v64, v64
	v_exp_f32_e32 v65, v65
	v_cvt_pk_bf16_f32 v182, v146, v66
	v_cvt_pk_bf16_f32 v183, v67, v68
	v_cvt_pk_bf16_f32 v184, v62, v63
	v_cvt_pk_bf16_f32 v185, v64, v65
	v_add_u32_e32 v147, 0x800, v155
	v_add_u32_e32 v152, 0x1000, v155
	s_waitcnt lgkmcnt(0)
	v_mfma_f32_16x16x32_bf16 v[160:163], v[166:169], v[182:185], v[162:165]
	v_add_u32_e32 v153, 0x1800, v155
	v_fma_f32 v58, v58, s71, -v135
	v_fma_f32 v54, v54, s71, -v135
	ds_read2_b64 v[164:167], v147 offset0:32 offset1:36
	s_waitcnt lgkmcnt(0)
	v_mfma_f32_16x16x32_bf16 v[156:159], v[164:167], v[182:185], v[156:159]
	ds_read2_b64 v[164:167], v152 offset0:64 offset1:68
	v_fma_f32 v59, v59, s71, -v135
	v_fma_f32 v55, v55, s71, -v135
	s_waitcnt lgkmcnt(0)
	v_mfma_f32_16x16x32_bf16 v[164:167], v[164:167], v[182:185], v[170:173]
	s_nop 2
	ds_read2_b64 v[168:171], v153 offset0:96 offset1:100
	v_fma_f32 v60, v60, s71, -v135
	v_fma_f32 v56, v56, s71, -v135
	s_waitcnt lgkmcnt(0)
	v_mfma_f32_16x16x32_bf16 v[148:151], v[168:171], v[182:185], v[148:151]
	ds_read2_b64 v[168:171], v155 offset0:8 offset1:12
	v_fma_f32 v61, v61, s71, -v135
	v_fma_f32 v57, v57, s71, -v135
	v_mul_f32_e32 v58, 0x3fb8aa3b, v58
	v_mul_f32_e32 v54, 0x3fb8aa3b, v54
	v_mul_f32_e32 v59, 0x3fb8aa3b, v59
	v_mul_f32_e32 v55, 0x3fb8aa3b, v55
	v_mul_f32_e32 v60, 0x3fb8aa3b, v60
	v_mul_f32_e32 v56, 0x3fb8aa3b, v56
	v_mul_f32_e32 v61, 0x3fb8aa3b, v61
	v_mul_f32_e32 v57, 0x3fb8aa3b, v57
	v_exp_f32_e32 v58, v58
	v_exp_f32_e32 v54, v54
	v_exp_f32_e32 v59, v59
	v_exp_f32_e32 v55, v55
	v_exp_f32_e32 v60, v60
	v_exp_f32_e32 v56, v56
	v_exp_f32_e32 v61, v61
	v_exp_f32_e32 v57, v57
	v_cvt_pk_bf16_f32 v182, v58, v59
	v_cvt_pk_bf16_f32 v184, v54, v55
	v_cvt_pk_bf16_f32 v183, v60, v61
	v_cvt_pk_bf16_f32 v185, v56, v57
	v_fma_f32 v46, v46, s71, -v135
	v_fma_f32 v47, v47, s71, -v135
	s_waitcnt lgkmcnt(0)
	v_mfma_f32_16x16x32_bf16 v[160:163], v[168:171], v[182:185], v[160:163]
	ds_read2_b64 v[168:171], v147 offset0:40 offset1:44
	v_fma_f32 v48, v48, s71, -v135
	v_mul_f32_e32 v46, 0x3fb8aa3b, v46
	s_waitcnt lgkmcnt(0)
	v_mfma_f32_16x16x32_bf16 v[156:159], v[168:171], v[182:185], v[156:159]
	ds_read2_b64 v[168:171], v152 offset0:72 offset1:76
	v_mul_f32_e32 v47, 0x3fb8aa3b, v47
	v_mul_f32_e32 v48, 0x3fb8aa3b, v48
	s_waitcnt lgkmcnt(0)
	v_mfma_f32_16x16x32_bf16 v[164:167], v[168:171], v[182:185], v[164:167]
	ds_read2_b64 v[168:171], v153 offset0:104 offset1:108
	v_exp_f32_e32 v69, v46
	v_fma_f32 v46, v50, s71, -v135
	v_exp_f32_e32 v50, v47
	v_fma_f32 v47, v51, s71, -v135
	v_exp_f32_e32 v51, v48
	v_fma_f32 v48, v52, s71, -v135
	v_add_u32_e32 v52, 0x4800, v155
	global_load_dwordx4 v[186:189], v[6:7], off offset:256
	global_load_dwordx4 v[190:193], v[8:9], off offset:256
	s_waitcnt lgkmcnt(0)
	v_mfma_f32_16x16x32_bf16 v[148:151], v[168:171], v[182:185], v[148:151]
	s_waitcnt vmcnt(3)
	ds_write_b128 v75, v[174:177] offset:18432
	s_waitcnt vmcnt(2)
	ds_write_b128 v75, v[178:181] offset:27648
	s_waitcnt lgkmcnt(0)
	s_barrier
; #define LAS __attribute__((address_space(3)))
; __device__ __forceinline__ unsigned cvt_pk_bf16(float lo, float hi) { const float __attribute__((ext_vector_type(2))) v = {lo, hi}; return __builtin_bit_cast(unsigned, __builtin_convertvector(v, bf16x2_t)); }
; template <bool LOCAL>
; __device__ __forceinline__ void na_unit(const bf16* P, const bf16* VT, bf16* YCAT, const LAS float* rpb_l, LAS bf16* buf, int b, int gr, int hp, int qblk, int tid) {
;     ...
;                 const int cc = c - NLOC;
; #pragma unroll
;                 for (int p2 = 0; p2 < 2; ++p2) {
;                     float p[8];
; #pragma unroll
;                     for (int e = 0; e < 4; ++e) { p[e] = __expf(sc[4 * (cc >= 0 ? cc : 0) + 2 * p2][e] - m); p[4 + e] = __expf(sc[4 * (cc >= 0 ? cc : 0) + 2 * p2 + 1][e] - m); }
; #pragma unroll
;                     for (int e = 0; e < 8; ++e) lsum += p[e];
;                     const bf16x8 pf = __builtin_bit_cast(bf16x8, (v4u){pg8::cvt_pk_bf16(p[0], p[1]), pg8::cvt_pk_bf16(p[2], p[3]), pg8::cvt_pk_bf16(p[4], p[5]), pg8::cvt_pk_bf16(p[6], p[7])});
; #pragma unroll
;                     for (int dt = 0; dt < 4; ++dt) { const LAS bf16* vp = cb + (16 * dt + fr) * 72 + 32 * p2 + 4 * fq;
;                         o[dt] = __builtin_amdgcn_mfma_f32_16x16x32_bf16(frag44(vp, vp + 16), pf, o[dt], 0, 0, 0); }
;                 }
	v_fma_f32 v49, v49, s71, -v135
	ds_read2_b64 v[168:171], v52 offset1:4
	v_mul_f32_e32 v49, 0x3fb8aa3b, v49
	v_exp_f32_e32 v154, v49
	v_fma_f32 v49, v53, s71, -v135
	v_mul_f32_e32 v46, 0x3fb8aa3b, v46
	v_mul_f32_e32 v47, 0x3fb8aa3b, v47
	v_mul_f32_e32 v48, 0x3fb8aa3b, v48
	v_mul_f32_e32 v49, 0x3fb8aa3b, v49
	v_exp_f32_e32 v46, v46
	v_exp_f32_e32 v47, v47
	v_exp_f32_e32 v48, v48
	v_exp_f32_e32 v53, v49
	v_cvt_pk_bf16_f32 v172, v69, v50
	v_cvt_pk_bf16_f32 v173, v51, v154
	v_cvt_pk_bf16_f32 v174, v46, v47
	v_cvt_pk_bf16_f32 v175, v48, v53
	v_add_u32_e32 v176, 0x5000, v155
	v_add_u32_e32 v177, 0x5800, v155
	s_waitcnt lgkmcnt(0)
	v_mfma_f32_16x16x32_bf16 v[160:163], v[168:171], v[172:175], v[160:163]
	ds_read2_b64 v[168:171], v176 offset0:32 offset1:36
	v_add_u32_e32 v49, 0x6000, v155
	v_fma_f32 v38, v38, s71, -v135
	s_waitcnt lgkmcnt(0)
	v_mfma_f32_16x16x32_bf16 v[156:159], v[168:171], v[172:175], v[156:159]
	ds_read2_b64 v[168:171], v177 offset0:64 offset1:68
	v_mul_f32_e32 v38, 0x3fb8aa3b, v38
	v_fma_f32 v42, v42, s71, -v135
	s_waitcnt lgkmcnt(0)
	v_mfma_f32_16x16x32_bf16 v[164:167], v[168:171], v[172:175], v[164:167]
	ds_read2_b64 v[168:171], v49 offset0:96 offset1:100
	v_mul_f32_e32 v42, 0x3fb8aa3b, v42
	v_fma_f32 v30, v30, s71, -v135
	s_waitcnt lgkmcnt(0)
	v_mfma_f32_16x16x32_bf16 v[148:151], v[168:171], v[172:175], v[148:151]
	v_exp_f32_e32 v173, v38
	v_fma_f32 v38, v43, s71, -v135
	v_mul_f32_e32 v38, 0x3fb8aa3b, v38
	v_exp_f32_e32 v174, v38
	v_fma_f32 v38, v39, s71, -v135
	v_mul_f32_e32 v38, 0x3fb8aa3b, v38
	v_exp_f32_e32 v175, v38
	v_fma_f32 v38, v44, s71, -v135
	v_mul_f32_e32 v38, 0x3fb8aa3b, v38
	v_exp_f32_e32 v178, v38
	v_fma_f32 v38, v40, s71, -v135
	v_mul_f32_e32 v38, 0x3fb8aa3b, v38
	v_exp_f32_e32 v172, v42
	v_exp_f32_e32 v179, v38
	v_fma_f32 v38, v45, s71, -v135
	ds_read2_b64 v[42:45], v52 offset0:8 offset1:12
	v_mul_f32_e32 v38, 0x3fb8aa3b, v38
	v_exp_f32_e32 v180, v38
	v_fma_f32 v38, v41, s71, -v135
	v_mul_f32_e32 v38, 0x3fb8aa3b, v38
	v_exp_f32_e32 v181, v38
	v_cvt_pk_bf16_f32 v38, v172, v174
	v_cvt_pk_bf16_f32 v39, v178, v180
	v_cvt_pk_bf16_f32 v40, v173, v175
	v_cvt_pk_bf16_f32 v41, v179, v181
	v_mul_f32_e32 v30, 0x3fb8aa3b, v30
	v_fma_f32 v22, v22, s71, -v135
	s_waitcnt lgkmcnt(0)
	v_mfma_f32_16x16x32_bf16 v[42:45], v[42:45], v[38:41], v[160:163]
	v_mul_f32_e32 v22, 0x3fb8aa3b, v22
	v_fma_f32 v26, v26, s71, -v135
	v_mul_f32_e32 v26, 0x3fb8aa3b, v26
	ds_read2_b64 v[160:163], v176 offset0:40 offset1:44
	s_waitcnt lgkmcnt(0)
	v_mfma_f32_16x16x32_bf16 v[156:159], v[160:163], v[38:41], v[156:159]
	ds_read2_b64 v[160:163], v177 offset0:72 offset1:76
	v_fma_f32 v2, v2, s71, -v135
	v_mul_f32_e32 v2, 0x3fb8aa3b, v2
	s_waitcnt lgkmcnt(0)
	v_mfma_f32_16x16x32_bf16 v[160:163], v[160:163], v[38:41], v[164:167]
	s_nop 2
	ds_read2_b64 v[164:167], v49 offset0:104 offset1:108
	global_load_dwordx4 v[168:171], v[6:7], off offset:384
	s_nop 0
	global_load_dwordx4 v[6:9], v[8:9], off offset:384
	s_waitcnt vmcnt(3)
	ds_write_b128 v75, v[186:189]
	s_waitcnt vmcnt(2)
	ds_write_b128 v75, v[190:193] offset:9216
	s_waitcnt lgkmcnt(2)
	v_mfma_f32_16x16x32_bf16 v[38:41], v[164:167], v[38:41], v[148:151]
	v_exp_f32_e32 v164, v30
	v_fma_f32 v30, v34, s71, -v135
	v_mul_f32_e32 v30, 0x3fb8aa3b, v30
	v_exp_f32_e32 v165, v30
	v_fma_f32 v30, v31, s71, -v135
	v_mul_f32_e32 v30, 0x3fb8aa3b, v30
	v_exp_f32_e32 v166, v30
	v_fma_f32 v30, v35, s71, -v135
	v_mul_f32_e32 v30, 0x3fb8aa3b, v30
	v_exp_f32_e32 v167, v30
	v_fma_f32 v30, v32, s71, -v135
	v_mul_f32_e32 v30, 0x3fb8aa3b, v30
	v_exp_f32_e32 v182, v30
	v_fma_f32 v30, v36, s71, -v135
	v_mul_f32_e32 v30, 0x3fb8aa3b, v30
	v_exp_f32_e32 v183, v30
	v_fma_f32 v30, v33, s71, -v135
	s_waitcnt lgkmcnt(0)
	s_barrier
	v_mul_f32_e32 v34, 0x3fb8aa3b, v30
	ds_read2_b64 v[30:33], v155 offset1:4
	v_exp_f32_e32 v184, v34
	v_fma_f32 v34, v37, s71, -v135
	v_mul_f32_e32 v34, 0x3fb8aa3b, v34
	v_exp_f32_e32 v185, v34
	v_cvt_pk_bf16_f32 v34, v164, v166
	v_cvt_pk_bf16_f32 v35, v182, v184
	v_cvt_pk_bf16_f32 v36, v165, v167
	v_cvt_pk_bf16_f32 v37, v183, v185
	ds_read2_b64 v[148:151], v152 offset0:64 offset1:68
	v_fma_f32 v10, v10, s71, -v135
	s_waitcnt lgkmcnt(1)
	v_mfma_f32_16x16x32_bf16 v[30:33], v[30:33], v[34:37], v[42:45]
	v_mul_f32_e32 v10, 0x3fb8aa3b, v10
	s_nop 1
	ds_read2_b64 v[42:45], v147 offset0:32 offset1:36
	s_waitcnt lgkmcnt(0)
	v_mfma_f32_16x16x32_bf16 v[42:45], v[42:45], v[34:37], v[156:159]
	s_nop 2
	ds_read2_b64 v[156:159], v153 offset0:96 offset1:100
	v_mfma_f32_16x16x32_bf16 v[148:151], v[148:151], v[34:37], v[160:163]
	s_waitcnt lgkmcnt(0)
	v_mfma_f32_16x16x32_bf16 v[34:37], v[156:159], v[34:37], v[38:41]
	v_exp_f32_e32 v157, v22
	v_fma_f32 v22, v27, s71, -v135
	v_mul_f32_e32 v22, 0x3fb8aa3b, v22
	v_exp_f32_e32 v158, v22
	v_fma_f32 v22, v23, s71, -v135
	v_mul_f32_e32 v22, 0x3fb8aa3b, v22
	v_exp_f32_e32 v159, v22
	v_fma_f32 v22, v28, s71, -v135
	v_mul_f32_e32 v22, 0x3fb8aa3b, v22
	v_exp_f32_e32 v160, v22
	v_fma_f32 v22, v24, s71, -v135
	v_mul_f32_e32 v22, 0x3fb8aa3b, v22
	v_exp_f32_e32 v156, v26
	v_exp_f32_e32 v161, v22
	v_fma_f32 v22, v29, s71, -v135
	ds_read2_b64 v[26:29], v155 offset0:8 offset1:12
	v_mul_f32_e32 v22, 0x3fb8aa3b, v22
	v_exp_f32_e32 v155, v22
	v_fma_f32 v22, v25, s71, -v135
	v_mul_f32_e32 v22, 0x3fb8aa3b, v22
	v_exp_f32_e32 v162, v22
	v_cvt_pk_bf16_f32 v22, v156, v158
	v_cvt_pk_bf16_f32 v23, v160, v155
	v_cvt_pk_bf16_f32 v24, v157, v159
	v_cvt_pk_bf16_f32 v25, v161, v162
	ds_read2_b64 v[38:41], v152 offset0:72 offset1:76
	s_waitcnt lgkmcnt(1)
	v_mfma_f32_16x16x32_bf16 v[26:29], v[26:29], v[22:25], v[30:33]
	s_nop 2
	ds_read2_b64 v[30:33], v147 offset0:40 offset1:44
	s_waitcnt lgkmcnt(0)
	v_mfma_f32_16x16x32_bf16 v[30:33], v[30:33], v[22:25], v[42:45]
	s_nop 2
	ds_read2_b64 v[42:45], v153 offset0:104 offset1:108
	s_waitcnt vmcnt(1)
	ds_write_b128 v75, v[168:171] offset:18432
	s_waitcnt vmcnt(0)
	ds_write_b128 v75, v[6:9] offset:27648
	v_fma_f32 v6, v14, s71, -v135
	v_mul_f32_e32 v6, 0x3fb8aa3b, v6
	v_mfma_f32_16x16x32_bf16 v[38:41], v[38:41], v[22:25], v[148:151]
	s_waitcnt lgkmcnt(0)
	s_barrier
; #define LAS __attribute__((address_space(3)))
; __device__ __forceinline__ unsigned cvt_pk_bf16(float lo, float hi) { const float __attribute__((ext_vector_type(2))) v = {lo, hi}; return __builtin_bit_cast(unsigned, __builtin_convertvector(v, bf16x2_t)); }
; #define NA_STORE(sidx) do { LAS bf16* d_ = buf + ((sidx) & 1) * 9216; _Pragma("unroll") for (int q_ = 0; q_ < 2; ++q_) *(LAS v4u*)(d_ + q_ * 4608 + lrow * 72 + lseg * 8) = ld[(sidx) & 1][q_]; } while (0)
; template <bool LOCAL>
; __device__ __forceinline__ void na_unit(const bf16* P, const bf16* VT, bf16* YCAT, const LAS float* rpb_l, LAS bf16* buf, int b, int gr, int hp, int qblk, int tid) {
;     ...
;                 const int cc = c - NLOC;
; #pragma unroll
;                 for (int p2 = 0; p2 < 2; ++p2) {
;                     float p[8];
; #pragma unroll
;                     for (int e = 0; e < 4; ++e) { p[e] = __expf(sc[4 * (cc >= 0 ? cc : 0) + 2 * p2][e] - m); p[4 + e] = __expf(sc[4 * (cc >= 0 ? cc : 0) + 2 * p2 + 1][e] - m); }
; #pragma unroll
;                     for (int e = 0; e < 8; ++e) lsum += p[e];
;                     const bf16x8 pf = __builtin_bit_cast(bf16x8, (v4u){pg8::cvt_pk_bf16(p[0], p[1]), pg8::cvt_pk_bf16(p[2], p[3]), pg8::cvt_pk_bf16(p[4], p[5]), pg8::cvt_pk_bf16(p[6], p[7])});
; #pragma unroll
;                     for (int dt = 0; dt < 4; ++dt) { const LAS bf16* vp = cb + (16 * dt + fr) * 72 + 32 * p2 + 4 * fq;
;                         o[dt] = __builtin_amdgcn_mfma_f32_16x16x32_bf16(frag44(vp, vp + 16), pf, o[dt], 0, 0, 0); }
;                 }
;             }
;         }
;         if (sidx + 1 < 2 * NCH) NA_STORE(sidx + 1);
;         __syncthreads();
;     }
;     ...
;     lsum += __shfl_xor(lsum, 16); lsum += __shfl_xor(lsum, 32);
	v_mfma_f32_16x16x32_bf16 v[22:25], v[42:45], v[22:25], v[34:37]
	v_ashrrev_i32_e32 v75, 31, v74
	s_nop 1
	v_exp_f32_e32 v34, v6
	v_fma_f32 v6, v18, s71, -v135
	v_mul_f32_e32 v6, 0x3fb8aa3b, v6
	v_exp_f32_e32 v35, v6
	v_fma_f32 v6, v15, s71, -v135
	v_mul_f32_e32 v6, 0x3fb8aa3b, v6
	v_exp_f32_e32 v36, v6
	v_fma_f32 v6, v19, s71, -v135
	v_mul_f32_e32 v6, 0x3fb8aa3b, v6
	v_exp_f32_e32 v37, v6
	v_fma_f32 v6, v16, s71, -v135
	v_mul_f32_e32 v6, 0x3fb8aa3b, v6
	v_exp_f32_e32 v42, v6
	v_fma_f32 v6, v20, s71, -v135
	v_mul_f32_e32 v6, 0x3fb8aa3b, v6
	v_exp_f32_e32 v43, v6
	v_fma_f32 v6, v17, s71, -v135
	v_mul_f32_e32 v14, 0x3fb8aa3b, v6
	ds_read2_b64 v[6:9], v52 offset1:4
	v_exp_f32_e32 v44, v14
	v_fma_f32 v14, v21, s71, -v135
	v_mul_f32_e32 v14, 0x3fb8aa3b, v14
	v_exp_f32_e32 v45, v14
	v_cvt_pk_bf16_f32 v14, v34, v36
	v_cvt_pk_bf16_f32 v15, v42, v44
	v_cvt_pk_bf16_f32 v16, v35, v37
	v_cvt_pk_bf16_f32 v17, v43, v45
	ds_read2_b64 v[18:21], v176 offset0:32 offset1:36
	s_waitcnt lgkmcnt(1)
	v_mfma_f32_16x16x32_bf16 v[6:9], v[6:9], v[14:17], v[26:29]
	s_nop 2
	ds_read2_b64 v[26:29], v177 offset0:64 offset1:68
	s_waitcnt lgkmcnt(0)
	v_mfma_f32_16x16x32_bf16 v[26:29], v[26:29], v[14:17], v[38:41]
	s_nop 2
	v_add_f32_e32 v38, 0, v130
	v_add_f32_e32 v38, v95, v38
	v_add_f32_e32 v38, v94, v38
	v_add_f32_e32 v38, v98, v38
	v_add_f32_e32 v38, v91, v38
	v_add_f32_e32 v38, v90, v38
	v_add_f32_e32 v38, v93, v38
	v_add_f32_e32 v38, v92, v38
	v_add_f32_e32 v38, v85, v38
	v_add_f32_e32 v38, v89, v38
	v_add_f32_e32 v38, v97, v38
	v_add_f32_e32 v38, v99, v38
	v_add_f32_e32 v38, v76, v38
	v_add_f32_e32 v38, v86, v38
	v_add_f32_e32 v38, v96, v38
	v_add_f32_e32 v38, v100, v38
	v_add_f32_e32 v38, v102, v38
	v_add_f32_e32 v38, v104, v38
	v_add_f32_e32 v38, v106, v38
	v_add_f32_e32 v38, v107, v38
	v_add_f32_e32 v38, v101, v38
	v_add_f32_e32 v38, v103, v38
	v_add_f32_e32 v38, v105, v38
	v_add_f32_e32 v38, v108, v38
	v_add_f32_e32 v38, v110, v38
	v_add_f32_e32 v38, v112, v38
	v_add_f32_e32 v38, v114, v38
	v_add_f32_e32 v38, v115, v38
	v_add_f32_e32 v38, v109, v38
	v_add_f32_e32 v38, v111, v38
	v_add_f32_e32 v38, v113, v38
	v_add_f32_e32 v38, v116, v38
	v_add_f32_e32 v38, v118, v38
	v_add_f32_e32 v38, v120, v38
	v_add_f32_e32 v38, v122, v38
	v_add_f32_e32 v38, v123, v38
	v_add_f32_e32 v38, v117, v38
	v_add_f32_e32 v38, v119, v38
	v_add_f32_e32 v38, v121, v38
	v_add_f32_e32 v38, v124, v38
	v_add_f32_e32 v38, v126, v38
	v_add_f32_e32 v38, v128, v38
	v_add_f32_e32 v38, v131, v38
	v_add_f32_e32 v38, v132, v38
	v_add_f32_e32 v38, v125, v38
	v_add_f32_e32 v38, v127, v38
	v_add_f32_e32 v38, v129, v38
	v_add_f32_e32 v38, v133, v38
	v_add_f32_e32 v38, v136, v38
	v_add_f32_e32 v38, v138, v38
	v_add_f32_e32 v38, v140, v38
	v_add_f32_e32 v38, v141, v38
	v_add_f32_e32 v38, v134, v38
	v_add_f32_e32 v38, v137, v38
	v_add_f32_e32 v38, v139, v38
	v_add_f32_e32 v38, v142, v38
	v_add_f32_e32 v38, v78, v38
	v_add_f32_e32 v38, v80, v38
	v_add_f32_e32 v38, v143, v38
	v_add_f32_e32 v38, v145, v38
	v_add_f32_e32 v38, v70, v38
	v_add_f32_e32 v38, v79, v38
	v_add_f32_e32 v38, v81, v38
	v_add_f32_e32 v38, v144, v38
	v_add_f32_e32 v38, v146, v38
	v_add_f32_e32 v38, v66, v38
	v_add_f32_e32 v38, v67, v38
	v_add_f32_e32 v38, v68, v38
	v_add_f32_e32 v38, v62, v38
	v_add_f32_e32 v38, v63, v38
	v_add_f32_e32 v38, v64, v38
	v_add_f32_e32 v38, v65, v38
	v_add_f32_e32 v38, v58, v38
	v_add_f32_e32 v38, v59, v38
	v_add_f32_e32 v38, v60, v38
	v_add_f32_e32 v38, v61, v38
	v_add_f32_e32 v38, v54, v38
	v_add_f32_e32 v38, v55, v38
	v_add_f32_e32 v38, v56, v38
	v_add_f32_e32 v38, v57, v38
	v_add_f32_e32 v38, v69, v38
	v_add_f32_e32 v38, v50, v38
	v_add_f32_e32 v38, v51, v38
	v_add_f32_e32 v38, v154, v38
	v_add_f32_e32 v38, v46, v38
	v_add_f32_e32 v38, v47, v38
	v_add_f32_e32 v38, v48, v38
	v_add_f32_e32 v38, v53, v38
	v_add_f32_e32 v38, v172, v38
	v_mfma_f32_16x16x32_bf16 v[18:21], v[18:21], v[14:17], v[30:33]
	v_add_f32_e32 v38, v174, v38
	v_add_f32_e32 v38, v178, v38
	v_add_f32_e32 v38, v180, v38
	ds_read2_b64 v[30:33], v49 offset0:96 offset1:100
	v_add_f32_e32 v38, v173, v38
	v_add_f32_e32 v38, v175, v38
	v_add_f32_e32 v38, v179, v38
	v_add_f32_e32 v38, v181, v38
	v_add_f32_e32 v38, v164, v38
	v_add_f32_e32 v38, v166, v38
	s_waitcnt lgkmcnt(0)
	v_mfma_f32_16x16x32_bf16 v[14:17], v[30:33], v[14:17], v[22:25]
	v_add_f32_e32 v38, v182, v38
	s_nop 1
	v_exp_f32_e32 v23, v2
	v_fma_f32 v2, v11, s71, -v135
	v_mul_f32_e32 v2, 0x3fb8aa3b, v2
	v_add_f32_e32 v38, v184, v38
	v_exp_f32_e32 v24, v2
	v_fma_f32 v2, v3, s71, -v135
	v_add_f32_e32 v38, v165, v38
	v_mul_f32_e32 v2, 0x3fb8aa3b, v2
	v_add_f32_e32 v38, v167, v38
	v_exp_f32_e32 v25, v2
	v_fma_f32 v2, v12, s71, -v135
	v_add_f32_e32 v38, v183, v38
	v_mul_f32_e32 v2, 0x3fb8aa3b, v2
	v_add_f32_e32 v38, v185, v38
	v_exp_f32_e32 v30, v2
	v_fma_f32 v2, v4, s71, -v135
	v_add_f32_e32 v38, v156, v38
	v_mul_f32_e32 v2, 0x3fb8aa3b, v2
	v_add_f32_e32 v38, v158, v38
	v_exp_f32_e32 v22, v10
	v_exp_f32_e32 v31, v2
	v_fma_f32 v2, v13, s71, -v135
	ds_read2_b64 v[10:13], v52 offset0:8 offset1:12
	v_add_f32_e32 v38, v160, v38
	v_mul_f32_e32 v2, 0x3fb8aa3b, v2
	v_add_f32_e32 v38, v155, v38
	v_exp_f32_e32 v32, v2
	v_fma_f32 v2, v5, s71, -v135
	v_add_f32_e32 v38, v157, v38
	v_mul_f32_e32 v2, 0x3fb8aa3b, v2
	v_add_f32_e32 v38, v159, v38
	v_exp_f32_e32 v33, v2
	v_add_f32_e32 v38, v161, v38
	v_add_f32_e32 v38, v162, v38
	v_add_f32_e32 v34, v34, v38
	v_add_f32_e32 v34, v36, v34
	v_cvt_pk_bf16_f32 v2, v22, v24
	v_cvt_pk_bf16_f32 v3, v30, v32
	v_cvt_pk_bf16_f32 v4, v23, v25
	v_cvt_pk_bf16_f32 v5, v31, v33
	v_add_f32_e32 v34, v42, v34
	v_add_f32_e32 v34, v44, v34
	s_waitcnt lgkmcnt(0)
	v_mfma_f32_16x16x32_bf16 v[6:9], v[10:13], v[2:5], v[6:9]
	ds_read2_b64 v[10:13], v176 offset0:40 offset1:44
	v_add_f32_e32 v34, v35, v34
	v_add_f32_e32 v34, v37, v34
	v_add_f32_e32 v34, v43, v34
	v_add_f32_e32 v34, v45, v34
	v_add_f32_e32 v22, v22, v34
	v_add_f32_e32 v22, v24, v22
	v_add_f32_e32 v22, v30, v22
	v_add_f32_e32 v22, v32, v22
	s_waitcnt lgkmcnt(0)
	v_mfma_f32_16x16x32_bf16 v[10:13], v[10:13], v[2:5], v[18:21]
	v_add_f32_e32 v22, v23, v22
	v_add_f32_e32 v22, v25, v22
	v_add_f32_e32 v22, v31, v22
	ds_read2_b64 v[18:21], v177 offset0:72 offset1:76
	v_add_f32_e32 v30, v33, v22
	ds_bpermute_b32 v31, v87, v30
	ds_read2_b64 v[22:25], v49 offset0:104 offset1:108
	s_waitcnt lgkmcnt(2)
	v_mfma_f32_16x16x32_bf16 v[18:21], v[18:21], v[2:5], v[26:29]
	s_waitcnt lgkmcnt(1)
	s_nop 1
	v_add_f32_e32 v26, v30, v31
	ds_bpermute_b32 v27, v88, v26
	v_lshlrev_b32_e32 v70, 1, v77
	s_waitcnt lgkmcnt(1)
	v_mfma_f32_16x16x32_bf16 v[14:17], v[22:25], v[2:5], v[14:17]
	s_waitcnt lgkmcnt(0)
	s_barrier
; __device__ __forceinline__ unsigned cvt_pk_bf16(float lo, float hi) { const float __attribute__((ext_vector_type(2))) v = {lo, hi}; return __builtin_bit_cast(unsigned, __builtin_convertvector(v, bf16x2_t)); }
; template <bool LOCAL>
; __device__ __forceinline__ void na_unit(const bf16* P, const bf16* VT, bf16* YCAT, const LAS float* rpb_l, LAS bf16* buf, int b, int gr, int hp, int qblk, int tid) {
;     ...
;     lsum += __shfl_xor(lsum, 16); lsum += __shfl_xor(lsum, 32);
;     const float inv = 1.f / lsum;
;     bf16* op = YCAT + (size_t)(qrow0 + fr) * D + 512 + h * 64 + 4 * fq;
; #pragma unroll
;     for (int dt = 0; dt < 4; ++dt) { v2u w; w.x = pg8::cvt_pk_bf16(o[dt][0] * inv, o[dt][1] * inv); w.y = pg8::cvt_pk_bf16(o[dt][2] * inv, o[dt][3] * inv); *(v2u*)(op + dt * 16) = w; }
	v_add_f32_e32 v2, v26, v27
	v_div_scale_f32 v3, s[0:1], v2, v2, 1.0
	v_rcp_f32_e32 v4, v3
	s_nop 0
	v_fma_f32 v5, -v3, v4, 1.0
	v_fmac_f32_e32 v4, v5, v4
	v_div_scale_f32 v5, vcc, 1.0, v2, 1.0
	v_mul_f32_e32 v22, v5, v4
	v_fma_f32 v23, -v3, v22, v5
	v_fmac_f32_e32 v22, v23, v4
	v_fma_f32 v3, -v3, v22, v5
	v_div_fmas_f32 v3, v3, v4, v22
	v_div_fixup_f32 v22, v3, v2, 1.0
	v_lshlrev_b64 v[2:3], 11, v[74:75]
	v_lshl_add_u64 v[2:3], s[10:11], 0, v[2:3]
	v_lshl_add_u64 v[2:3], v[72:73], 1, v[2:3]
	v_pk_mul_f32 v[6:7], v[6:7], v[22:23] op_sel_hi:[1,0]
	v_pk_mul_f32 v[8:9], v[8:9], v[22:23] op_sel_hi:[1,0]
	v_lshl_add_u64 v[4:5], v[2:3], 0, v[70:71]
	v_cvt_pk_bf16_f32 v6, v6, v7
	v_cvt_pk_bf16_f32 v7, v8, v9
	global_store_dwordx2 v[4:5], v[6:7], off offset:1024
	v_pk_mul_f32 v[6:7], v[10:11], v[22:23] op_sel_hi:[1,0]
	v_pk_mul_f32 v[8:9], v[12:13], v[22:23] op_sel_hi:[1,0]
	v_cvt_pk_bf16_f32 v6, v6, v7
	v_cvt_pk_bf16_f32 v7, v8, v9
	global_store_dwordx2 v[4:5], v[6:7], off offset:1056
	v_pk_mul_f32 v[6:7], v[18:19], v[22:23] op_sel_hi:[1,0]
	v_pk_mul_f32 v[8:9], v[20:21], v[22:23] op_sel_hi:[1,0]
	v_cvt_pk_bf16_f32 v6, v6, v7
	v_cvt_pk_bf16_f32 v7, v8, v9
	v_lshl_add_u64 v[2:3], v[4:5], 0, s[12:13]
	global_store_dwordx2 v[4:5], v[6:7], off offset:1088
	v_pk_mul_f32 v[4:5], v[14:15], v[22:23] op_sel_hi:[1,0]
	v_pk_mul_f32 v[6:7], v[16:17], v[22:23] op_sel_hi:[1,0]
	v_cvt_pk_bf16_f32 v4, v4, v5

; #define LAS __attribute__((address_space(3)))
; template <bool LOCAL>
; __device__ __forceinline__ void na_unit(const bf16* P, const bf16* VT, bf16* YCAT, const LAS float* rpb_l, LAS bf16* buf, int b, int gr, int hp, int qblk, int tid) {
;     typedef pg8::bf16x8 bf16x8;
;     constexpr int NCH = LOCAL ? 12 : 4, NLOC = LOCAL ? 8 : 0;
;     const int lane = tid & 63, wv = tid >> 6, fr = lane & 15, fq = lane >> 4, hh = wv >> 2, qb = wv & 3, h = 2 * hp + hh;
;     const int qrow0 = LOCAL ? NCTX + b * SEQ + gr * 64 + 16 * qb : b * CTXL + qblk * 64 + 16 * qb;
;     const int r0 = min(max(gr - 4, 0), 24);
;     const int kc0 = qb == 0 ? 0 : qb == 1 ? 8 : qb == 2 ? 24 : 32;
;     const int qcol = 16 * qb + fr, cs = min(max(qcol - 8, 0), 48);
;     const LAS float* rpb = rpb_l + h * 15 * 31;
;     v4u ld[2][2];
;     const int lrow = (tid >> 3) & 63, lseg = tid & 7;
;     ...
;     bf16x8 qf[2];
; #pragma unroll
;     for (int ks = 0; ks < 2; ++ks) qf[ks] = *(const bf16x8*)(P + (size_t)(qrow0 + fr) * DINP + h * 64 + 32 * ks + 8 * fq);
;     f32x4 sl[16], sc[16];
;     float m = -1.0e30f, lsum = 0.f;
;     f32x4 o[4];
; #pragma unroll
;     for (int dt = 0; dt < 4; ++dt) o[dt] = (f32x4){0.f, 0.f, 0.f, 0.f};
;     NA_ISSUE(0); NA_ISSUE(1); NA_STORE(0);
;     __syncthreads();
; #pragma unroll
;     for (int sidx = 0; sidx < 2 * NCH; ++sidx) {
;         if (sidx + 2 < 2 * NCH) NA_ISSUE(sidx + 2);
;         const LAS bf16* cb = buf + (sidx & 1) * 9216 + hh * 4608;
;         if (sidx < NCH) {
;             const int c = sidx;
;             if (LOCAL && c < 8) {
; #pragma unroll
;                 for (int t2 = 0; t2 < 2; ++t2) {
;                     const LAS bf16* kp = cb + (kc0 + 16 * t2 + fr) * 72 + 8 * fq;
;                     f32x4 acc = {0.f, 0.f, 0.f, 0.f};
;                     acc = __builtin_amdgcn_mfma_f32_16x16x32_bf16(*(const LAS bf16x8*)(kp), qf[0], acc, 0, 0, 0);
;                     acc = __builtin_amdgcn_mfma_f32_16x16x32_bf16(*(const LAS bf16x8*)(kp + 32), qf[1], acc, 0, 0, 0);
;                     const LAS float* rb = rpb + (r0 + c - gr + 7) * 31 + 15 - qcol;
; #pragma unroll
;                     for (int e = 0; e < 4; ++e) { const int kcol = kc0 + 16 * t2 + 4 * fq + e; const bool ok = (kcol >= cs) && (kcol < cs + 16);
;                         const float sv = ok ? acc[e] * 0.125f + rb[ok ? kcol : qcol] : -1.0e30f; acc[e] = sv; m = fmaxf(m, sv); }
.LBB0_2659:
	s_or_b64 exec, exec, s[0:1]
	s_bfe_u32 s19, s80, 0x50002
	v_sub_u32_e64 v3, s19, 4 clamp
	s_ashr_i32 s17, s80, 7
	v_readfirstlane_b32 s0, v3
	s_lshl_b32 s26, s17, 11
	s_min_u32 s20, s0, 24
	s_add_i32 s14, s26, 0x1000
	s_lshl_b32 s15, s20, 6
	s_or_b32 s16, s15, s14
	v_mov_b64_e32 v[18:19], s[8:9]
	v_and_b32_e32 v32, 7, v94
	v_or_b32_e32 v3, s16, v89
	s_and_b32 s18, s80, 3
	v_mad_i64_i32 v[4:5], s[0:1], v3, s72, v[18:19]
	v_lshlrev_b32_e32 v26, 4, v32
	v_mov_b32_e32 v27, v71
	v_lshl_add_u64 v[4:5], v[4:5], 0, v[26:27]
	s_lshl_b32 s2, s18, 8
	v_lshl_add_u64 v[4:5], v[4:5], 0, s[2:3]
	global_load_dwordx4 v[10:13], v[4:5], off offset:1024
	global_load_dwordx4 v[14:17], v[4:5], off offset:1152
	s_lshl_b32 s0, s19, 6
	v_lshl_or_b32 v31, v2, 4, v90
	v_lshl_add_u32 v33, s18, 1, v93
	s_or_b32 s0, s14, s0
	v_mad_u32_u24 v2, v89, s73, 0
	v_lshlrev_b32_e32 v72, 6, v33
	s_add_i32 s50, s26, 0x1040
	v_or_b32_e32 v74, s0, v31
	v_add_u32_e32 v75, v2, v26
	v_ashrrev_i32_e32 v73, 31, v72
	v_or_b32_e32 v4, s50, v89
	v_mad_i64_i32 v[2:3], s[0:1], v74, s72, v[18:19]
	v_add_u32_e32 v4, s15, v4
	v_lshl_add_u64 v[2:3], v[72:73], 1, v[2:3]
	v_mad_i64_i32 v[4:5], s[0:1], v4, s72, v[18:19]
	v_lshl_add_u64 v[2:3], v[2:3], 0, v[70:71]
	v_lshl_add_u64 v[20:21], v[4:5], 0, v[26:27]
	global_load_dwordx4 v[6:9], v[2:3], off
	s_nop 0
	global_load_dwordx4 v[2:5], v[2:3], off offset:64
	s_or_b32 s14, s26, s15
	s_addk_i32 s14, 0x1080
	v_or_b32_e32 v24, s14, v89
	v_mad_i64_i32 v[28:29], s[0:1], v24, s72, v[18:19]
	v_lshl_add_u64 v[26:27], v[28:29], 0, v[26:27]
	v_lshl_add_u64 v[22:23], v[20:21], 0, s[2:3]
	v_lshl_add_u64 v[26:27], v[26:27], 0, s[2:3]
	global_load_dwordx4 v[18:21], v[22:23], off offset:1024
	s_nop 0
	global_load_dwordx4 v[22:25], v[22:23], off offset:1152
	v_add_u32_e32 v30, v87, v70
	v_add_u32_e32 v34, v91, v90
	v_mad_u32_u24 v36, v34, s73, v30
	s_movk_i32 s0, 0x744
	v_mul_lo_u32 v33, v33, s0
	s_sub_i32 s0, s20, s19
	s_mulk_i32 s0, 0x7c
	v_sub_u32_e64 v35, v31, 8 clamp
	s_add_i32 s0, s0, 0
	v_min_u32_e32 v35, 48, v35
	v_lshlrev_b32_e32 v77, 2, v92
	v_add_u32_e32 v33, s0, v33
	v_lshlrev_b32_e32 v31, 2, v31
	v_sub_u32_e32 v31, v33, v31
	v_add_u32_e32 v33, v91, v77
	v_cmp_ge_u32_e32 vcc, v33, v35
	v_mov_b32_e32 v92, 0xf149f2ca
	v_lshl_add_u32 v31, v33, 2, v31
	v_mov_b32_e32 v93, 0xf149f2ca
	s_waitcnt vmcnt(5)
	ds_write_b128 v75, v[10:13]
	s_waitcnt vmcnt(4)
	ds_write_b128 v75, v[14:17] offset:9216
	s_waitcnt lgkmcnt(0)
	s_barrier
	ds_read_b32 v240, v31 offset:37792
	ds_read_b32 v241, v31 offset:37796
	ds_read_b32 v242, v31 offset:37800
	ds_read_b32 v243, v31 offset:37804
	ds_read_b32 v244, v31 offset:37856
	ds_read_b32 v245, v31 offset:37860
	ds_read_b32 v246, v31 offset:37864
	ds_read_b32 v247, v31 offset:37868
	global_load_dwordx4 v[10:13], v[26:27], off offset:1024
	global_load_dwordx4 v[14:17], v[26:27], off offset:1152
	ds_read_b128 v[26:29], v36
	ds_read_b128 v[38:41], v36 offset:64
	s_waitcnt vmcnt(5) lgkmcnt(1)
	v_mfma_f32_16x16x32_bf16 v[26:29], v[26:29], v[6:9], 0
	v_add_u32_e32 v36, 16, v35
	v_cmp_lt_u32_e64 s[0:1], v33, v36
	s_and_b64 s[28:29], vcc, s[0:1]
	s_waitcnt vmcnt(4) lgkmcnt(0)
	v_mfma_f32_16x16x32_bf16 v[26:29], v[38:41], v[2:5], v[26:29]
	s_nop 2
	s_waitcnt lgkmcnt(0)
	s_nop 3
	v_fmac_f32_e32 v240, 0x3e000000, v26
	v_cndmask_b32_e64 v93, v93, v240, s[28:29]
	s_nop 4
	v_or_b32_e32 v26, 1, v33
	v_cmp_ge_u32_e32 vcc, v26, v35
	v_cmp_lt_u32_e64 s[0:1], v26, v36
	s_and_b64 s[30:31], vcc, s[0:1]
	s_nop 2
	s_waitcnt lgkmcnt(0)
	v_fmac_f32_e32 v241, 0x3e000000, v27
	v_cndmask_b32_e64 v92, v92, v241, s[30:31]
	v_or_b32_e32 v26, 2, v33
	v_cmp_ge_u32_e32 vcc, v26, v35
	v_cmp_lt_u32_e64 s[0:1], v26, v36
	s_and_b64 s[34:35], vcc, s[0:1]
	v_mov_b32_e32 v94, 0xf149f2ca
	v_mov_b32_e32 v95, 0xf149f2ca
	s_nop 2
	s_waitcnt lgkmcnt(0)
	v_fmac_f32_e32 v242, 0x3e000000, v28
	v_cndmask_b32_e64 v95, v95, v242, s[34:35]
	v_or_b32_e32 v26, 3, v33
	v_cmp_ge_u32_e32 vcc, v26, v35
	v_cmp_lt_u32_e64 s[0:1], v26, v36
	s_and_b64 s[36:37], vcc, s[0:1]
	s_nop 2
	s_waitcnt lgkmcnt(0)
	v_fmac_f32_e32 v243, 0x3e000000, v29
	v_cndmask_b32_e64 v94, v94, v243, s[36:37]
	v_add_u32_e32 v37, 16, v91
	v_add_u32_e32 v33, v37, v90
	v_mad_u32_u24 v38, v33, s73, v30
	ds_read_b128 v[26:29], v38
	ds_read_b128 v[38:41], v38 offset:64
	v_add_u32_e32 v37, v37, v77
	v_cmp_ge_u32_e32 vcc, v37, v35
	v_cmp_lt_u32_e64 s[0:1], v37, v36
	s_waitcnt lgkmcnt(1)
	v_mfma_f32_16x16x32_bf16 v[26:29], v[26:29], v[6:9], 0
	s_and_b64 s[38:39], vcc, s[0:1]
	v_mov_b32_e32 v96, 0xf149f2ca
	v_mov_b32_e32 v97, 0xf149f2ca
	s_waitcnt lgkmcnt(0)
	v_mfma_f32_16x16x32_bf16 v[26:29], v[38:41], v[2:5], v[26:29]
	s_nop 2
	s_waitcnt lgkmcnt(0)
	s_nop 3
	v_fmac_f32_e32 v244, 0x3e000000, v26
	v_cndmask_b32_e64 v97, v97, v244, s[38:39]
	s_nop 4
	v_or_b32_e32 v26, 1, v37
	v_cmp_ge_u32_e32 vcc, v26, v35
	v_cmp_lt_u32_e64 s[0:1], v26, v36
	s_and_b64 s[44:45], vcc, s[0:1]
	s_nop 2
	s_waitcnt lgkmcnt(0)
	v_fmac_f32_e32 v245, 0x3e000000, v27
	v_cndmask_b32_e64 v96, v96, v245, s[44:45]
	v_or_b32_e32 v26, 2, v37
	v_cmp_ge_u32_e32 vcc, v26, v35
	v_cmp_lt_u32_e64 s[0:1], v26, v36
	s_and_b64 s[46:47], vcc, s[0:1]
	v_mov_b32_e32 v98, 0xf149f2ca
	v_mov_b32_e32 v100, 0xf149f2ca
	s_nop 2
	s_waitcnt lgkmcnt(0)
	v_fmac_f32_e32 v246, 0x3e000000, v28
	v_cndmask_b32_e64 v100, v100, v246, s[46:47]
	v_or_b32_e32 v26, 3, v37
	v_cmp_ge_u32_e32 vcc, v26, v35
	v_cmp_lt_u32_e64 s[0:1], v26, v36
	s_and_b64 s[66:67], vcc, s[0:1]
	s_nop 2
	s_waitcnt lgkmcnt(0)
	v_fmac_f32_e32 v247, 0x3e000000, v29
	v_cndmask_b32_e64 v98, v98, v247, s[66:67]
	v_mul_u32_u24_e32 v27, 0x90, v34
	v_lshlrev_b32_e32 v26, 3, v32
	v_add_u32_e32 v32, v30, v27
	s_waitcnt vmcnt(3)
	ds_write_b128 v75, v[18:21] offset:18432
	s_waitcnt vmcnt(2)
	ds_write_b128 v75, v[22:25] offset:27648
	s_waitcnt lgkmcnt(0)
	s_barrier
; #define LAS __attribute__((address_space(3)))
; template <bool LOCAL>
; __device__ __forceinline__ void na_unit(const bf16* P, const bf16* VT, bf16* YCAT, const LAS float* rpb_l, LAS bf16* buf, int b, int gr, int hp, int qblk, int tid) {
;     ...
;         if (sidx < NCH) {
;             const int c = sidx;
;             if (LOCAL && c < 8) {
; #pragma unroll
;                 for (int t2 = 0; t2 < 2; ++t2) {
;                     const LAS bf16* kp = cb + (kc0 + 16 * t2 + fr) * 72 + 8 * fq;
;                     f32x4 acc = {0.f, 0.f, 0.f, 0.f};
;                     acc = __builtin_amdgcn_mfma_f32_16x16x32_bf16(*(const LAS bf16x8*)(kp), qf[0], acc, 0, 0, 0);
;                     acc = __builtin_amdgcn_mfma_f32_16x16x32_bf16(*(const LAS bf16x8*)(kp + 32), qf[1], acc, 0, 0, 0);
;                     const LAS float* rb = rpb + (r0 + c - gr + 7) * 31 + 15 - qcol;
; #pragma unroll
;                     for (int e = 0; e < 4; ++e) { const int kcol = kc0 + 16 * t2 + 4 * fq + e; const bool ok = (kcol >= cs) && (kcol < cs + 16);
;                         const float sv = ok ? acc[e] * 0.125f + rb[ok ? kcol : qcol] : -1.0e30f; acc[e] = sv; m = fmaxf(m, sv); }
;                     sl[2 * (c < 8 ? c : 0) + t2] = acc; }
	ds_read_b32 v240, v31 offset:37916
	ds_read_b32 v241, v31 offset:37920
	ds_read_b32 v242, v31 offset:37924
	ds_read_b32 v243, v31 offset:37928
	ds_read_b32 v244, v31 offset:37980
	ds_read_b32 v245, v31 offset:37984
	ds_read_b32 v246, v31 offset:37988
	ds_read_b32 v247, v31 offset:37992
	ds_read_b128 v[18:21], v32 offset:18432
	s_add_i32 s26, s26, s15
	s_add_i32 s0, s26, 0x10c0
	v_or_b32_e32 v24, s0, v89
	v_mov_b64_e32 v[22:23], s[8:9]
	s_lshl_b32 s1, s18, 7
	v_mad_i64_i32 v[22:23], s[18:19], v24, s72, v[22:23]
	v_lshlrev_b32_e32 v70, 1, v26
	v_lshl_add_u64 v[22:23], v[22:23], 0, v[70:71]
	s_lshl_b32 s2, s1, 1
	v_lshl_add_u64 v[22:23], v[22:23], 0, s[2:3]
	ds_read_b128 v[26:29], v32 offset:18496
	s_waitcnt lgkmcnt(1)
	v_mfma_f32_16x16x32_bf16 v[34:37], v[18:21], v[6:9], 0
	global_load_dwordx4 v[18:21], v[22:23], off offset:1024
	s_nop 0
	global_load_dwordx4 v[22:25], v[22:23], off offset:1152
	v_mov_b32_e32 v99, 0xf149f2ca
	v_mov_b32_e32 v101, 0xf149f2ca
	s_waitcnt lgkmcnt(0)
	v_mfma_f32_16x16x32_bf16 v[26:29], v[26:29], v[2:5], v[34:37]
	s_nop 2
	s_waitcnt lgkmcnt(0)
	s_nop 3
	v_fmac_f32_e32 v240, 0x3e000000, v26
	v_cndmask_b32_e64 v101, v101, v240, s[28:29]
	s_nop 2
	s_waitcnt lgkmcnt(0)
	s_nop 0
	v_fmac_f32_e32 v241, 0x3e000000, v27
	v_cndmask_b32_e64 v99, v99, v241, s[30:31]
	v_mov_b32_e32 v102, 0xf149f2ca
	v_mov_b32_e32 v103, 0xf149f2ca
	s_nop 2
	s_waitcnt lgkmcnt(0)
	v_fmac_f32_e32 v242, 0x3e000000, v28
	v_cndmask_b32_e64 v103, v103, v242, s[34:35]
	s_nop 2
	s_waitcnt lgkmcnt(0)
	v_fmac_f32_e32 v243, 0x3e000000, v29
	v_cndmask_b32_e64 v102, v102, v243, s[36:37]
	v_mul_u32_u24_e32 v26, 0x90, v33
	v_add_u32_e32 v33, v30, v26
	ds_read_b128 v[26:29], v33 offset:18432
	ds_read_b128 v[34:37], v33 offset:18496
	v_mov_b32_e32 v104, 0xf149f2ca
	v_mov_b32_e32 v106, 0xf149f2ca
	s_waitcnt lgkmcnt(1)
	v_mfma_f32_16x16x32_bf16 v[26:29], v[26:29], v[6:9], 0
	s_waitcnt lgkmcnt(0)
	v_mfma_f32_16x16x32_bf16 v[26:29], v[34:37], v[2:5], v[26:29]
	s_nop 2
	s_waitcnt lgkmcnt(0)
	s_nop 3
	v_fmac_f32_e32 v244, 0x3e000000, v26
	v_cndmask_b32_e64 v106, v106, v244, s[38:39]
	s_nop 2
	s_waitcnt lgkmcnt(0)
	s_nop 0
	v_fmac_f32_e32 v245, 0x3e000000, v27
	v_cndmask_b32_e64 v104, v104, v245, s[44:45]
	v_mov_b32_e32 v108, 0xf149f2ca
	v_mov_b32_e32 v110, 0xf149f2ca
	s_nop 2
	s_waitcnt lgkmcnt(0)
	v_fmac_f32_e32 v246, 0x3e000000, v28
	v_cndmask_b32_e64 v110, v110, v246, s[46:47]
	s_nop 2
	s_waitcnt lgkmcnt(0)
	v_fmac_f32_e32 v247, 0x3e000000, v29
	v_cndmask_b32_e64 v108, v108, v247, s[66:67]
	s_waitcnt vmcnt(3)
	ds_write_b128 v75, v[10:13]
	s_waitcnt vmcnt(2)
	ds_write_b128 v75, v[14:17] offset:9216
	s_waitcnt lgkmcnt(0)
	s_barrier
	ds_read_b32 v240, v31 offset:38040
	ds_read_b32 v241, v31 offset:38044
	ds_read_b32 v242, v31 offset:38048
	ds_read_b32 v243, v31 offset:38052
	ds_read_b32 v244, v31 offset:38104
	ds_read_b32 v245, v31 offset:38108
	ds_read_b32 v246, v31 offset:38112
	ds_read_b32 v247, v31 offset:38116
	ds_read_b128 v[10:13], v32
	ds_read_b128 v[26:29], v32 offset:64
	s_add_i32 s18, s26, 0x1100
	v_or_b32_e32 v16, s18, v89
	v_mov_b64_e32 v[14:15], s[8:9]
	v_mad_i64_i32 v[14:15], s[20:21], v16, s72, v[14:15]
	v_lshl_add_u64 v[14:15], v[14:15], 0, v[70:71]
	v_lshl_add_u64 v[14:15], v[14:15], 0, s[2:3]
	s_waitcnt lgkmcnt(1)
	v_mfma_f32_16x16x32_bf16 v[34:37], v[10:13], v[6:9], 0
	global_load_dwordx4 v[10:13], v[14:15], off offset:1024
	s_nop 0
	global_load_dwordx4 v[14:17], v[14:15], off offset:1152
	v_mov_b32_e32 v105, 0xf149f2ca
	v_mov_b32_e32 v107, 0xf149f2ca
	s_waitcnt lgkmcnt(0)
	v_mfma_f32_16x16x32_bf16 v[26:29], v[26:29], v[2:5], v[34:37]
	s_nop 2
	s_waitcnt lgkmcnt(0)
	s_nop 3
	v_fmac_f32_e32 v240, 0x3e000000, v26
	v_cndmask_b32_e64 v107, v107, v240, s[28:29]
	s_nop 2
	s_waitcnt lgkmcnt(0)
	s_nop 0
	v_fmac_f32_e32 v241, 0x3e000000, v27
	v_cndmask_b32_e64 v105, v105, v241, s[30:31]
	v_mov_b32_e32 v109, 0xf149f2ca
	v_mov_b32_e32 v111, 0xf149f2ca
	s_nop 2
	s_waitcnt lgkmcnt(0)
	v_fmac_f32_e32 v242, 0x3e000000, v28
	v_cndmask_b32_e64 v111, v111, v242, s[34:35]
	s_nop 2
	s_waitcnt lgkmcnt(0)
	v_fmac_f32_e32 v243, 0x3e000000, v29
	v_cndmask_b32_e64 v109, v109, v243, s[36:37]
	ds_read_b128 v[26:29], v33
	ds_read_b128 v[34:37], v33 offset:64
	v_mov_b32_e32 v112, 0xf149f2ca
	v_mov_b32_e32 v114, 0xf149f2ca
	s_waitcnt lgkmcnt(1)
	v_mfma_f32_16x16x32_bf16 v[26:29], v[26:29], v[6:9], 0
	s_waitcnt lgkmcnt(0)
	v_mfma_f32_16x16x32_bf16 v[26:29], v[34:37], v[2:5], v[26:29]
	s_nop 2
	s_waitcnt lgkmcnt(0)
	s_nop 3
	v_fmac_f32_e32 v244, 0x3e000000, v26
	v_cndmask_b32_e64 v114, v114, v244, s[38:39]
	s_nop 2
	s_waitcnt lgkmcnt(0)
	s_nop 0
	v_fmac_f32_e32 v245, 0x3e000000, v27
	v_cndmask_b32_e64 v112, v112, v245, s[44:45]
	v_mov_b32_e32 v113, 0xf149f2ca
	v_mov_b32_e32 v117, 0xf149f2ca
	s_nop 2
	s_waitcnt lgkmcnt(0)
	v_fmac_f32_e32 v246, 0x3e000000, v28
	v_cndmask_b32_e64 v117, v117, v246, s[46:47]
	s_nop 2
	s_waitcnt lgkmcnt(0)
	v_fmac_f32_e32 v247, 0x3e000000, v29
	v_cndmask_b32_e64 v113, v113, v247, s[66:67]
	s_waitcnt vmcnt(3)
	ds_write_b128 v75, v[18:21] offset:18432
	s_waitcnt vmcnt(2)
	ds_write_b128 v75, v[22:25] offset:27648
	s_waitcnt lgkmcnt(0)
	s_barrier
; #define LAS __attribute__((address_space(3)))
; template <bool LOCAL>
; __device__ __forceinline__ void na_unit(const bf16* P, const bf16* VT, bf16* YCAT, const LAS float* rpb_l, LAS bf16* buf, int b, int gr, int hp, int qblk, int tid) {
;     ...
;         if (sidx < NCH) {
;             const int c = sidx;
;             if (LOCAL && c < 8) {
; #pragma unroll
;                 for (int t2 = 0; t2 < 2; ++t2) {
;                     const LAS bf16* kp = cb + (kc0 + 16 * t2 + fr) * 72 + 8 * fq;
;                     f32x4 acc = {0.f, 0.f, 0.f, 0.f};
;                     acc = __builtin_amdgcn_mfma_f32_16x16x32_bf16(*(const LAS bf16x8*)(kp), qf[0], acc, 0, 0, 0);
;                     acc = __builtin_amdgcn_mfma_f32_16x16x32_bf16(*(const LAS bf16x8*)(kp + 32), qf[1], acc, 0, 0, 0);
;                     const LAS float* rb = rpb + (r0 + c - gr + 7) * 31 + 15 - qcol;
; #pragma unroll
;                     for (int e = 0; e < 4; ++e) { const int kcol = kc0 + 16 * t2 + 4 * fq + e; const bool ok = (kcol >= cs) && (kcol < cs + 16);
;                         const float sv = ok ? acc[e] * 0.125f + rb[ok ? kcol : qcol] : -1.0e30f; acc[e] = sv; m = fmaxf(m, sv); }
;                     sl[2 * (c < 8 ? c : 0) + t2] = acc; }
	ds_read_b32 v240, v31 offset:38164
	ds_read_b32 v241, v31 offset:38168
	ds_read_b32 v242, v31 offset:38172
	ds_read_b32 v243, v31 offset:38176
	ds_read_b32 v244, v31 offset:38228
	ds_read_b32 v245, v31 offset:38232
	ds_read_b32 v246, v31 offset:38236
	ds_read_b32 v247, v31 offset:38240
	ds_read_b128 v[18:21], v32 offset:18432
	ds_read_b128 v[26:29], v32 offset:18496
	s_add_i32 s20, s26, 0x1140
	v_or_b32_e32 v24, s20, v89
	v_mov_b64_e32 v[22:23], s[8:9]
	v_mad_i64_i32 v[22:23], s[22:23], v24, s72, v[22:23]
	v_lshl_add_u64 v[22:23], v[22:23], 0, v[70:71]
	v_lshl_add_u64 v[22:23], v[22:23], 0, s[2:3]
	s_waitcnt lgkmcnt(1)
	v_mfma_f32_16x16x32_bf16 v[34:37], v[18:21], v[6:9], 0
	global_load_dwordx4 v[18:21], v[22:23], off offset:1024
	s_nop 0
	global_load_dwordx4 v[22:25], v[22:23], off offset:1152
	v_mov_b32_e32 v115, 0xf149f2ca
	v_mov_b32_e32 v116, 0xf149f2ca
	s_waitcnt lgkmcnt(0)
	v_mfma_f32_16x16x32_bf16 v[26:29], v[26:29], v[2:5], v[34:37]
	s_nop 2
	s_waitcnt lgkmcnt(0)
	s_nop 3
	v_fmac_f32_e32 v240, 0x3e000000, v26
	v_cndmask_b32_e64 v116, v116, v240, s[28:29]
	s_nop 2
	s_waitcnt lgkmcnt(0)
	s_nop 0
	v_fmac_f32_e32 v241, 0x3e000000, v27
	v_cndmask_b32_e64 v115, v115, v241, s[30:31]
	v_mov_b32_e32 v118, 0xf149f2ca
	v_mov_b32_e32 v119, 0xf149f2ca
	s_nop 2
	s_waitcnt lgkmcnt(0)
	v_fmac_f32_e32 v242, 0x3e000000, v28
	v_cndmask_b32_e64 v119, v119, v242, s[34:35]
	s_nop 2
	s_waitcnt lgkmcnt(0)
	v_fmac_f32_e32 v243, 0x3e000000, v29
	v_cndmask_b32_e64 v118, v118, v243, s[36:37]
	ds_read_b128 v[26:29], v33 offset:18432
	ds_read_b128 v[34:37], v33 offset:18496
	v_mov_b32_e32 v120, 0xf149f2ca
	v_mov_b32_e32 v122, 0xf149f2ca
	s_waitcnt lgkmcnt(1)
	v_mfma_f32_16x16x32_bf16 v[26:29], v[26:29], v[6:9], 0
	s_waitcnt lgkmcnt(0)
	v_mfma_f32_16x16x32_bf16 v[26:29], v[34:37], v[2:5], v[26:29]
	s_nop 2
	s_waitcnt lgkmcnt(0)
	s_nop 3
	v_fmac_f32_e32 v244, 0x3e000000, v26
	v_cndmask_b32_e64 v122, v122, v244, s[38:39]
	s_nop 2
	s_waitcnt lgkmcnt(0)
	s_nop 0
	v_fmac_f32_e32 v245, 0x3e000000, v27
	v_cndmask_b32_e64 v120, v120, v245, s[44:45]
	v_mov_b32_e32 v121, 0xf149f2ca
	v_mov_b32_e32 v125, 0xf149f2ca
	s_nop 2
	s_waitcnt lgkmcnt(0)
	v_fmac_f32_e32 v246, 0x3e000000, v28
	v_cndmask_b32_e64 v125, v125, v246, s[46:47]
	s_nop 2
	s_waitcnt lgkmcnt(0)
	v_fmac_f32_e32 v247, 0x3e000000, v29
	v_cndmask_b32_e64 v121, v121, v247, s[66:67]
	s_waitcnt vmcnt(3)
	ds_write_b128 v75, v[10:13]
	s_waitcnt vmcnt(2)
	ds_write_b128 v75, v[14:17] offset:9216
	s_waitcnt lgkmcnt(0)
	s_barrier
	ds_read_b32 v240, v31 offset:38288
	ds_read_b32 v241, v31 offset:38292
	ds_read_b32 v242, v31 offset:38296
	ds_read_b32 v243, v31 offset:38300
	ds_read_b32 v244, v31 offset:38352
	ds_read_b32 v245, v31 offset:38356
	ds_read_b32 v246, v31 offset:38360
	ds_read_b32 v247, v31 offset:38364
	ds_read_b128 v[10:13], v32
	ds_read_b128 v[26:29], v32 offset:64
	s_add_i32 s22, s26, 0x1180
	v_or_b32_e32 v16, s22, v89
	v_mov_b64_e32 v[14:15], s[8:9]
	v_mad_i64_i32 v[14:15], s[24:25], v16, s72, v[14:15]
	v_lshl_add_u64 v[14:15], v[14:15], 0, v[70:71]
	v_lshl_add_u64 v[14:15], v[14:15], 0, s[2:3]
	s_waitcnt lgkmcnt(1)
	v_mfma_f32_16x16x32_bf16 v[34:37], v[10:13], v[6:9], 0
	global_load_dwordx4 v[10:13], v[14:15], off offset:1024
	s_nop 0
	global_load_dwordx4 v[14:17], v[14:15], off offset:1152
	v_mov_b32_e32 v123, 0xf149f2ca
	v_mov_b32_e32 v124, 0xf149f2ca
	s_waitcnt lgkmcnt(0)
	v_mfma_f32_16x16x32_bf16 v[26:29], v[26:29], v[2:5], v[34:37]
	s_nop 2
	s_waitcnt lgkmcnt(0)
	s_nop 3
	v_fmac_f32_e32 v240, 0x3e000000, v26
	v_cndmask_b32_e64 v124, v124, v240, s[28:29]
	s_nop 2
	s_waitcnt lgkmcnt(0)
	s_nop 0
	v_fmac_f32_e32 v241, 0x3e000000, v27
	v_cndmask_b32_e64 v123, v123, v241, s[30:31]
	v_mov_b32_e32 v126, 0xf149f2ca
	v_mov_b32_e32 v127, 0xf149f2ca
	s_nop 2
	s_waitcnt lgkmcnt(0)
	v_fmac_f32_e32 v242, 0x3e000000, v28
	v_cndmask_b32_e64 v127, v127, v242, s[34:35]
	s_nop 2
	s_waitcnt lgkmcnt(0)
	v_fmac_f32_e32 v243, 0x3e000000, v29
	v_cndmask_b32_e64 v126, v126, v243, s[36:37]
	ds_read_b128 v[26:29], v33
	ds_read_b128 v[34:37], v33 offset:64
	v_mov_b32_e32 v128, 0xf149f2ca
	v_mov_b32_e32 v130, 0xf149f2ca
	s_waitcnt lgkmcnt(1)
	v_mfma_f32_16x16x32_bf16 v[26:29], v[26:29], v[6:9], 0
	s_waitcnt lgkmcnt(0)
	v_mfma_f32_16x16x32_bf16 v[26:29], v[34:37], v[2:5], v[26:29]
	s_nop 2
	s_waitcnt lgkmcnt(0)
	s_nop 3
	v_fmac_f32_e32 v244, 0x3e000000, v26
	v_cndmask_b32_e64 v130, v130, v244, s[38:39]
	s_nop 2
	s_waitcnt lgkmcnt(0)
	s_nop 0
	v_fmac_f32_e32 v245, 0x3e000000, v27
	v_cndmask_b32_e64 v128, v128, v245, s[44:45]
	v_mov_b32_e32 v129, 0xf149f2ca
	v_mov_b32_e32 v134, 0xf149f2ca
	s_nop 2
	s_waitcnt lgkmcnt(0)
	v_fmac_f32_e32 v246, 0x3e000000, v28
	v_cndmask_b32_e64 v134, v134, v246, s[46:47]
	s_nop 2
	s_waitcnt lgkmcnt(0)
	v_fmac_f32_e32 v247, 0x3e000000, v29
	v_cndmask_b32_e64 v129, v129, v247, s[66:67]
	s_waitcnt vmcnt(3)
	ds_write_b128 v75, v[18:21] offset:18432
	s_waitcnt vmcnt(2)
	ds_write_b128 v75, v[22:25] offset:27648
	s_waitcnt lgkmcnt(0)
	s_barrier
; #define LAS __attribute__((address_space(3)))
; template <bool LOCAL>
; __device__ __forceinline__ void na_unit(const bf16* P, const bf16* VT, bf16* YCAT, const LAS float* rpb_l, LAS bf16* buf, int b, int gr, int hp, int qblk, int tid) {
;     ...
;         if (sidx < NCH) {
;             const int c = sidx;
;             if (LOCAL && c < 8) {
; #pragma unroll
;                 for (int t2 = 0; t2 < 2; ++t2) {
;                     const LAS bf16* kp = cb + (kc0 + 16 * t2 + fr) * 72 + 8 * fq;
;                     f32x4 acc = {0.f, 0.f, 0.f, 0.f};
;                     acc = __builtin_amdgcn_mfma_f32_16x16x32_bf16(*(const LAS bf16x8*)(kp), qf[0], acc, 0, 0, 0);
;                     acc = __builtin_amdgcn_mfma_f32_16x16x32_bf16(*(const LAS bf16x8*)(kp + 32), qf[1], acc, 0, 0, 0);
;                     const LAS float* rb = rpb + (r0 + c - gr + 7) * 31 + 15 - qcol;
; #pragma unroll
;                     for (int e = 0; e < 4; ++e) { const int kcol = kc0 + 16 * t2 + 4 * fq + e; const bool ok = (kcol >= cs) && (kcol < cs + 16);
;                         const float sv = ok ? acc[e] * 0.125f + rb[ok ? kcol : qcol] : -1.0e30f; acc[e] = sv; m = fmaxf(m, sv); }
;                     sl[2 * (c < 8 ? c : 0) + t2] = acc; }
	ds_read_b32 v240, v31 offset:38412
	ds_read_b32 v241, v31 offset:38416
	ds_read_b32 v242, v31 offset:38420
	ds_read_b32 v243, v31 offset:38424
	ds_read_b32 v244, v31 offset:38476
	ds_read_b32 v245, v31 offset:38480
	ds_read_b32 v246, v31 offset:38484
	ds_read_b32 v247, v31 offset:38488
	ds_read_b128 v[18:21], v32 offset:18432
	ds_read_b128 v[26:29], v32 offset:18496
	s_add_i32 s24, s26, 0x11c0
	v_or_b32_e32 v24, s24, v89
	v_mov_b64_e32 v[22:23], s[8:9]
	v_mad_i64_i32 v[22:23], s[26:27], v24, s72, v[22:23]
	v_lshl_add_u64 v[22:23], v[22:23], 0, v[70:71]
	v_lshl_add_u64 v[22:23], v[22:23], 0, s[2:3]
	s_waitcnt lgkmcnt(1)
	v_mfma_f32_16x16x32_bf16 v[34:37], v[18:21], v[6:9], 0
	global_load_dwordx4 v[18:21], v[22:23], off offset:1024
	s_nop 0
	global_load_dwordx4 v[22:25], v[22:23], off offset:1152
	v_mov_b32_e32 v131, 0xf149f2ca
	v_mov_b32_e32 v132, 0xf149f2ca
	s_waitcnt lgkmcnt(0)
	v_mfma_f32_16x16x32_bf16 v[26:29], v[26:29], v[2:5], v[34:37]
	s_nop 2
	s_waitcnt lgkmcnt(0)
	s_nop 3
	v_fmac_f32_e32 v240, 0x3e000000, v26
	v_cndmask_b32_e64 v132, v132, v240, s[28:29]
	s_nop 2
	s_waitcnt lgkmcnt(0)
	s_nop 0
	v_fmac_f32_e32 v241, 0x3e000000, v27
	v_cndmask_b32_e64 v131, v131, v241, s[30:31]
	v_mov_b32_e32 v135, 0xf149f2ca
	v_mov_b32_e32 v136, 0xf149f2ca
	s_nop 2
	s_waitcnt lgkmcnt(0)
	v_fmac_f32_e32 v242, 0x3e000000, v28
	v_cndmask_b32_e64 v136, v136, v242, s[34:35]
	s_nop 2
	s_waitcnt lgkmcnt(0)
	v_fmac_f32_e32 v243, 0x3e000000, v29
	v_cndmask_b32_e64 v135, v135, v243, s[36:37]
	ds_read_b128 v[26:29], v33 offset:18432
	ds_read_b128 v[34:37], v33 offset:18496
	v_mov_b32_e32 v138, 0xf149f2ca
	v_mov_b32_e32 v140, 0xf149f2ca
	s_waitcnt lgkmcnt(1)
	v_mfma_f32_16x16x32_bf16 v[26:29], v[26:29], v[6:9], 0
	s_waitcnt lgkmcnt(0)
	v_mfma_f32_16x16x32_bf16 v[26:29], v[34:37], v[2:5], v[26:29]
	s_nop 2
	s_waitcnt lgkmcnt(0)
	s_nop 3
	v_fmac_f32_e32 v244, 0x3e000000, v26
	v_cndmask_b32_e64 v140, v140, v244, s[38:39]
	s_nop 2
	s_waitcnt lgkmcnt(0)
	s_nop 0
	v_fmac_f32_e32 v245, 0x3e000000, v27
	v_cndmask_b32_e64 v138, v138, v245, s[44:45]
	v_mov_b32_e32 v139, 0xf149f2ca
	v_mov_b32_e32 v143, 0xf149f2ca
	s_nop 2
	s_waitcnt lgkmcnt(0)
	v_fmac_f32_e32 v246, 0x3e000000, v28
	v_cndmask_b32_e64 v143, v143, v246, s[46:47]
	s_nop 2
	s_waitcnt lgkmcnt(0)
	v_fmac_f32_e32 v247, 0x3e000000, v29
	v_cndmask_b32_e64 v139, v139, v247, s[66:67]
	s_waitcnt vmcnt(3)
	ds_write_b128 v75, v[10:13]
	s_waitcnt vmcnt(2)
	ds_write_b128 v75, v[14:17] offset:9216
	s_waitcnt lgkmcnt(0)
	s_barrier
	ds_read_b32 v240, v31 offset:38536
	ds_read_b32 v241, v31 offset:38540
	ds_read_b32 v242, v31 offset:38544
	ds_read_b32 v243, v31 offset:38548
	ds_read_b32 v244, v31 offset:38600
	ds_read_b32 v245, v31 offset:38604
	ds_read_b32 v246, v31 offset:38608
	ds_read_b32 v247, v31 offset:38612
	ds_read_b128 v[10:13], v32
	ds_read_b128 v[26:29], v32 offset:64
	s_lshl_b32 s26, s17, 8
	v_or_b32_e32 v34, s26, v89
	v_mov_b64_e32 v[14:15], s[8:9]
	v_mad_i64_i32 v[14:15], s[52:53], v34, s72, v[14:15]
	v_lshl_add_u64 v[14:15], v[14:15], 0, v[70:71]
	v_lshl_add_u64 v[14:15], v[14:15], 0, s[2:3]
	s_waitcnt lgkmcnt(1)
	v_mfma_f32_16x16x32_bf16 v[36:39], v[10:13], v[6:9], 0
	global_load_dwordx4 v[10:13], v[14:15], off offset:1024
	s_nop 0
	global_load_dwordx4 v[14:17], v[14:15], off offset:1152
	v_mov_b32_e32 v141, 0xf149f2ca
	v_mov_b32_e32 v142, 0xf149f2ca
	s_waitcnt lgkmcnt(0)
	v_mfma_f32_16x16x32_bf16 v[26:29], v[26:29], v[2:5], v[36:39]
	s_nop 2
	s_waitcnt lgkmcnt(0)
	s_nop 3
	v_fmac_f32_e32 v240, 0x3e000000, v26
	v_cndmask_b32_e64 v142, v142, v240, s[28:29]
	s_nop 2
	s_waitcnt lgkmcnt(0)
	s_nop 0
	v_fmac_f32_e32 v241, 0x3e000000, v27
	v_cndmask_b32_e64 v141, v141, v241, s[30:31]
	v_mov_b32_e32 v144, 0xf149f2ca
	v_mov_b32_e32 v145, 0xf149f2ca
	s_nop 2
	s_waitcnt lgkmcnt(0)
	v_fmac_f32_e32 v242, 0x3e000000, v28
	v_cndmask_b32_e64 v145, v145, v242, s[34:35]
	s_nop 2
	s_waitcnt lgkmcnt(0)
	v_fmac_f32_e32 v243, 0x3e000000, v29
	v_cndmask_b32_e64 v144, v144, v243, s[36:37]
	ds_read_b128 v[26:29], v33
	ds_read_b128 v[36:39], v33 offset:64
	v_mov_b32_e32 v146, 0xf149f2ca
	v_mov_b32_e32 v148, 0xf149f2ca
	s_waitcnt lgkmcnt(1)
	v_mfma_f32_16x16x32_bf16 v[26:29], v[26:29], v[6:9], 0
	s_waitcnt lgkmcnt(0)
	v_mfma_f32_16x16x32_bf16 v[26:29], v[36:39], v[2:5], v[26:29]
	s_nop 2
	s_waitcnt lgkmcnt(0)
	s_nop 3
	v_fmac_f32_e32 v244, 0x3e000000, v26
	v_cndmask_b32_e64 v148, v148, v244, s[38:39]
	s_nop 2
	s_waitcnt lgkmcnt(0)
	s_nop 0
	v_fmac_f32_e32 v245, 0x3e000000, v27
	v_cndmask_b32_e64 v146, v146, v245, s[44:45]
	v_mov_b32_e32 v147, 0xf149f2ca
	v_mov_b32_e32 v151, 0xf149f2ca
	s_nop 2
	s_waitcnt lgkmcnt(0)
	v_fmac_f32_e32 v246, 0x3e000000, v28
	v_cndmask_b32_e64 v151, v151, v246, s[46:47]
	s_nop 2
	s_waitcnt lgkmcnt(0)
	v_fmac_f32_e32 v247, 0x3e000000, v29
	v_cndmask_b32_e64 v147, v147, v247, s[66:67]
	s_waitcnt vmcnt(3)
	ds_write_b128 v75, v[18:21] offset:18432
	s_waitcnt vmcnt(2)
	ds_write_b128 v75, v[22:25] offset:27648
	s_waitcnt lgkmcnt(0)
	s_barrier
; #define LAS __attribute__((address_space(3)))
; template <bool LOCAL>
; __device__ __forceinline__ void na_unit(const bf16* P, const bf16* VT, bf16* YCAT, const LAS float* rpb_l, LAS bf16* buf, int b, int gr, int hp, int qblk, int tid) {
;     ...
;         if (sidx < NCH) {
;             const int c = sidx;
;             if (LOCAL && c < 8) {
; #pragma unroll
;                 for (int t2 = 0; t2 < 2; ++t2) {
;                     const LAS bf16* kp = cb + (kc0 + 16 * t2 + fr) * 72 + 8 * fq;
;                     f32x4 acc = {0.f, 0.f, 0.f, 0.f};
;                     acc = __builtin_amdgcn_mfma_f32_16x16x32_bf16(*(const LAS bf16x8*)(kp), qf[0], acc, 0, 0, 0);
;                     acc = __builtin_amdgcn_mfma_f32_16x16x32_bf16(*(const LAS bf16x8*)(kp + 32), qf[1], acc, 0, 0, 0);
;                     const LAS float* rb = rpb + (r0 + c - gr + 7) * 31 + 15 - qcol;
; #pragma unroll
;                     for (int e = 0; e < 4; ++e) { const int kcol = kc0 + 16 * t2 + 4 * fq + e; const bool ok = (kcol >= cs) && (kcol < cs + 16);
;                         const float sv = ok ? acc[e] * 0.125f + rb[ok ? kcol : qcol] : -1.0e30f; acc[e] = sv; m = fmaxf(m, sv); }
;                     sl[2 * (c < 8 ? c : 0) + t2] = acc; }
;             } else {
;                 const int cc = c - NLOC;
; #pragma unroll
;                 for (int t4 = 0; t4 < 4; ++t4) {
;                     const LAS bf16* kp = cb + (16 * t4 + fr) * 72 + 8 * fq;
;                     f32x4 acc = {0.f, 0.f, 0.f, 0.f};
;                     acc = __builtin_amdgcn_mfma_f32_16x16x32_bf16(*(const LAS bf16x8*)(kp), qf[0], acc, 0, 0, 0);
;                     acc = __builtin_amdgcn_mfma_f32_16x16x32_bf16(*(const LAS bf16x8*)(kp + 32), qf[1], acc, 0, 0, 0);
; #pragma unroll
;                     for (int e = 0; e < 4; ++e) { acc[e] *= 0.125f; m = fmaxf(m, acc[e]); }
;                     sc[4 * (cc >= 0 ? cc : 0) + t4] = acc; }
;             }
;             if (sidx == NCH - 1) { m = fmaxf(m, __shfl_xor(m, 16)); m = fmaxf(m, __shfl_xor(m, 32)); }
	ds_read_b32 v240, v31 offset:38660
	ds_read_b32 v241, v31 offset:38664
	ds_read_b32 v242, v31 offset:38668
	ds_read_b32 v243, v31 offset:38672
	ds_read_b32 v244, v31 offset:38724
	ds_read_b32 v245, v31 offset:38728
	ds_read_b32 v246, v31 offset:38732
	ds_read_b32 v247, v31 offset:38736
	ds_read_b128 v[18:21], v32 offset:18432
	ds_read_b128 v[26:29], v32 offset:18496
	v_or_b32_e32 v24, 64, v34
	v_mov_b64_e32 v[22:23], s[8:9]
	v_mad_i64_i32 v[22:23], s[52:53], v24, s72, v[22:23]
	v_lshl_add_u64 v[22:23], v[22:23], 0, v[70:71]
	v_lshl_add_u64 v[22:23], v[22:23], 0, s[2:3]
	s_waitcnt lgkmcnt(1)
	v_mfma_f32_16x16x32_bf16 v[36:39], v[18:21], v[6:9], 0
	global_load_dwordx4 v[18:21], v[22:23], off offset:1024
	s_nop 0
	global_load_dwordx4 v[22:25], v[22:23], off offset:1152
	v_mov_b32_e32 v149, 0xf149f2ca
	v_mov_b32_e32 v150, 0xf149f2ca
	s_waitcnt lgkmcnt(0)
	v_mfma_f32_16x16x32_bf16 v[26:29], v[26:29], v[2:5], v[36:39]
	s_nop 2
	s_waitcnt lgkmcnt(0)
	s_nop 3
	v_fmac_f32_e32 v240, 0x3e000000, v26
	v_cndmask_b32_e64 v150, v150, v240, s[28:29]
	s_nop 2
	s_waitcnt lgkmcnt(0)
	s_nop 0
	v_fmac_f32_e32 v241, 0x3e000000, v27
	v_cndmask_b32_e64 v149, v149, v241, s[30:31]
	v_mov_b32_e32 v152, 0xf149f2ca
	v_mov_b32_e32 v153, 0xf149f2ca
	s_nop 2
	s_waitcnt lgkmcnt(0)
	v_fmac_f32_e32 v242, 0x3e000000, v28
	v_cndmask_b32_e64 v153, v153, v242, s[34:35]
	s_nop 2
	s_waitcnt lgkmcnt(0)
	v_fmac_f32_e32 v243, 0x3e000000, v29
	v_cndmask_b32_e64 v152, v152, v243, s[36:37]
	ds_read_b128 v[26:29], v33 offset:18432
	ds_read_b128 v[36:39], v33 offset:18496
	v_mov_b32_e32 v154, 0xf149f2ca
	v_mov_b32_e32 v156, 0xf149f2ca
	s_waitcnt lgkmcnt(1)
	v_mfma_f32_16x16x32_bf16 v[26:29], v[26:29], v[6:9], 0
	s_waitcnt lgkmcnt(0)
	v_mfma_f32_16x16x32_bf16 v[26:29], v[36:39], v[2:5], v[26:29]
	s_nop 2
	s_waitcnt lgkmcnt(0)
	s_nop 3
	v_fmac_f32_e32 v244, 0x3e000000, v26
	v_cndmask_b32_e64 v156, v156, v244, s[38:39]
	s_nop 2
	s_waitcnt lgkmcnt(0)
	s_nop 0
	v_fmac_f32_e32 v245, 0x3e000000, v27
	v_cndmask_b32_e64 v154, v154, v245, s[44:45]
	v_mov_b32_e32 v155, 0xf149f2ca
	v_mov_b32_e32 v158, 0xf149f2ca
	s_nop 2
	s_waitcnt lgkmcnt(0)
	v_fmac_f32_e32 v246, 0x3e000000, v28
	v_cndmask_b32_e64 v158, v158, v246, s[46:47]
	s_nop 2
	s_waitcnt lgkmcnt(0)
	v_fmac_f32_e32 v247, 0x3e000000, v29
	v_cndmask_b32_e64 v155, v155, v247, s[66:67]
	v_max3_f32 v26, v93, s75, v92
	v_max3_f32 v26, v26, v95, v94
	v_max3_f32 v26, v26, v97, v96
	v_max3_f32 v26, v26, v100, v98
	v_max3_f32 v26, v26, v101, v99
	v_max3_f32 v26, v26, v103, v102
	v_max3_f32 v26, v26, v106, v104
	v_max3_f32 v26, v26, v110, v108
	v_max3_f32 v26, v26, v107, v105
	v_max3_f32 v26, v26, v111, v109
	v_max3_f32 v26, v26, v114, v112
	v_max3_f32 v26, v26, v117, v113
	v_max3_f32 v26, v26, v116, v115
	v_max3_f32 v26, v26, v119, v118
	v_max3_f32 v26, v26, v122, v120
	v_max3_f32 v26, v26, v125, v121
	v_max3_f32 v26, v26, v124, v123
	v_max3_f32 v26, v26, v127, v126
	v_max3_f32 v26, v26, v130, v128
	v_max3_f32 v26, v26, v134, v129
	v_max3_f32 v26, v26, v132, v131
	v_max3_f32 v26, v26, v136, v135
	v_max3_f32 v26, v26, v140, v138
	v_max3_f32 v26, v26, v143, v139
	v_max3_f32 v26, v26, v142, v141
	v_max3_f32 v26, v26, v145, v144
	v_mad_u32_u24 v90, v90, s73, v30
	v_max3_f32 v26, v26, v148, v146
	s_waitcnt vmcnt(3)
	ds_write_b128 v75, v[10:13]
	s_waitcnt vmcnt(2)
	ds_write_b128 v75, v[14:17] offset:9216
	s_waitcnt lgkmcnt(0)
	s_barrier
	ds_read_b128 v[10:13], v90
	ds_read_b128 v[14:17], v90 offset:64
	v_max3_f32 v26, v26, v151, v147
	v_max3_f32 v26, v26, v150, v149
	v_max3_f32 v26, v26, v153, v152
	v_max3_f32 v26, v26, v156, v154
	v_max3_f32 v35, v26, v158, v155
	v_or_b32_e32 v26, 0x80, v34
	v_mov_b64_e32 v[44:45], s[8:9]
	v_mad_i64_i32 v[26:27], s[28:29], v26, s72, v[44:45]
	v_lshl_add_u64 v[26:27], v[26:27], 0, v[70:71]
	v_lshl_add_u64 v[30:31], v[26:27], 0, s[2:3]
	s_waitcnt lgkmcnt(1)
	v_mfma_f32_16x16x32_bf16 v[10:13], v[10:13], v[6:9], 0
	global_load_dwordx4 v[26:29], v[30:31], off offset:1024
	s_nop 0
	global_load_dwordx4 v[30:33], v[30:31], off offset:1152
	ds_read_b128 v[36:39], v90 offset:2304
	v_lshl_add_u64 v[78:79], s[4:5], 0, v[70:71]
	s_waitcnt lgkmcnt(1)
	v_mfma_f32_16x16x32_bf16 v[62:65], v[14:17], v[2:5], v[10:13]
	s_ashr_i32 s17, s16, 31
	v_mov_b32_e32 v81, v71
	v_cmp_lt_i32_e32 vcc, v84, v85
	ds_read_b128 v[10:13], v90 offset:2368
	v_add3_u32 v157, v87, v76, v88
	s_nop 2
	v_mul_f32_e32 v14, 0x3e000000, v62
	v_mul_f32_e32 v15, 0x3e000000, v63
	v_max3_f32 v35, v35, v14, v15
	v_mul_f32_e32 v40, 0x3e000000, v64
	s_waitcnt lgkmcnt(1)
	v_mfma_f32_16x16x32_bf16 v[14:17], v[36:39], v[6:9], 0
	v_mul_f32_e32 v36, 0x3e000000, v65
	v_max3_f32 v35, v35, v40, v36
	ds_read_b128 v[36:39], v90 offset:4608
	s_waitcnt lgkmcnt(1)
	v_mfma_f32_16x16x32_bf16 v[66:69], v[10:13], v[2:5], v[14:17]
	ds_read_b128 v[10:13], v90 offset:4672
	s_ashr_i32 s19, s18, 31
	s_ashr_i32 s21, s20, 31
	s_ashr_i32 s23, s22, 31
	s_ashr_i32 s25, s24, 31
	s_nop 2
	v_mul_f32_e32 v14, 0x3e000000, v66
	v_mul_f32_e32 v15, 0x3e000000, v67
	v_max3_f32 v35, v35, v14, v15
	s_waitcnt lgkmcnt(1)
	v_mfma_f32_16x16x32_bf16 v[14:17], v[36:39], v[6:9], 0
	v_mul_f32_e32 v40, 0x3e000000, v68
	v_mul_f32_e32 v41, 0x3e000000, v69
	v_max3_f32 v35, v35, v40, v41
	s_waitcnt lgkmcnt(0)
	v_mfma_f32_16x16x32_bf16 v[58:61], v[10:13], v[2:5], v[14:17]
	ds_read_b128 v[36:39], v90 offset:6912
	ds_read_b128 v[40:43], v90 offset:6976
	s_waitcnt vmcnt(3)
	ds_write_b128 v75, v[18:21] offset:18432
	s_waitcnt vmcnt(2)
	ds_write_b128 v75, v[22:25] offset:27648
	s_waitcnt lgkmcnt(0)
	s_nop 0
	v_mul_f32_e32 v10, 0x3e000000, v58
	v_mul_f32_e32 v11, 0x3e000000, v59
	v_max3_f32 v14, v35, v10, v11
	v_mfma_f32_16x16x32_bf16 v[10:13], v[36:39], v[6:9], 0
	v_mul_f32_e32 v15, 0x3e000000, v60
	v_mul_f32_e32 v16, 0x3e000000, v61
	v_max3_f32 v14, v14, v15, v16
	v_mfma_f32_16x16x32_bf16 v[54:57], v[40:43], v[2:5], v[10:13]
	s_barrier
; #define LAS __attribute__((address_space(3)))
; template <bool LOCAL>
; __device__ __forceinline__ void na_unit(const bf16* P, const bf16* VT, bf16* YCAT, const LAS float* rpb_l, LAS bf16* buf, int b, int gr, int hp, int qblk, int tid) {
;     ...
;                 const int cc = c - NLOC;
; #pragma unroll
;                 for (int t4 = 0; t4 < 4; ++t4) {
;                     const LAS bf16* kp = cb + (16 * t4 + fr) * 72 + 8 * fq;
;                     f32x4 acc = {0.f, 0.f, 0.f, 0.f};
;                     acc = __builtin_amdgcn_mfma_f32_16x16x32_bf16(*(const LAS bf16x8*)(kp), qf[0], acc, 0, 0, 0);
;                     acc = __builtin_amdgcn_mfma_f32_16x16x32_bf16(*(const LAS bf16x8*)(kp + 32), qf[1], acc, 0, 0, 0);
; #pragma unroll
;                     for (int e = 0; e < 4; ++e) { acc[e] *= 0.125f; m = fmaxf(m, acc[e]); }
;                     sc[4 * (cc >= 0 ? cc : 0) + t4] = acc; }
;             }
;             if (sidx == NCH - 1) { m = fmaxf(m, __shfl_xor(m, 16)); m = fmaxf(m, __shfl_xor(m, 32)); }
	v_or_b32_e32 v18, 0xc0, v34
	v_mad_i64_i32 v[18:19], s[28:29], v18, s72, v[44:45]
	v_lshl_add_u64 v[18:19], v[18:19], 0, v[70:71]
	s_nop 3
	v_mul_f32_e32 v10, 0x3e000000, v54
	v_mul_f32_e32 v11, 0x3e000000, v55
	v_max3_f32 v14, v14, v10, v11
	ds_read_b128 v[10:13], v90 offset:18432
	v_mul_f32_e32 v15, 0x3e000000, v56
	v_mul_f32_e32 v16, 0x3e000000, v57
	v_max3_f32 v35, v14, v15, v16
	ds_read_b128 v[14:17], v90 offset:18496
	v_lshl_add_u64 v[22:23], v[18:19], 0, s[2:3]
	s_waitcnt lgkmcnt(1)
	v_mfma_f32_16x16x32_bf16 v[10:13], v[10:13], v[6:9], 0
	global_load_dwordx4 v[18:21], v[22:23], off offset:1024
	global_load_dwordx4 v[160:163], v[22:23], off offset:1152
	ds_read_b128 v[22:25], v90 offset:20736
	s_ashr_i32 s27, s26, 31
	s_waitcnt lgkmcnt(1)
	v_mfma_f32_16x16x32_bf16 v[46:49], v[14:17], v[2:5], v[10:13]
	s_nop 2
	ds_read_b128 v[10:13], v90 offset:20800
	s_nop 3
	v_mul_f32_e32 v14, 0x3e000000, v46
	v_mul_f32_e32 v15, 0x3e000000, v47
	v_max3_f32 v34, v35, v14, v15
	v_mul_f32_e32 v35, 0x3e000000, v48
	s_waitcnt lgkmcnt(1)
	v_mfma_f32_16x16x32_bf16 v[14:17], v[22:25], v[6:9], 0
	v_mul_f32_e32 v22, 0x3e000000, v49
	v_max3_f32 v34, v34, v35, v22
	ds_read_b128 v[22:25], v90 offset:23040
	s_waitcnt lgkmcnt(1)
	v_mfma_f32_16x16x32_bf16 v[50:53], v[10:13], v[2:5], v[14:17]
	ds_read_b128 v[10:13], v90 offset:23104
	s_nop 6
	v_mul_f32_e32 v14, 0x3e000000, v50
	v_mul_f32_e32 v15, 0x3e000000, v51
	v_max3_f32 v34, v34, v14, v15
	s_waitcnt lgkmcnt(1)
	v_mfma_f32_16x16x32_bf16 v[14:17], v[22:25], v[6:9], 0
	v_mul_f32_e32 v35, 0x3e000000, v52
	v_mul_f32_e32 v36, 0x3e000000, v53
	v_max3_f32 v38, v34, v35, v36
	s_waitcnt lgkmcnt(0)
	v_mfma_f32_16x16x32_bf16 v[42:45], v[10:13], v[2:5], v[14:17]
	ds_read_b128 v[22:25], v90 offset:25344
	ds_read_b128 v[34:37], v90 offset:25408
	s_waitcnt vmcnt(3)
	ds_write_b128 v75, v[26:29]
	s_waitcnt vmcnt(2)
	ds_write_b128 v75, v[30:33] offset:9216
	s_waitcnt lgkmcnt(0)
	s_nop 0
	v_mul_f32_e32 v10, 0x3e000000, v42
	v_mul_f32_e32 v11, 0x3e000000, v43
	v_max3_f32 v14, v38, v10, v11
	v_mfma_f32_16x16x32_bf16 v[10:13], v[22:25], v[6:9], 0
	v_mul_f32_e32 v15, 0x3e000000, v44
	v_mul_f32_e32 v16, 0x3e000000, v45
	v_max3_f32 v14, v14, v15, v16
	v_mfma_f32_16x16x32_bf16 v[38:41], v[34:37], v[2:5], v[10:13]
	s_barrier
	v_add3_u32 v26, v89, s1, 64
	v_mul_u32_u24_e32 v26, 0x9000, v26
	v_lshl_add_u64 v[22:23], s[16:17], 1, v[78:79]
	s_nop 3
	v_mul_f32_e32 v10, 0x3e000000, v38
	v_mul_f32_e32 v11, 0x3e000000, v39
	v_max3_f32 v10, v14, v10, v11
	v_mul_f32_e32 v11, 0x3e000000, v40
	v_mul_f32_e32 v12, 0x3e000000, v41
	v_max3_f32 v34, v10, v11, v12
	v_or_b32_e32 v10, s1, v89
	v_mul_u32_u24_e32 v14, 0x9000, v10
	ds_read_b128 v[10:13], v90
	v_lshlrev_b32_e32 v70, 1, v14
	ds_read_b128 v[14:17], v90 offset:64
	v_lshlrev_b32_e32 v80, 1, v26
	v_lshl_add_u64 v[24:25], v[22:23], 0, v[70:71]
	v_lshl_add_u64 v[22:23], v[22:23], 0, v[80:81]
	s_waitcnt lgkmcnt(1)
	v_mfma_f32_16x16x32_bf16 v[10:13], v[10:13], v[6:9], 0
	global_load_dwordx4 v[164:167], v[24:25], off
	global_load_dwordx4 v[172:175], v[22:23], off
	ds_read_b128 v[22:25], v90 offset:2304
	s_add_i32 s16, s15, s50
	s_waitcnt lgkmcnt(1)
	v_mfma_f32_16x16x32_bf16 v[30:33], v[14:17], v[2:5], v[10:13]
	s_ashr_i32 s17, s16, 31
	s_ashr_i32 s15, s14, 31
	v_lshl_add_u64 v[168:169], s[14:15], 1, v[78:79]
	ds_read_b128 v[10:13], v90 offset:2368
	s_ashr_i32 s1, s0, 31
	s_nop 2
	v_mul_f32_e32 v14, 0x3e000000, v30
	v_mul_f32_e32 v15, 0x3e000000, v31
	v_max3_f32 v26, v34, v14, v15
	v_mul_f32_e32 v27, 0x3e000000, v32
	s_waitcnt lgkmcnt(1)
	v_mfma_f32_16x16x32_bf16 v[14:17], v[22:25], v[6:9], 0
	v_mul_f32_e32 v22, 0x3e000000, v33
	v_max3_f32 v26, v26, v27, v22
	ds_read_b128 v[22:25], v90 offset:4608
	s_waitcnt lgkmcnt(1)
	v_mfma_f32_16x16x32_bf16 v[34:37], v[10:13], v[2:5], v[14:17]
	ds_read_b128 v[10:13], v90 offset:4672
	s_nop 6
	v_mul_f32_e32 v14, 0x3e000000, v34
	v_mul_f32_e32 v15, 0x3e000000, v35
	v_max3_f32 v26, v26, v14, v15
	s_waitcnt lgkmcnt(1)
	v_mfma_f32_16x16x32_bf16 v[14:17], v[22:25], v[6:9], 0
	v_mul_f32_e32 v27, 0x3e000000, v36
	v_mul_f32_e32 v28, 0x3e000000, v37
	v_max3_f32 v89, v26, v27, v28
	s_waitcnt lgkmcnt(0)
	v_mfma_f32_16x16x32_bf16 v[26:29], v[10:13], v[2:5], v[14:17]
	ds_read_b128 v[22:25], v90 offset:6912
	ds_read_b128 v[176:179], v90 offset:6976
	s_waitcnt vmcnt(3)
	ds_write_b128 v75, v[18:21] offset:18432
	s_waitcnt vmcnt(2)
	ds_write_b128 v75, v[160:163] offset:27648
	s_waitcnt lgkmcnt(0)
	s_nop 0
	v_mul_f32_e32 v10, 0x3e000000, v26
	v_mul_f32_e32 v11, 0x3e000000, v27
	v_max3_f32 v14, v89, v10, v11
	v_mfma_f32_16x16x32_bf16 v[10:13], v[22:25], v[6:9], 0
	v_mul_f32_e32 v15, 0x3e000000, v28
	v_mul_f32_e32 v16, 0x3e000000, v29
	v_max3_f32 v14, v14, v15, v16
	v_mfma_f32_16x16x32_bf16 v[22:25], v[176:179], v[2:5], v[10:13]
	s_barrier
; #define LAS __attribute__((address_space(3)))
; __device__ __forceinline__ unsigned cvt_pk_bf16(float lo, float hi) { const float __attribute__((ext_vector_type(2))) v = {lo, hi}; return __builtin_bit_cast(unsigned, __builtin_convertvector(v, bf16x2_t)); }
; template <bool LOCAL>
; __device__ __forceinline__ void na_unit(const bf16* P, const bf16* VT, bf16* YCAT, const LAS float* rpb_l, LAS bf16* buf, int b, int gr, int hp, int qblk, int tid) {
;     ...
;                 const int cc = c - NLOC;
; #pragma unroll
;                 for (int t4 = 0; t4 < 4; ++t4) {
;                     const LAS bf16* kp = cb + (16 * t4 + fr) * 72 + 8 * fq;
;                     f32x4 acc = {0.f, 0.f, 0.f, 0.f};
;                     acc = __builtin_amdgcn_mfma_f32_16x16x32_bf16(*(const LAS bf16x8*)(kp), qf[0], acc, 0, 0, 0);
;                     acc = __builtin_amdgcn_mfma_f32_16x16x32_bf16(*(const LAS bf16x8*)(kp + 32), qf[1], acc, 0, 0, 0);
; #pragma unroll
;                     for (int e = 0; e < 4; ++e) { acc[e] *= 0.125f; m = fmaxf(m, acc[e]); }
;                     sc[4 * (cc >= 0 ? cc : 0) + t4] = acc; }
;             }
;             if (sidx == NCH - 1) { m = fmaxf(m, __shfl_xor(m, 16)); m = fmaxf(m, __shfl_xor(m, 32)); }
;         } else {
;             const int c = sidx - NCH;
;             if (LOCAL && c < 8) {
;                 float p[8];
; #pragma unroll
;                 for (int e = 0; e < 4; ++e) { p[e] = __expf(sl[2 * (c < 8 ? c : 0)][e] - m); p[4 + e] = __expf(sl[2 * (c < 8 ? c : 0) + 1][e] - m); }
; #pragma unroll
;                 for (int e = 0; e < 8; ++e) lsum += p[e];
;                 const bf16x8 pf = __builtin_bit_cast(bf16x8, (v4u){pg8::cvt_pk_bf16(p[0], p[1]), pg8::cvt_pk_bf16(p[2], p[3]), pg8::cvt_pk_bf16(p[4], p[5]), pg8::cvt_pk_bf16(p[6], p[7])});
; #pragma unroll
;                 for (int dt = 0; dt < 4; ++dt) { const LAS bf16* vp = cb + (16 * dt + fr) * 72 + kc0 + 4 * fq;
;                     o[dt] = __builtin_amdgcn_mfma_f32_16x16x32_bf16(frag44(vp, vp + 16), pf, o[dt], 0, 0, 0); }
	v_lshl_add_u64 v[18:19], s[16:17], 1, v[78:79]
	v_lshl_add_u64 v[20:21], v[18:19], 0, v[70:71]
	v_lshl_add_u64 v[18:19], v[18:19], 0, v[80:81]
	s_nop 3
	v_mul_f32_e32 v10, 0x3e000000, v22
	v_mul_f32_e32 v11, 0x3e000000, v23
	v_max3_f32 v14, v14, v10, v11
	ds_read_b128 v[10:13], v90 offset:18432
	v_mul_f32_e32 v15, 0x3e000000, v24
	v_mul_f32_e32 v16, 0x3e000000, v25
	v_max3_f32 v89, v14, v15, v16
	ds_read_b128 v[14:17], v90 offset:18496
	s_waitcnt lgkmcnt(1)
	v_mfma_f32_16x16x32_bf16 v[10:13], v[10:13], v[6:9], 0
	global_load_dwordx4 v[160:163], v[20:21], off
	global_load_dwordx4 v[176:179], v[18:19], off
	ds_read_b128 v[18:21], v90 offset:20736
	ds_read_b128 v[180:183], v90 offset:23040
	s_waitcnt lgkmcnt(2)
	v_mfma_f32_16x16x32_bf16 v[14:17], v[14:17], v[2:5], v[10:13]
	s_nop 2
	ds_read_b128 v[10:13], v90 offset:20800
	s_waitcnt lgkmcnt(2)
	v_mfma_f32_16x16x32_bf16 v[18:21], v[18:21], v[6:9], 0
	s_nop 1
	v_mul_f32_e32 v133, 0x3e000000, v14
	v_mul_f32_e32 v137, 0x3e000000, v15
	v_max3_f32 v89, v89, v133, v137
	s_waitcnt lgkmcnt(0)
	v_mfma_f32_16x16x32_bf16 v[18:21], v[10:13], v[2:5], v[18:21]
	ds_read_b128 v[10:13], v90 offset:23104
	ds_read_b128 v[184:187], v90 offset:25344
	ds_read_b128 v[188:191], v90 offset:25408
	v_mul_f32_e32 v133, 0x3e000000, v16
	v_mfma_f32_16x16x32_bf16 v[180:183], v[180:183], v[6:9], 0
	v_mul_f32_e32 v137, 0x3e000000, v17
	v_max3_f32 v89, v89, v133, v137
	s_nop 0
	v_mul_f32_e32 v133, 0x3e000000, v18
	s_waitcnt lgkmcnt(1)
	v_mfma_f32_16x16x32_bf16 v[6:9], v[184:187], v[6:9], 0
	v_mul_f32_e32 v137, 0x3e000000, v19
	v_max3_f32 v89, v89, v133, v137
	v_mul_f32_e32 v133, 0x3e000000, v20
	v_mfma_f32_16x16x32_bf16 v[10:13], v[10:13], v[2:5], v[180:183]
	v_mul_f32_e32 v137, 0x3e000000, v21
	v_max3_f32 v89, v89, v133, v137
	s_waitcnt vmcnt(3)
	ds_write_b128 v75, v[164:167]
	s_waitcnt vmcnt(2)
	ds_write_b128 v75, v[172:175] offset:9216
	s_waitcnt lgkmcnt(2)
	v_mfma_f32_16x16x32_bf16 v[2:5], v[188:191], v[2:5], v[6:9]
	v_mul_f32_e32 v90, 0x3e000000, v10
	v_mul_f32_e32 v133, 0x3e000000, v11
	v_max3_f32 v89, v89, v90, v133
	v_mul_f32_e32 v90, 0x3e000000, v12
	v_mul_f32_e32 v133, 0x3e000000, v13
	v_max3_f32 v89, v89, v90, v133
	s_nop 1
	v_mul_f32_e32 v6, 0x3e000000, v2
	v_mul_f32_e32 v7, 0x3e000000, v3
	v_max3_f32 v6, v89, v6, v7
	v_mul_f32_e32 v7, 0x3e000000, v4
	v_mul_f32_e32 v8, 0x3e000000, v5
	v_max3_f32 v6, v6, v7, v8
	v_cndmask_b32_e32 v7, v83, v84, vcc
	v_lshlrev_b32_e32 v89, 2, v7
	ds_bpermute_b32 v7, v89, v6
	v_cmp_lt_i32_e32 vcc, v86, v85
	v_lshl_add_u32 v8, v91, 1, v157
	v_lshl_add_u64 v[188:189], v[168:169], 0, v[70:71]
	s_waitcnt lgkmcnt(0)
	v_max_f32_e32 v7, v7, v7
	v_max_f32_e32 v6, v6, v7
	v_cndmask_b32_e32 v7, v83, v86, vcc
	v_lshlrev_b32_e32 v90, 2, v7
	ds_bpermute_b32 v7, v90, v6
	s_barrier
	s_waitcnt lgkmcnt(0)
	ds_read2_b64 v[164:167], v8 offset1:4
	v_lshl_add_u64 v[168:169], v[168:169], 0, v[80:81]
	v_max_f32_e32 v7, v7, v7
	v_max_f32_e32 v137, v6, v7
	v_sub_f32_e32 v6, v93, v137
	v_mul_f32_e32 v6, 0x3fb8aa3b, v6
	v_exp_f32_e32 v133, v6
	v_sub_f32_e32 v6, v97, v137
	v_mul_f32_e32 v6, 0x3fb8aa3b, v6
	v_exp_f32_e32 v93, v6
	v_sub_f32_e32 v6, v92, v137
	v_mul_f32_e32 v6, 0x3fb8aa3b, v6
	v_exp_f32_e32 v97, v6
	v_sub_f32_e32 v6, v96, v137
	v_mul_f32_e32 v6, 0x3fb8aa3b, v6
	v_exp_f32_e32 v92, v6
	v_sub_f32_e32 v6, v95, v137
	v_mul_f32_e32 v6, 0x3fb8aa3b, v6
	v_exp_f32_e32 v96, v6
	v_sub_f32_e32 v6, v100, v137
	v_mul_f32_e32 v6, 0x3fb8aa3b, v6
	v_exp_f32_e32 v95, v6
	v_sub_f32_e32 v6, v94, v137
	v_mul_f32_e32 v6, 0x3fb8aa3b, v6
	v_exp_f32_e32 v100, v6
	v_sub_f32_e32 v6, v98, v137
	v_mul_f32_e32 v6, 0x3fb8aa3b, v6
	v_exp_f32_e32 v94, v6
	v_add_u32_e32 v7, 0x800, v8
	v_add_u32_e32 v6, 0x1000, v8
	ds_read2_b64 v[180:183], v7 offset0:32 offset1:36
	ds_read2_b64 v[184:187], v6 offset0:64 offset1:68
	global_load_dwordx4 v[188:191], v[188:189], off
	s_nop 0
	global_load_dwordx4 v[192:195], v[168:169], off
	v_sub_f32_e32 v9, v101, v137
	v_mul_f32_e32 v9, 0x3fb8aa3b, v9
	v_add_u32_e32 v159, 0x1800, v8
	v_exp_f32_e32 v87, v9
	v_sub_f32_e32 v9, v106, v137
	ds_read2_b64 v[196:199], v159 offset0:96 offset1:100
	v_mul_f32_e32 v9, 0x3fb8aa3b, v9
	v_exp_f32_e32 v76, v9
	v_sub_f32_e32 v9, v99, v137
	v_mul_f32_e32 v9, 0x3fb8aa3b, v9
	v_exp_f32_e32 v91, v9
	v_sub_f32_e32 v9, v104, v137
	v_mul_f32_e32 v9, 0x3fb8aa3b, v9
	v_exp_f32_e32 v88, v9
	v_sub_f32_e32 v9, v103, v137
	v_mul_f32_e32 v9, 0x3fb8aa3b, v9
	v_exp_f32_e32 v99, v9
	v_sub_f32_e32 v9, v110, v137
	v_cvt_pk_bf16_f32 v172, v133, v97
	v_cvt_pk_bf16_f32 v173, v96, v100
	v_cvt_pk_bf16_f32 v174, v93, v92
	v_cvt_pk_bf16_f32 v175, v95, v94
	s_waitcnt vmcnt(3)
	ds_write_b128 v75, v[160:163] offset:18432
	s_waitcnt vmcnt(2)
	ds_write_b128 v75, v[176:179] offset:27648
	v_mul_f32_e32 v9, 0x3fb8aa3b, v9
	v_add_u32_e32 v161, 0x4800, v8
	v_add_u32_e32 v160, 0x5000, v8
	s_waitcnt lgkmcnt(5)
	v_mfma_f32_16x16x32_bf16 v[164:167], v[164:167], v[172:175], 0
	s_waitcnt lgkmcnt(0)
	s_barrier
; #define LAS __attribute__((address_space(3)))
; __device__ __forceinline__ unsigned cvt_pk_bf16(float lo, float hi) { const float __attribute__((ext_vector_type(2))) v = {lo, hi}; return __builtin_bit_cast(unsigned, __builtin_convertvector(v, bf16x2_t)); }
; template <bool LOCAL>
; __device__ __forceinline__ void na_unit(const bf16* P, const bf16* VT, bf16* YCAT, const LAS float* rpb_l, LAS bf16* buf, int b, int gr, int hp, int qblk, int tid) {
;     ...
;             if (LOCAL && c < 8) {
;                 float p[8];
; #pragma unroll
;                 for (int e = 0; e < 4; ++e) { p[e] = __expf(sl[2 * (c < 8 ? c : 0)][e] - m); p[4 + e] = __expf(sl[2 * (c < 8 ? c : 0) + 1][e] - m); }
; #pragma unroll
;                 for (int e = 0; e < 8; ++e) lsum += p[e];
;                 const bf16x8 pf = __builtin_bit_cast(bf16x8, (v4u){pg8::cvt_pk_bf16(p[0], p[1]), pg8::cvt_pk_bf16(p[2], p[3]), pg8::cvt_pk_bf16(p[4], p[5]), pg8::cvt_pk_bf16(p[6], p[7])});
; #pragma unroll
;                 for (int dt = 0; dt < 4; ++dt) { const LAS bf16* vp = cb + (16 * dt + fr) * 72 + kc0 + 4 * fq;
;                     o[dt] = __builtin_amdgcn_mfma_f32_16x16x32_bf16(frag44(vp, vp + 16), pf, o[dt], 0, 0, 0); }
;             } else {
;                 const int cc = c - NLOC;
; #pragma unroll
;                 for (int p2 = 0; p2 < 2; ++p2) {
;                     float p[8];
; #pragma unroll
;                     for (int e = 0; e < 4; ++e) { p[e] = __expf(sc[4 * (cc >= 0 ? cc : 0) + 2 * p2][e] - m); p[4 + e] = __expf(sc[4 * (cc >= 0 ? cc : 0) + 2 * p2 + 1][e] - m); }
; #pragma unroll
;                     for (int e = 0; e < 8; ++e) lsum += p[e];
;                     const bf16x8 pf = __builtin_bit_cast(bf16x8, (v4u){pg8::cvt_pk_bf16(p[0], p[1]), pg8::cvt_pk_bf16(p[2], p[3]), pg8::cvt_pk_bf16(p[4], p[5]), pg8::cvt_pk_bf16(p[6], p[7])});
; #pragma unroll
;                     for (int dt = 0; dt < 4; ++dt) { const LAS bf16* vp = cb + (16 * dt + fr) * 72 + 32 * p2 + 4 * fq;
;                         o[dt] = __builtin_amdgcn_mfma_f32_16x16x32_bf16(frag44(vp, vp + 16), pf, o[dt], 0, 0, 0); }
;                 }
;             }
;         }
;         if (sidx + 1 < 2 * NCH) NA_STORE(sidx + 1);
;         __syncthreads();
	v_mfma_f32_16x16x32_bf16 v[180:183], v[180:183], v[172:175], 0
	v_exp_f32_e32 v98, v9
	v_sub_f32_e32 v9, v102, v137
	ds_read2_b64 v[176:179], v161 offset1:4
	v_mfma_f32_16x16x32_bf16 v[184:187], v[184:187], v[172:175], 0
	v_mul_f32_e32 v9, 0x3fb8aa3b, v9
	v_exp_f32_e32 v101, v9
	v_sub_f32_e32 v9, v108, v137
	v_mfma_f32_16x16x32_bf16 v[172:175], v[196:199], v[172:175], 0
	ds_read2_b64 v[196:199], v160 offset0:32 offset1:36
	v_mul_f32_e32 v9, 0x3fb8aa3b, v9
	v_exp_f32_e32 v102, v9
	v_lshl_add_u64 v[162:163], s[0:1], 1, v[78:79]
	v_cvt_pk_bf16_f32 v200, v87, v91
	v_cvt_pk_bf16_f32 v201, v99, v101
	v_cvt_pk_bf16_f32 v202, v76, v88
	v_cvt_pk_bf16_f32 v203, v98, v102
	v_lshl_add_u64 v[168:169], v[162:163], 0, v[70:71]
	v_lshl_add_u64 v[204:205], v[162:163], 0, v[80:81]
	v_add_u32_e32 v162, 0x5800, v8
	s_waitcnt lgkmcnt(1)
	v_mfma_f32_16x16x32_bf16 v[164:167], v[176:179], v[200:203], v[164:167]
	v_sub_f32_e32 v9, v107, v137
	v_mul_f32_e32 v9, 0x3fb8aa3b, v9
	v_add_u32_e32 v163, 0x6000, v8
	s_waitcnt lgkmcnt(0)
	v_mfma_f32_16x16x32_bf16 v[176:179], v[196:199], v[200:203], v[180:183]
	v_exp_f32_e32 v104, v9
	v_sub_f32_e32 v9, v114, v137
	v_mul_f32_e32 v9, 0x3fb8aa3b, v9
	ds_read2_b64 v[180:183], v162 offset0:64 offset1:68
	global_load_dwordx4 v[196:199], v[168:169], off
	s_nop 0
	global_load_dwordx4 v[204:207], v[204:205], off
	s_waitcnt lgkmcnt(0)
	v_mfma_f32_16x16x32_bf16 v[180:183], v[180:183], v[200:203], v[184:187]
	s_nop 2
	ds_read2_b64 v[184:187], v163 offset0:96 offset1:100
	v_exp_f32_e32 v103, v9
	v_sub_f32_e32 v9, v105, v137
	v_mul_f32_e32 v9, 0x3fb8aa3b, v9
	v_exp_f32_e32 v106, v9
	v_sub_f32_e32 v9, v112, v137
	v_mul_f32_e32 v9, 0x3fb8aa3b, v9
	v_exp_f32_e32 v105, v9
	v_sub_f32_e32 v9, v111, v137
	v_mul_f32_e32 v9, 0x3fb8aa3b, v9
	v_exp_f32_e32 v108, v9
	v_sub_f32_e32 v9, v117, v137
	v_mul_f32_e32 v9, 0x3fb8aa3b, v9
	s_waitcnt lgkmcnt(0)
	v_mfma_f32_16x16x32_bf16 v[172:175], v[184:187], v[200:203], v[172:175]
	s_waitcnt vmcnt(3)
	ds_write_b128 v75, v[188:191]
	s_waitcnt vmcnt(2)
	ds_write_b128 v75, v[192:195] offset:9216
	s_waitcnt lgkmcnt(0)
	s_barrier
	v_exp_f32_e32 v107, v9
	v_sub_f32_e32 v9, v109, v137
	ds_read2_b64 v[184:187], v8 offset1:4
	ds_read2_b64 v[188:191], v7 offset0:32 offset1:36
	v_mul_f32_e32 v9, 0x3fb8aa3b, v9
	v_exp_f32_e32 v109, v9
	v_sub_f32_e32 v9, v113, v137
	v_mul_f32_e32 v9, 0x3fb8aa3b, v9
	v_exp_f32_e32 v110, v9
	v_lshl_add_u64 v[168:169], s[18:19], 1, v[78:79]
	v_cvt_pk_bf16_f32 v192, v104, v106
	v_cvt_pk_bf16_f32 v193, v108, v109
	v_cvt_pk_bf16_f32 v194, v103, v105
	v_cvt_pk_bf16_f32 v195, v107, v110
	v_lshl_add_u64 v[112:113], v[168:169], 0, v[70:71]
	v_lshl_add_u64 v[168:169], v[168:169], 0, v[80:81]
	s_waitcnt lgkmcnt(1)
	v_mfma_f32_16x16x32_bf16 v[164:167], v[184:187], v[192:195], v[164:167]
	ds_read2_b64 v[184:187], v6 offset0:64 offset1:68
	v_sub_f32_e32 v9, v116, v137
	v_mul_f32_e32 v9, 0x3fb8aa3b, v9
	s_waitcnt lgkmcnt(1)
	v_mfma_f32_16x16x32_bf16 v[176:179], v[188:191], v[192:195], v[176:179]
	global_load_dwordx4 v[188:191], v[112:113], off
	global_load_dwordx4 v[200:203], v[168:169], off
	v_exp_f32_e32 v112, v9
	v_sub_f32_e32 v9, v122, v137
	s_waitcnt lgkmcnt(0)
	v_mfma_f32_16x16x32_bf16 v[180:183], v[184:187], v[192:195], v[180:183]
	ds_read2_b64 v[184:187], v159 offset0:96 offset1:100
	v_mul_f32_e32 v9, 0x3fb8aa3b, v9
	v_exp_f32_e32 v111, v9
	v_sub_f32_e32 v9, v115, v137
	v_mul_f32_e32 v9, 0x3fb8aa3b, v9
	v_exp_f32_e32 v114, v9
	v_sub_f32_e32 v9, v120, v137
	v_mul_f32_e32 v9, 0x3fb8aa3b, v9
	v_exp_f32_e32 v113, v9
	v_sub_f32_e32 v9, v119, v137
	v_mul_f32_e32 v9, 0x3fb8aa3b, v9
	v_exp_f32_e32 v116, v9
	v_sub_f32_e32 v9, v125, v137
	v_mul_f32_e32 v9, 0x3fb8aa3b, v9
	s_waitcnt lgkmcnt(0)
	v_mfma_f32_16x16x32_bf16 v[172:175], v[184:187], v[192:195], v[172:175]
	s_waitcnt vmcnt(3)
	ds_write_b128 v75, v[196:199] offset:18432
	s_waitcnt vmcnt(2)
	ds_write_b128 v75, v[204:207] offset:27648
	s_waitcnt lgkmcnt(0)
	s_barrier
	v_exp_f32_e32 v115, v9
	v_sub_f32_e32 v9, v118, v137
	ds_read2_b64 v[184:187], v161 offset1:4
	v_mul_f32_e32 v9, 0x3fb8aa3b, v9
	v_exp_f32_e32 v117, v9
	v_sub_f32_e32 v9, v121, v137
	v_mul_f32_e32 v9, 0x3fb8aa3b, v9
	v_exp_f32_e32 v118, v9
	v_lshl_add_u64 v[168:169], s[20:21], 1, v[78:79]
	v_lshl_add_u64 v[204:205], v[168:169], 0, v[70:71]
	v_cvt_pk_bf16_f32 v196, v112, v114
	v_cvt_pk_bf16_f32 v197, v116, v117
	v_cvt_pk_bf16_f32 v198, v111, v113
	v_cvt_pk_bf16_f32 v199, v115, v118
	ds_read2_b64 v[192:195], v160 offset0:32 offset1:36
	v_lshl_add_u64 v[120:121], v[168:169], 0, v[80:81]
	s_waitcnt lgkmcnt(1)
	v_mfma_f32_16x16x32_bf16 v[164:167], v[184:187], v[196:199], v[164:167]
	global_load_dwordx4 v[184:187], v[204:205], off
	s_nop 0
	global_load_dwordx4 v[204:207], v[120:121], off
	v_sub_f32_e32 v9, v124, v137
	v_mul_f32_e32 v9, 0x3fb8aa3b, v9
	s_waitcnt lgkmcnt(0)
	v_mfma_f32_16x16x32_bf16 v[176:179], v[192:195], v[196:199], v[176:179]
	ds_read2_b64 v[192:195], v162 offset0:64 offset1:68
	v_exp_f32_e32 v120, v9
	v_sub_f32_e32 v9, v130, v137
	s_waitcnt lgkmcnt(0)
	v_mfma_f32_16x16x32_bf16 v[180:183], v[192:195], v[196:199], v[180:183]
	ds_read2_b64 v[192:195], v163 offset0:96 offset1:100
	v_mul_f32_e32 v9, 0x3fb8aa3b, v9
	v_exp_f32_e32 v119, v9
	v_sub_f32_e32 v9, v123, v137
	v_mul_f32_e32 v9, 0x3fb8aa3b, v9
	v_exp_f32_e32 v122, v9
	v_sub_f32_e32 v9, v128, v137
	v_mul_f32_e32 v9, 0x3fb8aa3b, v9
	v_exp_f32_e32 v121, v9
	v_sub_f32_e32 v9, v127, v137
	v_mul_f32_e32 v9, 0x3fb8aa3b, v9
	v_exp_f32_e32 v124, v9
	v_sub_f32_e32 v9, v134, v137
	v_mul_f32_e32 v9, 0x3fb8aa3b, v9
	s_waitcnt lgkmcnt(0)
	v_mfma_f32_16x16x32_bf16 v[172:175], v[192:195], v[196:199], v[172:175]
	s_waitcnt vmcnt(3)
	ds_write_b128 v75, v[188:191]
	s_waitcnt vmcnt(2)
	ds_write_b128 v75, v[200:203] offset:9216
	s_waitcnt lgkmcnt(0)
	s_barrier
; #define LAS __attribute__((address_space(3)))
; __device__ __forceinline__ unsigned cvt_pk_bf16(float lo, float hi) { const float __attribute__((ext_vector_type(2))) v = {lo, hi}; return __builtin_bit_cast(unsigned, __builtin_convertvector(v, bf16x2_t)); }
; template <bool LOCAL>
; __device__ __forceinline__ void na_unit(const bf16* P, const bf16* VT, bf16* YCAT, const LAS float* rpb_l, LAS bf16* buf, int b, int gr, int hp, int qblk, int tid) {
;     ...
;             if (LOCAL && c < 8) {
;                 float p[8];
; #pragma unroll
;                 for (int e = 0; e < 4; ++e) { p[e] = __expf(sl[2 * (c < 8 ? c : 0)][e] - m); p[4 + e] = __expf(sl[2 * (c < 8 ? c : 0) + 1][e] - m); }
; #pragma unroll
;                 for (int e = 0; e < 8; ++e) lsum += p[e];
;                 const bf16x8 pf = __builtin_bit_cast(bf16x8, (v4u){pg8::cvt_pk_bf16(p[0], p[1]), pg8::cvt_pk_bf16(p[2], p[3]), pg8::cvt_pk_bf16(p[4], p[5]), pg8::cvt_pk_bf16(p[6], p[7])});
; #pragma unroll
;                 for (int dt = 0; dt < 4; ++dt) { const LAS bf16* vp = cb + (16 * dt + fr) * 72 + kc0 + 4 * fq;
;                     o[dt] = __builtin_amdgcn_mfma_f32_16x16x32_bf16(frag44(vp, vp + 16), pf, o[dt], 0, 0, 0); }
;             } else {
;                 const int cc = c - NLOC;
; #pragma unroll
;                 for (int p2 = 0; p2 < 2; ++p2) {
;                     float p[8];
; #pragma unroll
;                     for (int e = 0; e < 4; ++e) { p[e] = __expf(sc[4 * (cc >= 0 ? cc : 0) + 2 * p2][e] - m); p[4 + e] = __expf(sc[4 * (cc >= 0 ? cc : 0) + 2 * p2 + 1][e] - m); }
; #pragma unroll
;                     for (int e = 0; e < 8; ++e) lsum += p[e];
;                     const bf16x8 pf = __builtin_bit_cast(bf16x8, (v4u){pg8::cvt_pk_bf16(p[0], p[1]), pg8::cvt_pk_bf16(p[2], p[3]), pg8::cvt_pk_bf16(p[4], p[5]), pg8::cvt_pk_bf16(p[6], p[7])});
; #pragma unroll
;                     for (int dt = 0; dt < 4; ++dt) { const LAS bf16* vp = cb + (16 * dt + fr) * 72 + 32 * p2 + 4 * fq;
;                         o[dt] = __builtin_amdgcn_mfma_f32_16x16x32_bf16(frag44(vp, vp + 16), pf, o[dt], 0, 0, 0); }
;                 }
;             }
;         }
;         if (sidx + 1 < 2 * NCH) NA_STORE(sidx + 1);
;         __syncthreads();
	v_exp_f32_e32 v123, v9
	v_sub_f32_e32 v9, v126, v137
	ds_read2_b64 v[188:191], v8 offset1:4
	ds_read2_b64 v[192:195], v7 offset0:32 offset1:36
	v_mul_f32_e32 v9, 0x3fb8aa3b, v9
	v_exp_f32_e32 v125, v9
	v_sub_f32_e32 v9, v129, v137
	v_mul_f32_e32 v9, 0x3fb8aa3b, v9
	v_exp_f32_e32 v126, v9
	v_lshl_add_u64 v[168:169], s[22:23], 1, v[78:79]
	v_cvt_pk_bf16_f32 v196, v120, v122
	v_cvt_pk_bf16_f32 v197, v124, v125
	v_cvt_pk_bf16_f32 v198, v119, v121
	v_cvt_pk_bf16_f32 v199, v123, v126
	v_lshl_add_u64 v[128:129], v[168:169], 0, v[70:71]
	v_lshl_add_u64 v[168:169], v[168:169], 0, v[80:81]
	s_waitcnt lgkmcnt(1)
	v_mfma_f32_16x16x32_bf16 v[164:167], v[188:191], v[196:199], v[164:167]
	ds_read2_b64 v[188:191], v6 offset0:64 offset1:68
	v_sub_f32_e32 v9, v132, v137
	v_mul_f32_e32 v9, 0x3fb8aa3b, v9
	s_waitcnt lgkmcnt(1)
	v_mfma_f32_16x16x32_bf16 v[176:179], v[192:195], v[196:199], v[176:179]
	global_load_dwordx4 v[192:195], v[128:129], off
	global_load_dwordx4 v[200:203], v[168:169], off
	v_exp_f32_e32 v128, v9
	v_sub_f32_e32 v9, v140, v137
	v_mul_f32_e32 v9, 0x3fb8aa3b, v9
	v_exp_f32_e32 v127, v9
	v_sub_f32_e32 v9, v131, v137
	v_mul_f32_e32 v9, 0x3fb8aa3b, v9
	v_exp_f32_e32 v130, v9
	v_sub_f32_e32 v9, v138, v137
	v_mul_f32_e32 v9, 0x3fb8aa3b, v9
	v_exp_f32_e32 v129, v9
	v_sub_f32_e32 v9, v136, v137
	v_mul_f32_e32 v9, 0x3fb8aa3b, v9
	v_exp_f32_e32 v132, v9
	v_sub_f32_e32 v9, v143, v137
	s_waitcnt lgkmcnt(0)
	v_mfma_f32_16x16x32_bf16 v[180:183], v[188:191], v[196:199], v[180:183]
	ds_read2_b64 v[188:191], v159 offset0:96 offset1:100
	v_mul_f32_e32 v9, 0x3fb8aa3b, v9
	s_waitcnt vmcnt(3)
	ds_write_b128 v75, v[184:187] offset:18432
	s_waitcnt vmcnt(2)
	ds_write_b128 v75, v[204:207] offset:27648
	s_waitcnt lgkmcnt(0)
	s_barrier
	v_exp_f32_e32 v131, v9
	v_sub_f32_e32 v9, v135, v137
	ds_read2_b64 v[184:187], v161 offset1:4
	v_mul_f32_e32 v9, 0x3fb8aa3b, v9
	v_exp_f32_e32 v134, v9
	v_sub_f32_e32 v9, v139, v137
	v_mul_f32_e32 v9, 0x3fb8aa3b, v9
	v_exp_f32_e32 v135, v9
	v_lshl_add_u64 v[168:169], s[24:25], 1, v[78:79]
	v_mfma_f32_16x16x32_bf16 v[172:175], v[188:191], v[196:199], v[172:175]
	v_lshl_add_u64 v[204:205], v[168:169], 0, v[70:71]
	v_cvt_pk_bf16_f32 v196, v128, v130
	v_cvt_pk_bf16_f32 v197, v132, v134
	v_cvt_pk_bf16_f32 v198, v127, v129
	v_cvt_pk_bf16_f32 v199, v131, v135
	ds_read2_b64 v[188:191], v160 offset0:32 offset1:36
	v_lshl_add_u64 v[138:139], v[168:169], 0, v[80:81]
	s_waitcnt lgkmcnt(1)
	v_mfma_f32_16x16x32_bf16 v[164:167], v[184:187], v[196:199], v[164:167]
	global_load_dwordx4 v[184:187], v[204:205], off
	s_nop 0
	global_load_dwordx4 v[204:207], v[138:139], off
	v_sub_f32_e32 v9, v142, v137
	v_mul_f32_e32 v9, 0x3fb8aa3b, v9
	s_waitcnt lgkmcnt(0)
	v_mfma_f32_16x16x32_bf16 v[176:179], v[188:191], v[196:199], v[176:179]
	ds_read2_b64 v[188:191], v162 offset0:64 offset1:68
	v_exp_f32_e32 v138, v9
	v_sub_f32_e32 v9, v148, v137
	s_waitcnt lgkmcnt(0)
	v_mfma_f32_16x16x32_bf16 v[180:183], v[188:191], v[196:199], v[180:183]
	ds_read2_b64 v[188:191], v163 offset0:96 offset1:100
	v_mul_f32_e32 v9, 0x3fb8aa3b, v9
	v_exp_f32_e32 v136, v9
	v_sub_f32_e32 v9, v141, v137
	v_mul_f32_e32 v9, 0x3fb8aa3b, v9
	v_exp_f32_e32 v140, v9
	v_sub_f32_e32 v9, v146, v137
	v_mul_f32_e32 v9, 0x3fb8aa3b, v9
	v_exp_f32_e32 v139, v9
	v_sub_f32_e32 v9, v145, v137
	v_mul_f32_e32 v9, 0x3fb8aa3b, v9
	s_waitcnt lgkmcnt(0)
	v_mfma_f32_16x16x32_bf16 v[172:175], v[188:191], v[196:199], v[172:175]
	s_waitcnt vmcnt(3)
	ds_write_b128 v75, v[192:195]
	s_waitcnt vmcnt(2)
	ds_write_b128 v75, v[200:203] offset:9216
	s_waitcnt lgkmcnt(0)
	s_barrier
	v_exp_f32_e32 v142, v9
	v_sub_f32_e32 v9, v151, v137
	ds_read2_b64 v[188:191], v8 offset1:4
	v_mul_f32_e32 v9, 0x3fb8aa3b, v9
	ds_read2_b64 v[196:199], v7 offset0:32 offset1:36
	v_exp_f32_e32 v141, v9
	v_sub_f32_e32 v9, v144, v137
	v_sub_f32_e32 v8, v147, v137
	v_mul_f32_e32 v9, 0x3fb8aa3b, v9
	v_mul_f32_e32 v8, 0x3fb8aa3b, v8
	v_exp_f32_e32 v143, v9
	v_exp_f32_e32 v144, v8
	v_cvt_pk_bf16_f32 v192, v138, v140
	v_cvt_pk_bf16_f32 v194, v136, v139
	v_cvt_pk_bf16_f32 v193, v142, v143
	v_cvt_pk_bf16_f32 v195, v141, v144
	v_lshl_add_u64 v[8:9], s[26:27], 1, v[78:79]
	v_sub_f32_e32 v146, v152, v137
	s_waitcnt lgkmcnt(1)
	v_mfma_f32_16x16x32_bf16 v[164:167], v[188:191], v[192:195], v[164:167]
	ds_read2_b64 v[188:191], v6 offset0:64 offset1:68
	v_lshl_add_u64 v[6:7], v[8:9], 0, v[70:71]
	v_lshl_add_u64 v[8:9], v[8:9], 0, v[80:81]
	s_waitcnt lgkmcnt(1)
	v_mfma_f32_16x16x32_bf16 v[176:179], v[196:199], v[192:195], v[176:179]
	global_load_dwordx4 v[196:199], v[6:7], off
	global_load_dwordx4 v[200:203], v[8:9], off
	ds_read2_b64 v[78:81], v159 offset0:96 offset1:100
	s_waitcnt vmcnt(3)
	ds_write_b128 v75, v[184:187] offset:18432
	s_waitcnt vmcnt(2)
	ds_write_b128 v75, v[204:207] offset:27648
	s_waitcnt lgkmcnt(2)
	v_mfma_f32_16x16x32_bf16 v[172:175], v[78:81], v[192:195], v[172:175]
	s_waitcnt lgkmcnt(0)
	s_barrier
; #define LAS __attribute__((address_space(3)))
; __device__ __forceinline__ unsigned cvt_pk_bf16(float lo, float hi) { const float __attribute__((ext_vector_type(2))) v = {lo, hi}; return __builtin_bit_cast(unsigned, __builtin_convertvector(v, bf16x2_t)); }
; template <bool LOCAL>
; __device__ __forceinline__ void na_unit(const bf16* P, const bf16* VT, bf16* YCAT, const LAS float* rpb_l, LAS bf16* buf, int b, int gr, int hp, int qblk, int tid) {
;     ...
;             if (LOCAL && c < 8) {
;                 float p[8];
; #pragma unroll
;                 for (int e = 0; e < 4; ++e) { p[e] = __expf(sl[2 * (c < 8 ? c : 0)][e] - m); p[4 + e] = __expf(sl[2 * (c < 8 ? c : 0) + 1][e] - m); }
; #pragma unroll
;                 for (int e = 0; e < 8; ++e) lsum += p[e];
;                 const bf16x8 pf = __builtin_bit_cast(bf16x8, (v4u){pg8::cvt_pk_bf16(p[0], p[1]), pg8::cvt_pk_bf16(p[2], p[3]), pg8::cvt_pk_bf16(p[4], p[5]), pg8::cvt_pk_bf16(p[6], p[7])});
; #pragma unroll
;                 for (int dt = 0; dt < 4; ++dt) { const LAS bf16* vp = cb + (16 * dt + fr) * 72 + kc0 + 4 * fq;
;                     o[dt] = __builtin_amdgcn_mfma_f32_16x16x32_bf16(frag44(vp, vp + 16), pf, o[dt], 0, 0, 0); }
;             } else {
;                 const int cc = c - NLOC;
; #pragma unroll
;                 for (int p2 = 0; p2 < 2; ++p2) {
;                     float p[8];
; #pragma unroll
;                     for (int e = 0; e < 4; ++e) { p[e] = __expf(sc[4 * (cc >= 0 ? cc : 0) + 2 * p2][e] - m); p[4 + e] = __expf(sc[4 * (cc >= 0 ? cc : 0) + 2 * p2 + 1][e] - m); }
; #pragma unroll
;                     for (int e = 0; e < 8; ++e) lsum += p[e];
;                     const bf16x8 pf = __builtin_bit_cast(bf16x8, (v4u){pg8::cvt_pk_bf16(p[0], p[1]), pg8::cvt_pk_bf16(p[2], p[3]), pg8::cvt_pk_bf16(p[4], p[5]), pg8::cvt_pk_bf16(p[6], p[7])});
; #pragma unroll
;                     for (int dt = 0; dt < 4; ++dt) { const LAS bf16* vp = cb + (16 * dt + fr) * 72 + 32 * p2 + 4 * fq;
;                         o[dt] = __builtin_amdgcn_mfma_f32_16x16x32_bf16(frag44(vp, vp + 16), pf, o[dt], 0, 0, 0); }
;                 }
;             }
;         }
;         if (sidx + 1 < 2 * NCH) NA_STORE(sidx + 1);
;         __syncthreads();
	v_sub_f32_e32 v70, v150, v137
	v_sub_f32_e32 v79, v149, v137
	v_sub_f32_e32 v81, v153, v137
	ds_read2_b64 v[148:151], v161 offset1:4
	v_mul_f32_e32 v70, 0x3fb8aa3b, v70
	v_mul_f32_e32 v79, 0x3fb8aa3b, v79
	v_mul_f32_e32 v81, 0x3fb8aa3b, v81
	v_mul_f32_e32 v146, 0x3fb8aa3b, v146
	v_exp_f32_e32 v78, v70
	v_sub_f32_e32 v70, v156, v137
	v_exp_f32_e32 v80, v79
	v_sub_f32_e32 v79, v154, v137
	v_exp_f32_e32 v145, v81
	v_sub_f32_e32 v81, v158, v137
	v_exp_f32_e32 v147, v146
	v_sub_f32_e32 v146, v155, v137
	v_mul_f32_e32 v70, 0x3fb8aa3b, v70
	v_mul_f32_e32 v79, 0x3fb8aa3b, v79
	v_mul_f32_e32 v81, 0x3fb8aa3b, v81
	v_mul_f32_e32 v146, 0x3fb8aa3b, v146
	v_exp_f32_e32 v70, v70
	v_exp_f32_e32 v79, v79
	v_exp_f32_e32 v81, v81
	v_exp_f32_e32 v146, v146
	v_cvt_pk_bf16_f32 v152, v78, v80
	v_cvt_pk_bf16_f32 v153, v145, v147
	v_cvt_pk_bf16_f32 v154, v70, v79
	v_cvt_pk_bf16_f32 v155, v81, v146
	v_mfma_f32_16x16x32_bf16 v[180:183], v[188:191], v[192:195], v[180:183]
	v_fma_f32 v62, v62, s74, -v137
	v_fma_f32 v63, v63, s74, -v137
	v_fma_f32 v64, v64, s74, -v137
	s_waitcnt lgkmcnt(0)
	v_mfma_f32_16x16x32_bf16 v[164:167], v[148:151], v[152:155], v[164:167]
	ds_read2_b64 v[148:151], v160 offset0:32 offset1:36
	v_fma_f32 v65, v65, s74, -v137
	v_mul_f32_e32 v62, 0x3fb8aa3b, v62
	s_waitcnt lgkmcnt(0)
	v_mfma_f32_16x16x32_bf16 v[158:161], v[148:151], v[152:155], v[176:179]
	ds_read2_b64 v[148:151], v162 offset0:64 offset1:68
	v_mul_f32_e32 v63, 0x3fb8aa3b, v63
	v_mul_f32_e32 v64, 0x3fb8aa3b, v64
	s_waitcnt lgkmcnt(0)
	v_mfma_f32_16x16x32_bf16 v[176:179], v[148:151], v[152:155], v[180:183]
	ds_read2_b64 v[148:151], v163 offset0:96 offset1:100
	s_nop 1
	global_load_dwordx4 v[180:183], v[6:7], off offset:128
	global_load_dwordx4 v[184:187], v[8:9], off offset:128
	s_waitcnt vmcnt(3)
	ds_write_b128 v75, v[196:199]
	s_waitcnt vmcnt(2)
	ds_write_b128 v75, v[200:203] offset:9216
	s_waitcnt lgkmcnt(2)
	v_mfma_f32_16x16x32_bf16 v[150:153], v[148:151], v[152:155], v[172:175]
	s_waitcnt lgkmcnt(0)
	s_barrier
	s_nop 0
	ds_read2_b64 v[172:175], v157 offset1:4
	v_mul_f32_e32 v65, 0x3fb8aa3b, v65
	v_exp_f32_e32 v148, v62
	v_fma_f32 v62, v66, s74, -v137
	v_exp_f32_e32 v66, v63
	v_fma_f32 v63, v67, s74, -v137
	v_exp_f32_e32 v67, v64
	v_fma_f32 v64, v68, s74, -v137
	v_exp_f32_e32 v68, v65
	v_fma_f32 v65, v69, s74, -v137
	v_mul_f32_e32 v62, 0x3fb8aa3b, v62
	v_mul_f32_e32 v63, 0x3fb8aa3b, v63
	v_mul_f32_e32 v64, 0x3fb8aa3b, v64
	v_mul_f32_e32 v65, 0x3fb8aa3b, v65
	v_exp_f32_e32 v62, v62
	v_exp_f32_e32 v63, v63
	v_exp_f32_e32 v64, v64
	v_exp_f32_e32 v65, v65
	v_cvt_pk_bf16_f32 v188, v148, v66
	v_cvt_pk_bf16_f32 v189, v67, v68
	v_cvt_pk_bf16_f32 v190, v62, v63
	v_cvt_pk_bf16_f32 v191, v64, v65
	v_add_u32_e32 v149, 0x800, v157
	v_add_u32_e32 v155, 0x1800, v157
	s_waitcnt lgkmcnt(0)
	v_mfma_f32_16x16x32_bf16 v[162:165], v[172:175], v[188:191], v[164:167]
	ds_read2_b64 v[172:175], v155 offset0:96 offset1:100
	v_add_u32_e32 v154, 0x1000, v157
	v_fma_f32 v58, v58, s74, -v137
	ds_read2_b64 v[166:169], v149 offset0:32 offset1:36
	s_waitcnt lgkmcnt(0)
	v_mfma_f32_16x16x32_bf16 v[158:161], v[166:169], v[188:191], v[158:161]
	ds_read2_b64 v[166:169], v154 offset0:64 offset1:68
	v_fma_f32 v54, v54, s74, -v137
	v_fma_f32 v59, v59, s74, -v137
	v_mfma_f32_16x16x32_bf16 v[150:153], v[172:175], v[188:191], v[150:153]
	ds_read2_b64 v[172:175], v157 offset0:8 offset1:12
	v_fma_f32 v55, v55, s74, -v137
	v_fma_f32 v60, v60, s74, -v137
	v_fma_f32 v56, v56, s74, -v137
	v_fma_f32 v61, v61, s74, -v137
	v_fma_f32 v57, v57, s74, -v137
	v_mul_f32_e32 v58, 0x3fb8aa3b, v58
	v_mul_f32_e32 v54, 0x3fb8aa3b, v54
	v_mul_f32_e32 v59, 0x3fb8aa3b, v59
	v_mul_f32_e32 v55, 0x3fb8aa3b, v55
	v_mul_f32_e32 v60, 0x3fb8aa3b, v60
	v_mul_f32_e32 v56, 0x3fb8aa3b, v56
	v_mul_f32_e32 v61, 0x3fb8aa3b, v61
	v_mul_f32_e32 v57, 0x3fb8aa3b, v57
	v_exp_f32_e32 v58, v58
	v_exp_f32_e32 v54, v54
	v_exp_f32_e32 v59, v59
	v_exp_f32_e32 v55, v55
	v_exp_f32_e32 v60, v60
	v_exp_f32_e32 v56, v56
	v_exp_f32_e32 v61, v61
	v_exp_f32_e32 v57, v57
	s_waitcnt lgkmcnt(1)
	v_mfma_f32_16x16x32_bf16 v[166:169], v[166:169], v[188:191], v[176:179]
	v_fma_f32 v46, v46, s74, -v137
	v_fma_f32 v47, v47, s74, -v137
	v_fma_f32 v48, v48, s74, -v137
	v_cvt_pk_bf16_f32 v176, v58, v59
	v_cvt_pk_bf16_f32 v177, v60, v61
	v_cvt_pk_bf16_f32 v178, v54, v55
	v_cvt_pk_bf16_f32 v179, v56, v57
	v_mul_f32_e32 v46, 0x3fb8aa3b, v46
	v_mul_f32_e32 v47, 0x3fb8aa3b, v47
	s_waitcnt lgkmcnt(0)
	v_mfma_f32_16x16x32_bf16 v[162:165], v[172:175], v[176:179], v[162:165]
	ds_read2_b64 v[172:175], v149 offset0:40 offset1:44
	v_mul_f32_e32 v48, 0x3fb8aa3b, v48
	v_exp_f32_e32 v69, v46
	s_waitcnt lgkmcnt(0)
	v_mfma_f32_16x16x32_bf16 v[158:161], v[172:175], v[176:179], v[158:161]
	ds_read2_b64 v[172:175], v154 offset0:72 offset1:76
	v_fma_f32 v46, v50, s74, -v137
	v_exp_f32_e32 v50, v47
	s_waitcnt lgkmcnt(0)
	v_mfma_f32_16x16x32_bf16 v[166:169], v[172:175], v[176:179], v[166:169]
	ds_read2_b64 v[172:175], v155 offset0:104 offset1:108
	v_fma_f32 v47, v51, s74, -v137
	v_exp_f32_e32 v51, v48
	v_fma_f32 v48, v52, s74, -v137
	v_add_u32_e32 v52, 0x4800, v157
	global_load_dwordx4 v[188:191], v[6:7], off offset:256
	global_load_dwordx4 v[192:195], v[8:9], off offset:256
	s_waitcnt lgkmcnt(0)
	v_mfma_f32_16x16x32_bf16 v[150:153], v[172:175], v[176:179], v[150:153]
	s_waitcnt vmcnt(3)
	ds_write_b128 v75, v[180:183] offset:18432
	s_waitcnt vmcnt(2)
	ds_write_b128 v75, v[184:187] offset:27648
	s_waitcnt lgkmcnt(0)
	s_barrier
; #define LAS __attribute__((address_space(3)))
; __device__ __forceinline__ unsigned cvt_pk_bf16(float lo, float hi) { const float __attribute__((ext_vector_type(2))) v = {lo, hi}; return __builtin_bit_cast(unsigned, __builtin_convertvector(v, bf16x2_t)); }
; #define NA_STORE(sidx) do { LAS bf16* d_ = buf + ((sidx) & 1) * 9216; _Pragma("unroll") for (int q_ = 0; q_ < 2; ++q_) *(LAS v4u*)(d_ + q_ * 4608 + lrow * 72 + lseg * 8) = ld[(sidx) & 1][q_]; } while (0)
; template <bool LOCAL>
; __device__ __forceinline__ void na_unit(const bf16* P, const bf16* VT, bf16* YCAT, const LAS float* rpb_l, LAS bf16* buf, int b, int gr, int hp, int qblk, int tid) {
;     ...
;             } else {
;                 const int cc = c - NLOC;
; #pragma unroll
;                 for (int p2 = 0; p2 < 2; ++p2) {
;                     float p[8];
; #pragma unroll
;                     for (int e = 0; e < 4; ++e) { p[e] = __expf(sc[4 * (cc >= 0 ? cc : 0) + 2 * p2][e] - m); p[4 + e] = __expf(sc[4 * (cc >= 0 ? cc : 0) + 2 * p2 + 1][e] - m); }
; #pragma unroll
;                     for (int e = 0; e < 8; ++e) lsum += p[e];
;                     const bf16x8 pf = __builtin_bit_cast(bf16x8, (v4u){pg8::cvt_pk_bf16(p[0], p[1]), pg8::cvt_pk_bf16(p[2], p[3]), pg8::cvt_pk_bf16(p[4], p[5]), pg8::cvt_pk_bf16(p[6], p[7])});
; #pragma unroll
;                     for (int dt = 0; dt < 4; ++dt) { const LAS bf16* vp = cb + (16 * dt + fr) * 72 + 32 * p2 + 4 * fq;
;                         o[dt] = __builtin_amdgcn_mfma_f32_16x16x32_bf16(frag44(vp, vp + 16), pf, o[dt], 0, 0, 0); }
;                 }
;             }
;         }
;         if (sidx + 1 < 2 * NCH) NA_STORE(sidx + 1);
;         __syncthreads();
	v_fma_f32 v49, v49, s74, -v137
	ds_read2_b64 v[172:175], v52 offset1:4
	v_mul_f32_e32 v49, 0x3fb8aa3b, v49
	v_exp_f32_e32 v156, v49
	v_fma_f32 v49, v53, s74, -v137
	v_mul_f32_e32 v46, 0x3fb8aa3b, v46
	v_mul_f32_e32 v47, 0x3fb8aa3b, v47
	v_mul_f32_e32 v48, 0x3fb8aa3b, v48
	v_mul_f32_e32 v49, 0x3fb8aa3b, v49
	v_exp_f32_e32 v46, v46
	v_exp_f32_e32 v47, v47
	v_exp_f32_e32 v48, v48
	v_exp_f32_e32 v53, v49
	v_cvt_pk_bf16_f32 v176, v69, v50
	v_cvt_pk_bf16_f32 v177, v51, v156
	v_cvt_pk_bf16_f32 v178, v46, v47
	v_cvt_pk_bf16_f32 v179, v48, v53
	v_add_u32_e32 v180, 0x5000, v157
	v_add_u32_e32 v181, 0x5800, v157
	s_waitcnt lgkmcnt(0)
	v_mfma_f32_16x16x32_bf16 v[162:165], v[172:175], v[176:179], v[162:165]
	ds_read2_b64 v[172:175], v180 offset0:32 offset1:36
	v_add_u32_e32 v49, 0x6000, v157
	v_fma_f32 v38, v38, s74, -v137
	s_waitcnt lgkmcnt(0)
	v_mfma_f32_16x16x32_bf16 v[158:161], v[172:175], v[176:179], v[158:161]
	ds_read2_b64 v[172:175], v181 offset0:64 offset1:68
	v_mul_f32_e32 v38, 0x3fb8aa3b, v38
	v_fma_f32 v42, v42, s74, -v137
	s_waitcnt lgkmcnt(0)
	v_mfma_f32_16x16x32_bf16 v[166:169], v[172:175], v[176:179], v[166:169]
	ds_read2_b64 v[172:175], v49 offset0:96 offset1:100
	v_mul_f32_e32 v42, 0x3fb8aa3b, v42
	v_fma_f32 v30, v30, s74, -v137
	s_waitcnt lgkmcnt(0)
	v_mfma_f32_16x16x32_bf16 v[150:153], v[172:175], v[176:179], v[150:153]
	v_exp_f32_e32 v177, v38
	v_fma_f32 v38, v43, s74, -v137
	v_mul_f32_e32 v38, 0x3fb8aa3b, v38
	v_exp_f32_e32 v178, v38
	v_fma_f32 v38, v39, s74, -v137
	v_mul_f32_e32 v38, 0x3fb8aa3b, v38
	v_exp_f32_e32 v179, v38
	v_fma_f32 v38, v44, s74, -v137
	v_mul_f32_e32 v38, 0x3fb8aa3b, v38
	v_exp_f32_e32 v182, v38
	v_fma_f32 v38, v40, s74, -v137
	v_mul_f32_e32 v38, 0x3fb8aa3b, v38
	v_exp_f32_e32 v176, v42
	v_exp_f32_e32 v183, v38
	v_fma_f32 v38, v45, s74, -v137
	ds_read2_b64 v[42:45], v52 offset0:8 offset1:12
	v_mul_f32_e32 v38, 0x3fb8aa3b, v38
	v_exp_f32_e32 v184, v38
	v_fma_f32 v38, v41, s74, -v137
	v_mul_f32_e32 v38, 0x3fb8aa3b, v38
	v_exp_f32_e32 v185, v38
	v_cvt_pk_bf16_f32 v38, v176, v178
	v_cvt_pk_bf16_f32 v39, v182, v184
	v_cvt_pk_bf16_f32 v40, v177, v179
	v_cvt_pk_bf16_f32 v41, v183, v185
	v_mul_f32_e32 v30, 0x3fb8aa3b, v30
	v_fma_f32 v22, v22, s74, -v137
	s_waitcnt lgkmcnt(0)
	v_mfma_f32_16x16x32_bf16 v[42:45], v[42:45], v[38:41], v[162:165]
	v_mul_f32_e32 v22, 0x3fb8aa3b, v22
	v_fma_f32 v26, v26, s74, -v137
	v_mul_f32_e32 v26, 0x3fb8aa3b, v26
	ds_read2_b64 v[162:165], v180 offset0:40 offset1:44
	s_waitcnt lgkmcnt(0)
	v_mfma_f32_16x16x32_bf16 v[158:161], v[162:165], v[38:41], v[158:161]
	ds_read2_b64 v[162:165], v181 offset0:72 offset1:76
	v_fma_f32 v2, v2, s74, -v137
	v_mul_f32_e32 v2, 0x3fb8aa3b, v2
	s_waitcnt lgkmcnt(0)
	v_mfma_f32_16x16x32_bf16 v[162:165], v[162:165], v[38:41], v[166:169]
	s_nop 2
	ds_read2_b64 v[166:169], v49 offset0:104 offset1:108
	global_load_dwordx4 v[172:175], v[6:7], off offset:384
	s_nop 0
	global_load_dwordx4 v[6:9], v[8:9], off offset:384
	s_waitcnt vmcnt(3)
	ds_write_b128 v75, v[188:191]
	s_waitcnt vmcnt(2)
	ds_write_b128 v75, v[192:195] offset:9216
	s_waitcnt lgkmcnt(2)
	v_mfma_f32_16x16x32_bf16 v[38:41], v[166:169], v[38:41], v[150:153]
	v_exp_f32_e32 v166, v30
	v_fma_f32 v30, v34, s74, -v137
	v_mul_f32_e32 v30, 0x3fb8aa3b, v30
	v_exp_f32_e32 v167, v30
	v_fma_f32 v30, v31, s74, -v137
	v_mul_f32_e32 v30, 0x3fb8aa3b, v30
	v_exp_f32_e32 v168, v30
	v_fma_f32 v30, v35, s74, -v137
	v_mul_f32_e32 v30, 0x3fb8aa3b, v30
	v_exp_f32_e32 v169, v30
	v_fma_f32 v30, v32, s74, -v137
	v_mul_f32_e32 v30, 0x3fb8aa3b, v30
	v_exp_f32_e32 v186, v30
	v_fma_f32 v30, v36, s74, -v137
	v_mul_f32_e32 v30, 0x3fb8aa3b, v30
	v_exp_f32_e32 v187, v30
	v_fma_f32 v30, v33, s74, -v137
	s_waitcnt lgkmcnt(0)
	s_barrier
	v_mul_f32_e32 v34, 0x3fb8aa3b, v30
	ds_read2_b64 v[30:33], v157 offset1:4
	v_exp_f32_e32 v188, v34
	v_fma_f32 v34, v37, s74, -v137
	v_mul_f32_e32 v34, 0x3fb8aa3b, v34
	v_exp_f32_e32 v189, v34
	v_cvt_pk_bf16_f32 v34, v166, v168
	v_cvt_pk_bf16_f32 v35, v186, v188
	v_cvt_pk_bf16_f32 v36, v167, v169
	v_cvt_pk_bf16_f32 v37, v187, v189
	ds_read2_b64 v[150:153], v154 offset0:64 offset1:68
	v_fma_f32 v10, v10, s74, -v137
	s_waitcnt lgkmcnt(1)
	v_mfma_f32_16x16x32_bf16 v[30:33], v[30:33], v[34:37], v[42:45]
	v_mul_f32_e32 v10, 0x3fb8aa3b, v10
	s_nop 1
	ds_read2_b64 v[42:45], v149 offset0:32 offset1:36
	s_waitcnt lgkmcnt(0)
	v_mfma_f32_16x16x32_bf16 v[42:45], v[42:45], v[34:37], v[158:161]
	s_nop 2
	ds_read2_b64 v[158:161], v155 offset0:96 offset1:100
	v_mfma_f32_16x16x32_bf16 v[150:153], v[150:153], v[34:37], v[162:165]
	s_waitcnt lgkmcnt(0)
	v_mfma_f32_16x16x32_bf16 v[34:37], v[158:161], v[34:37], v[38:41]
	v_exp_f32_e32 v159, v22
	v_fma_f32 v22, v27, s74, -v137
	v_mul_f32_e32 v22, 0x3fb8aa3b, v22
	v_exp_f32_e32 v160, v22
	v_fma_f32 v22, v23, s74, -v137
	v_mul_f32_e32 v22, 0x3fb8aa3b, v22
	v_exp_f32_e32 v161, v22
	v_fma_f32 v22, v28, s74, -v137
	v_mul_f32_e32 v22, 0x3fb8aa3b, v22
	v_exp_f32_e32 v162, v22
	v_fma_f32 v22, v24, s74, -v137
	v_mul_f32_e32 v22, 0x3fb8aa3b, v22
	v_exp_f32_e32 v158, v26
	v_exp_f32_e32 v163, v22
	v_fma_f32 v22, v29, s74, -v137
	ds_read2_b64 v[26:29], v157 offset0:8 offset1:12
	v_mul_f32_e32 v22, 0x3fb8aa3b, v22
	v_exp_f32_e32 v157, v22
	v_fma_f32 v22, v25, s74, -v137
	v_mul_f32_e32 v22, 0x3fb8aa3b, v22
	v_exp_f32_e32 v164, v22
	v_cvt_pk_bf16_f32 v22, v158, v160
	v_cvt_pk_bf16_f32 v23, v162, v157
	v_cvt_pk_bf16_f32 v24, v159, v161
	v_cvt_pk_bf16_f32 v25, v163, v164
	ds_read2_b64 v[38:41], v154 offset0:72 offset1:76
	s_waitcnt lgkmcnt(1)
	v_mfma_f32_16x16x32_bf16 v[26:29], v[26:29], v[22:25], v[30:33]
	s_nop 2
	ds_read2_b64 v[30:33], v149 offset0:40 offset1:44
	s_waitcnt lgkmcnt(0)
	v_mfma_f32_16x16x32_bf16 v[30:33], v[30:33], v[22:25], v[42:45]
	s_nop 2
	ds_read2_b64 v[42:45], v155 offset0:104 offset1:108
	s_waitcnt vmcnt(1)
	ds_write_b128 v75, v[172:175] offset:18432
	s_waitcnt vmcnt(0)
	ds_write_b128 v75, v[6:9] offset:27648
	v_fma_f32 v6, v14, s74, -v137
	v_mul_f32_e32 v6, 0x3fb8aa3b, v6
	v_mfma_f32_16x16x32_bf16 v[38:41], v[38:41], v[22:25], v[150:153]
	s_waitcnt lgkmcnt(0)
	s_barrier
; #define LAS __attribute__((address_space(3)))
; __device__ __forceinline__ unsigned cvt_pk_bf16(float lo, float hi) { const float __attribute__((ext_vector_type(2))) v = {lo, hi}; return __builtin_bit_cast(unsigned, __builtin_convertvector(v, bf16x2_t)); }
; #define NA_STORE(sidx) do { LAS bf16* d_ = buf + ((sidx) & 1) * 9216; _Pragma("unroll") for (int q_ = 0; q_ < 2; ++q_) *(LAS v4u*)(d_ + q_ * 4608 + lrow * 72 + lseg * 8) = ld[(sidx) & 1][q_]; } while (0)
; template <bool LOCAL>
; __device__ __forceinline__ void na_unit(const bf16* P, const bf16* VT, bf16* YCAT, const LAS float* rpb_l, LAS bf16* buf, int b, int gr, int hp, int qblk, int tid) {
;     ...
;             } else {
;                 const int cc = c - NLOC;
; #pragma unroll
;                 for (int p2 = 0; p2 < 2; ++p2) {
;                     float p[8];
; #pragma unroll
;                     for (int e = 0; e < 4; ++e) { p[e] = __expf(sc[4 * (cc >= 0 ? cc : 0) + 2 * p2][e] - m); p[4 + e] = __expf(sc[4 * (cc >= 0 ? cc : 0) + 2 * p2 + 1][e] - m); }
; #pragma unroll
;                     for (int e = 0; e < 8; ++e) lsum += p[e];
;                     const bf16x8 pf = __builtin_bit_cast(bf16x8, (v4u){pg8::cvt_pk_bf16(p[0], p[1]), pg8::cvt_pk_bf16(p[2], p[3]), pg8::cvt_pk_bf16(p[4], p[5]), pg8::cvt_pk_bf16(p[6], p[7])});
; #pragma unroll
;                     for (int dt = 0; dt < 4; ++dt) { const LAS bf16* vp = cb + (16 * dt + fr) * 72 + 32 * p2 + 4 * fq;
;                         o[dt] = __builtin_amdgcn_mfma_f32_16x16x32_bf16(frag44(vp, vp + 16), pf, o[dt], 0, 0, 0); }
;                 }
;             }
;         }
;         if (sidx + 1 < 2 * NCH) NA_STORE(sidx + 1);
;         __syncthreads();
;     }
;     ...
;     lsum += __shfl_xor(lsum, 16); lsum += __shfl_xor(lsum, 32);
	v_mfma_f32_16x16x32_bf16 v[22:25], v[42:45], v[22:25], v[34:37]
	v_ashrrev_i32_e32 v75, 31, v74
	s_nop 1
	v_exp_f32_e32 v34, v6
	v_fma_f32 v6, v18, s74, -v137
	v_mul_f32_e32 v6, 0x3fb8aa3b, v6
	v_exp_f32_e32 v35, v6
	v_fma_f32 v6, v15, s74, -v137
	v_mul_f32_e32 v6, 0x3fb8aa3b, v6
	v_exp_f32_e32 v36, v6
	v_fma_f32 v6, v19, s74, -v137
	v_mul_f32_e32 v6, 0x3fb8aa3b, v6
	v_exp_f32_e32 v37, v6
	v_fma_f32 v6, v16, s74, -v137
	v_mul_f32_e32 v6, 0x3fb8aa3b, v6
	v_exp_f32_e32 v42, v6
	v_fma_f32 v6, v20, s74, -v137
	v_mul_f32_e32 v6, 0x3fb8aa3b, v6
	v_exp_f32_e32 v43, v6
	v_fma_f32 v6, v17, s74, -v137
	v_mul_f32_e32 v14, 0x3fb8aa3b, v6
	ds_read2_b64 v[6:9], v52 offset1:4
	v_exp_f32_e32 v44, v14
	v_fma_f32 v14, v21, s74, -v137
	v_mul_f32_e32 v14, 0x3fb8aa3b, v14
	v_exp_f32_e32 v45, v14
	v_cvt_pk_bf16_f32 v14, v34, v36
	v_cvt_pk_bf16_f32 v15, v42, v44
	v_cvt_pk_bf16_f32 v16, v35, v37
	v_cvt_pk_bf16_f32 v17, v43, v45
	ds_read2_b64 v[18:21], v180 offset0:32 offset1:36
	s_waitcnt lgkmcnt(1)
	v_mfma_f32_16x16x32_bf16 v[6:9], v[6:9], v[14:17], v[26:29]
	s_nop 2
	ds_read2_b64 v[26:29], v181 offset0:64 offset1:68
	s_waitcnt lgkmcnt(0)
	v_mfma_f32_16x16x32_bf16 v[26:29], v[26:29], v[14:17], v[38:41]
	s_nop 2
	v_add_f32_e32 v38, 0, v133
	v_add_f32_e32 v38, v97, v38
	v_add_f32_e32 v38, v96, v38
	v_add_f32_e32 v38, v100, v38
	v_add_f32_e32 v38, v93, v38
	v_add_f32_e32 v38, v92, v38
	v_add_f32_e32 v38, v95, v38
	v_add_f32_e32 v38, v94, v38
	v_add_f32_e32 v38, v87, v38
	v_add_f32_e32 v38, v91, v38
	v_add_f32_e32 v38, v99, v38
	v_add_f32_e32 v38, v101, v38
	v_add_f32_e32 v38, v76, v38
	v_add_f32_e32 v38, v88, v38
	v_add_f32_e32 v38, v98, v38
	v_add_f32_e32 v38, v102, v38
	v_add_f32_e32 v38, v104, v38
	v_add_f32_e32 v38, v106, v38
	v_add_f32_e32 v38, v108, v38
	v_add_f32_e32 v38, v109, v38
	v_add_f32_e32 v38, v103, v38
	v_add_f32_e32 v38, v105, v38
	v_add_f32_e32 v38, v107, v38
	v_add_f32_e32 v38, v110, v38
	v_add_f32_e32 v38, v112, v38
	v_add_f32_e32 v38, v114, v38
	v_add_f32_e32 v38, v116, v38
	v_add_f32_e32 v38, v117, v38
	v_add_f32_e32 v38, v111, v38
	v_add_f32_e32 v38, v113, v38
	v_add_f32_e32 v38, v115, v38
	v_add_f32_e32 v38, v118, v38
	v_add_f32_e32 v38, v120, v38
	v_add_f32_e32 v38, v122, v38
	v_add_f32_e32 v38, v124, v38
	v_add_f32_e32 v38, v125, v38
	v_add_f32_e32 v38, v119, v38
	v_add_f32_e32 v38, v121, v38
	v_add_f32_e32 v38, v123, v38
	v_add_f32_e32 v38, v126, v38
	v_add_f32_e32 v38, v128, v38
	v_add_f32_e32 v38, v130, v38
	v_add_f32_e32 v38, v132, v38
	v_add_f32_e32 v38, v134, v38
	v_add_f32_e32 v38, v127, v38
	v_add_f32_e32 v38, v129, v38
	v_add_f32_e32 v38, v131, v38
	v_add_f32_e32 v38, v135, v38
	v_add_f32_e32 v38, v138, v38
	v_add_f32_e32 v38, v140, v38
	v_add_f32_e32 v38, v142, v38
	v_add_f32_e32 v38, v143, v38
	v_add_f32_e32 v38, v136, v38
	v_add_f32_e32 v38, v139, v38
	v_add_f32_e32 v38, v141, v38
	v_add_f32_e32 v38, v144, v38
	v_add_f32_e32 v38, v78, v38
	v_add_f32_e32 v38, v80, v38
	v_add_f32_e32 v38, v145, v38
	v_add_f32_e32 v38, v147, v38
	v_add_f32_e32 v38, v70, v38
	v_add_f32_e32 v38, v79, v38
	v_add_f32_e32 v38, v81, v38
	v_add_f32_e32 v38, v146, v38
	v_add_f32_e32 v38, v148, v38
	v_add_f32_e32 v38, v66, v38
	v_add_f32_e32 v38, v67, v38
	v_add_f32_e32 v38, v68, v38
	v_add_f32_e32 v38, v62, v38
	v_add_f32_e32 v38, v63, v38
	v_add_f32_e32 v38, v64, v38
	v_add_f32_e32 v38, v65, v38
	v_add_f32_e32 v38, v58, v38
	v_add_f32_e32 v38, v59, v38
	v_add_f32_e32 v38, v60, v38
	v_add_f32_e32 v38, v61, v38
	v_add_f32_e32 v38, v54, v38
	v_add_f32_e32 v38, v55, v38
	v_add_f32_e32 v38, v56, v38
	v_add_f32_e32 v38, v57, v38
	v_add_f32_e32 v38, v69, v38
	v_add_f32_e32 v38, v50, v38
	v_add_f32_e32 v38, v51, v38
	v_add_f32_e32 v38, v156, v38
	v_add_f32_e32 v38, v46, v38
	v_add_f32_e32 v38, v47, v38
	v_add_f32_e32 v38, v48, v38
	v_add_f32_e32 v38, v53, v38
	v_add_f32_e32 v38, v176, v38
	v_mfma_f32_16x16x32_bf16 v[18:21], v[18:21], v[14:17], v[30:33]
	v_add_f32_e32 v38, v178, v38
	v_add_f32_e32 v38, v182, v38
	v_add_f32_e32 v38, v184, v38
	ds_read2_b64 v[30:33], v49 offset0:96 offset1:100
	v_add_f32_e32 v38, v177, v38
	v_add_f32_e32 v38, v179, v38
	v_add_f32_e32 v38, v183, v38
	v_add_f32_e32 v38, v185, v38
	v_add_f32_e32 v38, v166, v38
	v_add_f32_e32 v38, v168, v38
	s_waitcnt lgkmcnt(0)
	v_mfma_f32_16x16x32_bf16 v[14:17], v[30:33], v[14:17], v[22:25]
	v_add_f32_e32 v38, v186, v38
	s_nop 1
	v_exp_f32_e32 v23, v2
	v_fma_f32 v2, v11, s74, -v137
	v_mul_f32_e32 v2, 0x3fb8aa3b, v2
	v_add_f32_e32 v38, v188, v38
	v_exp_f32_e32 v24, v2
	v_fma_f32 v2, v3, s74, -v137
	v_add_f32_e32 v38, v167, v38
	v_mul_f32_e32 v2, 0x3fb8aa3b, v2
	v_add_f32_e32 v38, v169, v38
	v_exp_f32_e32 v25, v2
	v_fma_f32 v2, v12, s74, -v137
	v_add_f32_e32 v38, v187, v38
	v_mul_f32_e32 v2, 0x3fb8aa3b, v2
	v_add_f32_e32 v38, v189, v38
	v_exp_f32_e32 v30, v2
	v_fma_f32 v2, v4, s74, -v137
	v_add_f32_e32 v38, v158, v38
	v_mul_f32_e32 v2, 0x3fb8aa3b, v2
	v_add_f32_e32 v38, v160, v38
	v_exp_f32_e32 v22, v10
	v_exp_f32_e32 v31, v2
	v_fma_f32 v2, v13, s74, -v137
	ds_read2_b64 v[10:13], v52 offset0:8 offset1:12
	v_add_f32_e32 v38, v162, v38
	v_mul_f32_e32 v2, 0x3fb8aa3b, v2
	v_add_f32_e32 v38, v157, v38
	v_exp_f32_e32 v32, v2
	v_fma_f32 v2, v5, s74, -v137
	v_add_f32_e32 v38, v159, v38
	v_mul_f32_e32 v2, 0x3fb8aa3b, v2
	v_add_f32_e32 v38, v161, v38
	v_exp_f32_e32 v33, v2
	v_add_f32_e32 v38, v163, v38
	v_add_f32_e32 v38, v164, v38
	v_add_f32_e32 v34, v34, v38
	v_add_f32_e32 v34, v36, v34
	v_cvt_pk_bf16_f32 v2, v22, v24
	v_cvt_pk_bf16_f32 v3, v30, v32
	v_cvt_pk_bf16_f32 v4, v23, v25
	v_cvt_pk_bf16_f32 v5, v31, v33
	v_add_f32_e32 v34, v42, v34
	v_add_f32_e32 v34, v44, v34
	s_waitcnt lgkmcnt(0)
	v_mfma_f32_16x16x32_bf16 v[6:9], v[10:13], v[2:5], v[6:9]
	ds_read2_b64 v[10:13], v180 offset0:40 offset1:44
	v_add_f32_e32 v34, v35, v34
	v_add_f32_e32 v34, v37, v34
	v_add_f32_e32 v34, v43, v34
	v_add_f32_e32 v34, v45, v34
	v_add_f32_e32 v22, v22, v34
	v_add_f32_e32 v22, v24, v22
	v_add_f32_e32 v22, v30, v22
	v_add_f32_e32 v22, v32, v22
	s_waitcnt lgkmcnt(0)
	v_mfma_f32_16x16x32_bf16 v[10:13], v[10:13], v[2:5], v[18:21]
	v_add_f32_e32 v22, v23, v22
	v_add_f32_e32 v22, v25, v22
	v_add_f32_e32 v22, v31, v22
	ds_read2_b64 v[18:21], v181 offset0:72 offset1:76
	v_add_f32_e32 v30, v33, v22
	ds_bpermute_b32 v31, v89, v30
	ds_read2_b64 v[22:25], v49 offset0:104 offset1:108
	s_waitcnt lgkmcnt(2)
	v_mfma_f32_16x16x32_bf16 v[18:21], v[18:21], v[2:5], v[26:29]
	s_waitcnt lgkmcnt(1)
	s_nop 1
	v_add_f32_e32 v26, v30, v31
	ds_bpermute_b32 v27, v90, v26
	v_lshlrev_b32_e32 v70, 1, v77
	s_waitcnt lgkmcnt(1)
	v_mfma_f32_16x16x32_bf16 v[14:17], v[22:25], v[2:5], v[14:17]
	s_waitcnt lgkmcnt(0)
	s_barrier
; __device__ __forceinline__ unsigned cvt_pk_bf16(float lo, float hi) { const float __attribute__((ext_vector_type(2))) v = {lo, hi}; return __builtin_bit_cast(unsigned, __builtin_convertvector(v, bf16x2_t)); }
; template <bool LOCAL>
; __device__ __forceinline__ void na_unit(const bf16* P, const bf16* VT, bf16* YCAT, const LAS float* rpb_l, LAS bf16* buf, int b, int gr, int hp, int qblk, int tid) {
;     ...
;     lsum += __shfl_xor(lsum, 16); lsum += __shfl_xor(lsum, 32);
;     const float inv = 1.f / lsum;
;     bf16* op = YCAT + (size_t)(qrow0 + fr) * D + 512 + h * 64 + 4 * fq;
; #pragma unroll
;     for (int dt = 0; dt < 4; ++dt) { v2u w; w.x = pg8::cvt_pk_bf16(o[dt][0] * inv, o[dt][1] * inv); w.y = pg8::cvt_pk_bf16(o[dt][2] * inv, o[dt][3] * inv); *(v2u*)(op + dt * 16) = w; }
	v_add_f32_e32 v2, v26, v27
	v_div_scale_f32 v3, s[0:1], v2, v2, 1.0
	v_rcp_f32_e32 v4, v3
	s_nop 0
	v_fma_f32 v5, -v3, v4, 1.0
	v_fmac_f32_e32 v4, v5, v4
	v_div_scale_f32 v5, vcc, 1.0, v2, 1.0
	v_mul_f32_e32 v22, v5, v4
	v_fma_f32 v23, -v3, v22, v5
	v_fmac_f32_e32 v22, v23, v4
	v_fma_f32 v3, -v3, v22, v5
	v_div_fmas_f32 v3, v3, v4, v22
	v_div_fixup_f32 v22, v3, v2, 1.0
	v_lshlrev_b64 v[2:3], 11, v[74:75]
	v_lshl_add_u64 v[2:3], s[10:11], 0, v[2:3]
	v_lshl_add_u64 v[2:3], v[72:73], 1, v[2:3]
	v_pk_mul_f32 v[6:7], v[6:7], v[22:23] op_sel_hi:[1,0]
	v_pk_mul_f32 v[8:9], v[8:9], v[22:23] op_sel_hi:[1,0]
	v_lshl_add_u64 v[4:5], v[2:3], 0, v[70:71]
	v_cvt_pk_bf16_f32 v6, v6, v7
	v_cvt_pk_bf16_f32 v7, v8, v9
	global_store_dwordx2 v[4:5], v[6:7], off offset:1024
	v_pk_mul_f32 v[6:7], v[10:11], v[22:23] op_sel_hi:[1,0]
	v_pk_mul_f32 v[8:9], v[12:13], v[22:23] op_sel_hi:[1,0]
	v_cvt_pk_bf16_f32 v6, v6, v7
	v_cvt_pk_bf16_f32 v7, v8, v9
	global_store_dwordx2 v[4:5], v[6:7], off offset:1056
	v_pk_mul_f32 v[6:7], v[18:19], v[22:23] op_sel_hi:[1,0]
	v_pk_mul_f32 v[8:9], v[20:21], v[22:23] op_sel_hi:[1,0]
	v_cvt_pk_bf16_f32 v6, v6, v7
	v_cvt_pk_bf16_f32 v7, v8, v9
	v_lshl_add_u64 v[2:3], v[4:5], 0, s[12:13]
	global_store_dwordx2 v[4:5], v[6:7], off offset:1088
	v_pk_mul_f32 v[4:5], v[14:15], v[22:23] op_sel_hi:[1,0]
	v_pk_mul_f32 v[6:7], v[16:17], v[22:23] op_sel_hi:[1,0]
	v_cvt_pk_bf16_f32 v4, v4, v5

; #define LAS __attribute__((address_space(3)))
; template <bool LOCAL>
; __device__ __forceinline__ void na_unit(const bf16* P, const bf16* VT, bf16* YCAT, const LAS float* rpb_l, LAS bf16* buf, int b, int gr, int hp, int qblk, int tid) {
;     ...
;     const int lane = tid & 63, wv = tid >> 6, fr = lane & 15, fq = lane >> 4, hh = wv >> 2, qb = wv & 3, h = 2 * hp + hh;
;     const int qrow0 = LOCAL ? NCTX + b * SEQ + gr * 64 + 16 * qb : b * CTXL + qblk * 64 + 16 * qb;
;     const int r0 = min(max(gr - 4, 0), 24);
;     const int kc0 = qb == 0 ? 0 : qb == 1 ? 8 : qb == 2 ? 24 : 32;
;     const int qcol = 16 * qb + fr, cs = min(max(qcol - 8, 0), 48);
;     const LAS float* rpb = rpb_l + h * 15 * 31;
;     v4u ld[2][2];
;     const int lrow = (tid >> 3) & 63, lseg = tid & 7;
;     ...
;     bf16x8 qf[2];
; #pragma unroll
;     for (int ks = 0; ks < 2; ++ks) qf[ks] = *(const bf16x8*)(P + (size_t)(qrow0 + fr) * DINP + h * 64 + 32 * ks + 8 * fq);
;     f32x4 sl[16], sc[16];
;     float m = -1.0e30f, lsum = 0.f;
;     f32x4 o[4];
; #pragma unroll
;     for (int dt = 0; dt < 4; ++dt) o[dt] = (f32x4){0.f, 0.f, 0.f, 0.f};
;     NA_ISSUE(0); NA_ISSUE(1); NA_STORE(0);
;     __syncthreads();
; #pragma unroll
;     for (int sidx = 0; sidx < 2 * NCH; ++sidx) {
;         if (sidx + 2 < 2 * NCH) NA_ISSUE(sidx + 2);
;         const LAS bf16* cb = buf + (sidx & 1) * 9216 + hh * 4608;
;         if (sidx < NCH) {
;             const int c = sidx;
;             if (LOCAL && c < 8) {
; #pragma unroll
;                 for (int t2 = 0; t2 < 2; ++t2) {
;                     const LAS bf16* kp = cb + (kc0 + 16 * t2 + fr) * 72 + 8 * fq;
;                     f32x4 acc = {0.f, 0.f, 0.f, 0.f};
;                     acc = __builtin_amdgcn_mfma_f32_16x16x32_bf16(*(const LAS bf16x8*)(kp), qf[0], acc, 0, 0, 0);
;                     acc = __builtin_amdgcn_mfma_f32_16x16x32_bf16(*(const LAS bf16x8*)(kp + 32), qf[1], acc, 0, 0, 0);
;                     const LAS float* rb = rpb + (r0 + c - gr + 7) * 31 + 15 - qcol;
; #pragma unroll
;                     for (int e = 0; e < 4; ++e) { const int kcol = kc0 + 16 * t2 + 4 * fq + e; const bool ok = (kcol >= cs) && (kcol < cs + 16);
;                         const float sv = ok ? acc[e] * 0.125f + rb[ok ? kcol : qcol] : -1.0e30f; acc[e] = sv; m = fmaxf(m, sv); }
;                     sl[2 * (c < 8 ? c : 0) + t2] = acc; }
.LBB0_2898:
	s_or_b64 exec, exec, s[0:1]
	s_bfe_u32 s19, s80, 0x50002
	v_sub_u32_e64 v3, s19, 4 clamp
	s_ashr_i32 s17, s80, 7
	v_readfirstlane_b32 s0, v3
	s_lshl_b32 s26, s17, 11
	s_min_u32 s20, s0, 24
	s_add_i32 s14, s26, 0x1000
	s_lshl_b32 s15, s20, 6
	s_or_b32 s16, s15, s14
	v_mov_b64_e32 v[18:19], s[8:9]
	v_and_b32_e32 v32, 7, v93
	v_or_b32_e32 v3, s16, v88
	s_and_b32 s18, s80, 3
	v_mad_i64_i32 v[4:5], s[0:1], v3, s72, v[18:19]
	v_lshlrev_b32_e32 v26, 4, v32
	v_mov_b32_e32 v27, v71
	v_lshl_add_u64 v[4:5], v[4:5], 0, v[26:27]
	s_lshl_b32 s2, s18, 8
	v_lshl_add_u64 v[4:5], v[4:5], 0, s[2:3]
	global_load_dwordx4 v[10:13], v[4:5], off offset:1024
	global_load_dwordx4 v[14:17], v[4:5], off offset:1152
	s_lshl_b32 s0, s19, 6
	v_lshl_or_b32 v31, v2, 4, v89
	v_lshl_add_u32 v33, s18, 1, v92
	s_or_b32 s0, s14, s0
	v_mad_u32_u24 v2, v88, s73, 0
	v_lshlrev_b32_e32 v72, 6, v33
	s_add_i32 s50, s26, 0x1040
	v_or_b32_e32 v74, s0, v31
	v_add_u32_e32 v75, v2, v26
	v_ashrrev_i32_e32 v73, 31, v72
	v_or_b32_e32 v4, s50, v88
	v_mad_i64_i32 v[2:3], s[0:1], v74, s72, v[18:19]
	v_add_u32_e32 v4, s15, v4
	v_lshl_add_u64 v[2:3], v[72:73], 1, v[2:3]
	v_mad_i64_i32 v[4:5], s[0:1], v4, s72, v[18:19]
	v_lshl_add_u64 v[2:3], v[2:3], 0, v[70:71]
	v_lshl_add_u64 v[20:21], v[4:5], 0, v[26:27]
	global_load_dwordx4 v[6:9], v[2:3], off
	s_nop 0
	global_load_dwordx4 v[2:5], v[2:3], off offset:64
	s_or_b32 s14, s26, s15
	s_addk_i32 s14, 0x1080
	v_or_b32_e32 v24, s14, v88
	v_mad_i64_i32 v[28:29], s[0:1], v24, s72, v[18:19]
	v_lshl_add_u64 v[26:27], v[28:29], 0, v[26:27]
	v_lshl_add_u64 v[22:23], v[20:21], 0, s[2:3]
	v_lshl_add_u64 v[26:27], v[26:27], 0, s[2:3]
	global_load_dwordx4 v[18:21], v[22:23], off offset:1024
	s_nop 0
	global_load_dwordx4 v[22:25], v[22:23], off offset:1152
	v_add_u32_e32 v30, v86, v70
	v_add_u32_e32 v34, v90, v89
	v_mad_u32_u24 v36, v34, s73, v30
	s_movk_i32 s0, 0x744
	v_mul_lo_u32 v33, v33, s0
	s_sub_i32 s0, s20, s19
	s_mulk_i32 s0, 0x7c
	v_sub_u32_e64 v35, v31, 8 clamp
	s_add_i32 s0, s0, 0
	v_min_u32_e32 v35, 48, v35
	v_lshlrev_b32_e32 v77, 2, v91
	v_add_u32_e32 v33, s0, v33
	v_lshlrev_b32_e32 v31, 2, v31
	v_sub_u32_e32 v31, v33, v31
	v_add_u32_e32 v33, v90, v77
	v_cmp_ge_u32_e32 vcc, v33, v35
	v_mov_b32_e32 v91, 0xf149f2ca
	v_lshl_add_u32 v31, v33, 2, v31
	v_mov_b32_e32 v92, 0xf149f2ca
	s_waitcnt vmcnt(5)
	ds_write_b128 v75, v[10:13]
	s_waitcnt vmcnt(4)
	ds_write_b128 v75, v[14:17] offset:9216
	s_waitcnt lgkmcnt(0)
	s_barrier
	ds_read_b32 v240, v31 offset:37792
	ds_read_b32 v241, v31 offset:37796
	ds_read_b32 v242, v31 offset:37800
	ds_read_b32 v243, v31 offset:37804
	ds_read_b32 v244, v31 offset:37856
	ds_read_b32 v245, v31 offset:37860
	ds_read_b32 v246, v31 offset:37864
	ds_read_b32 v247, v31 offset:37868
	global_load_dwordx4 v[10:13], v[26:27], off offset:1024
	global_load_dwordx4 v[14:17], v[26:27], off offset:1152
	ds_read_b128 v[26:29], v36
	ds_read_b128 v[38:41], v36 offset:64
	s_waitcnt vmcnt(5) lgkmcnt(1)
	v_mfma_f32_16x16x32_bf16 v[26:29], v[26:29], v[6:9], 0
	v_add_u32_e32 v36, 16, v35
	v_cmp_lt_u32_e64 s[0:1], v33, v36
	s_and_b64 s[28:29], vcc, s[0:1]
	s_waitcnt vmcnt(4) lgkmcnt(0)
	v_mfma_f32_16x16x32_bf16 v[26:29], v[38:41], v[2:5], v[26:29]
	s_nop 2
	s_waitcnt lgkmcnt(0)
	s_nop 3
	v_fmac_f32_e32 v240, 0x3e000000, v26
	v_cndmask_b32_e64 v92, v92, v240, s[28:29]
	s_nop 4
	v_or_b32_e32 v26, 1, v33
	v_cmp_ge_u32_e32 vcc, v26, v35
	v_cmp_lt_u32_e64 s[0:1], v26, v36
	s_and_b64 s[30:31], vcc, s[0:1]
	s_nop 2
	s_waitcnt lgkmcnt(0)
	v_fmac_f32_e32 v241, 0x3e000000, v27
	v_cndmask_b32_e64 v91, v91, v241, s[30:31]
	v_or_b32_e32 v26, 2, v33
	v_cmp_ge_u32_e32 vcc, v26, v35
	v_cmp_lt_u32_e64 s[0:1], v26, v36
	s_and_b64 s[34:35], vcc, s[0:1]
	v_mov_b32_e32 v93, 0xf149f2ca
	v_mov_b32_e32 v94, 0xf149f2ca
	s_nop 2
	s_waitcnt lgkmcnt(0)
	v_fmac_f32_e32 v242, 0x3e000000, v28
	v_cndmask_b32_e64 v94, v94, v242, s[34:35]
	v_or_b32_e32 v26, 3, v33
	v_cmp_ge_u32_e32 vcc, v26, v35
	v_cmp_lt_u32_e64 s[0:1], v26, v36
	s_and_b64 s[36:37], vcc, s[0:1]
	s_nop 2
	s_waitcnt lgkmcnt(0)
	v_fmac_f32_e32 v243, 0x3e000000, v29
	v_cndmask_b32_e64 v93, v93, v243, s[36:37]
	v_add_u32_e32 v37, 16, v90
	v_add_u32_e32 v33, v37, v89
	v_mad_u32_u24 v38, v33, s73, v30
	ds_read_b128 v[26:29], v38
	ds_read_b128 v[38:41], v38 offset:64
	v_add_u32_e32 v37, v37, v77
	v_cmp_ge_u32_e32 vcc, v37, v35
	v_cmp_lt_u32_e64 s[0:1], v37, v36
	s_waitcnt lgkmcnt(1)
	v_mfma_f32_16x16x32_bf16 v[26:29], v[26:29], v[6:9], 0
	s_and_b64 s[38:39], vcc, s[0:1]
	v_mov_b32_e32 v95, 0xf149f2ca
	v_mov_b32_e32 v96, 0xf149f2ca
	s_waitcnt lgkmcnt(0)
	v_mfma_f32_16x16x32_bf16 v[26:29], v[38:41], v[2:5], v[26:29]
	s_nop 2
	s_waitcnt lgkmcnt(0)
	s_nop 3
	v_fmac_f32_e32 v244, 0x3e000000, v26
	v_cndmask_b32_e64 v96, v96, v244, s[38:39]
	s_nop 4
	v_or_b32_e32 v26, 1, v37
	v_cmp_ge_u32_e32 vcc, v26, v35
	v_cmp_lt_u32_e64 s[0:1], v26, v36
	s_and_b64 s[44:45], vcc, s[0:1]
	s_nop 2
	s_waitcnt lgkmcnt(0)
	v_fmac_f32_e32 v245, 0x3e000000, v27
	v_cndmask_b32_e64 v95, v95, v245, s[44:45]
	v_or_b32_e32 v26, 2, v37
	v_cmp_ge_u32_e32 vcc, v26, v35
	v_cmp_lt_u32_e64 s[0:1], v26, v36
	s_and_b64 s[46:47], vcc, s[0:1]
	v_mov_b32_e32 v97, 0xf149f2ca
	v_mov_b32_e32 v99, 0xf149f2ca
	s_nop 2
	s_waitcnt lgkmcnt(0)
	v_fmac_f32_e32 v246, 0x3e000000, v28
	v_cndmask_b32_e64 v99, v99, v246, s[46:47]
	v_or_b32_e32 v26, 3, v37
	v_cmp_ge_u32_e32 vcc, v26, v35
	v_cmp_lt_u32_e64 s[0:1], v26, v36
	s_and_b64 s[66:67], vcc, s[0:1]
	s_nop 2
	s_waitcnt lgkmcnt(0)
	v_fmac_f32_e32 v247, 0x3e000000, v29
	v_cndmask_b32_e64 v97, v97, v247, s[66:67]
	v_mul_u32_u24_e32 v27, 0x90, v34
	v_lshlrev_b32_e32 v26, 3, v32
	v_add_u32_e32 v32, v30, v27
	s_waitcnt vmcnt(3)
	ds_write_b128 v75, v[18:21] offset:18432
	s_waitcnt vmcnt(2)
	ds_write_b128 v75, v[22:25] offset:27648
	s_waitcnt lgkmcnt(0)
	s_barrier
; #define LAS __attribute__((address_space(3)))
; #define NA_STORE(sidx) do { LAS bf16* d_ = buf + ((sidx) & 1) * 9216; _Pragma("unroll") for (int q_ = 0; q_ < 2; ++q_) *(LAS v4u*)(d_ + q_ * 4608 + lrow * 72 + lseg * 8) = ld[(sidx) & 1][q_]; } while (0)
; template <bool LOCAL>
; __device__ __forceinline__ void na_unit(const bf16* P, const bf16* VT, bf16* YCAT, const LAS float* rpb_l, LAS bf16* buf, int b, int gr, int hp, int qblk, int tid) {
;     ...
;         if (sidx + 2 < 2 * NCH) NA_ISSUE(sidx + 2);
;         const LAS bf16* cb = buf + (sidx & 1) * 9216 + hh * 4608;
;         if (sidx < NCH) {
;             const int c = sidx;
;             if (LOCAL && c < 8) {
; #pragma unroll
;                 for (int t2 = 0; t2 < 2; ++t2) {
;                     const LAS bf16* kp = cb + (kc0 + 16 * t2 + fr) * 72 + 8 * fq;
;                     f32x4 acc = {0.f, 0.f, 0.f, 0.f};
;                     acc = __builtin_amdgcn_mfma_f32_16x16x32_bf16(*(const LAS bf16x8*)(kp), qf[0], acc, 0, 0, 0);
;                     acc = __builtin_amdgcn_mfma_f32_16x16x32_bf16(*(const LAS bf16x8*)(kp + 32), qf[1], acc, 0, 0, 0);
;                     const LAS float* rb = rpb + (r0 + c - gr + 7) * 31 + 15 - qcol;
; #pragma unroll
;                     for (int e = 0; e < 4; ++e) { const int kcol = kc0 + 16 * t2 + 4 * fq + e; const bool ok = (kcol >= cs) && (kcol < cs + 16);
;                         const float sv = ok ? acc[e] * 0.125f + rb[ok ? kcol : qcol] : -1.0e30f; acc[e] = sv; m = fmaxf(m, sv); }
;                     sl[2 * (c < 8 ? c : 0) + t2] = acc; }
;     ...
;         if (sidx + 1 < 2 * NCH) NA_STORE(sidx + 1);
;         __syncthreads();
	ds_read_b32 v240, v31 offset:37916
	ds_read_b32 v241, v31 offset:37920
	ds_read_b32 v242, v31 offset:37924
	ds_read_b32 v243, v31 offset:37928
	ds_read_b32 v244, v31 offset:37980
	ds_read_b32 v245, v31 offset:37984
	ds_read_b32 v246, v31 offset:37988
	ds_read_b32 v247, v31 offset:37992
	ds_read_b128 v[18:21], v32 offset:18432
	s_add_i32 s26, s26, s15
	s_add_i32 s0, s26, 0x10c0
	v_or_b32_e32 v24, s0, v88
	v_mov_b64_e32 v[22:23], s[8:9]
	s_lshl_b32 s1, s18, 7
	v_mad_i64_i32 v[22:23], s[18:19], v24, s72, v[22:23]
	v_lshlrev_b32_e32 v70, 1, v26
	v_lshl_add_u64 v[22:23], v[22:23], 0, v[70:71]
	s_lshl_b32 s2, s1, 1
	v_lshl_add_u64 v[22:23], v[22:23], 0, s[2:3]
	ds_read_b128 v[26:29], v32 offset:18496
	s_waitcnt lgkmcnt(1)
	v_mfma_f32_16x16x32_bf16 v[34:37], v[18:21], v[6:9], 0
	global_load_dwordx4 v[18:21], v[22:23], off offset:1024
	s_nop 0
	global_load_dwordx4 v[22:25], v[22:23], off offset:1152
	v_mov_b32_e32 v98, 0xf149f2ca
	v_mov_b32_e32 v100, 0xf149f2ca
	s_waitcnt lgkmcnt(0)
	v_mfma_f32_16x16x32_bf16 v[26:29], v[26:29], v[2:5], v[34:37]
	s_nop 2
	s_waitcnt lgkmcnt(0)
	s_nop 3
	v_fmac_f32_e32 v240, 0x3e000000, v26
	v_cndmask_b32_e64 v100, v100, v240, s[28:29]
	s_nop 2
	s_waitcnt lgkmcnt(0)
	s_nop 0
	v_fmac_f32_e32 v241, 0x3e000000, v27
	v_cndmask_b32_e64 v98, v98, v241, s[30:31]
	v_mov_b32_e32 v101, 0xf149f2ca
	v_mov_b32_e32 v102, 0xf149f2ca
	s_nop 2
	s_waitcnt lgkmcnt(0)
	v_fmac_f32_e32 v242, 0x3e000000, v28
	v_cndmask_b32_e64 v102, v102, v242, s[34:35]
	s_nop 2
	s_waitcnt lgkmcnt(0)
	v_fmac_f32_e32 v243, 0x3e000000, v29
	v_cndmask_b32_e64 v101, v101, v243, s[36:37]
	v_mul_u32_u24_e32 v26, 0x90, v33
	v_add_u32_e32 v33, v30, v26
	ds_read_b128 v[26:29], v33 offset:18432
	ds_read_b128 v[34:37], v33 offset:18496
	v_mov_b32_e32 v103, 0xf149f2ca
	v_mov_b32_e32 v105, 0xf149f2ca
	s_waitcnt lgkmcnt(1)
	v_mfma_f32_16x16x32_bf16 v[26:29], v[26:29], v[6:9], 0
	s_waitcnt lgkmcnt(0)
	v_mfma_f32_16x16x32_bf16 v[26:29], v[34:37], v[2:5], v[26:29]
	s_nop 2
	s_waitcnt lgkmcnt(0)
	s_nop 3
	v_fmac_f32_e32 v244, 0x3e000000, v26
	v_cndmask_b32_e64 v105, v105, v244, s[38:39]
	s_nop 2
	s_waitcnt lgkmcnt(0)
	s_nop 0
	v_fmac_f32_e32 v245, 0x3e000000, v27
	v_cndmask_b32_e64 v103, v103, v245, s[44:45]
	v_mov_b32_e32 v107, 0xf149f2ca
	v_mov_b32_e32 v109, 0xf149f2ca
	s_nop 2
	s_waitcnt lgkmcnt(0)
	v_fmac_f32_e32 v246, 0x3e000000, v28
	v_cndmask_b32_e64 v109, v109, v246, s[46:47]
	s_nop 2
	s_waitcnt lgkmcnt(0)
	v_fmac_f32_e32 v247, 0x3e000000, v29
	v_cndmask_b32_e64 v107, v107, v247, s[66:67]
	s_waitcnt vmcnt(3)
	ds_write_b128 v75, v[10:13]
	s_waitcnt vmcnt(2)
	ds_write_b128 v75, v[14:17] offset:9216
	s_waitcnt lgkmcnt(0)
	s_barrier
	ds_read_b32 v240, v31 offset:38040
	ds_read_b32 v241, v31 offset:38044
	ds_read_b32 v242, v31 offset:38048
	ds_read_b32 v243, v31 offset:38052
	ds_read_b32 v244, v31 offset:38104
	ds_read_b32 v245, v31 offset:38108
	ds_read_b32 v246, v31 offset:38112
	ds_read_b32 v247, v31 offset:38116
	ds_read_b128 v[10:13], v32
	ds_read_b128 v[26:29], v32 offset:64
	s_add_i32 s18, s26, 0x1100
	v_or_b32_e32 v16, s18, v88
	v_mov_b64_e32 v[14:15], s[8:9]
	v_mad_i64_i32 v[14:15], s[20:21], v16, s72, v[14:15]
	v_lshl_add_u64 v[14:15], v[14:15], 0, v[70:71]
	v_lshl_add_u64 v[14:15], v[14:15], 0, s[2:3]
	s_waitcnt lgkmcnt(1)
	v_mfma_f32_16x16x32_bf16 v[34:37], v[10:13], v[6:9], 0
	global_load_dwordx4 v[10:13], v[14:15], off offset:1024
	s_nop 0
	global_load_dwordx4 v[14:17], v[14:15], off offset:1152
	v_mov_b32_e32 v104, 0xf149f2ca
	v_mov_b32_e32 v106, 0xf149f2ca
	s_waitcnt lgkmcnt(0)
	v_mfma_f32_16x16x32_bf16 v[26:29], v[26:29], v[2:5], v[34:37]
	s_nop 2
	s_waitcnt lgkmcnt(0)
	s_nop 3
	v_fmac_f32_e32 v240, 0x3e000000, v26
	v_cndmask_b32_e64 v106, v106, v240, s[28:29]
	s_nop 2
	s_waitcnt lgkmcnt(0)
	s_nop 0
	v_fmac_f32_e32 v241, 0x3e000000, v27
	v_cndmask_b32_e64 v104, v104, v241, s[30:31]
	v_mov_b32_e32 v108, 0xf149f2ca
	v_mov_b32_e32 v110, 0xf149f2ca
	s_nop 2
	s_waitcnt lgkmcnt(0)
	v_fmac_f32_e32 v242, 0x3e000000, v28
	v_cndmask_b32_e64 v110, v110, v242, s[34:35]
	s_nop 2
	s_waitcnt lgkmcnt(0)
	v_fmac_f32_e32 v243, 0x3e000000, v29
	v_cndmask_b32_e64 v108, v108, v243, s[36:37]
	ds_read_b128 v[26:29], v33
	ds_read_b128 v[34:37], v33 offset:64
	v_mov_b32_e32 v111, 0xf149f2ca
	v_mov_b32_e32 v113, 0xf149f2ca
	s_waitcnt lgkmcnt(1)
	v_mfma_f32_16x16x32_bf16 v[26:29], v[26:29], v[6:9], 0
	s_waitcnt lgkmcnt(0)
	v_mfma_f32_16x16x32_bf16 v[26:29], v[34:37], v[2:5], v[26:29]
	s_nop 2
	s_waitcnt lgkmcnt(0)
	s_nop 3
	v_fmac_f32_e32 v244, 0x3e000000, v26
	v_cndmask_b32_e64 v113, v113, v244, s[38:39]
	s_nop 2
	s_waitcnt lgkmcnt(0)
	s_nop 0
	v_fmac_f32_e32 v245, 0x3e000000, v27
	v_cndmask_b32_e64 v111, v111, v245, s[44:45]
	v_mov_b32_e32 v112, 0xf149f2ca
	v_mov_b32_e32 v116, 0xf149f2ca
	s_nop 2
	s_waitcnt lgkmcnt(0)
	v_fmac_f32_e32 v246, 0x3e000000, v28
	v_cndmask_b32_e64 v116, v116, v246, s[46:47]
	s_nop 2
	s_waitcnt lgkmcnt(0)
	v_fmac_f32_e32 v247, 0x3e000000, v29
	v_cndmask_b32_e64 v112, v112, v247, s[66:67]
	s_waitcnt vmcnt(3)
	ds_write_b128 v75, v[18:21] offset:18432
	s_waitcnt vmcnt(2)
	ds_write_b128 v75, v[22:25] offset:27648
	s_waitcnt lgkmcnt(0)
	s_barrier
; #define LAS __attribute__((address_space(3)))
; #define NA_STORE(sidx) do { LAS bf16* d_ = buf + ((sidx) & 1) * 9216; _Pragma("unroll") for (int q_ = 0; q_ < 2; ++q_) *(LAS v4u*)(d_ + q_ * 4608 + lrow * 72 + lseg * 8) = ld[(sidx) & 1][q_]; } while (0)
; template <bool LOCAL>
; __device__ __forceinline__ void na_unit(const bf16* P, const bf16* VT, bf16* YCAT, const LAS float* rpb_l, LAS bf16* buf, int b, int gr, int hp, int qblk, int tid) {
;     ...
;         if (sidx + 2 < 2 * NCH) NA_ISSUE(sidx + 2);
;         const LAS bf16* cb = buf + (sidx & 1) * 9216 + hh * 4608;
;         if (sidx < NCH) {
;             const int c = sidx;
;             if (LOCAL && c < 8) {
; #pragma unroll
;                 for (int t2 = 0; t2 < 2; ++t2) {
;                     const LAS bf16* kp = cb + (kc0 + 16 * t2 + fr) * 72 + 8 * fq;
;                     f32x4 acc = {0.f, 0.f, 0.f, 0.f};
;                     acc = __builtin_amdgcn_mfma_f32_16x16x32_bf16(*(const LAS bf16x8*)(kp), qf[0], acc, 0, 0, 0);
;                     acc = __builtin_amdgcn_mfma_f32_16x16x32_bf16(*(const LAS bf16x8*)(kp + 32), qf[1], acc, 0, 0, 0);
;                     const LAS float* rb = rpb + (r0 + c - gr + 7) * 31 + 15 - qcol;
; #pragma unroll
;                     for (int e = 0; e < 4; ++e) { const int kcol = kc0 + 16 * t2 + 4 * fq + e; const bool ok = (kcol >= cs) && (kcol < cs + 16);
;                         const float sv = ok ? acc[e] * 0.125f + rb[ok ? kcol : qcol] : -1.0e30f; acc[e] = sv; m = fmaxf(m, sv); }
;                     sl[2 * (c < 8 ? c : 0) + t2] = acc; }
;     ...
;         if (sidx + 1 < 2 * NCH) NA_STORE(sidx + 1);
;         __syncthreads();
	ds_read_b32 v240, v31 offset:38164
	ds_read_b32 v241, v31 offset:38168
	ds_read_b32 v242, v31 offset:38172
	ds_read_b32 v243, v31 offset:38176
	ds_read_b32 v244, v31 offset:38228
	ds_read_b32 v245, v31 offset:38232
	ds_read_b32 v246, v31 offset:38236
	ds_read_b32 v247, v31 offset:38240
	ds_read_b128 v[18:21], v32 offset:18432
	ds_read_b128 v[26:29], v32 offset:18496
	s_add_i32 s20, s26, 0x1140
	v_or_b32_e32 v24, s20, v88
	v_mov_b64_e32 v[22:23], s[8:9]
	v_mad_i64_i32 v[22:23], s[22:23], v24, s72, v[22:23]
	v_lshl_add_u64 v[22:23], v[22:23], 0, v[70:71]
	v_lshl_add_u64 v[22:23], v[22:23], 0, s[2:3]
	s_waitcnt lgkmcnt(1)
	v_mfma_f32_16x16x32_bf16 v[34:37], v[18:21], v[6:9], 0
	global_load_dwordx4 v[18:21], v[22:23], off offset:1024
	s_nop 0
	global_load_dwordx4 v[22:25], v[22:23], off offset:1152
	v_mov_b32_e32 v114, 0xf149f2ca
	v_mov_b32_e32 v115, 0xf149f2ca
	s_waitcnt lgkmcnt(0)
	v_mfma_f32_16x16x32_bf16 v[26:29], v[26:29], v[2:5], v[34:37]
	s_nop 2
	s_waitcnt lgkmcnt(0)
	s_nop 3
	v_fmac_f32_e32 v240, 0x3e000000, v26
	v_cndmask_b32_e64 v115, v115, v240, s[28:29]
	s_nop 2
	s_waitcnt lgkmcnt(0)
	s_nop 0
	v_fmac_f32_e32 v241, 0x3e000000, v27
	v_cndmask_b32_e64 v114, v114, v241, s[30:31]
	v_mov_b32_e32 v117, 0xf149f2ca
	v_mov_b32_e32 v118, 0xf149f2ca
	s_nop 2
	s_waitcnt lgkmcnt(0)
	v_fmac_f32_e32 v242, 0x3e000000, v28
	v_cndmask_b32_e64 v118, v118, v242, s[34:35]
	s_nop 2
	s_waitcnt lgkmcnt(0)
	v_fmac_f32_e32 v243, 0x3e000000, v29
	v_cndmask_b32_e64 v117, v117, v243, s[36:37]
	ds_read_b128 v[26:29], v33 offset:18432
	ds_read_b128 v[34:37], v33 offset:18496
	v_mov_b32_e32 v119, 0xf149f2ca
	v_mov_b32_e32 v121, 0xf149f2ca
	s_waitcnt lgkmcnt(1)
	v_mfma_f32_16x16x32_bf16 v[26:29], v[26:29], v[6:9], 0
	s_waitcnt lgkmcnt(0)
	v_mfma_f32_16x16x32_bf16 v[26:29], v[34:37], v[2:5], v[26:29]
	s_nop 2
	s_waitcnt lgkmcnt(0)
	s_nop 3
	v_fmac_f32_e32 v244, 0x3e000000, v26
	v_cndmask_b32_e64 v121, v121, v244, s[38:39]
	s_nop 2
	s_waitcnt lgkmcnt(0)
	s_nop 0
	v_fmac_f32_e32 v245, 0x3e000000, v27
	v_cndmask_b32_e64 v119, v119, v245, s[44:45]
	v_mov_b32_e32 v120, 0xf149f2ca
	v_mov_b32_e32 v124, 0xf149f2ca
	s_nop 2
	s_waitcnt lgkmcnt(0)
	v_fmac_f32_e32 v246, 0x3e000000, v28
	v_cndmask_b32_e64 v124, v124, v246, s[46:47]
	s_nop 2
	s_waitcnt lgkmcnt(0)
	v_fmac_f32_e32 v247, 0x3e000000, v29
	v_cndmask_b32_e64 v120, v120, v247, s[66:67]
	s_waitcnt vmcnt(3)
	ds_write_b128 v75, v[10:13]
	s_waitcnt vmcnt(2)
	ds_write_b128 v75, v[14:17] offset:9216
	s_waitcnt lgkmcnt(0)
	s_barrier
	ds_read_b32 v240, v31 offset:38288
	ds_read_b32 v241, v31 offset:38292
	ds_read_b32 v242, v31 offset:38296
	ds_read_b32 v243, v31 offset:38300
	ds_read_b32 v244, v31 offset:38352
	ds_read_b32 v245, v31 offset:38356
	ds_read_b32 v246, v31 offset:38360
	ds_read_b32 v247, v31 offset:38364
	ds_read_b128 v[10:13], v32
	ds_read_b128 v[26:29], v32 offset:64
	s_add_i32 s22, s26, 0x1180
	v_or_b32_e32 v16, s22, v88
	v_mov_b64_e32 v[14:15], s[8:9]
	v_mad_i64_i32 v[14:15], s[24:25], v16, s72, v[14:15]
	v_lshl_add_u64 v[14:15], v[14:15], 0, v[70:71]
	v_lshl_add_u64 v[14:15], v[14:15], 0, s[2:3]
	s_waitcnt lgkmcnt(1)
	v_mfma_f32_16x16x32_bf16 v[34:37], v[10:13], v[6:9], 0
	global_load_dwordx4 v[10:13], v[14:15], off offset:1024
	s_nop 0
	global_load_dwordx4 v[14:17], v[14:15], off offset:1152
	v_mov_b32_e32 v122, 0xf149f2ca
	v_mov_b32_e32 v123, 0xf149f2ca
	s_waitcnt lgkmcnt(0)
	v_mfma_f32_16x16x32_bf16 v[26:29], v[26:29], v[2:5], v[34:37]
	s_nop 2
	s_waitcnt lgkmcnt(0)
	s_nop 3
	v_fmac_f32_e32 v240, 0x3e000000, v26
	v_cndmask_b32_e64 v123, v123, v240, s[28:29]
	s_nop 2
	s_waitcnt lgkmcnt(0)
	s_nop 0
	v_fmac_f32_e32 v241, 0x3e000000, v27
	v_cndmask_b32_e64 v122, v122, v241, s[30:31]
	v_mov_b32_e32 v125, 0xf149f2ca
	v_mov_b32_e32 v126, 0xf149f2ca
	s_nop 2
	s_waitcnt lgkmcnt(0)
	v_fmac_f32_e32 v242, 0x3e000000, v28
	v_cndmask_b32_e64 v126, v126, v242, s[34:35]
	s_nop 2
	s_waitcnt lgkmcnt(0)
	v_fmac_f32_e32 v243, 0x3e000000, v29
	v_cndmask_b32_e64 v125, v125, v243, s[36:37]
	ds_read_b128 v[26:29], v33
	ds_read_b128 v[34:37], v33 offset:64
	v_mov_b32_e32 v127, 0xf149f2ca
	v_mov_b32_e32 v129, 0xf149f2ca
	s_waitcnt lgkmcnt(1)
	v_mfma_f32_16x16x32_bf16 v[26:29], v[26:29], v[6:9], 0
	s_waitcnt lgkmcnt(0)
	v_mfma_f32_16x16x32_bf16 v[26:29], v[34:37], v[2:5], v[26:29]
	s_nop 2
	s_waitcnt lgkmcnt(0)
	s_nop 3
	v_fmac_f32_e32 v244, 0x3e000000, v26
	v_cndmask_b32_e64 v129, v129, v244, s[38:39]
	s_nop 2
	s_waitcnt lgkmcnt(0)
	s_nop 0
	v_fmac_f32_e32 v245, 0x3e000000, v27
	v_cndmask_b32_e64 v127, v127, v245, s[44:45]
	v_mov_b32_e32 v128, 0xf149f2ca
	v_mov_b32_e32 v133, 0xf149f2ca
	s_nop 2
	s_waitcnt lgkmcnt(0)
	v_fmac_f32_e32 v246, 0x3e000000, v28
	v_cndmask_b32_e64 v133, v133, v246, s[46:47]
	s_nop 2
	s_waitcnt lgkmcnt(0)
	v_fmac_f32_e32 v247, 0x3e000000, v29
	v_cndmask_b32_e64 v128, v128, v247, s[66:67]
	s_waitcnt vmcnt(3)
	ds_write_b128 v75, v[18:21] offset:18432
	s_waitcnt vmcnt(2)
	ds_write_b128 v75, v[22:25] offset:27648
	s_waitcnt lgkmcnt(0)
	s_barrier
; #define LAS __attribute__((address_space(3)))
; #define NA_STORE(sidx) do { LAS bf16* d_ = buf + ((sidx) & 1) * 9216; _Pragma("unroll") for (int q_ = 0; q_ < 2; ++q_) *(LAS v4u*)(d_ + q_ * 4608 + lrow * 72 + lseg * 8) = ld[(sidx) & 1][q_]; } while (0)
; template <bool LOCAL>
; __device__ __forceinline__ void na_unit(const bf16* P, const bf16* VT, bf16* YCAT, const LAS float* rpb_l, LAS bf16* buf, int b, int gr, int hp, int qblk, int tid) {
;     ...
;         if (sidx + 2 < 2 * NCH) NA_ISSUE(sidx + 2);
;         const LAS bf16* cb = buf + (sidx & 1) * 9216 + hh * 4608;
;         if (sidx < NCH) {
;             const int c = sidx;
;             if (LOCAL && c < 8) {
; #pragma unroll
;                 for (int t2 = 0; t2 < 2; ++t2) {
;                     const LAS bf16* kp = cb + (kc0 + 16 * t2 + fr) * 72 + 8 * fq;
;                     f32x4 acc = {0.f, 0.f, 0.f, 0.f};
;                     acc = __builtin_amdgcn_mfma_f32_16x16x32_bf16(*(const LAS bf16x8*)(kp), qf[0], acc, 0, 0, 0);
;                     acc = __builtin_amdgcn_mfma_f32_16x16x32_bf16(*(const LAS bf16x8*)(kp + 32), qf[1], acc, 0, 0, 0);
;                     const LAS float* rb = rpb + (r0 + c - gr + 7) * 31 + 15 - qcol;
; #pragma unroll
;                     for (int e = 0; e < 4; ++e) { const int kcol = kc0 + 16 * t2 + 4 * fq + e; const bool ok = (kcol >= cs) && (kcol < cs + 16);
;                         const float sv = ok ? acc[e] * 0.125f + rb[ok ? kcol : qcol] : -1.0e30f; acc[e] = sv; m = fmaxf(m, sv); }
;                     sl[2 * (c < 8 ? c : 0) + t2] = acc; }
;     ...
;         if (sidx + 1 < 2 * NCH) NA_STORE(sidx + 1);
;         __syncthreads();
	ds_read_b32 v240, v31 offset:38412
	ds_read_b32 v241, v31 offset:38416
	ds_read_b32 v242, v31 offset:38420
	ds_read_b32 v243, v31 offset:38424
	ds_read_b32 v244, v31 offset:38476
	ds_read_b32 v245, v31 offset:38480
	ds_read_b32 v246, v31 offset:38484
	ds_read_b32 v247, v31 offset:38488
	ds_read_b128 v[18:21], v32 offset:18432
	ds_read_b128 v[26:29], v32 offset:18496
	s_add_i32 s24, s26, 0x11c0
	v_or_b32_e32 v24, s24, v88
	v_mov_b64_e32 v[22:23], s[8:9]
	v_mad_i64_i32 v[22:23], s[26:27], v24, s72, v[22:23]
	v_lshl_add_u64 v[22:23], v[22:23], 0, v[70:71]
	v_lshl_add_u64 v[22:23], v[22:23], 0, s[2:3]
	s_waitcnt lgkmcnt(1)
	v_mfma_f32_16x16x32_bf16 v[34:37], v[18:21], v[6:9], 0
	global_load_dwordx4 v[18:21], v[22:23], off offset:1024
	s_nop 0
	global_load_dwordx4 v[22:25], v[22:23], off offset:1152
	v_mov_b32_e32 v130, 0xf149f2ca
	v_mov_b32_e32 v131, 0xf149f2ca
	s_waitcnt lgkmcnt(0)
	v_mfma_f32_16x16x32_bf16 v[26:29], v[26:29], v[2:5], v[34:37]
	s_nop 2
	s_waitcnt lgkmcnt(0)
	s_nop 3
	v_fmac_f32_e32 v240, 0x3e000000, v26
	v_cndmask_b32_e64 v131, v131, v240, s[28:29]
	s_nop 2
	s_waitcnt lgkmcnt(0)
	s_nop 0
	v_fmac_f32_e32 v241, 0x3e000000, v27
	v_cndmask_b32_e64 v130, v130, v241, s[30:31]
	v_mov_b32_e32 v134, 0xf149f2ca
	v_mov_b32_e32 v135, 0xf149f2ca
	s_nop 2
	s_waitcnt lgkmcnt(0)
	v_fmac_f32_e32 v242, 0x3e000000, v28
	v_cndmask_b32_e64 v135, v135, v242, s[34:35]
	s_nop 2
	s_waitcnt lgkmcnt(0)
	v_fmac_f32_e32 v243, 0x3e000000, v29
	v_cndmask_b32_e64 v134, v134, v243, s[36:37]
	ds_read_b128 v[26:29], v33 offset:18432
	ds_read_b128 v[34:37], v33 offset:18496
	v_mov_b32_e32 v137, 0xf149f2ca
	v_mov_b32_e32 v139, 0xf149f2ca
	s_waitcnt lgkmcnt(1)
	v_mfma_f32_16x16x32_bf16 v[26:29], v[26:29], v[6:9], 0
	s_waitcnt lgkmcnt(0)
	v_mfma_f32_16x16x32_bf16 v[26:29], v[34:37], v[2:5], v[26:29]
	s_nop 2
	s_waitcnt lgkmcnt(0)
	s_nop 3
	v_fmac_f32_e32 v244, 0x3e000000, v26
	v_cndmask_b32_e64 v139, v139, v244, s[38:39]
	s_nop 2
	s_waitcnt lgkmcnt(0)
	s_nop 0
	v_fmac_f32_e32 v245, 0x3e000000, v27
	v_cndmask_b32_e64 v137, v137, v245, s[44:45]
	v_mov_b32_e32 v138, 0xf149f2ca
	v_mov_b32_e32 v142, 0xf149f2ca
	s_nop 2
	s_waitcnt lgkmcnt(0)
	v_fmac_f32_e32 v246, 0x3e000000, v28
	v_cndmask_b32_e64 v142, v142, v246, s[46:47]
	s_nop 2
	s_waitcnt lgkmcnt(0)
	v_fmac_f32_e32 v247, 0x3e000000, v29
	v_cndmask_b32_e64 v138, v138, v247, s[66:67]
	s_waitcnt vmcnt(3)
	ds_write_b128 v75, v[10:13]
	s_waitcnt vmcnt(2)
	ds_write_b128 v75, v[14:17] offset:9216
	s_waitcnt lgkmcnt(0)
	s_barrier
	ds_read_b32 v240, v31 offset:38536
	ds_read_b32 v241, v31 offset:38540
	ds_read_b32 v242, v31 offset:38544
	ds_read_b32 v243, v31 offset:38548
	ds_read_b32 v244, v31 offset:38600
	ds_read_b32 v245, v31 offset:38604
	ds_read_b32 v246, v31 offset:38608
	ds_read_b32 v247, v31 offset:38612
	ds_read_b128 v[10:13], v32
	ds_read_b128 v[26:29], v32 offset:64
	s_lshl_b32 s26, s17, 8
	v_or_b32_e32 v34, s26, v88
	v_mov_b64_e32 v[14:15], s[8:9]
	v_mad_i64_i32 v[14:15], s[52:53], v34, s72, v[14:15]
	v_lshl_add_u64 v[14:15], v[14:15], 0, v[70:71]
	v_lshl_add_u64 v[14:15], v[14:15], 0, s[2:3]
	s_waitcnt lgkmcnt(1)
	v_mfma_f32_16x16x32_bf16 v[36:39], v[10:13], v[6:9], 0
	global_load_dwordx4 v[10:13], v[14:15], off offset:1024
	s_nop 0
	global_load_dwordx4 v[14:17], v[14:15], off offset:1152
	v_mov_b32_e32 v140, 0xf149f2ca
	v_mov_b32_e32 v141, 0xf149f2ca
	s_waitcnt lgkmcnt(0)
	v_mfma_f32_16x16x32_bf16 v[26:29], v[26:29], v[2:5], v[36:39]
	s_nop 2
	s_waitcnt lgkmcnt(0)
	s_nop 3
	v_fmac_f32_e32 v240, 0x3e000000, v26
	v_cndmask_b32_e64 v141, v141, v240, s[28:29]
	s_nop 2
	s_waitcnt lgkmcnt(0)
	s_nop 0
	v_fmac_f32_e32 v241, 0x3e000000, v27
	v_cndmask_b32_e64 v140, v140, v241, s[30:31]
	v_mov_b32_e32 v143, 0xf149f2ca
	v_mov_b32_e32 v144, 0xf149f2ca
	s_nop 2
	s_waitcnt lgkmcnt(0)
	v_fmac_f32_e32 v242, 0x3e000000, v28
	v_cndmask_b32_e64 v144, v144, v242, s[34:35]
	s_nop 2
	s_waitcnt lgkmcnt(0)
	v_fmac_f32_e32 v243, 0x3e000000, v29
	v_cndmask_b32_e64 v143, v143, v243, s[36:37]
	ds_read_b128 v[26:29], v33
	ds_read_b128 v[36:39], v33 offset:64
	v_mov_b32_e32 v145, 0xf149f2ca
	v_mov_b32_e32 v147, 0xf149f2ca
	s_waitcnt lgkmcnt(1)
	v_mfma_f32_16x16x32_bf16 v[26:29], v[26:29], v[6:9], 0
	s_waitcnt lgkmcnt(0)
	v_mfma_f32_16x16x32_bf16 v[26:29], v[36:39], v[2:5], v[26:29]
	s_nop 2
	s_waitcnt lgkmcnt(0)
	s_nop 3
	v_fmac_f32_e32 v244, 0x3e000000, v26
	v_cndmask_b32_e64 v147, v147, v244, s[38:39]
	s_nop 2
	s_waitcnt lgkmcnt(0)
	s_nop 0
	v_fmac_f32_e32 v245, 0x3e000000, v27
	v_cndmask_b32_e64 v145, v145, v245, s[44:45]
	v_mov_b32_e32 v146, 0xf149f2ca
	v_mov_b32_e32 v150, 0xf149f2ca
	s_nop 2
	s_waitcnt lgkmcnt(0)
	v_fmac_f32_e32 v246, 0x3e000000, v28
	v_cndmask_b32_e64 v150, v150, v246, s[46:47]
	s_nop 2
	s_waitcnt lgkmcnt(0)
	v_fmac_f32_e32 v247, 0x3e000000, v29
	v_cndmask_b32_e64 v146, v146, v247, s[66:67]
	s_waitcnt vmcnt(3)
	ds_write_b128 v75, v[18:21] offset:18432
	s_waitcnt vmcnt(2)
	ds_write_b128 v75, v[22:25] offset:27648
	s_waitcnt lgkmcnt(0)
	s_barrier
; #define LAS __attribute__((address_space(3)))
; template <bool LOCAL>
; __device__ __forceinline__ void na_unit(const bf16* P, const bf16* VT, bf16* YCAT, const LAS float* rpb_l, LAS bf16* buf, int b, int gr, int hp, int qblk, int tid) {
;     ...
;         if (sidx < NCH) {
;             const int c = sidx;
;             if (LOCAL && c < 8) {
; #pragma unroll
;                 for (int t2 = 0; t2 < 2; ++t2) {
;                     const LAS bf16* kp = cb + (kc0 + 16 * t2 + fr) * 72 + 8 * fq;
;                     f32x4 acc = {0.f, 0.f, 0.f, 0.f};
;                     acc = __builtin_amdgcn_mfma_f32_16x16x32_bf16(*(const LAS bf16x8*)(kp), qf[0], acc, 0, 0, 0);
;                     acc = __builtin_amdgcn_mfma_f32_16x16x32_bf16(*(const LAS bf16x8*)(kp + 32), qf[1], acc, 0, 0, 0);
;                     const LAS float* rb = rpb + (r0 + c - gr + 7) * 31 + 15 - qcol;
; #pragma unroll
;                     for (int e = 0; e < 4; ++e) { const int kcol = kc0 + 16 * t2 + 4 * fq + e; const bool ok = (kcol >= cs) && (kcol < cs + 16);
;                         const float sv = ok ? acc[e] * 0.125f + rb[ok ? kcol : qcol] : -1.0e30f; acc[e] = sv; m = fmaxf(m, sv); }
;                     sl[2 * (c < 8 ? c : 0) + t2] = acc; }
;             } else {
;                 const int cc = c - NLOC;
; #pragma unroll
;                 for (int t4 = 0; t4 < 4; ++t4) {
;                     const LAS bf16* kp = cb + (16 * t4 + fr) * 72 + 8 * fq;
;                     f32x4 acc = {0.f, 0.f, 0.f, 0.f};
;                     acc = __builtin_amdgcn_mfma_f32_16x16x32_bf16(*(const LAS bf16x8*)(kp), qf[0], acc, 0, 0, 0);
;                     acc = __builtin_amdgcn_mfma_f32_16x16x32_bf16(*(const LAS bf16x8*)(kp + 32), qf[1], acc, 0, 0, 0);
; #pragma unroll
;                     for (int e = 0; e < 4; ++e) { acc[e] *= 0.125f; m = fmaxf(m, acc[e]); }
;                     sc[4 * (cc >= 0 ? cc : 0) + t4] = acc; }
;             }
;             if (sidx == NCH - 1) { m = fmaxf(m, __shfl_xor(m, 16)); m = fmaxf(m, __shfl_xor(m, 32)); }
	ds_read_b32 v240, v31 offset:38660
	ds_read_b32 v241, v31 offset:38664
	ds_read_b32 v242, v31 offset:38668
	ds_read_b32 v243, v31 offset:38672
	ds_read_b32 v244, v31 offset:38724
	ds_read_b32 v245, v31 offset:38728
	ds_read_b32 v246, v31 offset:38732
	ds_read_b32 v247, v31 offset:38736
	ds_read_b128 v[18:21], v32 offset:18432
	ds_read_b128 v[26:29], v32 offset:18496
	v_or_b32_e32 v24, 64, v34
	v_mov_b64_e32 v[22:23], s[8:9]
	v_mad_i64_i32 v[22:23], s[52:53], v24, s72, v[22:23]
	v_lshl_add_u64 v[22:23], v[22:23], 0, v[70:71]
	v_lshl_add_u64 v[22:23], v[22:23], 0, s[2:3]
	s_waitcnt lgkmcnt(1)
	v_mfma_f32_16x16x32_bf16 v[36:39], v[18:21], v[6:9], 0
	global_load_dwordx4 v[18:21], v[22:23], off offset:1024
	s_nop 0
	global_load_dwordx4 v[22:25], v[22:23], off offset:1152
	v_mov_b32_e32 v148, 0xf149f2ca
	v_mov_b32_e32 v149, 0xf149f2ca
	s_waitcnt lgkmcnt(0)
	v_mfma_f32_16x16x32_bf16 v[26:29], v[26:29], v[2:5], v[36:39]
	s_nop 2
	s_waitcnt lgkmcnt(0)
	s_nop 3
	v_fmac_f32_e32 v240, 0x3e000000, v26
	v_cndmask_b32_e64 v149, v149, v240, s[28:29]
	s_nop 2
	s_waitcnt lgkmcnt(0)
	s_nop 0
	v_fmac_f32_e32 v241, 0x3e000000, v27
	v_cndmask_b32_e64 v148, v148, v241, s[30:31]
	v_mov_b32_e32 v151, 0xf149f2ca
	v_mov_b32_e32 v152, 0xf149f2ca
	s_nop 2
	s_waitcnt lgkmcnt(0)
	v_fmac_f32_e32 v242, 0x3e000000, v28
	v_cndmask_b32_e64 v152, v152, v242, s[34:35]
	s_nop 2
	s_waitcnt lgkmcnt(0)
	v_fmac_f32_e32 v243, 0x3e000000, v29
	v_cndmask_b32_e64 v151, v151, v243, s[36:37]
	ds_read_b128 v[26:29], v33 offset:18432
	ds_read_b128 v[36:39], v33 offset:18496
	v_mov_b32_e32 v153, 0xf149f2ca
	v_mov_b32_e32 v155, 0xf149f2ca
	s_waitcnt lgkmcnt(1)
	v_mfma_f32_16x16x32_bf16 v[26:29], v[26:29], v[6:9], 0
	s_waitcnt lgkmcnt(0)
	v_mfma_f32_16x16x32_bf16 v[26:29], v[36:39], v[2:5], v[26:29]
	s_nop 2
	s_waitcnt lgkmcnt(0)
	s_nop 3
	v_fmac_f32_e32 v244, 0x3e000000, v26
	v_cndmask_b32_e64 v155, v155, v244, s[38:39]
	s_nop 2
	s_waitcnt lgkmcnt(0)
	s_nop 0
	v_fmac_f32_e32 v245, 0x3e000000, v27
	v_cndmask_b32_e64 v153, v153, v245, s[44:45]
	v_mov_b32_e32 v154, 0xf149f2ca
	v_mov_b32_e32 v157, 0xf149f2ca
	s_nop 2
	s_waitcnt lgkmcnt(0)
	v_fmac_f32_e32 v246, 0x3e000000, v28
	v_cndmask_b32_e64 v157, v157, v246, s[46:47]
	s_nop 2
	s_waitcnt lgkmcnt(0)
	v_fmac_f32_e32 v247, 0x3e000000, v29
	v_cndmask_b32_e64 v154, v154, v247, s[66:67]
	v_max3_f32 v26, v92, s75, v91
	v_max3_f32 v26, v26, v94, v93
	v_max3_f32 v26, v26, v96, v95
	v_max3_f32 v26, v26, v99, v97
	v_max3_f32 v26, v26, v100, v98
	v_max3_f32 v26, v26, v102, v101
	v_max3_f32 v26, v26, v105, v103
	v_max3_f32 v26, v26, v109, v107
	v_max3_f32 v26, v26, v106, v104
	v_max3_f32 v26, v26, v110, v108
	v_max3_f32 v26, v26, v113, v111
	v_max3_f32 v26, v26, v116, v112
	v_max3_f32 v26, v26, v115, v114
	v_max3_f32 v26, v26, v118, v117
	v_max3_f32 v26, v26, v121, v119
	v_max3_f32 v26, v26, v124, v120
	v_max3_f32 v26, v26, v123, v122
	v_max3_f32 v26, v26, v126, v125
	v_max3_f32 v26, v26, v129, v127
	v_max3_f32 v26, v26, v133, v128
	v_max3_f32 v26, v26, v131, v130
	v_max3_f32 v26, v26, v135, v134
	v_max3_f32 v26, v26, v139, v137
	v_max3_f32 v26, v26, v142, v138
	v_max3_f32 v26, v26, v141, v140
	v_max3_f32 v26, v26, v144, v143
	v_mad_u32_u24 v89, v89, s73, v30
	v_max3_f32 v26, v26, v147, v145
	s_waitcnt vmcnt(3)
	ds_write_b128 v75, v[10:13]
	s_waitcnt vmcnt(2)
	ds_write_b128 v75, v[14:17] offset:9216
	s_waitcnt lgkmcnt(0)
	s_barrier
	ds_read_b128 v[10:13], v89
	ds_read_b128 v[14:17], v89 offset:64
	v_max3_f32 v26, v26, v150, v146
	v_max3_f32 v26, v26, v149, v148
	v_max3_f32 v26, v26, v152, v151
	v_max3_f32 v26, v26, v155, v153
	v_max3_f32 v35, v26, v157, v154
	v_or_b32_e32 v26, 0x80, v34
	v_mov_b64_e32 v[44:45], s[8:9]
	v_mad_i64_i32 v[26:27], s[28:29], v26, s72, v[44:45]
	v_lshl_add_u64 v[26:27], v[26:27], 0, v[70:71]
	v_lshl_add_u64 v[30:31], v[26:27], 0, s[2:3]
	s_waitcnt lgkmcnt(1)
	v_mfma_f32_16x16x32_bf16 v[10:13], v[10:13], v[6:9], 0
	global_load_dwordx4 v[26:29], v[30:31], off offset:1024
	s_nop 0
	global_load_dwordx4 v[30:33], v[30:31], off offset:1152
	ds_read_b128 v[36:39], v89 offset:2304
	v_lshl_add_u64 v[78:79], s[4:5], 0, v[70:71]
	s_waitcnt lgkmcnt(1)
	v_mfma_f32_16x16x32_bf16 v[62:65], v[14:17], v[2:5], v[10:13]
	s_ashr_i32 s17, s16, 31
	v_mov_b32_e32 v81, v71
	v_cmp_lt_i32_e32 vcc, v83, v84
	ds_read_b128 v[10:13], v89 offset:2368
	v_add3_u32 v156, v86, v76, v87
	s_nop 2
	v_mul_f32_e32 v14, 0x3e000000, v62
	v_mul_f32_e32 v15, 0x3e000000, v63
	v_max3_f32 v35, v35, v14, v15
	v_mul_f32_e32 v40, 0x3e000000, v64
	s_waitcnt lgkmcnt(1)
	v_mfma_f32_16x16x32_bf16 v[14:17], v[36:39], v[6:9], 0
	v_mul_f32_e32 v36, 0x3e000000, v65
	v_max3_f32 v35, v35, v40, v36
	ds_read_b128 v[36:39], v89 offset:4608
	s_waitcnt lgkmcnt(1)
	v_mfma_f32_16x16x32_bf16 v[66:69], v[10:13], v[2:5], v[14:17]
	ds_read_b128 v[10:13], v89 offset:4672
	s_ashr_i32 s19, s18, 31
	s_ashr_i32 s21, s20, 31
	s_ashr_i32 s23, s22, 31
	s_ashr_i32 s25, s24, 31
	s_nop 2
	v_mul_f32_e32 v14, 0x3e000000, v66
	v_mul_f32_e32 v15, 0x3e000000, v67
	v_max3_f32 v35, v35, v14, v15
	s_waitcnt lgkmcnt(1)
	v_mfma_f32_16x16x32_bf16 v[14:17], v[36:39], v[6:9], 0
	v_mul_f32_e32 v40, 0x3e000000, v68
	v_mul_f32_e32 v41, 0x3e000000, v69
	v_max3_f32 v35, v35, v40, v41
	s_waitcnt lgkmcnt(0)
	v_mfma_f32_16x16x32_bf16 v[58:61], v[10:13], v[2:5], v[14:17]
	ds_read_b128 v[36:39], v89 offset:6912
	ds_read_b128 v[40:43], v89 offset:6976
	s_waitcnt vmcnt(3)
	ds_write_b128 v75, v[18:21] offset:18432
	s_waitcnt vmcnt(2)
	ds_write_b128 v75, v[22:25] offset:27648
	s_waitcnt lgkmcnt(0)
	s_nop 0
	v_mul_f32_e32 v10, 0x3e000000, v58
	v_mul_f32_e32 v11, 0x3e000000, v59
	v_max3_f32 v14, v35, v10, v11
	v_mfma_f32_16x16x32_bf16 v[10:13], v[36:39], v[6:9], 0
	v_mul_f32_e32 v15, 0x3e000000, v60
	v_mul_f32_e32 v16, 0x3e000000, v61
	v_max3_f32 v14, v14, v15, v16
	v_mfma_f32_16x16x32_bf16 v[54:57], v[40:43], v[2:5], v[10:13]
	s_barrier
; #define LAS __attribute__((address_space(3)))
; #define NA_STORE(sidx) do { LAS bf16* d_ = buf + ((sidx) & 1) * 9216; _Pragma("unroll") for (int q_ = 0; q_ < 2; ++q_) *(LAS v4u*)(d_ + q_ * 4608 + lrow * 72 + lseg * 8) = ld[(sidx) & 1][q_]; } while (0)
; template <bool LOCAL>
; __device__ __forceinline__ void na_unit(const bf16* P, const bf16* VT, bf16* YCAT, const LAS float* rpb_l, LAS bf16* buf, int b, int gr, int hp, int qblk, int tid) {
;     ...
;             } else {
;                 const int cc = c - NLOC;
; #pragma unroll
;                 for (int t4 = 0; t4 < 4; ++t4) {
;                     const LAS bf16* kp = cb + (16 * t4 + fr) * 72 + 8 * fq;
;                     f32x4 acc = {0.f, 0.f, 0.f, 0.f};
;                     acc = __builtin_amdgcn_mfma_f32_16x16x32_bf16(*(const LAS bf16x8*)(kp), qf[0], acc, 0, 0, 0);
;                     acc = __builtin_amdgcn_mfma_f32_16x16x32_bf16(*(const LAS bf16x8*)(kp + 32), qf[1], acc, 0, 0, 0);
; #pragma unroll
;                     for (int e = 0; e < 4; ++e) { acc[e] *= 0.125f; m = fmaxf(m, acc[e]); }
;                     sc[4 * (cc >= 0 ? cc : 0) + t4] = acc; }
;             }
;             if (sidx == NCH - 1) { m = fmaxf(m, __shfl_xor(m, 16)); m = fmaxf(m, __shfl_xor(m, 32)); }
;     ...
;         if (sidx + 1 < 2 * NCH) NA_STORE(sidx + 1);
;         __syncthreads();
	v_or_b32_e32 v18, 0xc0, v34
	v_mad_i64_i32 v[18:19], s[28:29], v18, s72, v[44:45]
	v_lshl_add_u64 v[18:19], v[18:19], 0, v[70:71]
	s_nop 3
	v_mul_f32_e32 v10, 0x3e000000, v54
	v_mul_f32_e32 v11, 0x3e000000, v55
	v_max3_f32 v14, v14, v10, v11
	ds_read_b128 v[10:13], v89 offset:18432
	v_mul_f32_e32 v15, 0x3e000000, v56
	v_mul_f32_e32 v16, 0x3e000000, v57
	v_max3_f32 v35, v14, v15, v16
	ds_read_b128 v[14:17], v89 offset:18496
	v_lshl_add_u64 v[22:23], v[18:19], 0, s[2:3]
	s_waitcnt lgkmcnt(1)
	v_mfma_f32_16x16x32_bf16 v[10:13], v[10:13], v[6:9], 0
	global_load_dwordx4 v[18:21], v[22:23], off offset:1024
	global_load_dwordx4 v[158:161], v[22:23], off offset:1152
	ds_read_b128 v[22:25], v89 offset:20736
	s_ashr_i32 s27, s26, 31
	s_waitcnt lgkmcnt(1)
	v_mfma_f32_16x16x32_bf16 v[46:49], v[14:17], v[2:5], v[10:13]
	s_nop 2
	ds_read_b128 v[10:13], v89 offset:20800
	s_nop 3
	v_mul_f32_e32 v14, 0x3e000000, v46
	v_mul_f32_e32 v15, 0x3e000000, v47
	v_max3_f32 v34, v35, v14, v15
	v_mul_f32_e32 v35, 0x3e000000, v48
	s_waitcnt lgkmcnt(1)
	v_mfma_f32_16x16x32_bf16 v[14:17], v[22:25], v[6:9], 0
	v_mul_f32_e32 v22, 0x3e000000, v49
	v_max3_f32 v34, v34, v35, v22
	ds_read_b128 v[22:25], v89 offset:23040
	s_waitcnt lgkmcnt(1)
	v_mfma_f32_16x16x32_bf16 v[50:53], v[10:13], v[2:5], v[14:17]
	ds_read_b128 v[10:13], v89 offset:23104
	s_nop 6
	v_mul_f32_e32 v14, 0x3e000000, v50
	v_mul_f32_e32 v15, 0x3e000000, v51
	v_max3_f32 v34, v34, v14, v15
	s_waitcnt lgkmcnt(1)
	v_mfma_f32_16x16x32_bf16 v[14:17], v[22:25], v[6:9], 0
	v_mul_f32_e32 v35, 0x3e000000, v52
	v_mul_f32_e32 v36, 0x3e000000, v53
	v_max3_f32 v38, v34, v35, v36
	s_waitcnt lgkmcnt(0)
	v_mfma_f32_16x16x32_bf16 v[42:45], v[10:13], v[2:5], v[14:17]
	ds_read_b128 v[22:25], v89 offset:25344
	ds_read_b128 v[34:37], v89 offset:25408
	s_waitcnt vmcnt(3)
	ds_write_b128 v75, v[26:29]
	s_waitcnt vmcnt(2)
	ds_write_b128 v75, v[30:33] offset:9216
	s_waitcnt lgkmcnt(0)
	s_nop 0
	v_mul_f32_e32 v10, 0x3e000000, v42
	v_mul_f32_e32 v11, 0x3e000000, v43
	v_max3_f32 v14, v38, v10, v11
	v_mfma_f32_16x16x32_bf16 v[10:13], v[22:25], v[6:9], 0
	v_mul_f32_e32 v15, 0x3e000000, v44
	v_mul_f32_e32 v16, 0x3e000000, v45
	v_max3_f32 v14, v14, v15, v16
	v_mfma_f32_16x16x32_bf16 v[38:41], v[34:37], v[2:5], v[10:13]
	s_barrier
	v_add3_u32 v26, v88, s1, 64
	v_mul_u32_u24_e32 v26, 0x9000, v26
	v_lshl_add_u64 v[22:23], s[16:17], 1, v[78:79]
	s_nop 3
	v_mul_f32_e32 v10, 0x3e000000, v38
	v_mul_f32_e32 v11, 0x3e000000, v39
	v_max3_f32 v10, v14, v10, v11
	v_mul_f32_e32 v11, 0x3e000000, v40
	v_mul_f32_e32 v12, 0x3e000000, v41
	v_max3_f32 v34, v10, v11, v12
	v_or_b32_e32 v10, s1, v88
	v_mul_u32_u24_e32 v14, 0x9000, v10
	ds_read_b128 v[10:13], v89
	v_lshlrev_b32_e32 v70, 1, v14
	ds_read_b128 v[14:17], v89 offset:64
	v_lshlrev_b32_e32 v80, 1, v26
	v_lshl_add_u64 v[24:25], v[22:23], 0, v[70:71]
	v_lshl_add_u64 v[22:23], v[22:23], 0, v[80:81]
	s_waitcnt lgkmcnt(1)
	v_mfma_f32_16x16x32_bf16 v[10:13], v[10:13], v[6:9], 0
	global_load_dwordx4 v[162:165], v[24:25], off
	global_load_dwordx4 v[166:169], v[22:23], off
	ds_read_b128 v[22:25], v89 offset:2304
	s_add_i32 s16, s15, s50
	s_waitcnt lgkmcnt(1)
	v_mfma_f32_16x16x32_bf16 v[30:33], v[14:17], v[2:5], v[10:13]
	s_ashr_i32 s17, s16, 31
	s_ashr_i32 s15, s14, 31
	v_lshl_add_u64 v[86:87], s[14:15], 1, v[78:79]
	ds_read_b128 v[10:13], v89 offset:2368
	s_ashr_i32 s1, s0, 31
	s_nop 2
	v_mul_f32_e32 v14, 0x3e000000, v30
	v_mul_f32_e32 v15, 0x3e000000, v31
	v_max3_f32 v26, v34, v14, v15
	v_mul_f32_e32 v27, 0x3e000000, v32
	s_waitcnt lgkmcnt(1)
	v_mfma_f32_16x16x32_bf16 v[14:17], v[22:25], v[6:9], 0
	v_mul_f32_e32 v22, 0x3e000000, v33
	v_max3_f32 v26, v26, v27, v22
	ds_read_b128 v[22:25], v89 offset:4608
	s_waitcnt lgkmcnt(1)
	v_mfma_f32_16x16x32_bf16 v[34:37], v[10:13], v[2:5], v[14:17]
	ds_read_b128 v[10:13], v89 offset:4672
	s_nop 6
	v_mul_f32_e32 v14, 0x3e000000, v34
	v_mul_f32_e32 v15, 0x3e000000, v35
	v_max3_f32 v26, v26, v14, v15
	s_waitcnt lgkmcnt(1)
	v_mfma_f32_16x16x32_bf16 v[14:17], v[22:25], v[6:9], 0
	v_mul_f32_e32 v27, 0x3e000000, v36
	v_mul_f32_e32 v28, 0x3e000000, v37
	v_max3_f32 v88, v26, v27, v28
	s_waitcnt lgkmcnt(0)
	v_mfma_f32_16x16x32_bf16 v[26:29], v[10:13], v[2:5], v[14:17]
	ds_read_b128 v[22:25], v89 offset:6912
	ds_read_b128 v[172:175], v89 offset:6976
	s_waitcnt vmcnt(3)
	ds_write_b128 v75, v[18:21] offset:18432
	s_waitcnt vmcnt(2)
	ds_write_b128 v75, v[158:161] offset:27648
	s_waitcnt lgkmcnt(0)
	s_nop 0
	v_mul_f32_e32 v10, 0x3e000000, v26
	v_mul_f32_e32 v11, 0x3e000000, v27
	v_max3_f32 v14, v88, v10, v11
	v_mfma_f32_16x16x32_bf16 v[10:13], v[22:25], v[6:9], 0
	v_mul_f32_e32 v15, 0x3e000000, v28
	v_mul_f32_e32 v16, 0x3e000000, v29
	v_max3_f32 v14, v14, v15, v16
	v_mfma_f32_16x16x32_bf16 v[22:25], v[172:175], v[2:5], v[10:13]
	s_barrier
; #define LAS __attribute__((address_space(3)))
; __device__ __forceinline__ unsigned cvt_pk_bf16(float lo, float hi) { const float __attribute__((ext_vector_type(2))) v = {lo, hi}; return __builtin_bit_cast(unsigned, __builtin_convertvector(v, bf16x2_t)); }
; template <bool LOCAL>
; __device__ __forceinline__ void na_unit(const bf16* P, const bf16* VT, bf16* YCAT, const LAS float* rpb_l, LAS bf16* buf, int b, int gr, int hp, int qblk, int tid) {
;     ...
;                     for (int e = 0; e < 4; ++e) { acc[e] *= 0.125f; m = fmaxf(m, acc[e]); }
;                     sc[4 * (cc >= 0 ? cc : 0) + t4] = acc; }
;             }
;             if (sidx == NCH - 1) { m = fmaxf(m, __shfl_xor(m, 16)); m = fmaxf(m, __shfl_xor(m, 32)); }
;         } else {
;             const int c = sidx - NCH;
;             if (LOCAL && c < 8) {
;                 float p[8];
; #pragma unroll
;                 for (int e = 0; e < 4; ++e) { p[e] = __expf(sl[2 * (c < 8 ? c : 0)][e] - m); p[4 + e] = __expf(sl[2 * (c < 8 ? c : 0) + 1][e] - m); }
; #pragma unroll
;                 for (int e = 0; e < 8; ++e) lsum += p[e];
;                 const bf16x8 pf = __builtin_bit_cast(bf16x8, (v4u){pg8::cvt_pk_bf16(p[0], p[1]), pg8::cvt_pk_bf16(p[2], p[3]), pg8::cvt_pk_bf16(p[4], p[5]), pg8::cvt_pk_bf16(p[6], p[7])});
; #pragma unroll
;                 for (int dt = 0; dt < 4; ++dt) { const LAS bf16* vp = cb + (16 * dt + fr) * 72 + kc0 + 4 * fq;
;                     o[dt] = __builtin_amdgcn_mfma_f32_16x16x32_bf16(frag44(vp, vp + 16), pf, o[dt], 0, 0, 0); }
	v_lshl_add_u64 v[18:19], s[16:17], 1, v[78:79]
	v_lshl_add_u64 v[20:21], v[18:19], 0, v[70:71]
	v_lshl_add_u64 v[18:19], v[18:19], 0, v[80:81]
	s_nop 3
	v_mul_f32_e32 v10, 0x3e000000, v22
	v_mul_f32_e32 v11, 0x3e000000, v23
	v_max3_f32 v14, v14, v10, v11
	ds_read_b128 v[10:13], v89 offset:18432
	v_mul_f32_e32 v15, 0x3e000000, v24
	v_mul_f32_e32 v16, 0x3e000000, v25
	v_max3_f32 v88, v14, v15, v16
	ds_read_b128 v[14:17], v89 offset:18496
	s_waitcnt lgkmcnt(1)
	v_mfma_f32_16x16x32_bf16 v[10:13], v[10:13], v[6:9], 0
	global_load_dwordx4 v[172:175], v[20:21], off
	global_load_dwordx4 v[176:179], v[18:19], off
	ds_read_b128 v[18:21], v89 offset:20736
	ds_read_b128 v[158:161], v89 offset:23040
	s_waitcnt lgkmcnt(2)
	v_mfma_f32_16x16x32_bf16 v[14:17], v[14:17], v[2:5], v[10:13]
	s_nop 2
	ds_read_b128 v[10:13], v89 offset:20800
	s_waitcnt lgkmcnt(2)
	v_mfma_f32_16x16x32_bf16 v[18:21], v[18:21], v[6:9], 0
	s_nop 1
	v_mul_f32_e32 v132, 0x3e000000, v14
	v_mul_f32_e32 v136, 0x3e000000, v15
	v_max3_f32 v88, v88, v132, v136
	s_waitcnt lgkmcnt(0)
	v_mfma_f32_16x16x32_bf16 v[18:21], v[10:13], v[2:5], v[18:21]
	ds_read_b128 v[10:13], v89 offset:23104
	ds_read_b128 v[180:183], v89 offset:25344
	ds_read_b128 v[184:187], v89 offset:25408
	v_mul_f32_e32 v132, 0x3e000000, v16
	v_mfma_f32_16x16x32_bf16 v[158:161], v[158:161], v[6:9], 0
	v_mul_f32_e32 v136, 0x3e000000, v17
	v_max3_f32 v88, v88, v132, v136
	s_nop 0
	v_mul_f32_e32 v132, 0x3e000000, v18
	s_waitcnt lgkmcnt(1)
	v_mfma_f32_16x16x32_bf16 v[6:9], v[180:183], v[6:9], 0
	v_mul_f32_e32 v136, 0x3e000000, v19
	v_max3_f32 v88, v88, v132, v136
	v_mul_f32_e32 v132, 0x3e000000, v20
	v_mfma_f32_16x16x32_bf16 v[10:13], v[10:13], v[2:5], v[158:161]
	v_mul_f32_e32 v136, 0x3e000000, v21
	v_max3_f32 v88, v88, v132, v136
	s_waitcnt vmcnt(3)
	ds_write_b128 v75, v[162:165]
	s_waitcnt vmcnt(2)
	ds_write_b128 v75, v[166:169] offset:9216
	s_waitcnt lgkmcnt(2)
	v_mfma_f32_16x16x32_bf16 v[2:5], v[184:187], v[2:5], v[6:9]
	v_mul_f32_e32 v89, 0x3e000000, v10
	v_mul_f32_e32 v132, 0x3e000000, v11
	v_max3_f32 v88, v88, v89, v132
	v_mul_f32_e32 v89, 0x3e000000, v12
	v_mul_f32_e32 v132, 0x3e000000, v13
	v_max3_f32 v88, v88, v89, v132
	s_nop 1
	v_mul_f32_e32 v6, 0x3e000000, v2
	v_mul_f32_e32 v7, 0x3e000000, v3
	v_max3_f32 v6, v88, v6, v7
	v_mul_f32_e32 v7, 0x3e000000, v4
	v_mul_f32_e32 v8, 0x3e000000, v5
	v_max3_f32 v6, v6, v7, v8
	v_cndmask_b32_e32 v7, v82, v83, vcc
	v_lshlrev_b32_e32 v88, 2, v7
	ds_bpermute_b32 v7, v88, v6
	v_cmp_lt_i32_e32 vcc, v85, v84
	v_lshl_add_u32 v8, v90, 1, v156
	s_waitcnt lgkmcnt(0)
	s_barrier
	v_max_f32_e32 v7, v7, v7
	v_max_f32_e32 v6, v6, v7
	v_cndmask_b32_e32 v7, v82, v85, vcc
	v_lshlrev_b32_e32 v89, 2, v7
	ds_bpermute_b32 v7, v89, v6
	s_waitcnt lgkmcnt(0)
	ds_read2_b64 v[158:161], v8 offset1:4
	v_max_f32_e32 v7, v7, v7
	v_max_f32_e32 v136, v6, v7
	v_sub_f32_e32 v6, v92, v136
	v_mul_f32_e32 v6, 0x3fb8aa3b, v6
	v_exp_f32_e32 v132, v6
	v_sub_f32_e32 v6, v96, v136
	v_mul_f32_e32 v6, 0x3fb8aa3b, v6
	v_exp_f32_e32 v92, v6
	v_sub_f32_e32 v6, v91, v136
	v_mul_f32_e32 v6, 0x3fb8aa3b, v6
	v_exp_f32_e32 v96, v6
	v_sub_f32_e32 v6, v95, v136
	v_mul_f32_e32 v6, 0x3fb8aa3b, v6
	v_exp_f32_e32 v91, v6
	v_sub_f32_e32 v6, v94, v136
	v_mul_f32_e32 v6, 0x3fb8aa3b, v6
	v_exp_f32_e32 v95, v6
	v_sub_f32_e32 v6, v99, v136
	v_mul_f32_e32 v6, 0x3fb8aa3b, v6
	v_exp_f32_e32 v94, v6
	v_sub_f32_e32 v6, v93, v136
	v_mul_f32_e32 v6, 0x3fb8aa3b, v6
	v_exp_f32_e32 v99, v6
	v_sub_f32_e32 v6, v97, v136
	v_mul_f32_e32 v6, 0x3fb8aa3b, v6
	v_exp_f32_e32 v93, v6
	v_cvt_pk_bf16_f32 v162, v132, v96
	v_cvt_pk_bf16_f32 v163, v95, v99
	v_cvt_pk_bf16_f32 v164, v92, v91
	v_cvt_pk_bf16_f32 v165, v94, v93
	v_add_u32_e32 v7, 0x800, v8
	v_add_u32_e32 v6, 0x1000, v8
	s_waitcnt lgkmcnt(0)
	v_mfma_f32_16x16x32_bf16 v[184:187], v[158:161], v[162:165], 0
	v_lshl_add_u64 v[158:159], v[86:87], 0, v[70:71]
	ds_read2_b64 v[166:169], v7 offset0:32 offset1:36
	ds_read2_b64 v[180:183], v6 offset0:64 offset1:68
	v_lshl_add_u64 v[86:87], v[86:87], 0, v[80:81]
	global_load_dwordx4 v[188:191], v[158:159], off
	global_load_dwordx4 v[192:195], v[86:87], off
	v_sub_f32_e32 v9, v100, v136
	v_mul_f32_e32 v9, 0x3fb8aa3b, v9
	v_add_u32_e32 v158, 0x1800, v8
	v_exp_f32_e32 v86, v9
	v_sub_f32_e32 v9, v105, v136
	ds_read2_b64 v[196:199], v158 offset0:96 offset1:100
	v_mul_f32_e32 v9, 0x3fb8aa3b, v9
	v_exp_f32_e32 v76, v9
	v_sub_f32_e32 v9, v98, v136
	v_mul_f32_e32 v9, 0x3fb8aa3b, v9
	v_exp_f32_e32 v90, v9
	v_sub_f32_e32 v9, v103, v136
	v_mul_f32_e32 v9, 0x3fb8aa3b, v9
	v_exp_f32_e32 v87, v9
	v_sub_f32_e32 v9, v102, v136
	v_mul_f32_e32 v9, 0x3fb8aa3b, v9
	v_exp_f32_e32 v98, v9
	v_sub_f32_e32 v9, v109, v136
	v_mul_f32_e32 v9, 0x3fb8aa3b, v9
	v_add_u32_e32 v160, 0x4800, v8
	s_waitcnt lgkmcnt(2)
	v_mfma_f32_16x16x32_bf16 v[166:169], v[166:169], v[162:165], 0
	s_waitcnt vmcnt(3)
	ds_write_b128 v75, v[172:175] offset:18432
	s_waitcnt vmcnt(2)
	ds_write_b128 v75, v[176:179] offset:27648
	s_waitcnt lgkmcnt(0)
	s_barrier
; #define LAS __attribute__((address_space(3)))
; __device__ __forceinline__ unsigned cvt_pk_bf16(float lo, float hi) { const float __attribute__((ext_vector_type(2))) v = {lo, hi}; return __builtin_bit_cast(unsigned, __builtin_convertvector(v, bf16x2_t)); }
; template <bool LOCAL>
; __device__ __forceinline__ void na_unit(const bf16* P, const bf16* VT, bf16* YCAT, const LAS float* rpb_l, LAS bf16* buf, int b, int gr, int hp, int qblk, int tid) {
;     ...
;             if (LOCAL && c < 8) {
;                 float p[8];
; #pragma unroll
;                 for (int e = 0; e < 4; ++e) { p[e] = __expf(sl[2 * (c < 8 ? c : 0)][e] - m); p[4 + e] = __expf(sl[2 * (c < 8 ? c : 0) + 1][e] - m); }
; #pragma unroll
;                 for (int e = 0; e < 8; ++e) lsum += p[e];
;                 const bf16x8 pf = __builtin_bit_cast(bf16x8, (v4u){pg8::cvt_pk_bf16(p[0], p[1]), pg8::cvt_pk_bf16(p[2], p[3]), pg8::cvt_pk_bf16(p[4], p[5]), pg8::cvt_pk_bf16(p[6], p[7])});
; #pragma unroll
;                 for (int dt = 0; dt < 4; ++dt) { const LAS bf16* vp = cb + (16 * dt + fr) * 72 + kc0 + 4 * fq;
;                     o[dt] = __builtin_amdgcn_mfma_f32_16x16x32_bf16(frag44(vp, vp + 16), pf, o[dt], 0, 0, 0); }
;             } else {
;                 const int cc = c - NLOC;
; #pragma unroll
;                 for (int p2 = 0; p2 < 2; ++p2) {
;                     float p[8];
; #pragma unroll
;                     for (int e = 0; e < 4; ++e) { p[e] = __expf(sc[4 * (cc >= 0 ? cc : 0) + 2 * p2][e] - m); p[4 + e] = __expf(sc[4 * (cc >= 0 ? cc : 0) + 2 * p2 + 1][e] - m); }
; #pragma unroll
;                     for (int e = 0; e < 8; ++e) lsum += p[e];
;                     const bf16x8 pf = __builtin_bit_cast(bf16x8, (v4u){pg8::cvt_pk_bf16(p[0], p[1]), pg8::cvt_pk_bf16(p[2], p[3]), pg8::cvt_pk_bf16(p[4], p[5]), pg8::cvt_pk_bf16(p[6], p[7])});
; #pragma unroll
;                     for (int dt = 0; dt < 4; ++dt) { const LAS bf16* vp = cb + (16 * dt + fr) * 72 + 32 * p2 + 4 * fq;
;                         o[dt] = __builtin_amdgcn_mfma_f32_16x16x32_bf16(frag44(vp, vp + 16), pf, o[dt], 0, 0, 0); }
;                 }
;             }
;         }
;         if (sidx + 1 < 2 * NCH) NA_STORE(sidx + 1);
;         __syncthreads();
	v_mfma_f32_16x16x32_bf16 v[180:183], v[180:183], v[162:165], 0
	v_exp_f32_e32 v97, v9
	v_sub_f32_e32 v9, v101, v136
	v_mfma_f32_16x16x32_bf16 v[196:199], v[196:199], v[162:165], 0
	ds_read2_b64 v[162:165], v160 offset1:4
	v_add_u32_e32 v159, 0x5000, v8
	v_mul_f32_e32 v9, 0x3fb8aa3b, v9
	ds_read2_b64 v[172:175], v159 offset0:32 offset1:36
	v_exp_f32_e32 v100, v9
	v_sub_f32_e32 v9, v107, v136
	v_mul_f32_e32 v9, 0x3fb8aa3b, v9
	v_exp_f32_e32 v101, v9
	v_cvt_pk_bf16_f32 v176, v86, v90
	v_cvt_pk_bf16_f32 v177, v98, v100
	v_cvt_pk_bf16_f32 v178, v76, v87
	v_cvt_pk_bf16_f32 v179, v97, v101
	v_lshl_add_u64 v[102:103], s[0:1], 1, v[78:79]
	v_add_u32_e32 v161, 0x5800, v8
	s_waitcnt lgkmcnt(1)
	v_mfma_f32_16x16x32_bf16 v[184:187], v[162:165], v[176:179], v[184:187]
	v_lshl_add_u64 v[162:163], v[102:103], 0, v[70:71]
	v_lshl_add_u64 v[102:103], v[102:103], 0, v[80:81]
	v_sub_f32_e32 v9, v106, v136
	s_waitcnt lgkmcnt(0)
	v_mfma_f32_16x16x32_bf16 v[164:167], v[172:175], v[176:179], v[166:169]
	ds_read2_b64 v[172:175], v161 offset0:64 offset1:68
	global_load_dwordx4 v[200:203], v[162:163], off
	global_load_dwordx4 v[204:207], v[102:103], off
	v_mul_f32_e32 v9, 0x3fb8aa3b, v9
	v_add_u32_e32 v162, 0x6000, v8
	v_exp_f32_e32 v103, v9
	v_sub_f32_e32 v9, v113, v136
	s_waitcnt lgkmcnt(0)
	v_mfma_f32_16x16x32_bf16 v[172:175], v[172:175], v[176:179], v[180:183]
	s_nop 2
	ds_read2_b64 v[180:183], v162 offset0:96 offset1:100
	v_mul_f32_e32 v9, 0x3fb8aa3b, v9
	v_exp_f32_e32 v102, v9
	v_sub_f32_e32 v9, v104, v136
	v_mul_f32_e32 v9, 0x3fb8aa3b, v9
	v_exp_f32_e32 v105, v9
	v_sub_f32_e32 v9, v111, v136
	v_mul_f32_e32 v9, 0x3fb8aa3b, v9
	v_exp_f32_e32 v104, v9
	v_sub_f32_e32 v9, v110, v136
	v_mul_f32_e32 v9, 0x3fb8aa3b, v9
	v_exp_f32_e32 v107, v9
	v_sub_f32_e32 v9, v116, v136
	v_mul_f32_e32 v9, 0x3fb8aa3b, v9
	s_waitcnt lgkmcnt(0)
	v_mfma_f32_16x16x32_bf16 v[176:179], v[180:183], v[176:179], v[196:199]
	s_waitcnt vmcnt(3)
	ds_write_b128 v75, v[188:191]
	s_waitcnt vmcnt(2)
	ds_write_b128 v75, v[192:195] offset:9216
	s_waitcnt lgkmcnt(0)
	s_barrier
	v_exp_f32_e32 v106, v9
	v_sub_f32_e32 v9, v108, v136
	ds_read2_b64 v[180:183], v8 offset1:4
	v_mul_f32_e32 v9, 0x3fb8aa3b, v9
	v_exp_f32_e32 v108, v9
	v_sub_f32_e32 v9, v112, v136
	v_mul_f32_e32 v9, 0x3fb8aa3b, v9
	v_exp_f32_e32 v109, v9
	v_lshl_add_u64 v[168:169], s[18:19], 1, v[78:79]
	v_cvt_pk_bf16_f32 v188, v103, v105
	v_cvt_pk_bf16_f32 v189, v107, v108
	v_cvt_pk_bf16_f32 v190, v102, v104
	v_cvt_pk_bf16_f32 v191, v106, v109
	v_lshl_add_u64 v[192:193], v[168:169], 0, v[70:71]
	ds_read2_b64 v[110:113], v7 offset0:32 offset1:36
	s_waitcnt lgkmcnt(1)
	v_mfma_f32_16x16x32_bf16 v[180:183], v[180:183], v[188:191], v[184:187]
	v_lshl_add_u64 v[168:169], v[168:169], 0, v[80:81]
	v_sub_f32_e32 v9, v115, v136
	v_mul_f32_e32 v9, 0x3fb8aa3b, v9
	ds_read2_b64 v[184:187], v6 offset0:64 offset1:68
	global_load_dwordx4 v[192:195], v[192:193], off
	s_nop 0
	global_load_dwordx4 v[196:199], v[168:169], off
	s_waitcnt lgkmcnt(1)
	v_mfma_f32_16x16x32_bf16 v[164:167], v[110:113], v[188:191], v[164:167]
	ds_read2_b64 v[110:113], v158 offset0:96 offset1:100
	s_waitcnt vmcnt(3)
	ds_write_b128 v75, v[200:203] offset:18432
	s_waitcnt vmcnt(2)
	ds_write_b128 v75, v[204:207] offset:27648
	s_waitcnt lgkmcnt(2)
	v_mfma_f32_16x16x32_bf16 v[176:179], v[110:113], v[188:191], v[176:179]
	v_exp_f32_e32 v111, v9
	v_sub_f32_e32 v9, v121, v136
	v_mul_f32_e32 v9, 0x3fb8aa3b, v9
	v_exp_f32_e32 v110, v9
	v_sub_f32_e32 v9, v114, v136
	v_mul_f32_e32 v9, 0x3fb8aa3b, v9
	v_exp_f32_e32 v113, v9
	v_sub_f32_e32 v9, v119, v136
	v_mul_f32_e32 v9, 0x3fb8aa3b, v9
	v_exp_f32_e32 v112, v9
	v_sub_f32_e32 v9, v118, v136
	v_mul_f32_e32 v9, 0x3fb8aa3b, v9
	v_exp_f32_e32 v115, v9
	v_sub_f32_e32 v9, v124, v136
	v_mul_f32_e32 v9, 0x3fb8aa3b, v9
	v_exp_f32_e32 v114, v9
	v_sub_f32_e32 v9, v117, v136
	v_mul_f32_e32 v9, 0x3fb8aa3b, v9
	v_mfma_f32_16x16x32_bf16 v[172:175], v[184:187], v[188:191], v[172:175]
	s_waitcnt lgkmcnt(0)
	s_barrier
	v_exp_f32_e32 v116, v9
	ds_read2_b64 v[184:187], v160 offset1:4
	v_sub_f32_e32 v9, v120, v136
	ds_read2_b64 v[118:121], v159 offset0:32 offset1:36
	v_mul_f32_e32 v9, 0x3fb8aa3b, v9
	v_exp_f32_e32 v117, v9
	v_lshl_add_u64 v[168:169], s[20:21], 1, v[78:79]
	v_lshl_add_u64 v[200:201], v[168:169], 0, v[70:71]
	v_cvt_pk_bf16_f32 v188, v111, v113
	v_cvt_pk_bf16_f32 v189, v115, v116
	v_cvt_pk_bf16_f32 v190, v110, v112
	v_cvt_pk_bf16_f32 v191, v114, v117
	v_lshl_add_u64 v[168:169], v[168:169], 0, v[80:81]
	v_sub_f32_e32 v9, v123, v136
	s_waitcnt lgkmcnt(1)
	v_mfma_f32_16x16x32_bf16 v[180:183], v[184:187], v[188:191], v[180:183]
	global_load_dwordx4 v[184:187], v[200:201], off
	s_nop 0
	global_load_dwordx4 v[200:203], v[168:169], off
	v_mul_f32_e32 v9, 0x3fb8aa3b, v9
	v_lshl_add_u64 v[168:169], s[22:23], 1, v[78:79]
	s_waitcnt lgkmcnt(0)
	v_mfma_f32_16x16x32_bf16 v[164:167], v[118:121], v[188:191], v[164:167]
	ds_read2_b64 v[118:121], v161 offset0:64 offset1:68
	v_fma_f32 v62, v62, s74, -v136
	v_fma_f32 v63, v63, s74, -v136
	s_waitcnt lgkmcnt(0)
	v_mfma_f32_16x16x32_bf16 v[172:175], v[118:121], v[188:191], v[172:175]
	ds_read2_b64 v[118:121], v162 offset0:96 offset1:100
	s_waitcnt vmcnt(3)
	ds_write_b128 v75, v[192:195]
	s_waitcnt vmcnt(2)
	ds_write_b128 v75, v[196:199] offset:9216
	s_waitcnt lgkmcnt(0)
	v_mfma_f32_16x16x32_bf16 v[176:179], v[118:121], v[188:191], v[176:179]
	v_exp_f32_e32 v119, v9
	v_sub_f32_e32 v9, v129, v136
	v_mul_f32_e32 v9, 0x3fb8aa3b, v9
	v_exp_f32_e32 v118, v9
	v_sub_f32_e32 v9, v122, v136
	v_mul_f32_e32 v9, 0x3fb8aa3b, v9
	v_exp_f32_e32 v121, v9
	v_sub_f32_e32 v9, v127, v136
	v_mul_f32_e32 v9, 0x3fb8aa3b, v9
	v_exp_f32_e32 v120, v9
	v_sub_f32_e32 v9, v126, v136
	v_mul_f32_e32 v9, 0x3fb8aa3b, v9
	v_exp_f32_e32 v123, v9
	v_sub_f32_e32 v9, v133, v136
	v_mul_f32_e32 v9, 0x3fb8aa3b, v9
	s_barrier
; #define LAS __attribute__((address_space(3)))
; __device__ __forceinline__ unsigned cvt_pk_bf16(float lo, float hi) { const float __attribute__((ext_vector_type(2))) v = {lo, hi}; return __builtin_bit_cast(unsigned, __builtin_convertvector(v, bf16x2_t)); }
; template <bool LOCAL>
; __device__ __forceinline__ void na_unit(const bf16* P, const bf16* VT, bf16* YCAT, const LAS float* rpb_l, LAS bf16* buf, int b, int gr, int hp, int qblk, int tid) {
;     ...
;             if (LOCAL && c < 8) {
;                 float p[8];
; #pragma unroll
;                 for (int e = 0; e < 4; ++e) { p[e] = __expf(sl[2 * (c < 8 ? c : 0)][e] - m); p[4 + e] = __expf(sl[2 * (c < 8 ? c : 0) + 1][e] - m); }
; #pragma unroll
;                 for (int e = 0; e < 8; ++e) lsum += p[e];
;                 const bf16x8 pf = __builtin_bit_cast(bf16x8, (v4u){pg8::cvt_pk_bf16(p[0], p[1]), pg8::cvt_pk_bf16(p[2], p[3]), pg8::cvt_pk_bf16(p[4], p[5]), pg8::cvt_pk_bf16(p[6], p[7])});
; #pragma unroll
;                 for (int dt = 0; dt < 4; ++dt) { const LAS bf16* vp = cb + (16 * dt + fr) * 72 + kc0 + 4 * fq;
;                     o[dt] = __builtin_amdgcn_mfma_f32_16x16x32_bf16(frag44(vp, vp + 16), pf, o[dt], 0, 0, 0); }
;             } else {
;                 const int cc = c - NLOC;
; #pragma unroll
;                 for (int p2 = 0; p2 < 2; ++p2) {
;                     float p[8];
; #pragma unroll
;                     for (int e = 0; e < 4; ++e) { p[e] = __expf(sc[4 * (cc >= 0 ? cc : 0) + 2 * p2][e] - m); p[4 + e] = __expf(sc[4 * (cc >= 0 ? cc : 0) + 2 * p2 + 1][e] - m); }
; #pragma unroll
;                     for (int e = 0; e < 8; ++e) lsum += p[e];
;                     const bf16x8 pf = __builtin_bit_cast(bf16x8, (v4u){pg8::cvt_pk_bf16(p[0], p[1]), pg8::cvt_pk_bf16(p[2], p[3]), pg8::cvt_pk_bf16(p[4], p[5]), pg8::cvt_pk_bf16(p[6], p[7])});
; #pragma unroll
;                     for (int dt = 0; dt < 4; ++dt) { const LAS bf16* vp = cb + (16 * dt + fr) * 72 + 32 * p2 + 4 * fq;
;                         o[dt] = __builtin_amdgcn_mfma_f32_16x16x32_bf16(frag44(vp, vp + 16), pf, o[dt], 0, 0, 0); }
;                 }
;             }
;         }
;         if (sidx + 1 < 2 * NCH) NA_STORE(sidx + 1);
;         __syncthreads();
	v_exp_f32_e32 v122, v9
	v_sub_f32_e32 v9, v125, v136
	ds_read2_b64 v[188:191], v8 offset1:4
	v_mul_f32_e32 v9, 0x3fb8aa3b, v9
	v_exp_f32_e32 v124, v9
	v_sub_f32_e32 v9, v128, v136
	v_mul_f32_e32 v9, 0x3fb8aa3b, v9
	v_exp_f32_e32 v125, v9
	v_cvt_pk_bf16_f32 v192, v119, v121
	v_cvt_pk_bf16_f32 v193, v123, v124
	v_cvt_pk_bf16_f32 v194, v118, v120
	v_cvt_pk_bf16_f32 v195, v122, v125
	v_lshl_add_u64 v[196:197], v[168:169], 0, v[70:71]
	ds_read2_b64 v[126:129], v7 offset0:32 offset1:36
	s_waitcnt lgkmcnt(1)
	v_mfma_f32_16x16x32_bf16 v[180:183], v[188:191], v[192:195], v[180:183]
	ds_read2_b64 v[188:191], v6 offset0:64 offset1:68
	v_lshl_add_u64 v[168:169], v[168:169], 0, v[80:81]
	global_load_dwordx4 v[196:199], v[196:197], off
	s_nop 0
	global_load_dwordx4 v[204:207], v[168:169], off
	s_waitcnt lgkmcnt(1)
	v_mfma_f32_16x16x32_bf16 v[164:167], v[126:129], v[192:195], v[164:167]
	ds_read2_b64 v[126:129], v158 offset0:96 offset1:100
	v_sub_f32_e32 v9, v131, v136
	v_mul_f32_e32 v9, 0x3fb8aa3b, v9
	s_waitcnt lgkmcnt(0)
	v_mfma_f32_16x16x32_bf16 v[176:179], v[126:129], v[192:195], v[176:179]
	v_exp_f32_e32 v127, v9
	v_sub_f32_e32 v9, v139, v136
	v_mul_f32_e32 v9, 0x3fb8aa3b, v9
	v_exp_f32_e32 v126, v9
	v_sub_f32_e32 v9, v130, v136
	v_mul_f32_e32 v9, 0x3fb8aa3b, v9
	v_exp_f32_e32 v129, v9
	v_sub_f32_e32 v9, v137, v136
	v_mul_f32_e32 v9, 0x3fb8aa3b, v9
	v_exp_f32_e32 v128, v9
	v_sub_f32_e32 v9, v135, v136
	v_mul_f32_e32 v9, 0x3fb8aa3b, v9
	v_exp_f32_e32 v131, v9
	v_sub_f32_e32 v9, v142, v136
	v_mul_f32_e32 v9, 0x3fb8aa3b, v9
	v_mfma_f32_16x16x32_bf16 v[172:175], v[188:191], v[192:195], v[172:175]
	s_waitcnt vmcnt(3)
	ds_write_b128 v75, v[184:187] offset:18432
	s_waitcnt vmcnt(2)
	ds_write_b128 v75, v[200:203] offset:27648
	s_waitcnt lgkmcnt(0)
	s_barrier
	v_exp_f32_e32 v130, v9
	v_sub_f32_e32 v9, v134, v136
	ds_read2_b64 v[184:187], v160 offset1:4
	ds_read2_b64 v[188:191], v159 offset0:32 offset1:36
	v_mul_f32_e32 v9, 0x3fb8aa3b, v9
	v_exp_f32_e32 v133, v9
	v_sub_f32_e32 v9, v138, v136
	v_mul_f32_e32 v9, 0x3fb8aa3b, v9
	v_exp_f32_e32 v134, v9
	v_lshl_add_u64 v[168:169], s[24:25], 1, v[78:79]
	v_lshl_add_u64 v[200:201], v[168:169], 0, v[70:71]
	v_cvt_pk_bf16_f32 v192, v127, v129
	v_cvt_pk_bf16_f32 v193, v131, v133
	v_cvt_pk_bf16_f32 v194, v126, v128
	v_cvt_pk_bf16_f32 v195, v130, v134
	v_lshl_add_u64 v[138:139], v[168:169], 0, v[80:81]
	v_sub_f32_e32 v9, v141, v136
	s_waitcnt lgkmcnt(1)
	v_mfma_f32_16x16x32_bf16 v[180:183], v[184:187], v[192:195], v[180:183]
	global_load_dwordx4 v[184:187], v[200:201], off
	s_nop 0
	global_load_dwordx4 v[200:203], v[138:139], off
	v_mul_f32_e32 v9, 0x3fb8aa3b, v9
	v_exp_f32_e32 v137, v9
	s_waitcnt lgkmcnt(0)
	v_mfma_f32_16x16x32_bf16 v[164:167], v[188:191], v[192:195], v[164:167]
	ds_read2_b64 v[188:191], v161 offset0:64 offset1:68
	v_sub_f32_e32 v9, v147, v136
	v_mul_f32_e32 v9, 0x3fb8aa3b, v9
	s_waitcnt lgkmcnt(0)
	v_mfma_f32_16x16x32_bf16 v[172:175], v[188:191], v[192:195], v[172:175]
	ds_read2_b64 v[188:191], v162 offset0:96 offset1:100
	v_exp_f32_e32 v135, v9
	v_sub_f32_e32 v9, v140, v136
	v_mul_f32_e32 v9, 0x3fb8aa3b, v9
	v_exp_f32_e32 v139, v9
	v_sub_f32_e32 v9, v145, v136
	v_mul_f32_e32 v9, 0x3fb8aa3b, v9
	v_exp_f32_e32 v138, v9
	v_sub_f32_e32 v9, v144, v136
	v_mul_f32_e32 v9, 0x3fb8aa3b, v9
	s_waitcnt lgkmcnt(0)
	v_mfma_f32_16x16x32_bf16 v[176:179], v[188:191], v[192:195], v[176:179]
	s_waitcnt vmcnt(3)
	ds_write_b128 v75, v[196:199]
	s_waitcnt vmcnt(2)
	ds_write_b128 v75, v[204:207] offset:9216
	s_waitcnt lgkmcnt(0)
	s_barrier
	v_exp_f32_e32 v141, v9
	v_sub_f32_e32 v9, v150, v136
	ds_read2_b64 v[188:191], v8 offset1:4
	v_mul_f32_e32 v9, 0x3fb8aa3b, v9
	ds_read2_b64 v[192:195], v7 offset0:32 offset1:36
	v_exp_f32_e32 v140, v9
	v_sub_f32_e32 v9, v143, v136
	v_sub_f32_e32 v8, v146, v136
	v_mul_f32_e32 v9, 0x3fb8aa3b, v9
	v_mul_f32_e32 v8, 0x3fb8aa3b, v8
	v_exp_f32_e32 v142, v9
	v_exp_f32_e32 v143, v8
	v_cvt_pk_bf16_f32 v144, v137, v139
	v_cvt_pk_bf16_f32 v146, v135, v138
	v_cvt_pk_bf16_f32 v145, v141, v142
	v_cvt_pk_bf16_f32 v147, v140, v143
	v_lshl_add_u64 v[8:9], s[26:27], 1, v[78:79]
	v_fma_f32 v64, v64, s74, -v136
	s_waitcnt lgkmcnt(1)
	v_mfma_f32_16x16x32_bf16 v[180:183], v[188:191], v[144:147], v[180:183]
	ds_read2_b64 v[188:191], v6 offset0:64 offset1:68
	v_lshl_add_u64 v[6:7], v[8:9], 0, v[70:71]
	v_lshl_add_u64 v[8:9], v[8:9], 0, v[80:81]
	s_waitcnt lgkmcnt(1)
	v_mfma_f32_16x16x32_bf16 v[164:167], v[192:195], v[144:147], v[164:167]
	global_load_dwordx4 v[192:195], v[6:7], off
	global_load_dwordx4 v[196:199], v[8:9], off
	ds_read2_b64 v[78:81], v158 offset0:96 offset1:100
	s_waitcnt vmcnt(3)
	ds_write_b128 v75, v[184:187] offset:18432
	s_waitcnt vmcnt(2)
	ds_write_b128 v75, v[200:203] offset:27648
	s_waitcnt lgkmcnt(3)
	v_mfma_f32_16x16x32_bf16 v[172:175], v[188:191], v[144:147], v[172:175]
	s_waitcnt lgkmcnt(0)
	s_barrier
; #define LAS __attribute__((address_space(3)))
; __device__ __forceinline__ unsigned cvt_pk_bf16(float lo, float hi) { const float __attribute__((ext_vector_type(2))) v = {lo, hi}; return __builtin_bit_cast(unsigned, __builtin_convertvector(v, bf16x2_t)); }
; template <bool LOCAL>
; __device__ __forceinline__ void na_unit(const bf16* P, const bf16* VT, bf16* YCAT, const LAS float* rpb_l, LAS bf16* buf, int b, int gr, int hp, int qblk, int tid) {
;     ...
;             if (LOCAL && c < 8) {
;                 float p[8];
; #pragma unroll
;                 for (int e = 0; e < 4; ++e) { p[e] = __expf(sl[2 * (c < 8 ? c : 0)][e] - m); p[4 + e] = __expf(sl[2 * (c < 8 ? c : 0) + 1][e] - m); }
; #pragma unroll
;                 for (int e = 0; e < 8; ++e) lsum += p[e];
;                 const bf16x8 pf = __builtin_bit_cast(bf16x8, (v4u){pg8::cvt_pk_bf16(p[0], p[1]), pg8::cvt_pk_bf16(p[2], p[3]), pg8::cvt_pk_bf16(p[4], p[5]), pg8::cvt_pk_bf16(p[6], p[7])});
; #pragma unroll
;                 for (int dt = 0; dt < 4; ++dt) { const LAS bf16* vp = cb + (16 * dt + fr) * 72 + kc0 + 4 * fq;
;                     o[dt] = __builtin_amdgcn_mfma_f32_16x16x32_bf16(frag44(vp, vp + 16), pf, o[dt], 0, 0, 0); }
;             } else {
;                 const int cc = c - NLOC;
; #pragma unroll
;                 for (int p2 = 0; p2 < 2; ++p2) {
;                     float p[8];
; #pragma unroll
;                     for (int e = 0; e < 4; ++e) { p[e] = __expf(sc[4 * (cc >= 0 ? cc : 0) + 2 * p2][e] - m); p[4 + e] = __expf(sc[4 * (cc >= 0 ? cc : 0) + 2 * p2 + 1][e] - m); }
; #pragma unroll
;                     for (int e = 0; e < 8; ++e) lsum += p[e];
;                     const bf16x8 pf = __builtin_bit_cast(bf16x8, (v4u){pg8::cvt_pk_bf16(p[0], p[1]), pg8::cvt_pk_bf16(p[2], p[3]), pg8::cvt_pk_bf16(p[4], p[5]), pg8::cvt_pk_bf16(p[6], p[7])});
; #pragma unroll
;                     for (int dt = 0; dt < 4; ++dt) { const LAS bf16* vp = cb + (16 * dt + fr) * 72 + 32 * p2 + 4 * fq;
;                         o[dt] = __builtin_amdgcn_mfma_f32_16x16x32_bf16(frag44(vp, vp + 16), pf, o[dt], 0, 0, 0); }
;                 }
;             }
;         }
;         if (sidx + 1 < 2 * NCH) NA_STORE(sidx + 1);
;         __syncthreads();
	v_mfma_f32_16x16x32_bf16 v[176:179], v[78:81], v[144:147], v[176:179]
	v_sub_f32_e32 v70, v149, v136
	v_sub_f32_e32 v79, v148, v136
	v_sub_f32_e32 v81, v152, v136
	v_sub_f32_e32 v145, v151, v136
	ds_read2_b64 v[148:151], v160 offset1:4
	v_mul_f32_e32 v70, 0x3fb8aa3b, v70
	v_mul_f32_e32 v79, 0x3fb8aa3b, v79
	v_mul_f32_e32 v81, 0x3fb8aa3b, v81
	v_mul_f32_e32 v145, 0x3fb8aa3b, v145
	v_exp_f32_e32 v78, v70
	v_sub_f32_e32 v70, v155, v136
	v_exp_f32_e32 v80, v79
	v_sub_f32_e32 v79, v153, v136
	v_exp_f32_e32 v144, v81
	v_sub_f32_e32 v81, v157, v136
	v_exp_f32_e32 v146, v145
	v_sub_f32_e32 v145, v154, v136
	v_mul_f32_e32 v70, 0x3fb8aa3b, v70
	v_mul_f32_e32 v79, 0x3fb8aa3b, v79
	v_mul_f32_e32 v81, 0x3fb8aa3b, v81
	v_mul_f32_e32 v145, 0x3fb8aa3b, v145
	v_exp_f32_e32 v70, v70
	v_exp_f32_e32 v79, v79
	v_exp_f32_e32 v81, v81
	v_exp_f32_e32 v145, v145
	v_cvt_pk_bf16_f32 v152, v78, v80
	v_cvt_pk_bf16_f32 v153, v144, v146
	v_cvt_pk_bf16_f32 v154, v70, v79
	v_cvt_pk_bf16_f32 v155, v81, v145
	v_fma_f32 v65, v65, s74, -v136
	v_mul_f32_e32 v62, 0x3fb8aa3b, v62
	s_waitcnt lgkmcnt(0)
	v_mfma_f32_16x16x32_bf16 v[148:151], v[148:151], v[152:155], v[180:183]
	v_mul_f32_e32 v63, 0x3fb8aa3b, v63
	v_mul_f32_e32 v64, 0x3fb8aa3b, v64
	v_mul_f32_e32 v65, 0x3fb8aa3b, v65
	ds_read2_b64 v[180:183], v159 offset0:32 offset1:36
	ds_read2_b64 v[158:161], v161 offset0:64 offset1:68
	s_waitcnt lgkmcnt(0)
	v_mfma_f32_16x16x32_bf16 v[158:161], v[158:161], v[152:155], v[172:175]
	s_nop 2
	ds_read2_b64 v[172:175], v162 offset0:96 offset1:100
	v_exp_f32_e32 v147, v62
	v_fma_f32 v62, v66, s74, -v136
	v_mfma_f32_16x16x32_bf16 v[164:167], v[180:183], v[152:155], v[164:167]
	global_load_dwordx4 v[180:183], v[6:7], off offset:128
	global_load_dwordx4 v[184:187], v[8:9], off offset:128
	s_waitcnt vmcnt(3)
	ds_write_b128 v75, v[192:195]
	s_waitcnt vmcnt(2)
	ds_write_b128 v75, v[196:199] offset:9216
	s_waitcnt lgkmcnt(0)
	v_mfma_f32_16x16x32_bf16 v[152:155], v[172:175], v[152:155], v[176:179]
	s_barrier
	ds_read2_b64 v[172:175], v156 offset1:4
	v_exp_f32_e32 v66, v63
	v_fma_f32 v63, v67, s74, -v136
	v_exp_f32_e32 v67, v64
	v_fma_f32 v64, v68, s74, -v136
	v_exp_f32_e32 v68, v65
	v_fma_f32 v65, v69, s74, -v136
	v_mul_f32_e32 v62, 0x3fb8aa3b, v62
	v_mul_f32_e32 v63, 0x3fb8aa3b, v63
	v_mul_f32_e32 v64, 0x3fb8aa3b, v64
	v_mul_f32_e32 v65, 0x3fb8aa3b, v65
	v_exp_f32_e32 v62, v62
	v_exp_f32_e32 v63, v63
	v_exp_f32_e32 v64, v64
	v_exp_f32_e32 v65, v65
	v_cvt_pk_bf16_f32 v176, v147, v66
	v_cvt_pk_bf16_f32 v177, v67, v68
	v_cvt_pk_bf16_f32 v178, v62, v63
	v_cvt_pk_bf16_f32 v179, v64, v65
	v_add_u32_e32 v157, 0x800, v156
	v_add_u32_e32 v192, 0x1000, v156
	s_waitcnt lgkmcnt(0)
	v_mfma_f32_16x16x32_bf16 v[148:151], v[172:175], v[176:179], v[148:151]
	ds_read2_b64 v[172:175], v157 offset0:32 offset1:36
	v_add_u32_e32 v193, 0x1800, v156
	v_fma_f32 v58, v58, s74, -v136
	s_waitcnt lgkmcnt(0)
	v_mfma_f32_16x16x32_bf16 v[162:165], v[172:175], v[176:179], v[164:167]
	s_nop 2
	ds_read2_b64 v[166:169], v192 offset0:64 offset1:68
	v_fma_f32 v54, v54, s74, -v136
	v_fma_f32 v59, v59, s74, -v136
	s_waitcnt lgkmcnt(0)
	v_mfma_f32_16x16x32_bf16 v[158:161], v[166:169], v[176:179], v[158:161]
	ds_read2_b64 v[166:169], v193 offset0:96 offset1:100
	v_fma_f32 v55, v55, s74, -v136
	v_fma_f32 v60, v60, s74, -v136
	s_waitcnt lgkmcnt(0)
	v_mfma_f32_16x16x32_bf16 v[152:155], v[166:169], v[176:179], v[152:155]
	ds_read2_b64 v[166:169], v156 offset0:8 offset1:12
	v_fma_f32 v56, v56, s74, -v136
	v_fma_f32 v61, v61, s74, -v136
	v_fma_f32 v57, v57, s74, -v136
	v_mul_f32_e32 v58, 0x3fb8aa3b, v58
	v_mul_f32_e32 v54, 0x3fb8aa3b, v54
	v_mul_f32_e32 v59, 0x3fb8aa3b, v59
	v_mul_f32_e32 v55, 0x3fb8aa3b, v55
	v_mul_f32_e32 v60, 0x3fb8aa3b, v60
	v_mul_f32_e32 v56, 0x3fb8aa3b, v56
	v_mul_f32_e32 v61, 0x3fb8aa3b, v61
	v_mul_f32_e32 v57, 0x3fb8aa3b, v57
	v_exp_f32_e32 v58, v58
	v_exp_f32_e32 v54, v54
	v_exp_f32_e32 v59, v59
	v_exp_f32_e32 v55, v55
	v_exp_f32_e32 v60, v60
	v_exp_f32_e32 v56, v56
	v_exp_f32_e32 v61, v61
	v_exp_f32_e32 v57, v57
	v_cvt_pk_bf16_f32 v172, v58, v59
	v_cvt_pk_bf16_f32 v174, v54, v55
	v_cvt_pk_bf16_f32 v173, v60, v61
	v_cvt_pk_bf16_f32 v175, v56, v57
	v_fma_f32 v46, v46, s74, -v136
	v_fma_f32 v47, v47, s74, -v136
	s_waitcnt lgkmcnt(0)
	v_mfma_f32_16x16x32_bf16 v[148:151], v[166:169], v[172:175], v[148:151]
	ds_read2_b64 v[166:169], v157 offset0:40 offset1:44
	v_fma_f32 v48, v48, s74, -v136
	v_mul_f32_e32 v46, 0x3fb8aa3b, v46
	s_waitcnt lgkmcnt(0)
	v_mfma_f32_16x16x32_bf16 v[162:165], v[166:169], v[172:175], v[162:165]
	ds_read2_b64 v[166:169], v192 offset0:72 offset1:76
	v_mul_f32_e32 v47, 0x3fb8aa3b, v47
	v_mul_f32_e32 v48, 0x3fb8aa3b, v48
	s_waitcnt lgkmcnt(0)
	v_mfma_f32_16x16x32_bf16 v[158:161], v[166:169], v[172:175], v[158:161]
	ds_read2_b64 v[166:169], v193 offset0:104 offset1:108
	v_exp_f32_e32 v69, v46
	v_fma_f32 v46, v50, s74, -v136
	v_exp_f32_e32 v50, v47
	v_fma_f32 v47, v51, s74, -v136
	v_exp_f32_e32 v51, v48
	v_fma_f32 v48, v52, s74, -v136
	v_add_u32_e32 v52, 0x4800, v156
	global_load_dwordx4 v[176:179], v[6:7], off offset:256
	global_load_dwordx4 v[188:191], v[8:9], off offset:256
	s_waitcnt lgkmcnt(0)
	v_mfma_f32_16x16x32_bf16 v[152:155], v[166:169], v[172:175], v[152:155]
	s_waitcnt vmcnt(3)
	ds_write_b128 v75, v[180:183] offset:18432
	s_waitcnt vmcnt(2)
	ds_write_b128 v75, v[184:187] offset:27648
	s_waitcnt lgkmcnt(0)
	s_barrier
; #define LAS __attribute__((address_space(3)))
; __device__ __forceinline__ unsigned cvt_pk_bf16(float lo, float hi) { const float __attribute__((ext_vector_type(2))) v = {lo, hi}; return __builtin_bit_cast(unsigned, __builtin_convertvector(v, bf16x2_t)); }
; #define NA_STORE(sidx) do { LAS bf16* d_ = buf + ((sidx) & 1) * 9216; _Pragma("unroll") for (int q_ = 0; q_ < 2; ++q_) *(LAS v4u*)(d_ + q_ * 4608 + lrow * 72 + lseg * 8) = ld[(sidx) & 1][q_]; } while (0)
; template <bool LOCAL>
; __device__ __forceinline__ void na_unit(const bf16* P, const bf16* VT, bf16* YCAT, const LAS float* rpb_l, LAS bf16* buf, int b, int gr, int hp, int qblk, int tid) {
;     ...
;             } else {
;                 const int cc = c - NLOC;
; #pragma unroll
;                 for (int p2 = 0; p2 < 2; ++p2) {
;                     float p[8];
; #pragma unroll
;                     for (int e = 0; e < 4; ++e) { p[e] = __expf(sc[4 * (cc >= 0 ? cc : 0) + 2 * p2][e] - m); p[4 + e] = __expf(sc[4 * (cc >= 0 ? cc : 0) + 2 * p2 + 1][e] - m); }
; #pragma unroll
;                     for (int e = 0; e < 8; ++e) lsum += p[e];
;                     const bf16x8 pf = __builtin_bit_cast(bf16x8, (v4u){pg8::cvt_pk_bf16(p[0], p[1]), pg8::cvt_pk_bf16(p[2], p[3]), pg8::cvt_pk_bf16(p[4], p[5]), pg8::cvt_pk_bf16(p[6], p[7])});
; #pragma unroll
;                     for (int dt = 0; dt < 4; ++dt) { const LAS bf16* vp = cb + (16 * dt + fr) * 72 + 32 * p2 + 4 * fq;
;                         o[dt] = __builtin_amdgcn_mfma_f32_16x16x32_bf16(frag44(vp, vp + 16), pf, o[dt], 0, 0, 0); }
;                 }
;             }
;         }
;         if (sidx + 1 < 2 * NCH) NA_STORE(sidx + 1);
;         __syncthreads();
	v_fma_f32 v49, v49, s74, -v136
	ds_read2_b64 v[166:169], v52 offset1:4
	v_mul_f32_e32 v49, 0x3fb8aa3b, v49
	v_exp_f32_e32 v180, v49
	v_fma_f32 v49, v53, s74, -v136
	v_mul_f32_e32 v46, 0x3fb8aa3b, v46
	v_mul_f32_e32 v47, 0x3fb8aa3b, v47
	v_mul_f32_e32 v48, 0x3fb8aa3b, v48
	v_mul_f32_e32 v49, 0x3fb8aa3b, v49
	v_exp_f32_e32 v46, v46
	v_exp_f32_e32 v47, v47
	v_exp_f32_e32 v48, v48
	v_exp_f32_e32 v53, v49
	v_cvt_pk_bf16_f32 v172, v69, v50
	v_cvt_pk_bf16_f32 v173, v51, v180
	v_cvt_pk_bf16_f32 v174, v46, v47
	v_cvt_pk_bf16_f32 v175, v48, v53
	v_add_u32_e32 v181, 0x5000, v156
	v_add_u32_e32 v182, 0x5800, v156
	s_waitcnt lgkmcnt(0)
	v_mfma_f32_16x16x32_bf16 v[148:151], v[166:169], v[172:175], v[148:151]
	ds_read2_b64 v[166:169], v181 offset0:32 offset1:36
	v_add_u32_e32 v49, 0x6000, v156
	v_fma_f32 v38, v38, s74, -v136
	s_waitcnt lgkmcnt(0)
	v_mfma_f32_16x16x32_bf16 v[162:165], v[166:169], v[172:175], v[162:165]
	ds_read2_b64 v[166:169], v182 offset0:64 offset1:68
	v_mul_f32_e32 v38, 0x3fb8aa3b, v38
	v_fma_f32 v42, v42, s74, -v136
	s_waitcnt lgkmcnt(0)
	v_mfma_f32_16x16x32_bf16 v[158:161], v[166:169], v[172:175], v[158:161]
	ds_read2_b64 v[166:169], v49 offset0:96 offset1:100
	v_mul_f32_e32 v42, 0x3fb8aa3b, v42
	v_fma_f32 v30, v30, s74, -v136
	s_waitcnt lgkmcnt(0)
	v_mfma_f32_16x16x32_bf16 v[152:155], v[166:169], v[172:175], v[152:155]
	v_exp_f32_e32 v173, v38
	v_fma_f32 v38, v43, s74, -v136
	v_mul_f32_e32 v38, 0x3fb8aa3b, v38
	v_exp_f32_e32 v174, v38
	v_fma_f32 v38, v39, s74, -v136
	v_mul_f32_e32 v38, 0x3fb8aa3b, v38
	v_exp_f32_e32 v175, v38
	v_fma_f32 v38, v44, s74, -v136
	v_mul_f32_e32 v38, 0x3fb8aa3b, v38
	v_exp_f32_e32 v183, v38
	v_fma_f32 v38, v40, s74, -v136
	v_mul_f32_e32 v38, 0x3fb8aa3b, v38
	v_exp_f32_e32 v172, v42
	v_exp_f32_e32 v184, v38
	v_fma_f32 v38, v45, s74, -v136
	ds_read2_b64 v[42:45], v52 offset0:8 offset1:12
	v_mul_f32_e32 v38, 0x3fb8aa3b, v38
	v_exp_f32_e32 v185, v38
	v_fma_f32 v38, v41, s74, -v136
	v_mul_f32_e32 v38, 0x3fb8aa3b, v38
	v_exp_f32_e32 v186, v38
	v_cvt_pk_bf16_f32 v38, v172, v174
	v_cvt_pk_bf16_f32 v39, v183, v185
	v_cvt_pk_bf16_f32 v40, v173, v175
	v_cvt_pk_bf16_f32 v41, v184, v186
	v_mul_f32_e32 v30, 0x3fb8aa3b, v30
	v_fma_f32 v22, v22, s74, -v136
	s_waitcnt lgkmcnt(0)
	v_mfma_f32_16x16x32_bf16 v[42:45], v[42:45], v[38:41], v[148:151]
	v_mul_f32_e32 v22, 0x3fb8aa3b, v22
	v_fma_f32 v26, v26, s74, -v136
	v_mul_f32_e32 v26, 0x3fb8aa3b, v26
	ds_read2_b64 v[148:151], v181 offset0:40 offset1:44
	s_waitcnt lgkmcnt(0)
	v_mfma_f32_16x16x32_bf16 v[148:151], v[148:151], v[38:41], v[162:165]
	s_nop 2
	ds_read2_b64 v[162:165], v182 offset0:72 offset1:76
	v_fma_f32 v2, v2, s74, -v136
	v_mul_f32_e32 v2, 0x3fb8aa3b, v2
	s_waitcnt lgkmcnt(0)
	v_mfma_f32_16x16x32_bf16 v[158:161], v[162:165], v[38:41], v[158:161]
	ds_read2_b64 v[162:165], v49 offset0:104 offset1:108
	global_load_dwordx4 v[166:169], v[6:7], off offset:384
	s_nop 0
	global_load_dwordx4 v[6:9], v[8:9], off offset:384
	s_waitcnt vmcnt(3)
	ds_write_b128 v75, v[176:179]
	s_waitcnt vmcnt(2)
	ds_write_b128 v75, v[188:191] offset:9216
	s_waitcnt lgkmcnt(2)
	v_mfma_f32_16x16x32_bf16 v[38:41], v[162:165], v[38:41], v[152:155]
	v_exp_f32_e32 v162, v30
	v_fma_f32 v30, v34, s74, -v136
	v_mul_f32_e32 v30, 0x3fb8aa3b, v30
	v_exp_f32_e32 v163, v30
	v_fma_f32 v30, v31, s74, -v136
	v_mul_f32_e32 v30, 0x3fb8aa3b, v30
	v_exp_f32_e32 v164, v30
	v_fma_f32 v30, v35, s74, -v136
	v_mul_f32_e32 v30, 0x3fb8aa3b, v30
	v_exp_f32_e32 v165, v30
	v_fma_f32 v30, v32, s74, -v136
	v_mul_f32_e32 v30, 0x3fb8aa3b, v30
	v_exp_f32_e32 v176, v30
	v_fma_f32 v30, v36, s74, -v136
	v_mul_f32_e32 v30, 0x3fb8aa3b, v30
	v_exp_f32_e32 v177, v30
	v_fma_f32 v30, v33, s74, -v136
	s_waitcnt lgkmcnt(0)
	s_barrier
	v_mul_f32_e32 v34, 0x3fb8aa3b, v30
	ds_read2_b64 v[30:33], v156 offset1:4
	v_exp_f32_e32 v178, v34
	v_fma_f32 v34, v37, s74, -v136
	v_mul_f32_e32 v34, 0x3fb8aa3b, v34
	v_exp_f32_e32 v179, v34
	v_cvt_pk_bf16_f32 v34, v162, v164
	v_cvt_pk_bf16_f32 v35, v176, v178
	v_cvt_pk_bf16_f32 v36, v163, v165
	v_cvt_pk_bf16_f32 v37, v177, v179
	ds_read2_b64 v[152:155], v193 offset0:96 offset1:100
	v_fma_f32 v10, v10, s74, -v136
	s_waitcnt lgkmcnt(1)
	v_mfma_f32_16x16x32_bf16 v[30:33], v[30:33], v[34:37], v[42:45]
	v_mul_f32_e32 v10, 0x3fb8aa3b, v10
	s_nop 1
	ds_read2_b64 v[42:45], v157 offset0:32 offset1:36
	s_waitcnt lgkmcnt(0)
	v_mfma_f32_16x16x32_bf16 v[42:45], v[42:45], v[34:37], v[148:151]
	s_nop 2
	ds_read2_b64 v[148:151], v192 offset0:64 offset1:68
	s_waitcnt lgkmcnt(0)
	v_mfma_f32_16x16x32_bf16 v[148:151], v[148:151], v[34:37], v[158:161]
	v_mfma_f32_16x16x32_bf16 v[34:37], v[152:155], v[34:37], v[38:41]
	v_exp_f32_e32 v153, v22
	v_fma_f32 v22, v27, s74, -v136
	v_mul_f32_e32 v22, 0x3fb8aa3b, v22
	v_exp_f32_e32 v154, v22
	v_fma_f32 v22, v23, s74, -v136
	v_mul_f32_e32 v22, 0x3fb8aa3b, v22
	v_exp_f32_e32 v155, v22
	v_fma_f32 v22, v28, s74, -v136
	v_mul_f32_e32 v22, 0x3fb8aa3b, v22
	v_exp_f32_e32 v158, v22
	v_fma_f32 v22, v24, s74, -v136
	v_mul_f32_e32 v22, 0x3fb8aa3b, v22
	v_exp_f32_e32 v152, v26
	v_exp_f32_e32 v159, v22
	v_fma_f32 v22, v29, s74, -v136
	ds_read2_b64 v[26:29], v156 offset0:8 offset1:12
	v_mul_f32_e32 v22, 0x3fb8aa3b, v22
	v_exp_f32_e32 v156, v22
	v_fma_f32 v22, v25, s74, -v136
	v_mul_f32_e32 v22, 0x3fb8aa3b, v22
	v_exp_f32_e32 v160, v22
	v_cvt_pk_bf16_f32 v22, v152, v154
	v_cvt_pk_bf16_f32 v23, v158, v156
	v_cvt_pk_bf16_f32 v24, v153, v155
	v_cvt_pk_bf16_f32 v25, v159, v160
	ds_read2_b64 v[38:41], v192 offset0:72 offset1:76
	s_waitcnt lgkmcnt(1)
	v_mfma_f32_16x16x32_bf16 v[26:29], v[26:29], v[22:25], v[30:33]
	s_nop 2
	ds_read2_b64 v[30:33], v157 offset0:40 offset1:44
	s_waitcnt lgkmcnt(0)
	v_mfma_f32_16x16x32_bf16 v[30:33], v[30:33], v[22:25], v[42:45]
	s_nop 2
	ds_read2_b64 v[42:45], v193 offset0:104 offset1:108
	s_waitcnt vmcnt(1)
	ds_write_b128 v75, v[166:169] offset:18432
	s_waitcnt vmcnt(0)
	ds_write_b128 v75, v[6:9] offset:27648
	v_fma_f32 v6, v14, s74, -v136
	v_mul_f32_e32 v6, 0x3fb8aa3b, v6
	v_mfma_f32_16x16x32_bf16 v[38:41], v[38:41], v[22:25], v[148:151]
	s_waitcnt lgkmcnt(0)
	s_barrier
; #define LAS __attribute__((address_space(3)))
; __device__ __forceinline__ unsigned cvt_pk_bf16(float lo, float hi) { const float __attribute__((ext_vector_type(2))) v = {lo, hi}; return __builtin_bit_cast(unsigned, __builtin_convertvector(v, bf16x2_t)); }
; #define NA_STORE(sidx) do { LAS bf16* d_ = buf + ((sidx) & 1) * 9216; _Pragma("unroll") for (int q_ = 0; q_ < 2; ++q_) *(LAS v4u*)(d_ + q_ * 4608 + lrow * 72 + lseg * 8) = ld[(sidx) & 1][q_]; } while (0)
; template <bool LOCAL>
; __device__ __forceinline__ void na_unit(const bf16* P, const bf16* VT, bf16* YCAT, const LAS float* rpb_l, LAS bf16* buf, int b, int gr, int hp, int qblk, int tid) {
;     ...
;             } else {
;                 const int cc = c - NLOC;
; #pragma unroll
;                 for (int p2 = 0; p2 < 2; ++p2) {
;                     float p[8];
; #pragma unroll
;                     for (int e = 0; e < 4; ++e) { p[e] = __expf(sc[4 * (cc >= 0 ? cc : 0) + 2 * p2][e] - m); p[4 + e] = __expf(sc[4 * (cc >= 0 ? cc : 0) + 2 * p2 + 1][e] - m); }
; #pragma unroll
;                     for (int e = 0; e < 8; ++e) lsum += p[e];
;                     const bf16x8 pf = __builtin_bit_cast(bf16x8, (v4u){pg8::cvt_pk_bf16(p[0], p[1]), pg8::cvt_pk_bf16(p[2], p[3]), pg8::cvt_pk_bf16(p[4], p[5]), pg8::cvt_pk_bf16(p[6], p[7])});
; #pragma unroll
;                     for (int dt = 0; dt < 4; ++dt) { const LAS bf16* vp = cb + (16 * dt + fr) * 72 + 32 * p2 + 4 * fq;
;                         o[dt] = __builtin_amdgcn_mfma_f32_16x16x32_bf16(frag44(vp, vp + 16), pf, o[dt], 0, 0, 0); }
;                 }
;             }
;         }
;         if (sidx + 1 < 2 * NCH) NA_STORE(sidx + 1);
;         __syncthreads();
;     }
;     ...
;     lsum += __shfl_xor(lsum, 16); lsum += __shfl_xor(lsum, 32);
	v_mfma_f32_16x16x32_bf16 v[22:25], v[42:45], v[22:25], v[34:37]
	v_ashrrev_i32_e32 v75, 31, v74
	s_nop 1
	v_exp_f32_e32 v34, v6
	v_fma_f32 v6, v18, s74, -v136
	v_mul_f32_e32 v6, 0x3fb8aa3b, v6
	v_exp_f32_e32 v35, v6
	v_fma_f32 v6, v15, s74, -v136
	v_mul_f32_e32 v6, 0x3fb8aa3b, v6
	v_exp_f32_e32 v36, v6
	v_fma_f32 v6, v19, s74, -v136
	v_mul_f32_e32 v6, 0x3fb8aa3b, v6
	v_exp_f32_e32 v37, v6
	v_fma_f32 v6, v16, s74, -v136
	v_mul_f32_e32 v6, 0x3fb8aa3b, v6
	v_exp_f32_e32 v42, v6
	v_fma_f32 v6, v20, s74, -v136
	v_mul_f32_e32 v6, 0x3fb8aa3b, v6
	v_exp_f32_e32 v43, v6
	v_fma_f32 v6, v17, s74, -v136
	v_mul_f32_e32 v14, 0x3fb8aa3b, v6
	ds_read2_b64 v[6:9], v52 offset1:4
	v_exp_f32_e32 v44, v14
	v_fma_f32 v14, v21, s74, -v136
	v_mul_f32_e32 v14, 0x3fb8aa3b, v14
	v_exp_f32_e32 v45, v14
	v_cvt_pk_bf16_f32 v14, v34, v36
	v_cvt_pk_bf16_f32 v15, v42, v44
	v_cvt_pk_bf16_f32 v16, v35, v37
	v_cvt_pk_bf16_f32 v17, v43, v45
	ds_read2_b64 v[18:21], v181 offset0:32 offset1:36
	s_waitcnt lgkmcnt(1)
	v_mfma_f32_16x16x32_bf16 v[6:9], v[6:9], v[14:17], v[26:29]
	s_nop 2
	ds_read2_b64 v[26:29], v182 offset0:64 offset1:68
	s_waitcnt lgkmcnt(0)
	v_mfma_f32_16x16x32_bf16 v[26:29], v[26:29], v[14:17], v[38:41]
	s_nop 2
	v_add_f32_e32 v38, 0, v132
	v_add_f32_e32 v38, v96, v38
	v_add_f32_e32 v38, v95, v38
	v_add_f32_e32 v38, v99, v38
	v_add_f32_e32 v38, v92, v38
	v_add_f32_e32 v38, v91, v38
	v_add_f32_e32 v38, v94, v38
	v_add_f32_e32 v38, v93, v38
	v_add_f32_e32 v38, v86, v38
	v_add_f32_e32 v38, v90, v38
	v_add_f32_e32 v38, v98, v38
	v_add_f32_e32 v38, v100, v38
	v_add_f32_e32 v38, v76, v38
	v_add_f32_e32 v38, v87, v38
	v_add_f32_e32 v38, v97, v38
	v_add_f32_e32 v38, v101, v38
	v_add_f32_e32 v38, v103, v38
	v_add_f32_e32 v38, v105, v38
	v_add_f32_e32 v38, v107, v38
	v_add_f32_e32 v38, v108, v38
	v_add_f32_e32 v38, v102, v38
	v_add_f32_e32 v38, v104, v38
	v_add_f32_e32 v38, v106, v38
	v_add_f32_e32 v38, v109, v38
	v_add_f32_e32 v38, v111, v38
	v_add_f32_e32 v38, v113, v38
	v_add_f32_e32 v38, v115, v38
	v_add_f32_e32 v38, v116, v38
	v_add_f32_e32 v38, v110, v38
	v_add_f32_e32 v38, v112, v38
	v_add_f32_e32 v38, v114, v38
	v_add_f32_e32 v38, v117, v38
	v_add_f32_e32 v38, v119, v38
	v_add_f32_e32 v38, v121, v38
	v_add_f32_e32 v38, v123, v38
	v_add_f32_e32 v38, v124, v38
	v_add_f32_e32 v38, v118, v38
	v_add_f32_e32 v38, v120, v38
	v_add_f32_e32 v38, v122, v38
	v_add_f32_e32 v38, v125, v38
	v_add_f32_e32 v38, v127, v38
	v_add_f32_e32 v38, v129, v38
	v_add_f32_e32 v38, v131, v38
	v_add_f32_e32 v38, v133, v38
	v_add_f32_e32 v38, v126, v38
	v_add_f32_e32 v38, v128, v38
	v_add_f32_e32 v38, v130, v38
	v_add_f32_e32 v38, v134, v38
	v_add_f32_e32 v38, v137, v38
	v_add_f32_e32 v38, v139, v38
	v_add_f32_e32 v38, v141, v38
	v_add_f32_e32 v38, v142, v38
	v_add_f32_e32 v38, v135, v38
	v_add_f32_e32 v38, v138, v38
	v_add_f32_e32 v38, v140, v38
	v_add_f32_e32 v38, v143, v38
	v_add_f32_e32 v38, v78, v38
	v_add_f32_e32 v38, v80, v38
	v_add_f32_e32 v38, v144, v38
	v_add_f32_e32 v38, v146, v38
	v_add_f32_e32 v38, v70, v38
	v_add_f32_e32 v38, v79, v38
	v_add_f32_e32 v38, v81, v38
	v_add_f32_e32 v38, v145, v38
	v_add_f32_e32 v38, v147, v38
	v_add_f32_e32 v38, v66, v38
	v_add_f32_e32 v38, v67, v38
	v_add_f32_e32 v38, v68, v38
	v_add_f32_e32 v38, v62, v38
	v_add_f32_e32 v38, v63, v38
	v_add_f32_e32 v38, v64, v38
	v_add_f32_e32 v38, v65, v38
	v_add_f32_e32 v38, v58, v38
	v_add_f32_e32 v38, v59, v38
	v_add_f32_e32 v38, v60, v38
	v_add_f32_e32 v38, v61, v38
	v_add_f32_e32 v38, v54, v38
	v_add_f32_e32 v38, v55, v38
	v_add_f32_e32 v38, v56, v38
	v_add_f32_e32 v38, v57, v38
	v_add_f32_e32 v38, v69, v38
	v_add_f32_e32 v38, v50, v38
	v_add_f32_e32 v38, v51, v38
	v_add_f32_e32 v38, v180, v38
	v_add_f32_e32 v38, v46, v38
	v_add_f32_e32 v38, v47, v38
	v_add_f32_e32 v38, v48, v38
	v_add_f32_e32 v38, v53, v38
	v_add_f32_e32 v38, v172, v38
	v_mfma_f32_16x16x32_bf16 v[18:21], v[18:21], v[14:17], v[30:33]
	v_add_f32_e32 v38, v174, v38
	v_add_f32_e32 v38, v183, v38
	v_add_f32_e32 v38, v185, v38
	ds_read2_b64 v[30:33], v49 offset0:96 offset1:100
	v_add_f32_e32 v38, v173, v38
	v_add_f32_e32 v38, v175, v38
	v_add_f32_e32 v38, v184, v38
	v_add_f32_e32 v38, v186, v38
	v_add_f32_e32 v38, v162, v38
	v_add_f32_e32 v38, v164, v38
	s_waitcnt lgkmcnt(0)
	v_mfma_f32_16x16x32_bf16 v[14:17], v[30:33], v[14:17], v[22:25]
	v_add_f32_e32 v38, v176, v38
	s_nop 1
	v_exp_f32_e32 v23, v2
	v_fma_f32 v2, v11, s74, -v136
	v_mul_f32_e32 v2, 0x3fb8aa3b, v2
	v_add_f32_e32 v38, v178, v38
	v_exp_f32_e32 v24, v2
	v_fma_f32 v2, v3, s74, -v136
	v_add_f32_e32 v38, v163, v38
	v_mul_f32_e32 v2, 0x3fb8aa3b, v2
	v_add_f32_e32 v38, v165, v38
	v_exp_f32_e32 v25, v2
	v_fma_f32 v2, v12, s74, -v136
	v_add_f32_e32 v38, v177, v38
	v_mul_f32_e32 v2, 0x3fb8aa3b, v2
	v_add_f32_e32 v38, v179, v38
	v_exp_f32_e32 v30, v2
	v_fma_f32 v2, v4, s74, -v136
	v_add_f32_e32 v38, v152, v38
	v_mul_f32_e32 v2, 0x3fb8aa3b, v2
	v_add_f32_e32 v38, v154, v38
	v_exp_f32_e32 v22, v10
	v_exp_f32_e32 v31, v2
	v_fma_f32 v2, v13, s74, -v136
	ds_read2_b64 v[10:13], v52 offset0:8 offset1:12
	v_add_f32_e32 v38, v158, v38
	v_mul_f32_e32 v2, 0x3fb8aa3b, v2
	v_add_f32_e32 v38, v156, v38
	v_exp_f32_e32 v32, v2
	v_fma_f32 v2, v5, s74, -v136
	v_add_f32_e32 v38, v153, v38
	v_mul_f32_e32 v2, 0x3fb8aa3b, v2
	v_add_f32_e32 v38, v155, v38
	v_exp_f32_e32 v33, v2
	v_add_f32_e32 v38, v159, v38
	v_add_f32_e32 v38, v160, v38
	v_add_f32_e32 v34, v34, v38
	v_add_f32_e32 v34, v36, v34
	v_cvt_pk_bf16_f32 v2, v22, v24
	v_cvt_pk_bf16_f32 v3, v30, v32
	v_cvt_pk_bf16_f32 v4, v23, v25
	v_cvt_pk_bf16_f32 v5, v31, v33
	v_add_f32_e32 v34, v42, v34
	v_add_f32_e32 v34, v44, v34
	s_waitcnt lgkmcnt(0)
	v_mfma_f32_16x16x32_bf16 v[6:9], v[10:13], v[2:5], v[6:9]
	ds_read2_b64 v[10:13], v181 offset0:40 offset1:44
	v_add_f32_e32 v34, v35, v34
	v_add_f32_e32 v34, v37, v34
	v_add_f32_e32 v34, v43, v34
	v_add_f32_e32 v34, v45, v34
	v_add_f32_e32 v22, v22, v34
	v_add_f32_e32 v22, v24, v22
	v_add_f32_e32 v22, v30, v22
	v_add_f32_e32 v22, v32, v22
	s_waitcnt lgkmcnt(0)
	v_mfma_f32_16x16x32_bf16 v[10:13], v[10:13], v[2:5], v[18:21]
	v_add_f32_e32 v22, v23, v22
	v_add_f32_e32 v22, v25, v22
	v_add_f32_e32 v22, v31, v22
	ds_read2_b64 v[18:21], v182 offset0:72 offset1:76
	v_add_f32_e32 v30, v33, v22
	ds_bpermute_b32 v31, v88, v30
	ds_read2_b64 v[22:25], v49 offset0:104 offset1:108
	s_waitcnt lgkmcnt(2)
	v_mfma_f32_16x16x32_bf16 v[18:21], v[18:21], v[2:5], v[26:29]
	s_waitcnt lgkmcnt(1)
	s_nop 1
	v_add_f32_e32 v26, v30, v31
	ds_bpermute_b32 v27, v89, v26
	v_lshlrev_b32_e32 v70, 1, v77
	s_waitcnt lgkmcnt(1)
	v_mfma_f32_16x16x32_bf16 v[14:17], v[22:25], v[2:5], v[14:17]
	s_waitcnt lgkmcnt(0)
	s_barrier
; __device__ __forceinline__ unsigned cvt_pk_bf16(float lo, float hi) { const float __attribute__((ext_vector_type(2))) v = {lo, hi}; return __builtin_bit_cast(unsigned, __builtin_convertvector(v, bf16x2_t)); }
; template <bool LOCAL>
; __device__ __forceinline__ void na_unit(const bf16* P, const bf16* VT, bf16* YCAT, const LAS float* rpb_l, LAS bf16* buf, int b, int gr, int hp, int qblk, int tid) {
;     ...
;     lsum += __shfl_xor(lsum, 16); lsum += __shfl_xor(lsum, 32);
;     const float inv = 1.f / lsum;
;     bf16* op = YCAT + (size_t)(qrow0 + fr) * D + 512 + h * 64 + 4 * fq;
; #pragma unroll
;     for (int dt = 0; dt < 4; ++dt) { v2u w; w.x = pg8::cvt_pk_bf16(o[dt][0] * inv, o[dt][1] * inv); w.y = pg8::cvt_pk_bf16(o[dt][2] * inv, o[dt][3] * inv); *(v2u*)(op + dt * 16) = w; }
	v_add_f32_e32 v2, v26, v27
	v_div_scale_f32 v3, s[0:1], v2, v2, 1.0
	v_rcp_f32_e32 v4, v3
	s_nop 0
	v_fma_f32 v5, -v3, v4, 1.0
	v_fmac_f32_e32 v4, v5, v4
	v_div_scale_f32 v5, vcc, 1.0, v2, 1.0
	v_mul_f32_e32 v22, v5, v4
	v_fma_f32 v23, -v3, v22, v5
	v_fmac_f32_e32 v22, v23, v4
	v_fma_f32 v3, -v3, v22, v5
	v_div_fmas_f32 v3, v3, v4, v22
	v_div_fixup_f32 v22, v3, v2, 1.0
	v_lshlrev_b64 v[2:3], 11, v[74:75]
	v_lshl_add_u64 v[2:3], s[10:11], 0, v[2:3]
	v_lshl_add_u64 v[2:3], v[72:73], 1, v[2:3]
	v_pk_mul_f32 v[6:7], v[6:7], v[22:23] op_sel_hi:[1,0]
	v_pk_mul_f32 v[8:9], v[8:9], v[22:23] op_sel_hi:[1,0]
	v_lshl_add_u64 v[4:5], v[2:3], 0, v[70:71]
	v_cvt_pk_bf16_f32 v6, v6, v7
	v_cvt_pk_bf16_f32 v7, v8, v9
	global_store_dwordx2 v[4:5], v[6:7], off offset:1024
	v_pk_mul_f32 v[6:7], v[10:11], v[22:23] op_sel_hi:[1,0]
	v_pk_mul_f32 v[8:9], v[12:13], v[22:23] op_sel_hi:[1,0]
	v_cvt_pk_bf16_f32 v6, v6, v7
	v_cvt_pk_bf16_f32 v7, v8, v9
	global_store_dwordx2 v[4:5], v[6:7], off offset:1056
	v_pk_mul_f32 v[6:7], v[18:19], v[22:23] op_sel_hi:[1,0]
	v_pk_mul_f32 v[8:9], v[20:21], v[22:23] op_sel_hi:[1,0]
	v_cvt_pk_bf16_f32 v6, v6, v7
	v_cvt_pk_bf16_f32 v7, v8, v9
	v_lshl_add_u64 v[2:3], v[4:5], 0, s[12:13]
	global_store_dwordx2 v[4:5], v[6:7], off offset:1088
	v_pk_mul_f32 v[4:5], v[14:15], v[22:23] op_sel_hi:[1,0]
	v_pk_mul_f32 v[6:7], v[16:17], v[22:23] op_sel_hi:[1,0]
	v_cvt_pk_bf16_f32 v4, v4, v5

; #define LAS __attribute__((address_space(3)))
; template <bool LOCAL>
; __device__ __forceinline__ void na_unit(const bf16* P, const bf16* VT, bf16* YCAT, const LAS float* rpb_l, LAS bf16* buf, int b, int gr, int hp, int qblk, int tid) {
;     ...
;     const int lane = tid & 63, wv = tid >> 6, fr = lane & 15, fq = lane >> 4, hh = wv >> 2, qb = wv & 3, h = 2 * hp + hh;
;     const int qrow0 = LOCAL ? NCTX + b * SEQ + gr * 64 + 16 * qb : b * CTXL + qblk * 64 + 16 * qb;
;     const int r0 = min(max(gr - 4, 0), 24);
;     const int kc0 = qb == 0 ? 0 : qb == 1 ? 8 : qb == 2 ? 24 : 32;
;     const int qcol = 16 * qb + fr, cs = min(max(qcol - 8, 0), 48);
;     const LAS float* rpb = rpb_l + h * 15 * 31;
;     v4u ld[2][2];
;     const int lrow = (tid >> 3) & 63, lseg = tid & 7;
;     ...
;     bf16x8 qf[2];
; #pragma unroll
;     for (int ks = 0; ks < 2; ++ks) qf[ks] = *(const bf16x8*)(P + (size_t)(qrow0 + fr) * DINP + h * 64 + 32 * ks + 8 * fq);
;     f32x4 sl[16], sc[16];
;     float m = -1.0e30f, lsum = 0.f;
;     f32x4 o[4];
; #pragma unroll
;     for (int dt = 0; dt < 4; ++dt) o[dt] = (f32x4){0.f, 0.f, 0.f, 0.f};
;     NA_ISSUE(0); NA_ISSUE(1); NA_STORE(0);
;     __syncthreads();
; #pragma unroll
;     for (int sidx = 0; sidx < 2 * NCH; ++sidx) {
;         if (sidx + 2 < 2 * NCH) NA_ISSUE(sidx + 2);
;         const LAS bf16* cb = buf + (sidx & 1) * 9216 + hh * 4608;
;         if (sidx < NCH) {
;             const int c = sidx;
;             if (LOCAL && c < 8) {
; #pragma unroll
;                 for (int t2 = 0; t2 < 2; ++t2) {
;                     const LAS bf16* kp = cb + (kc0 + 16 * t2 + fr) * 72 + 8 * fq;
;                     f32x4 acc = {0.f, 0.f, 0.f, 0.f};
;                     acc = __builtin_amdgcn_mfma_f32_16x16x32_bf16(*(const LAS bf16x8*)(kp), qf[0], acc, 0, 0, 0);
;                     acc = __builtin_amdgcn_mfma_f32_16x16x32_bf16(*(const LAS bf16x8*)(kp + 32), qf[1], acc, 0, 0, 0);
;                     const LAS float* rb = rpb + (r0 + c - gr + 7) * 31 + 15 - qcol;
; #pragma unroll
;                     for (int e = 0; e < 4; ++e) { const int kcol = kc0 + 16 * t2 + 4 * fq + e; const bool ok = (kcol >= cs) && (kcol < cs + 16);
;                         const float sv = ok ? acc[e] * 0.125f + rb[ok ? kcol : qcol] : -1.0e30f; acc[e] = sv; m = fmaxf(m, sv); }
;                     sl[2 * (c < 8 ? c : 0) + t2] = acc; }
.LBB0_3762:
	s_or_b64 exec, exec, s[0:1]
	s_bfe_u32 s19, s72, 0x50002
	v_sub_u32_e64 v3, s19, 4 clamp
	s_ashr_i32 s17, s72, 7
	v_readfirstlane_b32 s0, v3
	s_lshl_b32 s26, s17, 11
	s_min_u32 s20, s0, 24
	s_add_i32 s14, s26, 0x1000
	s_lshl_b32 s15, s20, 6
	s_or_b32 s16, s15, s14
	v_mov_b64_e32 v[18:19], s[8:9]
	v_and_b32_e32 v32, 7, v93
	v_or_b32_e32 v3, s16, v88
	s_and_b32 s18, s72, 3
	v_mad_i64_i32 v[4:5], s[0:1], v3, s57, v[18:19]
	v_lshlrev_b32_e32 v26, 4, v32
	v_mov_b32_e32 v27, v71
	v_lshl_add_u64 v[4:5], v[4:5], 0, v[26:27]
	s_lshl_b32 s2, s18, 8
	v_lshl_add_u64 v[4:5], v[4:5], 0, s[2:3]
	global_load_dwordx4 v[10:13], v[4:5], off offset:1024
	global_load_dwordx4 v[14:17], v[4:5], off offset:1152
	s_lshl_b32 s0, s19, 6
	v_lshl_or_b32 v31, v2, 4, v89
	v_lshl_add_u32 v34, s18, 1, v92
	s_or_b32 s0, s14, s0
	v_mad_u32_u24 v2, v88, s64, 0
	v_lshlrev_b32_e32 v72, 6, v34
	s_add_i32 s50, s26, 0x1040
	v_or_b32_e32 v74, s0, v31
	v_add_u32_e32 v75, v2, v26
	v_ashrrev_i32_e32 v73, 31, v72
	v_or_b32_e32 v4, s50, v88
	v_mad_i64_i32 v[2:3], s[0:1], v74, s57, v[18:19]
	v_add_u32_e32 v4, s15, v4
	v_lshl_add_u64 v[2:3], v[72:73], 1, v[2:3]
	v_mad_i64_i32 v[4:5], s[0:1], v4, s57, v[18:19]
	v_lshl_add_u64 v[2:3], v[2:3], 0, v[70:71]
	v_lshl_add_u64 v[20:21], v[4:5], 0, v[26:27]
	global_load_dwordx4 v[6:9], v[2:3], off
	s_nop 0
	global_load_dwordx4 v[2:5], v[2:3], off offset:64
	s_or_b32 s14, s26, s15
	s_addk_i32 s14, 0x1080
	v_or_b32_e32 v24, s14, v88
	v_mad_i64_i32 v[28:29], s[0:1], v24, s57, v[18:19]
	v_lshl_add_u64 v[26:27], v[28:29], 0, v[26:27]
	v_lshl_add_u64 v[22:23], v[20:21], 0, s[2:3]
	v_lshl_add_u64 v[26:27], v[26:27], 0, s[2:3]
	global_load_dwordx4 v[18:21], v[22:23], off offset:1024
	s_nop 0
	global_load_dwordx4 v[22:25], v[22:23], off offset:1152
	v_add_u32_e32 v30, v86, v70
	v_add_u32_e32 v33, v90, v89
	v_mad_u32_u24 v36, v33, s64, v30
	s_sub_i32 s0, s20, s19
	s_mulk_i32 s0, 0x7c
	v_sub_u32_e64 v35, v31, 8 clamp
	v_mul_lo_u32 v34, v34, s68
	s_add_i32 s0, s0, 0
	v_min_u32_e32 v35, 48, v35
	v_lshlrev_b32_e32 v77, 2, v91
	v_add_u32_e32 v34, s0, v34
	v_lshlrev_b32_e32 v31, 2, v31
	v_sub_u32_e32 v31, v34, v31
	v_add_u32_e32 v34, v90, v77
	v_cmp_ge_u32_e32 vcc, v34, v35
	v_mov_b32_e32 v91, 0xf149f2ca
	v_lshl_add_u32 v31, v34, 2, v31
	v_mov_b32_e32 v92, 0xf149f2ca
	s_waitcnt vmcnt(5)
	ds_write_b128 v75, v[10:13]
	s_waitcnt vmcnt(4)
	ds_write_b128 v75, v[14:17] offset:9216
	s_waitcnt lgkmcnt(0)
	s_barrier
	ds_read_b32 v240, v31 offset:37792
	ds_read_b32 v241, v31 offset:37796
	ds_read_b32 v242, v31 offset:37800
	ds_read_b32 v243, v31 offset:37804
	ds_read_b32 v244, v31 offset:37856
	ds_read_b32 v245, v31 offset:37860
	ds_read_b32 v246, v31 offset:37864
	ds_read_b32 v247, v31 offset:37868
	global_load_dwordx4 v[10:13], v[26:27], off offset:1024
	global_load_dwordx4 v[14:17], v[26:27], off offset:1152
	ds_read_b128 v[26:29], v36
	ds_read_b128 v[38:41], v36 offset:64
	s_waitcnt vmcnt(5) lgkmcnt(1)
	v_mfma_f32_16x16x32_bf16 v[26:29], v[26:29], v[6:9], 0
	v_add_u32_e32 v36, 16, v35
	v_cmp_lt_u32_e64 s[0:1], v34, v36
	s_and_b64 s[28:29], vcc, s[0:1]
	s_waitcnt vmcnt(4) lgkmcnt(0)
	v_mfma_f32_16x16x32_bf16 v[26:29], v[38:41], v[2:5], v[26:29]
	s_nop 2
	s_waitcnt lgkmcnt(0)
	s_nop 3
	v_fmac_f32_e32 v240, 0x3e000000, v26
	v_cndmask_b32_e64 v92, v92, v240, s[28:29]
	s_nop 4
	v_or_b32_e32 v26, 1, v34
	v_cmp_ge_u32_e32 vcc, v26, v35
	v_cmp_lt_u32_e64 s[0:1], v26, v36
	s_and_b64 s[30:31], vcc, s[0:1]
	s_nop 2
	s_waitcnt lgkmcnt(0)
	v_fmac_f32_e32 v241, 0x3e000000, v27
	v_cndmask_b32_e64 v91, v91, v241, s[30:31]
	v_or_b32_e32 v26, 2, v34
	v_cmp_ge_u32_e32 vcc, v26, v35
	v_cmp_lt_u32_e64 s[0:1], v26, v36
	s_and_b64 s[34:35], vcc, s[0:1]
	v_mov_b32_e32 v93, 0xf149f2ca
	v_mov_b32_e32 v94, 0xf149f2ca
	s_nop 2
	s_waitcnt lgkmcnt(0)
	v_fmac_f32_e32 v242, 0x3e000000, v28
	v_cndmask_b32_e64 v94, v94, v242, s[34:35]
	v_or_b32_e32 v26, 3, v34
	v_cmp_ge_u32_e32 vcc, v26, v35
	v_cmp_lt_u32_e64 s[0:1], v26, v36
	s_and_b64 s[36:37], vcc, s[0:1]
	s_nop 2
	s_waitcnt lgkmcnt(0)
	v_fmac_f32_e32 v243, 0x3e000000, v29
	v_cndmask_b32_e64 v93, v93, v243, s[36:37]
	v_add_u32_e32 v37, 16, v90
	v_add_u32_e32 v34, v37, v89
	v_mad_u32_u24 v38, v34, s64, v30
	ds_read_b128 v[26:29], v38
	ds_read_b128 v[38:41], v38 offset:64
	v_add_u32_e32 v37, v37, v77
	v_cmp_ge_u32_e32 vcc, v37, v35
	v_cmp_lt_u32_e64 s[0:1], v37, v36
	s_waitcnt lgkmcnt(1)
	v_mfma_f32_16x16x32_bf16 v[26:29], v[26:29], v[6:9], 0
	s_and_b64 s[38:39], vcc, s[0:1]
	v_mov_b32_e32 v95, 0xf149f2ca
	v_mov_b32_e32 v96, 0xf149f2ca
	s_waitcnt lgkmcnt(0)
	v_mfma_f32_16x16x32_bf16 v[26:29], v[38:41], v[2:5], v[26:29]
	s_nop 2
	s_waitcnt lgkmcnt(0)
	s_nop 3
	v_fmac_f32_e32 v244, 0x3e000000, v26
	v_cndmask_b32_e64 v96, v96, v244, s[38:39]
	s_nop 4
	v_or_b32_e32 v26, 1, v37
	v_cmp_ge_u32_e32 vcc, v26, v35
	v_cmp_lt_u32_e64 s[0:1], v26, v36
	s_and_b64 s[44:45], vcc, s[0:1]
	s_nop 2
	s_waitcnt lgkmcnt(0)
	v_fmac_f32_e32 v245, 0x3e000000, v27
	v_cndmask_b32_e64 v95, v95, v245, s[44:45]
	v_or_b32_e32 v26, 2, v37
	v_cmp_ge_u32_e32 vcc, v26, v35
	v_cmp_lt_u32_e64 s[0:1], v26, v36
	s_and_b64 s[46:47], vcc, s[0:1]
	v_mov_b32_e32 v99, 0xf149f2ca
	v_mov_b32_e32 v100, 0xf149f2ca
	s_nop 2
	s_waitcnt lgkmcnt(0)
	v_fmac_f32_e32 v246, 0x3e000000, v28
	v_cndmask_b32_e64 v100, v100, v246, s[46:47]
	v_or_b32_e32 v26, 3, v37
	v_cmp_ge_u32_e32 vcc, v26, v35
	v_cmp_lt_u32_e64 s[0:1], v26, v36
	s_and_b64 s[48:49], vcc, s[0:1]
	s_nop 2
	s_waitcnt lgkmcnt(0)
	v_fmac_f32_e32 v247, 0x3e000000, v29
	v_cndmask_b32_e64 v99, v99, v247, s[48:49]
	v_mul_u32_u24_e32 v27, 0x90, v33
	v_lshlrev_b32_e32 v26, 3, v32
	v_add_u32_e32 v32, v30, v27
	s_waitcnt vmcnt(3)
	ds_write_b128 v75, v[18:21] offset:18432
	s_waitcnt vmcnt(2)
	ds_write_b128 v75, v[22:25] offset:27648
	s_waitcnt lgkmcnt(0)
	s_barrier
; #define LAS __attribute__((address_space(3)))
; template <bool LOCAL>
; __device__ __forceinline__ void na_unit(const bf16* P, const bf16* VT, bf16* YCAT, const LAS float* rpb_l, LAS bf16* buf, int b, int gr, int hp, int qblk, int tid) {
;     ...
;     for (int sidx = 0; sidx < 2 * NCH; ++sidx) {
;         if (sidx + 2 < 2 * NCH) NA_ISSUE(sidx + 2);
;         const LAS bf16* cb = buf + (sidx & 1) * 9216 + hh * 4608;
;         if (sidx < NCH) {
;             const int c = sidx;
;             if (LOCAL && c < 8) {
; #pragma unroll
;                 for (int t2 = 0; t2 < 2; ++t2) {
;                     const LAS bf16* kp = cb + (kc0 + 16 * t2 + fr) * 72 + 8 * fq;
;                     f32x4 acc = {0.f, 0.f, 0.f, 0.f};
;                     acc = __builtin_amdgcn_mfma_f32_16x16x32_bf16(*(const LAS bf16x8*)(kp), qf[0], acc, 0, 0, 0);
;                     acc = __builtin_amdgcn_mfma_f32_16x16x32_bf16(*(const LAS bf16x8*)(kp + 32), qf[1], acc, 0, 0, 0);
;                     const LAS float* rb = rpb + (r0 + c - gr + 7) * 31 + 15 - qcol;
; #pragma unroll
;                     for (int e = 0; e < 4; ++e) { const int kcol = kc0 + 16 * t2 + 4 * fq + e; const bool ok = (kcol >= cs) && (kcol < cs + 16);
;                         const float sv = ok ? acc[e] * 0.125f + rb[ok ? kcol : qcol] : -1.0e30f; acc[e] = sv; m = fmaxf(m, sv); }
;                     sl[2 * (c < 8 ? c : 0) + t2] = acc; }
	ds_read_b32 v240, v31 offset:37916
	ds_read_b32 v241, v31 offset:37920
	ds_read_b32 v242, v31 offset:37924
	ds_read_b32 v243, v31 offset:37928
	ds_read_b32 v244, v31 offset:37980
	ds_read_b32 v245, v31 offset:37984
	ds_read_b32 v246, v31 offset:37988
	ds_read_b32 v247, v31 offset:37992
	ds_read_b128 v[18:21], v32 offset:18432
	s_add_i32 s26, s26, s15
	s_add_i32 s0, s26, 0x10c0
	v_or_b32_e32 v24, s0, v88
	v_mov_b64_e32 v[22:23], s[8:9]
	s_lshl_b32 s1, s18, 7
	v_mad_i64_i32 v[22:23], s[18:19], v24, s57, v[22:23]
	v_lshlrev_b32_e32 v70, 1, v26
	v_lshl_add_u64 v[22:23], v[22:23], 0, v[70:71]
	s_lshl_b32 s2, s1, 1
	v_lshl_add_u64 v[22:23], v[22:23], 0, s[2:3]
	ds_read_b128 v[26:29], v32 offset:18496
	s_waitcnt lgkmcnt(1)
	v_mfma_f32_16x16x32_bf16 v[36:39], v[18:21], v[6:9], 0
	global_load_dwordx4 v[18:21], v[22:23], off offset:1024
	s_nop 0
	global_load_dwordx4 v[22:25], v[22:23], off offset:1152
	v_mov_b32_e32 v97, 0xf149f2ca
	v_mov_b32_e32 v98, 0xf149f2ca
	s_waitcnt lgkmcnt(0)
	v_mfma_f32_16x16x32_bf16 v[26:29], v[26:29], v[2:5], v[36:39]
	s_nop 2
	s_waitcnt lgkmcnt(0)
	s_nop 3
	v_fmac_f32_e32 v240, 0x3e000000, v26
	v_cndmask_b32_e64 v98, v98, v240, s[28:29]
	s_nop 2
	s_waitcnt lgkmcnt(0)
	s_nop 0
	v_fmac_f32_e32 v241, 0x3e000000, v27
	v_cndmask_b32_e64 v97, v97, v241, s[30:31]
	v_mov_b32_e32 v101, 0xf149f2ca
	v_mov_b32_e32 v102, 0xf149f2ca
	s_nop 2
	s_waitcnt lgkmcnt(0)
	v_fmac_f32_e32 v242, 0x3e000000, v28
	v_cndmask_b32_e64 v102, v102, v242, s[34:35]
	s_nop 2
	s_waitcnt lgkmcnt(0)
	v_fmac_f32_e32 v243, 0x3e000000, v29
	v_cndmask_b32_e64 v101, v101, v243, s[36:37]
	v_mul_u32_u24_e32 v26, 0x90, v34
	v_add_u32_e32 v33, v30, v26
	ds_read_b128 v[26:29], v33 offset:18432
	ds_read_b128 v[34:37], v33 offset:18496
	v_mov_b32_e32 v104, 0xf149f2ca
	v_mov_b32_e32 v106, 0xf149f2ca
	s_waitcnt lgkmcnt(1)
	v_mfma_f32_16x16x32_bf16 v[26:29], v[26:29], v[6:9], 0
	s_waitcnt lgkmcnt(0)
	v_mfma_f32_16x16x32_bf16 v[26:29], v[34:37], v[2:5], v[26:29]
	s_nop 2
	s_waitcnt lgkmcnt(0)
	s_nop 3
	v_fmac_f32_e32 v244, 0x3e000000, v26
	v_cndmask_b32_e64 v106, v106, v244, s[38:39]
	s_nop 2
	s_waitcnt lgkmcnt(0)
	s_nop 0
	v_fmac_f32_e32 v245, 0x3e000000, v27
	v_cndmask_b32_e64 v104, v104, v245, s[44:45]
	v_mov_b32_e32 v108, 0xf149f2ca
	v_mov_b32_e32 v110, 0xf149f2ca
	s_nop 2
	s_waitcnt lgkmcnt(0)
	v_fmac_f32_e32 v246, 0x3e000000, v28
	v_cndmask_b32_e64 v110, v110, v246, s[46:47]
	s_nop 2
	s_waitcnt lgkmcnt(0)
	v_fmac_f32_e32 v247, 0x3e000000, v29
	v_cndmask_b32_e64 v108, v108, v247, s[48:49]
	s_waitcnt vmcnt(3)
	ds_write_b128 v75, v[10:13]
	s_waitcnt vmcnt(2)
	ds_write_b128 v75, v[14:17] offset:9216
	s_waitcnt lgkmcnt(0)
	s_barrier
	ds_read_b32 v240, v31 offset:38040
	ds_read_b32 v241, v31 offset:38044
	ds_read_b32 v242, v31 offset:38048
	ds_read_b32 v243, v31 offset:38052
	ds_read_b32 v244, v31 offset:38104
	ds_read_b32 v245, v31 offset:38108
	ds_read_b32 v246, v31 offset:38112
	ds_read_b32 v247, v31 offset:38116
	ds_read_b128 v[10:13], v32
	ds_read_b128 v[26:29], v32 offset:64
	s_add_i32 s18, s26, 0x1100
	v_or_b32_e32 v16, s18, v88
	v_mov_b64_e32 v[14:15], s[8:9]
	v_mad_i64_i32 v[14:15], s[20:21], v16, s57, v[14:15]
	v_lshl_add_u64 v[14:15], v[14:15], 0, v[70:71]
	v_lshl_add_u64 v[14:15], v[14:15], 0, s[2:3]
	s_waitcnt lgkmcnt(1)
	v_mfma_f32_16x16x32_bf16 v[34:37], v[10:13], v[6:9], 0
	global_load_dwordx4 v[10:13], v[14:15], off offset:1024
	s_nop 0
	global_load_dwordx4 v[14:17], v[14:15], off offset:1152
	v_mov_b32_e32 v103, 0xf149f2ca
	v_mov_b32_e32 v105, 0xf149f2ca
	s_waitcnt lgkmcnt(0)
	v_mfma_f32_16x16x32_bf16 v[26:29], v[26:29], v[2:5], v[34:37]
	s_nop 2
	s_waitcnt lgkmcnt(0)
	s_nop 3
	v_fmac_f32_e32 v240, 0x3e000000, v26
	v_cndmask_b32_e64 v105, v105, v240, s[28:29]
	s_nop 2
	s_waitcnt lgkmcnt(0)
	s_nop 0
	v_fmac_f32_e32 v241, 0x3e000000, v27
	v_cndmask_b32_e64 v103, v103, v241, s[30:31]
	v_mov_b32_e32 v107, 0xf149f2ca
	v_mov_b32_e32 v109, 0xf149f2ca
	s_nop 2
	s_waitcnt lgkmcnt(0)
	v_fmac_f32_e32 v242, 0x3e000000, v28
	v_cndmask_b32_e64 v109, v109, v242, s[34:35]
	s_nop 2
	s_waitcnt lgkmcnt(0)
	v_fmac_f32_e32 v243, 0x3e000000, v29
	v_cndmask_b32_e64 v107, v107, v243, s[36:37]
	ds_read_b128 v[26:29], v33
	ds_read_b128 v[34:37], v33 offset:64
	v_mov_b32_e32 v111, 0xf149f2ca
	v_mov_b32_e32 v114, 0xf149f2ca
	s_waitcnt lgkmcnt(1)
	v_mfma_f32_16x16x32_bf16 v[26:29], v[26:29], v[6:9], 0
	s_waitcnt lgkmcnt(0)
	v_mfma_f32_16x16x32_bf16 v[26:29], v[34:37], v[2:5], v[26:29]
	s_nop 2
	s_waitcnt lgkmcnt(0)
	s_nop 3
	v_fmac_f32_e32 v244, 0x3e000000, v26
	v_cndmask_b32_e64 v114, v114, v244, s[38:39]
	s_nop 2
	s_waitcnt lgkmcnt(0)
	s_nop 0
	v_fmac_f32_e32 v245, 0x3e000000, v27
	v_cndmask_b32_e64 v111, v111, v245, s[44:45]
	v_mov_b32_e32 v113, 0xf149f2ca
	v_mov_b32_e32 v117, 0xf149f2ca
	s_nop 2
	s_waitcnt lgkmcnt(0)
	v_fmac_f32_e32 v246, 0x3e000000, v28
	v_cndmask_b32_e64 v117, v117, v246, s[46:47]
	s_nop 2
	s_waitcnt lgkmcnt(0)
	v_fmac_f32_e32 v247, 0x3e000000, v29
	v_cndmask_b32_e64 v113, v113, v247, s[48:49]
	s_waitcnt vmcnt(3)
	ds_write_b128 v75, v[18:21] offset:18432
	s_waitcnt vmcnt(2)
	ds_write_b128 v75, v[22:25] offset:27648
	s_waitcnt lgkmcnt(0)
	s_barrier
; #define LAS __attribute__((address_space(3)))
; template <bool LOCAL>
; __device__ __forceinline__ void na_unit(const bf16* P, const bf16* VT, bf16* YCAT, const LAS float* rpb_l, LAS bf16* buf, int b, int gr, int hp, int qblk, int tid) {
;     ...
;     for (int sidx = 0; sidx < 2 * NCH; ++sidx) {
;         if (sidx + 2 < 2 * NCH) NA_ISSUE(sidx + 2);
;         const LAS bf16* cb = buf + (sidx & 1) * 9216 + hh * 4608;
;         if (sidx < NCH) {
;             const int c = sidx;
;             if (LOCAL && c < 8) {
; #pragma unroll
;                 for (int t2 = 0; t2 < 2; ++t2) {
;                     const LAS bf16* kp = cb + (kc0 + 16 * t2 + fr) * 72 + 8 * fq;
;                     f32x4 acc = {0.f, 0.f, 0.f, 0.f};
;                     acc = __builtin_amdgcn_mfma_f32_16x16x32_bf16(*(const LAS bf16x8*)(kp), qf[0], acc, 0, 0, 0);
;                     acc = __builtin_amdgcn_mfma_f32_16x16x32_bf16(*(const LAS bf16x8*)(kp + 32), qf[1], acc, 0, 0, 0);
;                     const LAS float* rb = rpb + (r0 + c - gr + 7) * 31 + 15 - qcol;
; #pragma unroll
;                     for (int e = 0; e < 4; ++e) { const int kcol = kc0 + 16 * t2 + 4 * fq + e; const bool ok = (kcol >= cs) && (kcol < cs + 16);
;                         const float sv = ok ? acc[e] * 0.125f + rb[ok ? kcol : qcol] : -1.0e30f; acc[e] = sv; m = fmaxf(m, sv); }
;                     sl[2 * (c < 8 ? c : 0) + t2] = acc; }
	ds_read_b32 v240, v31 offset:38164
	ds_read_b32 v241, v31 offset:38168
	ds_read_b32 v242, v31 offset:38172
	ds_read_b32 v243, v31 offset:38176
	ds_read_b32 v244, v31 offset:38228
	ds_read_b32 v245, v31 offset:38232
	ds_read_b32 v246, v31 offset:38236
	ds_read_b32 v247, v31 offset:38240
	ds_read_b128 v[18:21], v32 offset:18432
	ds_read_b128 v[26:29], v32 offset:18496
	s_add_i32 s20, s26, 0x1140
	v_or_b32_e32 v24, s20, v88
	v_mov_b64_e32 v[22:23], s[8:9]
	v_mad_i64_i32 v[22:23], s[22:23], v24, s57, v[22:23]
	v_lshl_add_u64 v[22:23], v[22:23], 0, v[70:71]
	v_lshl_add_u64 v[22:23], v[22:23], 0, s[2:3]
	s_waitcnt lgkmcnt(1)
	v_mfma_f32_16x16x32_bf16 v[34:37], v[18:21], v[6:9], 0
	global_load_dwordx4 v[18:21], v[22:23], off offset:1024
	s_nop 0
	global_load_dwordx4 v[22:25], v[22:23], off offset:1152
	v_mov_b32_e32 v112, 0xf149f2ca
	v_mov_b32_e32 v115, 0xf149f2ca
	s_waitcnt lgkmcnt(0)
	v_mfma_f32_16x16x32_bf16 v[26:29], v[26:29], v[2:5], v[34:37]
	s_nop 2
	s_waitcnt lgkmcnt(0)
	s_nop 3
	v_fmac_f32_e32 v240, 0x3e000000, v26
	v_cndmask_b32_e64 v115, v115, v240, s[28:29]
	s_nop 2
	s_waitcnt lgkmcnt(0)
	s_nop 0
	v_fmac_f32_e32 v241, 0x3e000000, v27
	v_cndmask_b32_e64 v112, v112, v241, s[30:31]
	v_mov_b32_e32 v116, 0xf149f2ca
	v_mov_b32_e32 v118, 0xf149f2ca
	s_nop 2
	s_waitcnt lgkmcnt(0)
	v_fmac_f32_e32 v242, 0x3e000000, v28
	v_cndmask_b32_e64 v118, v118, v242, s[34:35]
	s_nop 2
	s_waitcnt lgkmcnt(0)
	v_fmac_f32_e32 v243, 0x3e000000, v29
	v_cndmask_b32_e64 v116, v116, v243, s[36:37]
	ds_read_b128 v[26:29], v33 offset:18432
	ds_read_b128 v[34:37], v33 offset:18496
	v_mov_b32_e32 v119, 0xf149f2ca
	v_mov_b32_e32 v122, 0xf149f2ca
	s_waitcnt lgkmcnt(1)
	v_mfma_f32_16x16x32_bf16 v[26:29], v[26:29], v[6:9], 0
	s_waitcnt lgkmcnt(0)
	v_mfma_f32_16x16x32_bf16 v[26:29], v[34:37], v[2:5], v[26:29]
	s_nop 2
	s_waitcnt lgkmcnt(0)
	s_nop 3
	v_fmac_f32_e32 v244, 0x3e000000, v26
	v_cndmask_b32_e64 v122, v122, v244, s[38:39]
	s_nop 2
	s_waitcnt lgkmcnt(0)
	s_nop 0
	v_fmac_f32_e32 v245, 0x3e000000, v27
	v_cndmask_b32_e64 v119, v119, v245, s[44:45]
	v_mov_b32_e32 v121, 0xf149f2ca
	v_mov_b32_e32 v125, 0xf149f2ca
	s_nop 2
	s_waitcnt lgkmcnt(0)
	v_fmac_f32_e32 v246, 0x3e000000, v28
	v_cndmask_b32_e64 v125, v125, v246, s[46:47]
	s_nop 2
	s_waitcnt lgkmcnt(0)
	v_fmac_f32_e32 v247, 0x3e000000, v29
	v_cndmask_b32_e64 v121, v121, v247, s[48:49]
	s_waitcnt vmcnt(3)
	ds_write_b128 v75, v[10:13]
	s_waitcnt vmcnt(2)
	ds_write_b128 v75, v[14:17] offset:9216
	s_waitcnt lgkmcnt(0)
	s_barrier
	ds_read_b32 v240, v31 offset:38288
	ds_read_b32 v241, v31 offset:38292
	ds_read_b32 v242, v31 offset:38296
	ds_read_b32 v243, v31 offset:38300
	ds_read_b32 v244, v31 offset:38352
	ds_read_b32 v245, v31 offset:38356
	ds_read_b32 v246, v31 offset:38360
	ds_read_b32 v247, v31 offset:38364
	ds_read_b128 v[10:13], v32
	ds_read_b128 v[26:29], v32 offset:64
	s_add_i32 s22, s26, 0x1180
	v_or_b32_e32 v16, s22, v88
	v_mov_b64_e32 v[14:15], s[8:9]
	v_mad_i64_i32 v[14:15], s[24:25], v16, s57, v[14:15]
	v_lshl_add_u64 v[14:15], v[14:15], 0, v[70:71]
	v_lshl_add_u64 v[14:15], v[14:15], 0, s[2:3]
	s_waitcnt lgkmcnt(1)
	v_mfma_f32_16x16x32_bf16 v[34:37], v[10:13], v[6:9], 0
	global_load_dwordx4 v[10:13], v[14:15], off offset:1024
	s_nop 0
	global_load_dwordx4 v[14:17], v[14:15], off offset:1152
	v_mov_b32_e32 v120, 0xf149f2ca
	v_mov_b32_e32 v123, 0xf149f2ca
	s_waitcnt lgkmcnt(0)
	v_mfma_f32_16x16x32_bf16 v[26:29], v[26:29], v[2:5], v[34:37]
	s_nop 2
	s_waitcnt lgkmcnt(0)
	s_nop 3
	v_fmac_f32_e32 v240, 0x3e000000, v26
	v_cndmask_b32_e64 v123, v123, v240, s[28:29]
	s_nop 2
	s_waitcnt lgkmcnt(0)
	s_nop 0
	v_fmac_f32_e32 v241, 0x3e000000, v27
	v_cndmask_b32_e64 v120, v120, v241, s[30:31]
	v_mov_b32_e32 v124, 0xf149f2ca
	v_mov_b32_e32 v126, 0xf149f2ca
	s_nop 2
	s_waitcnt lgkmcnt(0)
	v_fmac_f32_e32 v242, 0x3e000000, v28
	v_cndmask_b32_e64 v126, v126, v242, s[34:35]
	s_nop 2
	s_waitcnt lgkmcnt(0)
	v_fmac_f32_e32 v243, 0x3e000000, v29
	v_cndmask_b32_e64 v124, v124, v243, s[36:37]
	ds_read_b128 v[26:29], v33
	ds_read_b128 v[34:37], v33 offset:64
	v_mov_b32_e32 v128, 0xf149f2ca
	v_mov_b32_e32 v131, 0xf149f2ca
	s_waitcnt lgkmcnt(1)
	v_mfma_f32_16x16x32_bf16 v[26:29], v[26:29], v[6:9], 0
	s_waitcnt lgkmcnt(0)
	v_mfma_f32_16x16x32_bf16 v[26:29], v[34:37], v[2:5], v[26:29]
	s_nop 2
	s_waitcnt lgkmcnt(0)
	s_nop 3
	v_fmac_f32_e32 v244, 0x3e000000, v26
	v_cndmask_b32_e64 v131, v131, v244, s[38:39]
	s_nop 2
	s_waitcnt lgkmcnt(0)
	s_nop 0
	v_fmac_f32_e32 v245, 0x3e000000, v27
	v_cndmask_b32_e64 v128, v128, v245, s[44:45]
	v_mov_b32_e32 v130, 0xf149f2ca
	v_mov_b32_e32 v135, 0xf149f2ca
	s_nop 2
	s_waitcnt lgkmcnt(0)
	v_fmac_f32_e32 v246, 0x3e000000, v28
	v_cndmask_b32_e64 v135, v135, v246, s[46:47]
	s_nop 2
	s_waitcnt lgkmcnt(0)
	v_fmac_f32_e32 v247, 0x3e000000, v29
	v_cndmask_b32_e64 v130, v130, v247, s[48:49]
	s_waitcnt vmcnt(3)
	ds_write_b128 v75, v[18:21] offset:18432
	s_waitcnt vmcnt(2)
	ds_write_b128 v75, v[22:25] offset:27648
	s_waitcnt lgkmcnt(0)
	s_barrier
; #define LAS __attribute__((address_space(3)))
; template <bool LOCAL>
; __device__ __forceinline__ void na_unit(const bf16* P, const bf16* VT, bf16* YCAT, const LAS float* rpb_l, LAS bf16* buf, int b, int gr, int hp, int qblk, int tid) {
;     ...
;     for (int sidx = 0; sidx < 2 * NCH; ++sidx) {
;         if (sidx + 2 < 2 * NCH) NA_ISSUE(sidx + 2);
;         const LAS bf16* cb = buf + (sidx & 1) * 9216 + hh * 4608;
;         if (sidx < NCH) {
;             const int c = sidx;
;             if (LOCAL && c < 8) {
; #pragma unroll
;                 for (int t2 = 0; t2 < 2; ++t2) {
;                     const LAS bf16* kp = cb + (kc0 + 16 * t2 + fr) * 72 + 8 * fq;
;                     f32x4 acc = {0.f, 0.f, 0.f, 0.f};
;                     acc = __builtin_amdgcn_mfma_f32_16x16x32_bf16(*(const LAS bf16x8*)(kp), qf[0], acc, 0, 0, 0);
;                     acc = __builtin_amdgcn_mfma_f32_16x16x32_bf16(*(const LAS bf16x8*)(kp + 32), qf[1], acc, 0, 0, 0);
;                     const LAS float* rb = rpb + (r0 + c - gr + 7) * 31 + 15 - qcol;
; #pragma unroll
;                     for (int e = 0; e < 4; ++e) { const int kcol = kc0 + 16 * t2 + 4 * fq + e; const bool ok = (kcol >= cs) && (kcol < cs + 16);
;                         const float sv = ok ? acc[e] * 0.125f + rb[ok ? kcol : qcol] : -1.0e30f; acc[e] = sv; m = fmaxf(m, sv); }
;                     sl[2 * (c < 8 ? c : 0) + t2] = acc; }
	ds_read_b32 v240, v31 offset:38412
	ds_read_b32 v241, v31 offset:38416
	ds_read_b32 v242, v31 offset:38420
	ds_read_b32 v243, v31 offset:38424
	ds_read_b32 v244, v31 offset:38476
	ds_read_b32 v245, v31 offset:38480
	ds_read_b32 v246, v31 offset:38484
	ds_read_b32 v247, v31 offset:38488
	ds_read_b128 v[18:21], v32 offset:18432
	ds_read_b128 v[26:29], v32 offset:18496
	s_add_i32 s24, s26, 0x11c0
	v_or_b32_e32 v24, s24, v88
	v_mov_b64_e32 v[22:23], s[8:9]
	v_mad_i64_i32 v[22:23], s[26:27], v24, s57, v[22:23]
	v_lshl_add_u64 v[22:23], v[22:23], 0, v[70:71]
	v_lshl_add_u64 v[22:23], v[22:23], 0, s[2:3]
	s_waitcnt lgkmcnt(1)
	v_mfma_f32_16x16x32_bf16 v[34:37], v[18:21], v[6:9], 0
	global_load_dwordx4 v[18:21], v[22:23], off offset:1024
	s_nop 0
	global_load_dwordx4 v[22:25], v[22:23], off offset:1152
	v_mov_b32_e32 v129, 0xf149f2ca
	v_mov_b32_e32 v132, 0xf149f2ca
	s_waitcnt lgkmcnt(0)
	v_mfma_f32_16x16x32_bf16 v[26:29], v[26:29], v[2:5], v[34:37]
	s_nop 2
	s_waitcnt lgkmcnt(0)
	s_nop 3
	v_fmac_f32_e32 v240, 0x3e000000, v26
	v_cndmask_b32_e64 v132, v132, v240, s[28:29]
	s_nop 2
	s_waitcnt lgkmcnt(0)
	s_nop 0
	v_fmac_f32_e32 v241, 0x3e000000, v27
	v_cndmask_b32_e64 v129, v129, v241, s[30:31]
	v_mov_b32_e32 v134, 0xf149f2ca
	v_mov_b32_e32 v136, 0xf149f2ca
	s_nop 2
	s_waitcnt lgkmcnt(0)
	v_fmac_f32_e32 v242, 0x3e000000, v28
	v_cndmask_b32_e64 v136, v136, v242, s[34:35]
	s_nop 2
	s_waitcnt lgkmcnt(0)
	v_fmac_f32_e32 v243, 0x3e000000, v29
	v_cndmask_b32_e64 v134, v134, v243, s[36:37]
	ds_read_b128 v[26:29], v33 offset:18432
	ds_read_b128 v[34:37], v33 offset:18496
	v_mov_b32_e32 v137, 0xf149f2ca
	v_mov_b32_e32 v140, 0xf149f2ca
	s_waitcnt lgkmcnt(1)
	v_mfma_f32_16x16x32_bf16 v[26:29], v[26:29], v[6:9], 0
	s_waitcnt lgkmcnt(0)
	v_mfma_f32_16x16x32_bf16 v[26:29], v[34:37], v[2:5], v[26:29]
	s_nop 2
	s_waitcnt lgkmcnt(0)
	s_nop 3
	v_fmac_f32_e32 v244, 0x3e000000, v26
	v_cndmask_b32_e64 v140, v140, v244, s[38:39]
	s_nop 2
	s_waitcnt lgkmcnt(0)
	s_nop 0
	v_fmac_f32_e32 v245, 0x3e000000, v27
	v_cndmask_b32_e64 v137, v137, v245, s[44:45]
	v_mov_b32_e32 v139, 0xf149f2ca
	v_mov_b32_e32 v143, 0xf149f2ca
	s_nop 2
	s_waitcnt lgkmcnt(0)
	v_fmac_f32_e32 v246, 0x3e000000, v28
	v_cndmask_b32_e64 v143, v143, v246, s[46:47]
	s_nop 2
	s_waitcnt lgkmcnt(0)
	v_fmac_f32_e32 v247, 0x3e000000, v29
	v_cndmask_b32_e64 v139, v139, v247, s[48:49]
	s_waitcnt vmcnt(3)
	ds_write_b128 v75, v[10:13]
	s_waitcnt vmcnt(2)
	ds_write_b128 v75, v[14:17] offset:9216
	s_waitcnt lgkmcnt(0)
	s_barrier
	ds_read_b32 v240, v31 offset:38536
	ds_read_b32 v241, v31 offset:38540
	ds_read_b32 v242, v31 offset:38544
	ds_read_b32 v243, v31 offset:38548
	ds_read_b32 v244, v31 offset:38600
	ds_read_b32 v245, v31 offset:38604
	ds_read_b32 v246, v31 offset:38608
	ds_read_b32 v247, v31 offset:38612
	ds_read_b128 v[10:13], v32
	ds_read_b128 v[26:29], v32 offset:64
	s_lshl_b32 s26, s17, 8
	v_or_b32_e32 v34, s26, v88
	v_mov_b64_e32 v[14:15], s[8:9]
	v_mad_i64_i32 v[14:15], s[52:53], v34, s57, v[14:15]
	v_lshl_add_u64 v[14:15], v[14:15], 0, v[70:71]
	v_lshl_add_u64 v[14:15], v[14:15], 0, s[2:3]
	s_waitcnt lgkmcnt(1)
	v_mfma_f32_16x16x32_bf16 v[36:39], v[10:13], v[6:9], 0
	global_load_dwordx4 v[10:13], v[14:15], off offset:1024
	s_nop 0
	global_load_dwordx4 v[14:17], v[14:15], off offset:1152
	v_mov_b32_e32 v138, 0xf149f2ca
	v_mov_b32_e32 v141, 0xf149f2ca
	s_waitcnt lgkmcnt(0)
	v_mfma_f32_16x16x32_bf16 v[26:29], v[26:29], v[2:5], v[36:39]
	s_nop 2
	s_waitcnt lgkmcnt(0)
	s_nop 3
	v_fmac_f32_e32 v240, 0x3e000000, v26
	v_cndmask_b32_e64 v141, v141, v240, s[28:29]
	s_nop 2
	s_waitcnt lgkmcnt(0)
	s_nop 0
	v_fmac_f32_e32 v241, 0x3e000000, v27
	v_cndmask_b32_e64 v138, v138, v241, s[30:31]
	v_mov_b32_e32 v142, 0xf149f2ca
	v_mov_b32_e32 v144, 0xf149f2ca
	s_nop 2
	s_waitcnt lgkmcnt(0)
	v_fmac_f32_e32 v242, 0x3e000000, v28
	v_cndmask_b32_e64 v144, v144, v242, s[34:35]
	s_nop 2
	s_waitcnt lgkmcnt(0)
	v_fmac_f32_e32 v243, 0x3e000000, v29
	v_cndmask_b32_e64 v142, v142, v243, s[36:37]
	ds_read_b128 v[26:29], v33
	ds_read_b128 v[36:39], v33 offset:64
	v_mov_b32_e32 v145, 0xf149f2ca
	v_mov_b32_e32 v148, 0xf149f2ca
	s_waitcnt lgkmcnt(1)
	v_mfma_f32_16x16x32_bf16 v[26:29], v[26:29], v[6:9], 0
	s_waitcnt lgkmcnt(0)
	v_mfma_f32_16x16x32_bf16 v[26:29], v[36:39], v[2:5], v[26:29]
	s_nop 2
	s_waitcnt lgkmcnt(0)
	s_nop 3
	v_fmac_f32_e32 v244, 0x3e000000, v26
	v_cndmask_b32_e64 v148, v148, v244, s[38:39]
	s_nop 2
	s_waitcnt lgkmcnt(0)
	s_nop 0
	v_fmac_f32_e32 v245, 0x3e000000, v27
	v_cndmask_b32_e64 v145, v145, v245, s[44:45]
	v_mov_b32_e32 v147, 0xf149f2ca
	v_mov_b32_e32 v151, 0xf149f2ca
	s_nop 2
	s_waitcnt lgkmcnt(0)
	v_fmac_f32_e32 v246, 0x3e000000, v28
	v_cndmask_b32_e64 v151, v151, v246, s[46:47]
	s_nop 2
	s_waitcnt lgkmcnt(0)
	v_fmac_f32_e32 v247, 0x3e000000, v29
	v_cndmask_b32_e64 v147, v147, v247, s[48:49]
	s_waitcnt vmcnt(3)
	ds_write_b128 v75, v[18:21] offset:18432
	s_waitcnt vmcnt(2)
	ds_write_b128 v75, v[22:25] offset:27648
	s_waitcnt lgkmcnt(0)
	s_barrier
; #define LAS __attribute__((address_space(3)))
; template <bool LOCAL>
; __device__ __forceinline__ void na_unit(const bf16* P, const bf16* VT, bf16* YCAT, const LAS float* rpb_l, LAS bf16* buf, int b, int gr, int hp, int qblk, int tid) {
;     ...
;     for (int sidx = 0; sidx < 2 * NCH; ++sidx) {
;         if (sidx + 2 < 2 * NCH) NA_ISSUE(sidx + 2);
;         const LAS bf16* cb = buf + (sidx & 1) * 9216 + hh * 4608;
;         if (sidx < NCH) {
;             const int c = sidx;
;             if (LOCAL && c < 8) {
; #pragma unroll
;                 for (int t2 = 0; t2 < 2; ++t2) {
;                     const LAS bf16* kp = cb + (kc0 + 16 * t2 + fr) * 72 + 8 * fq;
;                     f32x4 acc = {0.f, 0.f, 0.f, 0.f};
;                     acc = __builtin_amdgcn_mfma_f32_16x16x32_bf16(*(const LAS bf16x8*)(kp), qf[0], acc, 0, 0, 0);
;                     acc = __builtin_amdgcn_mfma_f32_16x16x32_bf16(*(const LAS bf16x8*)(kp + 32), qf[1], acc, 0, 0, 0);
;                     const LAS float* rb = rpb + (r0 + c - gr + 7) * 31 + 15 - qcol;
; #pragma unroll
;                     for (int e = 0; e < 4; ++e) { const int kcol = kc0 + 16 * t2 + 4 * fq + e; const bool ok = (kcol >= cs) && (kcol < cs + 16);
;                         const float sv = ok ? acc[e] * 0.125f + rb[ok ? kcol : qcol] : -1.0e30f; acc[e] = sv; m = fmaxf(m, sv); }
;                     sl[2 * (c < 8 ? c : 0) + t2] = acc; }
;             } else {
;                 const int cc = c - NLOC;
; #pragma unroll
;                 for (int t4 = 0; t4 < 4; ++t4) {
;                     const LAS bf16* kp = cb + (16 * t4 + fr) * 72 + 8 * fq;
;                     f32x4 acc = {0.f, 0.f, 0.f, 0.f};
;                     acc = __builtin_amdgcn_mfma_f32_16x16x32_bf16(*(const LAS bf16x8*)(kp), qf[0], acc, 0, 0, 0);
;                     acc = __builtin_amdgcn_mfma_f32_16x16x32_bf16(*(const LAS bf16x8*)(kp + 32), qf[1], acc, 0, 0, 0);
; #pragma unroll
;                     for (int e = 0; e < 4; ++e) { acc[e] *= 0.125f; m = fmaxf(m, acc[e]); }
;                     sc[4 * (cc >= 0 ? cc : 0) + t4] = acc; }
;             }
;             if (sidx == NCH - 1) { m = fmaxf(m, __shfl_xor(m, 16)); m = fmaxf(m, __shfl_xor(m, 32)); }
	ds_read_b32 v240, v31 offset:38660
	ds_read_b32 v241, v31 offset:38664
	ds_read_b32 v242, v31 offset:38668
	ds_read_b32 v243, v31 offset:38672
	ds_read_b32 v244, v31 offset:38724
	ds_read_b32 v245, v31 offset:38728
	ds_read_b32 v246, v31 offset:38732
	ds_read_b32 v247, v31 offset:38736
	ds_read_b128 v[18:21], v32 offset:18432
	ds_read_b128 v[26:29], v32 offset:18496
	v_or_b32_e32 v24, 64, v34
	v_mov_b64_e32 v[22:23], s[8:9]
	v_mad_i64_i32 v[22:23], s[52:53], v24, s57, v[22:23]
	v_lshl_add_u64 v[22:23], v[22:23], 0, v[70:71]
	v_lshl_add_u64 v[22:23], v[22:23], 0, s[2:3]
	s_waitcnt lgkmcnt(1)
	v_mfma_f32_16x16x32_bf16 v[36:39], v[18:21], v[6:9], 0
	global_load_dwordx4 v[18:21], v[22:23], off offset:1024
	s_nop 0
	global_load_dwordx4 v[22:25], v[22:23], off offset:1152
	v_mov_b32_e32 v146, 0xf149f2ca
	v_mov_b32_e32 v149, 0xf149f2ca
	s_waitcnt lgkmcnt(0)
	v_mfma_f32_16x16x32_bf16 v[26:29], v[26:29], v[2:5], v[36:39]
	s_nop 2
	s_waitcnt lgkmcnt(0)
	s_nop 3
	v_fmac_f32_e32 v240, 0x3e000000, v26
	v_cndmask_b32_e64 v149, v149, v240, s[28:29]
	s_nop 2
	s_waitcnt lgkmcnt(0)
	s_nop 0
	v_fmac_f32_e32 v241, 0x3e000000, v27
	v_cndmask_b32_e64 v146, v146, v241, s[30:31]
	v_mov_b32_e32 v150, 0xf149f2ca
	v_mov_b32_e32 v152, 0xf149f2ca
	s_nop 2
	s_waitcnt lgkmcnt(0)
	v_fmac_f32_e32 v242, 0x3e000000, v28
	v_cndmask_b32_e64 v152, v152, v242, s[34:35]
	s_nop 2
	s_waitcnt lgkmcnt(0)
	v_fmac_f32_e32 v243, 0x3e000000, v29
	v_cndmask_b32_e64 v150, v150, v243, s[36:37]
	ds_read_b128 v[26:29], v33 offset:18432
	ds_read_b128 v[36:39], v33 offset:18496
	v_mov_b32_e32 v153, 0xf149f2ca
	v_mov_b32_e32 v155, 0xf149f2ca
	s_waitcnt lgkmcnt(1)
	v_mfma_f32_16x16x32_bf16 v[26:29], v[26:29], v[6:9], 0
	s_waitcnt lgkmcnt(0)
	v_mfma_f32_16x16x32_bf16 v[26:29], v[36:39], v[2:5], v[26:29]
	s_nop 2
	s_waitcnt lgkmcnt(0)
	s_nop 3
	v_fmac_f32_e32 v244, 0x3e000000, v26
	v_cndmask_b32_e64 v155, v155, v244, s[38:39]
	s_nop 2
	s_waitcnt lgkmcnt(0)
	s_nop 0
	v_fmac_f32_e32 v245, 0x3e000000, v27
	v_cndmask_b32_e64 v153, v153, v245, s[44:45]
	v_mov_b32_e32 v154, 0xf149f2ca
	v_mov_b32_e32 v157, 0xf149f2ca
	s_nop 2
	s_waitcnt lgkmcnt(0)
	v_fmac_f32_e32 v246, 0x3e000000, v28
	v_cndmask_b32_e64 v157, v157, v246, s[46:47]
	s_nop 2
	s_waitcnt lgkmcnt(0)
	v_fmac_f32_e32 v247, 0x3e000000, v29
	v_cndmask_b32_e64 v154, v154, v247, s[48:49]
	v_max3_f32 v26, v92, s67, v91
	v_max3_f32 v26, v26, v94, v93
	v_max3_f32 v26, v26, v96, v95
	v_max3_f32 v26, v26, v100, v99
	v_max3_f32 v26, v26, v98, v97
	v_max3_f32 v26, v26, v102, v101
	v_max3_f32 v26, v26, v106, v104
	v_max3_f32 v26, v26, v110, v108
	v_max3_f32 v26, v26, v105, v103
	v_max3_f32 v26, v26, v109, v107
	v_max3_f32 v26, v26, v114, v111
	v_max3_f32 v26, v26, v117, v113
	v_max3_f32 v26, v26, v115, v112
	v_max3_f32 v26, v26, v118, v116
	v_max3_f32 v26, v26, v122, v119
	v_max3_f32 v26, v26, v125, v121
	v_max3_f32 v26, v26, v123, v120
	v_max3_f32 v26, v26, v126, v124
	v_max3_f32 v26, v26, v131, v128
	v_max3_f32 v26, v26, v135, v130
	v_max3_f32 v26, v26, v132, v129
	v_max3_f32 v26, v26, v136, v134
	v_max3_f32 v26, v26, v140, v137
	v_max3_f32 v26, v26, v143, v139
	v_max3_f32 v26, v26, v141, v138
	v_max3_f32 v26, v26, v144, v142
	v_mad_u32_u24 v89, v89, s64, v30
	v_max3_f32 v26, v26, v148, v145
	s_waitcnt vmcnt(3)
	ds_write_b128 v75, v[10:13]
	s_waitcnt vmcnt(2)
	ds_write_b128 v75, v[14:17] offset:9216
	s_waitcnt lgkmcnt(0)
	s_barrier
	ds_read_b128 v[10:13], v89
	ds_read_b128 v[14:17], v89 offset:64
	v_max3_f32 v26, v26, v151, v147
	v_max3_f32 v26, v26, v149, v146
	v_max3_f32 v26, v26, v152, v150
	v_max3_f32 v26, v26, v155, v153
	v_max3_f32 v35, v26, v157, v154
	v_or_b32_e32 v26, 0x80, v34
	v_mov_b64_e32 v[44:45], s[8:9]
	v_mad_i64_i32 v[26:27], s[28:29], v26, s57, v[44:45]
	v_lshl_add_u64 v[26:27], v[26:27], 0, v[70:71]
	v_lshl_add_u64 v[30:31], v[26:27], 0, s[2:3]
	s_waitcnt lgkmcnt(1)
	v_mfma_f32_16x16x32_bf16 v[10:13], v[10:13], v[6:9], 0
	global_load_dwordx4 v[26:29], v[30:31], off offset:1024
	s_nop 0
	global_load_dwordx4 v[30:33], v[30:31], off offset:1152
	ds_read_b128 v[36:39], v89 offset:2304
	v_lshl_add_u64 v[78:79], s[4:5], 0, v[70:71]
	s_waitcnt lgkmcnt(1)
	v_mfma_f32_16x16x32_bf16 v[62:65], v[14:17], v[2:5], v[10:13]
	s_ashr_i32 s17, s16, 31
	v_mov_b32_e32 v81, v71
	v_cmp_lt_i32_e32 vcc, v83, v84
	ds_read_b128 v[10:13], v89 offset:2368
	v_add3_u32 v156, v86, v76, v87
	s_nop 2
	v_mul_f32_e32 v14, 0x3e000000, v62
	v_mul_f32_e32 v15, 0x3e000000, v63
	v_max3_f32 v35, v35, v14, v15
	v_mul_f32_e32 v40, 0x3e000000, v64
	s_waitcnt lgkmcnt(1)
	v_mfma_f32_16x16x32_bf16 v[14:17], v[36:39], v[6:9], 0
	v_mul_f32_e32 v36, 0x3e000000, v65
	v_max3_f32 v35, v35, v40, v36
	ds_read_b128 v[36:39], v89 offset:4608
	s_waitcnt lgkmcnt(1)
	v_mfma_f32_16x16x32_bf16 v[66:69], v[10:13], v[2:5], v[14:17]
	ds_read_b128 v[10:13], v89 offset:4672
	s_ashr_i32 s19, s18, 31
	s_ashr_i32 s21, s20, 31
	s_ashr_i32 s23, s22, 31
	s_ashr_i32 s25, s24, 31
	s_nop 2
	v_mul_f32_e32 v14, 0x3e000000, v66
	v_mul_f32_e32 v15, 0x3e000000, v67
	v_max3_f32 v35, v35, v14, v15
	s_waitcnt lgkmcnt(1)
	v_mfma_f32_16x16x32_bf16 v[14:17], v[36:39], v[6:9], 0
	v_mul_f32_e32 v40, 0x3e000000, v68
	v_mul_f32_e32 v41, 0x3e000000, v69
	v_max3_f32 v35, v35, v40, v41
	s_waitcnt lgkmcnt(0)
	v_mfma_f32_16x16x32_bf16 v[58:61], v[10:13], v[2:5], v[14:17]
	ds_read_b128 v[36:39], v89 offset:6912
	ds_read_b128 v[40:43], v89 offset:6976
	s_waitcnt vmcnt(3)
	ds_write_b128 v75, v[18:21] offset:18432
	s_waitcnt vmcnt(2)
	ds_write_b128 v75, v[22:25] offset:27648
	s_waitcnt lgkmcnt(0)
	s_nop 0
	v_mul_f32_e32 v10, 0x3e000000, v58
	v_mul_f32_e32 v11, 0x3e000000, v59
	v_max3_f32 v14, v35, v10, v11
	v_mfma_f32_16x16x32_bf16 v[10:13], v[36:39], v[6:9], 0
	v_mul_f32_e32 v15, 0x3e000000, v60
	v_mul_f32_e32 v16, 0x3e000000, v61
	v_max3_f32 v14, v14, v15, v16
	v_mfma_f32_16x16x32_bf16 v[54:57], v[40:43], v[2:5], v[10:13]
	s_barrier
; #define LAS __attribute__((address_space(3)))
; template <bool LOCAL>
; __device__ __forceinline__ void na_unit(const bf16* P, const bf16* VT, bf16* YCAT, const LAS float* rpb_l, LAS bf16* buf, int b, int gr, int hp, int qblk, int tid) {
;     ...
;             } else {
;                 const int cc = c - NLOC;
; #pragma unroll
;                 for (int t4 = 0; t4 < 4; ++t4) {
;                     const LAS bf16* kp = cb + (16 * t4 + fr) * 72 + 8 * fq;
;                     f32x4 acc = {0.f, 0.f, 0.f, 0.f};
;                     acc = __builtin_amdgcn_mfma_f32_16x16x32_bf16(*(const LAS bf16x8*)(kp), qf[0], acc, 0, 0, 0);
;                     acc = __builtin_amdgcn_mfma_f32_16x16x32_bf16(*(const LAS bf16x8*)(kp + 32), qf[1], acc, 0, 0, 0);
; #pragma unroll
;                     for (int e = 0; e < 4; ++e) { acc[e] *= 0.125f; m = fmaxf(m, acc[e]); }
;                     sc[4 * (cc >= 0 ? cc : 0) + t4] = acc; }
;             }
;             if (sidx == NCH - 1) { m = fmaxf(m, __shfl_xor(m, 16)); m = fmaxf(m, __shfl_xor(m, 32)); }
	v_or_b32_e32 v18, 0xc0, v34
	v_mad_i64_i32 v[18:19], s[28:29], v18, s57, v[44:45]
	v_lshl_add_u64 v[18:19], v[18:19], 0, v[70:71]
	s_nop 3
	v_mul_f32_e32 v10, 0x3e000000, v54
	v_mul_f32_e32 v11, 0x3e000000, v55
	v_max3_f32 v14, v14, v10, v11
	ds_read_b128 v[10:13], v89 offset:18432
	v_mul_f32_e32 v15, 0x3e000000, v56
	v_mul_f32_e32 v16, 0x3e000000, v57
	v_max3_f32 v35, v14, v15, v16
	ds_read_b128 v[14:17], v89 offset:18496
	v_lshl_add_u64 v[22:23], v[18:19], 0, s[2:3]
	s_waitcnt lgkmcnt(1)
	v_mfma_f32_16x16x32_bf16 v[10:13], v[10:13], v[6:9], 0
	global_load_dwordx4 v[18:21], v[22:23], off offset:1024
	global_load_dwordx4 v[158:161], v[22:23], off offset:1152
	ds_read_b128 v[22:25], v89 offset:20736
	s_ashr_i32 s27, s26, 31
	s_waitcnt lgkmcnt(1)
	v_mfma_f32_16x16x32_bf16 v[46:49], v[14:17], v[2:5], v[10:13]
	s_nop 2
	ds_read_b128 v[10:13], v89 offset:20800
	s_nop 3
	v_mul_f32_e32 v14, 0x3e000000, v46
	v_mul_f32_e32 v15, 0x3e000000, v47
	v_max3_f32 v34, v35, v14, v15
	v_mul_f32_e32 v35, 0x3e000000, v48
	s_waitcnt lgkmcnt(1)
	v_mfma_f32_16x16x32_bf16 v[14:17], v[22:25], v[6:9], 0
	v_mul_f32_e32 v22, 0x3e000000, v49
	v_max3_f32 v34, v34, v35, v22
	ds_read_b128 v[22:25], v89 offset:23040
	s_waitcnt lgkmcnt(1)
	v_mfma_f32_16x16x32_bf16 v[50:53], v[10:13], v[2:5], v[14:17]
	ds_read_b128 v[10:13], v89 offset:23104
	s_nop 6
	v_mul_f32_e32 v14, 0x3e000000, v50
	v_mul_f32_e32 v15, 0x3e000000, v51
	v_max3_f32 v34, v34, v14, v15
	s_waitcnt lgkmcnt(1)
	v_mfma_f32_16x16x32_bf16 v[14:17], v[22:25], v[6:9], 0
	v_mul_f32_e32 v35, 0x3e000000, v52
	v_mul_f32_e32 v36, 0x3e000000, v53
	v_max3_f32 v38, v34, v35, v36
	s_waitcnt lgkmcnt(0)
	v_mfma_f32_16x16x32_bf16 v[42:45], v[10:13], v[2:5], v[14:17]
	ds_read_b128 v[22:25], v89 offset:25344
	ds_read_b128 v[34:37], v89 offset:25408
	s_waitcnt vmcnt(3)
	ds_write_b128 v75, v[26:29]
	s_waitcnt vmcnt(2)
	ds_write_b128 v75, v[30:33] offset:9216
	s_waitcnt lgkmcnt(0)
	s_nop 0
	v_mul_f32_e32 v10, 0x3e000000, v42
	v_mul_f32_e32 v11, 0x3e000000, v43
	v_max3_f32 v14, v38, v10, v11
	v_mfma_f32_16x16x32_bf16 v[10:13], v[22:25], v[6:9], 0
	v_mul_f32_e32 v15, 0x3e000000, v44
	v_mul_f32_e32 v16, 0x3e000000, v45
	v_max3_f32 v14, v14, v15, v16
	v_mfma_f32_16x16x32_bf16 v[38:41], v[34:37], v[2:5], v[10:13]
	s_barrier
	v_add3_u32 v26, v88, s1, 64
	v_mul_u32_u24_e32 v26, 0x9000, v26
	v_lshl_add_u64 v[22:23], s[16:17], 1, v[78:79]
	s_nop 3
	v_mul_f32_e32 v10, 0x3e000000, v38
	v_mul_f32_e32 v11, 0x3e000000, v39
	v_max3_f32 v10, v14, v10, v11
	v_mul_f32_e32 v11, 0x3e000000, v40
	v_mul_f32_e32 v12, 0x3e000000, v41
	v_max3_f32 v34, v10, v11, v12
	v_or_b32_e32 v10, s1, v88
	v_mul_u32_u24_e32 v14, 0x9000, v10
	ds_read_b128 v[10:13], v89
	v_lshlrev_b32_e32 v70, 1, v14
	ds_read_b128 v[14:17], v89 offset:64
	v_lshlrev_b32_e32 v80, 1, v26
	v_lshl_add_u64 v[24:25], v[22:23], 0, v[70:71]
	v_lshl_add_u64 v[22:23], v[22:23], 0, v[80:81]
	s_waitcnt lgkmcnt(1)
	v_mfma_f32_16x16x32_bf16 v[10:13], v[10:13], v[6:9], 0
	global_load_dwordx4 v[162:165], v[24:25], off
	global_load_dwordx4 v[166:169], v[22:23], off
	ds_read_b128 v[22:25], v89 offset:2304
	s_add_i32 s16, s15, s50
	s_waitcnt lgkmcnt(1)
	v_mfma_f32_16x16x32_bf16 v[30:33], v[14:17], v[2:5], v[10:13]
	s_ashr_i32 s17, s16, 31
	s_ashr_i32 s15, s14, 31
	v_lshl_add_u64 v[86:87], s[14:15], 1, v[78:79]
	ds_read_b128 v[10:13], v89 offset:2368
	s_ashr_i32 s1, s0, 31
	s_nop 2
	v_mul_f32_e32 v14, 0x3e000000, v30
	v_mul_f32_e32 v15, 0x3e000000, v31
	v_max3_f32 v26, v34, v14, v15
	v_mul_f32_e32 v27, 0x3e000000, v32
	s_waitcnt lgkmcnt(1)
	v_mfma_f32_16x16x32_bf16 v[14:17], v[22:25], v[6:9], 0
	v_mul_f32_e32 v22, 0x3e000000, v33
	v_max3_f32 v26, v26, v27, v22
	ds_read_b128 v[22:25], v89 offset:4608
	s_waitcnt lgkmcnt(1)
	v_mfma_f32_16x16x32_bf16 v[34:37], v[10:13], v[2:5], v[14:17]
	ds_read_b128 v[10:13], v89 offset:4672
	s_nop 6
	v_mul_f32_e32 v14, 0x3e000000, v34
	v_mul_f32_e32 v15, 0x3e000000, v35
	v_max3_f32 v26, v26, v14, v15
	s_waitcnt lgkmcnt(1)
	v_mfma_f32_16x16x32_bf16 v[14:17], v[22:25], v[6:9], 0
	v_mul_f32_e32 v27, 0x3e000000, v36
	v_mul_f32_e32 v28, 0x3e000000, v37
	v_max3_f32 v88, v26, v27, v28
	s_waitcnt lgkmcnt(0)
	v_mfma_f32_16x16x32_bf16 v[26:29], v[10:13], v[2:5], v[14:17]
	ds_read_b128 v[22:25], v89 offset:6912
	ds_read_b128 v[170:173], v89 offset:6976
	s_waitcnt vmcnt(3)
	ds_write_b128 v75, v[18:21] offset:18432
	s_waitcnt vmcnt(2)
	ds_write_b128 v75, v[158:161] offset:27648
	s_waitcnt lgkmcnt(0)
	s_nop 0
	v_mul_f32_e32 v10, 0x3e000000, v26
	v_mul_f32_e32 v11, 0x3e000000, v27
	v_max3_f32 v14, v88, v10, v11
	v_mfma_f32_16x16x32_bf16 v[10:13], v[22:25], v[6:9], 0
	v_mul_f32_e32 v15, 0x3e000000, v28
	v_mul_f32_e32 v16, 0x3e000000, v29
	v_max3_f32 v14, v14, v15, v16
	v_mfma_f32_16x16x32_bf16 v[22:25], v[170:173], v[2:5], v[10:13]
	s_barrier
; #define LAS __attribute__((address_space(3)))
; __device__ __forceinline__ unsigned cvt_pk_bf16(float lo, float hi) { const float __attribute__((ext_vector_type(2))) v = {lo, hi}; return __builtin_bit_cast(unsigned, __builtin_convertvector(v, bf16x2_t)); }
; template <bool LOCAL>
; __device__ __forceinline__ void na_unit(const bf16* P, const bf16* VT, bf16* YCAT, const LAS float* rpb_l, LAS bf16* buf, int b, int gr, int hp, int qblk, int tid) {
;     ...
;                 const int cc = c - NLOC;
; #pragma unroll
;                 for (int t4 = 0; t4 < 4; ++t4) {
;                     const LAS bf16* kp = cb + (16 * t4 + fr) * 72 + 8 * fq;
;                     f32x4 acc = {0.f, 0.f, 0.f, 0.f};
;                     acc = __builtin_amdgcn_mfma_f32_16x16x32_bf16(*(const LAS bf16x8*)(kp), qf[0], acc, 0, 0, 0);
;                     acc = __builtin_amdgcn_mfma_f32_16x16x32_bf16(*(const LAS bf16x8*)(kp + 32), qf[1], acc, 0, 0, 0);
; #pragma unroll
;                     for (int e = 0; e < 4; ++e) { acc[e] *= 0.125f; m = fmaxf(m, acc[e]); }
;                     sc[4 * (cc >= 0 ? cc : 0) + t4] = acc; }
;             }
;             if (sidx == NCH - 1) { m = fmaxf(m, __shfl_xor(m, 16)); m = fmaxf(m, __shfl_xor(m, 32)); }
;         } else {
;             const int c = sidx - NCH;
;             if (LOCAL && c < 8) {
;                 float p[8];
; #pragma unroll
;                 for (int e = 0; e < 4; ++e) { p[e] = __expf(sl[2 * (c < 8 ? c : 0)][e] - m); p[4 + e] = __expf(sl[2 * (c < 8 ? c : 0) + 1][e] - m); }
; #pragma unroll
;                 for (int e = 0; e < 8; ++e) lsum += p[e];
;                 const bf16x8 pf = __builtin_bit_cast(bf16x8, (v4u){pg8::cvt_pk_bf16(p[0], p[1]), pg8::cvt_pk_bf16(p[2], p[3]), pg8::cvt_pk_bf16(p[4], p[5]), pg8::cvt_pk_bf16(p[6], p[7])});
; #pragma unroll
;                 for (int dt = 0; dt < 4; ++dt) { const LAS bf16* vp = cb + (16 * dt + fr) * 72 + kc0 + 4 * fq;
;                     o[dt] = __builtin_amdgcn_mfma_f32_16x16x32_bf16(frag44(vp, vp + 16), pf, o[dt], 0, 0, 0); }
	v_lshl_add_u64 v[18:19], s[16:17], 1, v[78:79]
	v_lshl_add_u64 v[20:21], v[18:19], 0, v[70:71]
	v_lshl_add_u64 v[18:19], v[18:19], 0, v[80:81]
	s_nop 3
	v_mul_f32_e32 v10, 0x3e000000, v22
	v_mul_f32_e32 v11, 0x3e000000, v23
	v_max3_f32 v14, v14, v10, v11
	ds_read_b128 v[10:13], v89 offset:18432
	v_mul_f32_e32 v15, 0x3e000000, v24
	v_mul_f32_e32 v16, 0x3e000000, v25
	v_max3_f32 v88, v14, v15, v16
	ds_read_b128 v[14:17], v89 offset:18496
	s_waitcnt lgkmcnt(1)
	v_mfma_f32_16x16x32_bf16 v[10:13], v[10:13], v[6:9], 0
	global_load_dwordx4 v[170:173], v[20:21], off
	global_load_dwordx4 v[174:177], v[18:19], off
	ds_read_b128 v[18:21], v89 offset:20736
	ds_read_b128 v[158:161], v89 offset:23040
	s_waitcnt lgkmcnt(2)
	v_mfma_f32_16x16x32_bf16 v[14:17], v[14:17], v[2:5], v[10:13]
	s_nop 2
	ds_read_b128 v[10:13], v89 offset:20800
	s_waitcnt lgkmcnt(2)
	v_mfma_f32_16x16x32_bf16 v[18:21], v[18:21], v[6:9], 0
	s_nop 1
	v_mul_f32_e32 v127, 0x3e000000, v14
	v_mul_f32_e32 v133, 0x3e000000, v15
	v_max3_f32 v88, v88, v127, v133
	s_waitcnt lgkmcnt(0)
	v_mfma_f32_16x16x32_bf16 v[18:21], v[10:13], v[2:5], v[18:21]
	ds_read_b128 v[10:13], v89 offset:23104
	ds_read_b128 v[178:181], v89 offset:25344
	ds_read_b128 v[182:185], v89 offset:25408
	v_mul_f32_e32 v127, 0x3e000000, v16
	v_mfma_f32_16x16x32_bf16 v[158:161], v[158:161], v[6:9], 0
	v_mul_f32_e32 v133, 0x3e000000, v17
	v_max3_f32 v88, v88, v127, v133
	s_nop 0
	v_mul_f32_e32 v127, 0x3e000000, v18
	s_waitcnt lgkmcnt(1)
	v_mfma_f32_16x16x32_bf16 v[6:9], v[178:181], v[6:9], 0
	v_mul_f32_e32 v133, 0x3e000000, v19
	v_max3_f32 v88, v88, v127, v133
	v_mul_f32_e32 v127, 0x3e000000, v20
	v_mfma_f32_16x16x32_bf16 v[10:13], v[10:13], v[2:5], v[158:161]
	v_mul_f32_e32 v133, 0x3e000000, v21
	v_max3_f32 v88, v88, v127, v133
	s_waitcnt vmcnt(3)
	ds_write_b128 v75, v[162:165]
	s_waitcnt vmcnt(2)
	ds_write_b128 v75, v[166:169] offset:9216
	s_waitcnt lgkmcnt(2)
	v_mfma_f32_16x16x32_bf16 v[2:5], v[182:185], v[2:5], v[6:9]
	v_mul_f32_e32 v89, 0x3e000000, v10
	v_mul_f32_e32 v127, 0x3e000000, v11
	v_max3_f32 v88, v88, v89, v127
	v_mul_f32_e32 v89, 0x3e000000, v12
	v_mul_f32_e32 v127, 0x3e000000, v13
	v_max3_f32 v88, v88, v89, v127
	s_nop 1
	v_mul_f32_e32 v6, 0x3e000000, v2
	v_mul_f32_e32 v7, 0x3e000000, v3
	v_max3_f32 v6, v88, v6, v7
	v_mul_f32_e32 v7, 0x3e000000, v4
	v_mul_f32_e32 v8, 0x3e000000, v5
	v_max3_f32 v6, v6, v7, v8
	v_cndmask_b32_e32 v7, v82, v83, vcc
	v_lshlrev_b32_e32 v88, 2, v7
	ds_bpermute_b32 v7, v88, v6
	v_cmp_lt_i32_e32 vcc, v85, v84
	v_lshl_add_u32 v8, v90, 1, v156
	s_waitcnt lgkmcnt(0)
	s_barrier
	v_max_f32_e32 v7, v7, v7
	v_max_f32_e32 v6, v6, v7
	v_cndmask_b32_e32 v7, v82, v85, vcc
	v_lshlrev_b32_e32 v89, 2, v7
	ds_bpermute_b32 v7, v89, v6
	s_waitcnt lgkmcnt(0)
	ds_read2_b64 v[158:161], v8 offset1:4
	v_max_f32_e32 v7, v7, v7
	v_max_f32_e32 v133, v6, v7
	v_sub_f32_e32 v6, v92, v133
	v_mul_f32_e32 v6, 0x3fb8aa3b, v6
	v_exp_f32_e32 v127, v6
	v_sub_f32_e32 v6, v96, v133
	v_mul_f32_e32 v6, 0x3fb8aa3b, v6
	v_exp_f32_e32 v92, v6
	v_sub_f32_e32 v6, v91, v133
	v_mul_f32_e32 v6, 0x3fb8aa3b, v6
	v_exp_f32_e32 v96, v6
	v_sub_f32_e32 v6, v95, v133
	v_mul_f32_e32 v6, 0x3fb8aa3b, v6
	v_exp_f32_e32 v91, v6
	v_sub_f32_e32 v6, v94, v133
	v_mul_f32_e32 v6, 0x3fb8aa3b, v6
	v_exp_f32_e32 v95, v6
	v_sub_f32_e32 v6, v100, v133
	v_mul_f32_e32 v6, 0x3fb8aa3b, v6
	v_exp_f32_e32 v94, v6
	v_sub_f32_e32 v6, v93, v133
	v_mul_f32_e32 v6, 0x3fb8aa3b, v6
	v_exp_f32_e32 v100, v6
	v_sub_f32_e32 v6, v99, v133
	v_mul_f32_e32 v6, 0x3fb8aa3b, v6
	v_exp_f32_e32 v93, v6
	v_cvt_pk_bf16_f32 v162, v127, v96
	v_cvt_pk_bf16_f32 v163, v95, v100
	v_cvt_pk_bf16_f32 v164, v92, v91
	v_cvt_pk_bf16_f32 v165, v94, v93
	v_add_u32_e32 v7, 0x800, v8
	v_add_u32_e32 v6, 0x1000, v8
	s_waitcnt lgkmcnt(0)
	v_mfma_f32_16x16x32_bf16 v[182:185], v[158:161], v[162:165], 0
	v_lshl_add_u64 v[158:159], v[86:87], 0, v[70:71]
	ds_read2_b64 v[166:169], v7 offset0:32 offset1:36
	ds_read2_b64 v[178:181], v6 offset0:64 offset1:68
	v_lshl_add_u64 v[86:87], v[86:87], 0, v[80:81]
	global_load_dwordx4 v[186:189], v[158:159], off
	global_load_dwordx4 v[190:193], v[86:87], off
	v_sub_f32_e32 v9, v98, v133
	v_mul_f32_e32 v9, 0x3fb8aa3b, v9
	v_add_u32_e32 v158, 0x1800, v8
	v_exp_f32_e32 v86, v9
	v_sub_f32_e32 v9, v106, v133
	ds_read2_b64 v[194:197], v158 offset0:96 offset1:100
	v_mul_f32_e32 v9, 0x3fb8aa3b, v9
	v_exp_f32_e32 v76, v9
	v_sub_f32_e32 v9, v97, v133
	v_mul_f32_e32 v9, 0x3fb8aa3b, v9
	v_exp_f32_e32 v90, v9
	v_sub_f32_e32 v9, v104, v133
	v_mul_f32_e32 v9, 0x3fb8aa3b, v9
	v_exp_f32_e32 v87, v9
	v_sub_f32_e32 v9, v102, v133
	v_mul_f32_e32 v9, 0x3fb8aa3b, v9
	v_exp_f32_e32 v98, v9
	v_sub_f32_e32 v9, v110, v133
	v_mul_f32_e32 v9, 0x3fb8aa3b, v9
	v_add_u32_e32 v160, 0x4800, v8
	s_waitcnt lgkmcnt(2)
	v_mfma_f32_16x16x32_bf16 v[166:169], v[166:169], v[162:165], 0
	s_waitcnt vmcnt(3)
	ds_write_b128 v75, v[170:173] offset:18432
	s_waitcnt vmcnt(2)
	ds_write_b128 v75, v[174:177] offset:27648
	s_waitcnt lgkmcnt(0)
	s_barrier
; #define LAS __attribute__((address_space(3)))
; __device__ __forceinline__ unsigned cvt_pk_bf16(float lo, float hi) { const float __attribute__((ext_vector_type(2))) v = {lo, hi}; return __builtin_bit_cast(unsigned, __builtin_convertvector(v, bf16x2_t)); }
; template <bool LOCAL>
; __device__ __forceinline__ void na_unit(const bf16* P, const bf16* VT, bf16* YCAT, const LAS float* rpb_l, LAS bf16* buf, int b, int gr, int hp, int qblk, int tid) {
;     ...
;             const int c = sidx - NCH;
;             if (LOCAL && c < 8) {
;                 float p[8];
; #pragma unroll
;                 for (int e = 0; e < 4; ++e) { p[e] = __expf(sl[2 * (c < 8 ? c : 0)][e] - m); p[4 + e] = __expf(sl[2 * (c < 8 ? c : 0) + 1][e] - m); }
; #pragma unroll
;                 for (int e = 0; e < 8; ++e) lsum += p[e];
;                 const bf16x8 pf = __builtin_bit_cast(bf16x8, (v4u){pg8::cvt_pk_bf16(p[0], p[1]), pg8::cvt_pk_bf16(p[2], p[3]), pg8::cvt_pk_bf16(p[4], p[5]), pg8::cvt_pk_bf16(p[6], p[7])});
; #pragma unroll
;                 for (int dt = 0; dt < 4; ++dt) { const LAS bf16* vp = cb + (16 * dt + fr) * 72 + kc0 + 4 * fq;
;                     o[dt] = __builtin_amdgcn_mfma_f32_16x16x32_bf16(frag44(vp, vp + 16), pf, o[dt], 0, 0, 0); }
	v_mfma_f32_16x16x32_bf16 v[178:181], v[178:181], v[162:165], 0
	v_exp_f32_e32 v97, v9
	v_sub_f32_e32 v9, v101, v133
	v_mfma_f32_16x16x32_bf16 v[194:197], v[194:197], v[162:165], 0
	ds_read2_b64 v[162:165], v160 offset1:4
	v_mul_f32_e32 v9, 0x3fb8aa3b, v9
	v_add_u32_e32 v159, 0x5000, v8
	v_exp_f32_e32 v99, v9
	v_sub_f32_e32 v9, v108, v133
	ds_read2_b64 v[170:173], v159 offset0:32 offset1:36
	v_mul_f32_e32 v9, 0x3fb8aa3b, v9
	v_exp_f32_e32 v101, v9
	v_cvt_pk_bf16_f32 v174, v86, v90
	v_cvt_pk_bf16_f32 v175, v98, v99
	v_cvt_pk_bf16_f32 v176, v76, v87
	v_cvt_pk_bf16_f32 v177, v97, v101
	v_add_u32_e32 v161, 0x5800, v8
	v_sub_f32_e32 v9, v105, v133
	s_waitcnt lgkmcnt(1)
	v_mfma_f32_16x16x32_bf16 v[182:185], v[162:165], v[174:177], v[182:185]
	v_lshl_add_u64 v[162:163], s[0:1], 1, v[78:79]
	v_lshl_add_u64 v[198:199], v[162:163], 0, v[70:71]
	v_lshl_add_u64 v[162:163], v[162:163], 0, v[80:81]
	s_waitcnt lgkmcnt(0)
	v_mfma_f32_16x16x32_bf16 v[164:167], v[170:173], v[174:177], v[166:169]
	v_mul_f32_e32 v9, 0x3fb8aa3b, v9
	v_exp_f32_e32 v104, v9
	v_sub_f32_e32 v9, v114, v133
	ds_read2_b64 v[168:171], v161 offset0:64 offset1:68
	global_load_dwordx4 v[198:201], v[198:199], off
	s_nop 0
	global_load_dwordx4 v[202:205], v[162:163], off
	v_add_u32_e32 v162, 0x6000, v8
	s_waitcnt lgkmcnt(0)
	v_mfma_f32_16x16x32_bf16 v[168:171], v[168:171], v[174:177], v[178:181]
	s_nop 2
	ds_read2_b64 v[178:181], v162 offset0:96 offset1:100
	v_mul_f32_e32 v9, 0x3fb8aa3b, v9
	v_exp_f32_e32 v102, v9
	v_sub_f32_e32 v9, v103, v133
	v_mul_f32_e32 v9, 0x3fb8aa3b, v9
	v_exp_f32_e32 v105, v9
	v_sub_f32_e32 v9, v111, v133
	v_mul_f32_e32 v9, 0x3fb8aa3b, v9
	v_exp_f32_e32 v103, v9
	v_sub_f32_e32 v9, v109, v133
	v_mul_f32_e32 v9, 0x3fb8aa3b, v9
	v_exp_f32_e32 v108, v9
	v_sub_f32_e32 v9, v117, v133
	v_mul_f32_e32 v9, 0x3fb8aa3b, v9
	s_waitcnt lgkmcnt(0)
	v_mfma_f32_16x16x32_bf16 v[172:175], v[178:181], v[174:177], v[194:197]
	s_waitcnt vmcnt(3)
	ds_write_b128 v75, v[186:189]
	s_waitcnt vmcnt(2)
	ds_write_b128 v75, v[190:193] offset:9216
	s_waitcnt lgkmcnt(0)
	s_barrier
	v_exp_f32_e32 v106, v9
	v_sub_f32_e32 v9, v107, v133
	ds_read2_b64 v[176:179], v8 offset1:4
	ds_read2_b64 v[186:189], v7 offset0:32 offset1:36
	v_mul_f32_e32 v9, 0x3fb8aa3b, v9
	v_exp_f32_e32 v107, v9
	v_sub_f32_e32 v9, v113, v133
	v_mul_f32_e32 v9, 0x3fb8aa3b, v9
	v_exp_f32_e32 v109, v9
	v_lshl_add_u64 v[194:195], s[18:19], 1, v[78:79]
	v_cvt_pk_bf16_f32 v190, v104, v105
	v_cvt_pk_bf16_f32 v191, v108, v107
	v_cvt_pk_bf16_f32 v192, v102, v103
	v_cvt_pk_bf16_f32 v193, v106, v109
	v_lshl_add_u64 v[110:111], v[194:195], 0, v[70:71]
	v_lshl_add_u64 v[194:195], v[194:195], 0, v[80:81]
	s_waitcnt lgkmcnt(1)
	v_mfma_f32_16x16x32_bf16 v[176:179], v[176:179], v[190:193], v[182:185]
	v_sub_f32_e32 v9, v115, v133
	v_mul_f32_e32 v9, 0x3fb8aa3b, v9
	v_fma_f32 v62, v62, s66, -v133
	ds_read2_b64 v[180:183], v6 offset0:64 offset1:68
	s_waitcnt lgkmcnt(1)
	v_mfma_f32_16x16x32_bf16 v[164:167], v[186:189], v[190:193], v[164:167]
	global_load_dwordx4 v[184:187], v[110:111], off
	s_nop 0
	global_load_dwordx4 v[194:197], v[194:195], off
	v_exp_f32_e32 v111, v9
	v_sub_f32_e32 v9, v122, v133
	s_waitcnt lgkmcnt(0)
	v_mfma_f32_16x16x32_bf16 v[168:171], v[180:183], v[190:193], v[168:171]
	ds_read2_b64 v[180:183], v158 offset0:96 offset1:100
	v_mul_f32_e32 v9, 0x3fb8aa3b, v9
	v_exp_f32_e32 v110, v9
	v_sub_f32_e32 v9, v112, v133
	v_mul_f32_e32 v9, 0x3fb8aa3b, v9
	v_exp_f32_e32 v113, v9
	v_sub_f32_e32 v9, v119, v133
	v_mul_f32_e32 v9, 0x3fb8aa3b, v9
	v_exp_f32_e32 v112, v9
	v_sub_f32_e32 v9, v118, v133
	v_mul_f32_e32 v9, 0x3fb8aa3b, v9
	v_exp_f32_e32 v115, v9
	v_sub_f32_e32 v9, v125, v133
	v_mul_f32_e32 v9, 0x3fb8aa3b, v9
	s_waitcnt lgkmcnt(0)
	v_mfma_f32_16x16x32_bf16 v[172:175], v[180:183], v[190:193], v[172:175]
	s_waitcnt vmcnt(3)
	ds_write_b128 v75, v[198:201] offset:18432
	s_waitcnt vmcnt(2)
	ds_write_b128 v75, v[202:205] offset:27648
	s_waitcnt lgkmcnt(0)
	s_barrier
	v_exp_f32_e32 v114, v9
	v_sub_f32_e32 v9, v116, v133
	ds_read2_b64 v[180:183], v160 offset1:4
	ds_read2_b64 v[188:191], v159 offset0:32 offset1:36
	v_mul_f32_e32 v9, 0x3fb8aa3b, v9
	v_exp_f32_e32 v116, v9
	v_sub_f32_e32 v9, v121, v133
	v_mul_f32_e32 v9, 0x3fb8aa3b, v9
	v_exp_f32_e32 v117, v9
	v_lshl_add_u64 v[192:193], s[20:21], 1, v[78:79]
	v_lshl_add_u64 v[202:203], v[192:193], 0, v[70:71]
	v_cvt_pk_bf16_f32 v198, v111, v113
	v_cvt_pk_bf16_f32 v199, v115, v116
	v_cvt_pk_bf16_f32 v200, v110, v112
	v_cvt_pk_bf16_f32 v201, v114, v117
	v_lshl_add_u64 v[118:119], v[192:193], 0, v[80:81]
	v_sub_f32_e32 v9, v123, v133
	s_waitcnt lgkmcnt(1)
	v_mfma_f32_16x16x32_bf16 v[176:179], v[180:183], v[198:201], v[176:179]
	global_load_dwordx4 v[180:183], v[202:203], off
	s_nop 0
	global_load_dwordx4 v[202:205], v[118:119], off
	v_mul_f32_e32 v9, 0x3fb8aa3b, v9
	v_exp_f32_e32 v119, v9
	s_waitcnt lgkmcnt(0)
	v_mfma_f32_16x16x32_bf16 v[164:167], v[188:191], v[198:201], v[164:167]
	ds_read2_b64 v[188:191], v161 offset0:64 offset1:68
	v_sub_f32_e32 v9, v131, v133
	v_mul_f32_e32 v9, 0x3fb8aa3b, v9
	s_waitcnt lgkmcnt(0)
	v_mfma_f32_16x16x32_bf16 v[168:171], v[188:191], v[198:201], v[168:171]
	ds_read2_b64 v[188:191], v162 offset0:96 offset1:100
	v_exp_f32_e32 v118, v9
	v_sub_f32_e32 v9, v120, v133
	v_mul_f32_e32 v9, 0x3fb8aa3b, v9
	v_exp_f32_e32 v121, v9
	v_sub_f32_e32 v9, v128, v133
	v_mul_f32_e32 v9, 0x3fb8aa3b, v9
	v_exp_f32_e32 v120, v9
	v_sub_f32_e32 v9, v126, v133
	v_mul_f32_e32 v9, 0x3fb8aa3b, v9
	v_exp_f32_e32 v123, v9
	v_sub_f32_e32 v9, v135, v133
	v_mul_f32_e32 v9, 0x3fb8aa3b, v9
	s_waitcnt lgkmcnt(0)
	v_mfma_f32_16x16x32_bf16 v[172:175], v[188:191], v[198:201], v[172:175]
	s_waitcnt vmcnt(3)
	ds_write_b128 v75, v[184:187]
	s_waitcnt vmcnt(2)
	ds_write_b128 v75, v[194:197] offset:9216
	s_waitcnt lgkmcnt(0)
	s_barrier
; #define LAS __attribute__((address_space(3)))
; __device__ __forceinline__ unsigned cvt_pk_bf16(float lo, float hi) { const float __attribute__((ext_vector_type(2))) v = {lo, hi}; return __builtin_bit_cast(unsigned, __builtin_convertvector(v, bf16x2_t)); }
; template <bool LOCAL>
; __device__ __forceinline__ void na_unit(const bf16* P, const bf16* VT, bf16* YCAT, const LAS float* rpb_l, LAS bf16* buf, int b, int gr, int hp, int qblk, int tid) {
;     ...
;             const int c = sidx - NCH;
;             if (LOCAL && c < 8) {
;                 float p[8];
; #pragma unroll
;                 for (int e = 0; e < 4; ++e) { p[e] = __expf(sl[2 * (c < 8 ? c : 0)][e] - m); p[4 + e] = __expf(sl[2 * (c < 8 ? c : 0) + 1][e] - m); }
; #pragma unroll
;                 for (int e = 0; e < 8; ++e) lsum += p[e];
;                 const bf16x8 pf = __builtin_bit_cast(bf16x8, (v4u){pg8::cvt_pk_bf16(p[0], p[1]), pg8::cvt_pk_bf16(p[2], p[3]), pg8::cvt_pk_bf16(p[4], p[5]), pg8::cvt_pk_bf16(p[6], p[7])});
; #pragma unroll
;                 for (int dt = 0; dt < 4; ++dt) { const LAS bf16* vp = cb + (16 * dt + fr) * 72 + kc0 + 4 * fq;
;                     o[dt] = __builtin_amdgcn_mfma_f32_16x16x32_bf16(frag44(vp, vp + 16), pf, o[dt], 0, 0, 0); }
	v_exp_f32_e32 v122, v9
	v_sub_f32_e32 v9, v124, v133
	ds_read2_b64 v[184:187], v8 offset1:4
	ds_read2_b64 v[188:191], v7 offset0:32 offset1:36
	v_mul_f32_e32 v9, 0x3fb8aa3b, v9
	v_exp_f32_e32 v124, v9
	v_sub_f32_e32 v9, v130, v133
	v_mul_f32_e32 v9, 0x3fb8aa3b, v9
	v_exp_f32_e32 v125, v9
	v_lshl_add_u64 v[196:197], s[22:23], 1, v[78:79]
	v_cvt_pk_bf16_f32 v192, v119, v121
	v_cvt_pk_bf16_f32 v193, v123, v124
	v_cvt_pk_bf16_f32 v194, v118, v120
	v_cvt_pk_bf16_f32 v195, v122, v125
	v_lshl_add_u64 v[130:131], v[196:197], 0, v[70:71]
	v_lshl_add_u64 v[196:197], v[196:197], 0, v[80:81]
	s_waitcnt lgkmcnt(1)
	v_mfma_f32_16x16x32_bf16 v[176:179], v[184:187], v[192:195], v[176:179]
	ds_read2_b64 v[184:187], v6 offset0:64 offset1:68
	v_sub_f32_e32 v9, v132, v133
	v_mul_f32_e32 v9, 0x3fb8aa3b, v9
	s_waitcnt lgkmcnt(1)
	v_mfma_f32_16x16x32_bf16 v[164:167], v[188:191], v[192:195], v[164:167]
	global_load_dwordx4 v[188:191], v[130:131], off
	s_nop 0
	global_load_dwordx4 v[196:199], v[196:197], off
	v_exp_f32_e32 v128, v9
	v_sub_f32_e32 v9, v140, v133
	s_waitcnt lgkmcnt(0)
	v_mfma_f32_16x16x32_bf16 v[168:171], v[184:187], v[192:195], v[168:171]
	ds_read2_b64 v[184:187], v158 offset0:96 offset1:100
	v_mul_f32_e32 v9, 0x3fb8aa3b, v9
	v_exp_f32_e32 v126, v9
	v_sub_f32_e32 v9, v129, v133
	v_mul_f32_e32 v9, 0x3fb8aa3b, v9
	v_exp_f32_e32 v130, v9
	v_sub_f32_e32 v9, v137, v133
	v_mul_f32_e32 v9, 0x3fb8aa3b, v9
	v_exp_f32_e32 v129, v9
	v_sub_f32_e32 v9, v136, v133
	v_mul_f32_e32 v9, 0x3fb8aa3b, v9
	v_exp_f32_e32 v132, v9
	v_sub_f32_e32 v9, v143, v133
	v_mul_f32_e32 v9, 0x3fb8aa3b, v9
	s_waitcnt lgkmcnt(0)
	v_mfma_f32_16x16x32_bf16 v[172:175], v[184:187], v[192:195], v[172:175]
	s_waitcnt vmcnt(3)
	ds_write_b128 v75, v[180:183] offset:18432
	s_waitcnt vmcnt(2)
	ds_write_b128 v75, v[202:205] offset:27648
	s_waitcnt lgkmcnt(0)
	s_barrier
	v_exp_f32_e32 v131, v9
	v_sub_f32_e32 v9, v134, v133
	ds_read2_b64 v[180:183], v160 offset1:4
	ds_read2_b64 v[184:187], v159 offset0:32 offset1:36
	v_mul_f32_e32 v9, 0x3fb8aa3b, v9
	v_exp_f32_e32 v134, v9
	v_sub_f32_e32 v9, v139, v133
	v_mul_f32_e32 v9, 0x3fb8aa3b, v9
	v_exp_f32_e32 v135, v9
	v_lshl_add_u64 v[200:201], s[24:25], 1, v[78:79]
	v_lshl_add_u64 v[202:203], v[200:201], 0, v[70:71]
	v_cvt_pk_bf16_f32 v192, v128, v130
	v_cvt_pk_bf16_f32 v193, v132, v134
	v_cvt_pk_bf16_f32 v194, v126, v129
	v_cvt_pk_bf16_f32 v195, v131, v135
	v_lshl_add_u64 v[136:137], v[200:201], 0, v[80:81]
	v_sub_f32_e32 v9, v141, v133
	s_waitcnt lgkmcnt(1)
	v_mfma_f32_16x16x32_bf16 v[176:179], v[180:183], v[192:195], v[176:179]
	global_load_dwordx4 v[180:183], v[202:203], off
	s_nop 0
	global_load_dwordx4 v[200:203], v[136:137], off
	v_mul_f32_e32 v9, 0x3fb8aa3b, v9
	v_exp_f32_e32 v137, v9
	s_waitcnt lgkmcnt(0)
	v_mfma_f32_16x16x32_bf16 v[164:167], v[184:187], v[192:195], v[164:167]
	ds_read2_b64 v[184:187], v161 offset0:64 offset1:68
	v_sub_f32_e32 v9, v148, v133
	v_mul_f32_e32 v9, 0x3fb8aa3b, v9
	s_waitcnt lgkmcnt(0)
	v_mfma_f32_16x16x32_bf16 v[168:171], v[184:187], v[192:195], v[168:171]
	ds_read2_b64 v[184:187], v162 offset0:96 offset1:100
	v_exp_f32_e32 v136, v9
	v_sub_f32_e32 v9, v138, v133
	v_mul_f32_e32 v9, 0x3fb8aa3b, v9
	v_exp_f32_e32 v139, v9
	v_sub_f32_e32 v9, v145, v133
	v_mul_f32_e32 v9, 0x3fb8aa3b, v9
	v_exp_f32_e32 v138, v9
	v_sub_f32_e32 v9, v144, v133
	v_mul_f32_e32 v9, 0x3fb8aa3b, v9
	s_waitcnt lgkmcnt(0)
	v_mfma_f32_16x16x32_bf16 v[172:175], v[184:187], v[192:195], v[172:175]
	s_waitcnt vmcnt(3)
	ds_write_b128 v75, v[188:191]
	s_waitcnt vmcnt(2)
	ds_write_b128 v75, v[196:199] offset:9216
	s_waitcnt lgkmcnt(0)
	s_barrier
	v_exp_f32_e32 v141, v9
	v_sub_f32_e32 v9, v151, v133
	ds_read2_b64 v[184:187], v8 offset1:4
	v_mul_f32_e32 v9, 0x3fb8aa3b, v9
	ds_read2_b64 v[192:195], v7 offset0:32 offset1:36
	v_exp_f32_e32 v140, v9
	v_sub_f32_e32 v9, v142, v133
	v_sub_f32_e32 v8, v147, v133
	v_mul_f32_e32 v9, 0x3fb8aa3b, v9
	v_mul_f32_e32 v8, 0x3fb8aa3b, v8
	v_exp_f32_e32 v142, v9
	v_exp_f32_e32 v143, v8
	v_cvt_pk_bf16_f32 v188, v137, v139
	v_cvt_pk_bf16_f32 v190, v136, v138
	v_cvt_pk_bf16_f32 v189, v141, v142
	v_cvt_pk_bf16_f32 v191, v140, v143
	v_lshl_add_u64 v[8:9], s[26:27], 1, v[78:79]
	v_sub_f32_e32 v145, v150, v133
	s_waitcnt lgkmcnt(1)
	v_mfma_f32_16x16x32_bf16 v[176:179], v[184:187], v[188:191], v[176:179]
	ds_read2_b64 v[184:187], v6 offset0:64 offset1:68
	v_lshl_add_u64 v[6:7], v[8:9], 0, v[70:71]
	v_lshl_add_u64 v[8:9], v[8:9], 0, v[80:81]
	s_waitcnt lgkmcnt(1)
	v_mfma_f32_16x16x32_bf16 v[164:167], v[192:195], v[188:191], v[164:167]
	global_load_dwordx4 v[192:195], v[6:7], off
	global_load_dwordx4 v[196:199], v[8:9], off
	ds_read2_b64 v[78:81], v158 offset0:96 offset1:100
	s_waitcnt vmcnt(3)
	ds_write_b128 v75, v[180:183] offset:18432
	s_waitcnt vmcnt(2)
	ds_write_b128 v75, v[200:203] offset:27648
	s_waitcnt lgkmcnt(2)
	v_mfma_f32_16x16x32_bf16 v[172:175], v[78:81], v[188:191], v[172:175]
	s_waitcnt lgkmcnt(0)
	s_barrier
; #define LAS __attribute__((address_space(3)))
; __device__ __forceinline__ unsigned cvt_pk_bf16(float lo, float hi) { const float __attribute__((ext_vector_type(2))) v = {lo, hi}; return __builtin_bit_cast(unsigned, __builtin_convertvector(v, bf16x2_t)); }
; template <bool LOCAL>
; __device__ __forceinline__ void na_unit(const bf16* P, const bf16* VT, bf16* YCAT, const LAS float* rpb_l, LAS bf16* buf, int b, int gr, int hp, int qblk, int tid) {
;     ...
;             if (LOCAL && c < 8) {
;                 float p[8];
; #pragma unroll
;                 for (int e = 0; e < 4; ++e) { p[e] = __expf(sl[2 * (c < 8 ? c : 0)][e] - m); p[4 + e] = __expf(sl[2 * (c < 8 ? c : 0) + 1][e] - m); }
; #pragma unroll
;                 for (int e = 0; e < 8; ++e) lsum += p[e];
;                 const bf16x8 pf = __builtin_bit_cast(bf16x8, (v4u){pg8::cvt_pk_bf16(p[0], p[1]), pg8::cvt_pk_bf16(p[2], p[3]), pg8::cvt_pk_bf16(p[4], p[5]), pg8::cvt_pk_bf16(p[6], p[7])});
; #pragma unroll
;                 for (int dt = 0; dt < 4; ++dt) { const LAS bf16* vp = cb + (16 * dt + fr) * 72 + kc0 + 4 * fq;
;                     o[dt] = __builtin_amdgcn_mfma_f32_16x16x32_bf16(frag44(vp, vp + 16), pf, o[dt], 0, 0, 0); }
;             } else {
;                 const int cc = c - NLOC;
; #pragma unroll
;                 for (int p2 = 0; p2 < 2; ++p2) {
;                     float p[8];
; #pragma unroll
;                     for (int e = 0; e < 4; ++e) { p[e] = __expf(sc[4 * (cc >= 0 ? cc : 0) + 2 * p2][e] - m); p[4 + e] = __expf(sc[4 * (cc >= 0 ? cc : 0) + 2 * p2 + 1][e] - m); }
; #pragma unroll
;                     for (int e = 0; e < 8; ++e) lsum += p[e];
;                     const bf16x8 pf = __builtin_bit_cast(bf16x8, (v4u){pg8::cvt_pk_bf16(p[0], p[1]), pg8::cvt_pk_bf16(p[2], p[3]), pg8::cvt_pk_bf16(p[4], p[5]), pg8::cvt_pk_bf16(p[6], p[7])});
; #pragma unroll
;                     for (int dt = 0; dt < 4; ++dt) { const LAS bf16* vp = cb + (16 * dt + fr) * 72 + 32 * p2 + 4 * fq;
;                         o[dt] = __builtin_amdgcn_mfma_f32_16x16x32_bf16(frag44(vp, vp + 16), pf, o[dt], 0, 0, 0); }
	v_sub_f32_e32 v70, v149, v133
	v_sub_f32_e32 v79, v146, v133
	v_sub_f32_e32 v81, v152, v133
	ds_read2_b64 v[148:151], v160 offset1:4
	v_mul_f32_e32 v70, 0x3fb8aa3b, v70
	v_mul_f32_e32 v79, 0x3fb8aa3b, v79
	v_mul_f32_e32 v81, 0x3fb8aa3b, v81
	v_mul_f32_e32 v145, 0x3fb8aa3b, v145
	v_exp_f32_e32 v78, v70
	v_sub_f32_e32 v70, v155, v133
	v_exp_f32_e32 v80, v79
	v_sub_f32_e32 v79, v153, v133
	v_exp_f32_e32 v144, v81
	v_sub_f32_e32 v81, v157, v133
	v_exp_f32_e32 v146, v145
	v_sub_f32_e32 v145, v154, v133
	v_mul_f32_e32 v70, 0x3fb8aa3b, v70
	v_mul_f32_e32 v79, 0x3fb8aa3b, v79
	v_mul_f32_e32 v81, 0x3fb8aa3b, v81
	v_mul_f32_e32 v145, 0x3fb8aa3b, v145
	v_exp_f32_e32 v70, v70
	v_exp_f32_e32 v79, v79
	v_exp_f32_e32 v81, v81
	v_exp_f32_e32 v145, v145
	v_cvt_pk_bf16_f32 v152, v78, v80
	v_cvt_pk_bf16_f32 v153, v144, v146
	v_cvt_pk_bf16_f32 v154, v70, v79
	v_cvt_pk_bf16_f32 v155, v81, v145
	v_mfma_f32_16x16x32_bf16 v[168:171], v[184:187], v[188:191], v[168:171]
	v_fma_f32 v63, v63, s66, -v133
	v_fma_f32 v64, v64, s66, -v133
	v_fma_f32 v65, v65, s66, -v133
	s_waitcnt lgkmcnt(0)
	v_mfma_f32_16x16x32_bf16 v[148:151], v[148:151], v[152:155], v[176:179]
	v_mul_f32_e32 v62, 0x3fb8aa3b, v62
	v_mul_f32_e32 v63, 0x3fb8aa3b, v63
	v_mul_f32_e32 v64, 0x3fb8aa3b, v64
	ds_read2_b64 v[176:179], v159 offset0:32 offset1:36
	ds_read2_b64 v[158:161], v161 offset0:64 offset1:68
	s_waitcnt lgkmcnt(0)
	v_mfma_f32_16x16x32_bf16 v[158:161], v[158:161], v[152:155], v[168:171]
	s_nop 2
	ds_read2_b64 v[168:171], v162 offset0:96 offset1:100
	v_mul_f32_e32 v65, 0x3fb8aa3b, v65
	v_exp_f32_e32 v147, v62
	v_mfma_f32_16x16x32_bf16 v[164:167], v[176:179], v[152:155], v[164:167]
	global_load_dwordx4 v[176:179], v[6:7], off offset:128
	global_load_dwordx4 v[180:183], v[8:9], off offset:128
	s_waitcnt vmcnt(3)
	ds_write_b128 v75, v[192:195]
	s_waitcnt vmcnt(2)
	ds_write_b128 v75, v[196:199] offset:9216
	s_waitcnt lgkmcnt(2)
	v_mfma_f32_16x16x32_bf16 v[152:155], v[168:171], v[152:155], v[172:175]
	s_waitcnt lgkmcnt(0)
	s_barrier
	ds_read2_b64 v[168:171], v156 offset1:4
	v_fma_f32 v62, v66, s66, -v133
	v_exp_f32_e32 v66, v63
	v_fma_f32 v63, v67, s66, -v133
	v_exp_f32_e32 v67, v64
	v_fma_f32 v64, v68, s66, -v133
	v_exp_f32_e32 v68, v65
	v_fma_f32 v65, v69, s66, -v133
	v_mul_f32_e32 v62, 0x3fb8aa3b, v62
	v_mul_f32_e32 v63, 0x3fb8aa3b, v63
	v_mul_f32_e32 v64, 0x3fb8aa3b, v64
	v_mul_f32_e32 v65, 0x3fb8aa3b, v65
	v_exp_f32_e32 v62, v62
	v_exp_f32_e32 v63, v63
	v_exp_f32_e32 v64, v64
	v_exp_f32_e32 v65, v65
	v_cvt_pk_bf16_f32 v172, v147, v66
	v_cvt_pk_bf16_f32 v173, v67, v68
	v_cvt_pk_bf16_f32 v174, v62, v63
	v_cvt_pk_bf16_f32 v175, v64, v65
	v_add_u32_e32 v157, 0x800, v156
	v_add_u32_e32 v192, 0x1000, v156
	s_waitcnt lgkmcnt(0)
	v_mfma_f32_16x16x32_bf16 v[148:151], v[168:171], v[172:175], v[148:151]
	ds_read2_b64 v[168:171], v157 offset0:32 offset1:36
	v_add_u32_e32 v193, 0x1800, v156
	v_fma_f32 v58, v58, s66, -v133
	s_waitcnt lgkmcnt(0)
	v_mfma_f32_16x16x32_bf16 v[162:165], v[168:171], v[172:175], v[164:167]
	s_nop 2
	ds_read2_b64 v[166:169], v192 offset0:64 offset1:68
	v_fma_f32 v54, v54, s66, -v133
	v_fma_f32 v59, v59, s66, -v133
	s_waitcnt lgkmcnt(0)
	v_mfma_f32_16x16x32_bf16 v[158:161], v[166:169], v[172:175], v[158:161]
	ds_read2_b64 v[166:169], v193 offset0:96 offset1:100
	v_fma_f32 v55, v55, s66, -v133
	v_fma_f32 v60, v60, s66, -v133
	s_waitcnt lgkmcnt(0)
	v_mfma_f32_16x16x32_bf16 v[152:155], v[166:169], v[172:175], v[152:155]
	ds_read2_b64 v[166:169], v156 offset0:8 offset1:12
	v_fma_f32 v56, v56, s66, -v133
	v_fma_f32 v61, v61, s66, -v133
	v_fma_f32 v57, v57, s66, -v133
	v_mul_f32_e32 v58, 0x3fb8aa3b, v58
	v_mul_f32_e32 v54, 0x3fb8aa3b, v54
	v_mul_f32_e32 v59, 0x3fb8aa3b, v59
	v_mul_f32_e32 v55, 0x3fb8aa3b, v55
	v_mul_f32_e32 v60, 0x3fb8aa3b, v60
	v_mul_f32_e32 v56, 0x3fb8aa3b, v56
	v_mul_f32_e32 v61, 0x3fb8aa3b, v61
	v_mul_f32_e32 v57, 0x3fb8aa3b, v57
	v_exp_f32_e32 v58, v58
	v_exp_f32_e32 v54, v54
	v_exp_f32_e32 v59, v59
	v_exp_f32_e32 v55, v55
	v_exp_f32_e32 v60, v60
	v_exp_f32_e32 v56, v56
	v_exp_f32_e32 v61, v61
	v_exp_f32_e32 v57, v57
	v_cvt_pk_bf16_f32 v170, v58, v59
	v_cvt_pk_bf16_f32 v172, v54, v55
	v_cvt_pk_bf16_f32 v171, v60, v61
	v_cvt_pk_bf16_f32 v173, v56, v57
	v_fma_f32 v46, v46, s66, -v133
	v_fma_f32 v47, v47, s66, -v133
	s_waitcnt lgkmcnt(0)
	v_mfma_f32_16x16x32_bf16 v[148:151], v[166:169], v[170:173], v[148:151]
	ds_read2_b64 v[166:169], v157 offset0:40 offset1:44
	v_fma_f32 v48, v48, s66, -v133
	v_mul_f32_e32 v46, 0x3fb8aa3b, v46
	s_waitcnt lgkmcnt(0)
	v_mfma_f32_16x16x32_bf16 v[162:165], v[166:169], v[170:173], v[162:165]
	ds_read2_b64 v[166:169], v192 offset0:72 offset1:76
	v_mul_f32_e32 v47, 0x3fb8aa3b, v47
	v_mul_f32_e32 v48, 0x3fb8aa3b, v48
	s_waitcnt lgkmcnt(0)
	v_mfma_f32_16x16x32_bf16 v[158:161], v[166:169], v[170:173], v[158:161]
	ds_read2_b64 v[166:169], v193 offset0:104 offset1:108
	v_exp_f32_e32 v69, v46
	v_fma_f32 v46, v50, s66, -v133
	v_exp_f32_e32 v50, v47
	v_fma_f32 v47, v51, s66, -v133
	v_exp_f32_e32 v51, v48
	v_fma_f32 v48, v52, s66, -v133
	v_add_u32_e32 v52, 0x4800, v156
	global_load_dwordx4 v[184:187], v[6:7], off offset:256
	global_load_dwordx4 v[188:191], v[8:9], off offset:256
	s_waitcnt lgkmcnt(0)
	v_mfma_f32_16x16x32_bf16 v[152:155], v[166:169], v[170:173], v[152:155]
	s_waitcnt vmcnt(3)
	ds_write_b128 v75, v[176:179] offset:18432
	s_waitcnt vmcnt(2)
	ds_write_b128 v75, v[180:183] offset:27648
	s_waitcnt lgkmcnt(0)
	s_barrier
; #define LAS __attribute__((address_space(3)))
; __device__ __forceinline__ unsigned cvt_pk_bf16(float lo, float hi) { const float __attribute__((ext_vector_type(2))) v = {lo, hi}; return __builtin_bit_cast(unsigned, __builtin_convertvector(v, bf16x2_t)); }
; template <bool LOCAL>
; __device__ __forceinline__ void na_unit(const bf16* P, const bf16* VT, bf16* YCAT, const LAS float* rpb_l, LAS bf16* buf, int b, int gr, int hp, int qblk, int tid) {
;     ...
;             } else {
;                 const int cc = c - NLOC;
; #pragma unroll
;                 for (int p2 = 0; p2 < 2; ++p2) {
;                     float p[8];
; #pragma unroll
;                     for (int e = 0; e < 4; ++e) { p[e] = __expf(sc[4 * (cc >= 0 ? cc : 0) + 2 * p2][e] - m); p[4 + e] = __expf(sc[4 * (cc >= 0 ? cc : 0) + 2 * p2 + 1][e] - m); }
; #pragma unroll
;                     for (int e = 0; e < 8; ++e) lsum += p[e];
;                     const bf16x8 pf = __builtin_bit_cast(bf16x8, (v4u){pg8::cvt_pk_bf16(p[0], p[1]), pg8::cvt_pk_bf16(p[2], p[3]), pg8::cvt_pk_bf16(p[4], p[5]), pg8::cvt_pk_bf16(p[6], p[7])});
; #pragma unroll
;                     for (int dt = 0; dt < 4; ++dt) { const LAS bf16* vp = cb + (16 * dt + fr) * 72 + 32 * p2 + 4 * fq;
;                         o[dt] = __builtin_amdgcn_mfma_f32_16x16x32_bf16(frag44(vp, vp + 16), pf, o[dt], 0, 0, 0); }
	v_fma_f32 v49, v49, s66, -v133
	ds_read2_b64 v[166:169], v52 offset1:4
	v_mul_f32_e32 v49, 0x3fb8aa3b, v49
	v_exp_f32_e32 v174, v49
	v_fma_f32 v49, v53, s66, -v133
	v_mul_f32_e32 v46, 0x3fb8aa3b, v46
	v_mul_f32_e32 v47, 0x3fb8aa3b, v47
	v_mul_f32_e32 v48, 0x3fb8aa3b, v48
	v_mul_f32_e32 v49, 0x3fb8aa3b, v49
	v_exp_f32_e32 v46, v46
	v_exp_f32_e32 v47, v47
	v_exp_f32_e32 v48, v48
	v_exp_f32_e32 v53, v49
	v_cvt_pk_bf16_f32 v170, v69, v50
	v_cvt_pk_bf16_f32 v171, v51, v174
	v_cvt_pk_bf16_f32 v172, v46, v47
	v_cvt_pk_bf16_f32 v173, v48, v53
	v_add_u32_e32 v175, 0x5000, v156
	v_add_u32_e32 v176, 0x5800, v156
	s_waitcnt lgkmcnt(0)
	v_mfma_f32_16x16x32_bf16 v[148:151], v[166:169], v[170:173], v[148:151]
	ds_read2_b64 v[166:169], v175 offset0:32 offset1:36
	v_add_u32_e32 v49, 0x6000, v156
	v_fma_f32 v38, v38, s66, -v133
	s_waitcnt lgkmcnt(0)
	v_mfma_f32_16x16x32_bf16 v[162:165], v[166:169], v[170:173], v[162:165]
	ds_read2_b64 v[166:169], v176 offset0:64 offset1:68
	v_mul_f32_e32 v38, 0x3fb8aa3b, v38
	v_fma_f32 v42, v42, s66, -v133
	s_waitcnt lgkmcnt(0)
	v_mfma_f32_16x16x32_bf16 v[158:161], v[166:169], v[170:173], v[158:161]
	ds_read2_b64 v[166:169], v49 offset0:96 offset1:100
	v_mul_f32_e32 v42, 0x3fb8aa3b, v42
	v_fma_f32 v30, v30, s66, -v133
	s_waitcnt lgkmcnt(0)
	v_mfma_f32_16x16x32_bf16 v[152:155], v[166:169], v[170:173], v[152:155]
	v_exp_f32_e32 v171, v38
	v_fma_f32 v38, v43, s66, -v133
	v_mul_f32_e32 v38, 0x3fb8aa3b, v38
	v_exp_f32_e32 v172, v38
	v_fma_f32 v38, v39, s66, -v133
	v_mul_f32_e32 v38, 0x3fb8aa3b, v38
	v_exp_f32_e32 v173, v38
	v_fma_f32 v38, v44, s66, -v133
	v_mul_f32_e32 v38, 0x3fb8aa3b, v38
	v_exp_f32_e32 v177, v38
	v_fma_f32 v38, v40, s66, -v133
	v_mul_f32_e32 v38, 0x3fb8aa3b, v38
	v_exp_f32_e32 v170, v42
	v_exp_f32_e32 v178, v38
	v_fma_f32 v38, v45, s66, -v133
	ds_read2_b64 v[42:45], v52 offset0:8 offset1:12
	v_mul_f32_e32 v38, 0x3fb8aa3b, v38
	v_exp_f32_e32 v179, v38
	v_fma_f32 v38, v41, s66, -v133
	v_mul_f32_e32 v38, 0x3fb8aa3b, v38
	v_exp_f32_e32 v180, v38
	v_cvt_pk_bf16_f32 v38, v170, v172
	v_cvt_pk_bf16_f32 v39, v177, v179
	v_cvt_pk_bf16_f32 v40, v171, v173
	v_cvt_pk_bf16_f32 v41, v178, v180
	v_mul_f32_e32 v30, 0x3fb8aa3b, v30
	v_fma_f32 v22, v22, s66, -v133
	s_waitcnt lgkmcnt(0)
	v_mfma_f32_16x16x32_bf16 v[42:45], v[42:45], v[38:41], v[148:151]
	v_mul_f32_e32 v22, 0x3fb8aa3b, v22
	v_fma_f32 v26, v26, s66, -v133
	v_mul_f32_e32 v26, 0x3fb8aa3b, v26
	ds_read2_b64 v[148:151], v175 offset0:40 offset1:44
	s_waitcnt lgkmcnt(0)
	v_mfma_f32_16x16x32_bf16 v[148:151], v[148:151], v[38:41], v[162:165]
	s_nop 2
	ds_read2_b64 v[162:165], v176 offset0:72 offset1:76
	v_fma_f32 v2, v2, s66, -v133
	v_mul_f32_e32 v2, 0x3fb8aa3b, v2
	s_waitcnt lgkmcnt(0)
	v_mfma_f32_16x16x32_bf16 v[158:161], v[162:165], v[38:41], v[158:161]
	ds_read2_b64 v[162:165], v49 offset0:104 offset1:108
	global_load_dwordx4 v[166:169], v[6:7], off offset:384
	s_nop 0
	global_load_dwordx4 v[6:9], v[8:9], off offset:384
	s_waitcnt vmcnt(3)
	ds_write_b128 v75, v[184:187]
	s_waitcnt vmcnt(2)
	ds_write_b128 v75, v[188:191] offset:9216
	s_waitcnt lgkmcnt(2)
	v_mfma_f32_16x16x32_bf16 v[38:41], v[162:165], v[38:41], v[152:155]
	v_exp_f32_e32 v162, v30
	v_fma_f32 v30, v34, s66, -v133
	v_mul_f32_e32 v30, 0x3fb8aa3b, v30
	v_exp_f32_e32 v163, v30
	v_fma_f32 v30, v31, s66, -v133
	v_mul_f32_e32 v30, 0x3fb8aa3b, v30
	v_exp_f32_e32 v164, v30
	v_fma_f32 v30, v35, s66, -v133
	v_mul_f32_e32 v30, 0x3fb8aa3b, v30
	v_exp_f32_e32 v165, v30
	v_fma_f32 v30, v32, s66, -v133
	v_mul_f32_e32 v30, 0x3fb8aa3b, v30
	v_exp_f32_e32 v181, v30
	v_fma_f32 v30, v36, s66, -v133
	v_mul_f32_e32 v30, 0x3fb8aa3b, v30
	v_exp_f32_e32 v182, v30
	v_fma_f32 v30, v33, s66, -v133
	s_waitcnt lgkmcnt(0)
	s_barrier
	v_mul_f32_e32 v34, 0x3fb8aa3b, v30
	ds_read2_b64 v[30:33], v156 offset1:4
	v_exp_f32_e32 v183, v34
	v_fma_f32 v34, v37, s66, -v133
	v_mul_f32_e32 v34, 0x3fb8aa3b, v34
	v_exp_f32_e32 v184, v34
	v_cvt_pk_bf16_f32 v34, v162, v164
	v_cvt_pk_bf16_f32 v35, v181, v183
	v_cvt_pk_bf16_f32 v36, v163, v165
	v_cvt_pk_bf16_f32 v37, v182, v184
	ds_read2_b64 v[152:155], v193 offset0:96 offset1:100
	v_fma_f32 v10, v10, s66, -v133
	s_waitcnt lgkmcnt(1)
	v_mfma_f32_16x16x32_bf16 v[30:33], v[30:33], v[34:37], v[42:45]
	v_mul_f32_e32 v10, 0x3fb8aa3b, v10
	s_nop 1
	ds_read2_b64 v[42:45], v157 offset0:32 offset1:36
	s_waitcnt lgkmcnt(0)
	v_mfma_f32_16x16x32_bf16 v[42:45], v[42:45], v[34:37], v[148:151]
	s_nop 2
	ds_read2_b64 v[148:151], v192 offset0:64 offset1:68
	s_waitcnt lgkmcnt(0)
	v_mfma_f32_16x16x32_bf16 v[148:151], v[148:151], v[34:37], v[158:161]
	v_mfma_f32_16x16x32_bf16 v[34:37], v[152:155], v[34:37], v[38:41]
	v_exp_f32_e32 v153, v22
	v_fma_f32 v22, v27, s66, -v133
	v_mul_f32_e32 v22, 0x3fb8aa3b, v22
	v_exp_f32_e32 v154, v22
	v_fma_f32 v22, v23, s66, -v133
	v_mul_f32_e32 v22, 0x3fb8aa3b, v22
	v_exp_f32_e32 v155, v22
	v_fma_f32 v22, v28, s66, -v133
	v_mul_f32_e32 v22, 0x3fb8aa3b, v22
	v_exp_f32_e32 v158, v22
	v_fma_f32 v22, v24, s66, -v133
	v_mul_f32_e32 v22, 0x3fb8aa3b, v22
	v_exp_f32_e32 v152, v26
	v_exp_f32_e32 v159, v22
	v_fma_f32 v22, v29, s66, -v133
	ds_read2_b64 v[26:29], v156 offset0:8 offset1:12
	v_mul_f32_e32 v22, 0x3fb8aa3b, v22
	v_exp_f32_e32 v156, v22
	v_fma_f32 v22, v25, s66, -v133
	v_mul_f32_e32 v22, 0x3fb8aa3b, v22
	v_exp_f32_e32 v160, v22
	v_cvt_pk_bf16_f32 v22, v152, v154
	v_cvt_pk_bf16_f32 v23, v158, v156
	v_cvt_pk_bf16_f32 v24, v153, v155
	v_cvt_pk_bf16_f32 v25, v159, v160
	ds_read2_b64 v[38:41], v192 offset0:72 offset1:76
	s_waitcnt lgkmcnt(1)
	v_mfma_f32_16x16x32_bf16 v[26:29], v[26:29], v[22:25], v[30:33]
	s_nop 2
	ds_read2_b64 v[30:33], v157 offset0:40 offset1:44
	s_waitcnt lgkmcnt(0)
	v_mfma_f32_16x16x32_bf16 v[30:33], v[30:33], v[22:25], v[42:45]
	s_nop 2
	ds_read2_b64 v[42:45], v193 offset0:104 offset1:108
	s_waitcnt vmcnt(1)
	ds_write_b128 v75, v[166:169] offset:18432
	s_waitcnt vmcnt(0)
	ds_write_b128 v75, v[6:9] offset:27648
	v_fma_f32 v6, v14, s66, -v133
	v_mul_f32_e32 v6, 0x3fb8aa3b, v6
	v_mfma_f32_16x16x32_bf16 v[38:41], v[38:41], v[22:25], v[148:151]
	s_waitcnt lgkmcnt(0)
	s_barrier
; #define LAS __attribute__((address_space(3)))
; __device__ __forceinline__ unsigned cvt_pk_bf16(float lo, float hi) { const float __attribute__((ext_vector_type(2))) v = {lo, hi}; return __builtin_bit_cast(unsigned, __builtin_convertvector(v, bf16x2_t)); }
; #define NA_STORE(sidx) do { LAS bf16* d_ = buf + ((sidx) & 1) * 9216; _Pragma("unroll") for (int q_ = 0; q_ < 2; ++q_) *(LAS v4u*)(d_ + q_ * 4608 + lrow * 72 + lseg * 8) = ld[(sidx) & 1][q_]; } while (0)
; template <bool LOCAL>
; __device__ __forceinline__ void na_unit(const bf16* P, const bf16* VT, bf16* YCAT, const LAS float* rpb_l, LAS bf16* buf, int b, int gr, int hp, int qblk, int tid) {
;     ...
;             } else {
;                 const int cc = c - NLOC;
; #pragma unroll
;                 for (int p2 = 0; p2 < 2; ++p2) {
;                     float p[8];
; #pragma unroll
;                     for (int e = 0; e < 4; ++e) { p[e] = __expf(sc[4 * (cc >= 0 ? cc : 0) + 2 * p2][e] - m); p[4 + e] = __expf(sc[4 * (cc >= 0 ? cc : 0) + 2 * p2 + 1][e] - m); }
; #pragma unroll
;                     for (int e = 0; e < 8; ++e) lsum += p[e];
;                     const bf16x8 pf = __builtin_bit_cast(bf16x8, (v4u){pg8::cvt_pk_bf16(p[0], p[1]), pg8::cvt_pk_bf16(p[2], p[3]), pg8::cvt_pk_bf16(p[4], p[5]), pg8::cvt_pk_bf16(p[6], p[7])});
; #pragma unroll
;                     for (int dt = 0; dt < 4; ++dt) { const LAS bf16* vp = cb + (16 * dt + fr) * 72 + 32 * p2 + 4 * fq;
;                         o[dt] = __builtin_amdgcn_mfma_f32_16x16x32_bf16(frag44(vp, vp + 16), pf, o[dt], 0, 0, 0); }
;                 }
;             }
;         }
;         if (sidx + 1 < 2 * NCH) NA_STORE(sidx + 1);
;         __syncthreads();
;     }
;     ...
;     lsum += __shfl_xor(lsum, 16); lsum += __shfl_xor(lsum, 32);
	v_mfma_f32_16x16x32_bf16 v[22:25], v[42:45], v[22:25], v[34:37]
	v_ashrrev_i32_e32 v75, 31, v74
	s_nop 1
	v_exp_f32_e32 v34, v6
	v_fma_f32 v6, v18, s66, -v133
	v_mul_f32_e32 v6, 0x3fb8aa3b, v6
	v_exp_f32_e32 v35, v6
	v_fma_f32 v6, v15, s66, -v133
	v_mul_f32_e32 v6, 0x3fb8aa3b, v6
	v_exp_f32_e32 v36, v6
	v_fma_f32 v6, v19, s66, -v133
	v_mul_f32_e32 v6, 0x3fb8aa3b, v6
	v_exp_f32_e32 v37, v6
	v_fma_f32 v6, v16, s66, -v133
	v_mul_f32_e32 v6, 0x3fb8aa3b, v6
	v_exp_f32_e32 v42, v6
	v_fma_f32 v6, v20, s66, -v133
	v_mul_f32_e32 v6, 0x3fb8aa3b, v6
	v_exp_f32_e32 v43, v6
	v_fma_f32 v6, v17, s66, -v133
	v_mul_f32_e32 v14, 0x3fb8aa3b, v6
	ds_read2_b64 v[6:9], v52 offset1:4
	v_exp_f32_e32 v44, v14
	v_fma_f32 v14, v21, s66, -v133
	v_mul_f32_e32 v14, 0x3fb8aa3b, v14
	v_exp_f32_e32 v45, v14
	v_cvt_pk_bf16_f32 v14, v34, v36
	v_cvt_pk_bf16_f32 v15, v42, v44
	v_cvt_pk_bf16_f32 v16, v35, v37
	v_cvt_pk_bf16_f32 v17, v43, v45
	ds_read2_b64 v[18:21], v175 offset0:32 offset1:36
	s_waitcnt lgkmcnt(1)
	v_mfma_f32_16x16x32_bf16 v[6:9], v[6:9], v[14:17], v[26:29]
	s_nop 2
	ds_read2_b64 v[26:29], v176 offset0:64 offset1:68
	s_waitcnt lgkmcnt(0)
	v_mfma_f32_16x16x32_bf16 v[26:29], v[26:29], v[14:17], v[38:41]
	s_nop 2
	v_add_f32_e32 v38, 0, v127
	v_add_f32_e32 v38, v96, v38
	v_add_f32_e32 v38, v95, v38
	v_add_f32_e32 v38, v100, v38
	v_add_f32_e32 v38, v92, v38
	v_add_f32_e32 v38, v91, v38
	v_add_f32_e32 v38, v94, v38
	v_add_f32_e32 v38, v93, v38
	v_add_f32_e32 v38, v86, v38
	v_add_f32_e32 v38, v90, v38
	v_add_f32_e32 v38, v98, v38
	v_add_f32_e32 v38, v99, v38
	v_add_f32_e32 v38, v76, v38
	v_add_f32_e32 v38, v87, v38
	v_add_f32_e32 v38, v97, v38
	v_add_f32_e32 v38, v101, v38
	v_add_f32_e32 v38, v104, v38
	v_add_f32_e32 v38, v105, v38
	v_add_f32_e32 v38, v108, v38
	v_add_f32_e32 v38, v107, v38
	v_add_f32_e32 v38, v102, v38
	v_add_f32_e32 v38, v103, v38
	v_add_f32_e32 v38, v106, v38
	v_add_f32_e32 v38, v109, v38
	v_add_f32_e32 v38, v111, v38
	v_add_f32_e32 v38, v113, v38
	v_add_f32_e32 v38, v115, v38
	v_add_f32_e32 v38, v116, v38
	v_add_f32_e32 v38, v110, v38
	v_add_f32_e32 v38, v112, v38
	v_add_f32_e32 v38, v114, v38
	v_add_f32_e32 v38, v117, v38
	v_add_f32_e32 v38, v119, v38
	v_add_f32_e32 v38, v121, v38
	v_add_f32_e32 v38, v123, v38
	v_add_f32_e32 v38, v124, v38
	v_add_f32_e32 v38, v118, v38
	v_add_f32_e32 v38, v120, v38
	v_add_f32_e32 v38, v122, v38
	v_add_f32_e32 v38, v125, v38
	v_add_f32_e32 v38, v128, v38
	v_add_f32_e32 v38, v130, v38
	v_add_f32_e32 v38, v132, v38
	v_add_f32_e32 v38, v134, v38
	v_add_f32_e32 v38, v126, v38
	v_add_f32_e32 v38, v129, v38
	v_add_f32_e32 v38, v131, v38
	v_add_f32_e32 v38, v135, v38
	v_add_f32_e32 v38, v137, v38
	v_add_f32_e32 v38, v139, v38
	v_add_f32_e32 v38, v141, v38
	v_add_f32_e32 v38, v142, v38
	v_add_f32_e32 v38, v136, v38
	v_add_f32_e32 v38, v138, v38
	v_add_f32_e32 v38, v140, v38
	v_add_f32_e32 v38, v143, v38
	v_add_f32_e32 v38, v78, v38
	v_add_f32_e32 v38, v80, v38
	v_add_f32_e32 v38, v144, v38
	v_add_f32_e32 v38, v146, v38
	v_add_f32_e32 v38, v70, v38
	v_add_f32_e32 v38, v79, v38
	v_add_f32_e32 v38, v81, v38
	v_add_f32_e32 v38, v145, v38
	v_add_f32_e32 v38, v147, v38
	v_add_f32_e32 v38, v66, v38
	v_add_f32_e32 v38, v67, v38
	v_add_f32_e32 v38, v68, v38
	v_add_f32_e32 v38, v62, v38
	v_add_f32_e32 v38, v63, v38
	v_add_f32_e32 v38, v64, v38
	v_add_f32_e32 v38, v65, v38
	v_add_f32_e32 v38, v58, v38
	v_add_f32_e32 v38, v59, v38
	v_add_f32_e32 v38, v60, v38
	v_add_f32_e32 v38, v61, v38
	v_add_f32_e32 v38, v54, v38
	v_add_f32_e32 v38, v55, v38
	v_add_f32_e32 v38, v56, v38
	v_add_f32_e32 v38, v57, v38
	v_add_f32_e32 v38, v69, v38
	v_add_f32_e32 v38, v50, v38
	v_add_f32_e32 v38, v51, v38
	v_add_f32_e32 v38, v174, v38
	v_add_f32_e32 v38, v46, v38
	v_add_f32_e32 v38, v47, v38
	v_add_f32_e32 v38, v48, v38
	v_add_f32_e32 v38, v53, v38
	v_add_f32_e32 v38, v170, v38
	v_mfma_f32_16x16x32_bf16 v[18:21], v[18:21], v[14:17], v[30:33]
	v_add_f32_e32 v38, v172, v38
	v_add_f32_e32 v38, v177, v38
	v_add_f32_e32 v38, v179, v38
	ds_read2_b64 v[30:33], v49 offset0:96 offset1:100
	v_add_f32_e32 v38, v171, v38
	v_add_f32_e32 v38, v173, v38
	v_add_f32_e32 v38, v178, v38
	v_add_f32_e32 v38, v180, v38
	v_add_f32_e32 v38, v162, v38
	v_add_f32_e32 v38, v164, v38
	s_waitcnt lgkmcnt(0)
	v_mfma_f32_16x16x32_bf16 v[14:17], v[30:33], v[14:17], v[22:25]
	v_add_f32_e32 v38, v181, v38
	s_nop 1
	v_exp_f32_e32 v23, v2
	v_fma_f32 v2, v11, s66, -v133
	v_mul_f32_e32 v2, 0x3fb8aa3b, v2
	v_add_f32_e32 v38, v183, v38
	v_exp_f32_e32 v24, v2
	v_fma_f32 v2, v3, s66, -v133
	v_add_f32_e32 v38, v163, v38
	v_mul_f32_e32 v2, 0x3fb8aa3b, v2
	v_add_f32_e32 v38, v165, v38
	v_exp_f32_e32 v25, v2
	v_fma_f32 v2, v12, s66, -v133
	v_add_f32_e32 v38, v182, v38
	v_mul_f32_e32 v2, 0x3fb8aa3b, v2
	v_add_f32_e32 v38, v184, v38
	v_exp_f32_e32 v30, v2
	v_fma_f32 v2, v4, s66, -v133
	v_add_f32_e32 v38, v152, v38
	v_mul_f32_e32 v2, 0x3fb8aa3b, v2
	v_add_f32_e32 v38, v154, v38
	v_exp_f32_e32 v22, v10
	v_exp_f32_e32 v31, v2
	v_fma_f32 v2, v13, s66, -v133
	ds_read2_b64 v[10:13], v52 offset0:8 offset1:12
	v_add_f32_e32 v38, v158, v38
	v_mul_f32_e32 v2, 0x3fb8aa3b, v2
	v_add_f32_e32 v38, v156, v38
	v_exp_f32_e32 v32, v2
	v_fma_f32 v2, v5, s66, -v133
	v_add_f32_e32 v38, v153, v38
	v_mul_f32_e32 v2, 0x3fb8aa3b, v2
	v_add_f32_e32 v38, v155, v38
	v_exp_f32_e32 v33, v2
	v_add_f32_e32 v38, v159, v38
	v_add_f32_e32 v38, v160, v38
	v_add_f32_e32 v34, v34, v38
	v_add_f32_e32 v34, v36, v34
	v_cvt_pk_bf16_f32 v2, v22, v24
	v_cvt_pk_bf16_f32 v3, v30, v32
	v_cvt_pk_bf16_f32 v4, v23, v25
	v_cvt_pk_bf16_f32 v5, v31, v33
	v_add_f32_e32 v34, v42, v34
	v_add_f32_e32 v34, v44, v34
	s_waitcnt lgkmcnt(0)
	v_mfma_f32_16x16x32_bf16 v[6:9], v[10:13], v[2:5], v[6:9]
	ds_read2_b64 v[10:13], v175 offset0:40 offset1:44
	v_add_f32_e32 v34, v35, v34
	v_add_f32_e32 v34, v37, v34
	v_add_f32_e32 v34, v43, v34
	v_add_f32_e32 v34, v45, v34
	v_add_f32_e32 v22, v22, v34
	v_add_f32_e32 v22, v24, v22
	v_add_f32_e32 v22, v30, v22
	v_add_f32_e32 v22, v32, v22
	s_waitcnt lgkmcnt(0)
	v_mfma_f32_16x16x32_bf16 v[10:13], v[10:13], v[2:5], v[18:21]
	v_add_f32_e32 v22, v23, v22
	v_add_f32_e32 v22, v25, v22
	v_add_f32_e32 v22, v31, v22
	ds_read2_b64 v[18:21], v176 offset0:72 offset1:76
	v_add_f32_e32 v30, v33, v22
	ds_bpermute_b32 v31, v88, v30
	ds_read2_b64 v[22:25], v49 offset0:104 offset1:108
	s_waitcnt lgkmcnt(2)
	v_mfma_f32_16x16x32_bf16 v[18:21], v[18:21], v[2:5], v[26:29]
	s_waitcnt lgkmcnt(1)
	s_nop 1
	v_add_f32_e32 v26, v30, v31
	ds_bpermute_b32 v27, v89, v26
	v_lshlrev_b32_e32 v70, 1, v77
	s_waitcnt lgkmcnt(1)
	v_mfma_f32_16x16x32_bf16 v[14:17], v[22:25], v[2:5], v[14:17]
	s_waitcnt lgkmcnt(0)
	s_barrier
; __device__ __forceinline__ unsigned cvt_pk_bf16(float lo, float hi) { const float __attribute__((ext_vector_type(2))) v = {lo, hi}; return __builtin_bit_cast(unsigned, __builtin_convertvector(v, bf16x2_t)); }
; template <bool LOCAL>
; __device__ __forceinline__ void na_unit(const bf16* P, const bf16* VT, bf16* YCAT, const LAS float* rpb_l, LAS bf16* buf, int b, int gr, int hp, int qblk, int tid) {
;     ...
;     lsum += __shfl_xor(lsum, 16); lsum += __shfl_xor(lsum, 32);
;     const float inv = 1.f / lsum;
;     bf16* op = YCAT + (size_t)(qrow0 + fr) * D + 512 + h * 64 + 4 * fq;
; #pragma unroll
;     for (int dt = 0; dt < 4; ++dt) { v2u w; w.x = pg8::cvt_pk_bf16(o[dt][0] * inv, o[dt][1] * inv); w.y = pg8::cvt_pk_bf16(o[dt][2] * inv, o[dt][3] * inv); *(v2u*)(op + dt * 16) = w; }
	v_add_f32_e32 v2, v26, v27
	v_div_scale_f32 v3, s[0:1], v2, v2, 1.0
	v_rcp_f32_e32 v4, v3
	s_nop 0
	v_fma_f32 v5, -v3, v4, 1.0
	v_fmac_f32_e32 v4, v5, v4
	v_div_scale_f32 v5, vcc, 1.0, v2, 1.0
	v_mul_f32_e32 v22, v5, v4
	v_fma_f32 v23, -v3, v22, v5
	v_fmac_f32_e32 v22, v23, v4
	v_fma_f32 v3, -v3, v22, v5
	v_div_fmas_f32 v3, v3, v4, v22
	v_div_fixup_f32 v22, v3, v2, 1.0
	v_lshlrev_b64 v[2:3], 11, v[74:75]
	v_lshl_add_u64 v[2:3], s[10:11], 0, v[2:3]
	v_lshl_add_u64 v[2:3], v[72:73], 1, v[2:3]
	v_pk_mul_f32 v[6:7], v[6:7], v[22:23] op_sel_hi:[1,0]
	v_pk_mul_f32 v[8:9], v[8:9], v[22:23] op_sel_hi:[1,0]
	v_lshl_add_u64 v[4:5], v[2:3], 0, v[70:71]
	v_cvt_pk_bf16_f32 v6, v6, v7
	v_cvt_pk_bf16_f32 v7, v8, v9
	global_store_dwordx2 v[4:5], v[6:7], off offset:1024
	v_pk_mul_f32 v[6:7], v[10:11], v[22:23] op_sel_hi:[1,0]
	v_pk_mul_f32 v[8:9], v[12:13], v[22:23] op_sel_hi:[1,0]
	v_cvt_pk_bf16_f32 v6, v6, v7
	v_cvt_pk_bf16_f32 v7, v8, v9
	global_store_dwordx2 v[4:5], v[6:7], off offset:1056
	v_pk_mul_f32 v[6:7], v[18:19], v[22:23] op_sel_hi:[1,0]
	v_pk_mul_f32 v[8:9], v[20:21], v[22:23] op_sel_hi:[1,0]
	v_cvt_pk_bf16_f32 v6, v6, v7
	v_cvt_pk_bf16_f32 v7, v8, v9
	v_lshl_add_u64 v[2:3], v[4:5], 0, s[12:13]
	global_store_dwordx2 v[4:5], v[6:7], off offset:1088
	v_pk_mul_f32 v[4:5], v[14:15], v[22:23] op_sel_hi:[1,0]
	v_pk_mul_f32 v[6:7], v[16:17], v[22:23] op_sel_hi:[1,0]
	v_cvt_pk_bf16_f32 v4, v4, v5

; #define LAS __attribute__((address_space(3)))
; template <bool LOCAL>
; __device__ __forceinline__ void na_unit(const bf16* P, const bf16* VT, bf16* YCAT, const LAS float* rpb_l, LAS bf16* buf, int b, int gr, int hp, int qblk, int tid) {
;     ...
;     const int lane = tid & 63, wv = tid >> 6, fr = lane & 15, fq = lane >> 4, hh = wv >> 2, qb = wv & 3, h = 2 * hp + hh;
;     const int qrow0 = LOCAL ? NCTX + b * SEQ + gr * 64 + 16 * qb : b * CTXL + qblk * 64 + 16 * qb;
;     const int r0 = min(max(gr - 4, 0), 24);
;     const int kc0 = qb == 0 ? 0 : qb == 1 ? 8 : qb == 2 ? 24 : 32;
;     const int qcol = 16 * qb + fr, cs = min(max(qcol - 8, 0), 48);
;     const LAS float* rpb = rpb_l + h * 15 * 31;
;     v4u ld[2][2];
;     const int lrow = (tid >> 3) & 63, lseg = tid & 7;
;     ...
;     bf16x8 qf[2];
; #pragma unroll
;     for (int ks = 0; ks < 2; ++ks) qf[ks] = *(const bf16x8*)(P + (size_t)(qrow0 + fr) * DINP + h * 64 + 32 * ks + 8 * fq);
;     f32x4 sl[16], sc[16];
;     float m = -1.0e30f, lsum = 0.f;
;     f32x4 o[4];
; #pragma unroll
;     for (int dt = 0; dt < 4; ++dt) o[dt] = (f32x4){0.f, 0.f, 0.f, 0.f};
;     NA_ISSUE(0); NA_ISSUE(1); NA_STORE(0);
;     __syncthreads();
; #pragma unroll
;     for (int sidx = 0; sidx < 2 * NCH; ++sidx) {
;         if (sidx + 2 < 2 * NCH) NA_ISSUE(sidx + 2);
;         const LAS bf16* cb = buf + (sidx & 1) * 9216 + hh * 4608;
;         if (sidx < NCH) {
;             const int c = sidx;
;             if (LOCAL && c < 8) {
; #pragma unroll
;                 for (int t2 = 0; t2 < 2; ++t2) {
;                     const LAS bf16* kp = cb + (kc0 + 16 * t2 + fr) * 72 + 8 * fq;
;                     f32x4 acc = {0.f, 0.f, 0.f, 0.f};
;                     acc = __builtin_amdgcn_mfma_f32_16x16x32_bf16(*(const LAS bf16x8*)(kp), qf[0], acc, 0, 0, 0);
;                     acc = __builtin_amdgcn_mfma_f32_16x16x32_bf16(*(const LAS bf16x8*)(kp + 32), qf[1], acc, 0, 0, 0);
;                     const LAS float* rb = rpb + (r0 + c - gr + 7) * 31 + 15 - qcol;
; #pragma unroll
;                     for (int e = 0; e < 4; ++e) { const int kcol = kc0 + 16 * t2 + 4 * fq + e; const bool ok = (kcol >= cs) && (kcol < cs + 16);
;                         const float sv = ok ? acc[e] * 0.125f + rb[ok ? kcol : qcol] : -1.0e30f; acc[e] = sv; m = fmaxf(m, sv); }
;                     sl[2 * (c < 8 ? c : 0) + t2] = acc; }
.LBB0_4001:
	s_or_b64 exec, exec, s[0:1]
	s_bfe_u32 s19, s69, 0x50002
	v_sub_u32_e64 v3, s19, 4 clamp
	s_ashr_i32 s17, s69, 7
	v_readfirstlane_b32 s0, v3
	s_lshl_b32 s26, s17, 11
	s_min_u32 s20, s0, 24
	s_add_i32 s14, s26, 0x1000
	s_lshl_b32 s15, s20, 6
	s_or_b32 s16, s15, s14
	v_mov_b64_e32 v[18:19], s[8:9]
	v_and_b32_e32 v32, 7, v92
	v_or_b32_e32 v3, s16, v87
	s_and_b32 s18, s69, 3
	v_mad_i64_i32 v[4:5], s[0:1], v3, s57, v[18:19]
	v_lshlrev_b32_e32 v26, 4, v32
	v_mov_b32_e32 v27, v71
	v_lshl_add_u64 v[4:5], v[4:5], 0, v[26:27]
	s_lshl_b32 s2, s18, 8
	v_lshl_add_u64 v[4:5], v[4:5], 0, s[2:3]
	global_load_dwordx4 v[10:13], v[4:5], off offset:1024
	global_load_dwordx4 v[14:17], v[4:5], off offset:1152
	s_lshl_b32 s0, s19, 6
	v_lshl_or_b32 v31, v2, 4, v88
	v_lshl_add_u32 v34, s18, 1, v91
	s_or_b32 s0, s14, s0
	v_mad_u32_u24 v2, v87, s64, 0
	v_lshlrev_b32_e32 v72, 6, v34
	s_add_i32 s50, s26, 0x1040
	v_or_b32_e32 v74, s0, v31
	v_add_u32_e32 v75, v2, v26
	v_ashrrev_i32_e32 v73, 31, v72
	v_or_b32_e32 v4, s50, v87
	v_mad_i64_i32 v[2:3], s[0:1], v74, s57, v[18:19]
	v_add_u32_e32 v4, s15, v4
	v_lshl_add_u64 v[2:3], v[72:73], 1, v[2:3]
	v_mad_i64_i32 v[4:5], s[0:1], v4, s57, v[18:19]
	v_lshl_add_u64 v[2:3], v[2:3], 0, v[70:71]
	v_lshl_add_u64 v[20:21], v[4:5], 0, v[26:27]
	global_load_dwordx4 v[6:9], v[2:3], off
	s_nop 0
	global_load_dwordx4 v[2:5], v[2:3], off offset:64
	s_or_b32 s14, s26, s15
	s_addk_i32 s14, 0x1080
	v_or_b32_e32 v24, s14, v87
	v_mad_i64_i32 v[28:29], s[0:1], v24, s57, v[18:19]
	v_lshl_add_u64 v[26:27], v[28:29], 0, v[26:27]
	v_lshl_add_u64 v[22:23], v[20:21], 0, s[2:3]
	v_lshl_add_u64 v[26:27], v[26:27], 0, s[2:3]
	global_load_dwordx4 v[18:21], v[22:23], off offset:1024
	s_nop 0
	global_load_dwordx4 v[22:25], v[22:23], off offset:1152
	v_add_u32_e32 v30, v85, v70
	v_add_u32_e32 v33, v89, v88
	v_mad_u32_u24 v36, v33, s64, v30
	s_sub_i32 s0, s20, s19
	s_mulk_i32 s0, 0x7c
	v_sub_u32_e64 v35, v31, 8 clamp
	v_mul_lo_u32 v34, v34, s68
	s_add_i32 s0, s0, 0
	v_min_u32_e32 v35, 48, v35
	v_lshlrev_b32_e32 v77, 2, v90
	v_add_u32_e32 v34, s0, v34
	v_lshlrev_b32_e32 v31, 2, v31
	v_sub_u32_e32 v31, v34, v31
	v_add_u32_e32 v34, v89, v77
	v_cmp_ge_u32_e32 vcc, v34, v35
	v_mov_b32_e32 v90, 0xf149f2ca
	v_lshl_add_u32 v31, v34, 2, v31
	v_mov_b32_e32 v91, 0xf149f2ca
	s_waitcnt vmcnt(5)
	ds_write_b128 v75, v[10:13]
	s_waitcnt vmcnt(4)
	ds_write_b128 v75, v[14:17] offset:9216
	s_waitcnt lgkmcnt(0)
	s_barrier
	ds_read_b32 v240, v31 offset:37792
	ds_read_b32 v241, v31 offset:37796
	ds_read_b32 v242, v31 offset:37800
	ds_read_b32 v243, v31 offset:37804
	ds_read_b32 v244, v31 offset:37856
	ds_read_b32 v245, v31 offset:37860
	ds_read_b32 v246, v31 offset:37864
	ds_read_b32 v247, v31 offset:37868
	global_load_dwordx4 v[10:13], v[26:27], off offset:1024
	global_load_dwordx4 v[14:17], v[26:27], off offset:1152
	ds_read_b128 v[26:29], v36
	ds_read_b128 v[38:41], v36 offset:64
	s_waitcnt vmcnt(5) lgkmcnt(1)
	v_mfma_f32_16x16x32_bf16 v[26:29], v[26:29], v[6:9], 0
	v_add_u32_e32 v36, 16, v35
	v_cmp_lt_u32_e64 s[0:1], v34, v36
	s_and_b64 s[28:29], vcc, s[0:1]
	s_waitcnt vmcnt(4) lgkmcnt(0)
	v_mfma_f32_16x16x32_bf16 v[26:29], v[38:41], v[2:5], v[26:29]
	s_nop 2
	s_waitcnt lgkmcnt(0)
	s_nop 3
	v_fmac_f32_e32 v240, 0x3e000000, v26
	v_cndmask_b32_e64 v91, v91, v240, s[28:29]
	s_nop 4
	v_or_b32_e32 v26, 1, v34
	v_cmp_ge_u32_e32 vcc, v26, v35
	v_cmp_lt_u32_e64 s[0:1], v26, v36
	s_and_b64 s[30:31], vcc, s[0:1]
	s_nop 2
	s_waitcnt lgkmcnt(0)
	v_fmac_f32_e32 v241, 0x3e000000, v27
	v_cndmask_b32_e64 v90, v90, v241, s[30:31]
	v_or_b32_e32 v26, 2, v34
	v_cmp_ge_u32_e32 vcc, v26, v35
	v_cmp_lt_u32_e64 s[0:1], v26, v36
	s_and_b64 s[34:35], vcc, s[0:1]
	v_mov_b32_e32 v92, 0xf149f2ca
	v_mov_b32_e32 v93, 0xf149f2ca
	s_nop 2
	s_waitcnt lgkmcnt(0)
	v_fmac_f32_e32 v242, 0x3e000000, v28
	v_cndmask_b32_e64 v93, v93, v242, s[34:35]
	v_or_b32_e32 v26, 3, v34
	v_cmp_ge_u32_e32 vcc, v26, v35
	v_cmp_lt_u32_e64 s[0:1], v26, v36
	s_and_b64 s[36:37], vcc, s[0:1]
	s_nop 2
	s_waitcnt lgkmcnt(0)
	v_fmac_f32_e32 v243, 0x3e000000, v29
	v_cndmask_b32_e64 v92, v92, v243, s[36:37]
	v_add_u32_e32 v37, 16, v89
	v_add_u32_e32 v34, v37, v88
	v_mad_u32_u24 v38, v34, s64, v30
	ds_read_b128 v[26:29], v38
	ds_read_b128 v[38:41], v38 offset:64
	v_add_u32_e32 v37, v37, v77
	v_cmp_ge_u32_e32 vcc, v37, v35
	v_cmp_lt_u32_e64 s[0:1], v37, v36
	s_waitcnt lgkmcnt(1)
	v_mfma_f32_16x16x32_bf16 v[26:29], v[26:29], v[6:9], 0
	s_and_b64 s[38:39], vcc, s[0:1]
	v_mov_b32_e32 v94, 0xf149f2ca
	v_mov_b32_e32 v95, 0xf149f2ca
	s_waitcnt lgkmcnt(0)
	v_mfma_f32_16x16x32_bf16 v[26:29], v[38:41], v[2:5], v[26:29]
	s_nop 2
	s_waitcnt lgkmcnt(0)
	s_nop 3
	v_fmac_f32_e32 v244, 0x3e000000, v26
	v_cndmask_b32_e64 v95, v95, v244, s[38:39]
	s_nop 4
	v_or_b32_e32 v26, 1, v37
	v_cmp_ge_u32_e32 vcc, v26, v35
	v_cmp_lt_u32_e64 s[0:1], v26, v36
	s_and_b64 s[44:45], vcc, s[0:1]
	s_nop 2
	s_waitcnt lgkmcnt(0)
	v_fmac_f32_e32 v245, 0x3e000000, v27
	v_cndmask_b32_e64 v94, v94, v245, s[44:45]
	v_or_b32_e32 v26, 2, v37
	v_cmp_ge_u32_e32 vcc, v26, v35
	v_cmp_lt_u32_e64 s[0:1], v26, v36
	s_and_b64 s[46:47], vcc, s[0:1]
	v_mov_b32_e32 v98, 0xf149f2ca
	v_mov_b32_e32 v99, 0xf149f2ca
	s_nop 2
	s_waitcnt lgkmcnt(0)
	v_fmac_f32_e32 v246, 0x3e000000, v28
	v_cndmask_b32_e64 v99, v99, v246, s[46:47]
	v_or_b32_e32 v26, 3, v37
	v_cmp_ge_u32_e32 vcc, v26, v35
	v_cmp_lt_u32_e64 s[0:1], v26, v36
	s_and_b64 s[48:49], vcc, s[0:1]
	s_nop 2
	s_waitcnt lgkmcnt(0)
	v_fmac_f32_e32 v247, 0x3e000000, v29
	v_cndmask_b32_e64 v98, v98, v247, s[48:49]
	v_mul_u32_u24_e32 v27, 0x90, v33
	v_lshlrev_b32_e32 v26, 3, v32
	v_add_u32_e32 v32, v30, v27
	s_waitcnt vmcnt(3)
	ds_write_b128 v75, v[18:21] offset:18432
	s_waitcnt vmcnt(2)
	ds_write_b128 v75, v[22:25] offset:27648
	s_waitcnt lgkmcnt(0)
	s_barrier
; #define LAS __attribute__((address_space(3)))
; template <bool LOCAL>
; __device__ __forceinline__ void na_unit(const bf16* P, const bf16* VT, bf16* YCAT, const LAS float* rpb_l, LAS bf16* buf, int b, int gr, int hp, int qblk, int tid) {
;     ...
;     for (int sidx = 0; sidx < 2 * NCH; ++sidx) {
;         if (sidx + 2 < 2 * NCH) NA_ISSUE(sidx + 2);
;         const LAS bf16* cb = buf + (sidx & 1) * 9216 + hh * 4608;
;         if (sidx < NCH) {
;             const int c = sidx;
;             if (LOCAL && c < 8) {
; #pragma unroll
;                 for (int t2 = 0; t2 < 2; ++t2) {
;                     const LAS bf16* kp = cb + (kc0 + 16 * t2 + fr) * 72 + 8 * fq;
;                     f32x4 acc = {0.f, 0.f, 0.f, 0.f};
;                     acc = __builtin_amdgcn_mfma_f32_16x16x32_bf16(*(const LAS bf16x8*)(kp), qf[0], acc, 0, 0, 0);
;                     acc = __builtin_amdgcn_mfma_f32_16x16x32_bf16(*(const LAS bf16x8*)(kp + 32), qf[1], acc, 0, 0, 0);
;                     const LAS float* rb = rpb + (r0 + c - gr + 7) * 31 + 15 - qcol;
; #pragma unroll
;                     for (int e = 0; e < 4; ++e) { const int kcol = kc0 + 16 * t2 + 4 * fq + e; const bool ok = (kcol >= cs) && (kcol < cs + 16);
;                         const float sv = ok ? acc[e] * 0.125f + rb[ok ? kcol : qcol] : -1.0e30f; acc[e] = sv; m = fmaxf(m, sv); }
;                     sl[2 * (c < 8 ? c : 0) + t2] = acc; }
	ds_read_b32 v240, v31 offset:37916
	ds_read_b32 v241, v31 offset:37920
	ds_read_b32 v242, v31 offset:37924
	ds_read_b32 v243, v31 offset:37928
	ds_read_b32 v244, v31 offset:37980
	ds_read_b32 v245, v31 offset:37984
	ds_read_b32 v246, v31 offset:37988
	ds_read_b32 v247, v31 offset:37992
	ds_read_b128 v[18:21], v32 offset:18432
	s_add_i32 s26, s26, s15
	s_add_i32 s0, s26, 0x10c0
	v_or_b32_e32 v24, s0, v87
	v_mov_b64_e32 v[22:23], s[8:9]
	s_lshl_b32 s1, s18, 7
	v_mad_i64_i32 v[22:23], s[18:19], v24, s57, v[22:23]
	v_lshlrev_b32_e32 v70, 1, v26
	v_lshl_add_u64 v[22:23], v[22:23], 0, v[70:71]
	s_lshl_b32 s2, s1, 1
	v_lshl_add_u64 v[22:23], v[22:23], 0, s[2:3]
	ds_read_b128 v[26:29], v32 offset:18496
	s_waitcnt lgkmcnt(1)
	v_mfma_f32_16x16x32_bf16 v[36:39], v[18:21], v[6:9], 0
	global_load_dwordx4 v[18:21], v[22:23], off offset:1024
	s_nop 0
	global_load_dwordx4 v[22:25], v[22:23], off offset:1152
	v_mov_b32_e32 v96, 0xf149f2ca
	v_mov_b32_e32 v97, 0xf149f2ca
	s_waitcnt lgkmcnt(0)
	v_mfma_f32_16x16x32_bf16 v[26:29], v[26:29], v[2:5], v[36:39]
	s_nop 2
	s_waitcnt lgkmcnt(0)
	s_nop 3
	v_fmac_f32_e32 v240, 0x3e000000, v26
	v_cndmask_b32_e64 v97, v97, v240, s[28:29]
	s_nop 2
	s_waitcnt lgkmcnt(0)
	s_nop 0
	v_fmac_f32_e32 v241, 0x3e000000, v27
	v_cndmask_b32_e64 v96, v96, v241, s[30:31]
	v_mov_b32_e32 v100, 0xf149f2ca
	v_mov_b32_e32 v101, 0xf149f2ca
	s_nop 2
	s_waitcnt lgkmcnt(0)
	v_fmac_f32_e32 v242, 0x3e000000, v28
	v_cndmask_b32_e64 v101, v101, v242, s[34:35]
	s_nop 2
	s_waitcnt lgkmcnt(0)
	v_fmac_f32_e32 v243, 0x3e000000, v29
	v_cndmask_b32_e64 v100, v100, v243, s[36:37]
	v_mul_u32_u24_e32 v26, 0x90, v34
	v_add_u32_e32 v33, v30, v26
	ds_read_b128 v[26:29], v33 offset:18432
	ds_read_b128 v[34:37], v33 offset:18496
	v_mov_b32_e32 v103, 0xf149f2ca
	v_mov_b32_e32 v105, 0xf149f2ca
	s_waitcnt lgkmcnt(1)
	v_mfma_f32_16x16x32_bf16 v[26:29], v[26:29], v[6:9], 0
	s_waitcnt lgkmcnt(0)
	v_mfma_f32_16x16x32_bf16 v[26:29], v[34:37], v[2:5], v[26:29]
	s_nop 2
	s_waitcnt lgkmcnt(0)
	s_nop 3
	v_fmac_f32_e32 v244, 0x3e000000, v26
	v_cndmask_b32_e64 v105, v105, v244, s[38:39]
	s_nop 2
	s_waitcnt lgkmcnt(0)
	s_nop 0
	v_fmac_f32_e32 v245, 0x3e000000, v27
	v_cndmask_b32_e64 v103, v103, v245, s[44:45]
	v_mov_b32_e32 v107, 0xf149f2ca
	v_mov_b32_e32 v109, 0xf149f2ca
	s_nop 2
	s_waitcnt lgkmcnt(0)
	v_fmac_f32_e32 v246, 0x3e000000, v28
	v_cndmask_b32_e64 v109, v109, v246, s[46:47]
	s_nop 2
	s_waitcnt lgkmcnt(0)
	v_fmac_f32_e32 v247, 0x3e000000, v29
	v_cndmask_b32_e64 v107, v107, v247, s[48:49]
	s_waitcnt vmcnt(3)
	ds_write_b128 v75, v[10:13]
	s_waitcnt vmcnt(2)
	ds_write_b128 v75, v[14:17] offset:9216
	s_waitcnt lgkmcnt(0)
	s_barrier
	ds_read_b32 v240, v31 offset:38040
	ds_read_b32 v241, v31 offset:38044
	ds_read_b32 v242, v31 offset:38048
	ds_read_b32 v243, v31 offset:38052
	ds_read_b32 v244, v31 offset:38104
	ds_read_b32 v245, v31 offset:38108
	ds_read_b32 v246, v31 offset:38112
	ds_read_b32 v247, v31 offset:38116
	ds_read_b128 v[10:13], v32
	ds_read_b128 v[26:29], v32 offset:64
	s_add_i32 s18, s26, 0x1100
	v_or_b32_e32 v16, s18, v87
	v_mov_b64_e32 v[14:15], s[8:9]
	v_mad_i64_i32 v[14:15], s[20:21], v16, s57, v[14:15]
	v_lshl_add_u64 v[14:15], v[14:15], 0, v[70:71]
	v_lshl_add_u64 v[14:15], v[14:15], 0, s[2:3]
	s_waitcnt lgkmcnt(1)
	v_mfma_f32_16x16x32_bf16 v[34:37], v[10:13], v[6:9], 0
	global_load_dwordx4 v[10:13], v[14:15], off offset:1024
	s_nop 0
	global_load_dwordx4 v[14:17], v[14:15], off offset:1152
	v_mov_b32_e32 v102, 0xf149f2ca
	v_mov_b32_e32 v104, 0xf149f2ca
	s_waitcnt lgkmcnt(0)
	v_mfma_f32_16x16x32_bf16 v[26:29], v[26:29], v[2:5], v[34:37]
	s_nop 2
	s_waitcnt lgkmcnt(0)
	s_nop 3
	v_fmac_f32_e32 v240, 0x3e000000, v26
	v_cndmask_b32_e64 v104, v104, v240, s[28:29]
	s_nop 2
	s_waitcnt lgkmcnt(0)
	s_nop 0
	v_fmac_f32_e32 v241, 0x3e000000, v27
	v_cndmask_b32_e64 v102, v102, v241, s[30:31]
	v_mov_b32_e32 v106, 0xf149f2ca
	v_mov_b32_e32 v108, 0xf149f2ca
	s_nop 2
	s_waitcnt lgkmcnt(0)
	v_fmac_f32_e32 v242, 0x3e000000, v28
	v_cndmask_b32_e64 v108, v108, v242, s[34:35]
	s_nop 2
	s_waitcnt lgkmcnt(0)
	v_fmac_f32_e32 v243, 0x3e000000, v29
	v_cndmask_b32_e64 v106, v106, v243, s[36:37]
	ds_read_b128 v[26:29], v33
	ds_read_b128 v[34:37], v33 offset:64
	v_mov_b32_e32 v110, 0xf149f2ca
	v_mov_b32_e32 v113, 0xf149f2ca
	s_waitcnt lgkmcnt(1)
	v_mfma_f32_16x16x32_bf16 v[26:29], v[26:29], v[6:9], 0
	s_waitcnt lgkmcnt(0)
	v_mfma_f32_16x16x32_bf16 v[26:29], v[34:37], v[2:5], v[26:29]
	s_nop 2
	s_waitcnt lgkmcnt(0)
	s_nop 3
	v_fmac_f32_e32 v244, 0x3e000000, v26
	v_cndmask_b32_e64 v113, v113, v244, s[38:39]
	s_nop 2
	s_waitcnt lgkmcnt(0)
	s_nop 0
	v_fmac_f32_e32 v245, 0x3e000000, v27
	v_cndmask_b32_e64 v110, v110, v245, s[44:45]
	v_mov_b32_e32 v112, 0xf149f2ca
	v_mov_b32_e32 v116, 0xf149f2ca
	s_nop 2
	s_waitcnt lgkmcnt(0)
	v_fmac_f32_e32 v246, 0x3e000000, v28
	v_cndmask_b32_e64 v116, v116, v246, s[46:47]
	s_nop 2
	s_waitcnt lgkmcnt(0)
	v_fmac_f32_e32 v247, 0x3e000000, v29
	v_cndmask_b32_e64 v112, v112, v247, s[48:49]
	s_waitcnt vmcnt(3)
	ds_write_b128 v75, v[18:21] offset:18432
	s_waitcnt vmcnt(2)
	ds_write_b128 v75, v[22:25] offset:27648
	s_waitcnt lgkmcnt(0)
	s_barrier
; #define LAS __attribute__((address_space(3)))
; template <bool LOCAL>
; __device__ __forceinline__ void na_unit(const bf16* P, const bf16* VT, bf16* YCAT, const LAS float* rpb_l, LAS bf16* buf, int b, int gr, int hp, int qblk, int tid) {
;     ...
;     for (int sidx = 0; sidx < 2 * NCH; ++sidx) {
;         if (sidx + 2 < 2 * NCH) NA_ISSUE(sidx + 2);
;         const LAS bf16* cb = buf + (sidx & 1) * 9216 + hh * 4608;
;         if (sidx < NCH) {
;             const int c = sidx;
;             if (LOCAL && c < 8) {
; #pragma unroll
;                 for (int t2 = 0; t2 < 2; ++t2) {
;                     const LAS bf16* kp = cb + (kc0 + 16 * t2 + fr) * 72 + 8 * fq;
;                     f32x4 acc = {0.f, 0.f, 0.f, 0.f};
;                     acc = __builtin_amdgcn_mfma_f32_16x16x32_bf16(*(const LAS bf16x8*)(kp), qf[0], acc, 0, 0, 0);
;                     acc = __builtin_amdgcn_mfma_f32_16x16x32_bf16(*(const LAS bf16x8*)(kp + 32), qf[1], acc, 0, 0, 0);
;                     const LAS float* rb = rpb + (r0 + c - gr + 7) * 31 + 15 - qcol;
; #pragma unroll
;                     for (int e = 0; e < 4; ++e) { const int kcol = kc0 + 16 * t2 + 4 * fq + e; const bool ok = (kcol >= cs) && (kcol < cs + 16);
;                         const float sv = ok ? acc[e] * 0.125f + rb[ok ? kcol : qcol] : -1.0e30f; acc[e] = sv; m = fmaxf(m, sv); }
;                     sl[2 * (c < 8 ? c : 0) + t2] = acc; }
	ds_read_b32 v240, v31 offset:38164
	ds_read_b32 v241, v31 offset:38168
	ds_read_b32 v242, v31 offset:38172
	ds_read_b32 v243, v31 offset:38176
	ds_read_b32 v244, v31 offset:38228
	ds_read_b32 v245, v31 offset:38232
	ds_read_b32 v246, v31 offset:38236
	ds_read_b32 v247, v31 offset:38240
	ds_read_b128 v[18:21], v32 offset:18432
	ds_read_b128 v[26:29], v32 offset:18496
	s_add_i32 s20, s26, 0x1140
	v_or_b32_e32 v24, s20, v87
	v_mov_b64_e32 v[22:23], s[8:9]
	v_mad_i64_i32 v[22:23], s[22:23], v24, s57, v[22:23]
	v_lshl_add_u64 v[22:23], v[22:23], 0, v[70:71]
	v_lshl_add_u64 v[22:23], v[22:23], 0, s[2:3]
	s_waitcnt lgkmcnt(1)
	v_mfma_f32_16x16x32_bf16 v[34:37], v[18:21], v[6:9], 0
	global_load_dwordx4 v[18:21], v[22:23], off offset:1024
	s_nop 0
	global_load_dwordx4 v[22:25], v[22:23], off offset:1152
	v_mov_b32_e32 v111, 0xf149f2ca
	v_mov_b32_e32 v114, 0xf149f2ca
	s_waitcnt lgkmcnt(0)
	v_mfma_f32_16x16x32_bf16 v[26:29], v[26:29], v[2:5], v[34:37]
	s_nop 2
	s_waitcnt lgkmcnt(0)
	s_nop 3
	v_fmac_f32_e32 v240, 0x3e000000, v26
	v_cndmask_b32_e64 v114, v114, v240, s[28:29]
	s_nop 2
	s_waitcnt lgkmcnt(0)
	s_nop 0
	v_fmac_f32_e32 v241, 0x3e000000, v27
	v_cndmask_b32_e64 v111, v111, v241, s[30:31]
	v_mov_b32_e32 v115, 0xf149f2ca
	v_mov_b32_e32 v117, 0xf149f2ca
	s_nop 2
	s_waitcnt lgkmcnt(0)
	v_fmac_f32_e32 v242, 0x3e000000, v28
	v_cndmask_b32_e64 v117, v117, v242, s[34:35]
	s_nop 2
	s_waitcnt lgkmcnt(0)
	v_fmac_f32_e32 v243, 0x3e000000, v29
	v_cndmask_b32_e64 v115, v115, v243, s[36:37]
	ds_read_b128 v[26:29], v33 offset:18432
	ds_read_b128 v[34:37], v33 offset:18496
	v_mov_b32_e32 v118, 0xf149f2ca
	v_mov_b32_e32 v121, 0xf149f2ca
	s_waitcnt lgkmcnt(1)
	v_mfma_f32_16x16x32_bf16 v[26:29], v[26:29], v[6:9], 0
	s_waitcnt lgkmcnt(0)
	v_mfma_f32_16x16x32_bf16 v[26:29], v[34:37], v[2:5], v[26:29]
	s_nop 2
	s_waitcnt lgkmcnt(0)
	s_nop 3
	v_fmac_f32_e32 v244, 0x3e000000, v26
	v_cndmask_b32_e64 v121, v121, v244, s[38:39]
	s_nop 2
	s_waitcnt lgkmcnt(0)
	s_nop 0
	v_fmac_f32_e32 v245, 0x3e000000, v27
	v_cndmask_b32_e64 v118, v118, v245, s[44:45]
	v_mov_b32_e32 v120, 0xf149f2ca
	v_mov_b32_e32 v124, 0xf149f2ca
	s_nop 2
	s_waitcnt lgkmcnt(0)
	v_fmac_f32_e32 v246, 0x3e000000, v28
	v_cndmask_b32_e64 v124, v124, v246, s[46:47]
	s_nop 2
	s_waitcnt lgkmcnt(0)
	v_fmac_f32_e32 v247, 0x3e000000, v29
	v_cndmask_b32_e64 v120, v120, v247, s[48:49]
	s_waitcnt vmcnt(3)
	ds_write_b128 v75, v[10:13]
	s_waitcnt vmcnt(2)
	ds_write_b128 v75, v[14:17] offset:9216
	s_waitcnt lgkmcnt(0)
	s_barrier
	ds_read_b32 v240, v31 offset:38288
	ds_read_b32 v241, v31 offset:38292
	ds_read_b32 v242, v31 offset:38296
	ds_read_b32 v243, v31 offset:38300
	ds_read_b32 v244, v31 offset:38352
	ds_read_b32 v245, v31 offset:38356
	ds_read_b32 v246, v31 offset:38360
	ds_read_b32 v247, v31 offset:38364
	ds_read_b128 v[10:13], v32
	ds_read_b128 v[26:29], v32 offset:64
	s_add_i32 s22, s26, 0x1180
	v_or_b32_e32 v16, s22, v87
	v_mov_b64_e32 v[14:15], s[8:9]
	v_mad_i64_i32 v[14:15], s[24:25], v16, s57, v[14:15]
	v_lshl_add_u64 v[14:15], v[14:15], 0, v[70:71]
	v_lshl_add_u64 v[14:15], v[14:15], 0, s[2:3]
	s_waitcnt lgkmcnt(1)
	v_mfma_f32_16x16x32_bf16 v[34:37], v[10:13], v[6:9], 0
	global_load_dwordx4 v[10:13], v[14:15], off offset:1024
	s_nop 0
	global_load_dwordx4 v[14:17], v[14:15], off offset:1152
	v_mov_b32_e32 v119, 0xf149f2ca
	v_mov_b32_e32 v122, 0xf149f2ca
	s_waitcnt lgkmcnt(0)
	v_mfma_f32_16x16x32_bf16 v[26:29], v[26:29], v[2:5], v[34:37]
	s_nop 2
	s_waitcnt lgkmcnt(0)
	s_nop 3
	v_fmac_f32_e32 v240, 0x3e000000, v26
	v_cndmask_b32_e64 v122, v122, v240, s[28:29]
	s_nop 2
	s_waitcnt lgkmcnt(0)
	s_nop 0
	v_fmac_f32_e32 v241, 0x3e000000, v27
	v_cndmask_b32_e64 v119, v119, v241, s[30:31]
	v_mov_b32_e32 v123, 0xf149f2ca
	v_mov_b32_e32 v125, 0xf149f2ca
	s_nop 2
	s_waitcnt lgkmcnt(0)
	v_fmac_f32_e32 v242, 0x3e000000, v28
	v_cndmask_b32_e64 v125, v125, v242, s[34:35]
	s_nop 2
	s_waitcnt lgkmcnt(0)
	v_fmac_f32_e32 v243, 0x3e000000, v29
	v_cndmask_b32_e64 v123, v123, v243, s[36:37]
	ds_read_b128 v[26:29], v33
	ds_read_b128 v[34:37], v33 offset:64
	v_mov_b32_e32 v127, 0xf149f2ca
	v_mov_b32_e32 v130, 0xf149f2ca
	s_waitcnt lgkmcnt(1)
	v_mfma_f32_16x16x32_bf16 v[26:29], v[26:29], v[6:9], 0
	s_waitcnt lgkmcnt(0)
	v_mfma_f32_16x16x32_bf16 v[26:29], v[34:37], v[2:5], v[26:29]
	s_nop 2
	s_waitcnt lgkmcnt(0)
	s_nop 3
	v_fmac_f32_e32 v244, 0x3e000000, v26
	v_cndmask_b32_e64 v130, v130, v244, s[38:39]
	s_nop 2
	s_waitcnt lgkmcnt(0)
	s_nop 0
	v_fmac_f32_e32 v245, 0x3e000000, v27
	v_cndmask_b32_e64 v127, v127, v245, s[44:45]
	v_mov_b32_e32 v129, 0xf149f2ca
	v_mov_b32_e32 v134, 0xf149f2ca
	s_nop 2
	s_waitcnt lgkmcnt(0)
	v_fmac_f32_e32 v246, 0x3e000000, v28
	v_cndmask_b32_e64 v134, v134, v246, s[46:47]
	s_nop 2
	s_waitcnt lgkmcnt(0)
	v_fmac_f32_e32 v247, 0x3e000000, v29
	v_cndmask_b32_e64 v129, v129, v247, s[48:49]
	s_waitcnt vmcnt(3)
	ds_write_b128 v75, v[18:21] offset:18432
	s_waitcnt vmcnt(2)
	ds_write_b128 v75, v[22:25] offset:27648
	s_waitcnt lgkmcnt(0)
	s_barrier
; #define LAS __attribute__((address_space(3)))
; template <bool LOCAL>
; __device__ __forceinline__ void na_unit(const bf16* P, const bf16* VT, bf16* YCAT, const LAS float* rpb_l, LAS bf16* buf, int b, int gr, int hp, int qblk, int tid) {
;     ...
;     for (int sidx = 0; sidx < 2 * NCH; ++sidx) {
;         if (sidx + 2 < 2 * NCH) NA_ISSUE(sidx + 2);
;         const LAS bf16* cb = buf + (sidx & 1) * 9216 + hh * 4608;
;         if (sidx < NCH) {
;             const int c = sidx;
;             if (LOCAL && c < 8) {
; #pragma unroll
;                 for (int t2 = 0; t2 < 2; ++t2) {
;                     const LAS bf16* kp = cb + (kc0 + 16 * t2 + fr) * 72 + 8 * fq;
;                     f32x4 acc = {0.f, 0.f, 0.f, 0.f};
;                     acc = __builtin_amdgcn_mfma_f32_16x16x32_bf16(*(const LAS bf16x8*)(kp), qf[0], acc, 0, 0, 0);
;                     acc = __builtin_amdgcn_mfma_f32_16x16x32_bf16(*(const LAS bf16x8*)(kp + 32), qf[1], acc, 0, 0, 0);
;                     const LAS float* rb = rpb + (r0 + c - gr + 7) * 31 + 15 - qcol;
; #pragma unroll
;                     for (int e = 0; e < 4; ++e) { const int kcol = kc0 + 16 * t2 + 4 * fq + e; const bool ok = (kcol >= cs) && (kcol < cs + 16);
;                         const float sv = ok ? acc[e] * 0.125f + rb[ok ? kcol : qcol] : -1.0e30f; acc[e] = sv; m = fmaxf(m, sv); }
;                     sl[2 * (c < 8 ? c : 0) + t2] = acc; }
	ds_read_b32 v240, v31 offset:38412
	ds_read_b32 v241, v31 offset:38416
	ds_read_b32 v242, v31 offset:38420
	ds_read_b32 v243, v31 offset:38424
	ds_read_b32 v244, v31 offset:38476
	ds_read_b32 v245, v31 offset:38480
	ds_read_b32 v246, v31 offset:38484
	ds_read_b32 v247, v31 offset:38488
	ds_read_b128 v[18:21], v32 offset:18432
	ds_read_b128 v[26:29], v32 offset:18496
	s_add_i32 s24, s26, 0x11c0
	v_or_b32_e32 v24, s24, v87
	v_mov_b64_e32 v[22:23], s[8:9]
	v_mad_i64_i32 v[22:23], s[26:27], v24, s57, v[22:23]
	v_lshl_add_u64 v[22:23], v[22:23], 0, v[70:71]
	v_lshl_add_u64 v[22:23], v[22:23], 0, s[2:3]
	s_waitcnt lgkmcnt(1)
	v_mfma_f32_16x16x32_bf16 v[34:37], v[18:21], v[6:9], 0
	global_load_dwordx4 v[18:21], v[22:23], off offset:1024
	s_nop 0
	global_load_dwordx4 v[22:25], v[22:23], off offset:1152
	v_mov_b32_e32 v128, 0xf149f2ca
	v_mov_b32_e32 v131, 0xf149f2ca
	s_waitcnt lgkmcnt(0)
	v_mfma_f32_16x16x32_bf16 v[26:29], v[26:29], v[2:5], v[34:37]
	s_nop 2
	s_waitcnt lgkmcnt(0)
	s_nop 3
	v_fmac_f32_e32 v240, 0x3e000000, v26
	v_cndmask_b32_e64 v131, v131, v240, s[28:29]
	s_nop 2
	s_waitcnt lgkmcnt(0)
	s_nop 0
	v_fmac_f32_e32 v241, 0x3e000000, v27
	v_cndmask_b32_e64 v128, v128, v241, s[30:31]
	v_mov_b32_e32 v133, 0xf149f2ca
	v_mov_b32_e32 v135, 0xf149f2ca
	s_nop 2
	s_waitcnt lgkmcnt(0)
	v_fmac_f32_e32 v242, 0x3e000000, v28
	v_cndmask_b32_e64 v135, v135, v242, s[34:35]
	s_nop 2
	s_waitcnt lgkmcnt(0)
	v_fmac_f32_e32 v243, 0x3e000000, v29
	v_cndmask_b32_e64 v133, v133, v243, s[36:37]
	ds_read_b128 v[26:29], v33 offset:18432
	ds_read_b128 v[34:37], v33 offset:18496
	v_mov_b32_e32 v136, 0xf149f2ca
	v_mov_b32_e32 v139, 0xf149f2ca
	s_waitcnt lgkmcnt(1)
	v_mfma_f32_16x16x32_bf16 v[26:29], v[26:29], v[6:9], 0
	s_waitcnt lgkmcnt(0)
	v_mfma_f32_16x16x32_bf16 v[26:29], v[34:37], v[2:5], v[26:29]
	s_nop 2
	s_waitcnt lgkmcnt(0)
	s_nop 3
	v_fmac_f32_e32 v244, 0x3e000000, v26
	v_cndmask_b32_e64 v139, v139, v244, s[38:39]
	s_nop 2
	s_waitcnt lgkmcnt(0)
	s_nop 0
	v_fmac_f32_e32 v245, 0x3e000000, v27
	v_cndmask_b32_e64 v136, v136, v245, s[44:45]
	v_mov_b32_e32 v138, 0xf149f2ca
	v_mov_b32_e32 v142, 0xf149f2ca
	s_nop 2
	s_waitcnt lgkmcnt(0)
	v_fmac_f32_e32 v246, 0x3e000000, v28
	v_cndmask_b32_e64 v142, v142, v246, s[46:47]
	s_nop 2
	s_waitcnt lgkmcnt(0)
	v_fmac_f32_e32 v247, 0x3e000000, v29
	v_cndmask_b32_e64 v138, v138, v247, s[48:49]
	s_waitcnt vmcnt(3)
	ds_write_b128 v75, v[10:13]
	s_waitcnt vmcnt(2)
	ds_write_b128 v75, v[14:17] offset:9216
	s_waitcnt lgkmcnt(0)
	s_barrier
	ds_read_b32 v240, v31 offset:38536
	ds_read_b32 v241, v31 offset:38540
	ds_read_b32 v242, v31 offset:38544
	ds_read_b32 v243, v31 offset:38548
	ds_read_b32 v244, v31 offset:38600
	ds_read_b32 v245, v31 offset:38604
	ds_read_b32 v246, v31 offset:38608
	ds_read_b32 v247, v31 offset:38612
	ds_read_b128 v[10:13], v32
	ds_read_b128 v[26:29], v32 offset:64
	s_lshl_b32 s26, s17, 8
	v_or_b32_e32 v34, s26, v87
	v_mov_b64_e32 v[14:15], s[8:9]
	v_mad_i64_i32 v[14:15], s[52:53], v34, s57, v[14:15]
	v_lshl_add_u64 v[14:15], v[14:15], 0, v[70:71]
	v_lshl_add_u64 v[14:15], v[14:15], 0, s[2:3]
	s_waitcnt lgkmcnt(1)
	v_mfma_f32_16x16x32_bf16 v[36:39], v[10:13], v[6:9], 0
	global_load_dwordx4 v[10:13], v[14:15], off offset:1024
	s_nop 0
	global_load_dwordx4 v[14:17], v[14:15], off offset:1152
	v_mov_b32_e32 v137, 0xf149f2ca
	v_mov_b32_e32 v140, 0xf149f2ca
	s_waitcnt lgkmcnt(0)
	v_mfma_f32_16x16x32_bf16 v[26:29], v[26:29], v[2:5], v[36:39]
	s_nop 2
	s_waitcnt lgkmcnt(0)
	s_nop 3
	v_fmac_f32_e32 v240, 0x3e000000, v26
	v_cndmask_b32_e64 v140, v140, v240, s[28:29]
	s_nop 2
	s_waitcnt lgkmcnt(0)
	s_nop 0
	v_fmac_f32_e32 v241, 0x3e000000, v27
	v_cndmask_b32_e64 v137, v137, v241, s[30:31]
	v_mov_b32_e32 v141, 0xf149f2ca
	v_mov_b32_e32 v143, 0xf149f2ca
	s_nop 2
	s_waitcnt lgkmcnt(0)
	v_fmac_f32_e32 v242, 0x3e000000, v28
	v_cndmask_b32_e64 v143, v143, v242, s[34:35]
	s_nop 2
	s_waitcnt lgkmcnt(0)
	v_fmac_f32_e32 v243, 0x3e000000, v29
	v_cndmask_b32_e64 v141, v141, v243, s[36:37]
	ds_read_b128 v[26:29], v33
	ds_read_b128 v[36:39], v33 offset:64
	v_mov_b32_e32 v144, 0xf149f2ca
	v_mov_b32_e32 v147, 0xf149f2ca
	s_waitcnt lgkmcnt(1)
	v_mfma_f32_16x16x32_bf16 v[26:29], v[26:29], v[6:9], 0
	s_waitcnt lgkmcnt(0)
	v_mfma_f32_16x16x32_bf16 v[26:29], v[36:39], v[2:5], v[26:29]
	s_nop 2
	s_waitcnt lgkmcnt(0)
	s_nop 3
	v_fmac_f32_e32 v244, 0x3e000000, v26
	v_cndmask_b32_e64 v147, v147, v244, s[38:39]
	s_nop 2
	s_waitcnt lgkmcnt(0)
	s_nop 0
	v_fmac_f32_e32 v245, 0x3e000000, v27
	v_cndmask_b32_e64 v144, v144, v245, s[44:45]
	v_mov_b32_e32 v146, 0xf149f2ca
	v_mov_b32_e32 v150, 0xf149f2ca
	s_nop 2
	s_waitcnt lgkmcnt(0)
	v_fmac_f32_e32 v246, 0x3e000000, v28
	v_cndmask_b32_e64 v150, v150, v246, s[46:47]
	s_nop 2
	s_waitcnt lgkmcnt(0)
	v_fmac_f32_e32 v247, 0x3e000000, v29
	v_cndmask_b32_e64 v146, v146, v247, s[48:49]
	s_waitcnt vmcnt(3)
	ds_write_b128 v75, v[18:21] offset:18432
	s_waitcnt vmcnt(2)
	ds_write_b128 v75, v[22:25] offset:27648
	s_waitcnt lgkmcnt(0)
	s_barrier
; #define LAS __attribute__((address_space(3)))
; template <bool LOCAL>
; __device__ __forceinline__ void na_unit(const bf16* P, const bf16* VT, bf16* YCAT, const LAS float* rpb_l, LAS bf16* buf, int b, int gr, int hp, int qblk, int tid) {
;     ...
;     for (int sidx = 0; sidx < 2 * NCH; ++sidx) {
;         if (sidx + 2 < 2 * NCH) NA_ISSUE(sidx + 2);
;         const LAS bf16* cb = buf + (sidx & 1) * 9216 + hh * 4608;
;         if (sidx < NCH) {
;             const int c = sidx;
;             if (LOCAL && c < 8) {
; #pragma unroll
;                 for (int t2 = 0; t2 < 2; ++t2) {
;                     const LAS bf16* kp = cb + (kc0 + 16 * t2 + fr) * 72 + 8 * fq;
;                     f32x4 acc = {0.f, 0.f, 0.f, 0.f};
;                     acc = __builtin_amdgcn_mfma_f32_16x16x32_bf16(*(const LAS bf16x8*)(kp), qf[0], acc, 0, 0, 0);
;                     acc = __builtin_amdgcn_mfma_f32_16x16x32_bf16(*(const LAS bf16x8*)(kp + 32), qf[1], acc, 0, 0, 0);
;                     const LAS float* rb = rpb + (r0 + c - gr + 7) * 31 + 15 - qcol;
; #pragma unroll
;                     for (int e = 0; e < 4; ++e) { const int kcol = kc0 + 16 * t2 + 4 * fq + e; const bool ok = (kcol >= cs) && (kcol < cs + 16);
;                         const float sv = ok ? acc[e] * 0.125f + rb[ok ? kcol : qcol] : -1.0e30f; acc[e] = sv; m = fmaxf(m, sv); }
;                     sl[2 * (c < 8 ? c : 0) + t2] = acc; }
;             } else {
;                 const int cc = c - NLOC;
; #pragma unroll
;                 for (int t4 = 0; t4 < 4; ++t4) {
;                     const LAS bf16* kp = cb + (16 * t4 + fr) * 72 + 8 * fq;
;                     f32x4 acc = {0.f, 0.f, 0.f, 0.f};
;                     acc = __builtin_amdgcn_mfma_f32_16x16x32_bf16(*(const LAS bf16x8*)(kp), qf[0], acc, 0, 0, 0);
;                     acc = __builtin_amdgcn_mfma_f32_16x16x32_bf16(*(const LAS bf16x8*)(kp + 32), qf[1], acc, 0, 0, 0);
; #pragma unroll
;                     for (int e = 0; e < 4; ++e) { acc[e] *= 0.125f; m = fmaxf(m, acc[e]); }
;                     sc[4 * (cc >= 0 ? cc : 0) + t4] = acc; }
;             }
;             if (sidx == NCH - 1) { m = fmaxf(m, __shfl_xor(m, 16)); m = fmaxf(m, __shfl_xor(m, 32)); }
	ds_read_b32 v240, v31 offset:38660
	ds_read_b32 v241, v31 offset:38664
	ds_read_b32 v242, v31 offset:38668
	ds_read_b32 v243, v31 offset:38672
	ds_read_b32 v244, v31 offset:38724
	ds_read_b32 v245, v31 offset:38728
	ds_read_b32 v246, v31 offset:38732
	ds_read_b32 v247, v31 offset:38736
	ds_read_b128 v[18:21], v32 offset:18432
	ds_read_b128 v[26:29], v32 offset:18496
	v_or_b32_e32 v24, 64, v34
	v_mov_b64_e32 v[22:23], s[8:9]
	v_mad_i64_i32 v[22:23], s[52:53], v24, s57, v[22:23]
	v_lshl_add_u64 v[22:23], v[22:23], 0, v[70:71]
	v_lshl_add_u64 v[22:23], v[22:23], 0, s[2:3]
	s_waitcnt lgkmcnt(1)
	v_mfma_f32_16x16x32_bf16 v[36:39], v[18:21], v[6:9], 0
	global_load_dwordx4 v[18:21], v[22:23], off offset:1024
	s_nop 0
	global_load_dwordx4 v[22:25], v[22:23], off offset:1152
	v_mov_b32_e32 v145, 0xf149f2ca
	v_mov_b32_e32 v148, 0xf149f2ca
	s_waitcnt lgkmcnt(0)
	v_mfma_f32_16x16x32_bf16 v[26:29], v[26:29], v[2:5], v[36:39]
	s_nop 2
	s_waitcnt lgkmcnt(0)
	s_nop 3
	v_fmac_f32_e32 v240, 0x3e000000, v26
	v_cndmask_b32_e64 v148, v148, v240, s[28:29]
	s_nop 2
	s_waitcnt lgkmcnt(0)
	s_nop 0
	v_fmac_f32_e32 v241, 0x3e000000, v27
	v_cndmask_b32_e64 v145, v145, v241, s[30:31]
	v_mov_b32_e32 v149, 0xf149f2ca
	v_mov_b32_e32 v151, 0xf149f2ca
	s_nop 2
	s_waitcnt lgkmcnt(0)
	v_fmac_f32_e32 v242, 0x3e000000, v28
	v_cndmask_b32_e64 v151, v151, v242, s[34:35]
	s_nop 2
	s_waitcnt lgkmcnt(0)
	v_fmac_f32_e32 v243, 0x3e000000, v29
	v_cndmask_b32_e64 v149, v149, v243, s[36:37]
	ds_read_b128 v[26:29], v33 offset:18432
	ds_read_b128 v[36:39], v33 offset:18496
	v_mov_b32_e32 v152, 0xf149f2ca
	v_mov_b32_e32 v154, 0xf149f2ca
	s_waitcnt lgkmcnt(1)
	v_mfma_f32_16x16x32_bf16 v[26:29], v[26:29], v[6:9], 0
	s_waitcnt lgkmcnt(0)
	v_mfma_f32_16x16x32_bf16 v[26:29], v[36:39], v[2:5], v[26:29]
	s_nop 2
	s_waitcnt lgkmcnt(0)
	s_nop 3
	v_fmac_f32_e32 v244, 0x3e000000, v26
	v_cndmask_b32_e64 v154, v154, v244, s[38:39]
	s_nop 2
	s_waitcnt lgkmcnt(0)
	s_nop 0
	v_fmac_f32_e32 v245, 0x3e000000, v27
	v_cndmask_b32_e64 v152, v152, v245, s[44:45]
	v_mov_b32_e32 v153, 0xf149f2ca
	v_mov_b32_e32 v156, 0xf149f2ca
	s_nop 2
	s_waitcnt lgkmcnt(0)
	v_fmac_f32_e32 v246, 0x3e000000, v28
	v_cndmask_b32_e64 v156, v156, v246, s[46:47]
	s_nop 2
	s_waitcnt lgkmcnt(0)
	v_fmac_f32_e32 v247, 0x3e000000, v29
	v_cndmask_b32_e64 v153, v153, v247, s[48:49]
	v_max3_f32 v26, v91, s67, v90
	v_max3_f32 v26, v26, v93, v92
	v_max3_f32 v26, v26, v95, v94
	v_max3_f32 v26, v26, v99, v98
	v_max3_f32 v26, v26, v97, v96
	v_max3_f32 v26, v26, v101, v100
	v_max3_f32 v26, v26, v105, v103
	v_max3_f32 v26, v26, v109, v107
	v_max3_f32 v26, v26, v104, v102
	v_max3_f32 v26, v26, v108, v106
	v_max3_f32 v26, v26, v113, v110
	v_max3_f32 v26, v26, v116, v112
	v_max3_f32 v26, v26, v114, v111
	v_max3_f32 v26, v26, v117, v115
	v_max3_f32 v26, v26, v121, v118
	v_max3_f32 v26, v26, v124, v120
	v_max3_f32 v26, v26, v122, v119
	v_max3_f32 v26, v26, v125, v123
	v_max3_f32 v26, v26, v130, v127
	v_max3_f32 v26, v26, v134, v129
	v_max3_f32 v26, v26, v131, v128
	v_max3_f32 v26, v26, v135, v133
	v_max3_f32 v26, v26, v139, v136
	v_max3_f32 v26, v26, v142, v138
	v_max3_f32 v26, v26, v140, v137
	v_max3_f32 v26, v26, v143, v141
	v_mad_u32_u24 v88, v88, s64, v30
	v_max3_f32 v26, v26, v147, v144
	s_waitcnt vmcnt(3)
	ds_write_b128 v75, v[10:13]
	s_waitcnt vmcnt(2)
	ds_write_b128 v75, v[14:17] offset:9216
	s_waitcnt lgkmcnt(0)
	s_barrier
	ds_read_b128 v[10:13], v88
	ds_read_b128 v[14:17], v88 offset:64
	v_max3_f32 v26, v26, v150, v146
	v_max3_f32 v26, v26, v148, v145
	v_max3_f32 v26, v26, v151, v149
	v_max3_f32 v26, v26, v154, v152
	v_max3_f32 v35, v26, v156, v153
	v_or_b32_e32 v26, 0x80, v34
	v_mov_b64_e32 v[44:45], s[8:9]
	v_mad_i64_i32 v[26:27], s[28:29], v26, s57, v[44:45]
	v_lshl_add_u64 v[26:27], v[26:27], 0, v[70:71]
	v_lshl_add_u64 v[30:31], v[26:27], 0, s[2:3]
	s_waitcnt lgkmcnt(1)
	v_mfma_f32_16x16x32_bf16 v[10:13], v[10:13], v[6:9], 0
	global_load_dwordx4 v[26:29], v[30:31], off offset:1024
	s_nop 0
	global_load_dwordx4 v[30:33], v[30:31], off offset:1152
	ds_read_b128 v[36:39], v88 offset:2304
	v_lshl_add_u64 v[78:79], s[4:5], 0, v[70:71]
	s_waitcnt lgkmcnt(1)
	v_mfma_f32_16x16x32_bf16 v[62:65], v[14:17], v[2:5], v[10:13]
	s_ashr_i32 s17, s16, 31
	v_mov_b32_e32 v81, v71
	v_cmp_lt_i32_e32 vcc, v82, v83
	ds_read_b128 v[10:13], v88 offset:2368
	v_add3_u32 v155, v85, v76, v86
	s_nop 2
	v_mul_f32_e32 v14, 0x3e000000, v62
	v_mul_f32_e32 v15, 0x3e000000, v63
	v_max3_f32 v35, v35, v14, v15
	v_mul_f32_e32 v40, 0x3e000000, v64
	s_waitcnt lgkmcnt(1)
	v_mfma_f32_16x16x32_bf16 v[14:17], v[36:39], v[6:9], 0
	v_mul_f32_e32 v36, 0x3e000000, v65
	v_max3_f32 v35, v35, v40, v36
	ds_read_b128 v[36:39], v88 offset:4608
	s_waitcnt lgkmcnt(1)
	v_mfma_f32_16x16x32_bf16 v[66:69], v[10:13], v[2:5], v[14:17]
	ds_read_b128 v[10:13], v88 offset:4672
	s_ashr_i32 s19, s18, 31
	s_ashr_i32 s21, s20, 31
	s_ashr_i32 s23, s22, 31
	s_ashr_i32 s25, s24, 31
	s_nop 2
	v_mul_f32_e32 v14, 0x3e000000, v66
	v_mul_f32_e32 v15, 0x3e000000, v67
	v_max3_f32 v35, v35, v14, v15
	s_waitcnt lgkmcnt(1)
	v_mfma_f32_16x16x32_bf16 v[14:17], v[36:39], v[6:9], 0
	v_mul_f32_e32 v40, 0x3e000000, v68
	v_mul_f32_e32 v41, 0x3e000000, v69
	v_max3_f32 v35, v35, v40, v41
	s_waitcnt lgkmcnt(0)
	v_mfma_f32_16x16x32_bf16 v[58:61], v[10:13], v[2:5], v[14:17]
	ds_read_b128 v[36:39], v88 offset:6912
	ds_read_b128 v[40:43], v88 offset:6976
	s_waitcnt vmcnt(3)
	ds_write_b128 v75, v[18:21] offset:18432
	s_waitcnt vmcnt(2)
	ds_write_b128 v75, v[22:25] offset:27648
	s_waitcnt lgkmcnt(0)
	s_nop 0
	v_mul_f32_e32 v10, 0x3e000000, v58
	v_mul_f32_e32 v11, 0x3e000000, v59
	v_max3_f32 v14, v35, v10, v11
	v_mfma_f32_16x16x32_bf16 v[10:13], v[36:39], v[6:9], 0
	v_mul_f32_e32 v15, 0x3e000000, v60
	v_mul_f32_e32 v16, 0x3e000000, v61
	v_max3_f32 v14, v14, v15, v16
	v_mfma_f32_16x16x32_bf16 v[54:57], v[40:43], v[2:5], v[10:13]
	s_barrier
; #define LAS __attribute__((address_space(3)))
; template <bool LOCAL>
; __device__ __forceinline__ void na_unit(const bf16* P, const bf16* VT, bf16* YCAT, const LAS float* rpb_l, LAS bf16* buf, int b, int gr, int hp, int qblk, int tid) {
;     ...
;             } else {
;                 const int cc = c - NLOC;
; #pragma unroll
;                 for (int t4 = 0; t4 < 4; ++t4) {
;                     const LAS bf16* kp = cb + (16 * t4 + fr) * 72 + 8 * fq;
;                     f32x4 acc = {0.f, 0.f, 0.f, 0.f};
;                     acc = __builtin_amdgcn_mfma_f32_16x16x32_bf16(*(const LAS bf16x8*)(kp), qf[0], acc, 0, 0, 0);
;                     acc = __builtin_amdgcn_mfma_f32_16x16x32_bf16(*(const LAS bf16x8*)(kp + 32), qf[1], acc, 0, 0, 0);
; #pragma unroll
;                     for (int e = 0; e < 4; ++e) { acc[e] *= 0.125f; m = fmaxf(m, acc[e]); }
;                     sc[4 * (cc >= 0 ? cc : 0) + t4] = acc; }
;             }
;             if (sidx == NCH - 1) { m = fmaxf(m, __shfl_xor(m, 16)); m = fmaxf(m, __shfl_xor(m, 32)); }
	v_or_b32_e32 v18, 0xc0, v34
	v_mad_i64_i32 v[18:19], s[28:29], v18, s57, v[44:45]
	v_lshl_add_u64 v[18:19], v[18:19], 0, v[70:71]
	s_nop 3
	v_mul_f32_e32 v10, 0x3e000000, v54
	v_mul_f32_e32 v11, 0x3e000000, v55
	v_max3_f32 v14, v14, v10, v11
	ds_read_b128 v[10:13], v88 offset:18432
	v_mul_f32_e32 v15, 0x3e000000, v56
	v_mul_f32_e32 v16, 0x3e000000, v57
	v_max3_f32 v35, v14, v15, v16
	ds_read_b128 v[14:17], v88 offset:18496
	v_lshl_add_u64 v[22:23], v[18:19], 0, s[2:3]
	s_waitcnt lgkmcnt(1)
	v_mfma_f32_16x16x32_bf16 v[10:13], v[10:13], v[6:9], 0
	global_load_dwordx4 v[18:21], v[22:23], off offset:1024
	global_load_dwordx4 v[158:161], v[22:23], off offset:1152
	ds_read_b128 v[22:25], v88 offset:20736
	s_ashr_i32 s27, s26, 31
	s_waitcnt lgkmcnt(1)
	v_mfma_f32_16x16x32_bf16 v[46:49], v[14:17], v[2:5], v[10:13]
	s_nop 2
	ds_read_b128 v[10:13], v88 offset:20800
	s_nop 3
	v_mul_f32_e32 v14, 0x3e000000, v46
	v_mul_f32_e32 v15, 0x3e000000, v47
	v_max3_f32 v34, v35, v14, v15
	v_mul_f32_e32 v35, 0x3e000000, v48
	s_waitcnt lgkmcnt(1)
	v_mfma_f32_16x16x32_bf16 v[14:17], v[22:25], v[6:9], 0
	v_mul_f32_e32 v22, 0x3e000000, v49
	v_max3_f32 v34, v34, v35, v22
	ds_read_b128 v[22:25], v88 offset:23040
	s_waitcnt lgkmcnt(1)
	v_mfma_f32_16x16x32_bf16 v[50:53], v[10:13], v[2:5], v[14:17]
	ds_read_b128 v[10:13], v88 offset:23104
	s_nop 6
	v_mul_f32_e32 v14, 0x3e000000, v50
	v_mul_f32_e32 v15, 0x3e000000, v51
	v_max3_f32 v34, v34, v14, v15
	s_waitcnt lgkmcnt(1)
	v_mfma_f32_16x16x32_bf16 v[14:17], v[22:25], v[6:9], 0
	v_mul_f32_e32 v35, 0x3e000000, v52
	v_mul_f32_e32 v36, 0x3e000000, v53
	v_max3_f32 v38, v34, v35, v36
	s_waitcnt lgkmcnt(0)
	v_mfma_f32_16x16x32_bf16 v[42:45], v[10:13], v[2:5], v[14:17]
	ds_read_b128 v[22:25], v88 offset:25344
	ds_read_b128 v[34:37], v88 offset:25408
	s_waitcnt vmcnt(3)
	ds_write_b128 v75, v[26:29]
	s_waitcnt vmcnt(2)
	ds_write_b128 v75, v[30:33] offset:9216
	s_waitcnt lgkmcnt(0)
	s_nop 0
	v_mul_f32_e32 v10, 0x3e000000, v42
	v_mul_f32_e32 v11, 0x3e000000, v43
	v_max3_f32 v14, v38, v10, v11
	v_mfma_f32_16x16x32_bf16 v[10:13], v[22:25], v[6:9], 0
	v_mul_f32_e32 v15, 0x3e000000, v44
	v_mul_f32_e32 v16, 0x3e000000, v45
	v_max3_f32 v14, v14, v15, v16
	v_mfma_f32_16x16x32_bf16 v[38:41], v[34:37], v[2:5], v[10:13]
	s_barrier
	v_add3_u32 v26, v87, s1, 64
	v_mul_u32_u24_e32 v26, 0x9000, v26
	v_lshl_add_u64 v[22:23], s[16:17], 1, v[78:79]
	s_nop 3
	v_mul_f32_e32 v10, 0x3e000000, v38
	v_mul_f32_e32 v11, 0x3e000000, v39
	v_max3_f32 v10, v14, v10, v11
	v_mul_f32_e32 v11, 0x3e000000, v40
	v_mul_f32_e32 v12, 0x3e000000, v41
	v_max3_f32 v34, v10, v11, v12
	v_or_b32_e32 v10, s1, v87
	v_mul_u32_u24_e32 v14, 0x9000, v10
	ds_read_b128 v[10:13], v88
	v_lshlrev_b32_e32 v70, 1, v14
	ds_read_b128 v[14:17], v88 offset:64
	v_lshlrev_b32_e32 v80, 1, v26
	v_lshl_add_u64 v[24:25], v[22:23], 0, v[70:71]
	v_lshl_add_u64 v[22:23], v[22:23], 0, v[80:81]
	s_waitcnt lgkmcnt(1)
	v_mfma_f32_16x16x32_bf16 v[10:13], v[10:13], v[6:9], 0
	global_load_dwordx4 v[162:165], v[24:25], off
	global_load_dwordx4 v[166:169], v[22:23], off
	ds_read_b128 v[22:25], v88 offset:2304
	s_add_i32 s16, s15, s50
	s_waitcnt lgkmcnt(1)
	v_mfma_f32_16x16x32_bf16 v[30:33], v[14:17], v[2:5], v[10:13]
	s_ashr_i32 s17, s16, 31
	s_ashr_i32 s15, s14, 31
	s_ashr_i32 s1, s0, 31
	ds_read_b128 v[10:13], v88 offset:2368
	s_nop 3
	v_mul_f32_e32 v14, 0x3e000000, v30
	v_mul_f32_e32 v15, 0x3e000000, v31
	v_max3_f32 v26, v34, v14, v15
	v_mul_f32_e32 v27, 0x3e000000, v32
	s_waitcnt lgkmcnt(1)
	v_mfma_f32_16x16x32_bf16 v[14:17], v[22:25], v[6:9], 0
	v_mul_f32_e32 v22, 0x3e000000, v33
	v_max3_f32 v26, v26, v27, v22
	ds_read_b128 v[22:25], v88 offset:4608
	s_waitcnt lgkmcnt(1)
	v_mfma_f32_16x16x32_bf16 v[34:37], v[10:13], v[2:5], v[14:17]
	ds_read_b128 v[10:13], v88 offset:4672
	s_nop 6
	v_mul_f32_e32 v14, 0x3e000000, v34
	v_mul_f32_e32 v15, 0x3e000000, v35
	v_max3_f32 v26, v26, v14, v15
	s_waitcnt lgkmcnt(1)
	v_mfma_f32_16x16x32_bf16 v[14:17], v[22:25], v[6:9], 0
	v_mul_f32_e32 v27, 0x3e000000, v36
	v_mul_f32_e32 v28, 0x3e000000, v37
	v_max3_f32 v87, v26, v27, v28
	s_waitcnt lgkmcnt(0)
	v_mfma_f32_16x16x32_bf16 v[26:29], v[10:13], v[2:5], v[14:17]
	ds_read_b128 v[22:25], v88 offset:6912
	ds_read_b128 v[170:173], v88 offset:6976
	s_waitcnt vmcnt(3)
	ds_write_b128 v75, v[18:21] offset:18432
	s_waitcnt vmcnt(2)
	ds_write_b128 v75, v[158:161] offset:27648
	s_waitcnt lgkmcnt(0)
	s_nop 0
	v_mul_f32_e32 v10, 0x3e000000, v26
	v_mul_f32_e32 v11, 0x3e000000, v27
	v_max3_f32 v14, v87, v10, v11
	v_mfma_f32_16x16x32_bf16 v[10:13], v[22:25], v[6:9], 0
	v_mul_f32_e32 v15, 0x3e000000, v28
	v_mul_f32_e32 v16, 0x3e000000, v29
	v_max3_f32 v14, v14, v15, v16
	v_mfma_f32_16x16x32_bf16 v[22:25], v[170:173], v[2:5], v[10:13]
	s_barrier
; #define LAS __attribute__((address_space(3)))
; __device__ __forceinline__ unsigned cvt_pk_bf16(float lo, float hi) { const float __attribute__((ext_vector_type(2))) v = {lo, hi}; return __builtin_bit_cast(unsigned, __builtin_convertvector(v, bf16x2_t)); }
; template <bool LOCAL>
; __device__ __forceinline__ void na_unit(const bf16* P, const bf16* VT, bf16* YCAT, const LAS float* rpb_l, LAS bf16* buf, int b, int gr, int hp, int qblk, int tid) {
;     ...
;                 const int cc = c - NLOC;
; #pragma unroll
;                 for (int t4 = 0; t4 < 4; ++t4) {
;                     const LAS bf16* kp = cb + (16 * t4 + fr) * 72 + 8 * fq;
;                     f32x4 acc = {0.f, 0.f, 0.f, 0.f};
;                     acc = __builtin_amdgcn_mfma_f32_16x16x32_bf16(*(const LAS bf16x8*)(kp), qf[0], acc, 0, 0, 0);
;                     acc = __builtin_amdgcn_mfma_f32_16x16x32_bf16(*(const LAS bf16x8*)(kp + 32), qf[1], acc, 0, 0, 0);
; #pragma unroll
;                     for (int e = 0; e < 4; ++e) { acc[e] *= 0.125f; m = fmaxf(m, acc[e]); }
;                     sc[4 * (cc >= 0 ? cc : 0) + t4] = acc; }
;             }
;             if (sidx == NCH - 1) { m = fmaxf(m, __shfl_xor(m, 16)); m = fmaxf(m, __shfl_xor(m, 32)); }
;         } else {
;             const int c = sidx - NCH;
;             if (LOCAL && c < 8) {
;                 float p[8];
; #pragma unroll
;                 for (int e = 0; e < 4; ++e) { p[e] = __expf(sl[2 * (c < 8 ? c : 0)][e] - m); p[4 + e] = __expf(sl[2 * (c < 8 ? c : 0) + 1][e] - m); }
; #pragma unroll
;                 for (int e = 0; e < 8; ++e) lsum += p[e];
;                 const bf16x8 pf = __builtin_bit_cast(bf16x8, (v4u){pg8::cvt_pk_bf16(p[0], p[1]), pg8::cvt_pk_bf16(p[2], p[3]), pg8::cvt_pk_bf16(p[4], p[5]), pg8::cvt_pk_bf16(p[6], p[7])});
; #pragma unroll
;                 for (int dt = 0; dt < 4; ++dt) { const LAS bf16* vp = cb + (16 * dt + fr) * 72 + kc0 + 4 * fq;
;                     o[dt] = __builtin_amdgcn_mfma_f32_16x16x32_bf16(frag44(vp, vp + 16), pf, o[dt], 0, 0, 0); }
	v_lshl_add_u64 v[18:19], s[16:17], 1, v[78:79]
	v_lshl_add_u64 v[20:21], v[18:19], 0, v[70:71]
	v_lshl_add_u64 v[18:19], v[18:19], 0, v[80:81]
	s_nop 3
	v_mul_f32_e32 v10, 0x3e000000, v22
	v_mul_f32_e32 v11, 0x3e000000, v23
	v_max3_f32 v14, v14, v10, v11
	ds_read_b128 v[10:13], v88 offset:18432
	v_mul_f32_e32 v15, 0x3e000000, v24
	v_mul_f32_e32 v16, 0x3e000000, v25
	v_max3_f32 v87, v14, v15, v16
	ds_read_b128 v[14:17], v88 offset:18496
	s_waitcnt lgkmcnt(1)
	v_mfma_f32_16x16x32_bf16 v[10:13], v[10:13], v[6:9], 0
	global_load_dwordx4 v[158:161], v[20:21], off
	global_load_dwordx4 v[170:173], v[18:19], off
	ds_read_b128 v[18:21], v88 offset:20736
	ds_read_b128 v[174:177], v88 offset:23040
	s_waitcnt lgkmcnt(2)
	v_mfma_f32_16x16x32_bf16 v[14:17], v[14:17], v[2:5], v[10:13]
	s_nop 2
	ds_read_b128 v[10:13], v88 offset:20800
	s_waitcnt lgkmcnt(2)
	v_mfma_f32_16x16x32_bf16 v[18:21], v[18:21], v[6:9], 0
	s_nop 1
	v_mul_f32_e32 v126, 0x3e000000, v14
	v_mul_f32_e32 v132, 0x3e000000, v15
	v_max3_f32 v87, v87, v126, v132
	s_waitcnt lgkmcnt(0)
	v_mfma_f32_16x16x32_bf16 v[18:21], v[10:13], v[2:5], v[18:21]
	ds_read_b128 v[10:13], v88 offset:23104
	ds_read_b128 v[178:181], v88 offset:25344
	ds_read_b128 v[182:185], v88 offset:25408
	v_mul_f32_e32 v126, 0x3e000000, v16
	v_mfma_f32_16x16x32_bf16 v[174:177], v[174:177], v[6:9], 0
	v_mul_f32_e32 v132, 0x3e000000, v17
	v_max3_f32 v87, v87, v126, v132
	s_nop 0
	v_mul_f32_e32 v126, 0x3e000000, v18
	s_waitcnt lgkmcnt(1)
	v_mfma_f32_16x16x32_bf16 v[6:9], v[178:181], v[6:9], 0
	v_mul_f32_e32 v132, 0x3e000000, v19
	v_max3_f32 v87, v87, v126, v132
	v_mul_f32_e32 v126, 0x3e000000, v20
	v_mfma_f32_16x16x32_bf16 v[10:13], v[10:13], v[2:5], v[174:177]
	v_mul_f32_e32 v132, 0x3e000000, v21
	v_max3_f32 v87, v87, v126, v132
	s_waitcnt vmcnt(3)
	ds_write_b128 v75, v[162:165]
	s_waitcnt vmcnt(2)
	ds_write_b128 v75, v[166:169] offset:9216
	s_waitcnt lgkmcnt(2)
	v_mfma_f32_16x16x32_bf16 v[2:5], v[182:185], v[2:5], v[6:9]
	v_mul_f32_e32 v88, 0x3e000000, v10
	v_mul_f32_e32 v126, 0x3e000000, v11
	v_max3_f32 v87, v87, v88, v126
	v_mul_f32_e32 v88, 0x3e000000, v12
	v_mul_f32_e32 v126, 0x3e000000, v13
	v_max3_f32 v87, v87, v88, v126
	s_nop 1
	v_mul_f32_e32 v6, 0x3e000000, v2
	v_mul_f32_e32 v7, 0x3e000000, v3
	v_max3_f32 v6, v87, v6, v7
	v_mul_f32_e32 v7, 0x3e000000, v4
	v_mul_f32_e32 v8, 0x3e000000, v5
	v_max3_f32 v6, v6, v7, v8
	v_cndmask_b32_e32 v7, v1, v82, vcc
	v_lshlrev_b32_e32 v87, 2, v7
	ds_bpermute_b32 v7, v87, v6
	v_cmp_lt_i32_e32 vcc, v84, v83
	v_lshl_add_u32 v8, v89, 1, v155
	v_lshl_add_u64 v[182:183], s[14:15], 1, v[78:79]
	v_lshl_add_u64 v[184:185], v[182:183], 0, v[70:71]
	s_waitcnt lgkmcnt(0)
	v_max_f32_e32 v7, v7, v7
	v_max_f32_e32 v6, v6, v7
	v_cndmask_b32_e32 v7, v1, v84, vcc
	v_lshlrev_b32_e32 v88, 2, v7
	ds_bpermute_b32 v7, v88, v6
	v_lshl_add_u64 v[186:187], v[182:183], 0, v[80:81]
	s_waitcnt lgkmcnt(0)
	s_barrier
	v_max_f32_e32 v7, v7, v7
	v_max_f32_e32 v132, v6, v7
	v_sub_f32_e32 v6, v91, v132
	v_mul_f32_e32 v6, 0x3fb8aa3b, v6
	v_exp_f32_e32 v126, v6
	v_sub_f32_e32 v6, v95, v132
	v_mul_f32_e32 v6, 0x3fb8aa3b, v6
	v_exp_f32_e32 v91, v6
	v_sub_f32_e32 v6, v90, v132
	v_mul_f32_e32 v6, 0x3fb8aa3b, v6
	v_exp_f32_e32 v95, v6
	v_sub_f32_e32 v6, v94, v132
	v_mul_f32_e32 v6, 0x3fb8aa3b, v6
	v_exp_f32_e32 v90, v6
	v_sub_f32_e32 v6, v93, v132
	v_mul_f32_e32 v6, 0x3fb8aa3b, v6
	v_exp_f32_e32 v94, v6
	v_sub_f32_e32 v6, v99, v132
	v_mul_f32_e32 v6, 0x3fb8aa3b, v6
	v_exp_f32_e32 v93, v6
	v_sub_f32_e32 v6, v92, v132
	v_mul_f32_e32 v6, 0x3fb8aa3b, v6
	v_exp_f32_e32 v99, v6
	v_sub_f32_e32 v6, v98, v132
	v_mul_f32_e32 v6, 0x3fb8aa3b, v6
	v_exp_f32_e32 v92, v6
	v_add_u32_e32 v7, 0x800, v8
	v_add_u32_e32 v6, 0x1000, v8
	ds_read2_b64 v[162:165], v8 offset1:4
	ds_read2_b64 v[174:177], v7 offset0:32 offset1:36
	ds_read2_b64 v[178:181], v6 offset0:64 offset1:68
	global_load_dwordx4 v[182:185], v[184:185], off
	s_nop 0
	global_load_dwordx4 v[186:189], v[186:187], off
	v_sub_f32_e32 v9, v97, v132
	v_mul_f32_e32 v9, 0x3fb8aa3b, v9
	v_add_u32_e32 v157, 0x1800, v8
	v_exp_f32_e32 v85, v9
	v_sub_f32_e32 v9, v105, v132
	ds_read2_b64 v[190:193], v157 offset0:96 offset1:100
	v_mul_f32_e32 v9, 0x3fb8aa3b, v9
	v_exp_f32_e32 v76, v9
	v_sub_f32_e32 v9, v96, v132
	v_mul_f32_e32 v9, 0x3fb8aa3b, v9
	v_exp_f32_e32 v89, v9
	v_sub_f32_e32 v9, v103, v132
	v_mul_f32_e32 v9, 0x3fb8aa3b, v9
	v_exp_f32_e32 v86, v9
	v_sub_f32_e32 v9, v101, v132
	v_mul_f32_e32 v9, 0x3fb8aa3b, v9
	v_exp_f32_e32 v97, v9
	v_sub_f32_e32 v9, v109, v132
	v_cvt_pk_bf16_f32 v166, v126, v95
	v_cvt_pk_bf16_f32 v167, v94, v99
	v_cvt_pk_bf16_f32 v168, v91, v90
	v_cvt_pk_bf16_f32 v169, v93, v92
	s_waitcnt vmcnt(3)
	ds_write_b128 v75, v[158:161] offset:18432
	s_waitcnt vmcnt(2)
	ds_write_b128 v75, v[170:173] offset:27648
	v_mul_f32_e32 v9, 0x3fb8aa3b, v9
	v_add_u32_e32 v159, 0x4800, v8
	v_add_u32_e32 v158, 0x5000, v8
	s_waitcnt lgkmcnt(5)
	v_mfma_f32_16x16x32_bf16 v[162:165], v[162:165], v[166:169], 0
	s_waitcnt lgkmcnt(0)
	s_barrier
; #define LAS __attribute__((address_space(3)))
; __device__ __forceinline__ unsigned cvt_pk_bf16(float lo, float hi) { const float __attribute__((ext_vector_type(2))) v = {lo, hi}; return __builtin_bit_cast(unsigned, __builtin_convertvector(v, bf16x2_t)); }
; template <bool LOCAL>
; __device__ __forceinline__ void na_unit(const bf16* P, const bf16* VT, bf16* YCAT, const LAS float* rpb_l, LAS bf16* buf, int b, int gr, int hp, int qblk, int tid) {
;     ...
;             if (LOCAL && c < 8) {
;                 float p[8];
; #pragma unroll
;                 for (int e = 0; e < 4; ++e) { p[e] = __expf(sl[2 * (c < 8 ? c : 0)][e] - m); p[4 + e] = __expf(sl[2 * (c < 8 ? c : 0) + 1][e] - m); }
; #pragma unroll
;                 for (int e = 0; e < 8; ++e) lsum += p[e];
;                 const bf16x8 pf = __builtin_bit_cast(bf16x8, (v4u){pg8::cvt_pk_bf16(p[0], p[1]), pg8::cvt_pk_bf16(p[2], p[3]), pg8::cvt_pk_bf16(p[4], p[5]), pg8::cvt_pk_bf16(p[6], p[7])});
; #pragma unroll
;                 for (int dt = 0; dt < 4; ++dt) { const LAS bf16* vp = cb + (16 * dt + fr) * 72 + kc0 + 4 * fq;
;                     o[dt] = __builtin_amdgcn_mfma_f32_16x16x32_bf16(frag44(vp, vp + 16), pf, o[dt], 0, 0, 0); }
	v_mfma_f32_16x16x32_bf16 v[174:177], v[174:177], v[166:169], 0
	v_exp_f32_e32 v96, v9
	v_sub_f32_e32 v9, v100, v132
	ds_read2_b64 v[170:173], v159 offset1:4
	v_mfma_f32_16x16x32_bf16 v[178:181], v[178:181], v[166:169], 0
	v_mul_f32_e32 v9, 0x3fb8aa3b, v9
	v_exp_f32_e32 v98, v9
	v_sub_f32_e32 v9, v107, v132
	v_mfma_f32_16x16x32_bf16 v[166:169], v[190:193], v[166:169], 0
	ds_read2_b64 v[190:193], v158 offset0:32 offset1:36
	v_mul_f32_e32 v9, 0x3fb8aa3b, v9
	v_exp_f32_e32 v100, v9
	v_lshl_add_u64 v[160:161], s[0:1], 1, v[78:79]
	v_cvt_pk_bf16_f32 v194, v85, v89
	v_cvt_pk_bf16_f32 v195, v97, v98
	v_cvt_pk_bf16_f32 v196, v76, v86
	v_cvt_pk_bf16_f32 v197, v96, v100
	v_lshl_add_u64 v[198:199], v[160:161], 0, v[70:71]
	v_lshl_add_u64 v[200:201], v[160:161], 0, v[80:81]
	v_add_u32_e32 v160, 0x5800, v8
	s_waitcnt lgkmcnt(1)
	v_mfma_f32_16x16x32_bf16 v[162:165], v[170:173], v[194:197], v[162:165]
	v_sub_f32_e32 v9, v104, v132
	v_mul_f32_e32 v9, 0x3fb8aa3b, v9
	v_add_u32_e32 v161, 0x6000, v8
	s_waitcnt lgkmcnt(0)
	v_mfma_f32_16x16x32_bf16 v[170:173], v[190:193], v[194:197], v[174:177]
	v_exp_f32_e32 v103, v9
	v_sub_f32_e32 v9, v113, v132
	v_mul_f32_e32 v9, 0x3fb8aa3b, v9
	ds_read2_b64 v[174:177], v160 offset0:64 offset1:68
	global_load_dwordx4 v[190:193], v[198:199], off
	s_nop 0
	global_load_dwordx4 v[198:201], v[200:201], off
	s_waitcnt lgkmcnt(0)
	v_mfma_f32_16x16x32_bf16 v[174:177], v[174:177], v[194:197], v[178:181]
	s_nop 2
	ds_read2_b64 v[178:181], v161 offset0:96 offset1:100
	v_exp_f32_e32 v101, v9
	v_sub_f32_e32 v9, v102, v132
	v_mul_f32_e32 v9, 0x3fb8aa3b, v9
	v_exp_f32_e32 v104, v9
	v_sub_f32_e32 v9, v110, v132
	v_mul_f32_e32 v9, 0x3fb8aa3b, v9
	v_exp_f32_e32 v102, v9
	v_sub_f32_e32 v9, v108, v132
	v_mul_f32_e32 v9, 0x3fb8aa3b, v9
	v_exp_f32_e32 v107, v9
	v_sub_f32_e32 v9, v116, v132
	v_mul_f32_e32 v9, 0x3fb8aa3b, v9
	s_waitcnt lgkmcnt(0)
	v_mfma_f32_16x16x32_bf16 v[166:169], v[178:181], v[194:197], v[166:169]
	s_waitcnt vmcnt(3)
	ds_write_b128 v75, v[182:185]
	s_waitcnt vmcnt(2)
	ds_write_b128 v75, v[186:189] offset:9216
	s_waitcnt lgkmcnt(0)
	s_barrier
	v_exp_f32_e32 v105, v9
	v_sub_f32_e32 v9, v106, v132
	ds_read2_b64 v[178:181], v8 offset1:4
	ds_read2_b64 v[182:185], v7 offset0:32 offset1:36
	v_mul_f32_e32 v9, 0x3fb8aa3b, v9
	v_exp_f32_e32 v106, v9
	v_sub_f32_e32 v9, v112, v132
	v_mul_f32_e32 v9, 0x3fb8aa3b, v9
	v_exp_f32_e32 v108, v9
	v_lshl_add_u64 v[194:195], s[18:19], 1, v[78:79]
	v_cvt_pk_bf16_f32 v186, v103, v104
	v_cvt_pk_bf16_f32 v187, v107, v106
	v_cvt_pk_bf16_f32 v188, v101, v102
	v_cvt_pk_bf16_f32 v189, v105, v108
	v_lshl_add_u64 v[112:113], v[194:195], 0, v[70:71]
	v_lshl_add_u64 v[194:195], v[194:195], 0, v[80:81]
	s_waitcnt lgkmcnt(1)
	v_mfma_f32_16x16x32_bf16 v[162:165], v[178:181], v[186:189], v[162:165]
	ds_read2_b64 v[178:181], v6 offset0:64 offset1:68
	v_sub_f32_e32 v9, v114, v132
	v_mul_f32_e32 v9, 0x3fb8aa3b, v9
	s_waitcnt lgkmcnt(1)
	v_mfma_f32_16x16x32_bf16 v[170:173], v[182:185], v[186:189], v[170:173]
	global_load_dwordx4 v[182:185], v[112:113], off
	s_nop 0
	global_load_dwordx4 v[194:197], v[194:195], off
	v_exp_f32_e32 v110, v9
	v_sub_f32_e32 v9, v121, v132
	s_waitcnt lgkmcnt(0)
	v_mfma_f32_16x16x32_bf16 v[174:177], v[178:181], v[186:189], v[174:177]
	ds_read2_b64 v[178:181], v157 offset0:96 offset1:100
	v_mul_f32_e32 v9, 0x3fb8aa3b, v9
	v_exp_f32_e32 v109, v9
	v_sub_f32_e32 v9, v111, v132
	v_mul_f32_e32 v9, 0x3fb8aa3b, v9
	v_exp_f32_e32 v112, v9
	v_sub_f32_e32 v9, v118, v132
	v_mul_f32_e32 v9, 0x3fb8aa3b, v9
	v_exp_f32_e32 v111, v9
	v_sub_f32_e32 v9, v117, v132
	v_mul_f32_e32 v9, 0x3fb8aa3b, v9
	v_exp_f32_e32 v114, v9
	v_sub_f32_e32 v9, v124, v132
	v_mul_f32_e32 v9, 0x3fb8aa3b, v9
	s_waitcnt lgkmcnt(0)
	v_mfma_f32_16x16x32_bf16 v[166:169], v[178:181], v[186:189], v[166:169]
	s_waitcnt vmcnt(3)
	ds_write_b128 v75, v[190:193] offset:18432
	s_waitcnt vmcnt(2)
	ds_write_b128 v75, v[198:201] offset:27648
	s_waitcnt lgkmcnt(0)
	s_barrier
	v_exp_f32_e32 v113, v9
	v_sub_f32_e32 v9, v115, v132
	ds_read2_b64 v[178:181], v159 offset1:4
	v_mul_f32_e32 v9, 0x3fb8aa3b, v9
	v_exp_f32_e32 v115, v9
	v_sub_f32_e32 v9, v120, v132
	v_mul_f32_e32 v9, 0x3fb8aa3b, v9
	v_exp_f32_e32 v116, v9
	v_lshl_add_u64 v[198:199], s[20:21], 1, v[78:79]
	v_lshl_add_u64 v[200:201], v[198:199], 0, v[70:71]
	ds_read2_b64 v[186:189], v158 offset0:32 offset1:36
	v_cvt_pk_bf16_f32 v190, v110, v112
	v_cvt_pk_bf16_f32 v191, v114, v115
	v_cvt_pk_bf16_f32 v192, v109, v111
	v_cvt_pk_bf16_f32 v193, v113, v116
	v_lshl_add_u64 v[120:121], v[198:199], 0, v[80:81]
	v_sub_f32_e32 v9, v122, v132
	s_waitcnt lgkmcnt(1)
	v_mfma_f32_16x16x32_bf16 v[162:165], v[178:181], v[190:193], v[162:165]
	global_load_dwordx4 v[178:181], v[200:201], off
	s_nop 0
	global_load_dwordx4 v[198:201], v[120:121], off
	v_mul_f32_e32 v9, 0x3fb8aa3b, v9
	v_exp_f32_e32 v118, v9
	s_waitcnt lgkmcnt(0)
	v_mfma_f32_16x16x32_bf16 v[170:173], v[186:189], v[190:193], v[170:173]
	ds_read2_b64 v[186:189], v160 offset0:64 offset1:68
	v_sub_f32_e32 v9, v130, v132
	v_mul_f32_e32 v9, 0x3fb8aa3b, v9
	s_waitcnt lgkmcnt(0)
	v_mfma_f32_16x16x32_bf16 v[174:177], v[186:189], v[190:193], v[174:177]
	ds_read2_b64 v[186:189], v161 offset0:96 offset1:100
	v_exp_f32_e32 v117, v9
	v_sub_f32_e32 v9, v119, v132
	v_mul_f32_e32 v9, 0x3fb8aa3b, v9
	v_exp_f32_e32 v120, v9
	v_sub_f32_e32 v9, v127, v132
	v_mul_f32_e32 v9, 0x3fb8aa3b, v9
	v_exp_f32_e32 v119, v9
	v_sub_f32_e32 v9, v125, v132
	v_mul_f32_e32 v9, 0x3fb8aa3b, v9
	v_exp_f32_e32 v122, v9
	v_sub_f32_e32 v9, v134, v132
	v_mul_f32_e32 v9, 0x3fb8aa3b, v9
	s_waitcnt lgkmcnt(0)
	v_mfma_f32_16x16x32_bf16 v[166:169], v[186:189], v[190:193], v[166:169]
	s_waitcnt vmcnt(3)
	ds_write_b128 v75, v[182:185]
	s_waitcnt vmcnt(2)
	ds_write_b128 v75, v[194:197] offset:9216
	s_waitcnt lgkmcnt(0)
	s_barrier
; #define LAS __attribute__((address_space(3)))
; __device__ __forceinline__ unsigned cvt_pk_bf16(float lo, float hi) { const float __attribute__((ext_vector_type(2))) v = {lo, hi}; return __builtin_bit_cast(unsigned, __builtin_convertvector(v, bf16x2_t)); }
; #define NA_STORE(sidx) do { LAS bf16* d_ = buf + ((sidx) & 1) * 9216; _Pragma("unroll") for (int q_ = 0; q_ < 2; ++q_) *(LAS v4u*)(d_ + q_ * 4608 + lrow * 72 + lseg * 8) = ld[(sidx) & 1][q_]; } while (0)
; template <bool LOCAL>
; __device__ __forceinline__ void na_unit(const bf16* P, const bf16* VT, bf16* YCAT, const LAS float* rpb_l, LAS bf16* buf, int b, int gr, int hp, int qblk, int tid) {
;     ...
;             if (LOCAL && c < 8) {
;                 float p[8];
; #pragma unroll
;                 for (int e = 0; e < 4; ++e) { p[e] = __expf(sl[2 * (c < 8 ? c : 0)][e] - m); p[4 + e] = __expf(sl[2 * (c < 8 ? c : 0) + 1][e] - m); }
; #pragma unroll
;                 for (int e = 0; e < 8; ++e) lsum += p[e];
;                 const bf16x8 pf = __builtin_bit_cast(bf16x8, (v4u){pg8::cvt_pk_bf16(p[0], p[1]), pg8::cvt_pk_bf16(p[2], p[3]), pg8::cvt_pk_bf16(p[4], p[5]), pg8::cvt_pk_bf16(p[6], p[7])});
; #pragma unroll
;                 for (int dt = 0; dt < 4; ++dt) { const LAS bf16* vp = cb + (16 * dt + fr) * 72 + kc0 + 4 * fq;
;                     o[dt] = __builtin_amdgcn_mfma_f32_16x16x32_bf16(frag44(vp, vp + 16), pf, o[dt], 0, 0, 0); }
;     ...
;         if (sidx + 1 < 2 * NCH) NA_STORE(sidx + 1);
;         __syncthreads();
	v_exp_f32_e32 v121, v9
	v_sub_f32_e32 v9, v123, v132
	ds_read2_b64 v[182:185], v8 offset1:4
	ds_read2_b64 v[186:189], v7 offset0:32 offset1:36
	v_mul_f32_e32 v9, 0x3fb8aa3b, v9
	v_exp_f32_e32 v123, v9
	v_sub_f32_e32 v9, v129, v132
	v_mul_f32_e32 v9, 0x3fb8aa3b, v9
	v_exp_f32_e32 v124, v9
	v_lshl_add_u64 v[194:195], s[22:23], 1, v[78:79]
	v_cvt_pk_bf16_f32 v190, v118, v120
	v_cvt_pk_bf16_f32 v191, v122, v123
	v_cvt_pk_bf16_f32 v192, v117, v119
	v_cvt_pk_bf16_f32 v193, v121, v124
	v_lshl_add_u64 v[196:197], v[194:195], 0, v[70:71]
	v_lshl_add_u64 v[194:195], v[194:195], 0, v[80:81]
	s_waitcnt lgkmcnt(1)
	v_mfma_f32_16x16x32_bf16 v[162:165], v[182:185], v[190:193], v[162:165]
	ds_read2_b64 v[182:185], v6 offset0:64 offset1:68
	v_sub_f32_e32 v9, v131, v132
	v_mul_f32_e32 v9, 0x3fb8aa3b, v9
	s_waitcnt lgkmcnt(1)
	v_mfma_f32_16x16x32_bf16 v[170:173], v[186:189], v[190:193], v[170:173]
	global_load_dwordx4 v[186:189], v[196:197], off
	s_nop 0
	global_load_dwordx4 v[194:197], v[194:195], off
	v_exp_f32_e32 v127, v9
	v_sub_f32_e32 v9, v139, v132
	v_mul_f32_e32 v9, 0x3fb8aa3b, v9
	v_exp_f32_e32 v125, v9
	v_sub_f32_e32 v9, v128, v132
	v_mul_f32_e32 v9, 0x3fb8aa3b, v9
	v_exp_f32_e32 v129, v9
	v_sub_f32_e32 v9, v136, v132
	v_mul_f32_e32 v9, 0x3fb8aa3b, v9
	v_exp_f32_e32 v128, v9
	v_sub_f32_e32 v9, v135, v132
	v_mul_f32_e32 v9, 0x3fb8aa3b, v9
	v_exp_f32_e32 v131, v9
	v_sub_f32_e32 v9, v142, v132
	s_waitcnt lgkmcnt(0)
	v_mfma_f32_16x16x32_bf16 v[174:177], v[182:185], v[190:193], v[174:177]
	ds_read2_b64 v[182:185], v157 offset0:96 offset1:100
	v_mul_f32_e32 v9, 0x3fb8aa3b, v9
	s_waitcnt vmcnt(3)
	ds_write_b128 v75, v[178:181] offset:18432
	s_waitcnt vmcnt(2)
	ds_write_b128 v75, v[198:201] offset:27648
	s_waitcnt lgkmcnt(0)
	s_barrier
	v_exp_f32_e32 v130, v9
	v_sub_f32_e32 v9, v133, v132
	ds_read2_b64 v[178:181], v159 offset1:4
	v_mul_f32_e32 v9, 0x3fb8aa3b, v9
	v_exp_f32_e32 v133, v9
	v_sub_f32_e32 v9, v138, v132
	v_mul_f32_e32 v9, 0x3fb8aa3b, v9
	v_exp_f32_e32 v134, v9
	v_lshl_add_u64 v[198:199], s[24:25], 1, v[78:79]
	v_mfma_f32_16x16x32_bf16 v[166:169], v[182:185], v[190:193], v[166:169]
	v_lshl_add_u64 v[200:201], v[198:199], 0, v[70:71]
	ds_read2_b64 v[182:185], v158 offset0:32 offset1:36
	v_cvt_pk_bf16_f32 v190, v127, v129
	v_cvt_pk_bf16_f32 v191, v131, v133
	v_cvt_pk_bf16_f32 v192, v125, v128
	v_cvt_pk_bf16_f32 v193, v130, v134
	v_lshl_add_u64 v[138:139], v[198:199], 0, v[80:81]
	v_sub_f32_e32 v9, v140, v132
	s_waitcnt lgkmcnt(1)
	v_mfma_f32_16x16x32_bf16 v[162:165], v[178:181], v[190:193], v[162:165]
	global_load_dwordx4 v[178:181], v[200:201], off
	s_nop 0
	global_load_dwordx4 v[198:201], v[138:139], off
	v_mul_f32_e32 v9, 0x3fb8aa3b, v9
	v_exp_f32_e32 v136, v9
	s_waitcnt lgkmcnt(0)
	v_mfma_f32_16x16x32_bf16 v[170:173], v[182:185], v[190:193], v[170:173]
	ds_read2_b64 v[182:185], v160 offset0:64 offset1:68
	v_sub_f32_e32 v9, v147, v132
	v_mul_f32_e32 v9, 0x3fb8aa3b, v9
	s_waitcnt lgkmcnt(0)
	v_mfma_f32_16x16x32_bf16 v[174:177], v[182:185], v[190:193], v[174:177]
	ds_read2_b64 v[182:185], v161 offset0:96 offset1:100
	v_exp_f32_e32 v135, v9
	v_sub_f32_e32 v9, v137, v132
	v_mul_f32_e32 v9, 0x3fb8aa3b, v9
	v_exp_f32_e32 v138, v9
	v_sub_f32_e32 v9, v144, v132
	v_mul_f32_e32 v9, 0x3fb8aa3b, v9
	v_exp_f32_e32 v137, v9
	v_sub_f32_e32 v9, v143, v132
	v_mul_f32_e32 v9, 0x3fb8aa3b, v9
	s_waitcnt lgkmcnt(0)
	v_mfma_f32_16x16x32_bf16 v[166:169], v[182:185], v[190:193], v[166:169]
	s_waitcnt vmcnt(3)
	ds_write_b128 v75, v[186:189]
	s_waitcnt vmcnt(2)
	ds_write_b128 v75, v[194:197] offset:9216
	s_waitcnt lgkmcnt(0)
	s_barrier
	v_exp_f32_e32 v140, v9
	v_sub_f32_e32 v9, v150, v132
	ds_read2_b64 v[182:185], v8 offset1:4
	v_mul_f32_e32 v9, 0x3fb8aa3b, v9
	ds_read2_b64 v[190:193], v7 offset0:32 offset1:36
	v_exp_f32_e32 v139, v9
	v_sub_f32_e32 v9, v141, v132
	v_sub_f32_e32 v8, v146, v132
	v_mul_f32_e32 v9, 0x3fb8aa3b, v9
	v_mul_f32_e32 v8, 0x3fb8aa3b, v8
	v_exp_f32_e32 v141, v9
	v_exp_f32_e32 v142, v8
	v_cvt_pk_bf16_f32 v186, v136, v138
	v_cvt_pk_bf16_f32 v188, v135, v137
	v_cvt_pk_bf16_f32 v187, v140, v141
	v_cvt_pk_bf16_f32 v189, v139, v142
	v_lshl_add_u64 v[8:9], s[26:27], 1, v[78:79]
	v_sub_f32_e32 v144, v149, v132
	s_waitcnt lgkmcnt(1)
	v_mfma_f32_16x16x32_bf16 v[162:165], v[182:185], v[186:189], v[162:165]
	ds_read2_b64 v[182:185], v6 offset0:64 offset1:68
	v_lshl_add_u64 v[6:7], v[8:9], 0, v[70:71]
	v_lshl_add_u64 v[8:9], v[8:9], 0, v[80:81]
	s_waitcnt lgkmcnt(1)
	v_mfma_f32_16x16x32_bf16 v[170:173], v[190:193], v[186:189], v[170:173]
	global_load_dwordx4 v[190:193], v[6:7], off
	global_load_dwordx4 v[194:197], v[8:9], off
	ds_read2_b64 v[78:81], v157 offset0:96 offset1:100
	s_waitcnt vmcnt(3)
	ds_write_b128 v75, v[178:181] offset:18432
	s_waitcnt vmcnt(2)
	ds_write_b128 v75, v[198:201] offset:27648
	s_waitcnt lgkmcnt(2)
	v_mfma_f32_16x16x32_bf16 v[166:169], v[78:81], v[186:189], v[166:169]
	s_waitcnt lgkmcnt(0)
	s_barrier
; #define LAS __attribute__((address_space(3)))
; __device__ __forceinline__ unsigned cvt_pk_bf16(float lo, float hi) { const float __attribute__((ext_vector_type(2))) v = {lo, hi}; return __builtin_bit_cast(unsigned, __builtin_convertvector(v, bf16x2_t)); }
; template <bool LOCAL>
; __device__ __forceinline__ void na_unit(const bf16* P, const bf16* VT, bf16* YCAT, const LAS float* rpb_l, LAS bf16* buf, int b, int gr, int hp, int qblk, int tid) {
;     ...
;                 for (int e = 0; e < 4; ++e) { p[e] = __expf(sl[2 * (c < 8 ? c : 0)][e] - m); p[4 + e] = __expf(sl[2 * (c < 8 ? c : 0) + 1][e] - m); }
; #pragma unroll
;                 for (int e = 0; e < 8; ++e) lsum += p[e];
;                 const bf16x8 pf = __builtin_bit_cast(bf16x8, (v4u){pg8::cvt_pk_bf16(p[0], p[1]), pg8::cvt_pk_bf16(p[2], p[3]), pg8::cvt_pk_bf16(p[4], p[5]), pg8::cvt_pk_bf16(p[6], p[7])});
; #pragma unroll
;                 for (int dt = 0; dt < 4; ++dt) { const LAS bf16* vp = cb + (16 * dt + fr) * 72 + kc0 + 4 * fq;
;                     o[dt] = __builtin_amdgcn_mfma_f32_16x16x32_bf16(frag44(vp, vp + 16), pf, o[dt], 0, 0, 0); }
;             } else {
;                 const int cc = c - NLOC;
; #pragma unroll
;                 for (int p2 = 0; p2 < 2; ++p2) {
;                     float p[8];
; #pragma unroll
;                     for (int e = 0; e < 4; ++e) { p[e] = __expf(sc[4 * (cc >= 0 ? cc : 0) + 2 * p2][e] - m); p[4 + e] = __expf(sc[4 * (cc >= 0 ? cc : 0) + 2 * p2 + 1][e] - m); }
; #pragma unroll
;                     for (int e = 0; e < 8; ++e) lsum += p[e];
;                     const bf16x8 pf = __builtin_bit_cast(bf16x8, (v4u){pg8::cvt_pk_bf16(p[0], p[1]), pg8::cvt_pk_bf16(p[2], p[3]), pg8::cvt_pk_bf16(p[4], p[5]), pg8::cvt_pk_bf16(p[6], p[7])});
; #pragma unroll
;                     for (int dt = 0; dt < 4; ++dt) { const LAS bf16* vp = cb + (16 * dt + fr) * 72 + 32 * p2 + 4 * fq;
;                         o[dt] = __builtin_amdgcn_mfma_f32_16x16x32_bf16(frag44(vp, vp + 16), pf, o[dt], 0, 0, 0); }
	v_sub_f32_e32 v70, v148, v132
	v_sub_f32_e32 v79, v145, v132
	v_sub_f32_e32 v81, v151, v132
	ds_read2_b64 v[146:149], v159 offset1:4
	v_mul_f32_e32 v70, 0x3fb8aa3b, v70
	v_mul_f32_e32 v79, 0x3fb8aa3b, v79
	v_mul_f32_e32 v81, 0x3fb8aa3b, v81
	v_mul_f32_e32 v144, 0x3fb8aa3b, v144
	v_exp_f32_e32 v78, v70
	v_sub_f32_e32 v70, v154, v132
	v_exp_f32_e32 v80, v79
	v_sub_f32_e32 v79, v152, v132
	v_exp_f32_e32 v143, v81
	v_sub_f32_e32 v81, v156, v132
	v_exp_f32_e32 v145, v144
	v_sub_f32_e32 v144, v153, v132
	v_mul_f32_e32 v70, 0x3fb8aa3b, v70
	v_mul_f32_e32 v79, 0x3fb8aa3b, v79
	v_mul_f32_e32 v81, 0x3fb8aa3b, v81
	v_mul_f32_e32 v144, 0x3fb8aa3b, v144
	v_exp_f32_e32 v70, v70
	v_exp_f32_e32 v79, v79
	v_exp_f32_e32 v81, v81
	v_exp_f32_e32 v144, v144
	v_cvt_pk_bf16_f32 v150, v78, v80
	v_cvt_pk_bf16_f32 v151, v143, v145
	v_cvt_pk_bf16_f32 v152, v70, v79
	v_cvt_pk_bf16_f32 v153, v81, v144
	v_mfma_f32_16x16x32_bf16 v[174:177], v[182:185], v[186:189], v[174:177]
	v_fma_f32 v62, v62, s66, -v132
	v_fma_f32 v63, v63, s66, -v132
	v_fma_f32 v64, v64, s66, -v132
	s_waitcnt lgkmcnt(0)
	v_mfma_f32_16x16x32_bf16 v[162:165], v[146:149], v[150:153], v[162:165]
	ds_read2_b64 v[146:149], v158 offset0:32 offset1:36
	v_fma_f32 v65, v65, s66, -v132
	v_mul_f32_e32 v62, 0x3fb8aa3b, v62
	s_waitcnt lgkmcnt(0)
	v_mfma_f32_16x16x32_bf16 v[156:159], v[146:149], v[150:153], v[170:173]
	ds_read2_b64 v[146:149], v160 offset0:64 offset1:68
	v_mul_f32_e32 v63, 0x3fb8aa3b, v63
	v_mul_f32_e32 v64, 0x3fb8aa3b, v64
	s_waitcnt lgkmcnt(0)
	v_mfma_f32_16x16x32_bf16 v[170:173], v[146:149], v[150:153], v[174:177]
	ds_read2_b64 v[146:149], v161 offset0:96 offset1:100
	s_nop 1
	global_load_dwordx4 v[174:177], v[6:7], off offset:128
	global_load_dwordx4 v[178:181], v[8:9], off offset:128
	s_waitcnt vmcnt(3)
	ds_write_b128 v75, v[190:193]
	s_waitcnt vmcnt(2)
	ds_write_b128 v75, v[194:197] offset:9216
	s_waitcnt lgkmcnt(2)
	v_mfma_f32_16x16x32_bf16 v[148:151], v[146:149], v[150:153], v[166:169]
	s_waitcnt lgkmcnt(0)
	s_barrier
	s_nop 0
	ds_read2_b64 v[166:169], v155 offset1:4
	v_mul_f32_e32 v65, 0x3fb8aa3b, v65
	v_exp_f32_e32 v146, v62
	v_fma_f32 v62, v66, s66, -v132
	v_exp_f32_e32 v66, v63
	v_fma_f32 v63, v67, s66, -v132
	v_exp_f32_e32 v67, v64
	v_fma_f32 v64, v68, s66, -v132
	v_exp_f32_e32 v68, v65
	v_fma_f32 v65, v69, s66, -v132
	v_mul_f32_e32 v62, 0x3fb8aa3b, v62
	v_mul_f32_e32 v63, 0x3fb8aa3b, v63
	v_mul_f32_e32 v64, 0x3fb8aa3b, v64
	v_mul_f32_e32 v65, 0x3fb8aa3b, v65
	v_exp_f32_e32 v62, v62
	v_exp_f32_e32 v63, v63
	v_exp_f32_e32 v64, v64
	v_exp_f32_e32 v65, v65
	v_cvt_pk_bf16_f32 v182, v146, v66
	v_cvt_pk_bf16_f32 v183, v67, v68
	v_cvt_pk_bf16_f32 v184, v62, v63
	v_cvt_pk_bf16_f32 v185, v64, v65
	v_add_u32_e32 v147, 0x800, v155
	v_add_u32_e32 v152, 0x1000, v155
	s_waitcnt lgkmcnt(0)
	v_mfma_f32_16x16x32_bf16 v[160:163], v[166:169], v[182:185], v[162:165]
	v_add_u32_e32 v153, 0x1800, v155
	v_fma_f32 v58, v58, s66, -v132
	v_fma_f32 v54, v54, s66, -v132
	ds_read2_b64 v[164:167], v147 offset0:32 offset1:36
	s_waitcnt lgkmcnt(0)
	v_mfma_f32_16x16x32_bf16 v[156:159], v[164:167], v[182:185], v[156:159]
	ds_read2_b64 v[164:167], v152 offset0:64 offset1:68
	v_fma_f32 v59, v59, s66, -v132
	v_fma_f32 v55, v55, s66, -v132
	s_waitcnt lgkmcnt(0)
	v_mfma_f32_16x16x32_bf16 v[164:167], v[164:167], v[182:185], v[170:173]
	s_nop 2
	ds_read2_b64 v[168:171], v153 offset0:96 offset1:100
	v_fma_f32 v60, v60, s66, -v132
	v_fma_f32 v56, v56, s66, -v132
	s_waitcnt lgkmcnt(0)
	v_mfma_f32_16x16x32_bf16 v[148:151], v[168:171], v[182:185], v[148:151]
	ds_read2_b64 v[168:171], v155 offset0:8 offset1:12
	v_fma_f32 v61, v61, s66, -v132
	v_fma_f32 v57, v57, s66, -v132
	v_mul_f32_e32 v58, 0x3fb8aa3b, v58
	v_mul_f32_e32 v54, 0x3fb8aa3b, v54
	v_mul_f32_e32 v59, 0x3fb8aa3b, v59
	v_mul_f32_e32 v55, 0x3fb8aa3b, v55
	v_mul_f32_e32 v60, 0x3fb8aa3b, v60
	v_mul_f32_e32 v56, 0x3fb8aa3b, v56
	v_mul_f32_e32 v61, 0x3fb8aa3b, v61
	v_mul_f32_e32 v57, 0x3fb8aa3b, v57
	v_exp_f32_e32 v58, v58
	v_exp_f32_e32 v54, v54
	v_exp_f32_e32 v59, v59
	v_exp_f32_e32 v55, v55
	v_exp_f32_e32 v60, v60
	v_exp_f32_e32 v56, v56
	v_exp_f32_e32 v61, v61
	v_exp_f32_e32 v57, v57
	v_cvt_pk_bf16_f32 v182, v58, v59
	v_cvt_pk_bf16_f32 v184, v54, v55
	v_cvt_pk_bf16_f32 v183, v60, v61
	v_cvt_pk_bf16_f32 v185, v56, v57
	v_fma_f32 v46, v46, s66, -v132
	v_fma_f32 v47, v47, s66, -v132
	s_waitcnt lgkmcnt(0)
	v_mfma_f32_16x16x32_bf16 v[160:163], v[168:171], v[182:185], v[160:163]
	ds_read2_b64 v[168:171], v147 offset0:40 offset1:44
	v_fma_f32 v48, v48, s66, -v132
	v_mul_f32_e32 v46, 0x3fb8aa3b, v46
	s_waitcnt lgkmcnt(0)
	v_mfma_f32_16x16x32_bf16 v[156:159], v[168:171], v[182:185], v[156:159]
	ds_read2_b64 v[168:171], v152 offset0:72 offset1:76
	v_mul_f32_e32 v47, 0x3fb8aa3b, v47
	v_mul_f32_e32 v48, 0x3fb8aa3b, v48
	s_waitcnt lgkmcnt(0)
	v_mfma_f32_16x16x32_bf16 v[164:167], v[168:171], v[182:185], v[164:167]
	ds_read2_b64 v[168:171], v153 offset0:104 offset1:108
	v_exp_f32_e32 v69, v46
	v_fma_f32 v46, v50, s66, -v132
	v_exp_f32_e32 v50, v47
	v_fma_f32 v47, v51, s66, -v132
	v_exp_f32_e32 v51, v48
	v_fma_f32 v48, v52, s66, -v132
	v_add_u32_e32 v52, 0x4800, v155
	global_load_dwordx4 v[186:189], v[6:7], off offset:256
	global_load_dwordx4 v[190:193], v[8:9], off offset:256
	s_waitcnt lgkmcnt(0)
	v_mfma_f32_16x16x32_bf16 v[148:151], v[168:171], v[182:185], v[148:151]
	s_waitcnt vmcnt(3)
	ds_write_b128 v75, v[174:177] offset:18432
	s_waitcnt vmcnt(2)
	ds_write_b128 v75, v[178:181] offset:27648
	s_waitcnt lgkmcnt(0)
	s_barrier
; #define LAS __attribute__((address_space(3)))
; __device__ __forceinline__ unsigned cvt_pk_bf16(float lo, float hi) { const float __attribute__((ext_vector_type(2))) v = {lo, hi}; return __builtin_bit_cast(unsigned, __builtin_convertvector(v, bf16x2_t)); }
; template <bool LOCAL>
; __device__ __forceinline__ void na_unit(const bf16* P, const bf16* VT, bf16* YCAT, const LAS float* rpb_l, LAS bf16* buf, int b, int gr, int hp, int qblk, int tid) {
;     ...
;             } else {
;                 const int cc = c - NLOC;
; #pragma unroll
;                 for (int p2 = 0; p2 < 2; ++p2) {
;                     float p[8];
; #pragma unroll
;                     for (int e = 0; e < 4; ++e) { p[e] = __expf(sc[4 * (cc >= 0 ? cc : 0) + 2 * p2][e] - m); p[4 + e] = __expf(sc[4 * (cc >= 0 ? cc : 0) + 2 * p2 + 1][e] - m); }
; #pragma unroll
;                     for (int e = 0; e < 8; ++e) lsum += p[e];
;                     const bf16x8 pf = __builtin_bit_cast(bf16x8, (v4u){pg8::cvt_pk_bf16(p[0], p[1]), pg8::cvt_pk_bf16(p[2], p[3]), pg8::cvt_pk_bf16(p[4], p[5]), pg8::cvt_pk_bf16(p[6], p[7])});
; #pragma unroll
;                     for (int dt = 0; dt < 4; ++dt) { const LAS bf16* vp = cb + (16 * dt + fr) * 72 + 32 * p2 + 4 * fq;
;                         o[dt] = __builtin_amdgcn_mfma_f32_16x16x32_bf16(frag44(vp, vp + 16), pf, o[dt], 0, 0, 0); }
;                 }
	v_fma_f32 v49, v49, s66, -v132
	ds_read2_b64 v[168:171], v52 offset1:4
	v_mul_f32_e32 v49, 0x3fb8aa3b, v49
	v_exp_f32_e32 v154, v49
	v_fma_f32 v49, v53, s66, -v132
	v_mul_f32_e32 v46, 0x3fb8aa3b, v46
	v_mul_f32_e32 v47, 0x3fb8aa3b, v47
	v_mul_f32_e32 v48, 0x3fb8aa3b, v48
	v_mul_f32_e32 v49, 0x3fb8aa3b, v49
	v_exp_f32_e32 v46, v46
	v_exp_f32_e32 v47, v47
	v_exp_f32_e32 v48, v48
	v_exp_f32_e32 v53, v49
	v_cvt_pk_bf16_f32 v172, v69, v50
	v_cvt_pk_bf16_f32 v173, v51, v154
	v_cvt_pk_bf16_f32 v174, v46, v47
	v_cvt_pk_bf16_f32 v175, v48, v53
	v_add_u32_e32 v176, 0x5000, v155
	v_add_u32_e32 v177, 0x5800, v155
	s_waitcnt lgkmcnt(0)
	v_mfma_f32_16x16x32_bf16 v[160:163], v[168:171], v[172:175], v[160:163]
	ds_read2_b64 v[168:171], v176 offset0:32 offset1:36
	v_add_u32_e32 v49, 0x6000, v155
	v_fma_f32 v38, v38, s66, -v132
	s_waitcnt lgkmcnt(0)
	v_mfma_f32_16x16x32_bf16 v[156:159], v[168:171], v[172:175], v[156:159]
	ds_read2_b64 v[168:171], v177 offset0:64 offset1:68
	v_mul_f32_e32 v38, 0x3fb8aa3b, v38
	v_fma_f32 v42, v42, s66, -v132
	s_waitcnt lgkmcnt(0)
	v_mfma_f32_16x16x32_bf16 v[164:167], v[168:171], v[172:175], v[164:167]
	ds_read2_b64 v[168:171], v49 offset0:96 offset1:100
	v_mul_f32_e32 v42, 0x3fb8aa3b, v42
	v_fma_f32 v30, v30, s66, -v132
	s_waitcnt lgkmcnt(0)
	v_mfma_f32_16x16x32_bf16 v[148:151], v[168:171], v[172:175], v[148:151]
	v_exp_f32_e32 v173, v38
	v_fma_f32 v38, v43, s66, -v132
	v_mul_f32_e32 v38, 0x3fb8aa3b, v38
	v_exp_f32_e32 v174, v38
	v_fma_f32 v38, v39, s66, -v132
	v_mul_f32_e32 v38, 0x3fb8aa3b, v38
	v_exp_f32_e32 v175, v38
	v_fma_f32 v38, v44, s66, -v132
	v_mul_f32_e32 v38, 0x3fb8aa3b, v38
	v_exp_f32_e32 v178, v38
	v_fma_f32 v38, v40, s66, -v132
	v_mul_f32_e32 v38, 0x3fb8aa3b, v38
	v_exp_f32_e32 v172, v42
	v_exp_f32_e32 v179, v38
	v_fma_f32 v38, v45, s66, -v132
	ds_read2_b64 v[42:45], v52 offset0:8 offset1:12
	v_mul_f32_e32 v38, 0x3fb8aa3b, v38
	v_exp_f32_e32 v180, v38
	v_fma_f32 v38, v41, s66, -v132
	v_mul_f32_e32 v38, 0x3fb8aa3b, v38
	v_exp_f32_e32 v181, v38
	v_cvt_pk_bf16_f32 v38, v172, v174
	v_cvt_pk_bf16_f32 v39, v178, v180
	v_cvt_pk_bf16_f32 v40, v173, v175
	v_cvt_pk_bf16_f32 v41, v179, v181
	v_mul_f32_e32 v30, 0x3fb8aa3b, v30
	v_fma_f32 v22, v22, s66, -v132
	s_waitcnt lgkmcnt(0)
	v_mfma_f32_16x16x32_bf16 v[42:45], v[42:45], v[38:41], v[160:163]
	v_mul_f32_e32 v22, 0x3fb8aa3b, v22
	v_fma_f32 v26, v26, s66, -v132
	v_mul_f32_e32 v26, 0x3fb8aa3b, v26
	ds_read2_b64 v[160:163], v176 offset0:40 offset1:44
	s_waitcnt lgkmcnt(0)
	v_mfma_f32_16x16x32_bf16 v[156:159], v[160:163], v[38:41], v[156:159]
	ds_read2_b64 v[160:163], v177 offset0:72 offset1:76
	v_fma_f32 v2, v2, s66, -v132
	v_mul_f32_e32 v2, 0x3fb8aa3b, v2
	s_waitcnt lgkmcnt(0)
	v_mfma_f32_16x16x32_bf16 v[160:163], v[160:163], v[38:41], v[164:167]
	s_nop 2
	ds_read2_b64 v[164:167], v49 offset0:104 offset1:108
	global_load_dwordx4 v[168:171], v[6:7], off offset:384
	s_nop 0
	global_load_dwordx4 v[6:9], v[8:9], off offset:384
	s_waitcnt vmcnt(3)
	ds_write_b128 v75, v[186:189]
	s_waitcnt vmcnt(2)
	ds_write_b128 v75, v[190:193] offset:9216
	s_waitcnt lgkmcnt(2)
	v_mfma_f32_16x16x32_bf16 v[38:41], v[164:167], v[38:41], v[148:151]
	v_exp_f32_e32 v164, v30
	v_fma_f32 v30, v34, s66, -v132
	v_mul_f32_e32 v30, 0x3fb8aa3b, v30
	v_exp_f32_e32 v165, v30
	v_fma_f32 v30, v31, s66, -v132
	v_mul_f32_e32 v30, 0x3fb8aa3b, v30
	v_exp_f32_e32 v166, v30
	v_fma_f32 v30, v35, s66, -v132
	v_mul_f32_e32 v30, 0x3fb8aa3b, v30
	v_exp_f32_e32 v167, v30
	v_fma_f32 v30, v32, s66, -v132
	v_mul_f32_e32 v30, 0x3fb8aa3b, v30
	v_exp_f32_e32 v182, v30
	v_fma_f32 v30, v36, s66, -v132
	v_mul_f32_e32 v30, 0x3fb8aa3b, v30
	v_exp_f32_e32 v183, v30
	v_fma_f32 v30, v33, s66, -v132
	s_waitcnt lgkmcnt(0)
	s_barrier
	v_mul_f32_e32 v34, 0x3fb8aa3b, v30
	ds_read2_b64 v[30:33], v155 offset1:4
	v_exp_f32_e32 v184, v34
	v_fma_f32 v34, v37, s66, -v132
	v_mul_f32_e32 v34, 0x3fb8aa3b, v34
	v_exp_f32_e32 v185, v34
	v_cvt_pk_bf16_f32 v34, v164, v166
	v_cvt_pk_bf16_f32 v35, v182, v184
	v_cvt_pk_bf16_f32 v36, v165, v167
	v_cvt_pk_bf16_f32 v37, v183, v185
	ds_read2_b64 v[148:151], v152 offset0:64 offset1:68
	v_fma_f32 v10, v10, s66, -v132
	s_waitcnt lgkmcnt(1)
	v_mfma_f32_16x16x32_bf16 v[30:33], v[30:33], v[34:37], v[42:45]
	v_mul_f32_e32 v10, 0x3fb8aa3b, v10
	s_nop 1
	ds_read2_b64 v[42:45], v147 offset0:32 offset1:36
	s_waitcnt lgkmcnt(0)
	v_mfma_f32_16x16x32_bf16 v[42:45], v[42:45], v[34:37], v[156:159]
	s_nop 2
	ds_read2_b64 v[156:159], v153 offset0:96 offset1:100
	v_mfma_f32_16x16x32_bf16 v[148:151], v[148:151], v[34:37], v[160:163]
	s_waitcnt lgkmcnt(0)
	v_mfma_f32_16x16x32_bf16 v[34:37], v[156:159], v[34:37], v[38:41]
	v_exp_f32_e32 v157, v22
	v_fma_f32 v22, v27, s66, -v132
	v_mul_f32_e32 v22, 0x3fb8aa3b, v22
	v_exp_f32_e32 v158, v22
	v_fma_f32 v22, v23, s66, -v132
	v_mul_f32_e32 v22, 0x3fb8aa3b, v22
	v_exp_f32_e32 v159, v22
	v_fma_f32 v22, v28, s66, -v132
	v_mul_f32_e32 v22, 0x3fb8aa3b, v22
	v_exp_f32_e32 v160, v22
	v_fma_f32 v22, v24, s66, -v132
	v_mul_f32_e32 v22, 0x3fb8aa3b, v22
	v_exp_f32_e32 v156, v26
	v_exp_f32_e32 v161, v22
	v_fma_f32 v22, v29, s66, -v132
	ds_read2_b64 v[26:29], v155 offset0:8 offset1:12
	v_mul_f32_e32 v22, 0x3fb8aa3b, v22
	v_exp_f32_e32 v155, v22
	v_fma_f32 v22, v25, s66, -v132
	v_mul_f32_e32 v22, 0x3fb8aa3b, v22
	v_exp_f32_e32 v162, v22
	v_cvt_pk_bf16_f32 v22, v156, v158
	v_cvt_pk_bf16_f32 v23, v160, v155
	v_cvt_pk_bf16_f32 v24, v157, v159
	v_cvt_pk_bf16_f32 v25, v161, v162
	ds_read2_b64 v[38:41], v152 offset0:72 offset1:76
	s_waitcnt lgkmcnt(1)
	v_mfma_f32_16x16x32_bf16 v[26:29], v[26:29], v[22:25], v[30:33]
	s_nop 2
	ds_read2_b64 v[30:33], v147 offset0:40 offset1:44
	s_waitcnt lgkmcnt(0)
	v_mfma_f32_16x16x32_bf16 v[30:33], v[30:33], v[22:25], v[42:45]
	s_nop 2
	ds_read2_b64 v[42:45], v153 offset0:104 offset1:108
	s_waitcnt vmcnt(1)
	ds_write_b128 v75, v[168:171] offset:18432
	s_waitcnt vmcnt(0)
	ds_write_b128 v75, v[6:9] offset:27648
	v_fma_f32 v6, v14, s66, -v132
	v_mul_f32_e32 v6, 0x3fb8aa3b, v6
	v_mfma_f32_16x16x32_bf16 v[38:41], v[38:41], v[22:25], v[148:151]
	s_waitcnt lgkmcnt(0)
	s_barrier
; #define LAS __attribute__((address_space(3)))
; __device__ __forceinline__ unsigned cvt_pk_bf16(float lo, float hi) { const float __attribute__((ext_vector_type(2))) v = {lo, hi}; return __builtin_bit_cast(unsigned, __builtin_convertvector(v, bf16x2_t)); }
; #define NA_STORE(sidx) do { LAS bf16* d_ = buf + ((sidx) & 1) * 9216; _Pragma("unroll") for (int q_ = 0; q_ < 2; ++q_) *(LAS v4u*)(d_ + q_ * 4608 + lrow * 72 + lseg * 8) = ld[(sidx) & 1][q_]; } while (0)
; template <bool LOCAL>
; __device__ __forceinline__ void na_unit(const bf16* P, const bf16* VT, bf16* YCAT, const LAS float* rpb_l, LAS bf16* buf, int b, int gr, int hp, int qblk, int tid) {
;     ...
;                     for (int e = 0; e < 4; ++e) { p[e] = __expf(sc[4 * (cc >= 0 ? cc : 0) + 2 * p2][e] - m); p[4 + e] = __expf(sc[4 * (cc >= 0 ? cc : 0) + 2 * p2 + 1][e] - m); }
; #pragma unroll
;                     for (int e = 0; e < 8; ++e) lsum += p[e];
;                     const bf16x8 pf = __builtin_bit_cast(bf16x8, (v4u){pg8::cvt_pk_bf16(p[0], p[1]), pg8::cvt_pk_bf16(p[2], p[3]), pg8::cvt_pk_bf16(p[4], p[5]), pg8::cvt_pk_bf16(p[6], p[7])});
; #pragma unroll
;                     for (int dt = 0; dt < 4; ++dt) { const LAS bf16* vp = cb + (16 * dt + fr) * 72 + 32 * p2 + 4 * fq;
;                         o[dt] = __builtin_amdgcn_mfma_f32_16x16x32_bf16(frag44(vp, vp + 16), pf, o[dt], 0, 0, 0); }
;                 }
;             }
;         }
;         if (sidx + 1 < 2 * NCH) NA_STORE(sidx + 1);
;         __syncthreads();
;     }
;     ...
;     lsum += __shfl_xor(lsum, 16); lsum += __shfl_xor(lsum, 32);
	v_mfma_f32_16x16x32_bf16 v[22:25], v[42:45], v[22:25], v[34:37]
	v_ashrrev_i32_e32 v75, 31, v74
	s_nop 1
	v_exp_f32_e32 v34, v6
	v_fma_f32 v6, v18, s66, -v132
	v_mul_f32_e32 v6, 0x3fb8aa3b, v6
	v_exp_f32_e32 v35, v6
	v_fma_f32 v6, v15, s66, -v132
	v_mul_f32_e32 v6, 0x3fb8aa3b, v6
	v_exp_f32_e32 v36, v6
	v_fma_f32 v6, v19, s66, -v132
	v_mul_f32_e32 v6, 0x3fb8aa3b, v6
	v_exp_f32_e32 v37, v6
	v_fma_f32 v6, v16, s66, -v132
	v_mul_f32_e32 v6, 0x3fb8aa3b, v6
	v_exp_f32_e32 v42, v6
	v_fma_f32 v6, v20, s66, -v132
	v_mul_f32_e32 v6, 0x3fb8aa3b, v6
	v_exp_f32_e32 v43, v6
	v_fma_f32 v6, v17, s66, -v132
	v_mul_f32_e32 v14, 0x3fb8aa3b, v6
	ds_read2_b64 v[6:9], v52 offset1:4
	v_exp_f32_e32 v44, v14
	v_fma_f32 v14, v21, s66, -v132
	v_mul_f32_e32 v14, 0x3fb8aa3b, v14
	v_exp_f32_e32 v45, v14
	v_cvt_pk_bf16_f32 v14, v34, v36
	v_cvt_pk_bf16_f32 v15, v42, v44
	v_cvt_pk_bf16_f32 v16, v35, v37
	v_cvt_pk_bf16_f32 v17, v43, v45
	ds_read2_b64 v[18:21], v176 offset0:32 offset1:36
	s_waitcnt lgkmcnt(1)
	v_mfma_f32_16x16x32_bf16 v[6:9], v[6:9], v[14:17], v[26:29]
	s_nop 2
	ds_read2_b64 v[26:29], v177 offset0:64 offset1:68
	s_waitcnt lgkmcnt(0)
	v_mfma_f32_16x16x32_bf16 v[26:29], v[26:29], v[14:17], v[38:41]
	s_nop 2
	v_add_f32_e32 v38, 0, v126
	v_add_f32_e32 v38, v95, v38
	v_add_f32_e32 v38, v94, v38
	v_add_f32_e32 v38, v99, v38
	v_add_f32_e32 v38, v91, v38
	v_add_f32_e32 v38, v90, v38
	v_add_f32_e32 v38, v93, v38
	v_add_f32_e32 v38, v92, v38
	v_add_f32_e32 v38, v85, v38
	v_add_f32_e32 v38, v89, v38
	v_add_f32_e32 v38, v97, v38
	v_add_f32_e32 v38, v98, v38
	v_add_f32_e32 v38, v76, v38
	v_add_f32_e32 v38, v86, v38
	v_add_f32_e32 v38, v96, v38
	v_add_f32_e32 v38, v100, v38
	v_add_f32_e32 v38, v103, v38
	v_add_f32_e32 v38, v104, v38
	v_add_f32_e32 v38, v107, v38
	v_add_f32_e32 v38, v106, v38
	v_add_f32_e32 v38, v101, v38
	v_add_f32_e32 v38, v102, v38
	v_add_f32_e32 v38, v105, v38
	v_add_f32_e32 v38, v108, v38
	v_add_f32_e32 v38, v110, v38
	v_add_f32_e32 v38, v112, v38
	v_add_f32_e32 v38, v114, v38
	v_add_f32_e32 v38, v115, v38
	v_add_f32_e32 v38, v109, v38
	v_add_f32_e32 v38, v111, v38
	v_add_f32_e32 v38, v113, v38
	v_add_f32_e32 v38, v116, v38
	v_add_f32_e32 v38, v118, v38
	v_add_f32_e32 v38, v120, v38
	v_add_f32_e32 v38, v122, v38
	v_add_f32_e32 v38, v123, v38
	v_add_f32_e32 v38, v117, v38
	v_add_f32_e32 v38, v119, v38
	v_add_f32_e32 v38, v121, v38
	v_add_f32_e32 v38, v124, v38
	v_add_f32_e32 v38, v127, v38
	v_add_f32_e32 v38, v129, v38
	v_add_f32_e32 v38, v131, v38
	v_add_f32_e32 v38, v133, v38
	v_add_f32_e32 v38, v125, v38
	v_add_f32_e32 v38, v128, v38
	v_add_f32_e32 v38, v130, v38
	v_add_f32_e32 v38, v134, v38
	v_add_f32_e32 v38, v136, v38
	v_add_f32_e32 v38, v138, v38
	v_add_f32_e32 v38, v140, v38
	v_add_f32_e32 v38, v141, v38
	v_add_f32_e32 v38, v135, v38
	v_add_f32_e32 v38, v137, v38
	v_add_f32_e32 v38, v139, v38
	v_add_f32_e32 v38, v142, v38
	v_add_f32_e32 v38, v78, v38
	v_add_f32_e32 v38, v80, v38
	v_add_f32_e32 v38, v143, v38
	v_add_f32_e32 v38, v145, v38
	v_add_f32_e32 v38, v70, v38
	v_add_f32_e32 v38, v79, v38
	v_add_f32_e32 v38, v81, v38
	v_add_f32_e32 v38, v144, v38
	v_add_f32_e32 v38, v146, v38
	v_add_f32_e32 v38, v66, v38
	v_add_f32_e32 v38, v67, v38
	v_add_f32_e32 v38, v68, v38
	v_add_f32_e32 v38, v62, v38
	v_add_f32_e32 v38, v63, v38
	v_add_f32_e32 v38, v64, v38
	v_add_f32_e32 v38, v65, v38
	v_add_f32_e32 v38, v58, v38
	v_add_f32_e32 v38, v59, v38
	v_add_f32_e32 v38, v60, v38
	v_add_f32_e32 v38, v61, v38
	v_add_f32_e32 v38, v54, v38
	v_add_f32_e32 v38, v55, v38
	v_add_f32_e32 v38, v56, v38
	v_add_f32_e32 v38, v57, v38
	v_add_f32_e32 v38, v69, v38
	v_add_f32_e32 v38, v50, v38
	v_add_f32_e32 v38, v51, v38
	v_add_f32_e32 v38, v154, v38
	v_add_f32_e32 v38, v46, v38
	v_add_f32_e32 v38, v47, v38
	v_add_f32_e32 v38, v48, v38
	v_add_f32_e32 v38, v53, v38
	v_add_f32_e32 v38, v172, v38
	v_mfma_f32_16x16x32_bf16 v[18:21], v[18:21], v[14:17], v[30:33]
	v_add_f32_e32 v38, v174, v38
	v_add_f32_e32 v38, v178, v38
	v_add_f32_e32 v38, v180, v38
	ds_read2_b64 v[30:33], v49 offset0:96 offset1:100
	v_add_f32_e32 v38, v173, v38
	v_add_f32_e32 v38, v175, v38
	v_add_f32_e32 v38, v179, v38
	v_add_f32_e32 v38, v181, v38
	v_add_f32_e32 v38, v164, v38
	v_add_f32_e32 v38, v166, v38
	s_waitcnt lgkmcnt(0)
	v_mfma_f32_16x16x32_bf16 v[14:17], v[30:33], v[14:17], v[22:25]
	v_add_f32_e32 v38, v182, v38
	s_nop 1
	v_exp_f32_e32 v23, v2
	v_fma_f32 v2, v11, s66, -v132
	v_mul_f32_e32 v2, 0x3fb8aa3b, v2
	v_add_f32_e32 v38, v184, v38
	v_exp_f32_e32 v24, v2
	v_fma_f32 v2, v3, s66, -v132
	v_add_f32_e32 v38, v165, v38
	v_mul_f32_e32 v2, 0x3fb8aa3b, v2
	v_add_f32_e32 v38, v167, v38
	v_exp_f32_e32 v25, v2
	v_fma_f32 v2, v12, s66, -v132
	v_add_f32_e32 v38, v183, v38
	v_mul_f32_e32 v2, 0x3fb8aa3b, v2
	v_add_f32_e32 v38, v185, v38
	v_exp_f32_e32 v30, v2
	v_fma_f32 v2, v4, s66, -v132
	v_add_f32_e32 v38, v156, v38
	v_mul_f32_e32 v2, 0x3fb8aa3b, v2
	v_add_f32_e32 v38, v158, v38
	v_exp_f32_e32 v22, v10
	v_exp_f32_e32 v31, v2
	v_fma_f32 v2, v13, s66, -v132
	ds_read2_b64 v[10:13], v52 offset0:8 offset1:12
	v_add_f32_e32 v38, v160, v38
	v_mul_f32_e32 v2, 0x3fb8aa3b, v2
	v_add_f32_e32 v38, v155, v38
	v_exp_f32_e32 v32, v2
	v_fma_f32 v2, v5, s66, -v132
	v_add_f32_e32 v38, v157, v38
	v_mul_f32_e32 v2, 0x3fb8aa3b, v2
	v_add_f32_e32 v38, v159, v38
	v_exp_f32_e32 v33, v2
	v_add_f32_e32 v38, v161, v38
	v_add_f32_e32 v38, v162, v38
	v_add_f32_e32 v34, v34, v38
	v_add_f32_e32 v34, v36, v34
	v_cvt_pk_bf16_f32 v2, v22, v24
	v_cvt_pk_bf16_f32 v3, v30, v32
	v_cvt_pk_bf16_f32 v4, v23, v25
	v_cvt_pk_bf16_f32 v5, v31, v33
	v_add_f32_e32 v34, v42, v34
	v_add_f32_e32 v34, v44, v34
	s_waitcnt lgkmcnt(0)
	v_mfma_f32_16x16x32_bf16 v[6:9], v[10:13], v[2:5], v[6:9]
	ds_read2_b64 v[10:13], v176 offset0:40 offset1:44
	v_add_f32_e32 v34, v35, v34
	v_add_f32_e32 v34, v37, v34
	v_add_f32_e32 v34, v43, v34
	v_add_f32_e32 v34, v45, v34
	v_add_f32_e32 v22, v22, v34
	v_add_f32_e32 v22, v24, v22
	v_add_f32_e32 v22, v30, v22
	v_add_f32_e32 v22, v32, v22
	s_waitcnt lgkmcnt(0)
	v_mfma_f32_16x16x32_bf16 v[10:13], v[10:13], v[2:5], v[18:21]
	v_add_f32_e32 v22, v23, v22
	v_add_f32_e32 v22, v25, v22
	v_add_f32_e32 v22, v31, v22
	ds_read2_b64 v[18:21], v177 offset0:72 offset1:76
	v_add_f32_e32 v30, v33, v22
	ds_bpermute_b32 v31, v87, v30
	ds_read2_b64 v[22:25], v49 offset0:104 offset1:108
	s_waitcnt lgkmcnt(2)
	v_mfma_f32_16x16x32_bf16 v[18:21], v[18:21], v[2:5], v[26:29]
	s_waitcnt lgkmcnt(1)
	s_nop 1
	v_add_f32_e32 v26, v30, v31
	ds_bpermute_b32 v27, v88, v26
	v_lshlrev_b32_e32 v70, 1, v77
	s_waitcnt lgkmcnt(1)
	v_mfma_f32_16x16x32_bf16 v[14:17], v[22:25], v[2:5], v[14:17]
	s_waitcnt lgkmcnt(0)
	s_barrier
; __device__ __forceinline__ unsigned cvt_pk_bf16(float lo, float hi) { const float __attribute__((ext_vector_type(2))) v = {lo, hi}; return __builtin_bit_cast(unsigned, __builtin_convertvector(v, bf16x2_t)); }
; template <bool LOCAL>
; __device__ __forceinline__ void na_unit(const bf16* P, const bf16* VT, bf16* YCAT, const LAS float* rpb_l, LAS bf16* buf, int b, int gr, int hp, int qblk, int tid) {
;     ...
;     lsum += __shfl_xor(lsum, 16); lsum += __shfl_xor(lsum, 32);
;     const float inv = 1.f / lsum;
;     bf16* op = YCAT + (size_t)(qrow0 + fr) * D + 512 + h * 64 + 4 * fq;
; #pragma unroll
;     for (int dt = 0; dt < 4; ++dt) { v2u w; w.x = pg8::cvt_pk_bf16(o[dt][0] * inv, o[dt][1] * inv); w.y = pg8::cvt_pk_bf16(o[dt][2] * inv, o[dt][3] * inv); *(v2u*)(op + dt * 16) = w; }
	v_add_f32_e32 v2, v26, v27
	v_div_scale_f32 v3, s[0:1], v2, v2, 1.0
	v_rcp_f32_e32 v4, v3
	s_nop 0
	v_fma_f32 v5, -v3, v4, 1.0
	v_fmac_f32_e32 v4, v5, v4
	v_div_scale_f32 v5, vcc, 1.0, v2, 1.0
	v_mul_f32_e32 v22, v5, v4
	v_fma_f32 v23, -v3, v22, v5
	v_fmac_f32_e32 v22, v23, v4
	v_fma_f32 v3, -v3, v22, v5
	v_div_fmas_f32 v3, v3, v4, v22
	v_div_fixup_f32 v22, v3, v2, 1.0
	v_lshlrev_b64 v[2:3], 11, v[74:75]
	v_lshl_add_u64 v[2:3], s[10:11], 0, v[2:3]
	v_lshl_add_u64 v[2:3], v[72:73], 1, v[2:3]
	v_pk_mul_f32 v[6:7], v[6:7], v[22:23] op_sel_hi:[1,0]
	v_pk_mul_f32 v[8:9], v[8:9], v[22:23] op_sel_hi:[1,0]
	v_lshl_add_u64 v[4:5], v[2:3], 0, v[70:71]
	v_cvt_pk_bf16_f32 v6, v6, v7
	v_cvt_pk_bf16_f32 v7, v8, v9
	global_store_dwordx2 v[4:5], v[6:7], off offset:1024
	v_pk_mul_f32 v[6:7], v[10:11], v[22:23] op_sel_hi:[1,0]
	v_pk_mul_f32 v[8:9], v[12:13], v[22:23] op_sel_hi:[1,0]
	v_cvt_pk_bf16_f32 v6, v6, v7
	v_cvt_pk_bf16_f32 v7, v8, v9
	global_store_dwordx2 v[4:5], v[6:7], off offset:1056
	v_pk_mul_f32 v[6:7], v[18:19], v[22:23] op_sel_hi:[1,0]
	v_pk_mul_f32 v[8:9], v[20:21], v[22:23] op_sel_hi:[1,0]
	v_cvt_pk_bf16_f32 v6, v6, v7
	v_cvt_pk_bf16_f32 v7, v8, v9
	v_lshl_add_u64 v[2:3], v[4:5], 0, s[12:13]
	global_store_dwordx2 v[4:5], v[6:7], off offset:1088
	v_pk_mul_f32 v[4:5], v[14:15], v[22:23] op_sel_hi:[1,0]
	v_pk_mul_f32 v[6:7], v[16:17], v[22:23] op_sel_hi:[1,0]
	v_cvt_pk_bf16_f32 v4, v4, v5
